# flat->global, kscale gain loads de-serialised, MIX1 queue order scan/ret_scan/fox/idx
# speedup vs baseline: 1.0108x; 1.0108x over previous
.LBB0_10:
	s_or_b64 exec, exec, s[4:5]
	v_mul_f32_e32 v8, v19, v19
	v_fmamk_f32 v16, v8, 0xb94c1982, v5
	v_fmaak_f32 v16, v8, v16, 0xbe2aaa9d
	v_mul_f32_e32 v16, v8, v16
	v_fmac_f32_e32 v19, v19, v16
	v_fmamk_f32 v16, v8, 0x37d75334, v11
	v_fmaak_f32 v16, v8, v16, 0x3d2aabf7
	v_fmaak_f32 v16, v8, v16, 0xbf000004
	v_fma_f32 v8, v8, v16, 1.0
	v_and_b32_e32 v16, 1, v18
	v_cmp_eq_u32_e32 vcc, 0, v16
	v_lshlrev_b32_e32 v16, 30, v18
	v_and_b32_e32 v16, 0x80000000, v16
	v_xor_b32_e32 v14, v15, v14
	v_cndmask_b32_e32 v8, v8, v19, vcc
	v_xor_b32_e32 v14, v14, v16
	v_xor_b32_e32 v8, v14, v8
	v_add_u32_e32 v4, s16, v4
	v_cndmask_b32_e64 v8, v13, v8, s[0:1]
	v_cmp_lt_i32_e32 vcc, s41, v4
	global_store_dword v[6:7], v8, off
	s_or_b64 s[20:21], vcc, s[20:21]
	v_lshl_add_u64 v[6:7], v[6:7], 0, s[18:19]
	s_andn2_b64 exec, exec, s[20:21]
	s_cbranch_execz .LBB0_19

.LBB0_13:
	s_or_saveexec_b64 s[0:1], s[22:23]
	v_mul_f32_e64 v8, |v14|, s37
	v_rndne_f32_e32 v8, v8
	s_xor_b64 exec, exec, s[0:1]
	v_cvt_i32_f32_e32 v18, v8
	v_fma_f32 v19, v8, s38, |v14|
	v_fmac_f32_e32 v19, 0xb3a22168, v8
	v_fmac_f32_e32 v19, 0xa7c234c4, v8
	s_or_b64 exec, exec, s[0:1]
	v_mul_f32_e32 v20, v19, v19
	v_fmamk_f32 v21, v20, 0xb94c1982, v5
	v_fmaak_f32 v21, v20, v21, 0xbe2aaa9d
	v_mul_f32_e32 v21, v20, v21
	v_fmac_f32_e32 v19, v19, v21
	v_fmamk_f32 v21, v20, 0x37d75334, v11
	v_fmaak_f32 v21, v20, v21, 0x3d2aabf7
	v_fmaak_f32 v21, v20, v21, 0xbf000004
	v_fma_f32 v20, v20, v21, 1.0
	v_and_b32_e32 v21, 1, v18
	v_cmp_eq_u32_e32 vcc, 0, v21
	v_lshlrev_b32_e32 v18, 30, v18
	v_cmp_class_f32_e64 s[0:1], v14, s40
	v_cndmask_b32_e64 v19, -v19, v20, vcc
	v_bitop3_b32 v18, v18, v19, s39 bitop3:0x6c
	v_cndmask_b32_e64 v20, v13, v18, s[0:1]
	v_add_co_u32_e32 v18, vcc, 0xfff00000, v6
	s_nop 1
	v_addc_co_u32_e32 v19, vcc, -1, v7, vcc
	global_store_dword v[18:19], v20, off
	s_and_saveexec_b64 s[4:5], s[8:9]
	s_xor_b64 s[22:23], exec, s[4:5]
	s_cbranch_execz .LBB0_17
	v_cmp_lt_u32_e32 vcc, 63, v17
	v_mad_u64_u32 v[18:19], s[8:9], v16, s27, 0
	s_nop 0
	v_cndmask_b32_e32 v8, 0, v3, vcc
	v_add_u32_e32 v8, v8, v17
	v_cmp_lt_u32_e64 s[4:5], 31, v8
	s_nop 1
	v_cndmask_b32_e64 v17, 0, v12, s[4:5]
	v_add_u32_e32 v8, v17, v8
	v_cmp_lt_u32_e64 s[6:7], 31, v8
	s_nop 1
	v_cndmask_b32_e64 v17, 0, v12, s[6:7]
	v_add_u32_e32 v30, v17, v8
	v_mov_b32_e32 v8, v19
	v_mad_u64_u32 v[20:21], s[8:9], v16, s28, v[8:9]
	v_mov_b32_e32 v8, v21
	v_mad_u64_u32 v[22:23], s[8:9], v16, s29, v[8:9]
	v_mov_b32_e32 v8, v23
	v_mad_u64_u32 v[24:25], s[8:9], v16, s30, v[8:9]
	v_mov_b32_e32 v8, v25
	v_mad_u64_u32 v[26:27], s[8:9], v16, s31, v[8:9]
	v_mov_b32_e32 v8, v27
	v_mad_u64_u32 v[28:29], s[8:9], v16, s34, v[8:9]
	v_mov_b32_e32 v8, v29
	v_mad_u64_u32 v[16:17], s[8:9], v16, s35, v[8:9]
	v_cndmask_b32_e32 v19, v28, v24, vcc
	v_cndmask_b32_e32 v8, v16, v26, vcc
	v_cndmask_b32_e32 v17, v17, v28, vcc
	v_cndmask_b32_e64 v16, v8, v19, s[4:5]
	v_cndmask_b32_e64 v8, v17, v8, s[4:5]
	v_cndmask_b32_e32 v17, v26, v22, vcc
	v_cndmask_b32_e64 v19, v19, v17, s[4:5]
	v_cndmask_b32_e32 v20, v24, v20, vcc
	v_cndmask_b32_e64 v8, v8, v16, s[6:7]
	v_cndmask_b32_e64 v16, v16, v19, s[6:7]
	v_sub_u32_e32 v21, 32, v30
	v_cndmask_b32_e64 v17, v17, v20, s[4:5]
	v_alignbit_b32 v23, v8, v16, v21
	v_cmp_eq_u32_e64 s[8:9], 0, v30
	v_cndmask_b32_e64 v19, v19, v17, s[6:7]
	v_cndmask_b32_e32 v18, v22, v18, vcc
	v_cndmask_b32_e64 v8, v23, v8, s[8:9]
	v_alignbit_b32 v23, v16, v19, v21
	v_cndmask_b32_e64 v16, v23, v16, s[8:9]
	v_bfe_u32 v25, v8, 29, 1
	v_cndmask_b32_e64 v18, v20, v18, s[4:5]
	v_alignbit_b32 v23, v8, v16, 30
	v_sub_u32_e32 v26, 0, v25
	v_cndmask_b32_e64 v17, v17, v18, s[6:7]
	v_xor_b32_e32 v23, v23, v26
	v_alignbit_b32 v18, v19, v17, v21
	v_cndmask_b32_e64 v18, v18, v19, s[8:9]
	v_ffbh_u32_e32 v19, v23
	v_alignbit_b32 v16, v16, v18, 30
	v_min_u32_e32 v19, 32, v19
	v_alignbit_b32 v17, v18, v17, 30
	v_xor_b32_e32 v16, v16, v26
	v_sub_u32_e32 v20, 31, v19
	v_xor_b32_e32 v17, v17, v26
	v_alignbit_b32 v21, v23, v16, v20
	v_alignbit_b32 v16, v16, v17, v20
	v_alignbit_b32 v17, v21, v16, 9
	v_ffbh_u32_e32 v18, v17
	v_min_u32_e32 v18, 32, v18
	v_lshrrev_b32_e32 v24, 29, v8
	v_not_b32_e32 v20, v18
	v_alignbit_b32 v16, v17, v16, v20
	v_lshlrev_b32_e32 v17, 31, v24
	v_or_b32_e32 v20, 0x33000000, v17
	v_add_lshl_u32 v18, v18, v19, 23
	v_lshrrev_b32_e32 v16, 9, v16
	v_sub_u32_e32 v18, v20, v18
	v_or_b32_e32 v17, 0.5, v17
	v_lshlrev_b32_e32 v19, 23, v19
	v_or_b32_e32 v16, v18, v16
	v_lshrrev_b32_e32 v18, 9, v21
	v_sub_u32_e32 v17, v17, v19
	v_or_b32_e32 v17, v18, v17
	v_mul_f32_e32 v18, 0x3fc90fda, v17
	v_fma_f32 v19, v17, s36, -v18
	v_fmac_f32_e32 v19, 0x33a22168, v17
	v_fmac_f32_e32 v19, 0x3fc90fda, v16
	v_lshrrev_b32_e32 v8, 30, v8
	v_add_f32_e32 v19, v18, v19
	v_add_u32_e32 v18, v25, v8

.LBB0_22:
	s_or_b64 exec, exec, s[14:15]
	v_ashrrev_i32_e32 v11, 7, v2
	v_add_u32_e32 v12, 0xfffffe00, v2
	v_cndmask_b32_e64 v11, v12, v11, s[0:1]
	v_lshl_add_u32 v10, v10, 2, v11
	v_ashrrev_i32_e32 v11, 31, v10
	s_waitcnt lgkmcnt(0)
	v_lshl_add_u64 v[10:11], v[10:11], 2, v[4:5]
	global_load_dword v10, v[10:11], off
	v_cmp_lt_i32_e32 vcc, 3, v2
	s_or_b64 s[6:7], vcc, s[6:7]
	v_add_u32_e32 v2, 0x200, v2
	s_waitcnt vmcnt(0) lgkmcnt(0)
	global_store_dword v[6:7], v10, off
	v_lshl_add_u64 v[6:7], v[6:7], 0, s[8:9]
	s_andn2_b64 exec, exec, s[6:7]
	s_cbranch_execz .LBB0_25

.LBB0_28:
	v_ashrrev_i32_e32 v5, 31, v4
	v_lshlrev_b64 v[4:5], 12, v[4:5]
	v_cndmask_b32_e64 v16, 0, 1.0, s[0:1]
	v_lshl_add_u64 v[4:5], s[22:23], 0, v[4:5]
	v_lshl_add_u64 v[22:23], s[26:27], 1, v[4:5]
	s_waitcnt vmcnt(0)
	v_pk_mul_f32 v[4:5], v[16:17], v[70:71] op_sel_hi:[0,1]
	v_cvt_pk_bf16_f32 v70, v4, v5
	v_pk_mul_f32 v[4:5], v[16:17], v[68:69] op_sel_hi:[0,1]
	v_cvt_pk_bf16_f32 v71, v4, v5
	v_pk_mul_f32 v[4:5], v[16:17], v[66:67] op_sel_hi:[0,1]
	v_cvt_pk_bf16_f32 v72, v4, v5
	v_pk_mul_f32 v[4:5], v[16:17], v[64:65] op_sel_hi:[0,1]
	v_cvt_pk_bf16_f32 v73, v4, v5
	v_pk_mul_f32 v[4:5], v[16:17], v[10:11] op_sel_hi:[0,1]
	v_pk_mul_f32 v[8:9], v[16:17], v[8:9] op_sel_hi:[0,1]
	v_pk_mul_f32 v[6:7], v[16:17], v[6:7] op_sel_hi:[0,1]
	v_pk_mul_f32 v[2:3], v[16:17], v[2:3] op_sel_hi:[0,1]
	v_cvt_pk_bf16_f32 v4, v4, v5
	v_cvt_pk_bf16_f32 v5, v8, v9
	v_cvt_pk_bf16_f32 v6, v6, v7
	v_cvt_pk_bf16_f32 v7, v2, v3
	global_store_dwordx4 v[22:23], v[4:7], off offset:16
	v_pk_mul_f32 v[2:3], v[16:17], v[20:21] op_sel_hi:[0,1]
	v_cvt_pk_bf16_f32 v2, v2, v3
	v_pk_mul_f32 v[4:5], v[16:17], v[18:19] op_sel_hi:[0,1]
	v_cvt_pk_bf16_f32 v3, v4, v5
	v_pk_mul_f32 v[4:5], v[16:17], v[14:15] op_sel_hi:[0,1]
	v_pk_mul_f32 v[6:7], v[16:17], v[12:13] op_sel_hi:[0,1]
	v_cvt_pk_bf16_f32 v4, v4, v5
	v_cvt_pk_bf16_f32 v5, v6, v7
	global_store_dwordx4 v[22:23], v[2:5], off offset:32
	v_pk_mul_f32 v[6:7], v[16:17], v[24:25] op_sel_hi:[0,1]
	global_store_dwordx4 v[22:23], v[70:73], off
	v_pk_mul_f32 v[2:3], v[16:17], v[30:31] op_sel_hi:[0,1]
	v_pk_mul_f32 v[4:5], v[16:17], v[28:29] op_sel_hi:[0,1]
	v_cvt_pk_bf16_f32 v2, v2, v3
	v_cvt_pk_bf16_f32 v3, v4, v5
	v_pk_mul_f32 v[4:5], v[16:17], v[26:27] op_sel_hi:[0,1]
	v_cvt_pk_bf16_f32 v4, v4, v5
	v_cvt_pk_bf16_f32 v5, v6, v7
	global_store_dwordx4 v[22:23], v[2:5], off offset:48
	v_pk_mul_f32 v[6:7], v[16:17], v[32:33] op_sel_hi:[0,1]
	s_nop 0
	v_pk_mul_f32 v[2:3], v[16:17], v[38:39] op_sel_hi:[0,1]
	v_pk_mul_f32 v[4:5], v[16:17], v[36:37] op_sel_hi:[0,1]
	v_cvt_pk_bf16_f32 v2, v2, v3
	v_cvt_pk_bf16_f32 v3, v4, v5
	v_pk_mul_f32 v[4:5], v[16:17], v[34:35] op_sel_hi:[0,1]
	v_cvt_pk_bf16_f32 v4, v4, v5
	v_cvt_pk_bf16_f32 v5, v6, v7
	global_store_dwordx4 v[22:23], v[2:5], off offset:64
	v_pk_mul_f32 v[6:7], v[16:17], v[40:41] op_sel_hi:[0,1]
	s_nop 0
	v_pk_mul_f32 v[2:3], v[16:17], v[46:47] op_sel_hi:[0,1]
	v_pk_mul_f32 v[4:5], v[16:17], v[44:45] op_sel_hi:[0,1]
	v_cvt_pk_bf16_f32 v2, v2, v3
	v_cvt_pk_bf16_f32 v3, v4, v5
	v_pk_mul_f32 v[4:5], v[16:17], v[42:43] op_sel_hi:[0,1]
	v_cvt_pk_bf16_f32 v4, v4, v5
	v_cvt_pk_bf16_f32 v5, v6, v7
	global_store_dwordx4 v[22:23], v[2:5], off offset:80
	v_pk_mul_f32 v[6:7], v[16:17], v[48:49] op_sel_hi:[0,1]
	s_nop 0
	v_pk_mul_f32 v[2:3], v[16:17], v[54:55] op_sel_hi:[0,1]
	v_pk_mul_f32 v[4:5], v[16:17], v[52:53] op_sel_hi:[0,1]
	v_cvt_pk_bf16_f32 v2, v2, v3
	v_cvt_pk_bf16_f32 v3, v4, v5
	v_pk_mul_f32 v[4:5], v[16:17], v[50:51] op_sel_hi:[0,1]
	v_cvt_pk_bf16_f32 v4, v4, v5
	v_cvt_pk_bf16_f32 v5, v6, v7
	global_store_dwordx4 v[22:23], v[2:5], off offset:96
	v_pk_mul_f32 v[6:7], v[16:17], v[56:57] op_sel_hi:[0,1]
	s_nop 0
	v_pk_mul_f32 v[2:3], v[16:17], v[62:63] op_sel_hi:[0,1]
	v_pk_mul_f32 v[4:5], v[16:17], v[60:61] op_sel_hi:[0,1]
	v_cvt_pk_bf16_f32 v2, v2, v3
	v_cvt_pk_bf16_f32 v3, v4, v5
	v_pk_mul_f32 v[4:5], v[16:17], v[58:59] op_sel_hi:[0,1]
	v_cvt_pk_bf16_f32 v4, v4, v5
	v_cvt_pk_bf16_f32 v5, v6, v7
	global_store_dwordx4 v[22:23], v[2:5], off offset:112

.LBB0_35:
	s_add_i32 s5, s28, 0xfff8bc00
	s_and_b32 s5, s5, 0x7c0
	v_or_b32_e32 v16, s5, v1
	s_lshl_b64 s[26:27], s[24:25], 13
	s_waitcnt lgkmcnt(0)
	v_lshl_add_u64 v[2:3], v[2:3], 0, s[26:27]
	v_lshlrev_b32_e32 v4, 2, v16
	v_mov_b32_e32 v5, v17
	v_lshl_add_u64 v[2:3], v[2:3], 0, v[4:5]
	v_add_co_u32_e32 v4, vcc, 0x2000, v2
	s_nop 1
	v_addc_co_u32_e32 v5, vcc, 0, v3, vcc
	v_add_co_u32_e32 v6, vcc, 0x4000, v2
	s_nop 1
	v_addc_co_u32_e32 v7, vcc, 0, v3, vcc
	v_add_co_u32_e32 v8, vcc, 0x6000, v2
	s_nop 1
	v_addc_co_u32_e32 v9, vcc, 0, v3, vcc
	v_add_co_u32_e32 v10, vcc, 0x8000, v2
	s_nop 1
	v_addc_co_u32_e32 v11, vcc, 0, v3, vcc
	v_add_co_u32_e32 v12, vcc, 0xa000, v2
	s_nop 1
	v_addc_co_u32_e32 v13, vcc, 0, v3, vcc
	v_add_co_u32_e32 v14, vcc, 0xc000, v2
	s_nop 1
	v_addc_co_u32_e32 v15, vcc, 0, v3, vcc
	v_add_co_u32_e32 v18, vcc, 0xe000, v2
	s_nop 1
	v_addc_co_u32_e32 v19, vcc, 0, v3, vcc
	global_load_dword v22, v[2:3], off
	global_load_dword v23, v[4:5], off
	global_load_dword v24, v[6:7], off
	global_load_dword v25, v[8:9], off
	global_load_dword v26, v[10:11], off
	global_load_dword v27, v[12:13], off
	global_load_dword v28, v[14:15], off
	global_load_dword v29, v[18:19], off
	v_add_co_u32_e32 v4, vcc, 0x10000, v2
	s_nop 1
	v_addc_co_u32_e32 v5, vcc, 0, v3, vcc
	v_add_co_u32_e32 v6, vcc, 0x12000, v2
	s_nop 1
	v_addc_co_u32_e32 v7, vcc, 0, v3, vcc
	v_add_co_u32_e32 v8, vcc, 0x14000, v2
	s_nop 1
	v_addc_co_u32_e32 v9, vcc, 0, v3, vcc
	v_add_co_u32_e32 v10, vcc, 0x16000, v2
	s_nop 1
	v_addc_co_u32_e32 v11, vcc, 0, v3, vcc
	v_add_co_u32_e32 v12, vcc, 0x18000, v2
	s_nop 1
	v_addc_co_u32_e32 v13, vcc, 0, v3, vcc
	v_add_co_u32_e32 v14, vcc, 0x1a000, v2
	s_nop 1
	v_addc_co_u32_e32 v15, vcc, 0, v3, vcc
	v_add_co_u32_e32 v18, vcc, 0x1c000, v2
	s_nop 1
	v_addc_co_u32_e32 v19, vcc, 0, v3, vcc
	v_add_co_u32_e32 v20, vcc, 0x1e000, v2
	s_nop 1
	v_addc_co_u32_e32 v21, vcc, 0, v3, vcc
	global_load_dword v30, v[4:5], off
	global_load_dword v31, v[6:7], off
	global_load_dword v32, v[8:9], off
	global_load_dword v33, v[10:11], off
	global_load_dword v34, v[12:13], off
	global_load_dword v35, v[14:15], off
	global_load_dword v36, v[18:19], off
	global_load_dword v37, v[20:21], off
	v_add_co_u32_e32 v4, vcc, 0x20000, v2
	s_nop 1
	v_addc_co_u32_e32 v5, vcc, 0, v3, vcc
	v_add_co_u32_e32 v6, vcc, 0x22000, v2
	s_nop 1
	v_addc_co_u32_e32 v7, vcc, 0, v3, vcc
	v_add_co_u32_e32 v8, vcc, 0x24000, v2
	s_nop 1
	v_addc_co_u32_e32 v9, vcc, 0, v3, vcc
	v_add_co_u32_e32 v10, vcc, 0x26000, v2
	s_nop 1
	v_addc_co_u32_e32 v11, vcc, 0, v3, vcc
	v_add_co_u32_e32 v12, vcc, 0x28000, v2
	s_nop 1
	v_addc_co_u32_e32 v13, vcc, 0, v3, vcc
	v_add_co_u32_e32 v14, vcc, 0x2a000, v2
	s_nop 1
	v_addc_co_u32_e32 v15, vcc, 0, v3, vcc
	v_add_co_u32_e32 v18, vcc, 0x2c000, v2
	s_nop 1
	v_addc_co_u32_e32 v19, vcc, 0, v3, vcc
	v_add_co_u32_e32 v20, vcc, 0x2e000, v2
	s_nop 1
	v_addc_co_u32_e32 v21, vcc, 0, v3, vcc
	global_load_dword v38, v[4:5], off
	global_load_dword v39, v[6:7], off
	global_load_dword v40, v[8:9], off
	global_load_dword v41, v[10:11], off
	global_load_dword v42, v[12:13], off
	global_load_dword v43, v[14:15], off
	global_load_dword v44, v[18:19], off
	global_load_dword v45, v[20:21], off
	v_add_co_u32_e32 v4, vcc, 0x30000, v2
	s_nop 1
	v_addc_co_u32_e32 v5, vcc, 0, v3, vcc
	v_add_co_u32_e32 v6, vcc, 0x32000, v2
	s_nop 1
	v_addc_co_u32_e32 v7, vcc, 0, v3, vcc
	v_add_co_u32_e32 v8, vcc, 0x34000, v2
	s_nop 1
	v_addc_co_u32_e32 v9, vcc, 0, v3, vcc
	v_add_co_u32_e32 v10, vcc, 0x36000, v2
	s_nop 1
	v_addc_co_u32_e32 v11, vcc, 0, v3, vcc
	v_add_co_u32_e32 v12, vcc, 0x38000, v2
	s_nop 1
	v_addc_co_u32_e32 v13, vcc, 0, v3, vcc
	v_add_co_u32_e32 v14, vcc, 0x3a000, v2
	s_nop 1
	v_addc_co_u32_e32 v15, vcc, 0, v3, vcc
	v_add_co_u32_e32 v18, vcc, 0x3c000, v2
	s_nop 1
	v_addc_co_u32_e32 v19, vcc, 0, v3, vcc
	v_add_co_u32_e32 v20, vcc, 0x3e000, v2
	s_nop 1
	v_addc_co_u32_e32 v21, vcc, 0, v3, vcc
	global_load_dword v46, v[4:5], off
	global_load_dword v47, v[6:7], off
	global_load_dword v48, v[8:9], off
	global_load_dword v49, v[10:11], off
	global_load_dword v50, v[12:13], off
	global_load_dword v51, v[14:15], off
	global_load_dword v52, v[18:19], off
	global_load_dword v53, v[20:21], off
	v_add_co_u32_e32 v4, vcc, 0x40000, v2
	s_nop 1
	v_addc_co_u32_e32 v5, vcc, 0, v3, vcc
	v_add_co_u32_e32 v6, vcc, 0x42000, v2
	s_nop 1
	v_addc_co_u32_e32 v7, vcc, 0, v3, vcc
	v_add_co_u32_e32 v8, vcc, 0x44000, v2
	s_nop 1
	v_addc_co_u32_e32 v9, vcc, 0, v3, vcc
	v_add_co_u32_e32 v10, vcc, 0x46000, v2
	s_nop 1
	v_addc_co_u32_e32 v11, vcc, 0, v3, vcc
	v_add_co_u32_e32 v12, vcc, 0x48000, v2
	s_nop 1
	v_addc_co_u32_e32 v13, vcc, 0, v3, vcc
	v_add_co_u32_e32 v14, vcc, 0x4a000, v2
	s_nop 1
	v_addc_co_u32_e32 v15, vcc, 0, v3, vcc
	v_add_co_u32_e32 v18, vcc, 0x4c000, v2
	s_nop 1
	v_addc_co_u32_e32 v19, vcc, 0, v3, vcc
	v_add_co_u32_e32 v20, vcc, 0x4e000, v2
	s_nop 1
	v_addc_co_u32_e32 v21, vcc, 0, v3, vcc
	global_load_dword v54, v[4:5], off
	global_load_dword v55, v[6:7], off
	global_load_dword v56, v[8:9], off
	global_load_dword v57, v[10:11], off
	global_load_dword v58, v[12:13], off
	global_load_dword v59, v[14:15], off
	global_load_dword v60, v[18:19], off
	global_load_dword v61, v[20:21], off
	v_add_co_u32_e32 v4, vcc, 0x50000, v2
	s_nop 1
	v_addc_co_u32_e32 v5, vcc, 0, v3, vcc
	v_add_co_u32_e32 v6, vcc, 0x52000, v2
	s_nop 1
	v_addc_co_u32_e32 v7, vcc, 0, v3, vcc
	v_add_co_u32_e32 v8, vcc, 0x54000, v2
	s_nop 1
	v_addc_co_u32_e32 v9, vcc, 0, v3, vcc
	v_add_co_u32_e32 v10, vcc, 0x56000, v2
	s_nop 1
	v_addc_co_u32_e32 v11, vcc, 0, v3, vcc
	v_add_co_u32_e32 v12, vcc, 0x58000, v2
	s_nop 1
	v_addc_co_u32_e32 v13, vcc, 0, v3, vcc
	v_add_co_u32_e32 v14, vcc, 0x5a000, v2
	s_nop 1
	v_addc_co_u32_e32 v15, vcc, 0, v3, vcc
	v_add_co_u32_e32 v18, vcc, 0x5c000, v2
	s_nop 1
	v_addc_co_u32_e32 v19, vcc, 0, v3, vcc
	v_add_co_u32_e32 v20, vcc, 0x5e000, v2
	s_nop 1
	v_addc_co_u32_e32 v21, vcc, 0, v3, vcc
	global_load_dword v62, v[4:5], off
	global_load_dword v63, v[6:7], off
	global_load_dword v64, v[8:9], off
	global_load_dword v65, v[10:11], off
	global_load_dword v66, v[12:13], off
	global_load_dword v67, v[14:15], off
	global_load_dword v68, v[18:19], off
	global_load_dword v69, v[20:21], off
	v_add_co_u32_e32 v4, vcc, 0x60000, v2
	s_nop 1
	v_addc_co_u32_e32 v5, vcc, 0, v3, vcc
	v_add_co_u32_e32 v6, vcc, 0x62000, v2
	s_nop 1
	v_addc_co_u32_e32 v7, vcc, 0, v3, vcc
	v_add_co_u32_e32 v8, vcc, 0x64000, v2
	s_nop 1
	v_addc_co_u32_e32 v9, vcc, 0, v3, vcc
	v_add_co_u32_e32 v10, vcc, 0x66000, v2
	s_nop 1
	v_addc_co_u32_e32 v11, vcc, 0, v3, vcc
	v_add_co_u32_e32 v12, vcc, 0x68000, v2
	s_nop 1
	v_addc_co_u32_e32 v13, vcc, 0, v3, vcc
	v_add_co_u32_e32 v14, vcc, 0x6a000, v2
	s_nop 1
	v_addc_co_u32_e32 v15, vcc, 0, v3, vcc
	v_add_co_u32_e32 v18, vcc, 0x6c000, v2
	s_nop 1
	v_addc_co_u32_e32 v19, vcc, 0, v3, vcc
	v_add_co_u32_e32 v20, vcc, 0x6e000, v2
	s_nop 1
	v_addc_co_u32_e32 v21, vcc, 0, v3, vcc
	global_load_dword v70, v[4:5], off
	global_load_dword v71, v[6:7], off
	global_load_dword v72, v[8:9], off
	global_load_dword v73, v[10:11], off
	global_load_dword v74, v[12:13], off
	global_load_dword v75, v[14:15], off
	global_load_dword v77, v[18:19], off
	s_nop 0
	global_load_dword v20, v[20:21], off
	v_add_co_u32_e32 v4, vcc, 0x70000, v2
	s_nop 1
	v_addc_co_u32_e32 v5, vcc, 0, v3, vcc
	v_add_co_u32_e32 v6, vcc, 0x72000, v2
	s_nop 1
	v_addc_co_u32_e32 v7, vcc, 0, v3, vcc
	v_add_co_u32_e32 v8, vcc, 0x74000, v2
	s_nop 1
	v_addc_co_u32_e32 v9, vcc, 0, v3, vcc
	v_add_co_u32_e32 v10, vcc, 0x76000, v2
	s_nop 1
	v_addc_co_u32_e32 v11, vcc, 0, v3, vcc
	v_add_co_u32_e32 v12, vcc, 0x78000, v2
	s_nop 1
	v_addc_co_u32_e32 v13, vcc, 0, v3, vcc
	v_add_co_u32_e32 v14, vcc, 0x7a000, v2
	s_nop 1
	v_addc_co_u32_e32 v15, vcc, 0, v3, vcc
	v_add_co_u32_e32 v18, vcc, 0x7c000, v2
	s_nop 1
	v_addc_co_u32_e32 v19, vcc, 0, v3, vcc
	v_add_co_u32_e32 v2, vcc, 0x7e000, v2
	s_nop 1
	v_addc_co_u32_e32 v3, vcc, 0, v3, vcc
	global_load_dword v21, v[4:5], off
	global_load_dword v78, v[6:7], off
	s_nop 0
	global_load_dword v8, v[8:9], off
	s_nop 0
	global_load_dword v9, v[10:11], off
	s_nop 0
	global_load_dword v10, v[12:13], off
	global_load_dword v11, v[14:15], off
	s_nop 0
	global_load_dword v12, v[18:19], off
	global_load_dword v13, v[2:3], off
	v_lshlrev_b64 v[2:3], s4, v[16:17]
	v_lshl_add_u64 v[2:3], s[0:1], 0, v[2:3]
	v_lshl_add_u64 v[6:7], s[24:25], 1, v[2:3]
	s_waitcnt vmcnt(0) lgkmcnt(0)
	v_cvt_pk_bf16_f32 v2, v22, v23
	v_cvt_pk_bf16_f32 v3, v24, v25
	v_cvt_pk_bf16_f32 v4, v26, v27
	v_cvt_pk_bf16_f32 v5, v28, v29
	global_store_dwordx4 v[6:7], v[2:5], off
	s_mov_b64 s[0:1], 0
	s_nop 0
	v_cvt_pk_bf16_f32 v2, v30, v31
	v_cvt_pk_bf16_f32 v3, v32, v33
	v_cvt_pk_bf16_f32 v4, v34, v35
	v_cvt_pk_bf16_f32 v5, v36, v37
	global_store_dwordx4 v[6:7], v[2:5], off offset:16
	s_nop 1
	v_cvt_pk_bf16_f32 v2, v38, v39
	v_cvt_pk_bf16_f32 v3, v40, v41
	v_cvt_pk_bf16_f32 v4, v42, v43
	v_cvt_pk_bf16_f32 v5, v44, v45
	global_store_dwordx4 v[6:7], v[2:5], off offset:32
	s_nop 1
	v_cvt_pk_bf16_f32 v2, v46, v47
	v_cvt_pk_bf16_f32 v3, v48, v49
	v_cvt_pk_bf16_f32 v4, v50, v51
	v_cvt_pk_bf16_f32 v5, v52, v53
	global_store_dwordx4 v[6:7], v[2:5], off offset:48
	s_nop 1
	v_cvt_pk_bf16_f32 v2, v54, v55
	v_cvt_pk_bf16_f32 v3, v56, v57
	v_cvt_pk_bf16_f32 v4, v58, v59
	v_cvt_pk_bf16_f32 v5, v60, v61
	global_store_dwordx4 v[6:7], v[2:5], off offset:64
	s_nop 1
	v_cvt_pk_bf16_f32 v2, v62, v63
	v_cvt_pk_bf16_f32 v3, v64, v65
	v_cvt_pk_bf16_f32 v4, v66, v67
	v_cvt_pk_bf16_f32 v5, v68, v69
	global_store_dwordx4 v[6:7], v[2:5], off offset:80
	s_nop 1
	v_cvt_pk_bf16_f32 v2, v70, v71
	v_cvt_pk_bf16_f32 v3, v72, v73
	v_cvt_pk_bf16_f32 v4, v74, v75
	v_cvt_pk_bf16_f32 v5, v77, v20
	global_store_dwordx4 v[6:7], v[2:5], off offset:96
	s_nop 1
	v_cvt_pk_bf16_f32 v2, v21, v78
	v_cvt_pk_bf16_f32 v3, v8, v9
	v_cvt_pk_bf16_f32 v4, v10, v11
	v_cvt_pk_bf16_f32 v5, v12, v13
	global_store_dwordx4 v[6:7], v[2:5], off offset:112
.LBB0_36:
	s_and_b64 vcc, exec, s[0:1]
	s_cbranch_vccz .LBB0_29
	s_waitcnt lgkmcnt(0)
	v_mov_b32_e32 v2, s71
	ds_read_b128 v[2:5], v2
	s_cmpk_gt_i32 s79, 0xc7f
	s_mov_b64 s[0:1], -1
	s_cbranch_scc0 .LBB0_50
	s_cmpk_gt_u32 s79, 0x1c7f
	s_cbranch_scc0 .LBB0_47
	v_mov_b32_e32 v6, s72
	ds_read_b128 v[6:9], v6
	s_mov_b64 s[4:5], -1
	s_cmpk_gt_u32 s79, 0x1caf
	s_waitcnt lgkmcnt(0)
	v_cmp_eq_u64_e64 s[0:1], 0, v[4:5]
	s_cbranch_scc0 .LBB0_43
	s_and_b32 s4, s30, 0x3c0
	s_and_b32 s5, s28, 0x3c0
	v_or_b32_e32 v74, s5, v1
	s_lshl_b32 s24, s4, 12
	v_lshl_add_u64 v[8:9], v[8:9], 0, s[24:25]
	v_lshlrev_b32_e32 v16, 2, v74
	v_lshl_add_u64 v[66:67], v[8:9], 0, v[16:17]
	v_add_co_u32_e32 v10, vcc, 0x1000, v66
	s_nop 1
	v_addc_co_u32_e32 v11, vcc, 0, v67, vcc
	v_add_co_u32_e32 v12, vcc, s40, v66
	s_nop 1
	v_addc_co_u32_e32 v13, vcc, 0, v67, vcc
	v_add_co_u32_e32 v14, vcc, 0x3000, v66
	s_nop 1
	v_addc_co_u32_e32 v15, vcc, 0, v67, vcc
	v_add_co_u32_e32 v18, vcc, s41, v66
	s_nop 1
	v_addc_co_u32_e32 v19, vcc, 0, v67, vcc
	v_add_co_u32_e32 v20, vcc, 0x5000, v66
	s_nop 1
	v_addc_co_u32_e32 v21, vcc, 0, v67, vcc
	v_add_co_u32_e32 v22, vcc, s42, v66
	s_nop 1
	v_addc_co_u32_e32 v23, vcc, 0, v67, vcc
	v_add_co_u32_e32 v24, vcc, 0x7000, v66
	s_nop 1
	v_addc_co_u32_e32 v25, vcc, 0, v67, vcc
	global_load_dword v8, v[66:67], off
	global_load_dword v9, v[10:11], off
	s_nop 0
	global_load_dword v10, v[12:13], off
	global_load_dword v11, v[14:15], off
	s_nop 0
	global_load_dword v12, v[18:19], off
	global_load_dword v13, v[20:21], off
	global_load_dword v14, v[22:23], off
	global_load_dword v15, v[24:25], off
	v_add_co_u32_e32 v18, vcc, s43, v66
	s_nop 1
	v_addc_co_u32_e32 v19, vcc, 0, v67, vcc
	v_add_co_u32_e32 v20, vcc, 0x9000, v66
	s_nop 1
	v_addc_co_u32_e32 v21, vcc, 0, v67, vcc
	v_add_co_u32_e32 v22, vcc, s44, v66
	s_nop 1
	v_addc_co_u32_e32 v23, vcc, 0, v67, vcc
	v_add_co_u32_e32 v24, vcc, 0xb000, v66
	s_nop 1
	v_addc_co_u32_e32 v25, vcc, 0, v67, vcc
	v_add_co_u32_e32 v26, vcc, s45, v66
	s_nop 1
	v_addc_co_u32_e32 v27, vcc, 0, v67, vcc
	v_add_co_u32_e32 v28, vcc, 0xd000, v66
	s_nop 1
	v_addc_co_u32_e32 v29, vcc, 0, v67, vcc
	v_add_co_u32_e32 v30, vcc, s46, v66
	s_nop 1
	v_addc_co_u32_e32 v31, vcc, 0, v67, vcc
	v_add_co_u32_e32 v32, vcc, 0xf000, v66
	s_nop 1
	v_addc_co_u32_e32 v33, vcc, 0, v67, vcc
	global_load_dword v18, v[18:19], off
	s_nop 0
	global_load_dword v19, v[20:21], off
	s_nop 0
	global_load_dword v20, v[22:23], off
	global_load_dword v21, v[24:25], off
	s_nop 0
	global_load_dword v22, v[26:27], off
	global_load_dword v23, v[28:29], off
	global_load_dword v24, v[30:31], off
	global_load_dword v25, v[32:33], off
	v_add_co_u32_e32 v26, vcc, s47, v66
	s_nop 1
	v_addc_co_u32_e32 v27, vcc, 0, v67, vcc
	v_add_co_u32_e32 v28, vcc, 0x11000, v66
	s_nop 1
	v_addc_co_u32_e32 v29, vcc, 0, v67, vcc
	v_add_co_u32_e32 v30, vcc, s48, v66
	s_nop 1
	v_addc_co_u32_e32 v31, vcc, 0, v67, vcc
	v_add_co_u32_e32 v32, vcc, 0x13000, v66
	s_nop 1
	v_addc_co_u32_e32 v33, vcc, 0, v67, vcc
	v_add_co_u32_e32 v34, vcc, s49, v66
	s_nop 1
	v_addc_co_u32_e32 v35, vcc, 0, v67, vcc
	v_add_co_u32_e32 v36, vcc, 0x15000, v66
	s_nop 1
	v_addc_co_u32_e32 v37, vcc, 0, v67, vcc
	v_add_co_u32_e32 v38, vcc, s50, v66
	s_nop 1
	v_addc_co_u32_e32 v39, vcc, 0, v67, vcc
	v_add_co_u32_e32 v40, vcc, 0x17000, v66
	s_nop 1
	v_addc_co_u32_e32 v41, vcc, 0, v67, vcc
	global_load_dword v26, v[26:27], off
	s_nop 0
	global_load_dword v27, v[28:29], off
	s_nop 0
	global_load_dword v28, v[30:31], off
	global_load_dword v29, v[32:33], off
	s_nop 0
	global_load_dword v30, v[34:35], off
	global_load_dword v31, v[36:37], off
	global_load_dword v32, v[38:39], off
	global_load_dword v33, v[40:41], off
	v_add_co_u32_e32 v34, vcc, s51, v66
	s_nop 1
	v_addc_co_u32_e32 v35, vcc, 0, v67, vcc
	v_add_co_u32_e32 v36, vcc, 0x19000, v66
	s_nop 1
	v_addc_co_u32_e32 v37, vcc, 0, v67, vcc
	v_add_co_u32_e32 v38, vcc, s52, v66
	s_nop 1
	v_addc_co_u32_e32 v39, vcc, 0, v67, vcc
	v_add_co_u32_e32 v40, vcc, 0x1b000, v66
	s_nop 1
	v_addc_co_u32_e32 v41, vcc, 0, v67, vcc
	v_add_co_u32_e32 v42, vcc, s53, v66
	s_nop 1
	v_addc_co_u32_e32 v43, vcc, 0, v67, vcc
	v_add_co_u32_e32 v44, vcc, 0x1d000, v66
	s_nop 1
	v_addc_co_u32_e32 v45, vcc, 0, v67, vcc
	v_add_co_u32_e32 v46, vcc, s54, v66
	s_nop 1
	v_addc_co_u32_e32 v47, vcc, 0, v67, vcc
	v_add_co_u32_e32 v48, vcc, 0x1f000, v66
	s_nop 1
	v_addc_co_u32_e32 v49, vcc, 0, v67, vcc
	global_load_dword v34, v[34:35], off
	s_nop 0
	global_load_dword v35, v[36:37], off
	s_nop 0
	global_load_dword v36, v[38:39], off
	global_load_dword v37, v[40:41], off
	s_nop 0
	global_load_dword v38, v[42:43], off
	global_load_dword v39, v[44:45], off
	global_load_dword v40, v[46:47], off
	global_load_dword v41, v[48:49], off
	v_add_co_u32_e32 v42, vcc, s55, v66
	s_nop 1
	v_addc_co_u32_e32 v43, vcc, 0, v67, vcc
	v_add_co_u32_e32 v44, vcc, 0x21000, v66
	s_nop 1
	v_addc_co_u32_e32 v45, vcc, 0, v67, vcc
	v_add_co_u32_e32 v46, vcc, s56, v66
	s_nop 1
	v_addc_co_u32_e32 v47, vcc, 0, v67, vcc
	v_add_co_u32_e32 v48, vcc, 0x23000, v66
	s_nop 1
	v_addc_co_u32_e32 v49, vcc, 0, v67, vcc
	v_add_co_u32_e32 v50, vcc, s57, v66
	s_nop 1
	v_addc_co_u32_e32 v51, vcc, 0, v67, vcc
	v_add_co_u32_e32 v52, vcc, 0x25000, v66
	s_nop 1
	v_addc_co_u32_e32 v53, vcc, 0, v67, vcc
	v_add_co_u32_e32 v54, vcc, s58, v66
	s_nop 1
	v_addc_co_u32_e32 v55, vcc, 0, v67, vcc
	v_add_co_u32_e32 v56, vcc, 0x27000, v66
	s_nop 1
	v_addc_co_u32_e32 v57, vcc, 0, v67, vcc
	global_load_dword v42, v[42:43], off
	s_nop 0
	global_load_dword v43, v[44:45], off
	s_nop 0
	global_load_dword v44, v[46:47], off
	global_load_dword v45, v[48:49], off
	s_nop 0
	global_load_dword v46, v[50:51], off
	global_load_dword v47, v[52:53], off
	global_load_dword v48, v[54:55], off
	global_load_dword v49, v[56:57], off
	v_add_co_u32_e32 v50, vcc, s59, v66
	s_nop 1
	v_addc_co_u32_e32 v51, vcc, 0, v67, vcc
	v_add_co_u32_e32 v52, vcc, 0x29000, v66
	s_nop 1
	v_addc_co_u32_e32 v53, vcc, 0, v67, vcc
	v_add_co_u32_e32 v54, vcc, s60, v66
	s_nop 1
	v_addc_co_u32_e32 v55, vcc, 0, v67, vcc
	v_add_co_u32_e32 v56, vcc, 0x2b000, v66
	s_nop 1
	v_addc_co_u32_e32 v57, vcc, 0, v67, vcc
	v_add_co_u32_e32 v58, vcc, s61, v66
	s_nop 1
	v_addc_co_u32_e32 v59, vcc, 0, v67, vcc
	v_add_co_u32_e32 v60, vcc, 0x2d000, v66
	s_nop 1
	v_addc_co_u32_e32 v61, vcc, 0, v67, vcc
	v_add_co_u32_e32 v62, vcc, s62, v66
	s_nop 1
	v_addc_co_u32_e32 v63, vcc, 0, v67, vcc
	v_add_co_u32_e32 v64, vcc, 0x2f000, v66
	s_nop 1
	v_addc_co_u32_e32 v65, vcc, 0, v67, vcc
	global_load_dword v50, v[50:51], off
	s_nop 0
	global_load_dword v51, v[52:53], off
	s_nop 0
	global_load_dword v52, v[54:55], off
	global_load_dword v53, v[56:57], off
	s_nop 0
	global_load_dword v54, v[58:59], off
	global_load_dword v55, v[60:61], off
	global_load_dword v56, v[62:63], off
	global_load_dword v57, v[64:65], off
	v_add_co_u32_e32 v58, vcc, s63, v66
	s_nop 1
	v_addc_co_u32_e32 v59, vcc, 0, v67, vcc
	v_add_co_u32_e32 v60, vcc, 0x31000, v66
	s_nop 1
	v_addc_co_u32_e32 v61, vcc, 0, v67, vcc
	v_add_co_u32_e32 v62, vcc, s64, v66
	s_nop 1
	v_addc_co_u32_e32 v63, vcc, 0, v67, vcc
	v_add_co_u32_e32 v64, vcc, 0x33000, v66
	s_nop 1
	v_addc_co_u32_e32 v65, vcc, 0, v67, vcc
	v_add_co_u32_e32 v68, vcc, s65, v66
	s_nop 1
	v_addc_co_u32_e32 v69, vcc, 0, v67, vcc
	v_add_co_u32_e32 v70, vcc, 0x35000, v66
	s_nop 1
	v_addc_co_u32_e32 v71, vcc, 0, v67, vcc
	v_add_co_u32_e32 v72, vcc, s66, v66
	s_nop 1
	v_addc_co_u32_e32 v73, vcc, 0, v67, vcc
	v_add_co_u32_e32 v78, vcc, 0x37000, v66
	s_nop 1
	v_addc_co_u32_e32 v79, vcc, 0, v67, vcc
	global_load_dword v58, v[58:59], off
	s_nop 0
	global_load_dword v59, v[60:61], off
	s_nop 0
	global_load_dword v60, v[62:63], off
	global_load_dword v61, v[64:65], off
	s_nop 0
	global_load_dword v62, v[68:69], off
	global_load_dword v63, v[70:71], off
	global_load_dword v64, v[72:73], off
	global_load_dword v65, v[78:79], off
	v_add_co_u32_e32 v68, vcc, s67, v66
	s_nop 1
	v_addc_co_u32_e32 v69, vcc, 0, v67, vcc
	v_add_co_u32_e32 v70, vcc, 0x39000, v66
	s_nop 1
	v_addc_co_u32_e32 v71, vcc, 0, v67, vcc
	v_add_co_u32_e32 v72, vcc, s68, v66
	s_nop 1
	v_addc_co_u32_e32 v73, vcc, 0, v67, vcc
	v_add_co_u32_e32 v78, vcc, 0x3b000, v66
	s_nop 1
	v_addc_co_u32_e32 v79, vcc, 0, v67, vcc
	v_add_co_u32_e32 v80, vcc, s69, v66
	s_nop 1
	v_addc_co_u32_e32 v81, vcc, 0, v67, vcc
	v_add_co_u32_e32 v82, vcc, 0x3d000, v66
	s_nop 1
	v_addc_co_u32_e32 v83, vcc, 0, v67, vcc
	v_add_co_u32_e32 v84, vcc, s70, v66
	s_nop 1
	v_addc_co_u32_e32 v85, vcc, 0, v67, vcc
	v_add_co_u32_e32 v86, vcc, 0x3f000, v66
	s_nop 1
	v_addc_co_u32_e32 v87, vcc, 0, v67, vcc
	global_load_dword v66, v[68:69], off
	global_load_dword v67, v[70:71], off
	s_nop 0
	global_load_dword v68, v[72:73], off
	global_load_dword v69, v[78:79], off
	global_load_dword v70, v[80:81], off
	global_load_dword v71, v[82:83], off
	s_nop 0
	global_load_dword v72, v[84:85], off
	global_load_dword v73, v[86:87], off
	s_and_b64 vcc, exec, s[0:1]
	s_cbranch_vccnz .LBB0_42
	s_lshl_b32 s24, s4, 2
	v_lshl_add_u64 v[138:139], v[4:5], 0, s[24:25]
	global_load_dwordx4 v[78:81], v[138:139], off
	global_load_dwordx4 v[82:85], v[138:139], off offset:16
	global_load_dwordx4 v[86:89], v[138:139], off offset:32
	global_load_dwordx4 v[90:93], v[138:139], off offset:48
	global_load_dwordx4 v[94:97], v[138:139], off offset:64
	global_load_dwordx4 v[98:101], v[138:139], off offset:80
	global_load_dwordx4 v[102:105], v[138:139], off offset:96
	global_load_dwordx4 v[106:109], v[138:139], off offset:112
	global_load_dwordx4 v[110:113], v[138:139], off offset:128
	global_load_dwordx4 v[114:117], v[138:139], off offset:144
	global_load_dwordx4 v[118:121], v[138:139], off offset:160
	global_load_dwordx4 v[122:125], v[138:139], off offset:176
	global_load_dwordx4 v[126:129], v[138:139], off offset:192
	global_load_dwordx4 v[130:133], v[138:139], off offset:208
	global_load_dwordx4 v[134:137], v[138:139], off offset:224
	s_nop 0
	global_load_dwordx4 v[138:141], v[138:139], off offset:240
	s_waitcnt vmcnt(0) lgkmcnt(0)
	v_pk_mul_f32 v[8:9], v[8:9], v[78:79]
	v_pk_mul_f32 v[10:11], v[10:11], v[80:81]
	v_pk_mul_f32 v[12:13], v[12:13], v[82:83]
	v_pk_mul_f32 v[14:15], v[14:15], v[84:85]
	v_pk_mul_f32 v[18:19], v[18:19], v[86:87]
	v_pk_mul_f32 v[20:21], v[20:21], v[88:89]
	v_pk_mul_f32 v[22:23], v[22:23], v[90:91]
	v_pk_mul_f32 v[24:25], v[24:25], v[92:93]
	v_pk_mul_f32 v[26:27], v[26:27], v[94:95]
	v_pk_mul_f32 v[28:29], v[28:29], v[96:97]
	v_pk_mul_f32 v[30:31], v[30:31], v[98:99]
	v_pk_mul_f32 v[32:33], v[32:33], v[100:101]
	v_pk_mul_f32 v[34:35], v[34:35], v[102:103]
	v_pk_mul_f32 v[36:37], v[36:37], v[104:105]
	v_pk_mul_f32 v[38:39], v[38:39], v[106:107]
	v_pk_mul_f32 v[40:41], v[40:41], v[108:109]
	v_pk_mul_f32 v[42:43], v[42:43], v[110:111]
	v_pk_mul_f32 v[44:45], v[44:45], v[112:113]
	v_pk_mul_f32 v[46:47], v[46:47], v[114:115]
	v_pk_mul_f32 v[48:49], v[48:49], v[116:117]
	v_pk_mul_f32 v[50:51], v[50:51], v[118:119]
	v_pk_mul_f32 v[52:53], v[52:53], v[120:121]
	v_pk_mul_f32 v[54:55], v[54:55], v[122:123]
	v_pk_mul_f32 v[56:57], v[56:57], v[124:125]
	v_pk_mul_f32 v[58:59], v[58:59], v[126:127]
	v_pk_mul_f32 v[60:61], v[60:61], v[128:129]
	v_pk_mul_f32 v[62:63], v[62:63], v[130:131]
	v_pk_mul_f32 v[64:65], v[64:65], v[132:133]
	v_pk_mul_f32 v[66:67], v[66:67], v[134:135]
	v_pk_mul_f32 v[68:69], v[68:69], v[136:137]
	v_pk_mul_f32 v[70:71], v[70:71], v[138:139]
	v_pk_mul_f32 v[72:73], v[72:73], v[140:141]
.LBB0_42:
	v_mul_u32_u24_e32 v16, 0x300, v74
	v_lshl_add_u64 v[74:75], s[16:17], 0, v[16:17]
	s_lshl_b32 s24, s4, 1
	v_lshl_add_u64 v[74:75], v[74:75], 0, s[24:25]
	s_waitcnt vmcnt(0) lgkmcnt(0)
	v_cvt_pk_bf16_f32 v8, v8, v9
	v_cvt_pk_bf16_f32 v9, v10, v11
	v_cvt_pk_bf16_f32 v10, v12, v13
	v_cvt_pk_bf16_f32 v11, v14, v15
	global_store_dwordx4 v[74:75], v[8:11], off
	s_mov_b64 s[4:5], 0
	s_nop 0
	v_cvt_pk_bf16_f32 v8, v18, v19
	v_cvt_pk_bf16_f32 v9, v20, v21
	v_cvt_pk_bf16_f32 v10, v22, v23
	v_cvt_pk_bf16_f32 v11, v24, v25
	global_store_dwordx4 v[74:75], v[8:11], off offset:16
	s_nop 1
	v_cvt_pk_bf16_f32 v8, v26, v27
	v_cvt_pk_bf16_f32 v9, v28, v29
	v_cvt_pk_bf16_f32 v10, v30, v31
	v_cvt_pk_bf16_f32 v11, v32, v33
	global_store_dwordx4 v[74:75], v[8:11], off offset:32
	s_nop 1
	v_cvt_pk_bf16_f32 v8, v34, v35
	v_cvt_pk_bf16_f32 v9, v36, v37
	v_cvt_pk_bf16_f32 v10, v38, v39
	v_cvt_pk_bf16_f32 v11, v40, v41
	global_store_dwordx4 v[74:75], v[8:11], off offset:48
	s_nop 1
	v_cvt_pk_bf16_f32 v8, v42, v43
	v_cvt_pk_bf16_f32 v9, v44, v45
	v_cvt_pk_bf16_f32 v10, v46, v47
	v_cvt_pk_bf16_f32 v11, v48, v49
	global_store_dwordx4 v[74:75], v[8:11], off offset:64
	s_nop 1
	v_cvt_pk_bf16_f32 v8, v50, v51
	v_cvt_pk_bf16_f32 v9, v52, v53
	v_cvt_pk_bf16_f32 v10, v54, v55
	v_cvt_pk_bf16_f32 v11, v56, v57
	global_store_dwordx4 v[74:75], v[8:11], off offset:80
	s_nop 1
	v_cvt_pk_bf16_f32 v8, v58, v59
	v_cvt_pk_bf16_f32 v9, v60, v61
	v_cvt_pk_bf16_f32 v10, v62, v63
	v_cvt_pk_bf16_f32 v11, v64, v65
	global_store_dwordx4 v[74:75], v[8:11], off offset:96
	s_nop 1
	v_cvt_pk_bf16_f32 v8, v66, v67
	v_cvt_pk_bf16_f32 v9, v68, v69
	v_cvt_pk_bf16_f32 v10, v70, v71
	v_cvt_pk_bf16_f32 v11, v72, v73
	global_store_dwordx4 v[74:75], v[8:11], off offset:112
.LBB0_43:
	s_and_b64 vcc, exec, s[4:5]
	s_cbranch_vccz .LBB0_71
	s_and_b32 s4, s34, 0x7c0
	s_xor_b32 s4, s4, 0x400
	s_and_b32 s5, s28, 0x1c0
	v_or_b32_e32 v72, s5, v1
	s_lshl_b32 s24, s4, 11
	v_lshl_add_u64 v[6:7], v[6:7], 0, s[24:25]
	v_lshlrev_b32_e32 v16, 2, v72
	v_lshl_add_u64 v[64:65], v[6:7], 0, v[16:17]
	v_add_co_u32_e32 v10, vcc, 0x1000, v64
	s_nop 1
	v_addc_co_u32_e32 v11, vcc, 0, v65, vcc
	v_add_co_u32_e32 v12, vcc, s40, v64
	s_nop 1
	v_addc_co_u32_e32 v13, vcc, 0, v65, vcc
	v_add_co_u32_e32 v14, vcc, 0x3000, v64
	s_nop 1
	v_addc_co_u32_e32 v15, vcc, 0, v65, vcc
	v_add_co_u32_e32 v18, vcc, s41, v64
	global_load_dword v6, v[64:65], off
	global_load_dword v7, v[64:65], off offset:2048
	global_load_dword v8, v[10:11], off
	global_load_dword v9, v[10:11], off offset:2048
	s_nop 0
	global_load_dword v10, v[12:13], off
	global_load_dword v11, v[12:13], off offset:2048
	s_nop 0
	global_load_dword v12, v[14:15], off
	global_load_dword v13, v[14:15], off offset:2048
	v_addc_co_u32_e32 v19, vcc, 0, v65, vcc
	v_add_co_u32_e32 v20, vcc, 0x5000, v64
	s_nop 1
	v_addc_co_u32_e32 v21, vcc, 0, v65, vcc
	v_add_co_u32_e32 v22, vcc, s42, v64
	s_nop 1
	v_addc_co_u32_e32 v23, vcc, 0, v65, vcc
	v_add_co_u32_e32 v24, vcc, 0x7000, v64
	s_nop 1
	v_addc_co_u32_e32 v25, vcc, 0, v65, vcc
	v_add_co_u32_e32 v26, vcc, s43, v64
	global_load_dword v14, v[18:19], off
	global_load_dword v15, v[18:19], off offset:2048
	s_nop 0
	global_load_dword v18, v[20:21], off
	global_load_dword v19, v[20:21], off offset:2048
	s_nop 0
	global_load_dword v20, v[22:23], off
	global_load_dword v21, v[22:23], off offset:2048
	s_nop 0
	global_load_dword v22, v[24:25], off
	global_load_dword v23, v[24:25], off offset:2048
	v_addc_co_u32_e32 v27, vcc, 0, v65, vcc
	v_add_co_u32_e32 v28, vcc, 0x9000, v64
	s_nop 1
	v_addc_co_u32_e32 v29, vcc, 0, v65, vcc
	v_add_co_u32_e32 v30, vcc, s44, v64
	s_nop 1
	v_addc_co_u32_e32 v31, vcc, 0, v65, vcc
	v_add_co_u32_e32 v32, vcc, 0xb000, v64
	s_nop 1
	v_addc_co_u32_e32 v33, vcc, 0, v65, vcc
	v_add_co_u32_e32 v34, vcc, s45, v64
	global_load_dword v24, v[26:27], off
	global_load_dword v25, v[26:27], off offset:2048
	s_nop 0
	global_load_dword v26, v[28:29], off
	global_load_dword v27, v[28:29], off offset:2048
	s_nop 0
	global_load_dword v28, v[30:31], off
	global_load_dword v29, v[30:31], off offset:2048
	s_nop 0
	global_load_dword v30, v[32:33], off
	global_load_dword v31, v[32:33], off offset:2048
	v_addc_co_u32_e32 v35, vcc, 0, v65, vcc
	v_add_co_u32_e32 v36, vcc, 0xd000, v64
	s_nop 1
	v_addc_co_u32_e32 v37, vcc, 0, v65, vcc
	v_add_co_u32_e32 v38, vcc, s46, v64
	s_nop 1
	v_addc_co_u32_e32 v39, vcc, 0, v65, vcc
	v_add_co_u32_e32 v40, vcc, 0xf000, v64
	s_nop 1
	v_addc_co_u32_e32 v41, vcc, 0, v65, vcc
	v_add_co_u32_e32 v42, vcc, s47, v64
	global_load_dword v32, v[34:35], off
	global_load_dword v33, v[34:35], off offset:2048
	s_nop 0
	global_load_dword v34, v[36:37], off
	global_load_dword v35, v[36:37], off offset:2048
	s_nop 0
	global_load_dword v36, v[38:39], off
	global_load_dword v37, v[38:39], off offset:2048
	s_nop 0
	global_load_dword v38, v[40:41], off
	global_load_dword v39, v[40:41], off offset:2048
	v_addc_co_u32_e32 v43, vcc, 0, v65, vcc
	v_add_co_u32_e32 v44, vcc, 0x11000, v64
	s_nop 1
	v_addc_co_u32_e32 v45, vcc, 0, v65, vcc
	v_add_co_u32_e32 v46, vcc, s48, v64
	s_nop 1
	v_addc_co_u32_e32 v47, vcc, 0, v65, vcc
	v_add_co_u32_e32 v48, vcc, 0x13000, v64
	s_nop 1
	v_addc_co_u32_e32 v49, vcc, 0, v65, vcc
	v_add_co_u32_e32 v50, vcc, s49, v64
	global_load_dword v40, v[42:43], off
	global_load_dword v41, v[42:43], off offset:2048
	s_nop 0
	global_load_dword v42, v[44:45], off
	global_load_dword v43, v[44:45], off offset:2048
	s_nop 0
	global_load_dword v44, v[46:47], off
	global_load_dword v45, v[46:47], off offset:2048
	s_nop 0
	global_load_dword v46, v[48:49], off
	global_load_dword v47, v[48:49], off offset:2048
	v_addc_co_u32_e32 v51, vcc, 0, v65, vcc
	v_add_co_u32_e32 v52, vcc, 0x15000, v64
	s_nop 1
	v_addc_co_u32_e32 v53, vcc, 0, v65, vcc
	v_add_co_u32_e32 v54, vcc, s50, v64
	s_nop 1
	v_addc_co_u32_e32 v55, vcc, 0, v65, vcc
	v_add_co_u32_e32 v56, vcc, 0x17000, v64
	s_nop 1
	v_addc_co_u32_e32 v57, vcc, 0, v65, vcc
	v_add_co_u32_e32 v58, vcc, s51, v64
	global_load_dword v48, v[50:51], off
	global_load_dword v49, v[50:51], off offset:2048
	s_nop 0
	global_load_dword v50, v[52:53], off
	global_load_dword v51, v[52:53], off offset:2048
	s_nop 0
	global_load_dword v52, v[54:55], off
	global_load_dword v53, v[54:55], off offset:2048
	s_nop 0
	global_load_dword v54, v[56:57], off
	global_load_dword v55, v[56:57], off offset:2048
	v_addc_co_u32_e32 v59, vcc, 0, v65, vcc
	v_add_co_u32_e32 v60, vcc, 0x19000, v64
	s_nop 1
	v_addc_co_u32_e32 v61, vcc, 0, v65, vcc
	v_add_co_u32_e32 v62, vcc, s52, v64
	s_nop 1
	v_addc_co_u32_e32 v63, vcc, 0, v65, vcc
	v_add_co_u32_e32 v66, vcc, 0x1b000, v64
	s_nop 1
	v_addc_co_u32_e32 v67, vcc, 0, v65, vcc
	global_load_dword v56, v[58:59], off
	global_load_dword v57, v[58:59], off offset:2048
	s_nop 0
	global_load_dword v58, v[60:61], off
	global_load_dword v59, v[60:61], off offset:2048
	s_nop 0
	global_load_dword v60, v[62:63], off
	global_load_dword v61, v[62:63], off offset:2048
	s_nop 0
	global_load_dword v62, v[66:67], off
	global_load_dword v63, v[66:67], off offset:2048
	v_add_co_u32_e32 v66, vcc, s53, v64
	s_nop 1
	v_addc_co_u32_e32 v67, vcc, 0, v65, vcc
	v_add_co_u32_e32 v68, vcc, 0x1d000, v64
	s_nop 1
	v_addc_co_u32_e32 v69, vcc, 0, v65, vcc
	v_add_co_u32_e32 v70, vcc, s54, v64
	s_nop 1
	v_addc_co_u32_e32 v71, vcc, 0, v65, vcc
	v_add_co_u32_e32 v74, vcc, 0x1f000, v64
	s_nop 1
	v_addc_co_u32_e32 v75, vcc, 0, v65, vcc
	global_load_dword v64, v[66:67], off
	global_load_dword v65, v[66:67], off offset:2048
	s_nop 0
	global_load_dword v66, v[68:69], off
	global_load_dword v67, v[68:69], off offset:2048
	s_nop 0
	global_load_dword v68, v[70:71], off
	global_load_dword v69, v[70:71], off offset:2048
	s_nop 0
	global_load_dword v70, v[74:75], off
	global_load_dword v71, v[74:75], off offset:2048
	s_and_b64 vcc, exec, s[0:1]
	s_cbranch_vccnz .LBB0_46
	s_lshl_b32 s24, s4, 2
	v_lshl_add_u64 v[4:5], v[4:5], 0, s[24:25]
	global_load_dwordx4 v[78:81], v[4:5], off
	global_load_dwordx4 v[82:85], v[4:5], off offset:16
	global_load_dwordx4 v[86:89], v[4:5], off offset:32
	global_load_dwordx4 v[90:93], v[4:5], off offset:48
	global_load_dwordx4 v[94:97], v[4:5], off offset:64
	global_load_dwordx4 v[98:101], v[4:5], off offset:80
	global_load_dwordx4 v[102:105], v[4:5], off offset:96
	global_load_dwordx4 v[106:109], v[4:5], off offset:112
	global_load_dwordx4 v[110:113], v[4:5], off offset:128
	global_load_dwordx4 v[114:117], v[4:5], off offset:144
	global_load_dwordx4 v[118:121], v[4:5], off offset:160
	global_load_dwordx4 v[122:125], v[4:5], off offset:176
	global_load_dwordx4 v[126:129], v[4:5], off offset:192
	global_load_dwordx4 v[130:133], v[4:5], off offset:208
	global_load_dwordx4 v[134:137], v[4:5], off offset:224
	global_load_dwordx4 v[138:141], v[4:5], off offset:240
	s_waitcnt vmcnt(0) lgkmcnt(0)
	v_pk_mul_f32 v[6:7], v[6:7], v[78:79]
	v_pk_mul_f32 v[8:9], v[8:9], v[80:81]
	v_pk_mul_f32 v[10:11], v[10:11], v[82:83]
	v_pk_mul_f32 v[12:13], v[12:13], v[84:85]
	v_pk_mul_f32 v[14:15], v[14:15], v[86:87]
	v_pk_mul_f32 v[18:19], v[18:19], v[88:89]
	v_pk_mul_f32 v[20:21], v[20:21], v[90:91]
	v_pk_mul_f32 v[22:23], v[22:23], v[92:93]
	v_pk_mul_f32 v[24:25], v[24:25], v[94:95]
	v_pk_mul_f32 v[26:27], v[26:27], v[96:97]
	v_pk_mul_f32 v[28:29], v[28:29], v[98:99]
	v_pk_mul_f32 v[30:31], v[30:31], v[100:101]
	v_pk_mul_f32 v[32:33], v[32:33], v[102:103]
	v_pk_mul_f32 v[34:35], v[34:35], v[104:105]
	v_pk_mul_f32 v[36:37], v[36:37], v[106:107]
	v_pk_mul_f32 v[38:39], v[38:39], v[108:109]
	v_pk_mul_f32 v[40:41], v[40:41], v[110:111]
	v_pk_mul_f32 v[42:43], v[42:43], v[112:113]
	v_pk_mul_f32 v[44:45], v[44:45], v[114:115]
	v_pk_mul_f32 v[46:47], v[46:47], v[116:117]
	v_pk_mul_f32 v[48:49], v[48:49], v[118:119]
	v_pk_mul_f32 v[50:51], v[50:51], v[120:121]
	v_pk_mul_f32 v[52:53], v[52:53], v[122:123]
	v_pk_mul_f32 v[54:55], v[54:55], v[124:125]
	v_pk_mul_f32 v[56:57], v[56:57], v[126:127]
	v_pk_mul_f32 v[58:59], v[58:59], v[128:129]
	v_pk_mul_f32 v[60:61], v[60:61], v[130:131]
	v_pk_mul_f32 v[62:63], v[62:63], v[132:133]
	v_pk_mul_f32 v[64:65], v[64:65], v[134:135]
	v_pk_mul_f32 v[66:67], v[66:67], v[136:137]
	v_pk_mul_f32 v[68:69], v[68:69], v[138:139]
	v_pk_mul_f32 v[70:71], v[70:71], v[140:141]
.LBB0_46:
	v_mul_u32_u24_e32 v16, 0x300, v72
	v_lshl_add_u64 v[4:5], s[18:19], 0, v[16:17]
	s_lshl_b32 s24, s4, 1
	v_lshl_add_u64 v[72:73], v[4:5], 0, s[24:25]
	s_waitcnt vmcnt(0) lgkmcnt(0)
	v_cvt_pk_bf16_f32 v4, v6, v7
	v_cvt_pk_bf16_f32 v5, v8, v9
	v_cvt_pk_bf16_f32 v6, v10, v11
	v_cvt_pk_bf16_f32 v7, v12, v13
	global_store_dwordx4 v[72:73], v[4:7], off
	s_mov_b64 s[0:1], 0
	s_nop 0
	v_cvt_pk_bf16_f32 v4, v14, v15
	v_cvt_pk_bf16_f32 v5, v18, v19
	v_cvt_pk_bf16_f32 v6, v20, v21
	v_cvt_pk_bf16_f32 v7, v22, v23
	global_store_dwordx4 v[72:73], v[4:7], off offset:16
	s_nop 1
	v_cvt_pk_bf16_f32 v4, v24, v25
	v_cvt_pk_bf16_f32 v5, v26, v27
	v_cvt_pk_bf16_f32 v6, v28, v29
	v_cvt_pk_bf16_f32 v7, v30, v31
	global_store_dwordx4 v[72:73], v[4:7], off offset:32
	s_nop 1
	v_cvt_pk_bf16_f32 v4, v32, v33
	v_cvt_pk_bf16_f32 v5, v34, v35
	v_cvt_pk_bf16_f32 v6, v36, v37
	v_cvt_pk_bf16_f32 v7, v38, v39
	global_store_dwordx4 v[72:73], v[4:7], off offset:48
	s_nop 1
	v_cvt_pk_bf16_f32 v4, v40, v41
	v_cvt_pk_bf16_f32 v5, v42, v43
	v_cvt_pk_bf16_f32 v6, v44, v45
	v_cvt_pk_bf16_f32 v7, v46, v47
	global_store_dwordx4 v[72:73], v[4:7], off offset:64
	s_nop 1
	v_cvt_pk_bf16_f32 v4, v48, v49
	v_cvt_pk_bf16_f32 v5, v50, v51
	v_cvt_pk_bf16_f32 v6, v52, v53
	v_cvt_pk_bf16_f32 v7, v54, v55
	global_store_dwordx4 v[72:73], v[4:7], off offset:80
	s_nop 1
	v_cvt_pk_bf16_f32 v4, v56, v57
	v_cvt_pk_bf16_f32 v5, v58, v59
	v_cvt_pk_bf16_f32 v6, v60, v61
	v_cvt_pk_bf16_f32 v7, v62, v63
	global_store_dwordx4 v[72:73], v[4:7], off offset:96
	s_nop 1
	v_cvt_pk_bf16_f32 v4, v64, v65
	v_cvt_pk_bf16_f32 v5, v66, v67
	v_cvt_pk_bf16_f32 v6, v68, v69
	v_cvt_pk_bf16_f32 v7, v70, v71
	global_store_dwordx4 v[72:73], v[4:7], off offset:112

.LBB0_48:
	s_add_i32 s0, s79, 0xfffff380
	s_lshr_b32 s0, s0, 1
	s_add_i32 s1, s28, 0xfffce000
	s_and_b32 s24, s0, 0x7c0
	s_and_b32 s1, s1, 0x1fc0
	s_waitcnt lgkmcnt(0)
	v_mov_b32_e32 v4, s73
	v_or_b32_e32 v24, s1, v1
	s_mul_i32 s4, s24, 0xe370
	s_mov_b32 s5, s25
	ds_read_b64 v[18:19], v4
	v_lshl_add_u64 v[4:5], v[2:3], 0, s[4:5]
	v_lshlrev_b32_e32 v16, 2, v24
	v_lshl_add_u64 v[20:21], v[4:5], 0, v[16:17]
	v_add_co_u32_e32 v4, vcc, 0x6000, v20
	s_lshl_b32 s4, s24, 2
	s_nop 0
	v_addc_co_u32_e32 v5, vcc, 0, v21, vcc
	v_add_co_u32_e32 v6, vcc, 0x14000, v20
	s_or_b32 s0, s0, 63
	s_nop 0
	v_addc_co_u32_e32 v7, vcc, 0, v21, vcc
	v_add_co_u32_e32 v8, vcc, 0x22000, v20
	s_mov_b32 s1, s25
	s_nop 0
	v_addc_co_u32_e32 v9, vcc, 0, v21, vcc
	v_add_co_u32_e32 v10, vcc, 0x30000, v20
	s_lshl_b64 s[0:1], s[0:1], 2
	s_nop 0
	v_addc_co_u32_e32 v11, vcc, 0, v21, vcc
	v_add_co_u32_e32 v12, vcc, 0x3f000, v20
	s_nop 1
	v_addc_co_u32_e32 v13, vcc, 0, v21, vcc
	v_add_co_u32_e32 v14, vcc, 0x4d000, v20
	s_nop 1
	v_addc_co_u32_e32 v15, vcc, 0, v21, vcc
	v_add_co_u32_e32 v22, vcc, 0x5b000, v20
	s_nop 1
	v_addc_co_u32_e32 v23, vcc, 0, v21, vcc
	v_add_co_u32_e32 v36, vcc, 0x69000, v20
	s_nop 1
	v_addc_co_u32_e32 v37, vcc, 0, v21, vcc
	global_load_dword v34, v[4:5], off offset:880
	global_load_dword v33, v[6:7], off offset:1760
	global_load_dword v30, v[8:9], off offset:2640
	global_load_dword v28, v[10:11], off offset:3520
	global_load_dword v27, v[12:13], off offset:304
	global_load_dword v26, v[14:15], off offset:1184
	global_load_dword v16, v[22:23], off offset:2064
	global_load_dword v25, v[36:37], off offset:2944
	v_add_co_u32_e32 v4, vcc, 0x77000, v20
	s_nop 1
	v_addc_co_u32_e32 v5, vcc, 0, v21, vcc
	v_add_co_u32_e32 v6, vcc, 0x86000, v20
	s_nop 1
	v_addc_co_u32_e32 v7, vcc, 0, v21, vcc
	v_add_co_u32_e32 v8, vcc, 0x94000, v20
	s_nop 1
	v_addc_co_u32_e32 v9, vcc, 0, v21, vcc
	v_add_co_u32_e32 v10, vcc, 0xa2000, v20
	s_nop 1
	v_addc_co_u32_e32 v11, vcc, 0, v21, vcc
	v_add_co_u32_e32 v12, vcc, 0xb0000, v20
	s_nop 1
	v_addc_co_u32_e32 v13, vcc, 0, v21, vcc
	v_add_co_u32_e32 v14, vcc, 0xbf000, v20
	s_nop 1
	v_addc_co_u32_e32 v15, vcc, 0, v21, vcc
	v_add_co_u32_e32 v22, vcc, 0xcd000, v20
	s_nop 1
	v_addc_co_u32_e32 v23, vcc, 0, v21, vcc
	v_add_co_u32_e32 v40, vcc, 0xdb000, v20
	s_nop 1
	v_addc_co_u32_e32 v41, vcc, 0, v21, vcc
	global_load_dword v39, v[4:5], off offset:3824
	global_load_dword v38, v[6:7], off offset:608
	global_load_dword v37, v[8:9], off offset:1488
	global_load_dword v36, v[10:11], off offset:2368
	global_load_dword v35, v[12:13], off offset:3248
	global_load_dword v31, v[14:15], off offset:32
	global_load_dword v29, v[22:23], off offset:912
	global_load_dword v32, v[40:41], off offset:1792
	v_add_co_u32_e32 v4, vcc, 0xe9000, v20
	s_nop 1
	v_addc_co_u32_e32 v5, vcc, 0, v21, vcc
	v_add_co_u32_e32 v6, vcc, 0xf7000, v20
	s_nop 1
	v_addc_co_u32_e32 v7, vcc, 0, v21, vcc
	v_add_co_u32_e32 v8, vcc, 0x106000, v20
	s_nop 1
	v_addc_co_u32_e32 v9, vcc, 0, v21, vcc
	v_add_co_u32_e32 v10, vcc, 0x114000, v20
	s_nop 1
	v_addc_co_u32_e32 v11, vcc, 0, v21, vcc
	v_add_co_u32_e32 v12, vcc, 0x122000, v20
	s_nop 1
	v_addc_co_u32_e32 v13, vcc, 0, v21, vcc
	v_add_co_u32_e32 v14, vcc, 0x130000, v20
	s_nop 1
	v_addc_co_u32_e32 v15, vcc, 0, v21, vcc
	v_add_co_u32_e32 v22, vcc, 0x13e000, v20
	s_nop 1
	v_addc_co_u32_e32 v23, vcc, 0, v21, vcc
	v_add_co_u32_e32 v48, vcc, 0x14d000, v20
	s_nop 1
	v_addc_co_u32_e32 v49, vcc, 0, v21, vcc
	global_load_dword v47, v[4:5], off offset:2672
	global_load_dword v46, v[6:7], off offset:3552
	global_load_dword v45, v[8:9], off offset:336
	global_load_dword v44, v[10:11], off offset:1216
	global_load_dword v43, v[12:13], off offset:2096
	global_load_dword v41, v[14:15], off offset:2976
	global_load_dword v40, v[22:23], off offset:3856
	global_load_dword v42, v[48:49], off offset:640
	v_add_co_u32_e32 v4, vcc, 0x15b000, v20
	s_nop 1
	v_addc_co_u32_e32 v5, vcc, 0, v21, vcc
	v_add_co_u32_e32 v6, vcc, 0x169000, v20
	s_nop 1
	v_addc_co_u32_e32 v7, vcc, 0, v21, vcc
	v_add_co_u32_e32 v8, vcc, 0x177000, v20
	s_nop 1
	v_addc_co_u32_e32 v9, vcc, 0, v21, vcc
	v_add_co_u32_e32 v10, vcc, 0x186000, v20
	s_nop 1
	v_addc_co_u32_e32 v11, vcc, 0, v21, vcc
	v_add_co_u32_e32 v12, vcc, 0x194000, v20
	s_nop 1
	v_addc_co_u32_e32 v13, vcc, 0, v21, vcc
	v_add_co_u32_e32 v14, vcc, 0x1a2000, v20
	s_nop 1
	v_addc_co_u32_e32 v15, vcc, 0, v21, vcc
	v_add_co_u32_e32 v22, vcc, 0x1b0000, v20
	s_nop 1
	v_addc_co_u32_e32 v23, vcc, 0, v21, vcc
	v_add_co_u32_e32 v56, vcc, 0x1be000, v20
	s_nop 1
	v_addc_co_u32_e32 v57, vcc, 0, v21, vcc
	global_load_dword v55, v[4:5], off offset:1520
	global_load_dword v54, v[6:7], off offset:2400
	global_load_dword v53, v[8:9], off offset:3280
	global_load_dword v52, v[10:11], off offset:64
	global_load_dword v51, v[12:13], off offset:944
	global_load_dword v49, v[14:15], off offset:1824
	global_load_dword v48, v[22:23], off offset:2704
	global_load_dword v50, v[56:57], off offset:3584
	v_add_co_u32_e32 v4, vcc, 0x1cd000, v20
	s_nop 1
	v_addc_co_u32_e32 v5, vcc, 0, v21, vcc
	v_add_co_u32_e32 v6, vcc, 0x1db000, v20
	s_nop 1
	v_addc_co_u32_e32 v7, vcc, 0, v21, vcc
	v_add_co_u32_e32 v8, vcc, 0x1e9000, v20
	s_nop 1
	v_addc_co_u32_e32 v9, vcc, 0, v21, vcc
	v_add_co_u32_e32 v10, vcc, 0x1f7000, v20
	s_nop 1
	v_addc_co_u32_e32 v11, vcc, 0, v21, vcc
	v_add_co_u32_e32 v12, vcc, 0x205000, v20
	s_nop 1
	v_addc_co_u32_e32 v13, vcc, 0, v21, vcc
	v_add_co_u32_e32 v14, vcc, 0x214000, v20
	s_nop 1
	v_addc_co_u32_e32 v15, vcc, 0, v21, vcc
	v_add_co_u32_e32 v22, vcc, 0x222000, v20
	s_nop 1
	v_addc_co_u32_e32 v23, vcc, 0, v21, vcc
	v_add_co_u32_e32 v64, vcc, 0x230000, v20
	s_nop 1
	v_addc_co_u32_e32 v65, vcc, 0, v21, vcc
	global_load_dword v63, v[4:5], off offset:368
	global_load_dword v62, v[6:7], off offset:1248
	global_load_dword v61, v[8:9], off offset:2128
	global_load_dword v60, v[10:11], off offset:3008
	global_load_dword v59, v[12:13], off offset:3888
	global_load_dword v57, v[14:15], off offset:672
	global_load_dword v56, v[22:23], off offset:1552
	global_load_dword v58, v[64:65], off offset:2432
	v_add_co_u32_e32 v4, vcc, 0x23e000, v20
	s_nop 1
	v_addc_co_u32_e32 v5, vcc, 0, v21, vcc
	v_add_co_u32_e32 v6, vcc, 0x24d000, v20
	s_nop 1
	v_addc_co_u32_e32 v7, vcc, 0, v21, vcc
	v_add_co_u32_e32 v8, vcc, 0x25b000, v20
	s_nop 1
	v_addc_co_u32_e32 v9, vcc, 0, v21, vcc
	v_add_co_u32_e32 v10, vcc, 0x269000, v20
	s_nop 1
	v_addc_co_u32_e32 v11, vcc, 0, v21, vcc
	v_add_co_u32_e32 v12, vcc, 0x277000, v20
	s_nop 1
	v_addc_co_u32_e32 v13, vcc, 0, v21, vcc
	v_add_co_u32_e32 v14, vcc, 0x285000, v20
	s_nop 1
	v_addc_co_u32_e32 v15, vcc, 0, v21, vcc
	v_add_co_u32_e32 v22, vcc, 0x294000, v20
	s_nop 1
	v_addc_co_u32_e32 v23, vcc, 0, v21, vcc
	v_add_co_u32_e32 v72, vcc, 0x2a2000, v20
	s_nop 1
	v_addc_co_u32_e32 v73, vcc, 0, v21, vcc
	global_load_dword v71, v[4:5], off offset:3312
	global_load_dword v70, v[6:7], off offset:96
	global_load_dword v69, v[8:9], off offset:976
	global_load_dword v68, v[10:11], off offset:1856
	global_load_dword v64, v[12:13], off offset:2736
	global_load_dword v65, v[14:15], off offset:3616
	global_load_dword v66, v[22:23], off offset:400
	global_load_dword v67, v[72:73], off offset:1280
	v_add_co_u32_e32 v72, vcc, 0x2b0000, v20
	s_waitcnt lgkmcnt(0)
	v_lshl_add_u64 v[22:23], v[18:19], 0, s[4:5]
	v_addc_co_u32_e32 v73, vcc, 0, v21, vcc
	v_add_co_u32_e32 v74, vcc, 0x2be000, v20
	global_load_dwordx4 v[4:7], v[22:23], off
	global_load_dwordx4 v[12:15], v[22:23], off offset:16
	v_addc_co_u32_e32 v75, vcc, 0, v21, vcc
	v_add_co_u32_e32 v78, vcc, 0x2cc000, v20
	s_waitcnt vmcnt(0) lgkmcnt(0)
	v_mul_f32_e32 v4, 0x43000000, v4
	v_addc_co_u32_e32 v79, vcc, 0, v21, vcc
	v_add_co_u32_e32 v80, vcc, 0x2db000, v20
	v_mul_f32_e32 v34, v34, v4
	s_nop 0
	v_addc_co_u32_e32 v81, vcc, 0, v21, vcc
	v_add_co_u32_e32 v82, vcc, 0x2e9000, v20
	v_mul_f32_e32 v4, 0x43000000, v5
	s_nop 0
	v_addc_co_u32_e32 v83, vcc, 0, v21, vcc
	v_add_co_u32_e32 v84, vcc, 0x2f7000, v20
	v_mul_f32_e32 v33, v33, v4
	s_nop 0
	v_addc_co_u32_e32 v85, vcc, 0, v21, vcc
	v_add_co_u32_e32 v86, vcc, 0x305000, v20
	v_mul_f32_e32 v4, 0x43000000, v6
	s_nop 0
	v_addc_co_u32_e32 v87, vcc, 0, v21, vcc
	v_add_co_u32_e32 v88, vcc, 0x314000, v20
	s_nop 1
	v_addc_co_u32_e32 v89, vcc, 0, v21, vcc
	global_load_dwordx4 v[8:11], v[22:23], off offset:32
	global_load_dword v77, v[72:73], off offset:2160
	global_load_dword v112, v[74:75], off offset:3040
	global_load_dword v113, v[78:79], off offset:3920
	global_load_dword v114, v[80:81], off offset:704
	global_load_dword v115, v[82:83], off offset:1584
	global_load_dword v116, v[84:85], off offset:2464
	global_load_dword v117, v[86:87], off offset:3344
	global_load_dword v118, v[88:89], off offset:128
	global_load_dwordx4 v[72:75], v[22:23], off offset:48
	global_load_dwordx4 v[78:81], v[22:23], off offset:64
	v_add_co_u32_e32 v98, vcc, 0x322000, v20
	global_load_dwordx4 v[82:85], v[22:23], off offset:80
	global_load_dwordx4 v[86:89], v[22:23], off offset:96
	v_addc_co_u32_e32 v99, vcc, 0, v21, vcc
	v_add_co_u32_e32 v100, vcc, 0x330000, v20
	global_load_dwordx4 v[90:93], v[22:23], off offset:112
	s_nop 0
	v_addc_co_u32_e32 v101, vcc, 0, v21, vcc
	v_add_co_u32_e32 v102, vcc, 0x33e000, v20
	s_waitcnt vmcnt(0) lgkmcnt(0)
	v_mul_f32_e32 v8, 0x43000000, v8
	v_addc_co_u32_e32 v103, vcc, 0, v21, vcc
	v_add_co_u32_e32 v104, vcc, 0x34c000, v20
	v_mul_f32_e32 v39, v39, v8
	s_nop 0
	v_addc_co_u32_e32 v105, vcc, 0, v21, vcc
	v_add_co_u32_e32 v106, vcc, 0x35b000, v20
	v_mul_f32_e32 v8, 0x43000000, v9
	s_nop 0
	v_addc_co_u32_e32 v107, vcc, 0, v21, vcc
	v_add_co_u32_e32 v108, vcc, 0x369000, v20
	v_mul_f32_e32 v38, v38, v8
	s_nop 0
	v_addc_co_u32_e32 v109, vcc, 0, v21, vcc
	v_add_co_u32_e32 v110, vcc, 0x377000, v20
	v_mul_f32_e32 v8, 0x43000000, v10
	s_nop 0
	v_addc_co_u32_e32 v111, vcc, 0, v21, vcc
	v_add_co_u32_e32 v20, vcc, 0x385000, v20
	v_mul_f32_e32 v37, v37, v8
	s_nop 0
	v_addc_co_u32_e32 v21, vcc, 0, v21, vcc
	global_load_dwordx4 v[94:97], v[22:23], off offset:128
	global_load_dword v119, v[98:99], off offset:1008
	global_load_dword v120, v[100:101], off offset:1888
	s_nop 0
	global_load_dword v102, v[102:103], off offset:2768
	s_nop 0
	global_load_dword v103, v[104:105], off offset:3648
	s_nop 0
	global_load_dword v104, v[106:107], off offset:432
	global_load_dword v105, v[108:109], off offset:1312
	s_nop 0
	global_load_dword v106, v[110:111], off offset:2192
	global_load_dword v107, v[20:21], off offset:3072
	v_lshl_add_u64 v[98:99], v[18:19], 0, s[0:1]
	global_load_dwordx4 v[18:21], v[22:23], off offset:144
	global_load_dword v108, v[98:99], off
	v_mul_f32_e32 v109, v30, v4
	v_mul_f32_e32 v4, 0x43000000, v7
	global_load_dwordx4 v[98:101], v[22:23], off offset:160
	v_mul_f32_e32 v110, v28, v4
	v_mul_f32_e32 v4, 0x43000000, v12
	v_mul_f32_e32 v111, v27, v4
	v_mul_f32_e32 v4, 0x43000000, v13
	v_mul_f32_e32 v12, 0x43000000, v14
	v_mul_f32_e32 v121, v26, v4
	global_load_dwordx4 v[4:7], v[22:23], off offset:176
	v_mul_f32_e32 v122, v16, v12
	v_mul_f32_e32 v12, 0x43000000, v15
	v_mul_f32_e32 v25, v25, v12
	global_load_dwordx4 v[12:15], v[22:23], off offset:192
	v_mul_f32_e32 v8, 0x43000000, v11
	v_mul_f32_e32 v36, v36, v8
	v_mul_f32_e32 v8, 0x43000000, v72
	v_mul_f32_e32 v35, v35, v8
	global_load_dwordx4 v[8:11], v[22:23], off offset:208
	v_mul_f32_e32 v16, 0x43000000, v73
	v_mul_f32_e32 v72, v31, v16
	v_mul_f32_e32 v16, 0x43000000, v74
	v_mul_f32_e32 v73, v29, v16
	global_load_dwordx4 v[26:29], v[22:23], off offset:224
	v_mul_f32_e32 v16, 0x43000000, v75
	v_mul_f32_e32 v74, v32, v16
	global_load_dwordx3 v[30:32], v[22:23], off offset:240
	v_mul_f32_e32 v16, 0x43000000, v78
	v_mul_f32_e32 v47, v47, v16
	v_mul_f32_e32 v16, 0x43000000, v79
	v_mul_f32_e32 v46, v46, v16
	v_mul_f32_e32 v16, 0x43000000, v80
	v_mul_f32_e32 v45, v45, v16
	v_mul_f32_e32 v16, 0x43000000, v81
	v_mul_f32_e32 v44, v44, v16
	v_mul_f32_e32 v16, 0x43000000, v82
	v_mul_f32_e32 v43, v43, v16
	v_mul_f32_e32 v16, 0x43000000, v83
	v_mul_f32_e32 v41, v41, v16
	v_mul_f32_e32 v16, 0x43000000, v84
	v_mul_f32_e32 v40, v40, v16
	v_mul_f32_e32 v16, 0x43000000, v85
	v_mul_f32_e32 v42, v42, v16
	v_mul_f32_e32 v16, 0x43000000, v86
	v_mul_f32_e32 v55, v55, v16
	v_mul_f32_e32 v16, 0x43000000, v87
	v_mul_f32_e32 v54, v54, v16
	v_mul_f32_e32 v16, 0x43000000, v88
	v_mul_f32_e32 v53, v53, v16
	v_mul_f32_e32 v16, 0x43000000, v89
	v_mul_f32_e32 v52, v52, v16
	v_mul_f32_e32 v16, 0x43000000, v90
	v_mul_f32_e32 v51, v51, v16
	v_mul_f32_e32 v16, 0x43000000, v91
	v_mul_f32_e32 v49, v49, v16
	v_mul_f32_e32 v16, 0x43000000, v92
	v_mul_f32_e32 v48, v48, v16
	v_mul_f32_e32 v16, 0x43000000, v93
	v_mul_f32_e32 v50, v50, v16
	s_waitcnt vmcnt(0) lgkmcnt(0)
	v_mul_f32_e32 v16, 0x43000000, v94
	v_mul_f32_e32 v63, v63, v16
	v_mul_f32_e32 v16, 0x43000000, v95
	v_mul_f32_e32 v62, v62, v16
	v_mul_f32_e32 v16, 0x43000000, v96
	v_mul_f32_e32 v61, v61, v16
	v_mul_f32_e32 v16, 0x43000000, v97
	v_mul_f32_e32 v60, v60, v16
	v_mul_f32_e32 v16, 0x43000000, v18
	v_mul_f32_e32 v18, v59, v16
	v_mul_f32_e32 v16, 0x43000000, v19
	v_mul_f32_e32 v19, v57, v16
	v_mul_f32_e32 v16, 0x43000000, v20
	v_mul_f32_e32 v20, v56, v16
	v_mul_f32_e32 v16, 0x43000000, v21
	v_mul_f32_e32 v21, v58, v16
	v_mul_f32_e32 v16, 0x43000000, v98
	v_mul_f32_e32 v56, v71, v16
	v_mul_f32_e32 v16, 0x43000000, v99
	v_mul_f32_e32 v57, v70, v16
	v_mul_f32_e32 v16, 0x43000000, v100
	v_mul_f32_e32 v4, 0x43000000, v4
	v_mul_f32_e32 v58, v69, v16
	v_mul_f32_e32 v16, 0x43000000, v101
	v_mul_f32_e32 v64, v64, v4
	v_mul_f32_e32 v4, 0x43000000, v12
	v_mul_f32_e32 v59, v68, v16
	v_mul_f32_e32 v68, v77, v4
	v_mul_f32_e32 v4, 0x43000000, v13
	v_mul_f32_e32 v69, v112, v4
	v_mul_f32_e32 v4, 0x43000000, v14
	v_mul_f32_e32 v70, v113, v4
	v_mul_f32_e32 v4, 0x43000000, v15
	v_mul_f32_e32 v71, v114, v4
	v_mul_f32_e32 v4, 0x43000000, v8
	v_mul_f32_e32 v75, v115, v4
	v_mul_f32_e32 v4, 0x43000000, v9
	v_mul_f32_e32 v77, v116, v4
	v_mul_f32_e32 v4, 0x43000000, v10
	v_mul_f32_e32 v78, v117, v4
	v_mul_f32_e32 v4, 0x43000000, v11
	v_mul_f32_e32 v79, v118, v4
	v_mul_f32_e32 v4, 0x43000000, v26
	v_mul_f32_e32 v26, v119, v4
	v_mul_f32_e32 v4, 0x43000000, v27
	v_mul_f32_e32 v27, v120, v4
	v_mul_f32_e32 v4, 0x43000000, v28
	v_mul_f32_e32 v28, v102, v4
	v_mul_f32_e32 v4, 0x43000000, v29
	v_mul_f32_e32 v29, v103, v4
	v_mul_f32_e32 v4, 0x43000000, v30
	v_mul_f32_e32 v30, v104, v4
	v_mul_f32_e32 v4, 0x43000000, v31
	v_mul_f32_e32 v31, v105, v4
	v_mul_f32_e32 v4, 0x43000000, v32
	v_mul_f32_e32 v5, 0x43000000, v5
	v_mul_f32_e32 v32, v106, v4
	v_mul_f32_e32 v4, 0x43000000, v108
	v_lshlrev_b32_e32 v16, 11, v24
	v_mul_f32_e32 v6, 0x43000000, v6
	v_mul_f32_e32 v65, v65, v5
	v_mul_f32_e32 v80, v107, v4
	v_lshl_add_u64 v[4:5], s[20:21], 0, v[16:17]
	v_mul_f32_e32 v66, v66, v6
	v_lshl_add_u64 v[22:23], v[4:5], 0, s[24:25]
	v_med3_f32 v5, v34, s74, v76
	v_med3_f32 v6, v33, s74, v76
	v_mov_b32_e32 v4, v17
	v_cvt_pk_fp8_f32 v4, v5, v6
	v_med3_f32 v6, v111, s74, v76
	v_med3_f32 v9, v121, s74, v76
	v_mov_b32_e32 v5, v17
	v_cvt_pk_fp8_f32 v5, v6, v9
	v_mul_f32_e32 v7, 0x43000000, v7
	v_mul_f32_e32 v67, v67, v7
	v_med3_f32 v7, v109, s74, v76
	v_med3_f32 v8, v110, s74, v76
	v_cvt_pk_fp8_f32 v4, v7, v8 op_sel:[0,0,1]
	v_med3_f32 v6, v122, s74, v76
	v_med3_f32 v7, v25, s74, v76
	v_cvt_pk_fp8_f32 v5, v6, v7 op_sel:[0,0,1]
	v_med3_f32 v7, v39, s74, v76
	v_med3_f32 v8, v38, s74, v76
	v_mov_b32_e32 v6, v17
	v_cvt_pk_fp8_f32 v6, v7, v8
	v_med3_f32 v8, v35, s74, v76
	v_med3_f32 v11, v72, s74, v76
	v_mov_b32_e32 v7, v17
	v_cvt_pk_fp8_f32 v7, v8, v11
	v_med3_f32 v9, v37, s74, v76
	v_med3_f32 v10, v36, s74, v76
	v_cvt_pk_fp8_f32 v6, v9, v10 op_sel:[0,0,1]
	v_med3_f32 v8, v73, s74, v76
	v_med3_f32 v9, v74, s74, v76
	v_cvt_pk_fp8_f32 v7, v8, v9 op_sel:[0,0,1]
	v_med3_f32 v9, v47, s74, v76
	v_med3_f32 v10, v46, s74, v76
	v_mov_b32_e32 v8, v17
	v_cvt_pk_fp8_f32 v8, v9, v10
	v_med3_f32 v10, v43, s74, v76
	v_med3_f32 v13, v41, s74, v76
	v_mov_b32_e32 v9, v17
	v_cvt_pk_fp8_f32 v9, v10, v13
	v_med3_f32 v11, v45, s74, v76
	v_med3_f32 v12, v44, s74, v76
	v_cvt_pk_fp8_f32 v8, v11, v12 op_sel:[0,0,1]
	v_med3_f32 v10, v40, s74, v76
	v_med3_f32 v11, v42, s74, v76
	v_cvt_pk_fp8_f32 v9, v10, v11 op_sel:[0,0,1]
	v_med3_f32 v11, v55, s74, v76
	v_med3_f32 v12, v54, s74, v76
	v_mov_b32_e32 v10, v17
	v_cvt_pk_fp8_f32 v10, v11, v12
	v_med3_f32 v12, v51, s74, v76
	v_med3_f32 v15, v49, s74, v76
	v_mov_b32_e32 v11, v17
	v_cvt_pk_fp8_f32 v11, v12, v15
	v_med3_f32 v13, v53, s74, v76
	v_med3_f32 v14, v52, s74, v76
	v_cvt_pk_fp8_f32 v10, v13, v14 op_sel:[0,0,1]
	v_med3_f32 v12, v48, s74, v76
	v_med3_f32 v13, v50, s74, v76
	v_cvt_pk_fp8_f32 v11, v12, v13 op_sel:[0,0,1]
	v_med3_f32 v13, v63, s74, v76
	v_med3_f32 v14, v62, s74, v76
	v_mov_b32_e32 v12, v17
	v_cvt_pk_fp8_f32 v12, v13, v14
	v_med3_f32 v14, v18, s74, v76
	v_med3_f32 v18, v19, s74, v76
	v_mov_b32_e32 v13, v17
	v_cvt_pk_fp8_f32 v13, v14, v18
	v_med3_f32 v15, v61, s74, v76
	v_med3_f32 v16, v60, s74, v76
	v_cvt_pk_fp8_f32 v12, v15, v16 op_sel:[0,0,1]
	v_med3_f32 v14, v20, s74, v76
	v_med3_f32 v15, v21, s74, v76
	v_cvt_pk_fp8_f32 v13, v14, v15 op_sel:[0,0,1]
	v_med3_f32 v15, v56, s74, v76
	v_med3_f32 v16, v57, s74, v76
	v_mov_b32_e32 v14, v17
	v_cvt_pk_fp8_f32 v14, v15, v16
	v_med3_f32 v16, v64, s74, v76
	v_med3_f32 v20, v65, s74, v76
	v_mov_b32_e32 v15, v17
	v_cvt_pk_fp8_f32 v15, v16, v20
	v_med3_f32 v18, v58, s74, v76
	v_med3_f32 v19, v59, s74, v76
	v_cvt_pk_fp8_f32 v14, v18, v19 op_sel:[0,0,1]
	v_med3_f32 v16, v66, s74, v76
	v_med3_f32 v18, v67, s74, v76
	v_cvt_pk_fp8_f32 v15, v16, v18 op_sel:[0,0,1]
	v_med3_f32 v16, v68, s74, v76
	v_med3_f32 v19, v69, s74, v76
	v_mov_b32_e32 v18, v17
	v_cvt_pk_fp8_f32 v18, v16, v19
	v_med3_f32 v16, v75, s74, v76
	v_med3_f32 v24, v77, s74, v76
	v_mov_b32_e32 v19, v17
	v_cvt_pk_fp8_f32 v19, v16, v24
	v_med3_f32 v20, v70, s74, v76
	v_med3_f32 v21, v71, s74, v76
	v_cvt_pk_fp8_f32 v18, v20, v21 op_sel:[0,0,1]
	v_med3_f32 v16, v78, s74, v76
	v_med3_f32 v20, v79, s74, v76
	v_cvt_pk_fp8_f32 v19, v16, v20 op_sel:[0,0,1]
	v_med3_f32 v16, v26, s74, v76
	v_med3_f32 v21, v27, s74, v76
	v_mov_b32_e32 v20, v17
	v_cvt_pk_fp8_f32 v20, v16, v21
	v_med3_f32 v16, v30, s74, v76
	v_med3_f32 v26, v31, s74, v76
	v_mov_b32_e32 v21, v17
	v_cvt_pk_fp8_f32 v21, v16, v26
	v_med3_f32 v24, v28, s74, v76
	v_med3_f32 v25, v29, s74, v76
	v_cvt_pk_fp8_f32 v20, v24, v25 op_sel:[0,0,1]
	v_med3_f32 v16, v32, s74, v76
	v_med3_f32 v24, v80, s74, v76
	v_cvt_pk_fp8_f32 v21, v16, v24 op_sel:[0,0,1]
	global_store_dwordx4 v[22:23], v[4:7], off
	global_store_dwordx4 v[22:23], v[8:11], off offset:16
	global_store_dwordx4 v[22:23], v[12:15], off offset:32
	global_store_dwordx4 v[22:23], v[18:21], off offset:48

.LBB0_69:
	s_or_b64 exec, exec, s[0:1]
	s_lshl_b32 s26, s24, 6
	v_cmp_lt_i32_e64 s[0:1], -1, v5
	s_mul_i32 s4, s24, 0x38dc00
	s_mul_hi_i32 s5, s26, 0xe370
	v_cndmask_b32_e64 v16, 0, v5, s[0:1]
	v_lshl_add_u64 v[2:3], v[2:3], 0, s[4:5]
	v_lshl_add_u64 v[56:57], v[16:17], 2, v[2:3]
	v_add_co_u32_e32 v58, vcc, 0xe000, v56
	s_mov_b64 s[4:5], vcc
	v_add_co_u32_e32 v60, vcc, 0x1c000, v56
	s_ashr_i32 s27, s26, 31
	s_nop 0
	v_addc_co_u32_e32 v61, vcc, 0, v57, vcc
	v_add_co_u32_e32 v62, vcc, 0x2a000, v56
	s_nop 1
	v_addc_co_u32_e32 v63, vcc, 0, v57, vcc
	v_add_co_u32_e32 v64, vcc, 0x38000, v56
	s_nop 1
	v_addc_co_u32_e32 v65, vcc, 0, v57, vcc
	v_add_co_u32_e32 v70, vcc, 0x47000, v56
	s_nop 1
	v_addc_co_u32_e32 v71, vcc, 0, v57, vcc
	v_add_co_u32_e32 v72, vcc, 0x55000, v56
	s_nop 1
	v_addc_co_u32_e32 v73, vcc, 0, v57, vcc
	v_add_co_u32_e32 v74, vcc, 0x63000, v56
	s_nop 1
	v_addc_co_u32_e32 v75, vcc, 0, v57, vcc
	v_add_co_u32_e32 v2, vcc, 0x71000, v56
	s_nop 1
	v_addc_co_u32_e32 v3, vcc, 0, v57, vcc
	v_add_co_u32_e32 v6, vcc, 0x7f000, v56
	s_nop 1
	v_addc_co_u32_e32 v7, vcc, 0, v57, vcc
	v_add_co_u32_e32 v8, vcc, 0x8e000, v56
	s_nop 1
	v_addc_co_u32_e32 v9, vcc, 0, v57, vcc
	v_add_co_u32_e32 v12, vcc, 0x9c000, v56
	s_nop 1
	v_addc_co_u32_e32 v13, vcc, 0, v57, vcc
	v_add_co_u32_e32 v14, vcc, 0xaa000, v56
	s_nop 1
	v_addc_co_u32_e32 v15, vcc, 0, v57, vcc
	v_add_co_u32_e32 v18, vcc, 0xb8000, v56
	s_nop 1
	v_addc_co_u32_e32 v19, vcc, 0, v57, vcc
	v_add_co_u32_e32 v20, vcc, 0xc7000, v56
	s_nop 1
	v_addc_co_u32_e32 v21, vcc, 0, v57, vcc
	v_add_co_u32_e32 v24, vcc, 0xd5000, v56
	s_nop 1
	v_addc_co_u32_e32 v25, vcc, 0, v57, vcc
	global_load_dword v10, v[2:3], off offset:2944
	global_load_dword v11, v[6:7], off offset:3824
	s_nop 0
	global_load_dword v8, v[8:9], off offset:608
	s_nop 0
	global_load_dword v9, v[12:13], off offset:1488
	global_load_dword v6, v[14:15], off offset:2368
	global_load_dword v7, v[18:19], off offset:3248
	global_load_dword v2, v[20:21], off offset:32
	global_load_dword v3, v[24:25], off offset:912
	v_add_co_u32_e32 v12, vcc, 0xe3000, v56
	s_nop 1
	v_addc_co_u32_e32 v13, vcc, 0, v57, vcc
	v_add_co_u32_e32 v14, vcc, 0xf1000, v56
	s_nop 1
	v_addc_co_u32_e32 v15, vcc, 0, v57, vcc
	v_add_co_u32_e32 v18, vcc, 0xff000, v56
	s_nop 1
	v_addc_co_u32_e32 v19, vcc, 0, v57, vcc
	v_add_co_u32_e32 v24, vcc, 0x10e000, v56
	s_nop 1
	v_addc_co_u32_e32 v25, vcc, 0, v57, vcc
	v_add_co_u32_e32 v26, vcc, 0x11c000, v56
	s_nop 1
	v_addc_co_u32_e32 v27, vcc, 0, v57, vcc
	v_add_co_u32_e32 v28, vcc, 0x12a000, v56
	s_nop 1
	v_addc_co_u32_e32 v29, vcc, 0, v57, vcc
	v_add_co_u32_e32 v30, vcc, 0x138000, v56
	s_nop 1
	v_addc_co_u32_e32 v31, vcc, 0, v57, vcc
	v_add_co_u32_e32 v32, vcc, 0x146000, v56
	s_nop 1
	v_addc_co_u32_e32 v33, vcc, 0, v57, vcc
	global_load_dword v20, v[12:13], off offset:1792
	global_load_dword v21, v[14:15], off offset:2672
	s_nop 0
	global_load_dword v18, v[18:19], off offset:3552
	s_nop 0
	global_load_dword v19, v[24:25], off offset:336
	global_load_dword v14, v[26:27], off offset:1216
	global_load_dword v15, v[28:29], off offset:2096
	global_load_dword v12, v[30:31], off offset:2976
	global_load_dword v13, v[32:33], off offset:3856
	v_add_co_u32_e32 v24, vcc, 0x155000, v56
	s_nop 1
	v_addc_co_u32_e32 v25, vcc, 0, v57, vcc
	v_add_co_u32_e32 v26, vcc, 0x163000, v56
	s_nop 1
	v_addc_co_u32_e32 v27, vcc, 0, v57, vcc
	v_add_co_u32_e32 v28, vcc, 0x171000, v56
	s_nop 1
	v_addc_co_u32_e32 v29, vcc, 0, v57, vcc
	v_add_co_u32_e32 v32, vcc, 0x17f000, v56
	s_nop 1
	v_addc_co_u32_e32 v33, vcc, 0, v57, vcc
	v_add_co_u32_e32 v34, vcc, 0x18e000, v56
	s_nop 1
	v_addc_co_u32_e32 v35, vcc, 0, v57, vcc
	v_add_co_u32_e32 v36, vcc, 0x19c000, v56
	s_nop 1
	v_addc_co_u32_e32 v37, vcc, 0, v57, vcc
	v_add_co_u32_e32 v38, vcc, 0x1aa000, v56
	s_nop 1
	v_addc_co_u32_e32 v39, vcc, 0, v57, vcc
	v_add_co_u32_e32 v40, vcc, 0x1b8000, v56
	s_nop 1
	v_addc_co_u32_e32 v41, vcc, 0, v57, vcc
	global_load_dword v30, v[24:25], off offset:640
	global_load_dword v31, v[26:27], off offset:1520
	s_nop 0
	global_load_dword v28, v[28:29], off offset:2400
	s_nop 0
	global_load_dword v29, v[32:33], off offset:3280
	global_load_dword v26, v[34:35], off offset:64
	global_load_dword v27, v[36:37], off offset:944
	global_load_dword v24, v[38:39], off offset:1824
	global_load_dword v25, v[40:41], off offset:2704
	v_add_co_u32_e32 v32, vcc, 0x1c6000, v56
	s_nop 1
	v_addc_co_u32_e32 v33, vcc, 0, v57, vcc
	v_add_co_u32_e32 v34, vcc, 0x1d5000, v56
	s_nop 1
	v_addc_co_u32_e32 v35, vcc, 0, v57, vcc
	v_add_co_u32_e32 v36, vcc, 0x1e3000, v56
	s_nop 1
	v_addc_co_u32_e32 v37, vcc, 0, v57, vcc
	v_add_co_u32_e32 v40, vcc, 0x1f1000, v56
	s_nop 1
	v_addc_co_u32_e32 v41, vcc, 0, v57, vcc
	v_add_co_u32_e32 v42, vcc, 0x1ff000, v56
	s_nop 1
	v_addc_co_u32_e32 v43, vcc, 0, v57, vcc
	v_add_co_u32_e32 v44, vcc, 0x20d000, v56
	s_nop 1
	v_addc_co_u32_e32 v45, vcc, 0, v57, vcc
	v_add_co_u32_e32 v46, vcc, 0x21c000, v56
	s_nop 1
	v_addc_co_u32_e32 v47, vcc, 0, v57, vcc
	v_add_co_u32_e32 v48, vcc, 0x22a000, v56
	s_nop 1
	v_addc_co_u32_e32 v49, vcc, 0, v57, vcc
	global_load_dword v38, v[32:33], off offset:3584
	global_load_dword v39, v[34:35], off offset:368
	s_nop 0
	global_load_dword v36, v[36:37], off offset:1248
	s_nop 0
	global_load_dword v37, v[40:41], off offset:2128
	global_load_dword v34, v[42:43], off offset:3008
	global_load_dword v35, v[44:45], off offset:3888
	global_load_dword v32, v[46:47], off offset:672
	global_load_dword v33, v[48:49], off offset:1552
	v_add_co_u32_e32 v40, vcc, 0x238000, v56
	s_nop 1
	v_addc_co_u32_e32 v41, vcc, 0, v57, vcc
	v_add_co_u32_e32 v42, vcc, 0x246000, v56
	s_nop 1
	v_addc_co_u32_e32 v43, vcc, 0, v57, vcc
	v_add_co_u32_e32 v44, vcc, 0x255000, v56
	s_nop 1
	v_addc_co_u32_e32 v45, vcc, 0, v57, vcc
	v_add_co_u32_e32 v48, vcc, 0x263000, v56
	s_nop 1
	v_addc_co_u32_e32 v49, vcc, 0, v57, vcc
	v_add_co_u32_e32 v50, vcc, 0x271000, v56
	s_nop 1
	v_addc_co_u32_e32 v51, vcc, 0, v57, vcc
	v_add_co_u32_e32 v52, vcc, 0x27f000, v56
	s_nop 1
	v_addc_co_u32_e32 v53, vcc, 0, v57, vcc
	v_add_co_u32_e32 v54, vcc, 0x28d000, v56
	s_nop 1
	v_addc_co_u32_e32 v55, vcc, 0, v57, vcc
	v_add_co_u32_e32 v66, vcc, 0x29c000, v56
	s_nop 1
	v_addc_co_u32_e32 v67, vcc, 0, v57, vcc
	global_load_dword v46, v[40:41], off offset:2432
	global_load_dword v47, v[42:43], off offset:3312
	s_nop 0
	global_load_dword v44, v[44:45], off offset:96
	s_nop 0
	global_load_dword v45, v[48:49], off offset:976
	global_load_dword v42, v[50:51], off offset:1856
	global_load_dword v43, v[52:53], off offset:2736
	global_load_dword v40, v[54:55], off offset:3616
	global_load_dword v41, v[66:67], off offset:400
	v_add_co_u32_e32 v48, vcc, 0x2aa000, v56
	s_nop 1
	v_addc_co_u32_e32 v49, vcc, 0, v57, vcc
	v_add_co_u32_e32 v50, vcc, 0x2b8000, v56
	s_nop 1
	v_addc_co_u32_e32 v51, vcc, 0, v57, vcc
	v_add_co_u32_e32 v52, vcc, 0x2c6000, v56
	s_nop 1
	v_addc_co_u32_e32 v53, vcc, 0, v57, vcc
	v_add_co_u32_e32 v66, vcc, 0x2d4000, v56
	s_nop 1
	v_addc_co_u32_e32 v67, vcc, 0, v57, vcc
	v_add_co_u32_e32 v68, vcc, 0x2e3000, v56
	s_nop 1
	v_addc_co_u32_e32 v69, vcc, 0, v57, vcc
	v_add_co_u32_e32 v78, vcc, 0x2f1000, v56
	s_nop 1
	v_addc_co_u32_e32 v79, vcc, 0, v57, vcc
	v_add_co_u32_e32 v80, vcc, 0x2ff000, v56
	s_nop 1
	v_addc_co_u32_e32 v81, vcc, 0, v57, vcc
	v_add_co_u32_e32 v82, vcc, 0x30d000, v56
	s_nop 1
	v_addc_co_u32_e32 v83, vcc, 0, v57, vcc
	v_addc_co_u32_e64 v59, vcc, 0, v57, s[4:5]
	global_load_dword v54, v[48:49], off offset:1280
	global_load_dword v55, v[50:51], off offset:2160
	s_nop 0
	global_load_dword v52, v[52:53], off offset:3040
	s_nop 0
	global_load_dword v53, v[66:67], off offset:3920
	global_load_dword v50, v[68:69], off offset:704
	global_load_dword v51, v[78:79], off offset:1584
	global_load_dword v48, v[80:81], off offset:2464
	global_load_dword v49, v[82:83], off offset:3344
	s_nop 0
	global_load_dword v68, v[60:61], off offset:1760
	global_load_dword v69, v[62:63], off offset:2640
	global_load_dword v66, v[64:65], off offset:3520
	global_load_dword v67, v[70:71], off offset:304
	s_nop 0
	global_load_dword v64, v[72:73], off offset:1184
	global_load_dword v65, v[74:75], off offset:2064
	global_load_dword v71, v[58:59], off offset:880
	global_load_dword v70, v[56:57], off
	v_add_co_u32_e32 v58, vcc, 0x31c000, v56
	s_nop 1
	v_addc_co_u32_e32 v59, vcc, 0, v57, vcc
	v_add_co_u32_e32 v60, vcc, 0x32a000, v56
	s_nop 1
	v_addc_co_u32_e32 v61, vcc, 0, v57, vcc
	v_add_co_u32_e32 v72, vcc, 0x338000, v56
	s_nop 1
	v_addc_co_u32_e32 v73, vcc, 0, v57, vcc
	v_add_co_u32_e32 v74, vcc, 0x346000, v56
	s_nop 1
	v_addc_co_u32_e32 v75, vcc, 0, v57, vcc
	v_add_co_u32_e32 v78, vcc, 0x354000, v56
	s_nop 1
	v_addc_co_u32_e32 v79, vcc, 0, v57, vcc
	v_add_co_u32_e32 v80, vcc, 0x363000, v56
	s_nop 1
	v_addc_co_u32_e32 v81, vcc, 0, v57, vcc
	v_add_co_u32_e32 v82, vcc, 0x371000, v56
	s_nop 1
	v_addc_co_u32_e32 v83, vcc, 0, v57, vcc
	v_add_co_u32_e32 v84, vcc, 0x37f000, v56
	s_nop 1
	v_addc_co_u32_e32 v85, vcc, 0, v57, vcc
	global_load_dword v62, v[58:59], off offset:128
	global_load_dword v63, v[60:61], off offset:1008
	s_nop 0
	global_load_dword v60, v[72:73], off offset:1888
	global_load_dword v61, v[74:75], off offset:2768
	global_load_dword v58, v[78:79], off offset:3648
	global_load_dword v59, v[80:81], off offset:432
	global_load_dword v56, v[82:83], off offset:1312
	global_load_dword v57, v[84:85], off offset:2192
	s_waitcnt lgkmcnt(0)
	v_cmp_eq_u64_e32 vcc, 0, v[22:23]
	s_cbranch_vccnz .LBB0_28
	s_lshl_b64 s[4:5], s[26:27], 2
	v_lshl_add_u64 v[22:23], v[22:23], 0, s[4:5]
	global_load_dwordx4 v[72:75], v[22:23], off
	global_load_dwordx4 v[78:81], v[22:23], off offset:16
	global_load_dwordx4 v[82:85], v[22:23], off offset:32
	global_load_dwordx4 v[86:89], v[22:23], off offset:48
	global_load_dwordx4 v[90:93], v[22:23], off offset:64
	global_load_dwordx4 v[94:97], v[22:23], off offset:80
	global_load_dwordx4 v[98:101], v[22:23], off offset:96
	global_load_dwordx4 v[102:105], v[22:23], off offset:112
	global_load_dwordx4 v[106:109], v[22:23], off offset:128
	global_load_dwordx4 v[110:113], v[22:23], off offset:144
	global_load_dwordx4 v[114:117], v[22:23], off offset:160
	global_load_dwordx4 v[118:121], v[22:23], off offset:176
	global_load_dwordx4 v[122:125], v[22:23], off offset:192
	global_load_dwordx4 v[126:129], v[22:23], off offset:208
	global_load_dwordx4 v[130:133], v[22:23], off offset:224
	global_load_dwordx4 v[134:137], v[22:23], off offset:240
	s_waitcnt vmcnt(0) lgkmcnt(0)
	v_pk_mul_f32 v[70:71], v[70:71], v[72:73]
	v_pk_mul_f32 v[68:69], v[68:69], v[74:75]
	v_pk_mul_f32 v[66:67], v[66:67], v[78:79]
	v_pk_mul_f32 v[64:65], v[64:65], v[80:81]
	v_pk_mul_f32 v[10:11], v[10:11], v[82:83]
	v_pk_mul_f32 v[8:9], v[8:9], v[84:85]
	v_pk_mul_f32 v[6:7], v[6:7], v[86:87]
	v_pk_mul_f32 v[2:3], v[2:3], v[88:89]
	v_pk_mul_f32 v[20:21], v[20:21], v[90:91]
	v_pk_mul_f32 v[18:19], v[18:19], v[92:93]
	v_pk_mul_f32 v[14:15], v[14:15], v[94:95]
	v_pk_mul_f32 v[12:13], v[12:13], v[96:97]
	v_pk_mul_f32 v[30:31], v[30:31], v[98:99]
	v_pk_mul_f32 v[28:29], v[28:29], v[100:101]
	v_pk_mul_f32 v[26:27], v[26:27], v[102:103]
	v_pk_mul_f32 v[24:25], v[24:25], v[104:105]
	v_pk_mul_f32 v[38:39], v[38:39], v[106:107]
	v_pk_mul_f32 v[36:37], v[36:37], v[108:109]
	v_pk_mul_f32 v[34:35], v[34:35], v[110:111]
	v_pk_mul_f32 v[32:33], v[32:33], v[112:113]
	v_pk_mul_f32 v[46:47], v[46:47], v[114:115]
	v_pk_mul_f32 v[44:45], v[44:45], v[116:117]
	v_pk_mul_f32 v[42:43], v[42:43], v[118:119]
	v_pk_mul_f32 v[40:41], v[40:41], v[120:121]
	v_pk_mul_f32 v[54:55], v[54:55], v[122:123]
	v_pk_mul_f32 v[52:53], v[52:53], v[124:125]
	v_pk_mul_f32 v[50:51], v[50:51], v[126:127]
	v_pk_mul_f32 v[48:49], v[48:49], v[128:129]
	v_pk_mul_f32 v[62:63], v[62:63], v[130:131]
	v_pk_mul_f32 v[60:61], v[60:61], v[132:133]
	v_pk_mul_f32 v[58:59], v[58:59], v[134:135]
	v_pk_mul_f32 v[56:57], v[56:57], v[136:137]
	s_branch .LBB0_28

.LBB0_74:
	s_or_b64 exec, exec, s[22:23]
	s_waitcnt lgkmcnt(0)
	v_lshl_add_u64 v[48:49], s[12:13], 0, v[38:39]
	v_add_co_u32_e32 v48, vcc, 0x5000000, v48
	v_cvt_pk_bf16_f32 v50, v30, v31
	v_cvt_pk_bf16_f32 v51, v32, v33
	v_addc_co_u32_e32 v49, vcc, 0, v49, vcc
	v_max_f32_e32 v30, v30, v30
	v_max_f32_e32 v31, v31, v31
	global_store_dwordx2 v[48:49], v[50:51], off
	v_med3_f32 v30, v30, s7, v1
	v_med3_f32 v31, v31, s7, v1
	v_mov_b32_e32 v50, 0
	v_cvt_pk_fp8_f32 v50, v30, v31
	v_max_f32_e32 v32, v32, v32
	v_max_f32_e32 v31, v33, v33
	v_med3_f32 v30, v32, s7, v1
	v_med3_f32 v31, v31, s7, v1
	v_cvt_pk_fp8_f32 v50, v30, v31 op_sel:[0,0,1]
	v_max_f32_e32 v32, v26, v26
	v_max_f32_e32 v33, v27, v27
	v_lshl_add_u64 v[30:31], s[12:13], 0, v[36:37]
	v_med3_f32 v32, v32, s7, v1
	v_med3_f32 v33, v33, s7, v1
	v_mov_b32_e32 v51, 0
	v_add_co_u32_e32 v30, vcc, s9, v30
	v_cvt_pk_fp8_f32 v51, v32, v33
	s_nop 0
	v_addc_co_u32_e32 v31, vcc, 0, v31, vcc
	global_store_dword v[30:31], v50, off
	v_max_f32_e32 v50, v28, v28
	v_max_f32_e32 v33, v29, v29
	v_med3_f32 v32, v50, s7, v1
	v_med3_f32 v33, v33, s7, v1
	v_cvt_pk_fp8_f32 v51, v32, v33 op_sel:[0,0,1]
	v_cvt_pk_bf16_f32 v26, v26, v27
	v_cvt_pk_bf16_f32 v27, v28, v29
	global_store_dwordx2 v[48:49], v[26:27], off offset:512
	global_store_dword v[30:31], v51, off offset:256
	v_max_f32_e32 v26, v22, v22
	v_max_f32_e32 v27, v23, v23
	v_med3_f32 v26, v26, s7, v1
	v_med3_f32 v27, v27, s7, v1
	v_mov_b32_e32 v29, 0
	v_cvt_pk_fp8_f32 v29, v26, v27
	v_max_f32_e32 v28, v24, v24
	v_max_f32_e32 v27, v25, v25
	v_med3_f32 v26, v28, s7, v1
	v_med3_f32 v27, v27, s7, v1
	v_cvt_pk_fp8_f32 v29, v26, v27 op_sel:[0,0,1]
	v_cvt_pk_bf16_f32 v22, v22, v23
	v_cvt_pk_bf16_f32 v23, v24, v25
	global_store_dwordx2 v[48:49], v[22:23], off offset:1024
	global_store_dword v[30:31], v29, off offset:512
	v_max_f32_e32 v22, v18, v18
	v_max_f32_e32 v23, v19, v19
	v_med3_f32 v22, v22, s7, v1
	v_med3_f32 v23, v23, s7, v1
	v_mov_b32_e32 v25, 0
	v_cvt_pk_fp8_f32 v25, v22, v23
	v_max_f32_e32 v24, v20, v20
	v_max_f32_e32 v23, v21, v21
	v_med3_f32 v22, v24, s7, v1
	v_med3_f32 v23, v23, s7, v1
	v_cvt_pk_fp8_f32 v25, v22, v23 op_sel:[0,0,1]
	v_cvt_pk_bf16_f32 v18, v18, v19
	v_cvt_pk_bf16_f32 v19, v20, v21
	global_store_dwordx2 v[48:49], v[18:19], off offset:1536
	global_store_dword v[30:31], v25, off offset:768
	v_max_f32_e32 v18, v14, v14
	v_max_f32_e32 v19, v15, v15
	v_med3_f32 v18, v18, s7, v1
	v_med3_f32 v19, v19, s7, v1
	v_mov_b32_e32 v21, 0
	v_cvt_pk_fp8_f32 v21, v18, v19
	v_max_f32_e32 v20, v16, v16
	v_max_f32_e32 v19, v17, v17
	v_med3_f32 v18, v20, s7, v1
	v_med3_f32 v19, v19, s7, v1
	v_cvt_pk_fp8_f32 v21, v18, v19 op_sel:[0,0,1]
	v_cvt_pk_bf16_f32 v14, v14, v15
	v_cvt_pk_bf16_f32 v15, v16, v17
	global_store_dwordx2 v[48:49], v[14:15], off offset:2048
	global_store_dword v[30:31], v21, off offset:1024
	v_max_f32_e32 v14, v10, v10
	v_max_f32_e32 v15, v11, v11
	v_med3_f32 v14, v14, s7, v1
	v_med3_f32 v15, v15, s7, v1
	v_mov_b32_e32 v17, 0
	v_cvt_pk_fp8_f32 v17, v14, v15
	v_max_f32_e32 v16, v12, v12
	v_max_f32_e32 v15, v13, v13
	v_med3_f32 v14, v16, s7, v1
	v_med3_f32 v15, v15, s7, v1
	v_cvt_pk_fp8_f32 v17, v14, v15 op_sel:[0,0,1]
	v_cvt_pk_bf16_f32 v10, v10, v11
	v_cvt_pk_bf16_f32 v11, v12, v13
	global_store_dwordx2 v[48:49], v[10:11], off offset:2560
	global_store_dword v[30:31], v17, off offset:1280
	v_max_f32_e32 v10, v6, v6
	v_max_f32_e32 v11, v7, v7
	v_med3_f32 v10, v10, s7, v1
	v_med3_f32 v11, v11, s7, v1
	v_mov_b32_e32 v13, 0
	v_cvt_pk_fp8_f32 v13, v10, v11
	v_max_f32_e32 v12, v8, v8
	v_max_f32_e32 v11, v9, v9
	v_med3_f32 v10, v12, s7, v1
	v_med3_f32 v11, v11, s7, v1
	v_cvt_pk_fp8_f32 v13, v10, v11 op_sel:[0,0,1]
	v_cvt_pk_bf16_f32 v6, v6, v7
	v_cvt_pk_bf16_f32 v7, v8, v9
	global_store_dwordx2 v[48:49], v[6:7], off offset:3072
	global_store_dword v[30:31], v13, off offset:1536
	v_max_f32_e32 v6, v2, v2
	v_max_f32_e32 v7, v3, v3
	v_med3_f32 v6, v6, s7, v1
	v_med3_f32 v7, v7, s7, v1
	v_mov_b32_e32 v9, 0
	v_cvt_pk_fp8_f32 v9, v6, v7
	v_max_f32_e32 v8, v4, v4
	v_max_f32_e32 v7, v5, v5
	v_med3_f32 v6, v8, s7, v1
	v_med3_f32 v7, v7, s7, v1
	v_cvt_pk_fp8_f32 v9, v6, v7 op_sel:[0,0,1]
	s_add_i32 s6, s6, s8
	v_cvt_pk_bf16_f32 v2, v2, v3
	v_cvt_pk_bf16_f32 v3, v4, v5
	v_lshl_add_u64 v[34:35], v[34:35], 0, s[14:15]
	v_lshl_add_u64 v[36:37], v[36:37], 0, s[16:17]
	v_lshl_add_u64 v[38:39], v[38:39], 0, s[18:19]
	s_cmpk_lt_i32 s6, 0x4000
	v_lshl_add_u64 v[40:41], v[40:41], 0, s[20:21]
	global_store_dwordx2 v[48:49], v[2:3], off offset:3584
	global_store_dword v[30:31], v9, off offset:1792
	s_cbranch_scc0 .LBB0_77
.LBB0_75:
	v_add_co_u32_e32 v18, vcc, 0xfffff000, v40
	global_load_dwordx4 v[14:17], v[40:41], off
	global_load_dwordx4 v[10:13], v[40:41], off offset:1024
	global_load_dwordx4 v[6:9], v[40:41], off offset:2048
	global_load_dwordx4 v[2:5], v[40:41], off offset:3072
	v_addc_co_u32_e32 v19, vcc, -1, v41, vcc
	global_load_dwordx4 v[30:33], v[18:19], off
	v_add_co_u32_e32 v18, vcc, 0xfffff400, v40
	s_waitcnt vmcnt(0) lgkmcnt(0)
	v_mul_f32_e32 v48, v15, v15
	v_addc_co_u32_e32 v19, vcc, -1, v41, vcc
	v_add_co_u32_e32 v20, vcc, 0xfffff800, v40
	global_load_dwordx4 v[26:29], v[18:19], off
	s_nop 0
	v_addc_co_u32_e32 v21, vcc, -1, v41, vcc
	global_load_dwordx4 v[22:25], v[20:21], off
	v_add_co_u32_e32 v18, vcc, 0xfffffc00, v40
	v_mul_f32_e32 v49, v17, v17
	s_nop 0
	v_addc_co_u32_e32 v19, vcc, -1, v41, vcc
	global_load_dwordx4 v[18:21], v[18:19], off
	v_mul_f32_e32 v50, v11, v11
	v_mul_f32_e32 v51, v13, v13
	v_mul_f32_e32 v52, v7, v7
	v_mul_f32_e32 v53, v9, v9
	v_fmac_f32_e32 v48, v14, v14
	v_fmac_f32_e32 v49, v16, v16
	v_fmac_f32_e32 v50, v10, v10
	v_fmac_f32_e32 v51, v12, v12
	v_fmac_f32_e32 v52, v6, v6
	v_fmac_f32_e32 v53, v8, v8
	v_mul_f32_e32 v56, v31, v31
	v_mul_f32_e32 v57, v33, v33
	v_add_f32_e32 v48, v48, v49
	v_add_f32_e32 v49, v50, v51
	v_add_f32_e32 v50, v52, v53
	v_fmac_f32_e32 v56, v30, v30
	v_fmac_f32_e32 v57, v32, v32
	v_add_f32_e32 v53, v56, v57
	v_mul_f32_e32 v54, v3, v3
	v_mul_f32_e32 v55, v5, v5
	v_fmac_f32_e32 v54, v2, v2
	v_fmac_f32_e32 v55, v4, v4
	s_waitcnt vmcnt(0) lgkmcnt(0)
	v_mul_f32_e32 v51, v27, v27
	v_mul_f32_e32 v52, v29, v29
	v_fmac_f32_e32 v51, v26, v26
	v_fmac_f32_e32 v52, v28, v28
	v_mul_f32_e32 v56, v23, v23
	v_mul_f32_e32 v57, v25, v25
	v_add_f32_e32 v51, v51, v52
	v_fmac_f32_e32 v56, v22, v22
	v_fmac_f32_e32 v57, v24, v24
	v_mul_f32_e32 v52, v19, v19
	v_mul_f32_e32 v58, v21, v21
	v_add_f32_e32 v51, v53, v51
	v_add_f32_e32 v53, v56, v57
	v_fmac_f32_e32 v52, v18, v18
	v_fmac_f32_e32 v58, v20, v20
	v_add_f32_e32 v51, v51, v53
	v_add_f32_e32 v52, v52, v58
	v_add_f32_e32 v51, v51, v52
	v_add_f32_e32 v48, v51, v48
	v_add_f32_e32 v48, v48, v49
	v_add_f32_e32 v48, v48, v50
	v_add_f32_e32 v49, v54, v55
	v_add_f32_e32 v48, v48, v49
	ds_bpermute_b32 v49, v42, v48
	s_waitcnt lgkmcnt(0)
	v_add_f32_e32 v48, v48, v49
	ds_bpermute_b32 v49, v43, v48
	s_waitcnt lgkmcnt(0)
	v_add_f32_e32 v48, v48, v49
	ds_bpermute_b32 v49, v44, v48
	s_waitcnt lgkmcnt(0)
	v_add_f32_e32 v48, v48, v49
	ds_bpermute_b32 v49, v45, v48
	s_waitcnt lgkmcnt(0)
	v_add_f32_e32 v48, v48, v49
	ds_bpermute_b32 v49, v46, v48
	s_waitcnt lgkmcnt(0)
	v_add_f32_e32 v48, v48, v49
	ds_bpermute_b32 v49, v47, v48
	s_and_saveexec_b64 s[22:23], s[0:1]
	s_cbranch_execz .LBB0_74
	s_waitcnt lgkmcnt(0)
	v_add_f32_e32 v48, v48, v49
	v_lshl_add_u64 v[50:51], s[12:13], 0, v[34:35]
	v_cndmask_b32_e64 v48, 0, v48, s[4:5]
	global_store_dword v[50:51], v48, off
	s_branch .LBB0_74

.LBB0_147:
	s_ashr_i32 s10, s13, 3
	s_add_i32 s10, s15, s10
	s_ashr_i32 s11, s10, 31
	s_lshr_b32 s11, s11, 24
	s_add_i32 s11, s10, s11
	s_ashr_i32 s13, s11, 8
	s_lshl_b32 s13, s13, 3
	s_sub_i32 s14, 64, s13
	s_min_i32 s14, s14, 8
	s_abs_i32 s14, s14
	v_cvt_f32_u32_e32 v2, s14
	s_sub_i32 s15, 0, s14
	s_and_b32 s11, s11, 0xffffff00
	s_sub_i32 s10, s10, s11
	v_rcp_iflag_f32_e32 v2, v2
	s_ashr_i32 s11, s10, 31
	s_abs_i32 s10, s10
	v_mul_f32_e32 v2, 0x4f7ffffe, v2
	v_cvt_u32_f32_e32 v2, v2
	s_nop 0
	v_readfirstlane_b32 s16, v2
	s_mul_i32 s15, s15, s16
	s_mul_hi_u32 s15, s16, s15
	s_add_i32 s16, s16, s15
	s_mul_hi_u32 s15, s10, s16
	s_mul_i32 s15, s15, s14
	s_sub_i32 s10, s10, s15
	s_sub_i32 s15, s10, s14
	s_cmp_ge_u32 s10, s14
	s_cselect_b32 s10, s15, s10
	s_sub_i32 s15, s10, s14
	s_cmp_ge_u32 s10, s14
	s_cselect_b32 s10, s15, s10
	s_xor_b32 s10, s10, s11
	s_sub_i32 s10, s10, s11
	s_add_i32 s13, s13, s10
	s_cmp_eq_u32 s13, s12
	s_mov_b32 s14, s12
	s_cbranch_scc1 .LBB0_140
	v_lshl_add_u32 v6, s13, 8, v9
	v_ashrrev_i32_e32 v7, 31, v6
	s_waitcnt lgkmcnt(0)
	v_lshlrev_b64 v[10:11], 7, v[6:7]
	v_lshl_add_u64 v[22:23], v[4:5], 0, v[10:11]
	global_load_dwordx4 v[10:13], v[22:23], off
	global_load_dwordx4 v[14:17], v[22:23], off offset:16
	global_load_dwordx4 v[18:21], v[22:23], off offset:32
	s_nop 0
	global_load_dwordx4 v[22:25], v[22:23], off offset:48
	v_xor_b32_e32 v2, 1, v230
	v_cmp_lt_i32_e32 vcc, v2, v231
	s_nop 1
	v_cndmask_b32_e32 v26, v230, v2, vcc
	s_waitcnt vmcnt(0) lgkmcnt(0)
	v_add_f32_e32 v2, v10, v11
	v_add_f32_e32 v10, v12, v13
	v_add_f32_e32 v11, v14, v15
	v_add_f32_e32 v12, v16, v17
	v_add_f32_e32 v2, v2, v10
	v_add_f32_e32 v13, v18, v19
	v_add_f32_e32 v14, v20, v21
	v_add_f32_e32 v10, v11, v12
	v_add_f32_e32 v2, 0, v2
	v_add_f32_e32 v15, v22, v23
	v_add_f32_e32 v16, v24, v25
	v_add_f32_e32 v11, v13, v14
	v_add_f32_e32 v2, v2, v10
	v_add_f32_e32 v12, v15, v16
	v_add_f32_e32 v2, v2, v11
	v_add_f32_e32 v2, v2, v12
	v_lshlrev_b32_e32 v10, 2, v26
	ds_bpermute_b32 v10, v10, v2
	s_and_saveexec_b64 s[10:11], s[0:1]
	s_cbranch_execz .LBB0_139
	s_waitcnt lgkmcnt(0)
	v_add_f32_e32 v2, v2, v10
	v_fmamk_f32 v2, v2, 0x3a000000, v241
	v_mul_f32_e32 v10, 0x4b800000, v2
	v_cmp_gt_f32_e32 vcc, s25, v2
	v_lshl_add_u64 v[6:7], v[6:7], 2, s[4:5]
	s_nop 0
	v_cndmask_b32_e32 v2, v2, v10, vcc
	v_rsq_f32_e32 v2, v2
	s_nop 0
	v_mul_f32_e32 v10, 0x45800000, v2
	v_cndmask_b32_e32 v2, v2, v10, vcc
	global_store_dword v[6:7], v2, off
	s_branch .LBB0_139

.LBB0_154:
	v_mov_b64_e32 v[6:7], 0x63f
	v_cmp_gt_i64_e32 vcc, s[8:9], v[6:7]
	s_mov_b64 s[10:11], -1
	s_cbranch_vccnz .LBB0_153
	s_ashr_i32 s10, s8, 31
	s_lshr_b32 s10, s10, 29
	s_add_i32 s10, s8, s10
	s_ashr_i32 s11, s10, 3
	s_and_b32 s10, s10, -8
	s_sub_i32 s10, s8, s10
	s_cmp_lt_i32 s10, 0
	s_movk_i32 s13, 0xc9
	s_cselect_b32 s13, s13, 0xc8
	s_mul_i32 s10, s13, s10
	s_add_i32 s10, s10, s11
	s_mul_hi_i32 s11, s10, 0x51eb851f
	s_lshr_b32 s13, s11, 31
	s_ashr_i32 s11, s11, 6
	s_add_i32 s11, s11, s13
	s_lshl_b32 s13, s11, 3
	s_sub_i32 s14, 64, s13
	s_min_i32 s14, s14, 8
	s_abs_i32 s14, s14
	v_cvt_f32_u32_e32 v2, s14
	s_sub_i32 s15, 0, s14
	s_mulk_i32 s11, 0xc8
	s_sub_i32 s10, s10, s11
	v_rcp_iflag_f32_e32 v2, v2
	s_ashr_i32 s11, s10, 31
	s_abs_i32 s10, s10
	v_mul_f32_e32 v2, 0x4f7ffffe, v2
	v_cvt_u32_f32_e32 v2, v2
	s_nop 0
	v_readfirstlane_b32 s16, v2
	s_mul_i32 s15, s15, s16
	s_mul_hi_u32 s15, s16, s15
	s_add_i32 s16, s16, s15
	s_mul_hi_u32 s15, s10, s16
	s_mul_i32 s15, s15, s14
	s_sub_i32 s10, s10, s15
	s_sub_i32 s15, s10, s14
	s_cmp_ge_u32 s10, s14
	s_cselect_b32 s10, s15, s10
	s_sub_i32 s15, s10, s14
	s_cmp_ge_u32 s10, s14
	s_cselect_b32 s10, s15, s10
	s_xor_b32 s10, s10, s11
	s_sub_i32 s10, s10, s11
	s_add_i32 s13, s10, s13
	s_cmp_eq_u32 s13, s12
	s_cbranch_scc1 .LBB0_152
	v_lshl_add_u32 v6, s13, 8, v9
	v_ashrrev_i32_e32 v7, 31, v6
	s_waitcnt lgkmcnt(0)
	v_lshlrev_b64 v[10:11], 7, v[6:7]
	v_lshl_add_u64 v[22:23], v[4:5], 0, v[10:11]
	global_load_dwordx4 v[10:13], v[22:23], off
	global_load_dwordx4 v[14:17], v[22:23], off offset:16
	global_load_dwordx4 v[18:21], v[22:23], off offset:32
	s_nop 0
	global_load_dwordx4 v[22:25], v[22:23], off offset:48
	v_xor_b32_e32 v2, 1, v230
	v_cmp_lt_i32_e32 vcc, v2, v231
	s_nop 1
	v_cndmask_b32_e32 v26, v230, v2, vcc
	s_waitcnt vmcnt(0) lgkmcnt(0)
	v_add_f32_e32 v2, v10, v11
	v_add_f32_e32 v10, v12, v13
	v_add_f32_e32 v11, v14, v15
	v_add_f32_e32 v12, v16, v17
	v_add_f32_e32 v2, v2, v10
	v_add_f32_e32 v13, v18, v19
	v_add_f32_e32 v14, v20, v21
	v_add_f32_e32 v10, v11, v12
	v_add_f32_e32 v2, 0, v2
	v_add_f32_e32 v15, v22, v23
	v_add_f32_e32 v16, v24, v25
	v_add_f32_e32 v11, v13, v14
	v_add_f32_e32 v2, v2, v10
	v_add_f32_e32 v12, v15, v16
	v_add_f32_e32 v2, v2, v11
	v_add_f32_e32 v2, v2, v12
	v_lshlrev_b32_e32 v10, 2, v26
	ds_bpermute_b32 v10, v10, v2
	s_and_saveexec_b64 s[10:11], s[0:1]
	s_cbranch_execz .LBB0_151
	s_waitcnt lgkmcnt(0)
	v_add_f32_e32 v2, v2, v10
	v_fmamk_f32 v2, v2, 0x3a000000, v241
	v_mul_f32_e32 v10, 0x4b800000, v2
	v_cmp_gt_f32_e32 vcc, s25, v2
	v_lshl_add_u64 v[6:7], v[6:7], 2, s[4:5]
	s_nop 0
	v_cndmask_b32_e32 v2, v2, v10, vcc
	v_rsq_f32_e32 v2, v2
	s_nop 0
	v_mul_f32_e32 v10, 0x45800000, v2
	v_cndmask_b32_e32 v2, v2, v10, vcc
	global_store_dword v[6:7], v2, off
	s_branch .LBB0_151

.LBB0_178:
	v_lshl_add_u32 v8, s20, 8, v194
	v_ashrrev_i32_e32 v9, 31, v8
	s_nop 15
	s_nop 15
	v_lshl_add_u64 v[10:11], v[8:9], 2, s[4:5]
	global_load_dword v22, v[10:11], off
	v_or_b32_e32 v16, 16, v8
	v_ashrrev_i32_e32 v17, 31, v16
	v_lshl_add_u64 v[6:7], v[16:17], 2, s[4:5]
	global_load_dword v21, v[6:7], off
	v_or_b32_e32 v14, 32, v8
	v_ashrrev_i32_e32 v15, 31, v14
	v_or_b32_e32 v12, 48, v8
	v_lshl_add_u64 v[6:7], v[14:15], 2, s[4:5]
	v_ashrrev_i32_e32 v13, 31, v12
	global_load_dword v20, v[6:7], off
	v_lshl_add_u64 v[6:7], v[12:13], 2, s[4:5]
	v_lshl_or_b32 v4, s21, 8, v211
	global_load_dword v9, v[6:7], off
	v_mov_b64_e32 v[6:7], s[8:9]
	s_movk_i32 s13, 0x7200
	v_ashrrev_i32_e32 v5, 31, v4
	v_mad_i64_i32 v[18:19], s[20:21], v8, s13, v[6:7]
	v_lshl_add_u64 v[18:19], v[18:19], 0, v[4:5]
	s_andn2_b64 vcc, exec, s[36:37]
	s_waitcnt vmcnt(0) lgkmcnt(0)
	v_mul_f32_e32 v13, 0x3c000000, v22
	v_mul_f32_e32 v13, 0xbfb8aa3b, v13
	v_mul_f32_e32 v15, v160, v13
	v_mul_f32_e32 v17, v156, v13
	v_exp_f32_e32 v15, v15
	v_exp_f32_e32 v17, v17
	v_mul_f32_e32 v22, v161, v13
	v_mul_f32_e32 v23, v157, v13
	v_exp_f32_e32 v22, v22
	v_exp_f32_e32 v23, v23
	v_fmamk_f32 v15, v15, 0x3b808081, v227
	v_fmamk_f32 v17, v17, 0x3b808081, v227
	v_rcp_f32_e32 v15, v15
	v_rcp_f32_e32 v17, v17
	v_fmamk_f32 v22, v22, 0x3b808081, v227
	v_fmamk_f32 v23, v23, 0x3b808081, v227
	v_rcp_f32_e32 v22, v22
	v_rcp_f32_e32 v23, v23
	v_max_f32_e32 v15, 1.0, v15
	v_max_f32_e32 v17, 1.0, v17
	v_cvt_pk_u8_f32 v15, v15, 0, 0
	v_cvt_pk_u8_f32 v17, v17, 0, 0
	v_max_f32_e32 v22, 1.0, v22
	v_max_f32_e32 v23, 1.0, v23
	v_cvt_pk_u8_f32 v15, v22, 1, v15
	v_cvt_pk_u8_f32 v17, v23, 1, v17
	v_mul_f32_e32 v22, v162, v13
	v_mul_f32_e32 v23, v158, v13
	v_exp_f32_e32 v22, v22
	v_exp_f32_e32 v23, v23
	v_mul_f32_e32 v9, 0x3c000000, v9
	v_mul_f32_e32 v9, 0xbfb8aa3b, v9
	v_fmamk_f32 v22, v22, 0x3b808081, v227
	v_fmamk_f32 v23, v23, 0x3b808081, v227
	v_rcp_f32_e32 v22, v22
	v_rcp_f32_e32 v23, v23
	v_max_f32_e32 v22, 1.0, v22
	v_max_f32_e32 v23, 1.0, v23
	v_cvt_pk_u8_f32 v15, v22, 2, v15
	v_cvt_pk_u8_f32 v17, v23, 2, v17
	v_mul_f32_e32 v22, v163, v13
	v_mul_f32_e32 v23, v159, v13
	v_exp_f32_e32 v22, v22
	v_exp_f32_e32 v23, v23
	v_fmamk_f32 v22, v22, 0x3b808081, v227
	v_fmamk_f32 v23, v23, 0x3b808081, v227
	v_rcp_f32_e32 v22, v22
	v_rcp_f32_e32 v23, v23
	v_max_f32_e32 v22, 1.0, v22
	v_max_f32_e32 v23, 1.0, v23
	v_cvt_pk_u8_f32 v22, v22, 3, v15
	v_cvt_pk_u8_f32 v23, v23, 3, v17
	v_mul_f32_e32 v15, v152, v13
	global_store_dwordx2 v[18:19], v[22:23], off
	v_exp_f32_e32 v15, v15
	v_mul_f32_e32 v22, v153, v13
	v_exp_f32_e32 v22, v22
	v_mul_f32_e32 v17, v148, v13
	v_fmamk_f32 v15, v15, 0x3b808081, v227
	v_rcp_f32_e32 v15, v15
	v_fmamk_f32 v22, v22, 0x3b808081, v227
	v_rcp_f32_e32 v22, v22
	v_exp_f32_e32 v17, v17
	v_max_f32_e32 v15, 1.0, v15
	v_cvt_pk_u8_f32 v15, v15, 0, 0
	v_max_f32_e32 v22, 1.0, v22
	v_mul_f32_e32 v23, v149, v13
	v_exp_f32_e32 v23, v23
	v_cvt_pk_u8_f32 v15, v22, 1, v15
	v_mul_f32_e32 v22, v154, v13
	v_exp_f32_e32 v22, v22
	v_fmamk_f32 v17, v17, 0x3b808081, v227
	v_rcp_f32_e32 v17, v17
	v_fmamk_f32 v23, v23, 0x3b808081, v227
	v_rcp_f32_e32 v23, v23
	v_fmamk_f32 v22, v22, 0x3b808081, v227
	v_rcp_f32_e32 v22, v22
	v_max_f32_e32 v17, 1.0, v17
	v_cvt_pk_u8_f32 v17, v17, 0, 0
	v_max_f32_e32 v23, 1.0, v23
	v_cvt_pk_u8_f32 v17, v23, 1, v17
	v_max_f32_e32 v22, 1.0, v22
	v_mul_f32_e32 v23, v150, v13
	v_exp_f32_e32 v23, v23
	v_cvt_pk_u8_f32 v15, v22, 2, v15
	v_mul_f32_e32 v22, v155, v13
	v_mul_f32_e32 v13, v151, v13
	v_exp_f32_e32 v13, v13
	v_exp_f32_e32 v22, v22
	v_fmamk_f32 v23, v23, 0x3b808081, v227
	v_rcp_f32_e32 v23, v23
	v_fmamk_f32 v13, v13, 0x3b808081, v227
	v_fmamk_f32 v22, v22, 0x3b808081, v227
	v_rcp_f32_e32 v13, v13
	v_rcp_f32_e32 v22, v22
	v_max_f32_e32 v23, 1.0, v23
	v_cvt_pk_u8_f32 v17, v23, 2, v17
	v_max_f32_e32 v13, 1.0, v13
	v_max_f32_e32 v22, 1.0, v22
	v_cvt_pk_u8_f32 v23, v13, 3, v17
	v_mul_f32_e32 v13, 0x3c000000, v21
	v_cvt_pk_u8_f32 v22, v22, 3, v15
	v_mul_f32_e32 v13, 0xbfb8aa3b, v13
	global_store_dwordx2 v[18:19], v[22:23], off offset:128
	v_mul_f32_e32 v15, v144, v13
	v_mul_f32_e32 v18, v140, v13
	v_exp_f32_e32 v15, v15
	v_exp_f32_e32 v18, v18
	v_mul_f32_e32 v19, v145, v13
	v_mul_f32_e32 v21, v141, v13
	v_exp_f32_e32 v19, v19
	v_exp_f32_e32 v21, v21
	v_fmamk_f32 v15, v15, 0x3b808081, v227
	v_fmamk_f32 v18, v18, 0x3b808081, v227
	v_rcp_f32_e32 v15, v15
	v_rcp_f32_e32 v18, v18
	v_fmamk_f32 v19, v19, 0x3b808081, v227
	v_fmamk_f32 v21, v21, 0x3b808081, v227
	v_rcp_f32_e32 v19, v19
	v_rcp_f32_e32 v21, v21
	v_max_f32_e32 v15, 1.0, v15
	v_max_f32_e32 v18, 1.0, v18
	v_cvt_pk_u8_f32 v15, v15, 0, 0
	v_cvt_pk_u8_f32 v18, v18, 0, 0
	v_max_f32_e32 v19, 1.0, v19
	v_max_f32_e32 v21, 1.0, v21
	v_cvt_pk_u8_f32 v15, v19, 1, v15
	v_cvt_pk_u8_f32 v18, v21, 1, v18
	v_mul_f32_e32 v19, v146, v13
	v_mul_f32_e32 v21, v142, v13
	v_exp_f32_e32 v19, v19
	v_exp_f32_e32 v21, v21
	v_mad_i64_i32 v[16:17], s[20:21], v16, s13, v[6:7]
	v_fmamk_f32 v19, v19, 0x3b808081, v227
	v_fmamk_f32 v21, v21, 0x3b808081, v227
	v_rcp_f32_e32 v19, v19
	v_rcp_f32_e32 v21, v21
	v_lshl_add_u64 v[16:17], v[16:17], 0, v[4:5]
	v_max_f32_e32 v19, 1.0, v19
	v_max_f32_e32 v21, 1.0, v21
	v_cvt_pk_u8_f32 v15, v19, 2, v15
	v_cvt_pk_u8_f32 v19, v21, 2, v18
	v_mul_f32_e32 v18, v147, v13
	v_mul_f32_e32 v21, v143, v13
	v_exp_f32_e32 v18, v18
	v_exp_f32_e32 v21, v21
	v_fmamk_f32 v18, v18, 0x3b808081, v227
	v_fmamk_f32 v21, v21, 0x3b808081, v227
	v_rcp_f32_e32 v18, v18
	v_rcp_f32_e32 v21, v21
	v_max_f32_e32 v18, 1.0, v18
	v_max_f32_e32 v21, 1.0, v21
	v_cvt_pk_u8_f32 v18, v18, 3, v15
	v_cvt_pk_u8_f32 v19, v21, 3, v19
	global_store_dwordx2 v[16:17], v[18:19], off
	v_mul_f32_e32 v15, v136, v13
	v_mul_f32_e32 v18, v132, v13
	v_exp_f32_e32 v15, v15
	v_exp_f32_e32 v18, v18
	v_mul_f32_e32 v19, v137, v13
	v_mul_f32_e32 v21, v133, v13
	v_exp_f32_e32 v19, v19
	v_exp_f32_e32 v21, v21
	v_fmamk_f32 v15, v15, 0x3b808081, v227
	v_fmamk_f32 v18, v18, 0x3b808081, v227
	v_rcp_f32_e32 v15, v15
	v_rcp_f32_e32 v18, v18
	v_fmamk_f32 v19, v19, 0x3b808081, v227
	v_fmamk_f32 v21, v21, 0x3b808081, v227
	v_rcp_f32_e32 v19, v19
	v_rcp_f32_e32 v21, v21
	v_max_f32_e32 v15, 1.0, v15
	v_max_f32_e32 v18, 1.0, v18
	v_cvt_pk_u8_f32 v15, v15, 0, 0
	v_cvt_pk_u8_f32 v18, v18, 0, 0
	v_max_f32_e32 v19, 1.0, v19
	v_max_f32_e32 v21, 1.0, v21
	v_cvt_pk_u8_f32 v15, v19, 1, v15
	v_cvt_pk_u8_f32 v18, v21, 1, v18
	v_mul_f32_e32 v19, v138, v13
	v_mul_f32_e32 v21, v134, v13
	v_exp_f32_e32 v19, v19
	v_exp_f32_e32 v21, v21
	v_fmamk_f32 v19, v19, 0x3b808081, v227
	v_fmamk_f32 v21, v21, 0x3b808081, v227
	v_rcp_f32_e32 v19, v19
	v_rcp_f32_e32 v21, v21
	v_max_f32_e32 v19, 1.0, v19
	v_max_f32_e32 v21, 1.0, v21
	v_cvt_pk_u8_f32 v15, v19, 2, v15
	v_cvt_pk_u8_f32 v19, v21, 2, v18
	v_mul_f32_e32 v18, v139, v13
	v_mul_f32_e32 v13, v135, v13
	v_exp_f32_e32 v13, v13
	v_exp_f32_e32 v18, v18
	v_fmamk_f32 v13, v13, 0x3b808081, v227
	v_fmamk_f32 v18, v18, 0x3b808081, v227
	v_rcp_f32_e32 v13, v13
	v_rcp_f32_e32 v18, v18
	v_max_f32_e32 v13, 1.0, v13
	v_max_f32_e32 v18, 1.0, v18
	v_cvt_pk_u8_f32 v19, v13, 3, v19
	v_mul_f32_e32 v13, 0x3c000000, v20
	v_cvt_pk_u8_f32 v18, v18, 3, v15
	v_mul_f32_e32 v13, 0xbfb8aa3b, v13
	global_store_dwordx2 v[16:17], v[18:19], off offset:128
	v_mul_f32_e32 v16, v128, v13
	v_mul_f32_e32 v17, v124, v13
	v_exp_f32_e32 v16, v16
	v_exp_f32_e32 v17, v17
	v_mul_f32_e32 v18, v129, v13
	v_mul_f32_e32 v19, v125, v13
	v_exp_f32_e32 v18, v18
	v_exp_f32_e32 v19, v19
	v_fmamk_f32 v16, v16, 0x3b808081, v227
	v_fmamk_f32 v17, v17, 0x3b808081, v227
	v_rcp_f32_e32 v16, v16
	v_rcp_f32_e32 v17, v17
	v_fmamk_f32 v18, v18, 0x3b808081, v227
	v_fmamk_f32 v19, v19, 0x3b808081, v227
	v_rcp_f32_e32 v18, v18
	v_rcp_f32_e32 v19, v19
	v_max_f32_e32 v16, 1.0, v16
	v_max_f32_e32 v17, 1.0, v17
	v_cvt_pk_u8_f32 v16, v16, 0, 0
	v_cvt_pk_u8_f32 v17, v17, 0, 0
	v_max_f32_e32 v18, 1.0, v18
	v_max_f32_e32 v19, 1.0, v19
	v_cvt_pk_u8_f32 v16, v18, 1, v16
	v_cvt_pk_u8_f32 v17, v19, 1, v17
	v_mul_f32_e32 v18, v130, v13
	v_mul_f32_e32 v19, v126, v13
	v_exp_f32_e32 v18, v18
	v_exp_f32_e32 v19, v19
	v_mad_i64_i32 v[14:15], s[20:21], v14, s13, v[6:7]
	v_fmamk_f32 v18, v18, 0x3b808081, v227
	v_fmamk_f32 v19, v19, 0x3b808081, v227
	v_rcp_f32_e32 v18, v18
	v_rcp_f32_e32 v19, v19
	v_lshl_add_u64 v[14:15], v[14:15], 0, v[4:5]
	v_max_f32_e32 v18, 1.0, v18
	v_max_f32_e32 v19, 1.0, v19
	v_cvt_pk_u8_f32 v16, v18, 2, v16
	v_cvt_pk_u8_f32 v17, v19, 2, v17
	v_mul_f32_e32 v18, v131, v13
	v_mul_f32_e32 v19, v127, v13
	v_exp_f32_e32 v18, v18
	v_exp_f32_e32 v19, v19
	v_fmamk_f32 v18, v18, 0x3b808081, v227
	v_fmamk_f32 v19, v19, 0x3b808081, v227
	v_rcp_f32_e32 v18, v18
	v_rcp_f32_e32 v19, v19
	v_max_f32_e32 v18, 1.0, v18
	v_max_f32_e32 v19, 1.0, v19
	v_cvt_pk_u8_f32 v16, v18, 3, v16
	v_cvt_pk_u8_f32 v17, v19, 3, v17
	global_store_dwordx2 v[14:15], v[16:17], off
	v_mul_f32_e32 v16, v120, v13
	v_exp_f32_e32 v16, v16
	v_mul_f32_e32 v18, v121, v13
	v_exp_f32_e32 v18, v18
	v_mul_f32_e32 v17, v116, v13
	v_fmamk_f32 v16, v16, 0x3b808081, v227
	v_rcp_f32_e32 v16, v16
	v_fmamk_f32 v18, v18, 0x3b808081, v227
	v_rcp_f32_e32 v18, v18
	v_exp_f32_e32 v17, v17
	v_max_f32_e32 v16, 1.0, v16
	v_cvt_pk_u8_f32 v16, v16, 0, 0
	v_max_f32_e32 v18, 1.0, v18
	v_mul_f32_e32 v19, v117, v13
	v_exp_f32_e32 v19, v19
	v_cvt_pk_u8_f32 v16, v18, 1, v16
	v_mul_f32_e32 v18, v122, v13
	v_exp_f32_e32 v18, v18
	v_fmamk_f32 v17, v17, 0x3b808081, v227
	v_rcp_f32_e32 v17, v17
	v_fmamk_f32 v19, v19, 0x3b808081, v227
	v_rcp_f32_e32 v19, v19
	v_fmamk_f32 v18, v18, 0x3b808081, v227
	v_rcp_f32_e32 v18, v18
	v_max_f32_e32 v17, 1.0, v17
	v_cvt_pk_u8_f32 v17, v17, 0, 0
	v_max_f32_e32 v19, 1.0, v19
	v_cvt_pk_u8_f32 v17, v19, 1, v17
	v_max_f32_e32 v18, 1.0, v18
	v_mul_f32_e32 v19, v118, v13
	v_exp_f32_e32 v19, v19
	v_cvt_pk_u8_f32 v16, v18, 2, v16
	v_mul_f32_e32 v18, v123, v13
	v_mul_f32_e32 v13, v119, v13
	v_exp_f32_e32 v18, v18
	v_exp_f32_e32 v13, v13
	v_fmamk_f32 v19, v19, 0x3b808081, v227
	v_rcp_f32_e32 v19, v19
	v_fmamk_f32 v18, v18, 0x3b808081, v227
	v_fmamk_f32 v13, v13, 0x3b808081, v227
	v_rcp_f32_e32 v18, v18
	v_rcp_f32_e32 v13, v13
	v_max_f32_e32 v19, 1.0, v19
	v_cvt_pk_u8_f32 v17, v19, 2, v17
	v_max_f32_e32 v18, 1.0, v18
	v_max_f32_e32 v13, 1.0, v13
	v_cvt_pk_u8_f32 v16, v18, 3, v16
	v_cvt_pk_u8_f32 v17, v13, 3, v17
	global_store_dwordx2 v[14:15], v[16:17], off offset:128
	v_mul_f32_e32 v14, v112, v9
	v_mul_f32_e32 v15, v108, v9
	v_exp_f32_e32 v14, v14
	v_exp_f32_e32 v15, v15
	v_mul_f32_e32 v16, v113, v9
	v_mul_f32_e32 v17, v109, v9
	v_exp_f32_e32 v16, v16
	v_exp_f32_e32 v17, v17
	v_fmamk_f32 v14, v14, 0x3b808081, v227
	v_fmamk_f32 v15, v15, 0x3b808081, v227
	v_rcp_f32_e32 v14, v14
	v_rcp_f32_e32 v15, v15
	v_fmamk_f32 v16, v16, 0x3b808081, v227
	v_fmamk_f32 v17, v17, 0x3b808081, v227
	v_rcp_f32_e32 v16, v16
	v_rcp_f32_e32 v17, v17
	v_max_f32_e32 v14, 1.0, v14
	v_max_f32_e32 v15, 1.0, v15
	v_cvt_pk_u8_f32 v14, v14, 0, 0
	v_cvt_pk_u8_f32 v15, v15, 0, 0
	v_max_f32_e32 v16, 1.0, v16
	v_max_f32_e32 v17, 1.0, v17
	v_cvt_pk_u8_f32 v14, v16, 1, v14
	v_cvt_pk_u8_f32 v15, v17, 1, v15
	v_mul_f32_e32 v16, v114, v9
	v_mul_f32_e32 v17, v110, v9
	v_exp_f32_e32 v16, v16
	v_exp_f32_e32 v17, v17
	v_mad_i64_i32 v[12:13], s[20:21], v12, s13, v[6:7]
	v_fmamk_f32 v16, v16, 0x3b808081, v227
	v_fmamk_f32 v17, v17, 0x3b808081, v227
	v_rcp_f32_e32 v16, v16
	v_rcp_f32_e32 v17, v17
	v_lshl_add_u64 v[12:13], v[12:13], 0, v[4:5]
	v_add_u32_e32 v18, 0x90, v8
	v_max_f32_e32 v16, 1.0, v16
	v_max_f32_e32 v17, 1.0, v17
	v_cvt_pk_u8_f32 v14, v16, 2, v14
	v_cvt_pk_u8_f32 v15, v17, 2, v15
	v_mul_f32_e32 v16, v115, v9
	v_mul_f32_e32 v17, v111, v9
	v_exp_f32_e32 v16, v16
	v_exp_f32_e32 v17, v17
	v_fmamk_f32 v16, v16, 0x3b808081, v227
	v_fmamk_f32 v17, v17, 0x3b808081, v227
	v_rcp_f32_e32 v16, v16
	v_rcp_f32_e32 v17, v17
	v_max_f32_e32 v16, 1.0, v16
	v_max_f32_e32 v17, 1.0, v17
	v_cvt_pk_u8_f32 v14, v16, 3, v14
	v_cvt_pk_u8_f32 v15, v17, 3, v15
	global_store_dwordx2 v[12:13], v[14:15], off
	v_mul_f32_e32 v14, v104, v9
	v_exp_f32_e32 v14, v14
	v_mul_f32_e32 v16, v105, v9
	v_exp_f32_e32 v16, v16
	v_mul_f32_e32 v15, v100, v9
	v_fmamk_f32 v14, v14, 0x3b808081, v227
	v_rcp_f32_e32 v14, v14
	v_fmamk_f32 v16, v16, 0x3b808081, v227
	v_rcp_f32_e32 v16, v16
	v_exp_f32_e32 v15, v15
	v_max_f32_e32 v14, 1.0, v14
	v_cvt_pk_u8_f32 v14, v14, 0, 0
	v_max_f32_e32 v16, 1.0, v16
	v_mul_f32_e32 v17, v101, v9
	v_exp_f32_e32 v17, v17
	v_cvt_pk_u8_f32 v14, v16, 1, v14
	v_mul_f32_e32 v16, v106, v9
	v_exp_f32_e32 v16, v16
	v_fmamk_f32 v15, v15, 0x3b808081, v227
	v_rcp_f32_e32 v15, v15
	v_fmamk_f32 v17, v17, 0x3b808081, v227
	v_rcp_f32_e32 v17, v17
	v_fmamk_f32 v16, v16, 0x3b808081, v227
	v_rcp_f32_e32 v16, v16
	v_max_f32_e32 v15, 1.0, v15
	v_cvt_pk_u8_f32 v15, v15, 0, 0
	v_max_f32_e32 v17, 1.0, v17
	v_cvt_pk_u8_f32 v15, v17, 1, v15
	v_max_f32_e32 v16, 1.0, v16
	v_mul_f32_e32 v17, v102, v9
	v_exp_f32_e32 v17, v17
	v_cvt_pk_u8_f32 v14, v16, 2, v14
	v_mul_f32_e32 v16, v107, v9
	v_mul_f32_e32 v9, v103, v9
	v_exp_f32_e32 v16, v16
	v_exp_f32_e32 v9, v9
	v_fmamk_f32 v17, v17, 0x3b808081, v227
	v_rcp_f32_e32 v17, v17
	v_fmamk_f32 v16, v16, 0x3b808081, v227
	v_fmamk_f32 v9, v9, 0x3b808081, v227
	v_rcp_f32_e32 v16, v16
	v_rcp_f32_e32 v9, v9
	v_max_f32_e32 v17, 1.0, v17
	v_cvt_pk_u8_f32 v15, v17, 2, v15
	v_max_f32_e32 v16, 1.0, v16
	v_max_f32_e32 v9, 1.0, v9
	v_cvt_pk_u8_f32 v14, v16, 3, v14
	v_cvt_pk_u8_f32 v15, v9, 3, v15
	global_store_dwordx2 v[12:13], v[14:15], off offset:128
	global_load_dword v15, v[10:11], off offset:512
	v_add_u32_e32 v9, 0x80, v8
	global_load_dword v19, v[10:11], off offset:576
	global_load_dword v13, v[10:11], off offset:640
	v_add_u32_e32 v14, 0xa0, v8
	global_load_dword v10, v[10:11], off offset:704
	v_add_u32_e32 v12, 0xb0, v8
	v_mad_i64_i32 v[8:9], s[20:21], v9, s13, v[6:7]
	v_lshl_add_u64 v[8:9], v[8:9], 0, v[4:5]
	s_waitcnt vmcnt(0) lgkmcnt(0)
	v_mul_f32_e32 v11, 0x3c000000, v15
	v_mul_f32_e32 v11, 0xbfb8aa3b, v11
	v_mul_f32_e32 v15, v96, v11
	v_mul_f32_e32 v16, v92, v11
	v_exp_f32_e32 v15, v15
	v_exp_f32_e32 v16, v16
	v_mul_f32_e32 v17, v97, v11
	v_mul_f32_e32 v20, v93, v11
	v_exp_f32_e32 v17, v17
	v_exp_f32_e32 v20, v20
	v_fmamk_f32 v15, v15, 0x3b808081, v227
	v_fmamk_f32 v16, v16, 0x3b808081, v227
	v_rcp_f32_e32 v15, v15
	v_rcp_f32_e32 v16, v16
	v_fmamk_f32 v17, v17, 0x3b808081, v227
	v_fmamk_f32 v20, v20, 0x3b808081, v227
	v_rcp_f32_e32 v17, v17
	v_rcp_f32_e32 v20, v20
	v_max_f32_e32 v15, 1.0, v15
	v_max_f32_e32 v16, 1.0, v16
	v_cvt_pk_u8_f32 v15, v15, 0, 0
	v_cvt_pk_u8_f32 v16, v16, 0, 0
	v_max_f32_e32 v17, 1.0, v17
	v_max_f32_e32 v20, 1.0, v20
	v_cvt_pk_u8_f32 v15, v17, 1, v15
	v_cvt_pk_u8_f32 v16, v20, 1, v16
	v_mul_f32_e32 v17, v98, v11
	v_mul_f32_e32 v20, v94, v11
	v_exp_f32_e32 v17, v17
	v_exp_f32_e32 v20, v20
	v_fmamk_f32 v17, v17, 0x3b808081, v227
	v_fmamk_f32 v20, v20, 0x3b808081, v227
	v_rcp_f32_e32 v17, v17
	v_rcp_f32_e32 v20, v20
	v_max_f32_e32 v17, 1.0, v17
	v_max_f32_e32 v20, 1.0, v20
	v_cvt_pk_u8_f32 v15, v17, 2, v15
	v_cvt_pk_u8_f32 v17, v20, 2, v16
	v_mul_f32_e32 v16, v99, v11
	v_mul_f32_e32 v20, v95, v11
	v_exp_f32_e32 v16, v16
	v_exp_f32_e32 v20, v20
	v_fmamk_f32 v16, v16, 0x3b808081, v227
	v_fmamk_f32 v20, v20, 0x3b808081, v227
	v_rcp_f32_e32 v16, v16
	v_rcp_f32_e32 v20, v20
	v_max_f32_e32 v16, 1.0, v16
	v_max_f32_e32 v20, 1.0, v20
	v_cvt_pk_u8_f32 v16, v16, 3, v15
	v_cvt_pk_u8_f32 v17, v20, 3, v17
	global_store_dwordx2 v[8:9], v[16:17], off
	v_mul_f32_e32 v15, v88, v11
	v_mul_f32_e32 v16, v84, v11
	v_exp_f32_e32 v15, v15
	v_exp_f32_e32 v16, v16
	v_mul_f32_e32 v17, v89, v11
	v_mul_f32_e32 v20, v85, v11
	v_exp_f32_e32 v17, v17
	v_exp_f32_e32 v20, v20
	v_fmamk_f32 v15, v15, 0x3b808081, v227
	v_fmamk_f32 v16, v16, 0x3b808081, v227
	v_rcp_f32_e32 v15, v15
	v_rcp_f32_e32 v16, v16
	v_fmamk_f32 v17, v17, 0x3b808081, v227
	v_fmamk_f32 v20, v20, 0x3b808081, v227
	v_rcp_f32_e32 v17, v17
	v_rcp_f32_e32 v20, v20
	v_max_f32_e32 v15, 1.0, v15
	v_max_f32_e32 v16, 1.0, v16
	v_cvt_pk_u8_f32 v15, v15, 0, 0
	v_cvt_pk_u8_f32 v16, v16, 0, 0
	v_max_f32_e32 v17, 1.0, v17
	v_max_f32_e32 v20, 1.0, v20
	v_cvt_pk_u8_f32 v15, v17, 1, v15
	v_cvt_pk_u8_f32 v16, v20, 1, v16
	v_mul_f32_e32 v17, v90, v11
	v_mul_f32_e32 v20, v86, v11
	v_exp_f32_e32 v17, v17
	v_exp_f32_e32 v20, v20
	v_fmamk_f32 v17, v17, 0x3b808081, v227
	v_fmamk_f32 v20, v20, 0x3b808081, v227
	v_rcp_f32_e32 v17, v17
	v_rcp_f32_e32 v20, v20
	v_max_f32_e32 v17, 1.0, v17
	v_max_f32_e32 v20, 1.0, v20
	v_cvt_pk_u8_f32 v15, v17, 2, v15
	v_cvt_pk_u8_f32 v17, v20, 2, v16
	v_mul_f32_e32 v16, v91, v11
	v_mul_f32_e32 v11, v87, v11
	v_exp_f32_e32 v11, v11
	v_exp_f32_e32 v16, v16
	v_fmamk_f32 v11, v11, 0x3b808081, v227
	v_fmamk_f32 v16, v16, 0x3b808081, v227
	v_rcp_f32_e32 v11, v11
	v_rcp_f32_e32 v16, v16
	v_max_f32_e32 v11, 1.0, v11
	v_max_f32_e32 v16, 1.0, v16
	v_cvt_pk_u8_f32 v17, v11, 3, v17
	v_mul_f32_e32 v11, 0x3c000000, v19
	v_cvt_pk_u8_f32 v16, v16, 3, v15
	v_mul_f32_e32 v11, 0xbfb8aa3b, v11
	global_store_dwordx2 v[8:9], v[16:17], off offset:128
	v_mul_f32_e32 v15, v80, v11
	v_mul_f32_e32 v16, v76, v11
	v_mad_i64_i32 v[8:9], s[20:21], v18, s13, v[6:7]
	v_exp_f32_e32 v15, v15
	v_exp_f32_e32 v16, v16
	v_mul_f32_e32 v17, v81, v11
	v_mul_f32_e32 v18, v77, v11
	v_exp_f32_e32 v17, v17
	v_exp_f32_e32 v18, v18
	v_fmamk_f32 v15, v15, 0x3b808081, v227
	v_fmamk_f32 v16, v16, 0x3b808081, v227
	v_rcp_f32_e32 v15, v15
	v_rcp_f32_e32 v16, v16
	v_fmamk_f32 v17, v17, 0x3b808081, v227
	v_fmamk_f32 v18, v18, 0x3b808081, v227
	v_rcp_f32_e32 v17, v17
	v_rcp_f32_e32 v18, v18
	v_max_f32_e32 v15, 1.0, v15
	v_max_f32_e32 v16, 1.0, v16
	v_cvt_pk_u8_f32 v15, v15, 0, 0
	v_cvt_pk_u8_f32 v16, v16, 0, 0
	v_max_f32_e32 v17, 1.0, v17
	v_max_f32_e32 v18, 1.0, v18
	v_cvt_pk_u8_f32 v15, v17, 1, v15
	v_cvt_pk_u8_f32 v16, v18, 1, v16
	v_mul_f32_e32 v17, v82, v11
	v_mul_f32_e32 v18, v78, v11
	v_exp_f32_e32 v17, v17
	v_exp_f32_e32 v18, v18
	v_lshl_add_u64 v[8:9], v[8:9], 0, v[4:5]
	v_fmamk_f32 v17, v17, 0x3b808081, v227
	v_fmamk_f32 v18, v18, 0x3b808081, v227
	v_rcp_f32_e32 v17, v17
	v_rcp_f32_e32 v18, v18
	v_max_f32_e32 v17, 1.0, v17
	v_max_f32_e32 v18, 1.0, v18
	v_cvt_pk_u8_f32 v15, v17, 2, v15
	v_cvt_pk_u8_f32 v17, v18, 2, v16
	v_mul_f32_e32 v16, v83, v11
	v_mul_f32_e32 v18, v79, v11
	v_exp_f32_e32 v16, v16
	v_exp_f32_e32 v18, v18
	v_fmamk_f32 v16, v16, 0x3b808081, v227
	v_fmamk_f32 v18, v18, 0x3b808081, v227
	v_rcp_f32_e32 v16, v16
	v_rcp_f32_e32 v18, v18
	v_max_f32_e32 v16, 1.0, v16
	v_max_f32_e32 v18, 1.0, v18
	v_cvt_pk_u8_f32 v16, v16, 3, v15
	v_cvt_pk_u8_f32 v17, v18, 3, v17
	global_store_dwordx2 v[8:9], v[16:17], off
	v_mul_f32_e32 v15, v72, v11
	v_mul_f32_e32 v16, v68, v11
	v_exp_f32_e32 v15, v15
	v_exp_f32_e32 v16, v16
	v_mul_f32_e32 v17, v73, v11
	v_mul_f32_e32 v18, v69, v11
	v_exp_f32_e32 v17, v17
	v_exp_f32_e32 v18, v18
	v_fmamk_f32 v15, v15, 0x3b808081, v227
	v_fmamk_f32 v16, v16, 0x3b808081, v227
	v_rcp_f32_e32 v15, v15
	v_rcp_f32_e32 v16, v16
	v_fmamk_f32 v17, v17, 0x3b808081, v227
	v_fmamk_f32 v18, v18, 0x3b808081, v227
	v_rcp_f32_e32 v17, v17
	v_rcp_f32_e32 v18, v18
	v_max_f32_e32 v15, 1.0, v15
	v_max_f32_e32 v16, 1.0, v16
	v_cvt_pk_u8_f32 v15, v15, 0, 0
	v_cvt_pk_u8_f32 v16, v16, 0, 0
	v_max_f32_e32 v17, 1.0, v17
	v_max_f32_e32 v18, 1.0, v18
	v_cvt_pk_u8_f32 v15, v17, 1, v15
	v_cvt_pk_u8_f32 v16, v18, 1, v16
	v_mul_f32_e32 v17, v74, v11
	v_mul_f32_e32 v18, v70, v11
	v_exp_f32_e32 v17, v17
	v_exp_f32_e32 v18, v18
	v_fmamk_f32 v17, v17, 0x3b808081, v227
	v_fmamk_f32 v18, v18, 0x3b808081, v227
	v_rcp_f32_e32 v17, v17
	v_rcp_f32_e32 v18, v18
	v_max_f32_e32 v17, 1.0, v17
	v_max_f32_e32 v18, 1.0, v18
	v_cvt_pk_u8_f32 v15, v17, 2, v15
	v_cvt_pk_u8_f32 v17, v18, 2, v16
	v_mul_f32_e32 v16, v75, v11
	v_mul_f32_e32 v11, v71, v11
	v_exp_f32_e32 v11, v11
	v_exp_f32_e32 v16, v16
	v_fmamk_f32 v11, v11, 0x3b808081, v227
	v_fmamk_f32 v16, v16, 0x3b808081, v227
	v_rcp_f32_e32 v11, v11
	v_rcp_f32_e32 v16, v16
	v_max_f32_e32 v11, 1.0, v11
	v_max_f32_e32 v16, 1.0, v16
	v_cvt_pk_u8_f32 v17, v11, 3, v17
	v_mul_f32_e32 v11, 0x3c000000, v13
	v_cvt_pk_u8_f32 v16, v16, 3, v15
	v_mul_f32_e32 v11, 0xbfb8aa3b, v11
	global_store_dwordx2 v[8:9], v[16:17], off offset:128
	v_mad_i64_i32 v[8:9], s[20:21], v14, s13, v[6:7]
	v_mul_f32_e32 v13, v64, v11
	v_mul_f32_e32 v14, v60, v11
	v_exp_f32_e32 v13, v13
	v_exp_f32_e32 v14, v14
	v_mul_f32_e32 v15, v65, v11
	v_mul_f32_e32 v16, v61, v11
	v_exp_f32_e32 v15, v15
	v_exp_f32_e32 v16, v16
	v_fmamk_f32 v13, v13, 0x3b808081, v227
	v_fmamk_f32 v14, v14, 0x3b808081, v227
	v_rcp_f32_e32 v13, v13
	v_rcp_f32_e32 v14, v14
	v_fmamk_f32 v15, v15, 0x3b808081, v227
	v_fmamk_f32 v16, v16, 0x3b808081, v227
	v_rcp_f32_e32 v15, v15
	v_rcp_f32_e32 v16, v16
	v_max_f32_e32 v13, 1.0, v13
	v_max_f32_e32 v14, 1.0, v14
	v_cvt_pk_u8_f32 v13, v13, 0, 0
	v_cvt_pk_u8_f32 v14, v14, 0, 0
	v_max_f32_e32 v15, 1.0, v15
	v_max_f32_e32 v16, 1.0, v16
	v_cvt_pk_u8_f32 v13, v15, 1, v13
	v_cvt_pk_u8_f32 v14, v16, 1, v14
	v_mul_f32_e32 v15, v66, v11
	v_mul_f32_e32 v16, v62, v11
	v_exp_f32_e32 v15, v15
	v_exp_f32_e32 v16, v16
	v_lshl_add_u64 v[8:9], v[8:9], 0, v[4:5]
	v_mad_i64_i32 v[6:7], s[20:21], v12, s13, v[6:7]
	v_fmamk_f32 v15, v15, 0x3b808081, v227
	v_fmamk_f32 v16, v16, 0x3b808081, v227
	v_rcp_f32_e32 v15, v15
	v_rcp_f32_e32 v16, v16
	v_lshl_add_u64 v[4:5], v[6:7], 0, v[4:5]
	v_mul_f32_e32 v6, 0x3c000000, v10
	v_max_f32_e32 v15, 1.0, v15
	v_max_f32_e32 v16, 1.0, v16
	v_cvt_pk_u8_f32 v13, v15, 2, v13
	v_cvt_pk_u8_f32 v15, v16, 2, v14
	v_mul_f32_e32 v14, v67, v11
	v_mul_f32_e32 v16, v63, v11
	v_exp_f32_e32 v14, v14
	v_exp_f32_e32 v16, v16
	s_mov_b64 s[20:21], -1
	v_fmamk_f32 v14, v14, 0x3b808081, v227
	v_fmamk_f32 v16, v16, 0x3b808081, v227
	v_rcp_f32_e32 v14, v14
	v_rcp_f32_e32 v16, v16
	v_max_f32_e32 v14, 1.0, v14
	v_max_f32_e32 v16, 1.0, v16
	v_cvt_pk_u8_f32 v14, v14, 3, v13
	v_cvt_pk_u8_f32 v15, v16, 3, v15
	global_store_dwordx2 v[8:9], v[14:15], off
	v_mul_f32_e32 v13, v56, v11
	v_mul_f32_e32 v14, v52, v11
	v_exp_f32_e32 v13, v13
	v_exp_f32_e32 v14, v14
	v_mul_f32_e32 v15, v57, v11
	v_mul_f32_e32 v16, v53, v11
	v_exp_f32_e32 v15, v15
	v_exp_f32_e32 v16, v16
	v_fmamk_f32 v13, v13, 0x3b808081, v227
	v_fmamk_f32 v14, v14, 0x3b808081, v227
	v_rcp_f32_e32 v13, v13
	v_rcp_f32_e32 v14, v14
	v_fmamk_f32 v15, v15, 0x3b808081, v227
	v_fmamk_f32 v16, v16, 0x3b808081, v227
	v_rcp_f32_e32 v15, v15
	v_rcp_f32_e32 v16, v16
	v_max_f32_e32 v13, 1.0, v13
	v_max_f32_e32 v14, 1.0, v14
	v_cvt_pk_u8_f32 v13, v13, 0, 0
	v_cvt_pk_u8_f32 v14, v14, 0, 0
	v_max_f32_e32 v15, 1.0, v15
	v_max_f32_e32 v16, 1.0, v16
	v_cvt_pk_u8_f32 v13, v15, 1, v13
	v_cvt_pk_u8_f32 v14, v16, 1, v14
	v_mul_f32_e32 v15, v58, v11
	v_mul_f32_e32 v16, v54, v11
	v_exp_f32_e32 v15, v15
	v_exp_f32_e32 v16, v16
	v_fmamk_f32 v15, v15, 0x3b808081, v227
	v_fmamk_f32 v16, v16, 0x3b808081, v227
	v_rcp_f32_e32 v15, v15
	v_rcp_f32_e32 v16, v16
	v_max_f32_e32 v15, 1.0, v15
	v_max_f32_e32 v16, 1.0, v16
	v_cvt_pk_u8_f32 v13, v15, 2, v13
	v_cvt_pk_u8_f32 v15, v16, 2, v14
	v_mul_f32_e32 v14, v59, v11
	v_mul_f32_e32 v11, v55, v11
	v_exp_f32_e32 v14, v14
	v_exp_f32_e32 v11, v11
	v_fmamk_f32 v14, v14, 0x3b808081, v227
	v_fmamk_f32 v11, v11, 0x3b808081, v227
	v_rcp_f32_e32 v14, v14
	v_rcp_f32_e32 v11, v11
	v_max_f32_e32 v14, 1.0, v14
	v_max_f32_e32 v11, 1.0, v11
	v_cvt_pk_u8_f32 v14, v14, 3, v13
	v_cvt_pk_u8_f32 v15, v11, 3, v15
	global_store_dwordx2 v[8:9], v[14:15], off offset:128
	v_mul_f32_e32 v8, 0xbfb8aa3b, v6
	v_mul_f32_e32 v6, v48, v8
	v_mul_f32_e32 v7, v44, v8
	v_exp_f32_e32 v6, v6
	v_exp_f32_e32 v7, v7
	v_mul_f32_e32 v9, v49, v8
	v_mul_f32_e32 v10, v45, v8
	v_exp_f32_e32 v9, v9
	v_exp_f32_e32 v10, v10
	v_fmamk_f32 v6, v6, 0x3b808081, v227
	v_fmamk_f32 v7, v7, 0x3b808081, v227
	v_rcp_f32_e32 v6, v6
	v_rcp_f32_e32 v7, v7
	v_fmamk_f32 v9, v9, 0x3b808081, v227
	v_fmamk_f32 v10, v10, 0x3b808081, v227
	v_rcp_f32_e32 v9, v9
	v_rcp_f32_e32 v10, v10
	v_max_f32_e32 v6, 1.0, v6
	v_max_f32_e32 v7, 1.0, v7
	v_cvt_pk_u8_f32 v6, v6, 0, 0
	v_cvt_pk_u8_f32 v7, v7, 0, 0
	v_max_f32_e32 v9, 1.0, v9
	v_max_f32_e32 v10, 1.0, v10
	v_cvt_pk_u8_f32 v6, v9, 1, v6
	v_cvt_pk_u8_f32 v7, v10, 1, v7
	v_mul_f32_e32 v9, v50, v8
	v_mul_f32_e32 v10, v46, v8
	v_exp_f32_e32 v9, v9
	v_exp_f32_e32 v10, v10
	v_fmamk_f32 v9, v9, 0x3b808081, v227
	v_fmamk_f32 v10, v10, 0x3b808081, v227
	v_rcp_f32_e32 v9, v9
	v_rcp_f32_e32 v10, v10
	v_max_f32_e32 v9, 1.0, v9
	v_max_f32_e32 v10, 1.0, v10
	v_cvt_pk_u8_f32 v6, v9, 2, v6
	v_cvt_pk_u8_f32 v7, v10, 2, v7
	v_mul_f32_e32 v9, v51, v8
	v_mul_f32_e32 v10, v47, v8
	v_exp_f32_e32 v9, v9
	v_exp_f32_e32 v10, v10
	v_fmamk_f32 v9, v9, 0x3b808081, v227
	v_fmamk_f32 v10, v10, 0x3b808081, v227
	v_rcp_f32_e32 v9, v9
	v_rcp_f32_e32 v10, v10
	v_max_f32_e32 v9, 1.0, v9
	v_max_f32_e32 v10, 1.0, v10
	v_cvt_pk_u8_f32 v6, v9, 3, v6
	v_cvt_pk_u8_f32 v7, v10, 3, v7
	global_store_dwordx2 v[4:5], v[6:7], off
	v_mul_f32_e32 v6, v40, v8
	v_exp_f32_e32 v6, v6
	v_mul_f32_e32 v9, v41, v8
	v_exp_f32_e32 v9, v9
	v_mul_f32_e32 v7, v36, v8
	v_fmamk_f32 v6, v6, 0x3b808081, v227
	v_rcp_f32_e32 v6, v6
	v_fmamk_f32 v9, v9, 0x3b808081, v227
	v_rcp_f32_e32 v9, v9
	v_exp_f32_e32 v7, v7
	v_max_f32_e32 v6, 1.0, v6
	v_cvt_pk_u8_f32 v6, v6, 0, 0
	v_max_f32_e32 v9, 1.0, v9
	v_mul_f32_e32 v10, v37, v8
	v_exp_f32_e32 v10, v10
	v_cvt_pk_u8_f32 v6, v9, 1, v6
	v_mul_f32_e32 v9, v42, v8
	v_exp_f32_e32 v9, v9
	v_fmamk_f32 v7, v7, 0x3b808081, v227
	v_rcp_f32_e32 v7, v7
	v_fmamk_f32 v10, v10, 0x3b808081, v227
	v_rcp_f32_e32 v10, v10
	v_fmamk_f32 v9, v9, 0x3b808081, v227
	v_rcp_f32_e32 v9, v9
	v_max_f32_e32 v7, 1.0, v7
	v_cvt_pk_u8_f32 v7, v7, 0, 0
	v_max_f32_e32 v10, 1.0, v10
	v_cvt_pk_u8_f32 v7, v10, 1, v7
	v_max_f32_e32 v9, 1.0, v9
	v_mul_f32_e32 v10, v38, v8
	v_exp_f32_e32 v10, v10
	v_cvt_pk_u8_f32 v6, v9, 2, v6
	v_mul_f32_e32 v9, v43, v8
	v_mul_f32_e32 v8, v39, v8
	v_exp_f32_e32 v9, v9
	v_exp_f32_e32 v8, v8
	v_fmamk_f32 v10, v10, 0x3b808081, v227
	v_rcp_f32_e32 v10, v10
	v_fmamk_f32 v9, v9, 0x3b808081, v227
	v_fmamk_f32 v8, v8, 0x3b808081, v227
	v_rcp_f32_e32 v9, v9
	v_rcp_f32_e32 v8, v8
	v_max_f32_e32 v10, 1.0, v10
	v_cvt_pk_u8_f32 v7, v10, 2, v7
	v_max_f32_e32 v9, 1.0, v9
	v_max_f32_e32 v8, 1.0, v8
	v_cvt_pk_u8_f32 v6, v9, 3, v6
	v_cvt_pk_u8_f32 v7, v8, 3, v7
	global_store_dwordx2 v[4:5], v[6:7], off offset:128
	s_cbranch_vccnz .LBB0_167
	s_andn2_b64 vcc, exec, s[0:1]
	s_cbranch_vccnz .LBB0_166
	s_barrier
	s_branch .LBB0_166

.LBB0_194:
	v_lshl_add_u32 v146, s18, 8, v151
	v_ashrrev_i32_e32 v147, 31, v146
	v_lshl_add_u64 v[148:149], v[146:147], 2, s[4:5]
	global_load_dword v156, v[148:149], off offset:64
	global_load_dword v152, v[148:149], off offset:128
	global_load_dword v150, v[148:149], off offset:192
	global_load_dword v160, v[148:149], off
	v_lshl_or_b32 v144, s19, 8, v153
	v_ashrrev_i32_e32 v145, 31, v144
	v_mov_b64_e32 v[142:143], s[6:7]
	s_movk_i32 s24, 0x7200
	v_mad_i64_i32 v[158:159], s[18:19], v146, s24, v[142:143]
	v_lshlrev_b64 v[144:145], 1, v[144:145]
	v_lshl_add_u64 v[158:159], v[158:159], 0, v[144:145]
	s_andn2_b64 vcc, exec, s[36:37]
	s_mov_b32 s25, 0x800000
	s_waitcnt vmcnt(0) lgkmcnt(0)
	v_pk_mul_f32 v[114:115], v[114:115], v[156:157] op_sel_hi:[1,0]
	v_pk_mul_f32 v[106:107], v[106:107], v[156:157] op_sel_hi:[1,0]
	v_pk_mul_f32 v[98:99], v[98:99], v[152:153] op_sel_hi:[1,0]
	v_pk_mul_f32 v[162:163], v[126:127], v[160:161] op_sel_hi:[1,0]
	v_pk_mul_f32 v[126:127], v[124:125], v[160:161] op_sel_hi:[1,0]
	v_pk_mul_f32 v[130:131], v[130:131], v[160:161] op_sel_hi:[1,0]
	v_pk_mul_f32 v[124:125], v[128:129], v[160:161] op_sel_hi:[1,0]
	v_cvt_pk_bf16_f32 v126, v126, v127
	v_cvt_pk_bf16_f32 v124, v124, v125
	v_cvt_pk_bf16_f32 v125, v130, v131
	v_cvt_pk_bf16_f32 v127, v162, v163
	global_store_dwordx4 v[158:159], v[124:127], off
	v_pk_mul_f32 v[122:123], v[122:123], v[160:161] op_sel_hi:[1,0]
	v_pk_mul_f32 v[90:91], v[90:91], v[152:153] op_sel_hi:[1,0]
	v_pk_mul_f32 v[124:125], v[118:119], v[160:161] op_sel_hi:[1,0]
	v_pk_mul_f32 v[118:119], v[116:117], v[160:161] op_sel_hi:[1,0]
	v_pk_mul_f32 v[116:117], v[120:121], v[160:161] op_sel_hi:[1,0]
	v_cvt_pk_bf16_f32 v118, v118, v119
	v_cvt_pk_bf16_f32 v116, v116, v117
	v_cvt_pk_bf16_f32 v117, v122, v123
	v_cvt_pk_bf16_f32 v119, v124, v125
	global_store_dwordx4 v[158:159], v[116:119], off offset:256
	v_pk_mul_f32 v[82:83], v[82:83], v[150:151] op_sel_hi:[1,0]
	v_pk_mul_f32 v[74:75], v[74:75], v[150:151] op_sel_hi:[1,0]
	v_or_b32_e32 v116, 16, v146
	v_mad_i64_i32 v[116:117], s[18:19], v116, s24, v[142:143]
	v_pk_mul_f32 v[118:119], v[110:111], v[156:157] op_sel_hi:[1,0]
	v_pk_mul_f32 v[110:111], v[108:109], v[156:157] op_sel_hi:[1,0]
	v_pk_mul_f32 v[108:109], v[112:113], v[156:157] op_sel_hi:[1,0]
	v_lshl_add_u64 v[116:117], v[116:117], 0, v[144:145]
	v_cvt_pk_bf16_f32 v108, v108, v109
	v_cvt_pk_bf16_f32 v109, v114, v115
	v_cvt_pk_bf16_f32 v110, v110, v111
	v_cvt_pk_bf16_f32 v111, v118, v119
	global_store_dwordx4 v[116:117], v[108:111], off
	s_nop 1
	v_pk_mul_f32 v[108:109], v[102:103], v[156:157] op_sel_hi:[1,0]
	v_pk_mul_f32 v[102:103], v[100:101], v[156:157] op_sel_hi:[1,0]
	v_pk_mul_f32 v[100:101], v[104:105], v[156:157] op_sel_hi:[1,0]
	v_cvt_pk_bf16_f32 v102, v102, v103
	v_cvt_pk_bf16_f32 v100, v100, v101
	v_cvt_pk_bf16_f32 v101, v106, v107
	v_cvt_pk_bf16_f32 v103, v108, v109
	global_store_dwordx4 v[116:117], v[100:103], off offset:256
	s_nop 1
	v_or_b32_e32 v100, 32, v146
	v_mad_i64_i32 v[100:101], s[18:19], v100, s24, v[142:143]
	v_pk_mul_f32 v[102:103], v[94:95], v[152:153] op_sel_hi:[1,0]
	v_pk_mul_f32 v[94:95], v[92:93], v[152:153] op_sel_hi:[1,0]
	v_pk_mul_f32 v[92:93], v[96:97], v[152:153] op_sel_hi:[1,0]
	v_lshl_add_u64 v[100:101], v[100:101], 0, v[144:145]
	v_cvt_pk_bf16_f32 v92, v92, v93
	v_cvt_pk_bf16_f32 v93, v98, v99
	v_cvt_pk_bf16_f32 v94, v94, v95
	v_cvt_pk_bf16_f32 v95, v102, v103
	global_store_dwordx4 v[100:101], v[92:95], off
	s_nop 1
	v_pk_mul_f32 v[92:93], v[86:87], v[152:153] op_sel_hi:[1,0]
	v_pk_mul_f32 v[86:87], v[84:85], v[152:153] op_sel_hi:[1,0]
	v_pk_mul_f32 v[84:85], v[88:89], v[152:153] op_sel_hi:[1,0]
	v_cvt_pk_bf16_f32 v86, v86, v87
	v_cvt_pk_bf16_f32 v84, v84, v85
	v_cvt_pk_bf16_f32 v85, v90, v91
	v_cvt_pk_bf16_f32 v87, v92, v93
	global_store_dwordx4 v[100:101], v[84:87], off offset:256
	s_nop 1
	v_or_b32_e32 v84, 48, v146
	v_mad_i64_i32 v[84:85], s[18:19], v84, s24, v[142:143]
	v_pk_mul_f32 v[86:87], v[78:79], v[150:151] op_sel_hi:[1,0]
	v_pk_mul_f32 v[78:79], v[76:77], v[150:151] op_sel_hi:[1,0]
	v_pk_mul_f32 v[76:77], v[80:81], v[150:151] op_sel_hi:[1,0]
	v_lshl_add_u64 v[84:85], v[84:85], 0, v[144:145]
	v_cvt_pk_bf16_f32 v76, v76, v77
	v_cvt_pk_bf16_f32 v77, v82, v83
	v_cvt_pk_bf16_f32 v78, v78, v79
	v_cvt_pk_bf16_f32 v79, v86, v87
	global_store_dwordx4 v[84:85], v[76:79], off
	s_nop 1
	v_pk_mul_f32 v[76:77], v[70:71], v[150:151] op_sel_hi:[1,0]
	v_pk_mul_f32 v[70:71], v[68:69], v[150:151] op_sel_hi:[1,0]
	v_pk_mul_f32 v[68:69], v[72:73], v[150:151] op_sel_hi:[1,0]
	v_cvt_pk_bf16_f32 v70, v70, v71
	v_cvt_pk_bf16_f32 v68, v68, v69
	v_cvt_pk_bf16_f32 v69, v74, v75
	v_cvt_pk_bf16_f32 v71, v76, v77
	global_store_dwordx4 v[84:85], v[68:71], off offset:256
	global_load_dword v72, v[148:149], off offset:576
	s_nop 0
	global_load_dword v70, v[148:149], off offset:640
	global_load_dword v68, v[148:149], off offset:704
	global_load_dword v76, v[148:149], off offset:512
	v_add_u32_e32 v69, 0x80, v146
	v_mad_i64_i32 v[74:75], s[18:19], v69, s24, v[142:143]
	v_lshl_add_u64 v[74:75], v[74:75], 0, v[144:145]
	s_waitcnt vmcnt(0) lgkmcnt(0)
	v_pk_mul_f32 v[50:51], v[50:51], v[72:73] op_sel_hi:[1,0]
	v_pk_mul_f32 v[42:43], v[42:43], v[72:73] op_sel_hi:[1,0]
	v_pk_mul_f32 v[34:35], v[34:35], v[70:71] op_sel_hi:[1,0]
	v_pk_mul_f32 v[78:79], v[62:63], v[76:77] op_sel_hi:[1,0]
	v_pk_mul_f32 v[62:63], v[60:61], v[76:77] op_sel_hi:[1,0]
	v_pk_mul_f32 v[66:67], v[66:67], v[76:77] op_sel_hi:[1,0]
	v_pk_mul_f32 v[60:61], v[64:65], v[76:77] op_sel_hi:[1,0]
	v_cvt_pk_bf16_f32 v62, v62, v63
	v_cvt_pk_bf16_f32 v60, v60, v61
	v_cvt_pk_bf16_f32 v61, v66, v67
	v_cvt_pk_bf16_f32 v63, v78, v79
	global_store_dwordx4 v[74:75], v[60:63], off
	v_pk_mul_f32 v[58:59], v[58:59], v[76:77] op_sel_hi:[1,0]
	v_pk_mul_f32 v[26:27], v[26:27], v[70:71] op_sel_hi:[1,0]
	v_pk_mul_f32 v[60:61], v[54:55], v[76:77] op_sel_hi:[1,0]
	v_pk_mul_f32 v[54:55], v[52:53], v[76:77] op_sel_hi:[1,0]
	v_pk_mul_f32 v[52:53], v[56:57], v[76:77] op_sel_hi:[1,0]
	v_cvt_pk_bf16_f32 v54, v54, v55
	v_cvt_pk_bf16_f32 v52, v52, v53
	v_cvt_pk_bf16_f32 v53, v58, v59
	v_cvt_pk_bf16_f32 v55, v60, v61
	global_store_dwordx4 v[74:75], v[52:55], off offset:256
	v_pk_mul_f32 v[18:19], v[18:19], v[68:69] op_sel_hi:[1,0]
	v_pk_mul_f32 v[10:11], v[10:11], v[68:69] op_sel_hi:[1,0]
	v_add_u32_e32 v52, 0x90, v146
	v_mad_i64_i32 v[52:53], s[18:19], v52, s24, v[142:143]
	v_pk_mul_f32 v[54:55], v[46:47], v[72:73] op_sel_hi:[1,0]
	v_pk_mul_f32 v[46:47], v[44:45], v[72:73] op_sel_hi:[1,0]
	v_pk_mul_f32 v[44:45], v[48:49], v[72:73] op_sel_hi:[1,0]
	v_lshl_add_u64 v[52:53], v[52:53], 0, v[144:145]
	v_cvt_pk_bf16_f32 v44, v44, v45
	v_cvt_pk_bf16_f32 v45, v50, v51
	v_cvt_pk_bf16_f32 v46, v46, v47
	v_cvt_pk_bf16_f32 v47, v54, v55
	global_store_dwordx4 v[52:53], v[44:47], off
	s_nop 1
	v_pk_mul_f32 v[44:45], v[38:39], v[72:73] op_sel_hi:[1,0]
	v_pk_mul_f32 v[38:39], v[36:37], v[72:73] op_sel_hi:[1,0]
	v_pk_mul_f32 v[36:37], v[40:41], v[72:73] op_sel_hi:[1,0]
	v_cvt_pk_bf16_f32 v38, v38, v39
	v_cvt_pk_bf16_f32 v36, v36, v37
	v_cvt_pk_bf16_f32 v37, v42, v43
	v_cvt_pk_bf16_f32 v39, v44, v45
	global_store_dwordx4 v[52:53], v[36:39], off offset:256
	s_nop 1
	v_add_u32_e32 v36, 0xa0, v146
	v_mad_i64_i32 v[36:37], s[18:19], v36, s24, v[142:143]
	v_pk_mul_f32 v[38:39], v[30:31], v[70:71] op_sel_hi:[1,0]
	v_pk_mul_f32 v[30:31], v[28:29], v[70:71] op_sel_hi:[1,0]
	v_pk_mul_f32 v[28:29], v[32:33], v[70:71] op_sel_hi:[1,0]
	v_lshl_add_u64 v[36:37], v[36:37], 0, v[144:145]
	v_cvt_pk_bf16_f32 v28, v28, v29
	v_cvt_pk_bf16_f32 v29, v34, v35
	v_cvt_pk_bf16_f32 v30, v30, v31
	v_cvt_pk_bf16_f32 v31, v38, v39
	global_store_dwordx4 v[36:37], v[28:31], off
	s_nop 1
	v_pk_mul_f32 v[28:29], v[22:23], v[70:71] op_sel_hi:[1,0]
	v_pk_mul_f32 v[22:23], v[20:21], v[70:71] op_sel_hi:[1,0]
	v_pk_mul_f32 v[20:21], v[24:25], v[70:71] op_sel_hi:[1,0]
	v_cvt_pk_bf16_f32 v22, v22, v23
	v_cvt_pk_bf16_f32 v20, v20, v21
	v_cvt_pk_bf16_f32 v21, v26, v27
	v_cvt_pk_bf16_f32 v23, v28, v29
	global_store_dwordx4 v[36:37], v[20:23], off offset:256
	s_nop 1
	v_add_u32_e32 v20, 0xb0, v146
	v_mad_i64_i32 v[20:21], s[18:19], v20, s24, v[142:143]
	v_pk_mul_f32 v[22:23], v[14:15], v[68:69] op_sel_hi:[1,0]
	v_pk_mul_f32 v[14:15], v[12:13], v[68:69] op_sel_hi:[1,0]
	v_pk_mul_f32 v[12:13], v[16:17], v[68:69] op_sel_hi:[1,0]
	v_lshl_add_u64 v[20:21], v[20:21], 0, v[144:145]
	v_cvt_pk_bf16_f32 v12, v12, v13
	v_cvt_pk_bf16_f32 v13, v18, v19
	v_cvt_pk_bf16_f32 v14, v14, v15
	v_cvt_pk_bf16_f32 v15, v22, v23
	global_store_dwordx4 v[20:21], v[12:15], off
	s_mov_b64 s[18:19], -1
	s_nop 0
	v_pk_mul_f32 v[12:13], v[6:7], v[68:69] op_sel_hi:[1,0]
	v_pk_mul_f32 v[6:7], v[4:5], v[68:69] op_sel_hi:[1,0]
	v_pk_mul_f32 v[4:5], v[8:9], v[68:69] op_sel_hi:[1,0]
	v_cvt_pk_bf16_f32 v6, v6, v7
	v_cvt_pk_bf16_f32 v4, v4, v5
	v_cvt_pk_bf16_f32 v5, v10, v11
	v_cvt_pk_bf16_f32 v7, v12, v13
	global_store_dwordx4 v[20:21], v[4:7], off offset:256
	s_cbranch_vccnz .LBB0_187
	s_andn2_b64 vcc, exec, s[0:1]
	s_cbranch_vccnz .LBB0_186
	s_barrier
	s_branch .LBB0_186

.LBB0_257:
	s_waitcnt lgkmcnt(0)
	s_barrier
	s_and_saveexec_b64 s[0:1], s[36:37]
	s_cbranch_execz .LBB0_259
	v_mov_b64_e32 v[4:5], s[8:9]
	s_waitcnt vmcnt(0)
	global_atomic_add v1, v[4:5], v228, off sc0
	v_mov_b32_e32 v2, s23
	s_waitcnt vmcnt(0) lgkmcnt(0)
	ds_write_b32 v2, v1

.LBB0_262:
	s_lshl_b32 s14, s16, 4
	s_lshl_b32 s18, s16, 6
	s_and_b32 s14, s14, 0xfffff000
	s_and_b32 s18, s18, 0xfc0
	v_and_b32_e32 v22, 63, v20
	s_bfe_u32 s17, s16, 0x20006
	s_andn2_b64 vcc, exec, s[4:5]
	s_or_b32 s14, s14, s18
	s_cbranch_vccnz .LBB0_264
	v_or_b32_e32 v1, s14, v22
	v_mov_b64_e32 v[4:5], s[0:1]
	v_mad_i64_i32 v[4:5], s[4:5], v1, s45, v[4:5]
	v_readlane_b32 s44, v253, 17
	v_readlane_b32 s45, v253, 18
	s_lshl_b32 s44, s17, 1
	v_mov_b32_e32 v1, s30
	v_lshl_add_u64 v[8:9], v[4:5], 0, s[44:45]
	ds_read2_b64 v[4:7], v1 offset1:1
	s_mov_b32 s5, s45
	v_readlane_b32 s46, v253, 19
	v_readlane_b32 s47, v253, 20
	v_writelane_b32 v253, s4, 17
	v_add_co_u32_e32 v8, vcc, 0x3000, v8
	s_nop 0
	v_writelane_b32 v253, s5, 18
	s_or_b32 s44, s17, s22
	v_writelane_b32 v253, s6, 19
	v_addc_co_u32_e32 v9, vcc, 0, v9, vcc
	v_writelane_b32 v253, s7, 20
	s_lshl_b64 s[4:5], s[44:45], 2
	global_load_ushort v1, v[8:9], off offset:432
	s_waitcnt lgkmcnt(0)
	v_lshl_add_u64 v[6:7], v[6:7], 0, s[4:5]
	global_load_dword v2, v[6:7], off
	v_lshl_add_u64 v[4:5], v[4:5], 0, s[4:5]
	global_load_dword v4, v[4:5], off
	s_nop 0
	global_load_ushort v5, v[8:9], off offset:424
	v_mbcnt_hi_u32_b32 v27, -1, v251
	v_and_b32_e32 v33, 64, v27
	v_add_u32_e32 v6, -1, v27
	v_cmp_lt_i32_e32 vcc, v6, v33
	s_mov_b32 s4, 0x3f317217
	v_add_u32_e32 v7, -2, v27
	v_cndmask_b32_e32 v6, v6, v27, vcc
	v_lshlrev_b32_e32 v6, 2, v6
	v_add_u32_e32 v8, -4, v27
	s_waitcnt vmcnt(0)
	v_lshlrev_b32_e32 v1, 16, v1
	s_waitcnt lgkmcnt(0)
	v_add_f32_e32 v1, v2, v1
	v_mul_f32_e32 v2, 0x3fb8aa3b, v1
	v_exp_f32_e32 v2, v2
	v_mul_f32_e32 v4, 0x3fb8aa3b, v4
	v_exp_f32_e32 v4, v4
	v_lshlrev_b32_e32 v5, 16, v5
	v_add_f32_e32 v2, 1.0, v2
	v_cmp_gt_f32_e32 vcc, s43, v2
	v_mul_f32_e32 v5, 0xbfb8aa3b, v5
	v_exp_f32_e32 v5, v5
	v_cndmask_b32_e64 v9, 0, 32, vcc
	v_ldexp_f32 v2, v2, v9
	v_log_f32_e32 v2, v2
	v_mov_b32_e32 v9, 0x41b17218
	v_cndmask_b32_e32 v9, 0, v9, vcc
	v_add_f32_e32 v5, 1.0, v5
	v_mul_f32_e32 v10, 0x3f317217, v2
	v_fma_f32 v10, v2, s4, -v10
	v_fmac_f32_e32 v10, 0x3377d1cf, v2
	s_mov_b32 s4, 0x7f800000
	v_fmac_f32_e32 v10, 0x3f317217, v2
	v_cmp_lt_f32_e64 vcc, |v2|, s4
	s_mov_b32 s4, 0x41a00000
	v_rcp_f32_e32 v5, v5
	v_cndmask_b32_e32 v2, v2, v10, vcc
	v_sub_f32_e32 v2, v2, v9
	v_cmp_lt_f32_e32 vcc, s4, v1
	v_add_u32_e32 v9, -8, v27
	s_nop 0
	v_cndmask_b32_e32 v1, v2, v1, vcc
	v_mul_f32_e64 v2, v1, -v4
	ds_bpermute_b32 v6, v6, v2
	v_cmp_lt_i32_e32 vcc, v7, v33
	s_waitcnt lgkmcnt(0)
	v_fma_f32 v1, v1, -v4, v6
	v_cndmask_b32_e32 v7, v7, v27, vcc
	v_cmp_eq_u32_e32 vcc, 0, v22
	v_lshlrev_b32_e32 v7, 2, v7
	v_add_u32_e32 v4, -16, v27
	v_cndmask_b32_e32 v1, v1, v2, vcc
	ds_bpermute_b32 v2, v7, v1
	v_cmp_lt_i32_e32 vcc, v8, v33
	s_waitcnt lgkmcnt(0)
	v_add_f32_e32 v2, v1, v2
	v_cndmask_b32_e32 v6, v8, v27, vcc
	v_cmp_gt_u32_e32 vcc, 2, v22
	v_lshlrev_b32_e32 v6, 2, v6
	s_nop 0
	v_cndmask_b32_e32 v1, v2, v1, vcc
	ds_bpermute_b32 v2, v6, v1
	v_cmp_lt_i32_e32 vcc, v9, v33
	v_subrev_u32_e32 v6, 32, v27
	s_waitcnt lgkmcnt(0)
	v_add_f32_e32 v2, v1, v2
	v_cndmask_b32_e32 v7, v9, v27, vcc
	v_cmp_gt_u32_e32 vcc, 4, v22
	v_lshlrev_b32_e32 v7, 2, v7
	s_nop 0
	v_cndmask_b32_e32 v1, v2, v1, vcc
	ds_bpermute_b32 v2, v7, v1
	v_cmp_lt_i32_e32 vcc, v4, v33
	s_waitcnt lgkmcnt(0)
	v_add_f32_e32 v2, v1, v2
	v_cndmask_b32_e32 v4, v4, v27, vcc
	v_cmp_lt_i32_e32 vcc, v6, v33
	v_lshlrev_b32_e32 v4, 2, v4
	s_nop 0
	v_cndmask_b32_e32 v6, v6, v27, vcc
	v_cmp_gt_u32_e32 vcc, 8, v22
	s_nop 1
	v_cndmask_b32_e32 v1, v2, v1, vcc
	ds_bpermute_b32 v2, v4, v1
	v_cmp_gt_u32_e32 vcc, 16, v22
	v_lshlrev_b32_e32 v4, 2, v6
	s_waitcnt lgkmcnt(0)
	v_add_f32_e32 v2, v1, v2
	v_cndmask_b32_e32 v1, v2, v1, vcc
	ds_bpermute_b32 v2, v4, v1
	v_cmp_gt_u32_e32 vcc, 32, v22
	v_lshlrev_b32_e32 v4, 2, v22
	v_add_u32_e32 v6, s27, v4
	ds_write_b32 v6, v5
	s_waitcnt lgkmcnt(1)
	v_add_f32_e32 v2, v1, v2
	v_cndmask_b32_e32 v1, v2, v1, vcc
	v_mul_f32_e32 v2, 0x3fb8aa3b, v1
	v_exp_f32_e32 v2, v2
	v_add_u32_e32 v5, s28, v4
	ds_write_b32 v5, v1
	v_add_u32_e32 v1, s29, v4
	ds_write_b32 v1, v2
.LBB0_264:
	v_mov_b32_e32 v1, s31
	ds_read_b64 v[4:5], v1
	v_ashrrev_i32_e32 v1, 3, v20
	v_add_u32_e32 v32, s18, v1
	v_lshlrev_b32_e32 v2, 4, v20
	v_cmp_lt_i32_e32 vcc, 2, v32
	v_and_b32_e32 v23, 0x70, v2
	v_add_u32_e32 v36, s14, v1
	v_cndmask_b32_e64 v2, 0, -3, vcc
	s_waitcnt lgkmcnt(0)
	v_lshl_add_u64 v[30:31], v[4:5], 0, s[10:11]
	v_add_u32_e32 v2, v2, v36
	v_mov_b64_e32 v[4:5], s[0:1]
	s_movk_i32 s18, 0x7200
	v_mad_i64_i32 v[6:7], s[0:1], v2, s18, v[4:5]
	v_cmp_lt_i32_e64 s[0:1], 1, v32
	s_lshl_b32 s35, s17, 7
	s_mov_b64 s[38:39], 0x1c00
	v_cndmask_b32_e64 v2, 0, -2, s[0:1]
	v_add_u32_e32 v2, v2, v36
	v_or_b32_e32 v21, s35, v23
	v_lshl_add_u64 v[24:25], v[6:7], 0, s[38:39]
	v_mad_i64_i32 v[6:7], s[4:5], v2, s18, v[4:5]
	v_lshlrev_b32_e32 v2, 2, v21
	v_lshl_add_u64 v[42:43], v[30:31], 0, v[2:3]
	s_movk_i32 s21, 0x1000
	v_add_co_u32_e64 v8, s[4:5], s21, v42
	s_movk_i32 s19, 0x3000
	s_nop 0
	v_addc_co_u32_e64 v9, s[4:5], 0, v43, s[4:5]
	v_add_co_u32_e64 v44, s[4:5], s19, v42
	s_movk_i32 s17, 0x4000
	s_nop 0
	v_addc_co_u32_e64 v45, s[4:5], 0, v43, s[4:5]
	v_add_co_u32_e64 v10, s[4:5], s17, v42
	v_lshl_add_u64 v[28:29], v[6:7], 0, s[38:39]
	s_nop 0
	v_addc_co_u32_e64 v11, s[4:5], 0, v43, s[4:5]
	v_cmp_lt_i32_e64 s[4:5], 0, v32
	global_load_dwordx4 v[46:49], v[42:43], off
	global_load_dwordx4 v[50:53], v[8:9], off offset:2048
	v_cndmask_b32_e64 v26, 0, 1.0, s[4:5]
	v_subbrev_co_u32_e64 v2, s[4:5], 0, v36, s[4:5]
	v_mad_i64_i32 v[6:7], s[4:5], v2, s18, v[4:5]
	v_lshlrev_b32_e32 v2, 1, v21
	global_load_dwordx4 v[54:57], v[42:43], off offset:16
	global_load_dwordx4 v[58:61], v[44:45], off
	global_load_dwordx4 v[62:65], v[10:11], off offset:2048
	global_load_dwordx4 v[66:69], v[8:9], off offset:2064
	global_load_dwordx4 v[70:73], v[44:45], off offset:16
	global_load_dwordx4 v[74:77], v[10:11], off offset:2064
	global_load_dwordx4 v[78:81], v[42:43], off offset:32
	global_load_dwordx4 v[82:85], v[8:9], off offset:2080
	global_load_dwordx4 v[86:89], v[44:45], off offset:32
	global_load_dwordx4 v[90:93], v[10:11], off offset:2080
	global_load_dwordx4 v[94:97], v[42:43], off offset:48
	v_lshl_add_u64 v[34:35], v[6:7], 0, s[38:39]
	global_load_dwordx4 v[98:101], v[8:9], off offset:2096
	global_load_dwordx4 v[102:105], v[44:45], off offset:48
	v_lshl_add_u64 v[110:111], v[24:25], 0, v[2:3]
	global_load_dwordx4 v[106:109], v[10:11], off offset:2096
	global_load_dwordx4 v[16:19], v[110:111], off offset:16
	v_lshl_add_u64 v[114:115], v[28:29], 0, v[2:3]
	v_mad_i64_i32 v[4:5], s[4:5], v36, s18, v[4:5]
	global_load_dwordx4 v[12:15], v[114:115], off offset:16
	v_lshl_add_u64 v[118:119], v[34:35], 0, v[2:3]
	v_lshl_add_u64 v[40:41], v[4:5], 0, s[38:39]
	global_load_dwordx4 v[8:11], v[118:119], off offset:16
	v_lshl_add_u64 v[122:123], v[40:41], 0, v[2:3]
	global_load_dwordx4 v[4:7], v[122:123], off offset:16
	s_nop 0
	global_load_dwordx4 v[110:113], v[110:111], off
	s_nop 0
	global_load_dwordx4 v[114:117], v[114:115], off
	s_nop 0
	global_load_dwordx4 v[118:121], v[118:119], off
	s_nop 0
	global_load_dwordx4 v[122:125], v[122:123], off
	v_cndmask_b32_e64 v38, 0, 1.0, vcc
	v_cndmask_b32_e64 v36, 0, 1.0, s[0:1]
	v_cmp_lt_i32_e64 s[4:5], -1, v32
	s_mov_b32 s0, 0x800000
	s_movk_i32 s1, 0x2000
	v_cndmask_b32_e64 v32, 0, 1.0, s[4:5]
	v_or_b32_e32 v2, 0x400, v2
	s_movk_i32 s45, 0x7200
	s_mov_b32 s43, 0x800000
	s_waitcnt vmcnt(0) lgkmcnt(0)
	v_pk_mul_f32 v[128:129], v[38:39], v[46:47] op_sel_hi:[0,1]
	v_pk_mul_f32 v[134:135], v[36:37], v[52:53] op_sel_hi:[0,1]
	v_pk_mul_f32 v[136:137], v[36:37], v[50:51] op_sel_hi:[0,1]
	v_pk_mul_f32 v[126:127], v[38:39], v[48:49] op_sel_hi:[0,1]
	v_pk_mul_f32 v[130:131], v[38:39], v[56:57] op_sel_hi:[0,1]
	v_pk_mul_f32 v[132:133], v[38:39], v[54:55] op_sel_hi:[0,1]
	v_pk_mul_f32 v[68:69], v[36:37], v[68:69] op_sel_hi:[0,1]
	v_pk_mul_f32 v[66:67], v[36:37], v[66:67] op_sel_hi:[0,1]
	v_pk_mul_f32 v[52:53], v[38:39], v[80:81] op_sel_hi:[0,1]
	v_pk_mul_f32 v[56:57], v[36:37], v[82:83] op_sel_hi:[0,1]
	v_pk_mul_f32 v[80:81], v[38:39], v[96:97] op_sel_hi:[0,1]
	v_pk_mul_f32 v[82:83], v[38:39], v[94:95] op_sel_hi:[0,1]
	v_pk_mul_f32 v[54:55], v[26:27], v[86:87] op_sel_hi:[0,1]
	v_pk_mul_f32 v[86:87], v[36:37], v[98:99] op_sel_hi:[0,1]
	v_pk_mul_f32 v[46:47], v[32:33], v[92:93] op_sel_hi:[0,1]
	v_and_b32_e32 v97, 0xffff0000, v18
	v_lshlrev_b32_e32 v96, 16, v18
	v_pk_fma_f32 v[82:83], v[82:83], v[96:97], 0 op_sel_hi:[1,1,0]
	v_pk_mul_f32 v[92:93], v[26:27], v[102:103] op_sel_hi:[0,1]
	v_and_b32_e32 v97, 0xffff0000, v14
	v_lshlrev_b32_e32 v96, 16, v14
	v_pk_fma_f32 v[82:83], v[86:87], v[96:97], v[82:83]
	v_and_b32_e32 v87, 0xffff0000, v10
	v_lshlrev_b32_e32 v86, 16, v10
	v_pk_mul_f32 v[94:95], v[32:33], v[106:107] op_sel_hi:[0,1]
	v_pk_fma_f32 v[82:83], v[92:93], v[86:87], v[82:83]
	v_and_b32_e32 v87, 0xffff0000, v6
	v_lshlrev_b32_e32 v86, 16, v6
	v_pk_fma_f32 v[82:83], v[94:95], v[86:87], v[82:83]
	v_and_b32_e32 v93, 0xffff0000, v19
	v_mul_f32_e32 v10, 0xbfb8aa3b, v83
	v_exp_f32_e32 v10, v10
	v_lshlrev_b32_e32 v92, 16, v19
	v_pk_mul_f32 v[50:51], v[36:37], v[84:85] op_sel_hi:[0,1]
	v_pk_mul_f32 v[84:85], v[36:37], v[100:101] op_sel_hi:[0,1]
	v_mul_f32_e32 v6, 0xbfb8aa3b, v82
	v_pk_fma_f32 v[18:19], v[80:81], v[92:93], 0 op_sel_hi:[1,1,0]
	v_and_b32_e32 v81, 0xffff0000, v15
	v_lshlrev_b32_e32 v80, 16, v15
	v_pk_mul_f32 v[48:49], v[26:27], v[88:89] op_sel_hi:[0,1]
	v_pk_mul_f32 v[88:89], v[26:27], v[104:105] op_sel_hi:[0,1]
	v_exp_f32_e32 v6, v6
	v_pk_fma_f32 v[14:15], v[84:85], v[80:81], v[18:19]
	v_and_b32_e32 v19, 0xffff0000, v11
	v_lshlrev_b32_e32 v18, 16, v11
	v_pk_mul_f32 v[86:87], v[32:33], v[108:109] op_sel_hi:[0,1]
	v_add_f32_e32 v37, 1.0, v10
	v_pk_fma_f32 v[10:11], v[88:89], v[18:19], v[14:15]
	v_and_b32_e32 v15, 0xffff0000, v7
	v_lshlrev_b32_e32 v14, 16, v7
	v_pk_fma_f32 v[10:11], v[86:87], v[14:15], v[10:11]
	v_add_f32_e32 v6, 1.0, v6
	v_mul_f32_e32 v7, 0xbfb8aa3b, v10
	v_exp_f32_e32 v14, v7
	v_mul_f32_e32 v7, 0xbfb8aa3b, v11
	v_rcp_f32_e32 v6, v6
	v_exp_f32_e32 v15, v7
	v_rcp_f32_e32 v7, v37
	v_lshlrev_b32_e32 v84, 16, v114
	v_and_b32_e32 v85, 0xffff0000, v114
	v_pk_mul_f32 v[58:59], v[26:27], v[58:59] op_sel_hi:[0,1]
	v_pk_mul_f32 v[6:7], v[82:83], v[6:7]
	v_lshlrev_b32_e32 v82, 16, v110
	v_and_b32_e32 v83, 0xffff0000, v110
	v_pk_fma_f32 v[82:83], v[128:129], v[82:83], 0 op_sel_hi:[1,1,0]
	v_pk_mul_f32 v[62:63], v[32:33], v[62:63] op_sel_hi:[0,1]
	v_pk_fma_f32 v[82:83], v[136:137], v[84:85], v[82:83]
	v_lshlrev_b32_e32 v84, 16, v118
	v_and_b32_e32 v85, 0xffff0000, v118
	v_pk_mul_f32 v[78:79], v[38:39], v[78:79] op_sel_hi:[0,1]
	v_xor_b32_e32 v37, 1, v27
	v_add_u32_e32 v39, 64, v33
	v_pk_fma_f32 v[58:59], v[58:59], v[84:85], v[82:83]
	v_lshlrev_b32_e32 v82, 16, v122
	v_and_b32_e32 v83, 0xffff0000, v122
	v_cmp_lt_i32_e32 vcc, v37, v39
	v_pk_fma_f32 v[58:59], v[62:63], v[82:83], v[58:59]
	v_pk_mul_f32 v[64:65], v[32:33], v[64:65] op_sel_hi:[0,1]
	v_pk_mul_f32 v[76:77], v[32:33], v[76:77] op_sel_hi:[0,1]
	v_pk_mul_f32 v[74:75], v[32:33], v[74:75] op_sel_hi:[0,1]
	v_pk_mul_f32 v[18:19], v[32:33], v[90:91] op_sel_hi:[0,1]
	v_cndmask_b32_e32 v33, v27, v37, vcc
	v_mul_f32_e32 v37, 0xbfb8aa3b, v58
	v_exp_f32_e32 v37, v37
	v_mul_f32_e32 v62, 0xbfb8aa3b, v59
	v_exp_f32_e32 v63, v62
	v_lshlrev_b32_e32 v82, 16, v111
	v_and_b32_e32 v83, 0xffff0000, v111
	v_pk_fma_f32 v[82:83], v[126:127], v[82:83], 0 op_sel_hi:[1,1,0]
	v_lshlrev_b32_e32 v84, 16, v115
	v_and_b32_e32 v85, 0xffff0000, v115
	v_pk_mul_f32 v[60:61], v[26:27], v[60:61] op_sel_hi:[0,1]
	v_pk_fma_f32 v[82:83], v[134:135], v[84:85], v[82:83]
	v_lshlrev_b32_e32 v84, 16, v119
	v_and_b32_e32 v85, 0xffff0000, v119
	v_add_f32_e32 v37, 1.0, v37
	v_pk_fma_f32 v[60:61], v[60:61], v[84:85], v[82:83]
	v_lshlrev_b32_e32 v82, 16, v123
	v_and_b32_e32 v83, 0xffff0000, v123
	v_rcp_f32_e32 v62, v37
	v_add_f32_e32 v37, 1.0, v63
	v_pk_fma_f32 v[60:61], v[64:65], v[82:83], v[60:61]
	v_rcp_f32_e32 v63, v37
	v_mul_f32_e32 v37, 0xbfb8aa3b, v60
	v_exp_f32_e32 v37, v37
	v_mul_f32_e32 v64, 0xbfb8aa3b, v61
	v_exp_f32_e32 v64, v64
	v_pk_mul_f32 v[58:59], v[58:59], v[62:63]
	v_add_f32_e32 v37, 1.0, v37
	v_rcp_f32_e32 v62, v37
	v_add_f32_e32 v37, 1.0, v64
	v_lshlrev_b32_e32 v64, 16, v112
	v_and_b32_e32 v65, 0xffff0000, v112
	v_pk_fma_f32 v[64:65], v[132:133], v[64:65], 0 op_sel_hi:[1,1,0]
	v_lshlrev_b32_e32 v82, 16, v116
	v_and_b32_e32 v83, 0xffff0000, v116
	v_pk_mul_f32 v[70:71], v[26:27], v[70:71] op_sel_hi:[0,1]
	v_pk_fma_f32 v[64:65], v[66:67], v[82:83], v[64:65]
	v_lshlrev_b32_e32 v66, 16, v120
	v_and_b32_e32 v67, 0xffff0000, v120
	v_pk_fma_f32 v[64:65], v[70:71], v[66:67], v[64:65]
	v_lshlrev_b32_e32 v66, 16, v124
	v_and_b32_e32 v67, 0xffff0000, v124
	v_pk_fma_f32 v[64:65], v[74:75], v[66:67], v[64:65]
	v_lshlrev_b32_e32 v74, 16, v117
	v_mul_f32_e32 v63, 0xbfb8aa3b, v64
	v_exp_f32_e32 v66, v63
	v_mul_f32_e32 v63, 0xbfb8aa3b, v65
	v_exp_f32_e32 v67, v63
	v_rcp_f32_e32 v63, v37
	v_add_f32_e32 v37, 1.0, v66
	v_rcp_f32_e32 v66, v37
	v_add_f32_e32 v37, 1.0, v67
	v_rcp_f32_e32 v67, v37
	v_and_b32_e32 v75, 0xffff0000, v117
	v_pk_mul_f32 v[72:73], v[26:27], v[72:73] op_sel_hi:[0,1]
	v_pk_mul_f32 v[70:71], v[58:59], v[58:59]
	v_pk_mul_f32 v[64:65], v[64:65], v[66:67]
	v_lshlrev_b32_e32 v66, 16, v113
	v_and_b32_e32 v67, 0xffff0000, v113
	v_pk_fma_f32 v[66:67], v[130:131], v[66:67], 0 op_sel_hi:[1,1,0]
	v_pk_mul_f32 v[60:61], v[60:61], v[62:63]
	v_pk_fma_f32 v[66:67], v[68:69], v[74:75], v[66:67]
	v_lshlrev_b32_e32 v68, 16, v121
	v_and_b32_e32 v69, 0xffff0000, v121
	v_pk_fma_f32 v[66:67], v[72:73], v[68:69], v[66:67]
	v_lshlrev_b32_e32 v68, 16, v125
	v_and_b32_e32 v69, 0xffff0000, v125
	v_lshlrev_b32_e32 v74, 16, v16
	v_and_b32_e32 v75, 0xffff0000, v16
	v_pk_fma_f32 v[66:67], v[76:77], v[68:69], v[66:67]
	v_pk_fma_f32 v[74:75], v[78:79], v[74:75], 0 op_sel_hi:[1,1,0]
	v_lshlrev_b32_e32 v76, 16, v12
	v_and_b32_e32 v77, 0xffff0000, v12
	v_pk_fma_f32 v[56:57], v[56:57], v[76:77], v[74:75]
	v_lshlrev_b32_e32 v74, 16, v8
	v_and_b32_e32 v75, 0xffff0000, v8
	v_mul_f32_e32 v37, 0xbfb8aa3b, v66
	v_pk_fma_f32 v[54:55], v[54:55], v[74:75], v[56:57]
	v_lshlrev_b32_e32 v56, 16, v4
	v_and_b32_e32 v57, 0xffff0000, v4
	v_exp_f32_e32 v37, v37
	v_mul_f32_e32 v68, 0xbfb8aa3b, v67
	v_pk_fma_f32 v[18:19], v[18:19], v[56:57], v[54:55]
	v_exp_f32_e32 v73, v68
	v_mul_f32_e32 v8, 0xbfb8aa3b, v19
	v_exp_f32_e32 v8, v8
	v_add_f32_e32 v37, 1.0, v37
	v_lshlrev_b32_e32 v16, 16, v17
	v_and_b32_e32 v17, 0xffff0000, v17
	v_rcp_f32_e32 v72, v37
	v_add_f32_e32 v37, 1.0, v73
	v_pk_fma_f32 v[16:17], v[52:53], v[16:17], 0 op_sel_hi:[1,1,0]
	v_lshlrev_b32_e32 v12, 16, v13
	v_and_b32_e32 v13, 0xffff0000, v13
	v_rcp_f32_e32 v73, v37
	v_add_f32_e32 v37, 1.0, v8
	v_pk_fma_f32 v[12:13], v[50:51], v[12:13], v[16:17]
	v_lshlrev_b32_e32 v8, 16, v9
	v_and_b32_e32 v9, 0xffff0000, v9
	v_pk_fma_f32 v[8:9], v[48:49], v[8:9], v[12:13]
	v_lshlrev_b32_e32 v12, 16, v5
	v_and_b32_e32 v13, 0xffff0000, v5
	v_mul_f32_e32 v4, 0xbfb8aa3b, v18
	v_pk_fma_f32 v[8:9], v[46:47], v[12:13], v[8:9]
	v_exp_f32_e32 v4, v4
	v_mul_f32_e32 v5, 0xbfb8aa3b, v8
	v_exp_f32_e32 v12, v5
	v_mul_f32_e32 v5, 0xbfb8aa3b, v9
	v_exp_f32_e32 v13, v5
	v_pk_mul_f32 v[62:63], v[60:61], v[60:61]
	v_add_f32_e32 v4, 1.0, v4
	v_rcp_f32_e32 v5, v37
	v_add_f32_e32 v37, v70, v71
	v_rcp_f32_e32 v4, v4
	v_add_f32_e32 v37, v62, v37
	v_pk_mul_f32 v[68:69], v[64:65], v[64:65]
	v_add_f32_e32 v12, 1.0, v12
	v_add_f32_e32 v13, 1.0, v13
	v_add_f32_e32 v37, v63, v37
	v_pk_mul_f32 v[54:55], v[66:67], v[72:73]
	v_rcp_f32_e32 v12, v12
	v_rcp_f32_e32 v13, v13
	v_add_f32_e32 v37, v37, v68
	v_pk_mul_f32 v[16:17], v[54:55], v[54:55]
	v_add_f32_e32 v37, v69, v37
	v_pk_mul_f32 v[4:5], v[18:19], v[4:5]
	v_add_f32_e32 v16, v16, v37
	v_add_f32_e32 v14, 1.0, v14
	v_add_f32_e32 v15, 1.0, v15
	v_pk_mul_f32 v[18:19], v[4:5], v[4:5]
	v_add_f32_e32 v16, v17, v16
	v_rcp_f32_e32 v14, v14
	v_rcp_f32_e32 v15, v15
	v_pk_mul_f32 v[8:9], v[8:9], v[12:13]
	v_add_f32_e32 v16, v16, v18
	v_pk_mul_f32 v[12:13], v[8:9], v[8:9]
	v_add_f32_e32 v16, v19, v16
	v_add_f32_e32 v12, v12, v16
	v_pk_mul_f32 v[80:81], v[6:7], v[6:7]
	v_add_f32_e32 v12, v13, v12
	v_pk_mul_f32 v[10:11], v[10:11], v[14:15]
	v_add_f32_e32 v12, v80, v12
	v_pk_mul_f32 v[14:15], v[10:11], v[10:11]
	v_add_f32_e32 v12, v81, v12
	v_add_f32_e32 v12, v14, v12
	v_lshlrev_b32_e32 v33, 2, v33
	v_add_f32_e32 v12, v15, v12
	ds_bpermute_b32 v13, v33, v12
	v_xor_b32_e32 v14, 2, v27
	v_cmp_lt_i32_e32 vcc, v14, v39
	v_lshlrev_b32_e32 v136, 1, v23
	v_lshl_add_u64 v[110:111], v[34:35], 0, v[2:3]
	v_cndmask_b32_e32 v14, v27, v14, vcc
	v_lshlrev_b32_e32 v37, 2, v14
	s_waitcnt lgkmcnt(0)
	v_add_f32_e32 v12, v12, v13
	ds_bpermute_b32 v13, v37, v12
	v_xor_b32_e32 v14, 4, v27
	v_cmp_lt_i32_e32 vcc, v14, v39
	v_mul_lo_u32 v39, v1, s20
	v_lshl_add_u64 v[112:113], v[40:41], 0, v[2:3]
	v_cndmask_b32_e32 v14, v27, v14, vcc
	v_lshlrev_b32_e32 v27, 2, v14
	s_waitcnt lgkmcnt(0)
	v_add_f32_e32 v12, v12, v13
	ds_bpermute_b32 v13, v27, v12
	s_waitcnt lgkmcnt(0)
	v_add_f32_e32 v12, v12, v13
	v_add_f32_e32 v12, 0x358637bd, v12
	v_mul_f32_e32 v13, 0x4b800000, v12
	v_cmp_gt_f32_e32 vcc, s0, v12
	s_nop 1
	v_cndmask_b32_e32 v12, v12, v13, vcc
	v_rsq_f32_e32 v12, v12
	s_nop 0
	v_mul_f32_e32 v13, 0x45800000, v12
	v_cndmask_b32_e32 v12, v12, v13, vcc
	v_mul_f32_e32 v12, 0x3db504f3, v12
	v_pk_mul_f32 v[14:15], v[58:59], v[12:13] op_sel_hi:[1,0]
	v_pk_mul_f32 v[16:17], v[60:61], v[12:13] op_sel_hi:[1,0]
	v_pk_mul_f32 v[4:5], v[4:5], v[12:13] op_sel_hi:[1,0]
	v_pk_mul_f32 v[8:9], v[8:9], v[12:13] op_sel_hi:[1,0]
	v_pk_mul_f32 v[18:19], v[64:65], v[12:13] op_sel_hi:[1,0]
	v_pk_mul_f32 v[46:47], v[54:55], v[12:13] op_sel_hi:[1,0]
	v_pk_mul_f32 v[6:7], v[6:7], v[12:13] op_sel_hi:[1,0]
	v_pk_mul_f32 v[10:11], v[10:11], v[12:13] op_sel_hi:[1,0]
	v_add3_u32 v12, s25, v39, v136
	v_cvt_pk_bf16_f32 v13, v14, v15
	v_cvt_pk_bf16_f32 v14, v16, v17
	v_cvt_pk_bf16_f32 v4, v4, v5
	v_cvt_pk_bf16_f32 v5, v8, v9
	ds_write2_b32 v12, v13, v14 offset1:1
	v_cvt_pk_bf16_f32 v13, v18, v19
	v_cvt_pk_bf16_f32 v14, v46, v47
	ds_write2_b32 v12, v4, v5 offset0:4 offset1:5
	v_cvt_pk_bf16_f32 v4, v6, v7
	v_cvt_pk_bf16_f32 v5, v10, v11
	v_add_co_u32_e32 v82, vcc, s1, v42
	ds_write2_b32 v12, v13, v14 offset0:2 offset1:3
	ds_write2_b32 v12, v4, v5 offset0:6 offset1:7
	v_addc_co_u32_e32 v83, vcc, 0, v43, vcc
	global_load_dwordx4 v[4:7], v[42:43], off offset:2048
	global_load_dwordx4 v[8:11], v[82:83], off
	global_load_dwordx4 v[12:15], v[44:45], off offset:2048
	s_movk_i32 s1, 0x5000
	v_add_co_u32_e32 v106, vcc, s1, v42
	s_waitcnt vmcnt(0) lgkmcnt(0)
	v_pk_mul_f32 v[118:119], v[36:37], v[10:11] op_sel_hi:[0,1]
	v_addc_co_u32_e32 v107, vcc, 0, v43, vcc
	global_load_dwordx4 v[16:19], v[106:107], off
	global_load_dwordx4 v[46:49], v[42:43], off offset:2064
	global_load_dwordx4 v[50:53], v[82:83], off offset:16
	global_load_dwordx4 v[54:57], v[44:45], off offset:2064
	global_load_dwordx4 v[58:61], v[106:107], off offset:16
	global_load_dwordx4 v[62:65], v[42:43], off offset:2080
	global_load_dwordx4 v[66:69], v[82:83], off offset:32
	global_load_dwordx4 v[70:73], v[44:45], off offset:2080
	global_load_dwordx4 v[74:77], v[106:107], off offset:32
	global_load_dwordx4 v[78:81], v[42:43], off offset:2096
	s_nop 0
	global_load_dwordx4 v[82:85], v[82:83], off offset:48
	v_lshl_add_u64 v[42:43], v[24:25], 0, v[2:3]
	global_load_dwordx4 v[86:89], v[44:45], off offset:2096
	global_load_dwordx4 v[90:93], v[42:43], off
	v_lshl_add_u64 v[44:45], v[28:29], 0, v[2:3]
	global_load_dwordx4 v[94:97], v[44:45], off
	global_load_dwordx4 v[98:101], v[110:111], off
	global_load_dwordx4 v[102:105], v[112:113], off
	s_nop 0
	global_load_dwordx4 v[106:109], v[106:107], off offset:48
	v_pk_mul_f32 v[122:123], v[26:27], v[14:15] op_sel_hi:[0,1]
	v_pk_mul_f32 v[124:125], v[26:27], v[12:13] op_sel_hi:[0,1]
	global_load_dwordx4 v[12:15], v[44:45], off offset:16
	v_pk_mul_f32 v[120:121], v[36:37], v[8:9] op_sel_hi:[0,1]
	global_load_dwordx4 v[8:11], v[110:111], off offset:16
	v_pk_mul_f32 v[114:115], v[38:39], v[6:7] op_sel_hi:[0,1]
	v_pk_mul_f32 v[116:117], v[38:39], v[4:5] op_sel_hi:[0,1]
	global_load_dwordx4 v[4:7], v[112:113], off offset:16
	s_waitcnt vmcnt(0) lgkmcnt(0)
	v_pk_mul_f32 v[126:127], v[32:33], v[18:19] op_sel_hi:[0,1]
	v_pk_mul_f32 v[128:129], v[32:33], v[16:17] op_sel_hi:[0,1]
	global_load_dwordx4 v[16:19], v[42:43], off offset:16
	v_pk_mul_f32 v[130:131], v[38:39], v[48:49] op_sel_hi:[0,1]
	v_pk_mul_f32 v[134:135], v[36:37], v[50:51] op_sel_hi:[0,1]
	v_pk_mul_f32 v[132:133], v[38:39], v[46:47] op_sel_hi:[0,1]
	v_pk_mul_f32 v[54:55], v[26:27], v[54:55] op_sel_hi:[0,1]
	v_pk_mul_f32 v[58:59], v[32:33], v[58:59] op_sel_hi:[0,1]
	v_pk_mul_f32 v[52:53], v[36:37], v[52:53] op_sel_hi:[0,1]
	v_pk_mul_f32 v[46:47], v[38:39], v[80:81] op_sel_hi:[0,1]
	v_pk_mul_f32 v[80:81], v[36:37], v[82:83] op_sel_hi:[0,1]
	v_pk_mul_f32 v[56:57], v[26:27], v[56:57] op_sel_hi:[0,1]
	v_pk_mul_f32 v[82:83], v[26:27], v[86:87] op_sel_hi:[0,1]
	v_lshlrev_b32_e32 v48, 16, v90
	v_and_b32_e32 v49, 0xffff0000, v90
	v_pk_fma_f32 v[48:49], v[116:117], v[48:49], 0 op_sel_hi:[1,1,0]
	v_lshlrev_b32_e32 v50, 16, v94
	v_and_b32_e32 v51, 0xffff0000, v94
	v_pk_fma_f32 v[48:49], v[120:121], v[50:51], v[48:49]
	v_lshlrev_b32_e32 v50, 16, v98
	v_and_b32_e32 v51, 0xffff0000, v98
	v_pk_fma_f32 v[48:49], v[124:125], v[50:51], v[48:49]
	v_lshlrev_b32_e32 v50, 16, v102
	v_and_b32_e32 v51, 0xffff0000, v102
	v_pk_fma_f32 v[48:49], v[128:129], v[50:51], v[48:49]
	v_lshlrev_b32_e32 v86, 16, v91
	v_mul_f32_e32 v2, 0xbfb8aa3b, v48
	v_exp_f32_e32 v2, v2
	v_mul_f32_e32 v50, 0xbfb8aa3b, v49
	v_and_b32_e32 v87, 0xffff0000, v91
	v_pk_mul_f32 v[42:43], v[26:27], v[88:89] op_sel_hi:[0,1]
	v_exp_f32_e32 v51, v50
	v_pk_fma_f32 v[86:87], v[114:115], v[86:87], 0 op_sel_hi:[1,1,0]
	v_lshlrev_b32_e32 v88, 16, v95
	v_and_b32_e32 v89, 0xffff0000, v95
	v_pk_fma_f32 v[86:87], v[118:119], v[88:89], v[86:87]
	v_lshlrev_b32_e32 v88, 16, v99
	v_and_b32_e32 v89, 0xffff0000, v99
	v_pk_fma_f32 v[86:87], v[122:123], v[88:89], v[86:87]
	v_lshlrev_b32_e32 v88, 16, v103
	v_and_b32_e32 v89, 0xffff0000, v103
	v_add_f32_e32 v2, 1.0, v2
	v_pk_fma_f32 v[86:87], v[126:127], v[88:89], v[86:87]
	v_rcp_f32_e32 v50, v2
	v_add_f32_e32 v2, 1.0, v51
	v_mul_f32_e32 v51, 0xbfb8aa3b, v86
	v_exp_f32_e32 v88, v51
	v_mul_f32_e32 v51, 0xbfb8aa3b, v87
	v_exp_f32_e32 v89, v51
	v_rcp_f32_e32 v51, v2
	v_add_f32_e32 v2, 1.0, v88
	v_rcp_f32_e32 v88, v2
	v_add_f32_e32 v2, 1.0, v89
	v_rcp_f32_e32 v89, v2
	v_pk_mul_f32 v[48:49], v[48:49], v[50:51]
	v_pk_mul_f32 v[60:61], v[32:33], v[60:61] op_sel_hi:[0,1]
	v_pk_mul_f32 v[62:63], v[38:39], v[62:63] op_sel_hi:[0,1]
	v_pk_mul_f32 v[50:51], v[86:87], v[88:89]
	v_lshlrev_b32_e32 v86, 16, v92
	v_and_b32_e32 v87, 0xffff0000, v92
	v_pk_fma_f32 v[86:87], v[132:133], v[86:87], 0 op_sel_hi:[1,1,0]
	v_lshlrev_b32_e32 v88, 16, v96
	v_and_b32_e32 v89, 0xffff0000, v96
	v_pk_fma_f32 v[86:87], v[134:135], v[88:89], v[86:87]
	v_lshlrev_b32_e32 v88, 16, v100
	v_and_b32_e32 v89, 0xffff0000, v100
	v_pk_fma_f32 v[54:55], v[54:55], v[88:89], v[86:87]
	v_lshlrev_b32_e32 v86, 16, v104
	v_and_b32_e32 v87, 0xffff0000, v104
	v_pk_fma_f32 v[54:55], v[58:59], v[86:87], v[54:55]
	v_lshlrev_b32_e32 v88, 16, v93
	v_mul_f32_e32 v2, 0xbfb8aa3b, v54
	v_and_b32_e32 v89, 0xffff0000, v93
	v_exp_f32_e32 v2, v2
	v_mul_f32_e32 v58, 0xbfb8aa3b, v55
	v_pk_fma_f32 v[88:89], v[130:131], v[88:89], 0 op_sel_hi:[1,1,0]
	v_lshlrev_b32_e32 v92, 16, v97
	v_and_b32_e32 v93, 0xffff0000, v97
	v_exp_f32_e32 v87, v58
	v_pk_fma_f32 v[52:53], v[52:53], v[92:93], v[88:89]
	v_lshlrev_b32_e32 v88, 16, v101
	v_and_b32_e32 v89, 0xffff0000, v101
	v_pk_fma_f32 v[52:53], v[56:57], v[88:89], v[52:53]
	v_lshlrev_b32_e32 v56, 16, v105
	v_and_b32_e32 v57, 0xffff0000, v105
	v_pk_fma_f32 v[52:53], v[60:61], v[56:57], v[52:53]
	s_waitcnt vmcnt(0) lgkmcnt(0)
	v_lshlrev_b32_e32 v60, 16, v16
	v_and_b32_e32 v61, 0xffff0000, v16
	v_pk_mul_f32 v[66:67], v[36:37], v[66:67] op_sel_hi:[0,1]
	v_add_f32_e32 v2, 1.0, v2
	v_pk_fma_f32 v[60:61], v[62:63], v[60:61], 0 op_sel_hi:[1,1,0]
	v_lshlrev_b32_e32 v62, 16, v12
	v_and_b32_e32 v63, 0xffff0000, v12
	v_pk_mul_f32 v[70:71], v[26:27], v[70:71] op_sel_hi:[0,1]
	v_rcp_f32_e32 v86, v2
	v_add_f32_e32 v2, 1.0, v87
	v_pk_fma_f32 v[60:61], v[66:67], v[62:63], v[60:61]
	v_lshlrev_b32_e32 v62, 16, v8
	v_and_b32_e32 v63, 0xffff0000, v8
	v_pk_mul_f32 v[74:75], v[32:33], v[74:75] op_sel_hi:[0,1]
	v_rcp_f32_e32 v87, v2
	v_mul_f32_e32 v2, 0xbfb8aa3b, v52
	v_pk_fma_f32 v[60:61], v[70:71], v[62:63], v[60:61]
	v_lshlrev_b32_e32 v62, 16, v4
	v_and_b32_e32 v63, 0xffff0000, v4
	v_exp_f32_e32 v2, v2
	v_mul_f32_e32 v56, 0xbfb8aa3b, v53
	v_pk_fma_f32 v[60:61], v[74:75], v[62:63], v[60:61]
	v_exp_f32_e32 v57, v56
	v_mul_f32_e32 v4, 0xbfb8aa3b, v60
	v_exp_f32_e32 v4, v4
	v_mul_f32_e32 v8, 0xbfb8aa3b, v61
	v_exp_f32_e32 v8, v8
	v_add_f32_e32 v2, 1.0, v2
	v_pk_mul_f32 v[64:65], v[38:39], v[64:65] op_sel_hi:[0,1]
	v_rcp_f32_e32 v56, v2
	v_add_f32_e32 v2, 1.0, v57
	v_lshlrev_b32_e32 v16, 16, v17
	v_and_b32_e32 v17, 0xffff0000, v17
	v_pk_mul_f32 v[68:69], v[36:37], v[68:69] op_sel_hi:[0,1]
	v_rcp_f32_e32 v57, v2
	v_add_f32_e32 v2, 1.0, v4
	v_pk_fma_f32 v[16:17], v[64:65], v[16:17], 0 op_sel_hi:[1,1,0]
	v_lshlrev_b32_e32 v12, 16, v13
	v_and_b32_e32 v13, 0xffff0000, v13
	v_pk_mul_f32 v[72:73], v[26:27], v[72:73] op_sel_hi:[0,1]
	v_rcp_f32_e32 v62, v2
	v_add_f32_e32 v2, 1.0, v8
	v_pk_fma_f32 v[12:13], v[68:69], v[12:13], v[16:17]
	v_lshlrev_b32_e32 v8, 16, v9
	v_and_b32_e32 v9, 0xffff0000, v9
	v_pk_mul_f32 v[76:77], v[32:33], v[76:77] op_sel_hi:[0,1]
	v_pk_fma_f32 v[8:9], v[72:73], v[8:9], v[12:13]
	v_lshlrev_b32_e32 v4, 16, v5
	v_and_b32_e32 v5, 0xffff0000, v5
	v_rcp_f32_e32 v63, v2
	v_pk_fma_f32 v[4:5], v[76:77], v[4:5], v[8:9]
	v_pk_mul_f32 v[78:79], v[38:39], v[78:79] op_sel_hi:[0,1]
	v_mul_f32_e32 v2, 0xbfb8aa3b, v4
	v_exp_f32_e32 v2, v2
	v_mul_f32_e32 v8, 0xbfb8aa3b, v5
	v_exp_f32_e32 v13, v8
	v_lshlrev_b32_e32 v16, 16, v18
	v_and_b32_e32 v17, 0xffff0000, v18
	v_pk_mul_f32 v[60:61], v[60:61], v[62:63]
	v_pk_fma_f32 v[16:17], v[78:79], v[16:17], 0 op_sel_hi:[1,1,0]
	v_lshlrev_b32_e32 v62, 16, v14
	v_and_b32_e32 v63, 0xffff0000, v14
	v_pk_fma_f32 v[16:17], v[80:81], v[62:63], v[16:17]
	v_lshlrev_b32_e32 v62, 16, v10
	v_and_b32_e32 v63, 0xffff0000, v10
	v_pk_mul_f32 v[90:91], v[32:33], v[106:107] op_sel_hi:[0,1]
	v_add_f32_e32 v2, 1.0, v2
	v_pk_fma_f32 v[16:17], v[82:83], v[62:63], v[16:17]
	v_lshlrev_b32_e32 v62, 16, v6
	v_and_b32_e32 v63, 0xffff0000, v6
	v_rcp_f32_e32 v12, v2
	v_add_f32_e32 v2, 1.0, v13
	v_pk_fma_f32 v[16:17], v[90:91], v[62:63], v[16:17]
	v_rcp_f32_e32 v13, v2
	v_mul_f32_e32 v2, 0xbfb8aa3b, v16
	v_exp_f32_e32 v2, v2
	v_mul_f32_e32 v6, 0xbfb8aa3b, v17
	v_exp_f32_e32 v10, v6
	v_pk_mul_f32 v[4:5], v[4:5], v[12:13]
	v_lshlrev_b32_e32 v12, 16, v19
	v_and_b32_e32 v13, 0xffff0000, v19
	v_pk_mul_f32 v[44:45], v[36:37], v[84:85] op_sel_hi:[0,1]
	v_add_f32_e32 v2, 1.0, v2
	v_pk_fma_f32 v[12:13], v[46:47], v[12:13], 0 op_sel_hi:[1,1,0]
	v_lshlrev_b32_e32 v14, 16, v15
	v_and_b32_e32 v15, 0xffff0000, v15
	v_rcp_f32_e32 v6, v2
	v_add_f32_e32 v2, 1.0, v10
	v_pk_fma_f32 v[12:13], v[44:45], v[14:15], v[12:13]
	v_lshlrev_b32_e32 v10, 16, v11
	v_and_b32_e32 v11, 0xffff0000, v11
	v_pk_mul_f32 v[84:85], v[32:33], v[108:109] op_sel_hi:[0,1]
	v_pk_fma_f32 v[10:11], v[42:43], v[10:11], v[12:13]
	v_lshlrev_b32_e32 v12, 16, v7
	v_and_b32_e32 v13, 0xffff0000, v7
	v_pk_fma_f32 v[10:11], v[84:85], v[12:13], v[10:11]
	v_pk_mul_f32 v[94:95], v[48:49], v[48:49]
	v_mul_f32_e32 v7, 0xbfb8aa3b, v10
	v_exp_f32_e32 v12, v7
	v_mul_f32_e32 v7, 0xbfb8aa3b, v11
	v_exp_f32_e32 v13, v7
	v_rcp_f32_e32 v7, v2
	v_add_f32_e32 v2, 1.0, v12
	v_rcp_f32_e32 v12, v2
	v_add_f32_e32 v2, 1.0, v13
	v_pk_mul_f32 v[58:59], v[50:51], v[50:51]
	v_rcp_f32_e32 v13, v2
	v_add_f32_e32 v2, v94, v95
	v_pk_mul_f32 v[54:55], v[54:55], v[86:87]
	v_add_f32_e32 v2, v58, v2
	v_pk_mul_f32 v[66:67], v[54:55], v[54:55]
	v_add_f32_e32 v2, v59, v2
	v_pk_mul_f32 v[52:53], v[52:53], v[56:57]
	v_add_f32_e32 v2, v2, v66
	v_pk_mul_f32 v[56:57], v[52:53], v[52:53]
	v_add_f32_e32 v2, v67, v2
	v_add_f32_e32 v2, v56, v2
	v_pk_mul_f32 v[8:9], v[60:61], v[60:61]
	v_add_f32_e32 v2, v57, v2
	v_add_f32_e32 v2, v2, v8
	v_pk_mul_f32 v[14:15], v[4:5], v[4:5]
	v_add_f32_e32 v2, v9, v2
	v_pk_mul_f32 v[6:7], v[16:17], v[6:7]
	v_add_f32_e32 v2, v14, v2
	v_pk_mul_f32 v[16:17], v[6:7], v[6:7]
	v_add_f32_e32 v2, v15, v2
	v_pk_mul_f32 v[10:11], v[10:11], v[12:13]
	v_add_f32_e32 v2, v16, v2
	v_pk_mul_f32 v[12:13], v[10:11], v[10:11]
	v_add_f32_e32 v2, v17, v2
	v_add_f32_e32 v2, v12, v2
	v_add_f32_e32 v2, v13, v2
	ds_bpermute_b32 v8, v33, v2
	v_lshl_add_u32 v46, v23, 2, s33
	s_waitcnt lgkmcnt(0)
	v_add_f32_e32 v2, v2, v8
	ds_bpermute_b32 v8, v37, v2
	s_waitcnt lgkmcnt(0)
	v_add_f32_e32 v2, v2, v8
	ds_bpermute_b32 v8, v27, v2
	s_waitcnt lgkmcnt(0)
	v_add_f32_e32 v2, v2, v8
	v_add_f32_e32 v2, 0x358637bd, v2
	v_mul_f32_e32 v8, 0x4b800000, v2
	v_cmp_gt_f32_e32 vcc, s0, v2
	s_movk_i32 s0, 0x204
	s_nop 0
	v_cndmask_b32_e32 v2, v2, v8, vcc
	v_rsq_f32_e32 v2, v2
	v_mad_u64_u32 v[8:9], s[0:1], v1, s0, v[46:47]
	v_add3_u32 v9, s24, v39, v136
	v_mul_f32_e32 v12, 0x45800000, v2
	v_cndmask_b32_e32 v2, v2, v12, vcc
	v_pk_mul_f32 v[12:13], v[48:49], v[2:3] op_sel_hi:[1,0]
	v_pk_mul_f32 v[14:15], v[50:51], v[2:3] op_sel_hi:[1,0]
	v_pk_mul_f32 v[16:17], v[54:55], v[2:3] op_sel_hi:[1,0]
	v_pk_mul_f32 v[18:19], v[52:53], v[2:3] op_sel_hi:[1,0]
	v_pk_mul_f32 v[42:43], v[60:61], v[2:3] op_sel_hi:[1,0]
	v_pk_mul_f32 v[4:5], v[4:5], v[2:3] op_sel_hi:[1,0]
	v_pk_mul_f32 v[6:7], v[6:7], v[2:3] op_sel_hi:[1,0]
	v_pk_mul_f32 v[10:11], v[10:11], v[2:3] op_sel_hi:[1,0]
	v_cvt_pk_bf16_f32 v2, v12, v13
	v_cvt_pk_bf16_f32 v23, v14, v15
	ds_write2_b32 v9, v2, v23 offset1:1
	v_cvt_pk_bf16_f32 v2, v16, v17
	v_cvt_pk_bf16_f32 v23, v18, v19
	ds_write2_b32 v9, v2, v23 offset0:2 offset1:3
	v_cvt_pk_bf16_f32 v2, v42, v43
	v_cvt_pk_bf16_f32 v23, v4, v5
	ds_write2_b32 v9, v2, v23 offset0:4 offset1:5
	v_cvt_pk_bf16_f32 v2, v6, v7
	v_cvt_pk_bf16_f32 v23, v10, v11
	ds_write2_b32 v9, v2, v23 offset0:6 offset1:7
	ds_write2_b32 v8, v12, v13 offset1:1
	ds_write2_b32 v8, v14, v15 offset0:2 offset1:3
	ds_write2_b32 v8, v16, v17 offset0:4 offset1:5
	ds_write2_b32 v8, v18, v19 offset0:6 offset1:7
	ds_write2_b32 v8, v42, v43 offset0:8 offset1:9
	ds_write2_b32 v8, v4, v5 offset0:10 offset1:11
	ds_write2_b32 v8, v6, v7 offset0:12 offset1:13
	ds_write2_b32 v8, v10, v11 offset0:14 offset1:15
	v_or_b32_e32 v12, 0x400, v21
	v_lshlrev_b32_e32 v2, 2, v12
	v_lshl_add_u64 v[4:5], v[30:31], 0, v[2:3]
	v_add_co_u32_e32 v6, vcc, s21, v4
	v_lshlrev_b32_e32 v2, 1, v12
	s_nop 0
	v_addc_co_u32_e32 v7, vcc, 0, v5, vcc
	v_add_co_u32_e32 v8, vcc, s19, v4
	global_load_dwordx4 v[42:45], v[4:5], off offset:48
	global_load_dwordx4 v[48:51], v[6:7], off offset:2096
	v_addc_co_u32_e32 v9, vcc, 0, v5, vcc
	v_add_co_u32_e32 v10, vcc, s17, v4
	global_load_dwordx4 v[52:55], v[8:9], off offset:48
	s_nop 0
	v_addc_co_u32_e32 v11, vcc, 0, v5, vcc
	global_load_dwordx4 v[56:59], v[10:11], off offset:2096
	global_load_dwordx4 v[60:63], v[4:5], off offset:32
	global_load_dwordx4 v[64:67], v[6:7], off offset:2080
	global_load_dwordx4 v[68:71], v[8:9], off offset:32
	global_load_dwordx4 v[72:75], v[10:11], off offset:2080
	global_load_dwordx4 v[76:79], v[4:5], off offset:16
	global_load_dwordx4 v[80:83], v[6:7], off offset:2064
	global_load_dwordx4 v[84:87], v[8:9], off offset:16
	global_load_dwordx4 v[88:91], v[10:11], off offset:2064
	global_load_dwordx4 v[92:95], v[4:5], off
	global_load_dwordx4 v[96:99], v[6:7], off offset:2048
	global_load_dwordx4 v[100:103], v[8:9], off
	v_lshl_add_u64 v[4:5], v[24:25], 0, v[2:3]
	global_load_dwordx4 v[104:107], v[10:11], off offset:2048
	global_load_dwordx4 v[108:111], v[4:5], off
	v_lshl_add_u64 v[6:7], v[28:29], 0, v[2:3]
	global_load_dwordx4 v[112:115], v[6:7], off
	v_lshl_add_u64 v[8:9], v[34:35], 0, v[2:3]
	global_load_dwordx4 v[116:119], v[8:9], off
	v_lshl_add_u64 v[24:25], v[40:41], 0, v[2:3]
	global_load_dwordx4 v[120:123], v[24:25], off
	global_load_dwordx4 v[16:19], v[4:5], off offset:16
	global_load_dwordx4 v[12:15], v[6:7], off offset:16
	s_nop 0
	global_load_dwordx4 v[8:11], v[8:9], off offset:16
	s_nop 0
	global_load_dwordx4 v[4:7], v[24:25], off offset:16
	v_lshl_add_u32 v1, v1, 9, v46
	v_add_u32_e32 v23, 0x8100, v1
	s_ashr_i32 s0, s15, 6
	s_cmp_gt_u32 s0, 3
	s_cselect_b64 s[18:19], -1, 0
	s_lshl_b32 s1, s0, 4
	v_and_b32_e32 v2, 31, v20
	s_and_b32 s4, s1, 32
	s_lshl_b32 s1, s0, 5
	v_lshrrev_b32_e32 v21, 5, v22
	s_cmp_lt_u32 s0, 4
	s_cselect_b32 s0, s24, s25
	s_ashr_i32 s17, s16, 31
	s_mov_b64 s[20:21], -1
	s_waitcnt vmcnt(0) lgkmcnt(0)
	v_pk_mul_f32 v[40:41], v[32:33], v[56:57] op_sel_hi:[0,1]
	v_pk_mul_f32 v[34:35], v[38:39], v[44:45] op_sel_hi:[0,1]
	v_pk_mul_f32 v[46:47], v[38:39], v[42:43] op_sel_hi:[0,1]
	v_pk_mul_f32 v[30:31], v[36:37], v[50:51] op_sel_hi:[0,1]
	v_pk_mul_f32 v[44:45], v[36:37], v[48:49] op_sel_hi:[0,1]
	v_pk_mul_f32 v[48:49], v[38:39], v[62:63] op_sel_hi:[0,1]
	v_pk_mul_f32 v[50:51], v[38:39], v[60:61] op_sel_hi:[0,1]
	v_pk_mul_f32 v[28:29], v[26:27], v[54:55] op_sel_hi:[0,1]
	v_pk_mul_f32 v[42:43], v[26:27], v[52:53] op_sel_hi:[0,1]
	v_pk_mul_f32 v[52:53], v[36:37], v[66:67] op_sel_hi:[0,1]
	v_pk_mul_f32 v[54:55], v[36:37], v[64:65] op_sel_hi:[0,1]
	v_pk_mul_f32 v[56:57], v[26:27], v[70:71] op_sel_hi:[0,1]
	v_pk_mul_f32 v[64:65], v[38:39], v[78:79] op_sel_hi:[0,1]
	v_pk_mul_f32 v[66:67], v[38:39], v[76:77] op_sel_hi:[0,1]
	v_pk_mul_f32 v[70:71], v[36:37], v[80:81] op_sel_hi:[0,1]
	v_pk_mul_f32 v[78:79], v[32:33], v[88:89] op_sel_hi:[0,1]
	v_pk_mul_f32 v[80:81], v[38:39], v[94:95] op_sel_hi:[0,1]
	v_pk_mul_f32 v[38:39], v[38:39], v[92:93] op_sel_hi:[0,1]
	v_lshlrev_b32_e32 v88, 16, v108
	v_and_b32_e32 v89, 0xffff0000, v108
	v_pk_mul_f32 v[24:25], v[32:33], v[58:59] op_sel_hi:[0,1]
	v_pk_mul_f32 v[58:59], v[26:27], v[68:69] op_sel_hi:[0,1]
	v_pk_mul_f32 v[68:69], v[36:37], v[82:83] op_sel_hi:[0,1]
	v_pk_mul_f32 v[82:83], v[36:37], v[98:99] op_sel_hi:[0,1]
	v_pk_mul_f32 v[36:37], v[36:37], v[96:97] op_sel_hi:[0,1]
	v_pk_fma_f32 v[38:39], v[38:39], v[88:89], 0 op_sel_hi:[1,1,0]
	v_lshlrev_b32_e32 v88, 16, v112
	v_and_b32_e32 v89, 0xffff0000, v112
	v_pk_mul_f32 v[60:61], v[32:33], v[74:75] op_sel_hi:[0,1]
	v_pk_mul_f32 v[62:63], v[32:33], v[72:73] op_sel_hi:[0,1]
	v_pk_mul_f32 v[72:73], v[26:27], v[86:87] op_sel_hi:[0,1]
	v_pk_mul_f32 v[74:75], v[26:27], v[84:85] op_sel_hi:[0,1]
	v_pk_mul_f32 v[84:85], v[26:27], v[102:103] op_sel_hi:[0,1]
	v_pk_mul_f32 v[26:27], v[26:27], v[100:101] op_sel_hi:[0,1]
	v_pk_fma_f32 v[36:37], v[36:37], v[88:89], v[38:39]
	v_lshlrev_b32_e32 v38, 16, v116
	v_and_b32_e32 v39, 0xffff0000, v116
	v_pk_mul_f32 v[86:87], v[32:33], v[104:105] op_sel_hi:[0,1]
	v_pk_fma_f32 v[26:27], v[26:27], v[38:39], v[36:37]
	v_lshlrev_b32_e32 v36, 16, v120
	v_and_b32_e32 v37, 0xffff0000, v120
	v_pk_fma_f32 v[26:27], v[86:87], v[36:37], v[26:27]
	v_pk_mul_f32 v[76:77], v[32:33], v[90:91] op_sel_hi:[0,1]
	v_mul_f32_e32 v33, 0xbfb8aa3b, v27
	v_exp_f32_e32 v36, v33
	v_mul_f32_e32 v33, 0xbfb8aa3b, v26
	v_exp_f32_e32 v38, v33
	v_and_b32_e32 v39, 0xffff0000, v109
	v_add_f32_e32 v36, 1.0, v36
	v_rcp_f32_e32 v37, v36
	v_add_f32_e32 v36, 1.0, v38
	v_lshlrev_b32_e32 v38, 16, v109
	v_pk_fma_f32 v[38:39], v[80:81], v[38:39], 0 op_sel_hi:[1,1,0]
	v_lshlrev_b32_e32 v80, 16, v113
	v_and_b32_e32 v81, 0xffff0000, v113
	v_pk_fma_f32 v[38:39], v[82:83], v[80:81], v[38:39]
	v_lshlrev_b32_e32 v80, 16, v117
	v_and_b32_e32 v81, 0xffff0000, v117
	v_pk_mul_f32 v[32:33], v[32:33], v[106:107] op_sel_hi:[0,1]
	v_pk_fma_f32 v[38:39], v[84:85], v[80:81], v[38:39]
	v_lshlrev_b32_e32 v80, 16, v121
	v_and_b32_e32 v81, 0xffff0000, v121
	v_pk_fma_f32 v[32:33], v[32:33], v[80:81], v[38:39]
	v_rcp_f32_e32 v36, v36
	v_mul_f32_e32 v38, 0xbfb8aa3b, v33
	v_exp_f32_e32 v38, v38
	v_mul_f32_e32 v39, 0xbfb8aa3b, v32
	v_exp_f32_e32 v80, v39
	v_pk_mul_f32 v[26:27], v[26:27], v[36:37]
	v_add_f32_e32 v38, 1.0, v38
	v_rcp_f32_e32 v39, v38
	v_add_f32_e32 v38, 1.0, v80
	v_rcp_f32_e32 v38, v38
	ds_write2_b32 v23, v26, v27 offset1:1
	v_add_u32_e32 v23, 0x8108, v1
	v_lshlrev_b32_e32 v36, 16, v111
	v_pk_mul_f32 v[26:27], v[32:33], v[38:39]
	ds_write2_b32 v23, v26, v27 offset1:1
	v_lshlrev_b32_e32 v26, 16, v110
	v_and_b32_e32 v27, 0xffff0000, v110
	v_pk_fma_f32 v[26:27], v[66:67], v[26:27], 0 op_sel_hi:[1,1,0]
	v_lshlrev_b32_e32 v32, 16, v114
	v_and_b32_e32 v33, 0xffff0000, v114
	v_pk_fma_f32 v[26:27], v[70:71], v[32:33], v[26:27]
	v_lshlrev_b32_e32 v32, 16, v118
	v_and_b32_e32 v33, 0xffff0000, v118
	v_pk_fma_f32 v[26:27], v[74:75], v[32:33], v[26:27]
	v_lshlrev_b32_e32 v32, 16, v122
	v_and_b32_e32 v33, 0xffff0000, v122
	v_pk_fma_f32 v[26:27], v[78:79], v[32:33], v[26:27]
	v_and_b32_e32 v37, 0xffff0000, v111
	v_mul_f32_e32 v23, 0xbfb8aa3b, v27
	v_exp_f32_e32 v23, v23
	v_mul_f32_e32 v32, 0xbfb8aa3b, v26
	v_exp_f32_e32 v32, v32
	v_pk_fma_f32 v[36:37], v[64:65], v[36:37], 0 op_sel_hi:[1,1,0]
	v_lshlrev_b32_e32 v38, 16, v115
	v_and_b32_e32 v39, 0xffff0000, v115
	v_pk_fma_f32 v[36:37], v[68:69], v[38:39], v[36:37]
	v_lshlrev_b32_e32 v38, 16, v119
	v_and_b32_e32 v39, 0xffff0000, v119
	v_pk_fma_f32 v[36:37], v[72:73], v[38:39], v[36:37]
	v_lshlrev_b32_e32 v38, 16, v123
	v_and_b32_e32 v39, 0xffff0000, v123
	v_add_f32_e32 v23, 1.0, v23
	v_pk_fma_f32 v[36:37], v[76:77], v[38:39], v[36:37]
	v_rcp_f32_e32 v33, v23
	v_add_f32_e32 v23, 1.0, v32
	v_mul_f32_e32 v32, 0xbfb8aa3b, v37
	v_exp_f32_e32 v38, v32
	v_mul_f32_e32 v32, 0xbfb8aa3b, v36
	v_exp_f32_e32 v64, v32
	v_rcp_f32_e32 v32, v23
	v_add_f32_e32 v23, 1.0, v38
	v_rcp_f32_e32 v39, v23
	v_add_f32_e32 v23, 1.0, v64
	v_rcp_f32_e32 v38, v23
	v_add_u32_e32 v66, 0x8110, v1
	v_pk_mul_f32 v[26:27], v[26:27], v[32:33]
	ds_write2_b32 v66, v26, v27 offset1:1
	v_add_u32_e32 v23, 0x8118, v1
	v_pk_mul_f32 v[26:27], v[36:37], v[38:39]
	ds_write2_b32 v23, v26, v27 offset1:1
	v_lshlrev_b32_e32 v26, 16, v16
	v_and_b32_e32 v27, 0xffff0000, v16
	v_pk_fma_f32 v[26:27], v[50:51], v[26:27], 0 op_sel_hi:[1,1,0]
	v_lshlrev_b32_e32 v32, 16, v12
	v_and_b32_e32 v33, 0xffff0000, v12
	v_pk_fma_f32 v[26:27], v[54:55], v[32:33], v[26:27]
	v_lshlrev_b32_e32 v32, 16, v8
	v_and_b32_e32 v33, 0xffff0000, v8
	v_pk_fma_f32 v[26:27], v[58:59], v[32:33], v[26:27]
	v_lshlrev_b32_e32 v32, 16, v4
	v_and_b32_e32 v33, 0xffff0000, v4
	v_pk_fma_f32 v[26:27], v[62:63], v[32:33], v[26:27]
	v_lshlrev_b32_e32 v16, 16, v17
	v_mul_f32_e32 v4, 0xbfb8aa3b, v27
	v_mul_f32_e32 v8, 0xbfb8aa3b, v26
	v_exp_f32_e32 v4, v4
	v_exp_f32_e32 v8, v8
	v_and_b32_e32 v17, 0xffff0000, v17
	v_pk_fma_f32 v[16:17], v[48:49], v[16:17], 0 op_sel_hi:[1,1,0]
	v_lshlrev_b32_e32 v12, 16, v13
	v_and_b32_e32 v13, 0xffff0000, v13
	v_add_f32_e32 v4, 1.0, v4
	v_add_f32_e32 v32, 1.0, v8
	v_pk_fma_f32 v[12:13], v[52:53], v[12:13], v[16:17]
	v_lshlrev_b32_e32 v8, 16, v9
	v_and_b32_e32 v9, 0xffff0000, v9
	v_rcp_f32_e32 v33, v4
	v_pk_fma_f32 v[8:9], v[56:57], v[8:9], v[12:13]
	v_lshlrev_b32_e32 v4, 16, v5
	v_and_b32_e32 v5, 0xffff0000, v5
	v_pk_fma_f32 v[4:5], v[60:61], v[4:5], v[8:9]
	v_rcp_f32_e32 v32, v32
	v_mul_f32_e32 v8, 0xbfb8aa3b, v5
	v_exp_f32_e32 v8, v8
	v_mul_f32_e32 v9, 0xbfb8aa3b, v4
	v_exp_f32_e32 v12, v9
	v_add_u32_e32 v23, 0x8120, v1
	v_add_f32_e32 v8, 1.0, v8
	v_rcp_f32_e32 v9, v8
	v_add_f32_e32 v8, 1.0, v12
	v_rcp_f32_e32 v8, v8
	v_pk_mul_f32 v[12:13], v[26:27], v[32:33]
	ds_write2_b32 v23, v12, v13 offset1:1
	v_add_u32_e32 v12, 0x8128, v1
	v_pk_mul_f32 v[4:5], v[4:5], v[8:9]
	ds_write2_b32 v12, v4, v5 offset1:1
	v_lshlrev_b32_e32 v4, 16, v18
	v_and_b32_e32 v5, 0xffff0000, v18
	v_pk_fma_f32 v[4:5], v[46:47], v[4:5], 0 op_sel_hi:[1,1,0]
	v_lshlrev_b32_e32 v8, 16, v14
	v_and_b32_e32 v9, 0xffff0000, v14
	v_pk_fma_f32 v[4:5], v[44:45], v[8:9], v[4:5]
	v_lshlrev_b32_e32 v8, 16, v10
	v_and_b32_e32 v9, 0xffff0000, v10
	v_pk_fma_f32 v[4:5], v[42:43], v[8:9], v[4:5]
	v_lshlrev_b32_e32 v8, 16, v6
	v_and_b32_e32 v9, 0xffff0000, v6
	v_pk_fma_f32 v[4:5], v[40:41], v[8:9], v[4:5]
	v_lshlrev_b32_e32 v12, 16, v19
	v_mul_f32_e32 v6, 0xbfb8aa3b, v5
	v_exp_f32_e32 v6, v6
	v_and_b32_e32 v13, 0xffff0000, v19
	v_pk_fma_f32 v[12:13], v[34:35], v[12:13], 0 op_sel_hi:[1,1,0]
	v_lshlrev_b32_e32 v14, 16, v15
	v_and_b32_e32 v15, 0xffff0000, v15
	v_add_f32_e32 v6, 1.0, v6
	v_pk_fma_f32 v[12:13], v[30:31], v[14:15], v[12:13]
	v_lshlrev_b32_e32 v10, 16, v11
	v_and_b32_e32 v11, 0xffff0000, v11
	v_rcp_f32_e32 v9, v6
	v_pk_fma_f32 v[10:11], v[28:29], v[10:11], v[12:13]
	v_lshlrev_b32_e32 v6, 16, v7
	v_and_b32_e32 v7, 0xffff0000, v7
	v_pk_fma_f32 v[6:7], v[24:25], v[6:7], v[10:11]
	v_mul_f32_e32 v8, 0xbfb8aa3b, v4
	v_mul_f32_e32 v10, 0xbfb8aa3b, v7
	v_exp_f32_e32 v8, v8
	v_exp_f32_e32 v10, v10
	v_mul_f32_e32 v11, 0xbfb8aa3b, v6
	v_exp_f32_e32 v12, v11
	v_add_f32_e32 v8, 1.0, v8
	v_add_f32_e32 v10, 1.0, v10
	v_rcp_f32_e32 v8, v8
	v_rcp_f32_e32 v11, v10
	v_add_f32_e32 v10, 1.0, v12
	v_rcp_f32_e32 v10, v10
	v_add_u32_e32 v16, 0x8130, v1
	v_pk_mul_f32 v[4:5], v[4:5], v[8:9]
	ds_write2_b32 v16, v4, v5 offset1:1
	v_add_u32_e32 v1, 0x8138, v1
	v_pk_mul_f32 v[4:5], v[6:7], v[10:11]
	ds_write2_b32 v1, v4, v5 offset1:1
	v_or_b32_e32 v1, s4, v2
	v_mul_u32_u24_e32 v1, 0x110, v1
	v_lshlrev_b32_e32 v8, 4, v21
	v_add3_u32 v23, s0, v1, v8
	s_waitcnt lgkmcnt(0)
	s_barrier
	ds_read_b128 v[4:7], v23
	v_and_or_b32 v1, s1, 32, v2
	v_mul_u32_u24_e32 v2, 0x110, v1
	v_add3_u32 v2, s24, v2, v8
	ds_read_b128 v[8:11], v2
	ds_read_b128 v[24:27], v23 offset:32
	ds_read_b128 v[28:31], v2 offset:32
	s_waitcnt lgkmcnt(2)
	v_mfma_f32_32x32x16_bf16 v[4:19], v[4:7], v[8:11], 0
	v_lshl_or_b32 v21, v21, 2, s4
	s_lshl_b64 s[0:1], s[16:17], 13
	s_add_u32 s0, s12, s0
	s_addc_u32 s1, s13, s1
	s_add_u32 s4, s0, 0x46a00000
	s_addc_u32 s5, s1, 0
	s_and_b64 vcc, exec, s[18:19]
	s_waitcnt lgkmcnt(0)
	v_mfma_f32_32x32x16_bf16 v[4:19], v[24:27], v[28:31], v[4:19]
	ds_read_b128 v[24:27], v23 offset:64
	ds_read_b128 v[28:31], v2 offset:64
	ds_read_b128 v[32:35], v23 offset:96
	ds_read_b128 v[36:39], v2 offset:96
	v_cmp_ge_u32_e64 s[0:1], v21, v1
	s_waitcnt lgkmcnt(2)
	v_mfma_f32_32x32x16_bf16 v[4:19], v[24:27], v[28:31], v[4:19]
	s_waitcnt lgkmcnt(0)
	v_mfma_f32_32x32x16_bf16 v[4:19], v[32:35], v[36:39], v[4:19]
	ds_read_b128 v[24:27], v23 offset:128
	ds_read_b128 v[28:31], v2 offset:128
	ds_read_b128 v[32:35], v23 offset:160
	ds_read_b128 v[36:39], v2 offset:160
	s_waitcnt lgkmcnt(2)
	v_mfma_f32_32x32x16_bf16 v[4:19], v[24:27], v[28:31], v[4:19]
	s_waitcnt lgkmcnt(0)
	v_mfma_f32_32x32x16_bf16 v[4:19], v[32:35], v[36:39], v[4:19]
	ds_read_b128 v[24:27], v23 offset:192
	ds_read_b128 v[28:31], v2 offset:192
	ds_read_b128 v[32:35], v23 offset:224
	ds_read_b128 v[36:39], v2 offset:224
	v_lshl_add_u32 v2, v1, 2, s28
	v_lshl_add_u32 v23, v21, 2, s28
	s_waitcnt lgkmcnt(2)
	v_mfma_f32_32x32x16_bf16 v[4:19], v[24:27], v[28:31], v[4:19]
	ds_read_b32 v25, v2
	ds_read_b32 v2, v23
	v_lshlrev_b32_e32 v24, 1, v1
	s_waitcnt lgkmcnt(0)
	v_sub_f32_e32 v2, v2, v25
	v_min_f32_e32 v2, 0, v2
	v_mfma_f32_32x32x16_bf16 v[4:19], v[32:35], v[36:39], v[4:19]
	v_mul_f32_e32 v2, 0x3fb8aa3b, v2
	v_exp_f32_e32 v26, v2
	s_cbranch_vccz .LBB0_266
	s_nop 8
	v_mul_f32_e32 v2, v4, v26
	v_cvt_pk_bf16_f32 v2, v2, s0
	v_cndmask_b32_e64 v23, 0, v2, s[0:1]
	v_lshl_or_b32 v2, v21, 7, v24
	v_lshl_add_u64 v[28:29], s[4:5], 0, v[2:3]
	global_store_short v[28:29], v23, off
	s_mov_b64 s[20:21], 0

.LBB0_270:
	s_nop 3
	v_or_b32_e32 v4, 1, v21
	v_lshl_add_u32 v2, v4, 2, s28
	ds_read_b32 v2, v2
	s_andn2_b64 vcc, exec, s[18:19]
	s_waitcnt lgkmcnt(0)
	v_sub_f32_e32 v2, v2, v25
	v_min_f32_e32 v2, 0, v2
	v_mul_f32_e32 v2, 0x3fb8aa3b, v2
	v_exp_f32_e32 v26, v2
	v_cndmask_b32_e64 v2, 0, 1, s[18:19]
	v_cmp_ne_u32_e64 s[0:1], 1, v2
	s_mov_b64 s[18:19], -1
	s_cbranch_vccnz .LBB0_272
	v_mul_f32_e32 v2, v5, v26
	v_cvt_pk_bf16_f32 v2, v2, s0
	v_cmp_ge_u32_e32 vcc, v4, v1
	s_mov_b64 s[18:19], 0
	s_nop 0
	v_cndmask_b32_e32 v27, 0, v2, vcc
	v_lshl_or_b32 v2, v4, 7, v24
	v_lshl_add_u64 v[28:29], s[4:5], 0, v[2:3]
	global_store_short v[28:29], v27, off

.LBB0_276:
	v_or_b32_e32 v4, 2, v21
	v_lshl_add_u32 v2, v4, 2, s28
	ds_read_b32 v2, v2
	s_and_b64 vcc, exec, s[0:1]
	s_mov_b64 s[18:19], -1
	s_waitcnt lgkmcnt(0)
	v_sub_f32_e32 v2, v2, v25
	v_min_f32_e32 v2, 0, v2
	v_mul_f32_e32 v2, 0x3fb8aa3b, v2
	v_exp_f32_e32 v5, v2
	s_cbranch_vccnz .LBB0_278
	v_mul_f32_e32 v2, v6, v5
	v_cvt_pk_bf16_f32 v2, v2, s0
	v_cmp_ge_u32_e32 vcc, v4, v1
	s_mov_b64 s[18:19], 0
	s_nop 0
	v_cndmask_b32_e32 v28, 0, v2, vcc
	v_lshl_or_b32 v2, v4, 7, v24
	v_lshl_add_u64 v[26:27], s[4:5], 0, v[2:3]
	global_store_short v[26:27], v28, off

.LBB0_282:
	v_or_b32_e32 v4, 3, v21
	v_lshl_add_u32 v2, v4, 2, s28
	ds_read_b32 v2, v2
	s_and_b64 vcc, exec, s[0:1]
	s_mov_b64 s[18:19], -1
	s_waitcnt lgkmcnt(0)
	v_sub_f32_e32 v2, v2, v25
	v_min_f32_e32 v2, 0, v2
	v_mul_f32_e32 v2, 0x3fb8aa3b, v2
	v_exp_f32_e32 v5, v2
	s_cbranch_vccnz .LBB0_284
	v_mul_f32_e32 v2, v7, v5
	v_cvt_pk_bf16_f32 v2, v2, s0
	v_cmp_ge_u32_e32 vcc, v4, v1
	s_mov_b64 s[18:19], 0
	s_nop 0
	v_cndmask_b32_e32 v6, 0, v2, vcc
	v_lshl_or_b32 v2, v4, 7, v24
	v_lshl_add_u64 v[26:27], s[4:5], 0, v[2:3]
	global_store_short v[26:27], v6, off

.LBB0_288:
	v_or_b32_e32 v4, 8, v21
	v_lshl_add_u32 v2, v4, 2, s28
	ds_read_b32 v2, v2
	s_and_b64 vcc, exec, s[0:1]
	s_mov_b64 s[18:19], -1
	s_waitcnt lgkmcnt(0)
	v_sub_f32_e32 v2, v2, v25
	v_min_f32_e32 v2, 0, v2
	v_mul_f32_e32 v2, 0x3fb8aa3b, v2
	v_exp_f32_e32 v5, v2
	s_cbranch_vccnz .LBB0_290
	v_mul_f32_e32 v2, v8, v5
	v_cvt_pk_bf16_f32 v2, v2, s0
	v_cmp_ge_u32_e32 vcc, v4, v1
	s_mov_b64 s[18:19], 0
	s_nop 0
	v_cndmask_b32_e32 v26, 0, v2, vcc
	v_lshl_or_b32 v2, v4, 7, v24
	v_lshl_add_u64 v[6:7], s[4:5], 0, v[2:3]
	global_store_short v[6:7], v26, off

.LBB0_294:
	v_or_b32_e32 v4, 9, v21
	v_lshl_add_u32 v2, v4, 2, s28
	ds_read_b32 v2, v2
	s_and_b64 vcc, exec, s[0:1]
	s_mov_b64 s[18:19], -1
	s_waitcnt lgkmcnt(0)
	v_sub_f32_e32 v2, v2, v25
	v_min_f32_e32 v2, 0, v2
	v_mul_f32_e32 v2, 0x3fb8aa3b, v2
	v_exp_f32_e32 v5, v2
	s_cbranch_vccnz .LBB0_296
	v_mul_f32_e32 v2, v9, v5
	v_cvt_pk_bf16_f32 v2, v2, s0
	v_cmp_ge_u32_e32 vcc, v4, v1
	s_mov_b64 s[18:19], 0
	s_nop 0
	v_cndmask_b32_e32 v8, 0, v2, vcc
	v_lshl_or_b32 v2, v4, 7, v24
	v_lshl_add_u64 v[6:7], s[4:5], 0, v[2:3]
	global_store_short v[6:7], v8, off

.LBB0_300:
	v_or_b32_e32 v4, 10, v21
	v_lshl_add_u32 v2, v4, 2, s28
	ds_read_b32 v2, v2
	s_and_b64 vcc, exec, s[0:1]
	s_mov_b64 s[18:19], -1
	s_waitcnt lgkmcnt(0)
	v_sub_f32_e32 v2, v2, v25
	v_min_f32_e32 v2, 0, v2
	v_mul_f32_e32 v2, 0x3fb8aa3b, v2
	v_exp_f32_e32 v5, v2
	s_cbranch_vccnz .LBB0_302
	v_mul_f32_e32 v2, v10, v5
	v_cvt_pk_bf16_f32 v2, v2, s0
	v_cmp_ge_u32_e32 vcc, v4, v1
	s_mov_b64 s[18:19], 0
	s_nop 0
	v_cndmask_b32_e32 v8, 0, v2, vcc
	v_lshl_or_b32 v2, v4, 7, v24
	v_lshl_add_u64 v[6:7], s[4:5], 0, v[2:3]
	global_store_short v[6:7], v8, off

.LBB0_306:
	v_or_b32_e32 v4, 11, v21
	v_lshl_add_u32 v2, v4, 2, s28
	ds_read_b32 v2, v2
	s_and_b64 vcc, exec, s[0:1]
	s_mov_b64 s[18:19], -1
	s_waitcnt lgkmcnt(0)
	v_sub_f32_e32 v2, v2, v25
	v_min_f32_e32 v2, 0, v2
	v_mul_f32_e32 v2, 0x3fb8aa3b, v2
	v_exp_f32_e32 v5, v2
	s_cbranch_vccnz .LBB0_308
	v_mul_f32_e32 v2, v11, v5
	v_cvt_pk_bf16_f32 v2, v2, s0
	v_cmp_ge_u32_e32 vcc, v4, v1
	s_mov_b64 s[18:19], 0
	s_nop 0
	v_cndmask_b32_e32 v8, 0, v2, vcc
	v_lshl_or_b32 v2, v4, 7, v24
	v_lshl_add_u64 v[6:7], s[4:5], 0, v[2:3]
	global_store_short v[6:7], v8, off

.LBB0_312:
	v_or_b32_e32 v4, 16, v21
	v_lshl_add_u32 v2, v4, 2, s28
	ds_read_b32 v2, v2
	s_and_b64 vcc, exec, s[0:1]
	s_mov_b64 s[18:19], -1
	s_waitcnt lgkmcnt(0)
	v_sub_f32_e32 v2, v2, v25
	v_min_f32_e32 v2, 0, v2
	v_mul_f32_e32 v2, 0x3fb8aa3b, v2
	v_exp_f32_e32 v5, v2
	s_cbranch_vccnz .LBB0_314
	v_mul_f32_e32 v2, v12, v5
	v_cvt_pk_bf16_f32 v2, v2, s0
	v_cmp_ge_u32_e32 vcc, v4, v1
	s_mov_b64 s[18:19], 0
	s_nop 0
	v_cndmask_b32_e32 v8, 0, v2, vcc
	v_lshl_or_b32 v2, v4, 7, v24
	v_lshl_add_u64 v[6:7], s[4:5], 0, v[2:3]
	global_store_short v[6:7], v8, off

.LBB0_318:
	v_or_b32_e32 v4, 17, v21
	v_lshl_add_u32 v2, v4, 2, s28
	ds_read_b32 v2, v2
	s_and_b64 vcc, exec, s[0:1]
	s_mov_b64 s[18:19], -1
	s_waitcnt lgkmcnt(0)
	v_sub_f32_e32 v2, v2, v25
	v_min_f32_e32 v2, 0, v2
	v_mul_f32_e32 v2, 0x3fb8aa3b, v2
	v_exp_f32_e32 v5, v2
	s_cbranch_vccnz .LBB0_320
	v_mul_f32_e32 v2, v13, v5
	v_cvt_pk_bf16_f32 v2, v2, s0
	v_cmp_ge_u32_e32 vcc, v4, v1
	s_mov_b64 s[18:19], 0
	s_nop 0
	v_cndmask_b32_e32 v8, 0, v2, vcc
	v_lshl_or_b32 v2, v4, 7, v24
	v_lshl_add_u64 v[6:7], s[4:5], 0, v[2:3]
	global_store_short v[6:7], v8, off

.LBB0_324:
	v_or_b32_e32 v4, 18, v21
	v_lshl_add_u32 v2, v4, 2, s28
	ds_read_b32 v2, v2
	s_and_b64 vcc, exec, s[0:1]
	s_mov_b64 s[18:19], -1
	s_waitcnt lgkmcnt(0)
	v_sub_f32_e32 v2, v2, v25
	v_min_f32_e32 v2, 0, v2
	v_mul_f32_e32 v2, 0x3fb8aa3b, v2
	v_exp_f32_e32 v5, v2
	s_cbranch_vccnz .LBB0_326
	v_mul_f32_e32 v2, v14, v5
	v_cvt_pk_bf16_f32 v2, v2, s0
	v_cmp_ge_u32_e32 vcc, v4, v1
	s_mov_b64 s[18:19], 0
	s_nop 0
	v_cndmask_b32_e32 v8, 0, v2, vcc
	v_lshl_or_b32 v2, v4, 7, v24
	v_lshl_add_u64 v[6:7], s[4:5], 0, v[2:3]
	global_store_short v[6:7], v8, off

.LBB0_330:
	v_or_b32_e32 v4, 19, v21
	v_lshl_add_u32 v2, v4, 2, s28
	ds_read_b32 v2, v2
	s_and_b64 vcc, exec, s[0:1]
	s_mov_b64 s[18:19], -1
	s_waitcnt lgkmcnt(0)
	v_sub_f32_e32 v2, v2, v25
	v_min_f32_e32 v2, 0, v2
	v_mul_f32_e32 v2, 0x3fb8aa3b, v2
	v_exp_f32_e32 v5, v2
	s_cbranch_vccnz .LBB0_332
	v_mul_f32_e32 v2, v15, v5
	v_cvt_pk_bf16_f32 v2, v2, s0
	v_cmp_ge_u32_e32 vcc, v4, v1
	s_mov_b64 s[18:19], 0
	s_nop 0
	v_cndmask_b32_e32 v8, 0, v2, vcc
	v_lshl_or_b32 v2, v4, 7, v24
	v_lshl_add_u64 v[6:7], s[4:5], 0, v[2:3]
	global_store_short v[6:7], v8, off

.LBB0_336:
	v_or_b32_e32 v4, 24, v21
	v_lshl_add_u32 v2, v4, 2, s28
	ds_read_b32 v2, v2
	s_and_b64 vcc, exec, s[0:1]
	s_mov_b64 s[18:19], -1
	s_waitcnt lgkmcnt(0)
	v_sub_f32_e32 v2, v2, v25
	v_min_f32_e32 v2, 0, v2
	v_mul_f32_e32 v2, 0x3fb8aa3b, v2
	v_exp_f32_e32 v5, v2
	s_cbranch_vccnz .LBB0_338
	v_mul_f32_e32 v2, v16, v5
	v_cvt_pk_bf16_f32 v2, v2, s0
	v_cmp_ge_u32_e32 vcc, v4, v1
	s_mov_b64 s[18:19], 0
	s_nop 0
	v_cndmask_b32_e32 v8, 0, v2, vcc
	v_lshl_or_b32 v2, v4, 7, v24
	v_lshl_add_u64 v[6:7], s[4:5], 0, v[2:3]
	global_store_short v[6:7], v8, off

.LBB0_342:
	v_or_b32_e32 v4, 25, v21
	v_lshl_add_u32 v2, v4, 2, s28
	ds_read_b32 v2, v2
	s_and_b64 vcc, exec, s[0:1]
	s_mov_b64 s[18:19], -1
	s_waitcnt lgkmcnt(0)
	v_sub_f32_e32 v2, v2, v25
	v_min_f32_e32 v2, 0, v2
	v_mul_f32_e32 v2, 0x3fb8aa3b, v2
	v_exp_f32_e32 v5, v2
	s_cbranch_vccnz .LBB0_344
	v_mul_f32_e32 v2, v17, v5
	v_cvt_pk_bf16_f32 v2, v2, s0
	v_cmp_ge_u32_e32 vcc, v4, v1
	s_mov_b64 s[18:19], 0
	s_nop 0
	v_cndmask_b32_e32 v8, 0, v2, vcc
	v_lshl_or_b32 v2, v4, 7, v24
	v_lshl_add_u64 v[6:7], s[4:5], 0, v[2:3]
	global_store_short v[6:7], v8, off

.LBB0_348:
	v_or_b32_e32 v4, 26, v21
	v_lshl_add_u32 v2, v4, 2, s28
	ds_read_b32 v2, v2
	s_and_b64 vcc, exec, s[0:1]
	s_mov_b64 s[18:19], -1
	s_waitcnt lgkmcnt(0)
	v_sub_f32_e32 v2, v2, v25
	v_min_f32_e32 v2, 0, v2
	v_mul_f32_e32 v2, 0x3fb8aa3b, v2
	v_exp_f32_e32 v5, v2
	s_cbranch_vccnz .LBB0_350
	v_mul_f32_e32 v2, v18, v5
	v_cvt_pk_bf16_f32 v2, v2, s0
	v_cmp_ge_u32_e32 vcc, v4, v1
	s_mov_b64 s[18:19], 0
	s_nop 0
	v_cndmask_b32_e32 v8, 0, v2, vcc
	v_lshl_or_b32 v2, v4, 7, v24
	v_lshl_add_u64 v[6:7], s[4:5], 0, v[2:3]
	global_store_short v[6:7], v8, off

.LBB0_354:
	v_or_b32_e32 v4, 27, v21
	v_lshl_add_u32 v2, v4, 2, s28
	ds_read_b32 v2, v2
	s_and_b64 vcc, exec, s[0:1]
	s_mov_b64 s[0:1], -1
	s_waitcnt lgkmcnt(0)
	v_sub_f32_e32 v2, v2, v25
	v_min_f32_e32 v2, 0, v2
	v_mul_f32_e32 v2, 0x3fb8aa3b, v2
	v_exp_f32_e32 v5, v2
	s_cbranch_vccnz .LBB0_356
	v_mul_f32_e32 v2, v19, v5
	v_cvt_pk_bf16_f32 v2, v2, s0
	v_cmp_ge_u32_e32 vcc, v4, v1
	s_mov_b64 s[0:1], 0
	s_nop 0
	v_cndmask_b32_e32 v8, 0, v2, vcc
	v_lshl_or_b32 v2, v4, 7, v24
	v_lshl_add_u64 v[6:7], s[4:5], 0, v[2:3]
	global_store_short v[6:7], v8, off

.LBB0_362:
	v_add_u32_e32 v1, s4, v20
	v_add_u32_e32 v2, 0xffffff00, v1
	v_ashrrev_i32_e32 v8, 7, v2
	v_mad_u64_u32 v[10:11], s[18:19], v8, s20, v[4:5]
	ds_read_u16 v2, v10
	v_lshl_add_u32 v5, v8, 2, s29
	ds_read_b32 v5, v5
	v_ashrrev_i32_e32 v9, 31, v8
	v_lshlrev_b64 v[8:9], 10, v[8:9]
	s_waitcnt lgkmcnt(0)
	v_lshlrev_b32_e32 v2, 16, v2
	v_lshl_add_u64 v[8:9], v[6:7], 0, v[8:9]
	v_mul_f32_e32 v2, v5, v2
	v_cvt_pk_bf16_f32 v2, v2, s0
	global_store_short v[8:9], v2, off
	v_ashrrev_i32_e32 v8, 7, v1
	v_mad_u64_u32 v[10:11], s[18:19], v8, s20, v[4:5]
	ds_read_u16 v2, v10
	v_lshl_add_u32 v5, v8, 2, s29
	ds_read_b32 v5, v5
	v_ashrrev_i32_e32 v9, 31, v8
	v_lshlrev_b64 v[8:9], 10, v[8:9]
	s_waitcnt lgkmcnt(0)
	v_lshlrev_b32_e32 v2, 16, v2
	v_lshl_add_u64 v[8:9], v[6:7], 0, v[8:9]
	v_mul_f32_e32 v2, v5, v2
	v_cvt_pk_bf16_f32 v2, v2, s0
	global_store_short v[8:9], v2, off
	v_add_u32_e32 v2, 0x100, v1
	v_ashrrev_i32_e32 v8, 7, v2
	v_mad_u64_u32 v[10:11], s[18:19], v8, s20, v[4:5]
	ds_read_u16 v2, v10
	v_lshl_add_u32 v5, v8, 2, s29
	ds_read_b32 v5, v5
	v_ashrrev_i32_e32 v9, 31, v8
	v_lshlrev_b64 v[8:9], 10, v[8:9]
	s_waitcnt lgkmcnt(0)
	v_lshlrev_b32_e32 v2, 16, v2
	v_lshl_add_u64 v[8:9], v[6:7], 0, v[8:9]
	v_mul_f32_e32 v2, v5, v2
	v_cvt_pk_bf16_f32 v2, v2, s0
	v_add_u32_e32 v1, 0x200, v1
	global_store_short v[8:9], v2, off
	v_ashrrev_i32_e32 v8, 7, v1
	v_mad_u64_u32 v[10:11], s[18:19], v8, s20, v[4:5]
	ds_read_u16 v1, v10
	v_lshl_add_u32 v2, v8, 2, s29
	ds_read_b32 v2, v2
	v_ashrrev_i32_e32 v9, 31, v8
	v_lshlrev_b64 v[8:9], 10, v[8:9]
	s_waitcnt lgkmcnt(0)
	v_lshlrev_b32_e32 v1, 16, v1
	s_addk_i32 s4, 0x400
	v_mul_f32_e32 v1, v2, v1
	v_cvt_pk_bf16_f32 v1, v1, s0
	v_lshl_add_u64 v[8:9], v[6:7], 0, v[8:9]
	s_cmpk_eq_i32 s4, 0x2000
	global_store_short v[8:9], v1, off
	s_cbranch_scc0 .LBB0_362
	v_lshl_add_u32 v1, v22, 2, s28
	ds_read_b32 v1, v1
	s_lshl_b64 s[4:5], s[16:17], 14
	s_add_u32 s4, s12, s4
	s_addc_u32 s5, s13, s5
	v_add_u32_e32 v2, 0xffffff00, v20
	s_waitcnt lgkmcnt(0)
	v_sub_f32_e32 v1, v12, v1
	v_mul_f32_e32 v1, 0x3fb8aa3b, v1
	v_exp_f32_e32 v4, v1
	s_add_u32 s4, s4, 0x45a00000
	v_mov_b32_e32 v1, s33
	s_movk_i32 s15, 0x204
	v_add_u32_e32 v6, 0x100, v20
	v_add_u32_e32 v8, 0x300, v20
	v_add_u32_e32 v10, 0x500, v20
	s_addc_u32 s5, s5, 0
	v_mad_u32_u24 v14, v22, s15, v1
	v_mov_b32_e32 v5, v4
	v_mov_b32_e32 v1, v2
	v_mov_b32_e32 v7, v22
	v_mov_b32_e32 v9, v6
	v_mov_b32_e32 v11, v8
	v_mov_b32_e32 v13, v10
	s_mov_b32 s15, 1
	s_mov_b32 s18, 0
	s_mov_b32 s19, 32
.LBB0_364:
	s_lshl_b32 s20, s18, 8
	s_lshl_b32 s21, s15, 8
	v_add_u32_e32 v18, s20, v2
	v_add_u32_e32 v15, s21, v1
	v_ashrrev_i32_e32 v17, 6, v18
	v_ashrrev_i32_e32 v16, 6, v15
	v_lshl_add_u32 v17, v17, 2, v14
	v_lshl_add_u32 v19, v16, 2, v14
	ds_read_b32 v16, v17
	ds_read_b32 v17, v19
	v_and_b32_e32 v15, 0xffffffc0, v15
	s_add_i32 s18, s18, 8
	s_add_i32 s15, s15, 8
	s_add_i32 s19, s19, -8
	s_waitcnt lgkmcnt(0)
	v_pk_mul_f32 v[16:17], v[4:5], v[16:17]
	s_cmp_eq_u32 s19, 0
	v_cvt_pk_bf16_f32 v20, v16, v17
	v_and_b32_e32 v17, 0xffffffc0, v18
	v_or_b32_e32 v18, v17, v22
	v_or_b32_e32 v16, v15, v7
	v_ashrrev_i32_e32 v19, 31, v18
	v_ashrrev_i32_e32 v17, 31, v16
	v_lshl_add_u64 v[18:19], v[18:19], 1, s[4:5]
	v_lshl_add_u64 v[16:17], v[16:17], 1, s[4:5]
	global_store_short v[18:19], v20, off
	global_store_short_d16_hi v[16:17], v20, off
	v_add_u32_e32 v18, s20, v6
	v_add_u32_e32 v15, s21, v9
	v_ashrrev_i32_e32 v17, 6, v18
	v_ashrrev_i32_e32 v16, 6, v15
	v_lshl_add_u32 v17, v17, 2, v14
	v_lshl_add_u32 v19, v16, 2, v14
	ds_read_b32 v16, v17
	ds_read_b32 v17, v19
	v_and_b32_e32 v15, 0xffffffc0, v15
	s_waitcnt lgkmcnt(0)
	v_pk_mul_f32 v[16:17], v[4:5], v[16:17]
	s_nop 0
	v_cvt_pk_bf16_f32 v20, v16, v17
	v_and_b32_e32 v17, 0xffffffc0, v18
	v_or_b32_e32 v18, v17, v22
	v_or_b32_e32 v16, v15, v7
	v_ashrrev_i32_e32 v19, 31, v18
	v_ashrrev_i32_e32 v17, 31, v16
	v_lshl_add_u64 v[18:19], v[18:19], 1, s[4:5]
	v_lshl_add_u64 v[16:17], v[16:17], 1, s[4:5]
	global_store_short v[18:19], v20, off
	global_store_short_d16_hi v[16:17], v20, off
	v_add_u32_e32 v18, s20, v8
	v_add_u32_e32 v15, s21, v11
	v_ashrrev_i32_e32 v17, 6, v18
	v_ashrrev_i32_e32 v16, 6, v15
	v_lshl_add_u32 v17, v17, 2, v14
	v_lshl_add_u32 v19, v16, 2, v14
	ds_read_b32 v16, v17
	ds_read_b32 v17, v19
	v_and_b32_e32 v15, 0xffffffc0, v15
	s_waitcnt lgkmcnt(0)
	v_pk_mul_f32 v[16:17], v[4:5], v[16:17]
	s_nop 0
	v_cvt_pk_bf16_f32 v20, v16, v17
	v_and_b32_e32 v17, 0xffffffc0, v18
	v_or_b32_e32 v18, v17, v22
	v_or_b32_e32 v16, v15, v7
	v_ashrrev_i32_e32 v19, 31, v18
	v_ashrrev_i32_e32 v17, 31, v16
	v_lshl_add_u64 v[18:19], v[18:19], 1, s[4:5]
	v_lshl_add_u64 v[16:17], v[16:17], 1, s[4:5]
	global_store_short v[18:19], v20, off
	global_store_short_d16_hi v[16:17], v20, off
	v_add_u32_e32 v18, s20, v10
	v_add_u32_e32 v15, s21, v13
	v_ashrrev_i32_e32 v17, 6, v18
	v_ashrrev_i32_e32 v16, 6, v15
	v_lshl_add_u32 v17, v17, 2, v14
	v_lshl_add_u32 v19, v16, 2, v14
	ds_read_b32 v16, v17
	ds_read_b32 v17, v19
	v_and_b32_e32 v15, 0xffffffc0, v15
	s_waitcnt lgkmcnt(0)
	v_pk_mul_f32 v[16:17], v[4:5], v[16:17]
	s_nop 0
	v_cvt_pk_bf16_f32 v20, v16, v17
	v_and_b32_e32 v17, 0xffffffc0, v18
	v_or_b32_e32 v18, v17, v22
	v_or_b32_e32 v16, v15, v7
	v_ashrrev_i32_e32 v19, 31, v18
	v_ashrrev_i32_e32 v17, 31, v16
	v_lshl_add_u64 v[18:19], v[18:19], 1, s[4:5]
	v_lshl_add_u64 v[16:17], v[16:17], 1, s[4:5]
	global_store_short v[18:19], v20, off
	global_store_short_d16_hi v[16:17], v20, off
	s_cbranch_scc0 .LBB0_364
	v_cmp_eq_u32_e32 vcc, 0, v2
	s_and_saveexec_b64 s[4:5], vcc
	s_xor_b64 s[4:5], exec, s[4:5]
	s_cbranch_execz .LBB0_367
	s_lshl_b64 s[16:17], s[16:17], 2
	v_mul_f32_e32 v1, 0x3fb8aa3b, v12
	s_add_u32 s15, s12, s16
	v_exp_f32_e32 v1, v1
	s_addc_u32 s16, s13, s17
	v_mov_b32_e32 v2, s15
	v_add_co_u32_e32 v4, vcc, 0x49250000, v2
	v_mov_b32_e32 v2, s16
	s_nop 0
	v_addc_co_u32_e32 v5, vcc, 0, v2, vcc
	global_store_dword v[4:5], v1, off

.LBB0_373:
	s_or_b64 exec, exec, s[4:5]
	v_mov_b32_e32 v1, v3
	s_nop 0
	v_lshl_add_u32 v21, v1, 2, s26
	ds_read_b128 v[70:73], v21
	ds_read_b128 v[74:77], v21 offset:16
	ds_read_b128 v[78:81], v21 offset:32
	ds_read_b128 v[82:85], v21 offset:48
	ds_read_b128 v[86:89], v21 offset:64
	ds_read_b128 v[90:93], v21 offset:80
	ds_read_b128 v[94:97], v21 offset:96
	ds_read_b128 v[98:101], v21 offset:112
	ds_read_b128 v[102:105], v21 offset:128
	ds_read_b128 v[106:109], v21 offset:144
	ds_read_b128 v[110:113], v21 offset:160
	ds_read_b128 v[114:117], v21 offset:176
	ds_read_b128 v[118:121], v21 offset:192
	ds_read_b128 v[122:125], v21 offset:208
	ds_read_b128 v[126:129], v21 offset:224
	ds_read_b128 v[130:133], v21 offset:240
	ds_read_b128 v[134:137], v21 offset:272
	ds_read_b128 v[138:141], v21 offset:288
	ds_read_b128 v[142:145], v21 offset:304
	ds_read_b128 v[146:149], v21 offset:320
	ds_read_b128 v[150:153], v21 offset:336
	ds_read_b128 v[154:157], v21 offset:352
	ds_read_b128 v[158:161], v21 offset:368
	ds_read_b128 v[162:165], v21 offset:384
	ds_read_b128 v[166:169], v21 offset:400
	ds_read_b128 v[170:173], v21 offset:416
	ds_read_b128 v[174:177], v21 offset:432
	ds_read_b128 v[178:181], v21 offset:448
	ds_read_b128 v[182:185], v21 offset:464
	ds_read_b128 v[186:189], v21 offset:480
	ds_read_b128 v[194:197], v21 offset:496
	ds_read_b128 v[198:201], v21 offset:512
	s_waitcnt lgkmcnt(0)
	v_fma_f32 v1, -v4, v70, v4
	v_fma_f32 v2, -v4, v71, v5
	v_fma_f32 v5, -v4, v72, v6
	v_fma_f32 v6, -v4, v73, v7
	v_fma_f32 v7, -v4, v74, v8
	v_fma_f32 v74, -v4, v75, v9
	v_fma_f32 v75, -v4, v76, v10
	v_fma_f32 v76, -v4, v77, v11
	v_fma_f32 v77, -v4, v78, v12
	v_fma_f32 v78, -v4, v79, v13
	v_fma_f32 v79, -v4, v80, v14
	v_fma_f32 v80, -v4, v81, v15
	v_fma_f32 v81, -v4, v82, v16
	v_fma_f32 v82, -v4, v83, v17
	v_fma_f32 v83, -v4, v84, v18
	v_fma_f32 v84, -v4, v85, v19
	v_fma_f32 v85, -v4, v86, v22
	v_fma_f32 v86, -v4, v87, v23
	v_fma_f32 v87, -v4, v88, v24
	v_fma_f32 v88, -v4, v89, v25
	v_fma_f32 v89, -v4, v90, v26
	v_fma_f32 v90, -v4, v91, v27
	v_fma_f32 v91, -v4, v92, v28
	v_fma_f32 v92, -v4, v93, v29
	v_fma_f32 v93, -v4, v94, v30
	v_fma_f32 v94, -v4, v95, v31
	v_fma_f32 v95, -v4, v96, v32
	v_fma_f32 v96, -v4, v97, v33
	v_fma_f32 v97, -v4, v98, v34
	v_fma_f32 v98, -v4, v99, v35
	v_fma_f32 v99, -v4, v100, v36
	v_fma_f32 v100, -v4, v101, v37
	v_fma_f32 v101, -v4, v102, v38
	v_fma_f32 v102, -v4, v103, v39
	v_fma_f32 v103, -v4, v104, v40
	v_fma_f32 v104, -v4, v105, v41
	v_fma_f32 v105, -v4, v106, v42
	v_fma_f32 v106, -v4, v107, v43
	v_fma_f32 v107, -v4, v108, v44
	v_fma_f32 v108, -v4, v109, v45
	v_fma_f32 v109, -v4, v110, v46
	v_fma_f32 v110, -v4, v111, v47
	v_fma_f32 v111, -v4, v112, v48
	v_fma_f32 v112, -v4, v113, v49
	v_fma_f32 v113, -v4, v114, v50
	v_fma_f32 v114, -v4, v115, v51
	v_fma_f32 v115, -v4, v116, v52
	v_fma_f32 v116, -v4, v117, v53
	v_fma_f32 v117, -v4, v118, v54
	v_fma_f32 v118, -v4, v119, v55
	v_fma_f32 v119, -v4, v120, v56
	v_fma_f32 v120, -v4, v121, v57
	v_fma_f32 v121, -v4, v122, v58
	v_fma_f32 v122, -v4, v123, v59
	v_fma_f32 v123, -v4, v124, v60
	v_fma_f32 v124, -v4, v125, v61
	v_fma_f32 v125, -v4, v126, v62
	v_fma_f32 v126, -v4, v127, v63
	v_fma_f32 v127, -v4, v128, v64
	v_fma_f32 v128, -v4, v129, v65
	v_fma_f32 v129, -v4, v130, v66
	v_fma_f32 v130, -v4, v131, v67
	v_fma_f32 v131, -v4, v132, v68
	v_fma_f32 v4, -v4, v133, v69
	ds_read_b128 v[8:11], v21 offset:544
	ds_read_b128 v[12:15], v21 offset:560
	ds_read_b128 v[16:19], v21 offset:576
	ds_read_b128 v[22:25], v21 offset:592
	ds_read_b128 v[26:29], v21 offset:608
	ds_read_b128 v[30:33], v21 offset:624
	ds_read_b128 v[34:37], v21 offset:640
	ds_read_b128 v[38:41], v21 offset:656
	ds_read_b128 v[42:45], v21 offset:672
	ds_read_b128 v[46:49], v21 offset:688
	ds_read_b128 v[50:53], v21 offset:704
	ds_read_b128 v[54:57], v21 offset:720
	ds_read_b128 v[58:61], v21 offset:736
	ds_read_b128 v[62:65], v21 offset:752
	ds_read_b128 v[66:69], v21 offset:768
	ds_read_b128 v[70:73], v21 offset:784
	v_fma_f32 v1, -v2, v134, v1
	v_fma_f32 v134, -v2, v135, v2
	v_fma_f32 v5, -v2, v136, v5
	v_fma_f32 v135, -v2, v137, v6
	v_fma_f32 v136, -v2, v138, v7
	v_fma_f32 v137, -v2, v139, v74
	v_fma_f32 v138, -v2, v140, v75
	v_fma_f32 v139, -v2, v141, v76
	v_fma_f32 v140, -v2, v142, v77
	v_fma_f32 v141, -v2, v143, v78
	v_fma_f32 v142, -v2, v144, v79
	v_fma_f32 v143, -v2, v145, v80
	v_fma_f32 v144, -v2, v146, v81
	v_fma_f32 v145, -v2, v147, v82
	v_fma_f32 v146, -v2, v148, v83
	v_fma_f32 v147, -v2, v149, v84
	v_fma_f32 v148, -v2, v150, v85
	v_fma_f32 v149, -v2, v151, v86
	v_fma_f32 v150, -v2, v152, v87
	v_fma_f32 v151, -v2, v153, v88
	v_fma_f32 v152, -v2, v154, v89
	v_fma_f32 v153, -v2, v155, v90
	v_fma_f32 v154, -v2, v156, v91
	v_fma_f32 v155, -v2, v157, v92
	v_fma_f32 v156, -v2, v158, v93
	v_fma_f32 v157, -v2, v159, v94
	v_fma_f32 v158, -v2, v160, v95
	v_fma_f32 v159, -v2, v161, v96
	v_fma_f32 v160, -v2, v162, v97
	v_fma_f32 v161, -v2, v163, v98
	v_fma_f32 v162, -v2, v164, v99
	v_fma_f32 v163, -v2, v165, v100
	v_fma_f32 v164, -v2, v166, v101
	v_fma_f32 v165, -v2, v167, v102
	v_fma_f32 v166, -v2, v168, v103
	v_fma_f32 v167, -v2, v169, v104
	v_fma_f32 v168, -v2, v170, v105
	v_fma_f32 v169, -v2, v171, v106
	v_fma_f32 v170, -v2, v172, v107
	v_fma_f32 v171, -v2, v173, v108
	v_fma_f32 v172, -v2, v174, v109
	v_fma_f32 v173, -v2, v175, v110
	v_fma_f32 v174, -v2, v176, v111
	v_fma_f32 v175, -v2, v177, v112
	v_fma_f32 v176, -v2, v178, v113
	v_fma_f32 v177, -v2, v179, v114
	v_fma_f32 v178, -v2, v180, v115
	v_fma_f32 v179, -v2, v181, v116
	v_fma_f32 v180, -v2, v182, v117
	v_fma_f32 v181, -v2, v183, v118
	v_fma_f32 v182, -v2, v184, v119
	v_fma_f32 v183, -v2, v185, v120
	v_fma_f32 v184, -v2, v186, v121
	v_fma_f32 v185, -v2, v187, v122
	v_fma_f32 v186, -v2, v188, v123
	v_fma_f32 v187, -v2, v189, v124
	v_fma_f32 v188, -v2, v194, v125
	v_fma_f32 v189, -v2, v195, v126
	v_fma_f32 v190, -v2, v196, v127
	v_fma_f32 v191, -v2, v197, v128
	v_fma_f32 v192, -v2, v198, v129
	v_fma_f32 v193, -v2, v199, v130
	v_fma_f32 v194, -v2, v200, v131
	v_fma_f32 v4, -v2, v201, v4
	ds_read_b128 v[74:77], v21 offset:832
	ds_read_b128 v[78:81], v21 offset:848
	ds_read_b128 v[82:85], v21 offset:864
	ds_read_b128 v[86:89], v21 offset:880
	ds_read_b128 v[90:93], v21 offset:896
	ds_read_b128 v[94:97], v21 offset:912
	ds_read_b128 v[98:101], v21 offset:928
	ds_read_b128 v[102:105], v21 offset:944
	ds_read_b128 v[106:109], v21 offset:960
	ds_read_b128 v[110:113], v21 offset:976
	ds_read_b128 v[114:117], v21 offset:992
	ds_read_b128 v[118:121], v21 offset:1008
	ds_read_b128 v[122:125], v21 offset:1024
	ds_read_b128 v[126:129], v21 offset:1040
	ds_read_b128 v[130:133], v21 offset:1056
	s_waitcnt lgkmcnt(0)
	v_fma_f32 v7, -v5, v8, v1
	v_fma_f32 v6, -v5, v9, v134
	v_fma_f32 v2, -v5, v10, v5
	v_fma_f32 v1, -v5, v11, v135
	v_fma_f32 v134, -v5, v12, v136
	v_fma_f32 v135, -v5, v13, v137
	v_fma_f32 v136, -v5, v14, v138
	v_fma_f32 v137, -v5, v15, v139
	v_fma_f32 v138, -v5, v16, v140
	v_fma_f32 v139, -v5, v17, v141
	v_fma_f32 v140, -v5, v18, v142
	v_fma_f32 v141, -v5, v19, v143
	v_fma_f32 v142, -v5, v22, v144
	v_fma_f32 v143, -v5, v23, v145
	v_fma_f32 v144, -v5, v24, v146
	v_fma_f32 v145, -v5, v25, v147
	v_fma_f32 v146, -v5, v26, v148
	v_fma_f32 v147, -v5, v27, v149
	v_fma_f32 v148, -v5, v28, v150
	v_fma_f32 v149, -v5, v29, v151
	v_fma_f32 v150, -v5, v30, v152
	v_fma_f32 v151, -v5, v31, v153
	v_fma_f32 v152, -v5, v32, v154
	v_fma_f32 v153, -v5, v33, v155
	v_fma_f32 v154, -v5, v34, v156
	v_fma_f32 v155, -v5, v35, v157
	v_fma_f32 v156, -v5, v36, v158
	v_fma_f32 v157, -v5, v37, v159
	v_fma_f32 v158, -v5, v38, v160
	v_fma_f32 v159, -v5, v39, v161
	v_fma_f32 v160, -v5, v40, v162
	v_fma_f32 v161, -v5, v41, v163
	v_fma_f32 v162, -v5, v42, v164
	v_fma_f32 v163, -v5, v43, v165
	v_fma_f32 v164, -v5, v44, v166
	v_fma_f32 v165, -v5, v45, v167
	v_fma_f32 v166, -v5, v46, v168
	v_fma_f32 v167, -v5, v47, v169
	v_fma_f32 v168, -v5, v48, v170
	v_fma_f32 v169, -v5, v49, v171
	v_fma_f32 v170, -v5, v50, v172
	v_fma_f32 v171, -v5, v51, v173
	v_fma_f32 v172, -v5, v52, v174
	v_fma_f32 v173, -v5, v53, v175
	v_fma_f32 v174, -v5, v54, v176
	v_fma_f32 v175, -v5, v55, v177
	v_fma_f32 v176, -v5, v56, v178
	v_fma_f32 v177, -v5, v57, v179
	v_fma_f32 v178, -v5, v58, v180
	v_fma_f32 v179, -v5, v59, v181
	v_fma_f32 v180, -v5, v60, v182
	v_fma_f32 v181, -v5, v61, v183
	v_fma_f32 v182, -v5, v62, v184
	v_fma_f32 v183, -v5, v63, v185
	v_fma_f32 v184, -v5, v64, v186
	v_fma_f32 v185, -v5, v65, v187
	v_fma_f32 v186, -v5, v66, v188
	v_fma_f32 v187, -v5, v67, v189
	v_fma_f32 v188, -v5, v68, v190
	v_fma_f32 v189, -v5, v69, v191
	v_fma_f32 v70, -v5, v70, v192
	v_fma_f32 v71, -v5, v71, v193
	v_fma_f32 v72, -v5, v72, v194
	v_fma_f32 v4, -v5, v73, v4
	ds_read_b128 v[8:11], v21 offset:1104
	ds_read_b128 v[12:15], v21 offset:1120
	ds_read_b128 v[16:19], v21 offset:1136
	ds_read_b128 v[22:25], v21 offset:1152
	ds_read_b128 v[26:29], v21 offset:1168
	ds_read_b128 v[30:33], v21 offset:1184
	ds_read_b128 v[34:37], v21 offset:1200
	ds_read_b128 v[38:41], v21 offset:1216
	ds_read_b128 v[42:45], v21 offset:1232
	ds_read_b128 v[46:49], v21 offset:1248
	ds_read_b128 v[50:53], v21 offset:1264
	ds_read_b128 v[54:57], v21 offset:1280
	ds_read_b128 v[58:61], v21 offset:1296
	ds_read_b128 v[62:65], v21 offset:1312
	ds_read_b128 v[66:69], v21 offset:1328
	v_fma_f32 v5, -v1, v74, v134
	v_fma_f32 v134, -v1, v75, v135
	v_fma_f32 v135, -v1, v76, v136
	v_fma_f32 v136, -v1, v77, v137
	v_fma_f32 v137, -v1, v78, v138
	v_fma_f32 v138, -v1, v79, v139
	v_fma_f32 v139, -v1, v80, v140
	v_fma_f32 v140, -v1, v81, v141
	v_fma_f32 v141, -v1, v82, v142
	v_fma_f32 v142, -v1, v83, v143
	v_fma_f32 v143, -v1, v84, v144
	v_fma_f32 v144, -v1, v85, v145
	v_fma_f32 v145, -v1, v86, v146
	v_fma_f32 v146, -v1, v87, v147
	v_fma_f32 v147, -v1, v88, v148
	v_fma_f32 v148, -v1, v89, v149
	v_fma_f32 v149, -v1, v90, v150
	v_fma_f32 v150, -v1, v91, v151
	v_fma_f32 v151, -v1, v92, v152
	v_fma_f32 v152, -v1, v93, v153
	v_fma_f32 v153, -v1, v94, v154
	v_fma_f32 v154, -v1, v95, v155
	v_fma_f32 v155, -v1, v96, v156
	v_fma_f32 v156, -v1, v97, v157
	v_fma_f32 v157, -v1, v98, v158
	v_fma_f32 v158, -v1, v99, v159
	v_fma_f32 v159, -v1, v100, v160
	v_fma_f32 v160, -v1, v101, v161
	v_fma_f32 v161, -v1, v102, v162
	v_fma_f32 v162, -v1, v103, v163
	v_fma_f32 v163, -v1, v104, v164
	v_fma_f32 v164, -v1, v105, v165
	v_fma_f32 v165, -v1, v106, v166
	v_fma_f32 v166, -v1, v107, v167
	v_fma_f32 v167, -v1, v108, v168
	v_fma_f32 v168, -v1, v109, v169
	v_fma_f32 v169, -v1, v110, v170
	v_fma_f32 v170, -v1, v111, v171
	v_fma_f32 v171, -v1, v112, v172
	v_fma_f32 v172, -v1, v113, v173
	v_fma_f32 v173, -v1, v114, v174
	v_fma_f32 v174, -v1, v115, v175
	v_fma_f32 v175, -v1, v116, v176
	v_fma_f32 v176, -v1, v117, v177
	v_fma_f32 v177, -v1, v118, v178
	v_fma_f32 v178, -v1, v119, v179
	v_fma_f32 v179, -v1, v120, v180
	v_fma_f32 v180, -v1, v121, v181
	v_fma_f32 v181, -v1, v122, v182
	v_fma_f32 v182, -v1, v123, v183
	v_fma_f32 v183, -v1, v124, v184
	v_fma_f32 v184, -v1, v125, v185
	v_fma_f32 v185, -v1, v126, v186
	v_fma_f32 v186, -v1, v127, v187
	v_fma_f32 v187, -v1, v128, v188
	v_fma_f32 v188, -v1, v129, v189
	v_fma_f32 v130, -v1, v130, v70
	v_fma_f32 v131, -v1, v131, v71
	v_fma_f32 v132, -v1, v132, v72
	v_fma_f32 v4, -v1, v133, v4
	ds_read_b128 v[70:73], v21 offset:1376
	ds_read_b128 v[74:77], v21 offset:1392
	ds_read_b128 v[78:81], v21 offset:1408
	ds_read_b128 v[82:85], v21 offset:1424
	ds_read_b128 v[86:89], v21 offset:1440
	ds_read_b128 v[90:93], v21 offset:1456
	ds_read_b128 v[94:97], v21 offset:1472
	ds_read_b128 v[98:101], v21 offset:1488
	ds_read_b128 v[102:105], v21 offset:1504
	ds_read_b128 v[106:109], v21 offset:1520
	ds_read_b128 v[110:113], v21 offset:1536
	ds_read_b128 v[114:117], v21 offset:1552
	ds_read_b128 v[118:121], v21 offset:1568
	ds_read_b128 v[122:125], v21 offset:1584
	ds_read_b128 v[126:129], v21 offset:1600
	s_waitcnt lgkmcnt(0)
	v_fma_f32 v8, -v5, v8, v5
	v_fma_f32 v9, -v5, v9, v134
	v_fma_f32 v10, -v5, v10, v135
	v_fma_f32 v11, -v5, v11, v136
	v_fma_f32 v134, -v5, v12, v137
	v_fma_f32 v135, -v5, v13, v138
	v_fma_f32 v136, -v5, v14, v139
	v_fma_f32 v137, -v5, v15, v140
	v_fma_f32 v138, -v5, v16, v141
	v_fma_f32 v139, -v5, v17, v142
	v_fma_f32 v140, -v5, v18, v143
	v_fma_f32 v141, -v5, v19, v144
	v_fma_f32 v142, -v5, v22, v145
	v_fma_f32 v143, -v5, v23, v146
	v_fma_f32 v144, -v5, v24, v147
	v_fma_f32 v145, -v5, v25, v148
	v_fma_f32 v146, -v5, v26, v149
	v_fma_f32 v147, -v5, v27, v150
	v_fma_f32 v148, -v5, v28, v151
	v_fma_f32 v149, -v5, v29, v152
	v_fma_f32 v150, -v5, v30, v153
	v_fma_f32 v151, -v5, v31, v154
	v_fma_f32 v152, -v5, v32, v155
	v_fma_f32 v153, -v5, v33, v156
	v_fma_f32 v154, -v5, v34, v157
	v_fma_f32 v155, -v5, v35, v158
	v_fma_f32 v156, -v5, v36, v159
	v_fma_f32 v157, -v5, v37, v160
	v_fma_f32 v158, -v5, v38, v161
	v_fma_f32 v159, -v5, v39, v162
	v_fma_f32 v160, -v5, v40, v163
	v_fma_f32 v161, -v5, v41, v164
	v_fma_f32 v162, -v5, v42, v165
	v_fma_f32 v163, -v5, v43, v166
	v_fma_f32 v164, -v5, v44, v167
	v_fma_f32 v165, -v5, v45, v168
	v_fma_f32 v166, -v5, v46, v169
	v_fma_f32 v167, -v5, v47, v170
	v_fma_f32 v168, -v5, v48, v171
	v_fma_f32 v169, -v5, v49, v172
	v_fma_f32 v170, -v5, v50, v173
	v_fma_f32 v171, -v5, v51, v174
	v_fma_f32 v172, -v5, v52, v175
	v_fma_f32 v173, -v5, v53, v176
	v_fma_f32 v174, -v5, v54, v177
	v_fma_f32 v175, -v5, v55, v178
	v_fma_f32 v176, -v5, v56, v179
	v_fma_f32 v177, -v5, v57, v180
	v_fma_f32 v178, -v5, v58, v181
	v_fma_f32 v179, -v5, v59, v182
	v_fma_f32 v180, -v5, v60, v183
	v_fma_f32 v181, -v5, v61, v184
	v_fma_f32 v182, -v5, v62, v185
	v_fma_f32 v183, -v5, v63, v186
	v_fma_f32 v184, -v5, v64, v187
	v_fma_f32 v185, -v5, v65, v188
	v_fma_f32 v186, -v5, v66, v130
	v_fma_f32 v187, -v5, v67, v131
	v_fma_f32 v188, -v5, v68, v132
	v_fma_f32 v4, -v5, v69, v4
	ds_read_b128 v[12:15], v21 offset:1648
	ds_read_b128 v[16:19], v21 offset:1664
	ds_read_b128 v[22:25], v21 offset:1680
	ds_read_b128 v[26:29], v21 offset:1696
	ds_read_b128 v[30:33], v21 offset:1712
	ds_read_b128 v[34:37], v21 offset:1728
	ds_read_b128 v[38:41], v21 offset:1744
	ds_read_b128 v[42:45], v21 offset:1760
	ds_read_b128 v[46:49], v21 offset:1776
	ds_read_b128 v[50:53], v21 offset:1792
	ds_read_b128 v[54:57], v21 offset:1808
	ds_read_b128 v[58:61], v21 offset:1824
	ds_read_b128 v[62:65], v21 offset:1840
	ds_read_b128 v[66:69], v21 offset:1856
	ds_read_b128 v[130:133], v21 offset:1872
	v_fma_f32 v5, -v9, v70, v8
	v_fma_f32 v8, -v9, v71, v9
	v_fma_f32 v189, -v9, v72, v10
	v_fma_f32 v190, -v9, v73, v11
	v_fma_f32 v134, -v9, v74, v134
	v_fma_f32 v135, -v9, v75, v135
	v_fma_f32 v136, -v9, v76, v136
	v_fma_f32 v137, -v9, v77, v137
	v_fma_f32 v138, -v9, v78, v138
	v_fma_f32 v139, -v9, v79, v139
	v_fma_f32 v140, -v9, v80, v140
	v_fma_f32 v141, -v9, v81, v141
	v_fma_f32 v142, -v9, v82, v142
	v_fma_f32 v143, -v9, v83, v143
	v_fma_f32 v144, -v9, v84, v144
	v_fma_f32 v145, -v9, v85, v145
	v_fma_f32 v146, -v9, v86, v146
	v_fma_f32 v147, -v9, v87, v147
	v_fma_f32 v148, -v9, v88, v148
	v_fma_f32 v149, -v9, v89, v149
	v_fma_f32 v150, -v9, v90, v150
	v_fma_f32 v151, -v9, v91, v151
	v_fma_f32 v152, -v9, v92, v152
	v_fma_f32 v153, -v9, v93, v153
	v_fma_f32 v154, -v9, v94, v154
	v_fma_f32 v155, -v9, v95, v155
	v_fma_f32 v156, -v9, v96, v156
	v_fma_f32 v157, -v9, v97, v157
	v_fma_f32 v158, -v9, v98, v158
	v_fma_f32 v159, -v9, v99, v159
	v_fma_f32 v160, -v9, v100, v160
	v_fma_f32 v161, -v9, v101, v161
	v_fma_f32 v162, -v9, v102, v162
	v_fma_f32 v163, -v9, v103, v163
	v_fma_f32 v164, -v9, v104, v164
	v_fma_f32 v165, -v9, v105, v165
	v_fma_f32 v166, -v9, v106, v166
	v_fma_f32 v167, -v9, v107, v167
	v_fma_f32 v168, -v9, v108, v168
	v_fma_f32 v169, -v9, v109, v169
	v_fma_f32 v170, -v9, v110, v170
	v_fma_f32 v171, -v9, v111, v171
	v_fma_f32 v172, -v9, v112, v172
	v_fma_f32 v173, -v9, v113, v173
	v_fma_f32 v174, -v9, v114, v174
	v_fma_f32 v175, -v9, v115, v175
	v_fma_f32 v176, -v9, v116, v176
	v_fma_f32 v177, -v9, v117, v177
	v_fma_f32 v178, -v9, v118, v178
	v_fma_f32 v179, -v9, v119, v179
	v_fma_f32 v180, -v9, v120, v180
	v_fma_f32 v181, -v9, v121, v181
	v_fma_f32 v182, -v9, v122, v182
	v_fma_f32 v183, -v9, v123, v183
	v_fma_f32 v184, -v9, v124, v184
	v_fma_f32 v185, -v9, v125, v185
	v_fma_f32 v126, -v9, v126, v186
	v_fma_f32 v127, -v9, v127, v187
	v_fma_f32 v128, -v9, v128, v188
	v_fma_f32 v4, -v9, v129, v4
	ds_read_b128 v[70:73], v21 offset:1936
	ds_read_b128 v[74:77], v21 offset:1952
	ds_read_b128 v[78:81], v21 offset:1968
	ds_read_b128 v[82:85], v21 offset:1984
	ds_read_b128 v[86:89], v21 offset:2000
	ds_read_b128 v[90:93], v21 offset:2016
	ds_read_b128 v[94:97], v21 offset:2032
	ds_read_b128 v[98:101], v21 offset:2048
	ds_read_b128 v[102:105], v21 offset:2064
	ds_read_b128 v[106:109], v21 offset:2080
	ds_read_b128 v[110:113], v21 offset:2096
	ds_read_b128 v[114:117], v21 offset:2112
	ds_read_b128 v[118:121], v21 offset:2128
	ds_read_b128 v[122:125], v21 offset:2144
	s_waitcnt lgkmcnt(0)
	v_fma_f32 v11, -v189, v12, v5
	v_fma_f32 v10, -v189, v13, v8
	v_fma_f32 v9, -v189, v14, v189
	v_fma_f32 v8, -v189, v15, v190
	v_fma_f32 v5, -v189, v16, v134
	v_fma_f32 v129, -v189, v17, v135
	v_fma_f32 v134, -v189, v18, v136
	v_fma_f32 v135, -v189, v19, v137
	v_fma_f32 v136, -v189, v22, v138
	v_fma_f32 v137, -v189, v23, v139
	v_fma_f32 v138, -v189, v24, v140
	v_fma_f32 v139, -v189, v25, v141
	v_fma_f32 v140, -v189, v26, v142
	v_fma_f32 v141, -v189, v27, v143
	v_fma_f32 v142, -v189, v28, v144
	v_fma_f32 v143, -v189, v29, v145
	v_fma_f32 v144, -v189, v30, v146
	v_fma_f32 v145, -v189, v31, v147
	v_fma_f32 v146, -v189, v32, v148
	v_fma_f32 v147, -v189, v33, v149
	v_fma_f32 v148, -v189, v34, v150
	v_fma_f32 v149, -v189, v35, v151
	v_fma_f32 v150, -v189, v36, v152
	v_fma_f32 v151, -v189, v37, v153
	v_fma_f32 v152, -v189, v38, v154
	v_fma_f32 v153, -v189, v39, v155
	v_fma_f32 v154, -v189, v40, v156
	v_fma_f32 v155, -v189, v41, v157
	v_fma_f32 v156, -v189, v42, v158
	v_fma_f32 v157, -v189, v43, v159
	v_fma_f32 v158, -v189, v44, v160
	v_fma_f32 v159, -v189, v45, v161
	v_fma_f32 v160, -v189, v46, v162
	v_fma_f32 v161, -v189, v47, v163
	v_fma_f32 v162, -v189, v48, v164
	v_fma_f32 v163, -v189, v49, v165
	v_fma_f32 v164, -v189, v50, v166
	v_fma_f32 v165, -v189, v51, v167
	v_fma_f32 v166, -v189, v52, v168
	v_fma_f32 v167, -v189, v53, v169
	v_fma_f32 v168, -v189, v54, v170
	v_fma_f32 v169, -v189, v55, v171
	v_fma_f32 v170, -v189, v56, v172
	v_fma_f32 v171, -v189, v57, v173
	v_fma_f32 v172, -v189, v58, v174
	v_fma_f32 v173, -v189, v59, v175
	v_fma_f32 v174, -v189, v60, v176
	v_fma_f32 v175, -v189, v61, v177
	v_fma_f32 v176, -v189, v62, v178
	v_fma_f32 v177, -v189, v63, v179
	v_fma_f32 v178, -v189, v64, v180
	v_fma_f32 v179, -v189, v65, v181
	v_fma_f32 v180, -v189, v66, v182
	v_fma_f32 v181, -v189, v67, v183
	v_fma_f32 v182, -v189, v68, v184
	v_fma_f32 v183, -v189, v69, v185
	v_fma_f32 v126, -v189, v130, v126
	v_fma_f32 v127, -v189, v131, v127
	v_fma_f32 v128, -v189, v132, v128
	v_fma_f32 v4, -v189, v133, v4
	ds_read_b128 v[12:15], v21 offset:2208
	ds_read_b128 v[16:19], v21 offset:2224
	ds_read_b128 v[22:25], v21 offset:2240
	ds_read_b128 v[26:29], v21 offset:2256
	ds_read_b128 v[30:33], v21 offset:2272
	ds_read_b128 v[34:37], v21 offset:2288
	ds_read_b128 v[38:41], v21 offset:2304
	ds_read_b128 v[42:45], v21 offset:2320
	ds_read_b128 v[46:49], v21 offset:2336
	ds_read_b128 v[50:53], v21 offset:2352
	ds_read_b128 v[54:57], v21 offset:2368
	ds_read_b128 v[58:61], v21 offset:2384
	ds_read_b128 v[62:65], v21 offset:2400
	ds_read_b128 v[66:69], v21 offset:2416
	v_fma_f32 v5, -v8, v70, v5
	v_fma_f32 v129, -v8, v71, v129
	v_fma_f32 v130, -v8, v72, v134
	v_fma_f32 v131, -v8, v73, v135
	v_fma_f32 v132, -v8, v74, v136
	v_fma_f32 v133, -v8, v75, v137
	v_fma_f32 v134, -v8, v76, v138
	v_fma_f32 v135, -v8, v77, v139
	v_fma_f32 v136, -v8, v78, v140
	v_fma_f32 v137, -v8, v79, v141
	v_fma_f32 v138, -v8, v80, v142
	v_fma_f32 v139, -v8, v81, v143
	v_fma_f32 v140, -v8, v82, v144
	v_fma_f32 v141, -v8, v83, v145
	v_fma_f32 v142, -v8, v84, v146
	v_fma_f32 v143, -v8, v85, v147
	v_fma_f32 v144, -v8, v86, v148
	v_fma_f32 v145, -v8, v87, v149
	v_fma_f32 v146, -v8, v88, v150
	v_fma_f32 v147, -v8, v89, v151
	v_fma_f32 v148, -v8, v90, v152
	v_fma_f32 v149, -v8, v91, v153
	v_fma_f32 v150, -v8, v92, v154
	v_fma_f32 v151, -v8, v93, v155
	v_fma_f32 v152, -v8, v94, v156
	v_fma_f32 v153, -v8, v95, v157
	v_fma_f32 v154, -v8, v96, v158
	v_fma_f32 v155, -v8, v97, v159
	v_fma_f32 v156, -v8, v98, v160
	v_fma_f32 v157, -v8, v99, v161
	v_fma_f32 v158, -v8, v100, v162
	v_fma_f32 v159, -v8, v101, v163
	v_fma_f32 v160, -v8, v102, v164
	v_fma_f32 v161, -v8, v103, v165
	v_fma_f32 v162, -v8, v104, v166
	v_fma_f32 v163, -v8, v105, v167
	v_fma_f32 v164, -v8, v106, v168
	v_fma_f32 v165, -v8, v107, v169
	v_fma_f32 v166, -v8, v108, v170
	v_fma_f32 v167, -v8, v109, v171
	v_fma_f32 v168, -v8, v110, v172
	v_fma_f32 v169, -v8, v111, v173
	v_fma_f32 v170, -v8, v112, v174
	v_fma_f32 v171, -v8, v113, v175
	v_fma_f32 v172, -v8, v114, v176
	v_fma_f32 v173, -v8, v115, v177
	v_fma_f32 v174, -v8, v116, v178
	v_fma_f32 v175, -v8, v117, v179
	v_fma_f32 v176, -v8, v118, v180
	v_fma_f32 v177, -v8, v119, v181
	v_fma_f32 v178, -v8, v120, v182
	v_fma_f32 v179, -v8, v121, v183
	v_fma_f32 v126, -v8, v122, v126
	v_fma_f32 v127, -v8, v123, v127
	v_fma_f32 v128, -v8, v124, v128
	v_fma_f32 v4, -v8, v125, v4
	ds_read_b128 v[70:73], v21 offset:2480
	ds_read_b128 v[74:77], v21 offset:2496
	ds_read_b128 v[78:81], v21 offset:2512
	ds_read_b128 v[82:85], v21 offset:2528
	ds_read_b128 v[86:89], v21 offset:2544
	ds_read_b128 v[90:93], v21 offset:2560
	ds_read_b128 v[94:97], v21 offset:2576
	ds_read_b128 v[98:101], v21 offset:2592
	ds_read_b128 v[102:105], v21 offset:2608
	ds_read_b128 v[106:109], v21 offset:2624
	ds_read_b128 v[110:113], v21 offset:2640
	ds_read_b128 v[114:117], v21 offset:2656
	ds_read_b128 v[118:121], v21 offset:2672
	ds_read_b128 v[122:125], v21 offset:2688
	s_waitcnt lgkmcnt(0)
	v_fma_f32 v12, -v5, v12, v5
	v_fma_f32 v13, -v5, v13, v129
	v_fma_f32 v14, -v5, v14, v130
	v_fma_f32 v15, -v5, v15, v131
	v_fma_f32 v130, -v5, v16, v132
	v_fma_f32 v131, -v5, v17, v133
	v_fma_f32 v132, -v5, v18, v134
	v_fma_f32 v133, -v5, v19, v135
	v_fma_f32 v134, -v5, v22, v136
	v_fma_f32 v135, -v5, v23, v137
	v_fma_f32 v136, -v5, v24, v138
	v_fma_f32 v137, -v5, v25, v139
	v_fma_f32 v138, -v5, v26, v140
	v_fma_f32 v139, -v5, v27, v141
	v_fma_f32 v140, -v5, v28, v142
	v_fma_f32 v141, -v5, v29, v143
	v_fma_f32 v142, -v5, v30, v144
	v_fma_f32 v143, -v5, v31, v145
	v_fma_f32 v144, -v5, v32, v146
	v_fma_f32 v145, -v5, v33, v147
	v_fma_f32 v146, -v5, v34, v148
	v_fma_f32 v147, -v5, v35, v149
	v_fma_f32 v148, -v5, v36, v150
	v_fma_f32 v149, -v5, v37, v151
	v_fma_f32 v150, -v5, v38, v152
	v_fma_f32 v151, -v5, v39, v153
	v_fma_f32 v152, -v5, v40, v154
	v_fma_f32 v153, -v5, v41, v155
	v_fma_f32 v154, -v5, v42, v156
	v_fma_f32 v155, -v5, v43, v157
	v_fma_f32 v156, -v5, v44, v158
	v_fma_f32 v157, -v5, v45, v159
	v_fma_f32 v158, -v5, v46, v160
	v_fma_f32 v159, -v5, v47, v161
	v_fma_f32 v160, -v5, v48, v162
	v_fma_f32 v161, -v5, v49, v163
	v_fma_f32 v162, -v5, v50, v164
	v_fma_f32 v163, -v5, v51, v165
	v_fma_f32 v164, -v5, v52, v166
	v_fma_f32 v165, -v5, v53, v167
	v_fma_f32 v166, -v5, v54, v168
	v_fma_f32 v167, -v5, v55, v169
	v_fma_f32 v168, -v5, v56, v170
	v_fma_f32 v169, -v5, v57, v171
	v_fma_f32 v170, -v5, v58, v172
	v_fma_f32 v171, -v5, v59, v173
	v_fma_f32 v172, -v5, v60, v174
	v_fma_f32 v173, -v5, v61, v175
	v_fma_f32 v174, -v5, v62, v176
	v_fma_f32 v175, -v5, v63, v177
	v_fma_f32 v176, -v5, v64, v178
	v_fma_f32 v177, -v5, v65, v179
	v_fma_f32 v178, -v5, v66, v126
	v_fma_f32 v179, -v5, v67, v127
	v_fma_f32 v180, -v5, v68, v128
	v_fma_f32 v4, -v5, v69, v4
	ds_read_b128 v[16:19], v21 offset:2752
	ds_read_b128 v[22:25], v21 offset:2768
	ds_read_b128 v[26:29], v21 offset:2784
	ds_read_b128 v[30:33], v21 offset:2800
	ds_read_b128 v[34:37], v21 offset:2816
	ds_read_b128 v[38:41], v21 offset:2832
	ds_read_b128 v[42:45], v21 offset:2848
	ds_read_b128 v[46:49], v21 offset:2864
	ds_read_b128 v[50:53], v21 offset:2880
	ds_read_b128 v[54:57], v21 offset:2896
	ds_read_b128 v[58:61], v21 offset:2912
	ds_read_b128 v[62:65], v21 offset:2928
	ds_read_b128 v[66:69], v21 offset:2944
	ds_read_b128 v[126:129], v21 offset:2960
	v_fma_f32 v5, -v13, v70, v12
	v_fma_f32 v12, -v13, v71, v13
	v_fma_f32 v181, -v13, v72, v14
	v_fma_f32 v182, -v13, v73, v15
	v_fma_f32 v130, -v13, v74, v130
	v_fma_f32 v131, -v13, v75, v131
	v_fma_f32 v132, -v13, v76, v132
	v_fma_f32 v133, -v13, v77, v133
	v_fma_f32 v134, -v13, v78, v134
	v_fma_f32 v135, -v13, v79, v135
	v_fma_f32 v136, -v13, v80, v136
	v_fma_f32 v137, -v13, v81, v137
	v_fma_f32 v138, -v13, v82, v138
	v_fma_f32 v139, -v13, v83, v139
	v_fma_f32 v140, -v13, v84, v140
	v_fma_f32 v141, -v13, v85, v141
	v_fma_f32 v142, -v13, v86, v142
	v_fma_f32 v143, -v13, v87, v143
	v_fma_f32 v144, -v13, v88, v144
	v_fma_f32 v145, -v13, v89, v145
	v_fma_f32 v146, -v13, v90, v146
	v_fma_f32 v147, -v13, v91, v147
	v_fma_f32 v148, -v13, v92, v148
	v_fma_f32 v149, -v13, v93, v149
	v_fma_f32 v150, -v13, v94, v150
	v_fma_f32 v151, -v13, v95, v151
	v_fma_f32 v152, -v13, v96, v152
	v_fma_f32 v153, -v13, v97, v153
	v_fma_f32 v154, -v13, v98, v154
	v_fma_f32 v155, -v13, v99, v155
	v_fma_f32 v156, -v13, v100, v156
	v_fma_f32 v157, -v13, v101, v157
	v_fma_f32 v158, -v13, v102, v158
	v_fma_f32 v159, -v13, v103, v159
	v_fma_f32 v160, -v13, v104, v160
	v_fma_f32 v161, -v13, v105, v161
	v_fma_f32 v162, -v13, v106, v162
	v_fma_f32 v163, -v13, v107, v163
	v_fma_f32 v164, -v13, v108, v164
	v_fma_f32 v165, -v13, v109, v165
	v_fma_f32 v166, -v13, v110, v166
	v_fma_f32 v167, -v13, v111, v167
	v_fma_f32 v168, -v13, v112, v168
	v_fma_f32 v169, -v13, v113, v169
	v_fma_f32 v170, -v13, v114, v170
	v_fma_f32 v171, -v13, v115, v171
	v_fma_f32 v172, -v13, v116, v172
	v_fma_f32 v173, -v13, v117, v173
	v_fma_f32 v174, -v13, v118, v174
	v_fma_f32 v175, -v13, v119, v175
	v_fma_f32 v176, -v13, v120, v176
	v_fma_f32 v177, -v13, v121, v177
	v_fma_f32 v122, -v13, v122, v178
	v_fma_f32 v123, -v13, v123, v179
	v_fma_f32 v124, -v13, v124, v180
	v_fma_f32 v4, -v13, v125, v4
	ds_read_b128 v[70:73], v21 offset:3040
	ds_read_b128 v[74:77], v21 offset:3056
	ds_read_b128 v[78:81], v21 offset:3072
	ds_read_b128 v[82:85], v21 offset:3088
	ds_read_b128 v[86:89], v21 offset:3104
	ds_read_b128 v[90:93], v21 offset:3120
	ds_read_b128 v[94:97], v21 offset:3136
	ds_read_b128 v[98:101], v21 offset:3152
	ds_read_b128 v[102:105], v21 offset:3168
	ds_read_b128 v[106:109], v21 offset:3184
	ds_read_b128 v[110:113], v21 offset:3200
	ds_read_b128 v[114:117], v21 offset:3216
	ds_read_b128 v[118:121], v21 offset:3232
	s_waitcnt lgkmcnt(0)
	v_fma_f32 v15, -v181, v16, v5
	v_fma_f32 v14, -v181, v17, v12
	v_fma_f32 v13, -v181, v18, v181
	v_fma_f32 v12, -v181, v19, v182
	v_fma_f32 v5, -v181, v22, v130
	v_fma_f32 v125, -v181, v23, v131
	v_fma_f32 v130, -v181, v24, v132
	v_fma_f32 v131, -v181, v25, v133
	v_fma_f32 v132, -v181, v26, v134
	v_fma_f32 v133, -v181, v27, v135
	v_fma_f32 v134, -v181, v28, v136
	v_fma_f32 v135, -v181, v29, v137
	v_fma_f32 v136, -v181, v30, v138
	v_fma_f32 v137, -v181, v31, v139
	v_fma_f32 v138, -v181, v32, v140
	v_fma_f32 v139, -v181, v33, v141
	v_fma_f32 v140, -v181, v34, v142
	v_fma_f32 v141, -v181, v35, v143
	v_fma_f32 v142, -v181, v36, v144
	v_fma_f32 v143, -v181, v37, v145
	v_fma_f32 v144, -v181, v38, v146
	v_fma_f32 v145, -v181, v39, v147
	v_fma_f32 v146, -v181, v40, v148
	v_fma_f32 v147, -v181, v41, v149
	v_fma_f32 v148, -v181, v42, v150
	v_fma_f32 v149, -v181, v43, v151
	v_fma_f32 v150, -v181, v44, v152
	v_fma_f32 v151, -v181, v45, v153
	v_fma_f32 v152, -v181, v46, v154
	v_fma_f32 v153, -v181, v47, v155
	v_fma_f32 v154, -v181, v48, v156
	v_fma_f32 v155, -v181, v49, v157
	v_fma_f32 v156, -v181, v50, v158
	v_fma_f32 v157, -v181, v51, v159
	v_fma_f32 v158, -v181, v52, v160
	v_fma_f32 v159, -v181, v53, v161
	v_fma_f32 v160, -v181, v54, v162
	v_fma_f32 v161, -v181, v55, v163
	v_fma_f32 v162, -v181, v56, v164
	v_fma_f32 v163, -v181, v57, v165
	v_fma_f32 v164, -v181, v58, v166
	v_fma_f32 v165, -v181, v59, v167
	v_fma_f32 v166, -v181, v60, v168
	v_fma_f32 v167, -v181, v61, v169
	v_fma_f32 v168, -v181, v62, v170
	v_fma_f32 v169, -v181, v63, v171
	v_fma_f32 v170, -v181, v64, v172
	v_fma_f32 v171, -v181, v65, v173
	v_fma_f32 v172, -v181, v66, v174
	v_fma_f32 v173, -v181, v67, v175
	v_fma_f32 v174, -v181, v68, v176
	v_fma_f32 v175, -v181, v69, v177
	v_fma_f32 v122, -v181, v126, v122
	v_fma_f32 v123, -v181, v127, v123
	v_fma_f32 v124, -v181, v128, v124
	v_fma_f32 v4, -v181, v129, v4
	ds_read_b128 v[16:19], v21 offset:3312
	ds_read_b128 v[22:25], v21 offset:3328
	ds_read_b128 v[26:29], v21 offset:3344
	ds_read_b128 v[30:33], v21 offset:3360
	ds_read_b128 v[34:37], v21 offset:3376
	ds_read_b128 v[38:41], v21 offset:3392
	ds_read_b128 v[42:45], v21 offset:3408
	ds_read_b128 v[46:49], v21 offset:3424
	ds_read_b128 v[50:53], v21 offset:3440
	ds_read_b128 v[54:57], v21 offset:3456
	ds_read_b128 v[58:61], v21 offset:3472
	ds_read_b128 v[62:65], v21 offset:3488
	ds_read_b128 v[66:69], v21 offset:3504
	v_fma_f32 v5, -v12, v70, v5
	v_fma_f32 v125, -v12, v71, v125
	v_fma_f32 v126, -v12, v72, v130
	v_fma_f32 v127, -v12, v73, v131
	v_fma_f32 v128, -v12, v74, v132
	v_fma_f32 v129, -v12, v75, v133
	v_fma_f32 v130, -v12, v76, v134
	v_fma_f32 v131, -v12, v77, v135
	v_fma_f32 v132, -v12, v78, v136
	v_fma_f32 v133, -v12, v79, v137
	v_fma_f32 v134, -v12, v80, v138
	v_fma_f32 v135, -v12, v81, v139
	v_fma_f32 v136, -v12, v82, v140
	v_fma_f32 v137, -v12, v83, v141
	v_fma_f32 v138, -v12, v84, v142
	v_fma_f32 v139, -v12, v85, v143
	v_fma_f32 v140, -v12, v86, v144
	v_fma_f32 v141, -v12, v87, v145
	v_fma_f32 v142, -v12, v88, v146
	v_fma_f32 v143, -v12, v89, v147
	v_fma_f32 v144, -v12, v90, v148
	v_fma_f32 v145, -v12, v91, v149
	v_fma_f32 v146, -v12, v92, v150
	v_fma_f32 v147, -v12, v93, v151
	v_fma_f32 v148, -v12, v94, v152
	v_fma_f32 v149, -v12, v95, v153
	v_fma_f32 v150, -v12, v96, v154
	v_fma_f32 v151, -v12, v97, v155
	v_fma_f32 v152, -v12, v98, v156
	v_fma_f32 v153, -v12, v99, v157
	v_fma_f32 v154, -v12, v100, v158
	v_fma_f32 v155, -v12, v101, v159
	v_fma_f32 v156, -v12, v102, v160
	v_fma_f32 v157, -v12, v103, v161
	v_fma_f32 v158, -v12, v104, v162
	v_fma_f32 v159, -v12, v105, v163
	v_fma_f32 v160, -v12, v106, v164
	v_fma_f32 v161, -v12, v107, v165
	v_fma_f32 v162, -v12, v108, v166
	v_fma_f32 v163, -v12, v109, v167
	v_fma_f32 v164, -v12, v110, v168
	v_fma_f32 v165, -v12, v111, v169
	v_fma_f32 v166, -v12, v112, v170
	v_fma_f32 v167, -v12, v113, v171
	v_fma_f32 v168, -v12, v114, v172
	v_fma_f32 v169, -v12, v115, v173
	v_fma_f32 v170, -v12, v116, v174
	v_fma_f32 v171, -v12, v117, v175
	v_fma_f32 v122, -v12, v118, v122
	v_fma_f32 v123, -v12, v119, v123
	v_fma_f32 v124, -v12, v120, v124
	v_fma_f32 v4, -v12, v121, v4
	ds_read_b128 v[70:73], v21 offset:3584
	ds_read_b128 v[74:77], v21 offset:3600
	ds_read_b128 v[78:81], v21 offset:3616
	ds_read_b128 v[82:85], v21 offset:3632
	ds_read_b128 v[86:89], v21 offset:3648
	ds_read_b128 v[90:93], v21 offset:3664
	ds_read_b128 v[94:97], v21 offset:3680
	ds_read_b128 v[98:101], v21 offset:3696
	ds_read_b128 v[102:105], v21 offset:3712
	ds_read_b128 v[106:109], v21 offset:3728
	ds_read_b128 v[110:113], v21 offset:3744
	ds_read_b128 v[114:117], v21 offset:3760
	ds_read_b128 v[118:121], v21 offset:3776
	s_waitcnt lgkmcnt(0)
	v_fma_f32 v16, -v5, v16, v5
	v_fma_f32 v17, -v5, v17, v125
	v_fma_f32 v18, -v5, v18, v126
	v_fma_f32 v19, -v5, v19, v127
	v_fma_f32 v126, -v5, v22, v128
	v_fma_f32 v127, -v5, v23, v129
	v_fma_f32 v128, -v5, v24, v130
	v_fma_f32 v129, -v5, v25, v131
	v_fma_f32 v130, -v5, v26, v132
	v_fma_f32 v131, -v5, v27, v133
	v_fma_f32 v132, -v5, v28, v134
	v_fma_f32 v133, -v5, v29, v135
	v_fma_f32 v134, -v5, v30, v136
	v_fma_f32 v135, -v5, v31, v137
	v_fma_f32 v136, -v5, v32, v138
	v_fma_f32 v137, -v5, v33, v139
	v_fma_f32 v138, -v5, v34, v140
	v_fma_f32 v139, -v5, v35, v141
	v_fma_f32 v140, -v5, v36, v142
	v_fma_f32 v141, -v5, v37, v143
	v_fma_f32 v142, -v5, v38, v144
	v_fma_f32 v143, -v5, v39, v145
	v_fma_f32 v144, -v5, v40, v146
	v_fma_f32 v145, -v5, v41, v147
	v_fma_f32 v146, -v5, v42, v148
	v_fma_f32 v147, -v5, v43, v149
	v_fma_f32 v148, -v5, v44, v150
	v_fma_f32 v149, -v5, v45, v151
	v_fma_f32 v150, -v5, v46, v152
	v_fma_f32 v151, -v5, v47, v153
	v_fma_f32 v152, -v5, v48, v154
	v_fma_f32 v153, -v5, v49, v155
	v_fma_f32 v154, -v5, v50, v156
	v_fma_f32 v155, -v5, v51, v157
	v_fma_f32 v156, -v5, v52, v158
	v_fma_f32 v157, -v5, v53, v159
	v_fma_f32 v158, -v5, v54, v160
	v_fma_f32 v159, -v5, v55, v161
	v_fma_f32 v160, -v5, v56, v162
	v_fma_f32 v161, -v5, v57, v163
	v_fma_f32 v162, -v5, v58, v164
	v_fma_f32 v163, -v5, v59, v165
	v_fma_f32 v164, -v5, v60, v166
	v_fma_f32 v165, -v5, v61, v167
	v_fma_f32 v166, -v5, v62, v168
	v_fma_f32 v167, -v5, v63, v169
	v_fma_f32 v168, -v5, v64, v170
	v_fma_f32 v169, -v5, v65, v171
	v_fma_f32 v170, -v5, v66, v122
	v_fma_f32 v171, -v5, v67, v123
	v_fma_f32 v172, -v5, v68, v124
	v_fma_f32 v4, -v5, v69, v4
	ds_read_b128 v[22:25], v21 offset:3856
	ds_read_b128 v[26:29], v21 offset:3872
	ds_read_b128 v[30:33], v21 offset:3888
	ds_read_b128 v[34:37], v21 offset:3904
	ds_read_b128 v[38:41], v21 offset:3920
	ds_read_b128 v[42:45], v21 offset:3936
	ds_read_b128 v[46:49], v21 offset:3952
	ds_read_b128 v[50:53], v21 offset:3968
	ds_read_b128 v[54:57], v21 offset:3984
	ds_read_b128 v[58:61], v21 offset:4000
	ds_read_b128 v[62:65], v21 offset:4016
	ds_read_b128 v[66:69], v21 offset:4032
	ds_read_b128 v[122:125], v21 offset:4048
	v_fma_f32 v5, -v17, v70, v16
	v_fma_f32 v16, -v17, v71, v17
	v_fma_f32 v173, -v17, v72, v18
	v_fma_f32 v174, -v17, v73, v19
	v_fma_f32 v126, -v17, v74, v126
	v_fma_f32 v127, -v17, v75, v127
	v_fma_f32 v128, -v17, v76, v128
	v_fma_f32 v129, -v17, v77, v129
	v_fma_f32 v130, -v17, v78, v130
	v_fma_f32 v131, -v17, v79, v131
	v_fma_f32 v132, -v17, v80, v132
	v_fma_f32 v133, -v17, v81, v133
	v_fma_f32 v134, -v17, v82, v134
	v_fma_f32 v135, -v17, v83, v135
	v_fma_f32 v136, -v17, v84, v136
	v_fma_f32 v137, -v17, v85, v137
	v_fma_f32 v138, -v17, v86, v138
	v_fma_f32 v139, -v17, v87, v139
	v_fma_f32 v140, -v17, v88, v140
	v_fma_f32 v141, -v17, v89, v141
	v_fma_f32 v142, -v17, v90, v142
	v_fma_f32 v143, -v17, v91, v143
	v_fma_f32 v144, -v17, v92, v144
	v_fma_f32 v145, -v17, v93, v145
	v_fma_f32 v146, -v17, v94, v146
	v_fma_f32 v147, -v17, v95, v147
	v_fma_f32 v148, -v17, v96, v148
	v_fma_f32 v149, -v17, v97, v149
	v_fma_f32 v150, -v17, v98, v150
	v_fma_f32 v151, -v17, v99, v151
	v_fma_f32 v152, -v17, v100, v152
	v_fma_f32 v153, -v17, v101, v153
	v_fma_f32 v154, -v17, v102, v154
	v_fma_f32 v155, -v17, v103, v155
	v_fma_f32 v156, -v17, v104, v156
	v_fma_f32 v157, -v17, v105, v157
	v_fma_f32 v158, -v17, v106, v158
	v_fma_f32 v159, -v17, v107, v159
	v_fma_f32 v160, -v17, v108, v160
	v_fma_f32 v161, -v17, v109, v161
	v_fma_f32 v162, -v17, v110, v162
	v_fma_f32 v163, -v17, v111, v163
	v_fma_f32 v164, -v17, v112, v164
	v_fma_f32 v165, -v17, v113, v165
	v_fma_f32 v166, -v17, v114, v166
	v_fma_f32 v167, -v17, v115, v167
	v_fma_f32 v168, -v17, v116, v168
	v_fma_f32 v169, -v17, v117, v169
	v_fma_f32 v118, -v17, v118, v170
	v_fma_f32 v119, -v17, v119, v171
	v_fma_f32 v120, -v17, v120, v172
	v_fma_f32 v4, -v17, v121, v4
	ds_read_b128 v[70:73], v21 offset:4144
	ds_read_b128 v[74:77], v21 offset:4160
	ds_read_b128 v[78:81], v21 offset:4176
	ds_read_b128 v[82:85], v21 offset:4192
	ds_read_b128 v[86:89], v21 offset:4208
	ds_read_b128 v[90:93], v21 offset:4224
	ds_read_b128 v[94:97], v21 offset:4240
	ds_read_b128 v[98:101], v21 offset:4256
	ds_read_b128 v[102:105], v21 offset:4272
	ds_read_b128 v[106:109], v21 offset:4288
	ds_read_b128 v[110:113], v21 offset:4304
	ds_read_b128 v[114:117], v21 offset:4320
	s_waitcnt lgkmcnt(0)
	v_fma_f32 v19, -v173, v22, v5
	v_fma_f32 v18, -v173, v23, v16
	v_fma_f32 v17, -v173, v24, v173
	v_fma_f32 v16, -v173, v25, v174
	v_fma_f32 v5, -v173, v26, v126
	v_fma_f32 v121, -v173, v27, v127
	v_fma_f32 v126, -v173, v28, v128
	v_fma_f32 v127, -v173, v29, v129
	v_fma_f32 v128, -v173, v30, v130
	v_fma_f32 v129, -v173, v31, v131
	v_fma_f32 v130, -v173, v32, v132
	v_fma_f32 v131, -v173, v33, v133
	v_fma_f32 v132, -v173, v34, v134
	v_fma_f32 v133, -v173, v35, v135
	v_fma_f32 v134, -v173, v36, v136
	v_fma_f32 v135, -v173, v37, v137
	v_fma_f32 v136, -v173, v38, v138
	v_fma_f32 v137, -v173, v39, v139
	v_fma_f32 v138, -v173, v40, v140
	v_fma_f32 v139, -v173, v41, v141
	v_fma_f32 v140, -v173, v42, v142
	v_fma_f32 v141, -v173, v43, v143
	v_fma_f32 v142, -v173, v44, v144
	v_fma_f32 v143, -v173, v45, v145
	v_fma_f32 v144, -v173, v46, v146
	v_fma_f32 v145, -v173, v47, v147
	v_fma_f32 v146, -v173, v48, v148
	v_fma_f32 v147, -v173, v49, v149
	v_fma_f32 v148, -v173, v50, v150
	v_fma_f32 v149, -v173, v51, v151
	v_fma_f32 v150, -v173, v52, v152
	v_fma_f32 v151, -v173, v53, v153
	v_fma_f32 v152, -v173, v54, v154
	v_fma_f32 v153, -v173, v55, v155
	v_fma_f32 v154, -v173, v56, v156
	v_fma_f32 v155, -v173, v57, v157
	v_fma_f32 v156, -v173, v58, v158
	v_fma_f32 v157, -v173, v59, v159
	v_fma_f32 v158, -v173, v60, v160
	v_fma_f32 v159, -v173, v61, v161
	v_fma_f32 v160, -v173, v62, v162
	v_fma_f32 v161, -v173, v63, v163
	v_fma_f32 v162, -v173, v64, v164
	v_fma_f32 v163, -v173, v65, v165
	v_fma_f32 v164, -v173, v66, v166
	v_fma_f32 v165, -v173, v67, v167
	v_fma_f32 v166, -v173, v68, v168
	v_fma_f32 v167, -v173, v69, v169
	v_fma_f32 v118, -v173, v122, v118
	v_fma_f32 v119, -v173, v123, v119
	v_fma_f32 v120, -v173, v124, v120
	v_fma_f32 v4, -v173, v125, v4
	ds_read_b128 v[22:25], v21 offset:4416
	ds_read_b128 v[26:29], v21 offset:4432
	ds_read_b128 v[30:33], v21 offset:4448
	ds_read_b128 v[34:37], v21 offset:4464
	ds_read_b128 v[38:41], v21 offset:4480
	ds_read_b128 v[42:45], v21 offset:4496
	ds_read_b128 v[46:49], v21 offset:4512
	ds_read_b128 v[50:53], v21 offset:4528
	ds_read_b128 v[54:57], v21 offset:4544
	ds_read_b128 v[58:61], v21 offset:4560
	ds_read_b128 v[62:65], v21 offset:4576
	ds_read_b128 v[66:69], v21 offset:4592
	v_fma_f32 v5, -v16, v70, v5
	v_fma_f32 v121, -v16, v71, v121
	v_fma_f32 v122, -v16, v72, v126
	v_fma_f32 v123, -v16, v73, v127
	v_fma_f32 v124, -v16, v74, v128
	v_fma_f32 v125, -v16, v75, v129
	v_fma_f32 v126, -v16, v76, v130
	v_fma_f32 v127, -v16, v77, v131
	v_fma_f32 v128, -v16, v78, v132
	v_fma_f32 v129, -v16, v79, v133
	v_fma_f32 v130, -v16, v80, v134
	v_fma_f32 v131, -v16, v81, v135
	v_fma_f32 v132, -v16, v82, v136
	v_fma_f32 v133, -v16, v83, v137
	v_fma_f32 v134, -v16, v84, v138
	v_fma_f32 v135, -v16, v85, v139
	v_fma_f32 v136, -v16, v86, v140
	v_fma_f32 v137, -v16, v87, v141
	v_fma_f32 v138, -v16, v88, v142
	v_fma_f32 v139, -v16, v89, v143
	v_fma_f32 v140, -v16, v90, v144
	v_fma_f32 v141, -v16, v91, v145
	v_fma_f32 v142, -v16, v92, v146
	v_fma_f32 v143, -v16, v93, v147
	v_fma_f32 v144, -v16, v94, v148
	v_fma_f32 v145, -v16, v95, v149
	v_fma_f32 v146, -v16, v96, v150
	v_fma_f32 v147, -v16, v97, v151
	v_fma_f32 v148, -v16, v98, v152
	v_fma_f32 v149, -v16, v99, v153
	v_fma_f32 v150, -v16, v100, v154
	v_fma_f32 v151, -v16, v101, v155
	v_fma_f32 v152, -v16, v102, v156
	v_fma_f32 v153, -v16, v103, v157
	v_fma_f32 v154, -v16, v104, v158
	v_fma_f32 v155, -v16, v105, v159
	v_fma_f32 v156, -v16, v106, v160
	v_fma_f32 v157, -v16, v107, v161
	v_fma_f32 v158, -v16, v108, v162
	v_fma_f32 v159, -v16, v109, v163
	v_fma_f32 v160, -v16, v110, v164
	v_fma_f32 v161, -v16, v111, v165
	v_fma_f32 v162, -v16, v112, v166
	v_fma_f32 v163, -v16, v113, v167
	v_fma_f32 v118, -v16, v114, v118
	v_fma_f32 v119, -v16, v115, v119
	v_fma_f32 v120, -v16, v116, v120
	v_fma_f32 v4, -v16, v117, v4
	ds_read_b128 v[70:73], v21 offset:4688
	ds_read_b128 v[74:77], v21 offset:4704
	ds_read_b128 v[78:81], v21 offset:4720
	ds_read_b128 v[82:85], v21 offset:4736
	ds_read_b128 v[86:89], v21 offset:4752
	ds_read_b128 v[90:93], v21 offset:4768
	ds_read_b128 v[94:97], v21 offset:4784
	ds_read_b128 v[98:101], v21 offset:4800
	ds_read_b128 v[102:105], v21 offset:4816
	ds_read_b128 v[106:109], v21 offset:4832
	ds_read_b128 v[110:113], v21 offset:4848
	ds_read_b128 v[114:117], v21 offset:4864
	s_waitcnt lgkmcnt(0)
	v_fma_f32 v22, -v5, v22, v5
	v_fma_f32 v23, -v5, v23, v121
	v_fma_f32 v24, -v5, v24, v122
	v_fma_f32 v25, -v5, v25, v123
	v_fma_f32 v122, -v5, v26, v124
	v_fma_f32 v123, -v5, v27, v125
	v_fma_f32 v124, -v5, v28, v126
	v_fma_f32 v125, -v5, v29, v127
	v_fma_f32 v126, -v5, v30, v128
	v_fma_f32 v127, -v5, v31, v129
	v_fma_f32 v128, -v5, v32, v130
	v_fma_f32 v129, -v5, v33, v131
	v_fma_f32 v130, -v5, v34, v132
	v_fma_f32 v131, -v5, v35, v133
	v_fma_f32 v132, -v5, v36, v134
	v_fma_f32 v133, -v5, v37, v135
	v_fma_f32 v134, -v5, v38, v136
	v_fma_f32 v135, -v5, v39, v137
	v_fma_f32 v136, -v5, v40, v138
	v_fma_f32 v137, -v5, v41, v139
	v_fma_f32 v138, -v5, v42, v140
	v_fma_f32 v139, -v5, v43, v141
	v_fma_f32 v140, -v5, v44, v142
	v_fma_f32 v141, -v5, v45, v143
	v_fma_f32 v142, -v5, v46, v144
	v_fma_f32 v143, -v5, v47, v145
	v_fma_f32 v144, -v5, v48, v146
	v_fma_f32 v145, -v5, v49, v147
	v_fma_f32 v146, -v5, v50, v148
	v_fma_f32 v147, -v5, v51, v149
	v_fma_f32 v148, -v5, v52, v150
	v_fma_f32 v149, -v5, v53, v151
	v_fma_f32 v150, -v5, v54, v152
	v_fma_f32 v151, -v5, v55, v153
	v_fma_f32 v152, -v5, v56, v154
	v_fma_f32 v153, -v5, v57, v155
	v_fma_f32 v154, -v5, v58, v156
	v_fma_f32 v155, -v5, v59, v157
	v_fma_f32 v156, -v5, v60, v158
	v_fma_f32 v157, -v5, v61, v159
	v_fma_f32 v158, -v5, v62, v160
	v_fma_f32 v159, -v5, v63, v161
	v_fma_f32 v160, -v5, v64, v162
	v_fma_f32 v161, -v5, v65, v163
	v_fma_f32 v162, -v5, v66, v118
	v_fma_f32 v163, -v5, v67, v119
	v_fma_f32 v164, -v5, v68, v120
	v_fma_f32 v4, -v5, v69, v4
	ds_read_b128 v[26:29], v21 offset:4960
	ds_read_b128 v[30:33], v21 offset:4976
	ds_read_b128 v[34:37], v21 offset:4992
	ds_read_b128 v[38:41], v21 offset:5008
	ds_read_b128 v[42:45], v21 offset:5024
	ds_read_b128 v[46:49], v21 offset:5040
	ds_read_b128 v[50:53], v21 offset:5056
	ds_read_b128 v[54:57], v21 offset:5072
	ds_read_b128 v[58:61], v21 offset:5088
	ds_read_b128 v[62:65], v21 offset:5104
	ds_read_b128 v[66:69], v21 offset:5120
	ds_read_b128 v[118:121], v21 offset:5136
	v_fma_f32 v5, -v23, v70, v22
	v_fma_f32 v22, -v23, v71, v23
	v_fma_f32 v165, -v23, v72, v24
	v_fma_f32 v166, -v23, v73, v25
	v_fma_f32 v122, -v23, v74, v122
	v_fma_f32 v123, -v23, v75, v123
	v_fma_f32 v124, -v23, v76, v124
	v_fma_f32 v125, -v23, v77, v125
	v_fma_f32 v126, -v23, v78, v126
	v_fma_f32 v127, -v23, v79, v127
	v_fma_f32 v128, -v23, v80, v128
	v_fma_f32 v129, -v23, v81, v129
	v_fma_f32 v130, -v23, v82, v130
	v_fma_f32 v131, -v23, v83, v131
	v_fma_f32 v132, -v23, v84, v132
	v_fma_f32 v133, -v23, v85, v133
	v_fma_f32 v134, -v23, v86, v134
	v_fma_f32 v135, -v23, v87, v135
	v_fma_f32 v136, -v23, v88, v136
	v_fma_f32 v137, -v23, v89, v137
	v_fma_f32 v138, -v23, v90, v138
	v_fma_f32 v139, -v23, v91, v139
	v_fma_f32 v140, -v23, v92, v140
	v_fma_f32 v141, -v23, v93, v141
	v_fma_f32 v142, -v23, v94, v142
	v_fma_f32 v143, -v23, v95, v143
	v_fma_f32 v144, -v23, v96, v144
	v_fma_f32 v145, -v23, v97, v145
	v_fma_f32 v146, -v23, v98, v146
	v_fma_f32 v147, -v23, v99, v147
	v_fma_f32 v148, -v23, v100, v148
	v_fma_f32 v149, -v23, v101, v149
	v_fma_f32 v150, -v23, v102, v150
	v_fma_f32 v151, -v23, v103, v151
	v_fma_f32 v152, -v23, v104, v152
	v_fma_f32 v153, -v23, v105, v153
	v_fma_f32 v154, -v23, v106, v154
	v_fma_f32 v155, -v23, v107, v155
	v_fma_f32 v156, -v23, v108, v156
	v_fma_f32 v157, -v23, v109, v157
	v_fma_f32 v158, -v23, v110, v158
	v_fma_f32 v159, -v23, v111, v159
	v_fma_f32 v160, -v23, v112, v160
	v_fma_f32 v161, -v23, v113, v161
	v_fma_f32 v114, -v23, v114, v162
	v_fma_f32 v115, -v23, v115, v163
	v_fma_f32 v116, -v23, v116, v164
	v_fma_f32 v4, -v23, v117, v4
	ds_read_b128 v[70:73], v21 offset:5248
	ds_read_b128 v[74:77], v21 offset:5264
	ds_read_b128 v[78:81], v21 offset:5280
	ds_read_b128 v[82:85], v21 offset:5296
	ds_read_b128 v[86:89], v21 offset:5312
	ds_read_b128 v[90:93], v21 offset:5328
	ds_read_b128 v[94:97], v21 offset:5344
	ds_read_b128 v[98:101], v21 offset:5360
	ds_read_b128 v[102:105], v21 offset:5376
	ds_read_b128 v[106:109], v21 offset:5392
	ds_read_b128 v[110:113], v21 offset:5408
	s_waitcnt lgkmcnt(0)
	v_fma_f32 v25, -v165, v26, v5
	v_fma_f32 v24, -v165, v27, v22
	v_fma_f32 v23, -v165, v28, v165
	v_fma_f32 v22, -v165, v29, v166
	v_fma_f32 v5, -v165, v30, v122
	v_fma_f32 v117, -v165, v31, v123
	v_fma_f32 v122, -v165, v32, v124
	v_fma_f32 v123, -v165, v33, v125
	v_fma_f32 v124, -v165, v34, v126
	v_fma_f32 v125, -v165, v35, v127
	v_fma_f32 v126, -v165, v36, v128
	v_fma_f32 v127, -v165, v37, v129
	v_fma_f32 v128, -v165, v38, v130
	v_fma_f32 v129, -v165, v39, v131
	v_fma_f32 v130, -v165, v40, v132
	v_fma_f32 v131, -v165, v41, v133
	v_fma_f32 v132, -v165, v42, v134
	v_fma_f32 v133, -v165, v43, v135
	v_fma_f32 v134, -v165, v44, v136
	v_fma_f32 v135, -v165, v45, v137
	v_fma_f32 v136, -v165, v46, v138
	v_fma_f32 v137, -v165, v47, v139
	v_fma_f32 v138, -v165, v48, v140
	v_fma_f32 v139, -v165, v49, v141
	v_fma_f32 v140, -v165, v50, v142
	v_fma_f32 v141, -v165, v51, v143
	v_fma_f32 v142, -v165, v52, v144
	v_fma_f32 v143, -v165, v53, v145
	v_fma_f32 v144, -v165, v54, v146
	v_fma_f32 v145, -v165, v55, v147
	v_fma_f32 v146, -v165, v56, v148
	v_fma_f32 v147, -v165, v57, v149
	v_fma_f32 v148, -v165, v58, v150
	v_fma_f32 v149, -v165, v59, v151
	v_fma_f32 v150, -v165, v60, v152
	v_fma_f32 v151, -v165, v61, v153
	v_fma_f32 v152, -v165, v62, v154
	v_fma_f32 v153, -v165, v63, v155
	v_fma_f32 v154, -v165, v64, v156
	v_fma_f32 v155, -v165, v65, v157
	v_fma_f32 v156, -v165, v66, v158
	v_fma_f32 v157, -v165, v67, v159
	v_fma_f32 v158, -v165, v68, v160
	v_fma_f32 v159, -v165, v69, v161
	v_fma_f32 v114, -v165, v118, v114
	v_fma_f32 v115, -v165, v119, v115
	v_fma_f32 v116, -v165, v120, v116
	v_fma_f32 v4, -v165, v121, v4
	ds_read_b128 v[26:29], v21 offset:5520
	ds_read_b128 v[30:33], v21 offset:5536
	ds_read_b128 v[34:37], v21 offset:5552
	ds_read_b128 v[38:41], v21 offset:5568
	ds_read_b128 v[42:45], v21 offset:5584
	ds_read_b128 v[46:49], v21 offset:5600
	ds_read_b128 v[50:53], v21 offset:5616
	ds_read_b128 v[54:57], v21 offset:5632
	ds_read_b128 v[58:61], v21 offset:5648
	ds_read_b128 v[62:65], v21 offset:5664
	ds_read_b128 v[66:69], v21 offset:5680
	v_fma_f32 v5, -v22, v70, v5
	v_fma_f32 v117, -v22, v71, v117
	v_fma_f32 v118, -v22, v72, v122
	v_fma_f32 v119, -v22, v73, v123
	v_fma_f32 v120, -v22, v74, v124
	v_fma_f32 v121, -v22, v75, v125
	v_fma_f32 v122, -v22, v76, v126
	v_fma_f32 v123, -v22, v77, v127
	v_fma_f32 v124, -v22, v78, v128
	v_fma_f32 v125, -v22, v79, v129
	v_fma_f32 v126, -v22, v80, v130
	v_fma_f32 v127, -v22, v81, v131
	v_fma_f32 v128, -v22, v82, v132
	v_fma_f32 v129, -v22, v83, v133
	v_fma_f32 v130, -v22, v84, v134
	v_fma_f32 v131, -v22, v85, v135
	v_fma_f32 v132, -v22, v86, v136
	v_fma_f32 v133, -v22, v87, v137
	v_fma_f32 v134, -v22, v88, v138
	v_fma_f32 v135, -v22, v89, v139
	v_fma_f32 v136, -v22, v90, v140
	v_fma_f32 v137, -v22, v91, v141
	v_fma_f32 v138, -v22, v92, v142
	v_fma_f32 v139, -v22, v93, v143
	v_fma_f32 v140, -v22, v94, v144
	v_fma_f32 v141, -v22, v95, v145
	v_fma_f32 v142, -v22, v96, v146
	v_fma_f32 v143, -v22, v97, v147
	v_fma_f32 v144, -v22, v98, v148
	v_fma_f32 v145, -v22, v99, v149
	v_fma_f32 v146, -v22, v100, v150
	v_fma_f32 v147, -v22, v101, v151
	v_fma_f32 v148, -v22, v102, v152
	v_fma_f32 v149, -v22, v103, v153
	v_fma_f32 v150, -v22, v104, v154
	v_fma_f32 v151, -v22, v105, v155
	v_fma_f32 v152, -v22, v106, v156
	v_fma_f32 v153, -v22, v107, v157
	v_fma_f32 v154, -v22, v108, v158
	v_fma_f32 v155, -v22, v109, v159
	v_fma_f32 v114, -v22, v110, v114
	v_fma_f32 v115, -v22, v111, v115
	v_fma_f32 v116, -v22, v112, v116
	v_fma_f32 v4, -v22, v113, v4
	ds_read_b128 v[70:73], v21 offset:5792
	ds_read_b128 v[74:77], v21 offset:5808
	ds_read_b128 v[78:81], v21 offset:5824
	ds_read_b128 v[82:85], v21 offset:5840
	ds_read_b128 v[86:89], v21 offset:5856
	ds_read_b128 v[90:93], v21 offset:5872
	ds_read_b128 v[94:97], v21 offset:5888
	ds_read_b128 v[98:101], v21 offset:5904
	ds_read_b128 v[102:105], v21 offset:5920
	ds_read_b128 v[106:109], v21 offset:5936
	ds_read_b128 v[110:113], v21 offset:5952
	s_waitcnt lgkmcnt(0)
	v_fma_f32 v26, -v5, v26, v5
	v_fma_f32 v27, -v5, v27, v117
	v_fma_f32 v28, -v5, v28, v118
	v_fma_f32 v29, -v5, v29, v119
	v_fma_f32 v118, -v5, v30, v120
	v_fma_f32 v119, -v5, v31, v121
	v_fma_f32 v120, -v5, v32, v122
	v_fma_f32 v121, -v5, v33, v123
	v_fma_f32 v122, -v5, v34, v124
	v_fma_f32 v123, -v5, v35, v125
	v_fma_f32 v124, -v5, v36, v126
	v_fma_f32 v125, -v5, v37, v127
	v_fma_f32 v126, -v5, v38, v128
	v_fma_f32 v127, -v5, v39, v129
	v_fma_f32 v128, -v5, v40, v130
	v_fma_f32 v129, -v5, v41, v131
	v_fma_f32 v130, -v5, v42, v132
	v_fma_f32 v131, -v5, v43, v133
	v_fma_f32 v132, -v5, v44, v134
	v_fma_f32 v133, -v5, v45, v135
	v_fma_f32 v134, -v5, v46, v136
	v_fma_f32 v135, -v5, v47, v137
	v_fma_f32 v136, -v5, v48, v138
	v_fma_f32 v137, -v5, v49, v139
	v_fma_f32 v138, -v5, v50, v140
	v_fma_f32 v139, -v5, v51, v141
	v_fma_f32 v140, -v5, v52, v142
	v_fma_f32 v141, -v5, v53, v143
	v_fma_f32 v142, -v5, v54, v144
	v_fma_f32 v143, -v5, v55, v145
	v_fma_f32 v144, -v5, v56, v146
	v_fma_f32 v145, -v5, v57, v147
	v_fma_f32 v146, -v5, v58, v148
	v_fma_f32 v147, -v5, v59, v149
	v_fma_f32 v148, -v5, v60, v150
	v_fma_f32 v149, -v5, v61, v151
	v_fma_f32 v150, -v5, v62, v152
	v_fma_f32 v151, -v5, v63, v153
	v_fma_f32 v152, -v5, v64, v154
	v_fma_f32 v153, -v5, v65, v155
	v_fma_f32 v154, -v5, v66, v114
	v_fma_f32 v155, -v5, v67, v115
	v_fma_f32 v156, -v5, v68, v116
	v_fma_f32 v4, -v5, v69, v4
	ds_read_b128 v[30:33], v21 offset:6064
	ds_read_b128 v[34:37], v21 offset:6080
	ds_read_b128 v[38:41], v21 offset:6096
	ds_read_b128 v[42:45], v21 offset:6112
	ds_read_b128 v[46:49], v21 offset:6128
	ds_read_b128 v[50:53], v21 offset:6144
	ds_read_b128 v[54:57], v21 offset:6160
	ds_read_b128 v[58:61], v21 offset:6176
	ds_read_b128 v[62:65], v21 offset:6192
	ds_read_b128 v[66:69], v21 offset:6208
	ds_read_b128 v[114:117], v21 offset:6224
	v_fma_f32 v5, -v27, v70, v26
	v_fma_f32 v26, -v27, v71, v27
	v_fma_f32 v157, -v27, v72, v28
	v_fma_f32 v158, -v27, v73, v29
	v_fma_f32 v118, -v27, v74, v118
	v_fma_f32 v119, -v27, v75, v119
	v_fma_f32 v120, -v27, v76, v120
	v_fma_f32 v121, -v27, v77, v121
	v_fma_f32 v122, -v27, v78, v122
	v_fma_f32 v123, -v27, v79, v123
	v_fma_f32 v124, -v27, v80, v124
	v_fma_f32 v125, -v27, v81, v125
	v_fma_f32 v126, -v27, v82, v126
	v_fma_f32 v127, -v27, v83, v127
	v_fma_f32 v128, -v27, v84, v128
	v_fma_f32 v129, -v27, v85, v129
	v_fma_f32 v130, -v27, v86, v130
	v_fma_f32 v131, -v27, v87, v131
	v_fma_f32 v132, -v27, v88, v132
	v_fma_f32 v133, -v27, v89, v133
	v_fma_f32 v134, -v27, v90, v134
	v_fma_f32 v135, -v27, v91, v135
	v_fma_f32 v136, -v27, v92, v136
	v_fma_f32 v137, -v27, v93, v137
	v_fma_f32 v138, -v27, v94, v138
	v_fma_f32 v139, -v27, v95, v139
	v_fma_f32 v140, -v27, v96, v140
	v_fma_f32 v141, -v27, v97, v141
	v_fma_f32 v142, -v27, v98, v142
	v_fma_f32 v143, -v27, v99, v143
	v_fma_f32 v144, -v27, v100, v144
	v_fma_f32 v145, -v27, v101, v145
	v_fma_f32 v146, -v27, v102, v146
	v_fma_f32 v147, -v27, v103, v147
	v_fma_f32 v148, -v27, v104, v148
	v_fma_f32 v149, -v27, v105, v149
	v_fma_f32 v150, -v27, v106, v150
	v_fma_f32 v151, -v27, v107, v151
	v_fma_f32 v152, -v27, v108, v152
	v_fma_f32 v153, -v27, v109, v153
	v_fma_f32 v110, -v27, v110, v154
	v_fma_f32 v111, -v27, v111, v155
	v_fma_f32 v112, -v27, v112, v156
	v_fma_f32 v4, -v27, v113, v4
	ds_read_b128 v[70:73], v21 offset:6352
	ds_read_b128 v[74:77], v21 offset:6368
	ds_read_b128 v[78:81], v21 offset:6384
	ds_read_b128 v[82:85], v21 offset:6400
	ds_read_b128 v[86:89], v21 offset:6416
	ds_read_b128 v[90:93], v21 offset:6432
	ds_read_b128 v[94:97], v21 offset:6448
	ds_read_b128 v[98:101], v21 offset:6464
	ds_read_b128 v[102:105], v21 offset:6480
	ds_read_b128 v[106:109], v21 offset:6496
	s_waitcnt lgkmcnt(0)
	v_fma_f32 v29, -v157, v30, v5
	v_fma_f32 v28, -v157, v31, v26
	v_fma_f32 v27, -v157, v32, v157
	v_fma_f32 v26, -v157, v33, v158
	v_fma_f32 v5, -v157, v34, v118
	v_fma_f32 v113, -v157, v35, v119
	v_fma_f32 v118, -v157, v36, v120
	v_fma_f32 v119, -v157, v37, v121
	v_fma_f32 v120, -v157, v38, v122
	v_fma_f32 v121, -v157, v39, v123
	v_fma_f32 v122, -v157, v40, v124
	v_fma_f32 v123, -v157, v41, v125
	v_fma_f32 v124, -v157, v42, v126
	v_fma_f32 v125, -v157, v43, v127
	v_fma_f32 v126, -v157, v44, v128
	v_fma_f32 v127, -v157, v45, v129
	v_fma_f32 v128, -v157, v46, v130
	v_fma_f32 v129, -v157, v47, v131
	v_fma_f32 v130, -v157, v48, v132
	v_fma_f32 v131, -v157, v49, v133
	v_fma_f32 v132, -v157, v50, v134
	v_fma_f32 v133, -v157, v51, v135
	v_fma_f32 v134, -v157, v52, v136
	v_fma_f32 v135, -v157, v53, v137
	v_fma_f32 v136, -v157, v54, v138
	v_fma_f32 v137, -v157, v55, v139
	v_fma_f32 v138, -v157, v56, v140
	v_fma_f32 v139, -v157, v57, v141
	v_fma_f32 v140, -v157, v58, v142
	v_fma_f32 v141, -v157, v59, v143
	v_fma_f32 v142, -v157, v60, v144
	v_fma_f32 v143, -v157, v61, v145
	v_fma_f32 v144, -v157, v62, v146
	v_fma_f32 v145, -v157, v63, v147
	v_fma_f32 v146, -v157, v64, v148
	v_fma_f32 v147, -v157, v65, v149
	v_fma_f32 v148, -v157, v66, v150
	v_fma_f32 v149, -v157, v67, v151
	v_fma_f32 v150, -v157, v68, v152
	v_fma_f32 v151, -v157, v69, v153
	v_fma_f32 v110, -v157, v114, v110
	v_fma_f32 v111, -v157, v115, v111
	v_fma_f32 v112, -v157, v116, v112
	v_fma_f32 v4, -v157, v117, v4
	ds_read_b128 v[30:33], v21 offset:6624
	ds_read_b128 v[34:37], v21 offset:6640
	ds_read_b128 v[38:41], v21 offset:6656
	ds_read_b128 v[42:45], v21 offset:6672
	ds_read_b128 v[46:49], v21 offset:6688
	ds_read_b128 v[50:53], v21 offset:6704
	ds_read_b128 v[54:57], v21 offset:6720
	ds_read_b128 v[58:61], v21 offset:6736
	ds_read_b128 v[62:65], v21 offset:6752
	ds_read_b128 v[66:69], v21 offset:6768
	v_fma_f32 v5, -v26, v70, v5
	v_fma_f32 v113, -v26, v71, v113
	v_fma_f32 v114, -v26, v72, v118
	v_fma_f32 v115, -v26, v73, v119
	v_fma_f32 v116, -v26, v74, v120
	v_fma_f32 v117, -v26, v75, v121
	v_fma_f32 v118, -v26, v76, v122
	v_fma_f32 v119, -v26, v77, v123
	v_fma_f32 v120, -v26, v78, v124
	v_fma_f32 v121, -v26, v79, v125
	v_fma_f32 v122, -v26, v80, v126
	v_fma_f32 v123, -v26, v81, v127
	v_fma_f32 v124, -v26, v82, v128
	v_fma_f32 v125, -v26, v83, v129
	v_fma_f32 v126, -v26, v84, v130
	v_fma_f32 v127, -v26, v85, v131
	v_fma_f32 v128, -v26, v86, v132
	v_fma_f32 v129, -v26, v87, v133
	v_fma_f32 v130, -v26, v88, v134
	v_fma_f32 v131, -v26, v89, v135
	v_fma_f32 v132, -v26, v90, v136
	v_fma_f32 v133, -v26, v91, v137
	v_fma_f32 v134, -v26, v92, v138
	v_fma_f32 v135, -v26, v93, v139
	v_fma_f32 v136, -v26, v94, v140
	v_fma_f32 v137, -v26, v95, v141
	v_fma_f32 v138, -v26, v96, v142
	v_fma_f32 v139, -v26, v97, v143
	v_fma_f32 v140, -v26, v98, v144
	v_fma_f32 v141, -v26, v99, v145
	v_fma_f32 v142, -v26, v100, v146
	v_fma_f32 v143, -v26, v101, v147
	v_fma_f32 v144, -v26, v102, v148
	v_fma_f32 v145, -v26, v103, v149
	v_fma_f32 v146, -v26, v104, v150
	v_fma_f32 v147, -v26, v105, v151
	v_fma_f32 v110, -v26, v106, v110
	v_fma_f32 v111, -v26, v107, v111
	v_fma_f32 v112, -v26, v108, v112
	v_fma_f32 v4, -v26, v109, v4
	ds_read_b128 v[70:73], v21 offset:6896
	ds_read_b128 v[74:77], v21 offset:6912
	ds_read_b128 v[78:81], v21 offset:6928
	ds_read_b128 v[82:85], v21 offset:6944
	ds_read_b128 v[86:89], v21 offset:6960
	ds_read_b128 v[90:93], v21 offset:6976
	ds_read_b128 v[94:97], v21 offset:6992
	ds_read_b128 v[98:101], v21 offset:7008
	ds_read_b128 v[102:105], v21 offset:7024
	ds_read_b128 v[106:109], v21 offset:7040
	s_waitcnt lgkmcnt(0)
	v_fma_f32 v30, -v5, v30, v5
	v_fma_f32 v31, -v5, v31, v113
	v_fma_f32 v32, -v5, v32, v114
	v_fma_f32 v33, -v5, v33, v115
	v_fma_f32 v114, -v5, v34, v116
	v_fma_f32 v115, -v5, v35, v117
	v_fma_f32 v116, -v5, v36, v118
	v_fma_f32 v117, -v5, v37, v119
	v_fma_f32 v118, -v5, v38, v120
	v_fma_f32 v119, -v5, v39, v121
	v_fma_f32 v120, -v5, v40, v122
	v_fma_f32 v121, -v5, v41, v123
	v_fma_f32 v122, -v5, v42, v124
	v_fma_f32 v123, -v5, v43, v125
	v_fma_f32 v124, -v5, v44, v126
	v_fma_f32 v125, -v5, v45, v127
	v_fma_f32 v126, -v5, v46, v128
	v_fma_f32 v127, -v5, v47, v129
	v_fma_f32 v128, -v5, v48, v130
	v_fma_f32 v129, -v5, v49, v131
	v_fma_f32 v130, -v5, v50, v132
	v_fma_f32 v131, -v5, v51, v133
	v_fma_f32 v132, -v5, v52, v134
	v_fma_f32 v133, -v5, v53, v135
	v_fma_f32 v134, -v5, v54, v136
	v_fma_f32 v135, -v5, v55, v137
	v_fma_f32 v136, -v5, v56, v138
	v_fma_f32 v137, -v5, v57, v139
	v_fma_f32 v138, -v5, v58, v140
	v_fma_f32 v139, -v5, v59, v141
	v_fma_f32 v140, -v5, v60, v142
	v_fma_f32 v141, -v5, v61, v143
	v_fma_f32 v142, -v5, v62, v144
	v_fma_f32 v143, -v5, v63, v145
	v_fma_f32 v144, -v5, v64, v146
	v_fma_f32 v145, -v5, v65, v147
	v_fma_f32 v146, -v5, v66, v110
	v_fma_f32 v147, -v5, v67, v111
	v_fma_f32 v148, -v5, v68, v112
	v_fma_f32 v4, -v5, v69, v4
	ds_read_b128 v[34:37], v21 offset:7168
	ds_read_b128 v[38:41], v21 offset:7184
	ds_read_b128 v[42:45], v21 offset:7200
	ds_read_b128 v[46:49], v21 offset:7216
	ds_read_b128 v[50:53], v21 offset:7232
	ds_read_b128 v[54:57], v21 offset:7248
	ds_read_b128 v[58:61], v21 offset:7264
	ds_read_b128 v[62:65], v21 offset:7280
	ds_read_b128 v[66:69], v21 offset:7296
	ds_read_b128 v[110:113], v21 offset:7312
	v_fma_f32 v5, -v31, v70, v30
	v_fma_f32 v30, -v31, v71, v31
	v_fma_f32 v149, -v31, v72, v32
	v_fma_f32 v150, -v31, v73, v33
	v_fma_f32 v114, -v31, v74, v114
	v_fma_f32 v115, -v31, v75, v115
	v_fma_f32 v116, -v31, v76, v116
	v_fma_f32 v117, -v31, v77, v117
	v_fma_f32 v118, -v31, v78, v118
	v_fma_f32 v119, -v31, v79, v119
	v_fma_f32 v120, -v31, v80, v120
	v_fma_f32 v121, -v31, v81, v121
	v_fma_f32 v122, -v31, v82, v122
	v_fma_f32 v123, -v31, v83, v123
	v_fma_f32 v124, -v31, v84, v124
	v_fma_f32 v125, -v31, v85, v125
	v_fma_f32 v126, -v31, v86, v126
	v_fma_f32 v127, -v31, v87, v127
	v_fma_f32 v128, -v31, v88, v128
	v_fma_f32 v129, -v31, v89, v129
	v_fma_f32 v130, -v31, v90, v130
	v_fma_f32 v131, -v31, v91, v131
	v_fma_f32 v132, -v31, v92, v132
	v_fma_f32 v133, -v31, v93, v133
	v_fma_f32 v134, -v31, v94, v134
	v_fma_f32 v135, -v31, v95, v135
	v_fma_f32 v136, -v31, v96, v136
	v_fma_f32 v137, -v31, v97, v137
	v_fma_f32 v138, -v31, v98, v138
	v_fma_f32 v139, -v31, v99, v139
	v_fma_f32 v140, -v31, v100, v140
	v_fma_f32 v141, -v31, v101, v141
	v_fma_f32 v142, -v31, v102, v142
	v_fma_f32 v143, -v31, v103, v143
	v_fma_f32 v144, -v31, v104, v144
	v_fma_f32 v145, -v31, v105, v145
	v_fma_f32 v106, -v31, v106, v146
	v_fma_f32 v107, -v31, v107, v147
	v_fma_f32 v108, -v31, v108, v148
	v_fma_f32 v4, -v31, v109, v4
	ds_read_b128 v[70:73], v21 offset:7456
	ds_read_b128 v[74:77], v21 offset:7472
	ds_read_b128 v[78:81], v21 offset:7488
	ds_read_b128 v[82:85], v21 offset:7504
	ds_read_b128 v[86:89], v21 offset:7520
	ds_read_b128 v[90:93], v21 offset:7536
	ds_read_b128 v[94:97], v21 offset:7552
	ds_read_b128 v[98:101], v21 offset:7568
	ds_read_b128 v[102:105], v21 offset:7584
	s_waitcnt lgkmcnt(0)
	v_fma_f32 v33, -v149, v34, v5
	v_fma_f32 v32, -v149, v35, v30
	v_fma_f32 v31, -v149, v36, v149
	v_fma_f32 v30, -v149, v37, v150
	v_fma_f32 v5, -v149, v38, v114
	v_fma_f32 v109, -v149, v39, v115
	v_fma_f32 v114, -v149, v40, v116
	v_fma_f32 v115, -v149, v41, v117
	v_fma_f32 v116, -v149, v42, v118
	v_fma_f32 v117, -v149, v43, v119
	v_fma_f32 v118, -v149, v44, v120
	v_fma_f32 v119, -v149, v45, v121
	v_fma_f32 v120, -v149, v46, v122
	v_fma_f32 v121, -v149, v47, v123
	v_fma_f32 v122, -v149, v48, v124
	v_fma_f32 v123, -v149, v49, v125
	v_fma_f32 v124, -v149, v50, v126
	v_fma_f32 v125, -v149, v51, v127
	v_fma_f32 v126, -v149, v52, v128
	v_fma_f32 v127, -v149, v53, v129
	v_fma_f32 v128, -v149, v54, v130
	v_fma_f32 v129, -v149, v55, v131
	v_fma_f32 v130, -v149, v56, v132
	v_fma_f32 v131, -v149, v57, v133
	v_fma_f32 v132, -v149, v58, v134
	v_fma_f32 v133, -v149, v59, v135
	v_fma_f32 v134, -v149, v60, v136
	v_fma_f32 v135, -v149, v61, v137
	v_fma_f32 v136, -v149, v62, v138
	v_fma_f32 v137, -v149, v63, v139
	v_fma_f32 v138, -v149, v64, v140
	v_fma_f32 v139, -v149, v65, v141
	v_fma_f32 v140, -v149, v66, v142
	v_fma_f32 v141, -v149, v67, v143
	v_fma_f32 v142, -v149, v68, v144
	v_fma_f32 v143, -v149, v69, v145
	v_fma_f32 v106, -v149, v110, v106
	v_fma_f32 v107, -v149, v111, v107
	v_fma_f32 v108, -v149, v112, v108
	v_fma_f32 v4, -v149, v113, v4
	ds_read_b128 v[34:37], v21 offset:7728
	ds_read_b128 v[38:41], v21 offset:7744
	ds_read_b128 v[42:45], v21 offset:7760
	ds_read_b128 v[46:49], v21 offset:7776
	ds_read_b128 v[50:53], v21 offset:7792
	ds_read_b128 v[54:57], v21 offset:7808
	ds_read_b128 v[58:61], v21 offset:7824
	ds_read_b128 v[62:65], v21 offset:7840
	ds_read_b128 v[66:69], v21 offset:7856
	v_fma_f32 v5, -v30, v70, v5
	v_fma_f32 v109, -v30, v71, v109
	v_fma_f32 v110, -v30, v72, v114
	v_fma_f32 v111, -v30, v73, v115
	v_fma_f32 v112, -v30, v74, v116
	v_fma_f32 v113, -v30, v75, v117
	v_fma_f32 v114, -v30, v76, v118
	v_fma_f32 v115, -v30, v77, v119
	v_fma_f32 v116, -v30, v78, v120
	v_fma_f32 v117, -v30, v79, v121
	v_fma_f32 v118, -v30, v80, v122
	v_fma_f32 v119, -v30, v81, v123
	v_fma_f32 v120, -v30, v82, v124
	v_fma_f32 v121, -v30, v83, v125
	v_fma_f32 v122, -v30, v84, v126
	v_fma_f32 v123, -v30, v85, v127
	v_fma_f32 v124, -v30, v86, v128
	v_fma_f32 v125, -v30, v87, v129
	v_fma_f32 v126, -v30, v88, v130
	v_fma_f32 v127, -v30, v89, v131
	v_fma_f32 v128, -v30, v90, v132
	v_fma_f32 v129, -v30, v91, v133
	v_fma_f32 v130, -v30, v92, v134
	v_fma_f32 v131, -v30, v93, v135
	v_fma_f32 v132, -v30, v94, v136
	v_fma_f32 v133, -v30, v95, v137
	v_fma_f32 v134, -v30, v96, v138
	v_fma_f32 v135, -v30, v97, v139
	v_fma_f32 v136, -v30, v98, v140
	v_fma_f32 v137, -v30, v99, v141
	v_fma_f32 v138, -v30, v100, v142
	v_fma_f32 v139, -v30, v101, v143
	v_fma_f32 v106, -v30, v102, v106
	v_fma_f32 v107, -v30, v103, v107
	v_fma_f32 v108, -v30, v104, v108
	v_fma_f32 v4, -v30, v105, v4
	ds_read_b128 v[70:73], v21 offset:8000
	ds_read_b128 v[74:77], v21 offset:8016
	ds_read_b128 v[78:81], v21 offset:8032
	ds_read_b128 v[82:85], v21 offset:8048
	ds_read_b128 v[86:89], v21 offset:8064
	ds_read_b128 v[90:93], v21 offset:8080
	ds_read_b128 v[94:97], v21 offset:8096
	ds_read_b128 v[98:101], v21 offset:8112
	ds_read_b128 v[102:105], v21 offset:8128
	s_waitcnt lgkmcnt(0)
	v_fma_f32 v34, -v5, v34, v5
	v_fma_f32 v35, -v5, v35, v109
	v_fma_f32 v36, -v5, v36, v110
	v_fma_f32 v37, -v5, v37, v111
	v_fma_f32 v110, -v5, v38, v112
	v_fma_f32 v111, -v5, v39, v113
	v_fma_f32 v112, -v5, v40, v114
	v_fma_f32 v113, -v5, v41, v115
	v_fma_f32 v114, -v5, v42, v116
	v_fma_f32 v115, -v5, v43, v117
	v_fma_f32 v116, -v5, v44, v118
	v_fma_f32 v117, -v5, v45, v119
	v_fma_f32 v118, -v5, v46, v120
	v_fma_f32 v119, -v5, v47, v121
	v_fma_f32 v120, -v5, v48, v122
	v_fma_f32 v121, -v5, v49, v123
	v_fma_f32 v122, -v5, v50, v124
	v_fma_f32 v123, -v5, v51, v125
	v_fma_f32 v124, -v5, v52, v126
	v_fma_f32 v125, -v5, v53, v127
	v_fma_f32 v126, -v5, v54, v128
	v_fma_f32 v127, -v5, v55, v129
	v_fma_f32 v128, -v5, v56, v130
	v_fma_f32 v129, -v5, v57, v131
	v_fma_f32 v130, -v5, v58, v132
	v_fma_f32 v131, -v5, v59, v133
	v_fma_f32 v132, -v5, v60, v134
	v_fma_f32 v133, -v5, v61, v135
	v_fma_f32 v134, -v5, v62, v136
	v_fma_f32 v135, -v5, v63, v137
	v_fma_f32 v136, -v5, v64, v138
	v_fma_f32 v137, -v5, v65, v139
	v_fma_f32 v138, -v5, v66, v106
	v_fma_f32 v139, -v5, v67, v107
	v_fma_f32 v140, -v5, v68, v108
	v_fma_f32 v4, -v5, v69, v4
	ds_read_b128 v[38:41], v21 offset:8272
	ds_read_b128 v[42:45], v21 offset:8288
	ds_read_b128 v[46:49], v21 offset:8304
	ds_read_b128 v[50:53], v21 offset:8320
	ds_read_b128 v[54:57], v21 offset:8336
	ds_read_b128 v[58:61], v21 offset:8352
	ds_read_b128 v[62:65], v21 offset:8368
	ds_read_b128 v[66:69], v21 offset:8384
	ds_read_b128 v[106:109], v21 offset:8400
	v_fma_f32 v5, -v35, v70, v34
	v_fma_f32 v34, -v35, v71, v35
	v_fma_f32 v141, -v35, v72, v36
	v_fma_f32 v142, -v35, v73, v37
	v_fma_f32 v110, -v35, v74, v110
	v_fma_f32 v111, -v35, v75, v111
	v_fma_f32 v112, -v35, v76, v112
	v_fma_f32 v113, -v35, v77, v113
	v_fma_f32 v114, -v35, v78, v114
	v_fma_f32 v115, -v35, v79, v115
	v_fma_f32 v116, -v35, v80, v116
	v_fma_f32 v117, -v35, v81, v117
	v_fma_f32 v118, -v35, v82, v118
	v_fma_f32 v119, -v35, v83, v119
	v_fma_f32 v120, -v35, v84, v120
	v_fma_f32 v121, -v35, v85, v121
	v_fma_f32 v122, -v35, v86, v122
	v_fma_f32 v123, -v35, v87, v123
	v_fma_f32 v124, -v35, v88, v124
	v_fma_f32 v125, -v35, v89, v125
	v_fma_f32 v126, -v35, v90, v126
	v_fma_f32 v127, -v35, v91, v127
	v_fma_f32 v128, -v35, v92, v128
	v_fma_f32 v129, -v35, v93, v129
	v_fma_f32 v130, -v35, v94, v130
	v_fma_f32 v131, -v35, v95, v131
	v_fma_f32 v132, -v35, v96, v132
	v_fma_f32 v133, -v35, v97, v133
	v_fma_f32 v134, -v35, v98, v134
	v_fma_f32 v135, -v35, v99, v135
	v_fma_f32 v136, -v35, v100, v136
	v_fma_f32 v137, -v35, v101, v137
	v_fma_f32 v102, -v35, v102, v138
	v_fma_f32 v103, -v35, v103, v139
	v_fma_f32 v104, -v35, v104, v140
	v_fma_f32 v4, -v35, v105, v4
	ds_read_b128 v[70:73], v21 offset:8560
	ds_read_b128 v[74:77], v21 offset:8576
	ds_read_b128 v[78:81], v21 offset:8592
	ds_read_b128 v[82:85], v21 offset:8608
	ds_read_b128 v[86:89], v21 offset:8624
	ds_read_b128 v[90:93], v21 offset:8640
	ds_read_b128 v[94:97], v21 offset:8656
	ds_read_b128 v[98:101], v21 offset:8672
	s_waitcnt lgkmcnt(0)
	v_fma_f32 v37, -v141, v38, v5
	v_fma_f32 v36, -v141, v39, v34
	v_fma_f32 v35, -v141, v40, v141
	v_fma_f32 v34, -v141, v41, v142
	v_fma_f32 v5, -v141, v42, v110
	v_fma_f32 v105, -v141, v43, v111
	v_fma_f32 v110, -v141, v44, v112
	v_fma_f32 v111, -v141, v45, v113
	v_fma_f32 v112, -v141, v46, v114
	v_fma_f32 v113, -v141, v47, v115
	v_fma_f32 v114, -v141, v48, v116
	v_fma_f32 v115, -v141, v49, v117
	v_fma_f32 v116, -v141, v50, v118
	v_fma_f32 v117, -v141, v51, v119
	v_fma_f32 v118, -v141, v52, v120
	v_fma_f32 v119, -v141, v53, v121
	v_fma_f32 v120, -v141, v54, v122
	v_fma_f32 v121, -v141, v55, v123
	v_fma_f32 v122, -v141, v56, v124
	v_fma_f32 v123, -v141, v57, v125
	v_fma_f32 v124, -v141, v58, v126
	v_fma_f32 v125, -v141, v59, v127
	v_fma_f32 v126, -v141, v60, v128
	v_fma_f32 v127, -v141, v61, v129
	v_fma_f32 v128, -v141, v62, v130
	v_fma_f32 v129, -v141, v63, v131
	v_fma_f32 v130, -v141, v64, v132
	v_fma_f32 v131, -v141, v65, v133
	v_fma_f32 v132, -v141, v66, v134
	v_fma_f32 v133, -v141, v67, v135
	v_fma_f32 v134, -v141, v68, v136
	v_fma_f32 v135, -v141, v69, v137
	v_fma_f32 v102, -v141, v106, v102
	v_fma_f32 v103, -v141, v107, v103
	v_fma_f32 v104, -v141, v108, v104
	v_fma_f32 v4, -v141, v109, v4
	ds_read_b128 v[38:41], v21 offset:8832
	ds_read_b128 v[42:45], v21 offset:8848
	ds_read_b128 v[46:49], v21 offset:8864
	ds_read_b128 v[50:53], v21 offset:8880
	ds_read_b128 v[54:57], v21 offset:8896
	ds_read_b128 v[58:61], v21 offset:8912
	ds_read_b128 v[62:65], v21 offset:8928
	ds_read_b128 v[66:69], v21 offset:8944
	v_fma_f32 v5, -v34, v70, v5
	v_fma_f32 v105, -v34, v71, v105
	v_fma_f32 v106, -v34, v72, v110
	v_fma_f32 v107, -v34, v73, v111
	v_fma_f32 v108, -v34, v74, v112
	v_fma_f32 v109, -v34, v75, v113
	v_fma_f32 v110, -v34, v76, v114
	v_fma_f32 v111, -v34, v77, v115
	v_fma_f32 v112, -v34, v78, v116
	v_fma_f32 v113, -v34, v79, v117
	v_fma_f32 v114, -v34, v80, v118
	v_fma_f32 v115, -v34, v81, v119
	v_fma_f32 v116, -v34, v82, v120
	v_fma_f32 v117, -v34, v83, v121
	v_fma_f32 v118, -v34, v84, v122
	v_fma_f32 v119, -v34, v85, v123
	v_fma_f32 v120, -v34, v86, v124
	v_fma_f32 v121, -v34, v87, v125
	v_fma_f32 v122, -v34, v88, v126
	v_fma_f32 v123, -v34, v89, v127
	v_fma_f32 v124, -v34, v90, v128
	v_fma_f32 v125, -v34, v91, v129
	v_fma_f32 v126, -v34, v92, v130
	v_fma_f32 v127, -v34, v93, v131
	v_fma_f32 v128, -v34, v94, v132
	v_fma_f32 v129, -v34, v95, v133
	v_fma_f32 v130, -v34, v96, v134
	v_fma_f32 v131, -v34, v97, v135
	v_fma_f32 v102, -v34, v98, v102
	v_fma_f32 v103, -v34, v99, v103
	v_fma_f32 v104, -v34, v100, v104
	v_fma_f32 v4, -v34, v101, v4
	ds_read_b128 v[70:73], v21 offset:9104
	ds_read_b128 v[74:77], v21 offset:9120
	ds_read_b128 v[78:81], v21 offset:9136
	ds_read_b128 v[82:85], v21 offset:9152
	ds_read_b128 v[86:89], v21 offset:9168
	ds_read_b128 v[90:93], v21 offset:9184
	ds_read_b128 v[94:97], v21 offset:9200
	ds_read_b128 v[98:101], v21 offset:9216
	s_waitcnt lgkmcnt(0)
	v_fma_f32 v38, -v5, v38, v5
	v_fma_f32 v39, -v5, v39, v105
	v_fma_f32 v40, -v5, v40, v106
	v_fma_f32 v41, -v5, v41, v107
	v_fma_f32 v106, -v5, v42, v108
	v_fma_f32 v107, -v5, v43, v109
	v_fma_f32 v108, -v5, v44, v110
	v_fma_f32 v109, -v5, v45, v111
	v_fma_f32 v110, -v5, v46, v112
	v_fma_f32 v111, -v5, v47, v113
	v_fma_f32 v112, -v5, v48, v114
	v_fma_f32 v113, -v5, v49, v115
	v_fma_f32 v114, -v5, v50, v116
	v_fma_f32 v115, -v5, v51, v117
	v_fma_f32 v116, -v5, v52, v118
	v_fma_f32 v117, -v5, v53, v119
	v_fma_f32 v118, -v5, v54, v120
	v_fma_f32 v119, -v5, v55, v121
	v_fma_f32 v120, -v5, v56, v122
	v_fma_f32 v121, -v5, v57, v123
	v_fma_f32 v122, -v5, v58, v124
	v_fma_f32 v123, -v5, v59, v125
	v_fma_f32 v124, -v5, v60, v126
	v_fma_f32 v125, -v5, v61, v127
	v_fma_f32 v126, -v5, v62, v128
	v_fma_f32 v127, -v5, v63, v129
	v_fma_f32 v128, -v5, v64, v130
	v_fma_f32 v129, -v5, v65, v131
	v_fma_f32 v130, -v5, v66, v102
	v_fma_f32 v131, -v5, v67, v103
	v_fma_f32 v132, -v5, v68, v104
	v_fma_f32 v4, -v5, v69, v4
	ds_read_b128 v[42:45], v21 offset:9376
	ds_read_b128 v[46:49], v21 offset:9392
	ds_read_b128 v[50:53], v21 offset:9408
	ds_read_b128 v[54:57], v21 offset:9424
	ds_read_b128 v[58:61], v21 offset:9440
	ds_read_b128 v[62:65], v21 offset:9456
	ds_read_b128 v[66:69], v21 offset:9472
	ds_read_b128 v[102:105], v21 offset:9488
	v_fma_f32 v5, -v39, v70, v38
	v_fma_f32 v38, -v39, v71, v39
	v_fma_f32 v133, -v39, v72, v40
	v_fma_f32 v134, -v39, v73, v41
	v_fma_f32 v106, -v39, v74, v106
	v_fma_f32 v107, -v39, v75, v107
	v_fma_f32 v108, -v39, v76, v108
	v_fma_f32 v109, -v39, v77, v109
	v_fma_f32 v110, -v39, v78, v110
	v_fma_f32 v111, -v39, v79, v111
	v_fma_f32 v112, -v39, v80, v112
	v_fma_f32 v113, -v39, v81, v113
	v_fma_f32 v114, -v39, v82, v114
	v_fma_f32 v115, -v39, v83, v115
	v_fma_f32 v116, -v39, v84, v116
	v_fma_f32 v117, -v39, v85, v117
	v_fma_f32 v118, -v39, v86, v118
	v_fma_f32 v119, -v39, v87, v119
	v_fma_f32 v120, -v39, v88, v120
	v_fma_f32 v121, -v39, v89, v121
	v_fma_f32 v122, -v39, v90, v122
	v_fma_f32 v123, -v39, v91, v123
	v_fma_f32 v124, -v39, v92, v124
	v_fma_f32 v125, -v39, v93, v125
	v_fma_f32 v126, -v39, v94, v126
	v_fma_f32 v127, -v39, v95, v127
	v_fma_f32 v128, -v39, v96, v128
	v_fma_f32 v129, -v39, v97, v129
	v_fma_f32 v98, -v39, v98, v130
	v_fma_f32 v99, -v39, v99, v131
	v_fma_f32 v100, -v39, v100, v132
	v_fma_f32 v4, -v39, v101, v4
	ds_read_b128 v[70:73], v21 offset:9664
	ds_read_b128 v[74:77], v21 offset:9680
	ds_read_b128 v[78:81], v21 offset:9696
	ds_read_b128 v[82:85], v21 offset:9712
	ds_read_b128 v[86:89], v21 offset:9728
	ds_read_b128 v[90:93], v21 offset:9744
	ds_read_b128 v[94:97], v21 offset:9760
	s_waitcnt lgkmcnt(0)
	v_fma_f32 v41, -v133, v42, v5
	v_fma_f32 v40, -v133, v43, v38
	v_fma_f32 v39, -v133, v44, v133
	v_fma_f32 v38, -v133, v45, v134
	v_fma_f32 v5, -v133, v46, v106
	v_fma_f32 v101, -v133, v47, v107
	v_fma_f32 v106, -v133, v48, v108
	v_fma_f32 v107, -v133, v49, v109
	v_fma_f32 v108, -v133, v50, v110
	v_fma_f32 v109, -v133, v51, v111
	v_fma_f32 v110, -v133, v52, v112
	v_fma_f32 v111, -v133, v53, v113
	v_fma_f32 v112, -v133, v54, v114
	v_fma_f32 v113, -v133, v55, v115
	v_fma_f32 v114, -v133, v56, v116
	v_fma_f32 v115, -v133, v57, v117
	v_fma_f32 v116, -v133, v58, v118
	v_fma_f32 v117, -v133, v59, v119
	v_fma_f32 v118, -v133, v60, v120
	v_fma_f32 v119, -v133, v61, v121
	v_fma_f32 v120, -v133, v62, v122
	v_fma_f32 v121, -v133, v63, v123
	v_fma_f32 v122, -v133, v64, v124
	v_fma_f32 v123, -v133, v65, v125
	v_fma_f32 v124, -v133, v66, v126
	v_fma_f32 v125, -v133, v67, v127
	v_fma_f32 v126, -v133, v68, v128
	v_fma_f32 v127, -v133, v69, v129
	v_fma_f32 v98, -v133, v102, v98
	v_fma_f32 v99, -v133, v103, v99
	v_fma_f32 v100, -v133, v104, v100
	v_fma_f32 v4, -v133, v105, v4
	ds_read_b128 v[42:45], v21 offset:9936
	ds_read_b128 v[46:49], v21 offset:9952
	ds_read_b128 v[50:53], v21 offset:9968
	ds_read_b128 v[54:57], v21 offset:9984
	ds_read_b128 v[58:61], v21 offset:10000
	ds_read_b128 v[62:65], v21 offset:10016
	ds_read_b128 v[66:69], v21 offset:10032
	v_fma_f32 v5, -v38, v70, v5
	v_fma_f32 v101, -v38, v71, v101
	v_fma_f32 v102, -v38, v72, v106
	v_fma_f32 v103, -v38, v73, v107
	v_fma_f32 v104, -v38, v74, v108
	v_fma_f32 v105, -v38, v75, v109
	v_fma_f32 v106, -v38, v76, v110
	v_fma_f32 v107, -v38, v77, v111
	v_fma_f32 v108, -v38, v78, v112
	v_fma_f32 v109, -v38, v79, v113
	v_fma_f32 v110, -v38, v80, v114
	v_fma_f32 v111, -v38, v81, v115
	v_fma_f32 v112, -v38, v82, v116
	v_fma_f32 v113, -v38, v83, v117
	v_fma_f32 v114, -v38, v84, v118
	v_fma_f32 v115, -v38, v85, v119
	v_fma_f32 v116, -v38, v86, v120
	v_fma_f32 v117, -v38, v87, v121
	v_fma_f32 v118, -v38, v88, v122
	v_fma_f32 v119, -v38, v89, v123
	v_fma_f32 v120, -v38, v90, v124
	v_fma_f32 v121, -v38, v91, v125
	v_fma_f32 v122, -v38, v92, v126
	v_fma_f32 v123, -v38, v93, v127
	v_fma_f32 v98, -v38, v94, v98
	v_fma_f32 v99, -v38, v95, v99
	v_fma_f32 v100, -v38, v96, v100
	v_fma_f32 v4, -v38, v97, v4
	ds_read_b128 v[70:73], v21 offset:10208
	ds_read_b128 v[74:77], v21 offset:10224
	ds_read_b128 v[78:81], v21 offset:10240
	ds_read_b128 v[82:85], v21 offset:10256
	ds_read_b128 v[86:89], v21 offset:10272
	ds_read_b128 v[90:93], v21 offset:10288
	ds_read_b128 v[94:97], v21 offset:10304
	s_waitcnt lgkmcnt(0)
	v_fma_f32 v42, -v5, v42, v5
	v_fma_f32 v43, -v5, v43, v101
	v_fma_f32 v44, -v5, v44, v102
	v_fma_f32 v45, -v5, v45, v103
	v_fma_f32 v102, -v5, v46, v104
	v_fma_f32 v103, -v5, v47, v105
	v_fma_f32 v104, -v5, v48, v106
	v_fma_f32 v105, -v5, v49, v107
	v_fma_f32 v106, -v5, v50, v108
	v_fma_f32 v107, -v5, v51, v109
	v_fma_f32 v108, -v5, v52, v110
	v_fma_f32 v109, -v5, v53, v111
	v_fma_f32 v110, -v5, v54, v112
	v_fma_f32 v111, -v5, v55, v113
	v_fma_f32 v112, -v5, v56, v114
	v_fma_f32 v113, -v5, v57, v115
	v_fma_f32 v114, -v5, v58, v116
	v_fma_f32 v115, -v5, v59, v117
	v_fma_f32 v116, -v5, v60, v118
	v_fma_f32 v117, -v5, v61, v119
	v_fma_f32 v118, -v5, v62, v120
	v_fma_f32 v119, -v5, v63, v121
	v_fma_f32 v120, -v5, v64, v122
	v_fma_f32 v121, -v5, v65, v123
	v_fma_f32 v122, -v5, v66, v98
	v_fma_f32 v123, -v5, v67, v99
	v_fma_f32 v124, -v5, v68, v100
	v_fma_f32 v4, -v5, v69, v4
	ds_read_b128 v[46:49], v21 offset:10480
	ds_read_b128 v[50:53], v21 offset:10496
	ds_read_b128 v[54:57], v21 offset:10512
	ds_read_b128 v[58:61], v21 offset:10528
	ds_read_b128 v[62:65], v21 offset:10544
	ds_read_b128 v[66:69], v21 offset:10560
	ds_read_b128 v[98:101], v21 offset:10576
	v_fma_f32 v5, -v43, v70, v42
	v_fma_f32 v42, -v43, v71, v43
	v_fma_f32 v125, -v43, v72, v44
	v_fma_f32 v126, -v43, v73, v45
	v_fma_f32 v102, -v43, v74, v102
	v_fma_f32 v103, -v43, v75, v103
	v_fma_f32 v104, -v43, v76, v104
	v_fma_f32 v105, -v43, v77, v105
	v_fma_f32 v106, -v43, v78, v106
	v_fma_f32 v107, -v43, v79, v107
	v_fma_f32 v108, -v43, v80, v108
	v_fma_f32 v109, -v43, v81, v109
	v_fma_f32 v110, -v43, v82, v110
	v_fma_f32 v111, -v43, v83, v111
	v_fma_f32 v112, -v43, v84, v112
	v_fma_f32 v113, -v43, v85, v113
	v_fma_f32 v114, -v43, v86, v114
	v_fma_f32 v115, -v43, v87, v115
	v_fma_f32 v116, -v43, v88, v116
	v_fma_f32 v117, -v43, v89, v117
	v_fma_f32 v118, -v43, v90, v118
	v_fma_f32 v119, -v43, v91, v119
	v_fma_f32 v120, -v43, v92, v120
	v_fma_f32 v121, -v43, v93, v121
	v_fma_f32 v94, -v43, v94, v122
	v_fma_f32 v95, -v43, v95, v123
	v_fma_f32 v96, -v43, v96, v124
	v_fma_f32 v4, -v43, v97, v4
	ds_read_b128 v[70:73], v21 offset:10768
	ds_read_b128 v[74:77], v21 offset:10784
	ds_read_b128 v[78:81], v21 offset:10800
	ds_read_b128 v[82:85], v21 offset:10816
	ds_read_b128 v[86:89], v21 offset:10832
	ds_read_b128 v[90:93], v21 offset:10848
	s_waitcnt lgkmcnt(0)
	v_fma_f32 v45, -v125, v46, v5
	v_fma_f32 v44, -v125, v47, v42
	v_fma_f32 v43, -v125, v48, v125
	v_fma_f32 v42, -v125, v49, v126
	v_fma_f32 v5, -v125, v50, v102
	v_fma_f32 v97, -v125, v51, v103
	v_fma_f32 v102, -v125, v52, v104
	v_fma_f32 v103, -v125, v53, v105
	v_fma_f32 v104, -v125, v54, v106
	v_fma_f32 v105, -v125, v55, v107
	v_fma_f32 v106, -v125, v56, v108
	v_fma_f32 v107, -v125, v57, v109
	v_fma_f32 v108, -v125, v58, v110
	v_fma_f32 v109, -v125, v59, v111
	v_fma_f32 v110, -v125, v60, v112
	v_fma_f32 v111, -v125, v61, v113
	v_fma_f32 v112, -v125, v62, v114
	v_fma_f32 v113, -v125, v63, v115
	v_fma_f32 v114, -v125, v64, v116
	v_fma_f32 v115, -v125, v65, v117
	v_fma_f32 v116, -v125, v66, v118
	v_fma_f32 v117, -v125, v67, v119
	v_fma_f32 v118, -v125, v68, v120
	v_fma_f32 v119, -v125, v69, v121
	v_fma_f32 v94, -v125, v98, v94
	v_fma_f32 v95, -v125, v99, v95
	v_fma_f32 v96, -v125, v100, v96
	v_fma_f32 v4, -v125, v101, v4
	ds_read_b128 v[46:49], v21 offset:11040
	ds_read_b128 v[50:53], v21 offset:11056
	ds_read_b128 v[54:57], v21 offset:11072
	ds_read_b128 v[58:61], v21 offset:11088
	ds_read_b128 v[62:65], v21 offset:11104
	ds_read_b128 v[66:69], v21 offset:11120
	v_fma_f32 v5, -v42, v70, v5
	v_fma_f32 v97, -v42, v71, v97
	v_fma_f32 v98, -v42, v72, v102
	v_fma_f32 v99, -v42, v73, v103
	v_fma_f32 v100, -v42, v74, v104
	v_fma_f32 v101, -v42, v75, v105
	v_fma_f32 v102, -v42, v76, v106
	v_fma_f32 v103, -v42, v77, v107
	v_fma_f32 v104, -v42, v78, v108
	v_fma_f32 v105, -v42, v79, v109
	v_fma_f32 v106, -v42, v80, v110
	v_fma_f32 v107, -v42, v81, v111
	v_fma_f32 v108, -v42, v82, v112
	v_fma_f32 v109, -v42, v83, v113
	v_fma_f32 v110, -v42, v84, v114
	v_fma_f32 v111, -v42, v85, v115
	v_fma_f32 v112, -v42, v86, v116
	v_fma_f32 v113, -v42, v87, v117
	v_fma_f32 v114, -v42, v88, v118
	v_fma_f32 v115, -v42, v89, v119
	v_fma_f32 v94, -v42, v90, v94
	v_fma_f32 v95, -v42, v91, v95
	v_fma_f32 v96, -v42, v92, v96
	v_fma_f32 v4, -v42, v93, v4
	ds_read_b128 v[70:73], v21 offset:11312
	ds_read_b128 v[74:77], v21 offset:11328
	ds_read_b128 v[78:81], v21 offset:11344
	ds_read_b128 v[82:85], v21 offset:11360
	ds_read_b128 v[86:89], v21 offset:11376
	ds_read_b128 v[90:93], v21 offset:11392
	s_waitcnt lgkmcnt(0)
	v_fma_f32 v46, -v5, v46, v5
	v_fma_f32 v47, -v5, v47, v97
	v_fma_f32 v48, -v5, v48, v98
	v_fma_f32 v49, -v5, v49, v99
	v_fma_f32 v98, -v5, v50, v100
	v_fma_f32 v99, -v5, v51, v101
	v_fma_f32 v100, -v5, v52, v102
	v_fma_f32 v101, -v5, v53, v103
	v_fma_f32 v102, -v5, v54, v104
	v_fma_f32 v103, -v5, v55, v105
	v_fma_f32 v104, -v5, v56, v106
	v_fma_f32 v105, -v5, v57, v107
	v_fma_f32 v106, -v5, v58, v108
	v_fma_f32 v107, -v5, v59, v109
	v_fma_f32 v108, -v5, v60, v110
	v_fma_f32 v109, -v5, v61, v111
	v_fma_f32 v110, -v5, v62, v112
	v_fma_f32 v111, -v5, v63, v113
	v_fma_f32 v112, -v5, v64, v114
	v_fma_f32 v113, -v5, v65, v115
	v_fma_f32 v114, -v5, v66, v94
	v_fma_f32 v115, -v5, v67, v95
	v_fma_f32 v116, -v5, v68, v96
	v_fma_f32 v4, -v5, v69, v4
	ds_read_b128 v[50:53], v21 offset:11584
	ds_read_b128 v[54:57], v21 offset:11600
	ds_read_b128 v[58:61], v21 offset:11616
	ds_read_b128 v[62:65], v21 offset:11632
	ds_read_b128 v[66:69], v21 offset:11648
	ds_read_b128 v[94:97], v21 offset:11664
	v_fma_f32 v5, -v47, v70, v46
	v_fma_f32 v46, -v47, v71, v47
	v_fma_f32 v117, -v47, v72, v48
	v_fma_f32 v118, -v47, v73, v49
	v_fma_f32 v98, -v47, v74, v98
	v_fma_f32 v99, -v47, v75, v99
	v_fma_f32 v100, -v47, v76, v100
	v_fma_f32 v101, -v47, v77, v101
	v_fma_f32 v102, -v47, v78, v102
	v_fma_f32 v103, -v47, v79, v103
	v_fma_f32 v104, -v47, v80, v104
	v_fma_f32 v105, -v47, v81, v105
	v_fma_f32 v106, -v47, v82, v106
	v_fma_f32 v107, -v47, v83, v107
	v_fma_f32 v108, -v47, v84, v108
	v_fma_f32 v109, -v47, v85, v109
	v_fma_f32 v110, -v47, v86, v110
	v_fma_f32 v111, -v47, v87, v111
	v_fma_f32 v112, -v47, v88, v112
	v_fma_f32 v113, -v47, v89, v113
	v_fma_f32 v90, -v47, v90, v114
	v_fma_f32 v91, -v47, v91, v115
	v_fma_f32 v92, -v47, v92, v116
	v_fma_f32 v4, -v47, v93, v4
	ds_read_b128 v[70:73], v21 offset:11872
	ds_read_b128 v[74:77], v21 offset:11888
	ds_read_b128 v[78:81], v21 offset:11904
	ds_read_b128 v[82:85], v21 offset:11920
	ds_read_b128 v[86:89], v21 offset:11936
	s_waitcnt lgkmcnt(0)
	v_fma_f32 v49, -v117, v50, v5
	v_fma_f32 v48, -v117, v51, v46
	v_fma_f32 v47, -v117, v52, v117
	v_fma_f32 v46, -v117, v53, v118
	v_fma_f32 v5, -v117, v54, v98
	v_fma_f32 v93, -v117, v55, v99
	v_fma_f32 v98, -v117, v56, v100
	v_fma_f32 v99, -v117, v57, v101
	v_fma_f32 v100, -v117, v58, v102
	v_fma_f32 v101, -v117, v59, v103
	v_fma_f32 v102, -v117, v60, v104
	v_fma_f32 v103, -v117, v61, v105
	v_fma_f32 v104, -v117, v62, v106
	v_fma_f32 v105, -v117, v63, v107
	v_fma_f32 v106, -v117, v64, v108
	v_fma_f32 v107, -v117, v65, v109
	v_fma_f32 v108, -v117, v66, v110
	v_fma_f32 v109, -v117, v67, v111
	v_fma_f32 v110, -v117, v68, v112
	v_fma_f32 v111, -v117, v69, v113
	v_fma_f32 v90, -v117, v94, v90
	v_fma_f32 v91, -v117, v95, v91
	v_fma_f32 v92, -v117, v96, v92
	v_fma_f32 v4, -v117, v97, v4
	ds_read_b128 v[50:53], v21 offset:12144
	ds_read_b128 v[54:57], v21 offset:12160
	ds_read_b128 v[58:61], v21 offset:12176
	ds_read_b128 v[62:65], v21 offset:12192
	ds_read_b128 v[66:69], v21 offset:12208
	v_fma_f32 v5, -v46, v70, v5
	v_fma_f32 v93, -v46, v71, v93
	v_fma_f32 v94, -v46, v72, v98
	v_fma_f32 v95, -v46, v73, v99
	v_fma_f32 v96, -v46, v74, v100
	v_fma_f32 v97, -v46, v75, v101
	v_fma_f32 v98, -v46, v76, v102
	v_fma_f32 v99, -v46, v77, v103
	v_fma_f32 v100, -v46, v78, v104
	v_fma_f32 v101, -v46, v79, v105
	v_fma_f32 v102, -v46, v80, v106
	v_fma_f32 v103, -v46, v81, v107
	v_fma_f32 v104, -v46, v82, v108
	v_fma_f32 v105, -v46, v83, v109
	v_fma_f32 v106, -v46, v84, v110
	v_fma_f32 v107, -v46, v85, v111
	v_fma_f32 v90, -v46, v86, v90
	v_fma_f32 v91, -v46, v87, v91
	v_fma_f32 v92, -v46, v88, v92
	v_fma_f32 v4, -v46, v89, v4
	ds_read_b128 v[70:73], v21 offset:12416
	ds_read_b128 v[74:77], v21 offset:12432
	ds_read_b128 v[78:81], v21 offset:12448
	ds_read_b128 v[82:85], v21 offset:12464
	ds_read_b128 v[86:89], v21 offset:12480
	s_waitcnt lgkmcnt(0)
	v_fma_f32 v50, -v5, v50, v5
	v_fma_f32 v51, -v5, v51, v93
	v_fma_f32 v52, -v5, v52, v94
	v_fma_f32 v53, -v5, v53, v95
	v_fma_f32 v94, -v5, v54, v96
	v_fma_f32 v95, -v5, v55, v97
	v_fma_f32 v96, -v5, v56, v98
	v_fma_f32 v97, -v5, v57, v99
	v_fma_f32 v98, -v5, v58, v100
	v_fma_f32 v99, -v5, v59, v101
	v_fma_f32 v100, -v5, v60, v102
	v_fma_f32 v101, -v5, v61, v103
	v_fma_f32 v102, -v5, v62, v104
	v_fma_f32 v103, -v5, v63, v105
	v_fma_f32 v104, -v5, v64, v106
	v_fma_f32 v105, -v5, v65, v107
	v_fma_f32 v106, -v5, v66, v90
	v_fma_f32 v107, -v5, v67, v91
	v_fma_f32 v108, -v5, v68, v92
	v_fma_f32 v4, -v5, v69, v4
	ds_read_b128 v[54:57], v21 offset:12688
	ds_read_b128 v[58:61], v21 offset:12704
	ds_read_b128 v[62:65], v21 offset:12720
	ds_read_b128 v[66:69], v21 offset:12736
	ds_read_b128 v[90:93], v21 offset:12752
	v_fma_f32 v5, -v51, v70, v50
	v_fma_f32 v50, -v51, v71, v51
	v_fma_f32 v109, -v51, v72, v52
	v_fma_f32 v110, -v51, v73, v53
	v_fma_f32 v94, -v51, v74, v94
	v_fma_f32 v95, -v51, v75, v95
	v_fma_f32 v96, -v51, v76, v96
	v_fma_f32 v97, -v51, v77, v97
	v_fma_f32 v98, -v51, v78, v98
	v_fma_f32 v99, -v51, v79, v99
	v_fma_f32 v100, -v51, v80, v100
	v_fma_f32 v101, -v51, v81, v101
	v_fma_f32 v102, -v51, v82, v102
	v_fma_f32 v103, -v51, v83, v103
	v_fma_f32 v104, -v51, v84, v104
	v_fma_f32 v105, -v51, v85, v105
	v_fma_f32 v86, -v51, v86, v106
	v_fma_f32 v87, -v51, v87, v107
	v_fma_f32 v88, -v51, v88, v108
	v_fma_f32 v4, -v51, v89, v4
	ds_read_b128 v[70:73], v21 offset:12976
	ds_read_b128 v[74:77], v21 offset:12992
	ds_read_b128 v[78:81], v21 offset:13008
	ds_read_b128 v[82:85], v21 offset:13024
	s_waitcnt lgkmcnt(0)
	v_fma_f32 v53, -v109, v54, v5
	v_fma_f32 v52, -v109, v55, v50
	v_fma_f32 v51, -v109, v56, v109
	v_fma_f32 v50, -v109, v57, v110
	v_fma_f32 v5, -v109, v58, v94
	v_fma_f32 v89, -v109, v59, v95
	v_fma_f32 v94, -v109, v60, v96
	v_fma_f32 v95, -v109, v61, v97
	v_fma_f32 v96, -v109, v62, v98
	v_fma_f32 v97, -v109, v63, v99
	v_fma_f32 v98, -v109, v64, v100
	v_fma_f32 v99, -v109, v65, v101
	v_fma_f32 v100, -v109, v66, v102
	v_fma_f32 v101, -v109, v67, v103
	v_fma_f32 v102, -v109, v68, v104
	v_fma_f32 v103, -v109, v69, v105
	v_fma_f32 v86, -v109, v90, v86
	v_fma_f32 v87, -v109, v91, v87
	v_fma_f32 v88, -v109, v92, v88
	v_fma_f32 v4, -v109, v93, v4
	ds_read_b128 v[54:57], v21 offset:13248
	ds_read_b128 v[58:61], v21 offset:13264
	ds_read_b128 v[62:65], v21 offset:13280
	ds_read_b128 v[66:69], v21 offset:13296
	v_fma_f32 v5, -v50, v70, v5
	v_fma_f32 v89, -v50, v71, v89
	v_fma_f32 v90, -v50, v72, v94
	v_fma_f32 v91, -v50, v73, v95
	v_fma_f32 v92, -v50, v74, v96
	v_fma_f32 v93, -v50, v75, v97
	v_fma_f32 v94, -v50, v76, v98
	v_fma_f32 v95, -v50, v77, v99
	v_fma_f32 v96, -v50, v78, v100
	v_fma_f32 v97, -v50, v79, v101
	v_fma_f32 v98, -v50, v80, v102
	v_fma_f32 v99, -v50, v81, v103
	v_fma_f32 v86, -v50, v82, v86
	v_fma_f32 v87, -v50, v83, v87
	v_fma_f32 v88, -v50, v84, v88
	v_fma_f32 v4, -v50, v85, v4
	ds_read_b128 v[70:73], v21 offset:13520
	ds_read_b128 v[74:77], v21 offset:13536
	ds_read_b128 v[78:81], v21 offset:13552
	ds_read_b128 v[82:85], v21 offset:13568
	s_waitcnt lgkmcnt(0)
	v_fma_f32 v54, -v5, v54, v5
	v_fma_f32 v55, -v5, v55, v89
	v_fma_f32 v56, -v5, v56, v90
	v_fma_f32 v57, -v5, v57, v91
	v_fma_f32 v90, -v5, v58, v92
	v_fma_f32 v91, -v5, v59, v93
	v_fma_f32 v92, -v5, v60, v94
	v_fma_f32 v93, -v5, v61, v95
	v_fma_f32 v94, -v5, v62, v96
	v_fma_f32 v95, -v5, v63, v97
	v_fma_f32 v96, -v5, v64, v98
	v_fma_f32 v97, -v5, v65, v99
	v_fma_f32 v98, -v5, v66, v86
	v_fma_f32 v99, -v5, v67, v87
	v_fma_f32 v100, -v5, v68, v88
	v_fma_f32 v4, -v5, v69, v4
	ds_read_b128 v[58:61], v21 offset:13792
	ds_read_b128 v[62:65], v21 offset:13808
	ds_read_b128 v[66:69], v21 offset:13824
	ds_read_b128 v[86:89], v21 offset:13840
	v_fma_f32 v5, -v55, v70, v54
	v_fma_f32 v54, -v55, v71, v55
	v_fma_f32 v101, -v55, v72, v56
	v_fma_f32 v102, -v55, v73, v57
	v_fma_f32 v90, -v55, v74, v90
	v_fma_f32 v91, -v55, v75, v91
	v_fma_f32 v92, -v55, v76, v92
	v_fma_f32 v93, -v55, v77, v93
	v_fma_f32 v94, -v55, v78, v94
	v_fma_f32 v95, -v55, v79, v95
	v_fma_f32 v96, -v55, v80, v96
	v_fma_f32 v97, -v55, v81, v97
	v_fma_f32 v82, -v55, v82, v98
	v_fma_f32 v83, -v55, v83, v99
	v_fma_f32 v84, -v55, v84, v100
	v_fma_f32 v4, -v55, v85, v4
	ds_read_b128 v[70:73], v21 offset:14080
	ds_read_b128 v[74:77], v21 offset:14096
	ds_read_b128 v[78:81], v21 offset:14112
	s_waitcnt lgkmcnt(0)
	v_fma_f32 v57, -v101, v58, v5
	v_fma_f32 v56, -v101, v59, v54
	v_fma_f32 v55, -v101, v60, v101
	v_fma_f32 v54, -v101, v61, v102
	v_fma_f32 v5, -v101, v62, v90
	v_fma_f32 v85, -v101, v63, v91
	v_fma_f32 v90, -v101, v64, v92
	v_fma_f32 v91, -v101, v65, v93
	v_fma_f32 v92, -v101, v66, v94
	v_fma_f32 v93, -v101, v67, v95
	v_fma_f32 v94, -v101, v68, v96
	v_fma_f32 v95, -v101, v69, v97
	v_fma_f32 v82, -v101, v86, v82
	v_fma_f32 v83, -v101, v87, v83
	v_fma_f32 v84, -v101, v88, v84
	v_fma_f32 v4, -v101, v89, v4
	ds_read_b128 v[58:61], v21 offset:14352
	ds_read_b128 v[62:65], v21 offset:14368
	ds_read_b128 v[66:69], v21 offset:14384
	v_fma_f32 v5, -v54, v70, v5
	v_fma_f32 v85, -v54, v71, v85
	v_fma_f32 v86, -v54, v72, v90
	v_fma_f32 v87, -v54, v73, v91
	v_fma_f32 v88, -v54, v74, v92
	v_fma_f32 v89, -v54, v75, v93
	v_fma_f32 v90, -v54, v76, v94
	v_fma_f32 v91, -v54, v77, v95
	v_fma_f32 v82, -v54, v78, v82
	v_fma_f32 v83, -v54, v79, v83
	v_fma_f32 v84, -v54, v80, v84
	v_fma_f32 v4, -v54, v81, v4
	ds_read_b128 v[70:73], v21 offset:14624
	ds_read_b128 v[74:77], v21 offset:14640
	ds_read_b128 v[78:81], v21 offset:14656
	s_waitcnt lgkmcnt(0)
	v_fma_f32 v58, -v5, v58, v5
	v_fma_f32 v59, -v5, v59, v85
	v_fma_f32 v60, -v5, v60, v86
	v_fma_f32 v61, -v5, v61, v87
	v_fma_f32 v86, -v5, v62, v88
	v_fma_f32 v87, -v5, v63, v89
	v_fma_f32 v88, -v5, v64, v90
	v_fma_f32 v89, -v5, v65, v91
	v_fma_f32 v90, -v5, v66, v82
	v_fma_f32 v91, -v5, v67, v83
	v_fma_f32 v92, -v5, v68, v84
	v_fma_f32 v4, -v5, v69, v4
	ds_read_b128 v[62:65], v21 offset:14896
	ds_read_b128 v[66:69], v21 offset:14912
	ds_read_b128 v[82:85], v21 offset:14928
	v_fma_f32 v5, -v59, v70, v58
	v_fma_f32 v58, -v59, v71, v59
	v_fma_f32 v93, -v59, v72, v60
	v_fma_f32 v94, -v59, v73, v61
	v_fma_f32 v86, -v59, v74, v86
	v_fma_f32 v87, -v59, v75, v87
	v_fma_f32 v88, -v59, v76, v88
	v_fma_f32 v89, -v59, v77, v89
	v_fma_f32 v78, -v59, v78, v90
	v_fma_f32 v79, -v59, v79, v91
	v_fma_f32 v80, -v59, v80, v92
	v_fma_f32 v4, -v59, v81, v4
	ds_read_b128 v[70:73], v21 offset:15184
	ds_read_b128 v[74:77], v21 offset:15200
	s_waitcnt lgkmcnt(0)
	v_fma_f32 v61, -v93, v62, v5
	v_fma_f32 v60, -v93, v63, v58
	v_fma_f32 v59, -v93, v64, v93
	v_fma_f32 v58, -v93, v65, v94
	v_fma_f32 v5, -v93, v66, v86
	v_fma_f32 v81, -v93, v67, v87
	v_fma_f32 v86, -v93, v68, v88
	v_fma_f32 v87, -v93, v69, v89
	v_fma_f32 v78, -v93, v82, v78
	v_fma_f32 v79, -v93, v83, v79
	v_fma_f32 v80, -v93, v84, v80
	v_fma_f32 v4, -v93, v85, v4
	ds_read_b128 v[62:65], v21 offset:15456
	ds_read_b128 v[66:69], v21 offset:15472
	v_fma_f32 v5, -v58, v70, v5
	v_fma_f32 v81, -v58, v71, v81
	v_fma_f32 v82, -v58, v72, v86
	v_fma_f32 v83, -v58, v73, v87
	v_fma_f32 v78, -v58, v74, v78
	v_fma_f32 v79, -v58, v75, v79
	v_fma_f32 v80, -v58, v76, v80
	v_fma_f32 v4, -v58, v77, v4
	ds_read_b128 v[70:73], v21 offset:15728
	ds_read_b128 v[74:77], v21 offset:15744
	s_waitcnt lgkmcnt(0)
	v_fma_f32 v66, -v5, v66, v78
	v_fma_f32 v67, -v5, v67, v79
	v_fma_f32 v68, -v5, v68, v80
	v_fma_f32 v84, -v5, v62, v5
	v_fma_f32 v85, -v5, v63, v81
	v_fma_f32 v82, -v5, v64, v82
	v_fma_f32 v83, -v5, v65, v83
	v_fma_f32 v4, -v5, v69, v4
	ds_read_b128 v[62:65], v21 offset:16000
	ds_read_b128 v[78:81], v21 offset:16016
	v_fma_f32 v5, -v85, v70, v84
	v_fma_f32 v84, -v85, v71, v85
	v_fma_f32 v72, -v85, v72, v82
	v_fma_f32 v73, -v85, v73, v83
	v_fma_f32 v74, -v85, v74, v66
	v_fma_f32 v75, -v85, v75, v67
	v_fma_f32 v76, -v85, v76, v68
	v_fma_f32 v4, -v85, v77, v4
	ds_read_b128 v[68:71], v21 offset:16288
	s_waitcnt lgkmcnt(0)
	v_fma_f32 v67, -v72, v62, v5
	v_fma_f32 v66, -v72, v63, v84
	v_fma_f32 v63, -v72, v64, v72
	v_fma_f32 v62, -v72, v65, v73
	v_fma_f32 v64, -v72, v79, v75
	v_fma_f32 v65, -v72, v80, v76
	v_fma_f32 v5, -v72, v78, v74
	v_fma_f32 v4, -v72, v81, v4
	ds_read_b128 v[72:75], v21 offset:16560
	v_fma_f32 v64, -v62, v69, v64
	v_fma_f32 v65, -v62, v70, v65
	v_fma_f32 v5, -v62, v68, v5
	v_fma_f32 v4, -v62, v71, v4
	ds_read_b128 v[68:71], v21 offset:16832
	s_waitcnt lgkmcnt(0)
	v_fma_f32 v64, -v5, v73, v64
	v_fma_f32 v65, -v5, v74, v65
	v_fma_f32 v76, -v5, v72, v5
	v_fma_f32 v4, -v5, v75, v4
	ds_read_b128 v[72:75], v21 offset:17104
	v_fma_f32 v5, -v64, v68, v76
	v_fma_f32 v21, -v64, v69, v64
	v_fma_f32 v70, -v64, v70, v65
	v_fma_f32 v4, -v64, v71, v4
	s_waitcnt lgkmcnt(0)
	v_fma_f32 v69, -v70, v72, v5
	v_fma_f32 v68, -v70, v73, v21
	v_fma_f32 v65, -v70, v74, v70
	v_fma_f32 v64, -v70, v75, v4
	s_and_saveexec_b64 s[4:5], vcc
	s_xor_b64 s[4:5], exec, s[4:5]
	s_cbranch_execz .LBB0_375
	s_ashr_i32 s15, s14, 31
	s_lshl_b64 s[16:17], s[14:15], 10
	s_add_u32 s15, s12, s16
	s_addc_u32 s17, s13, s17
	s_lshl_b32 s16, s35, 1
	s_add_u32 s16, s15, s16
	s_addc_u32 s17, s17, 0
	v_mov_b32_e32 v21, v3
	v_lshl_add_u64 v[4:5], v[20:21], 1, s[16:17]
	s_mov_b32 s15, 0x439ff000
	v_add_co_u32_e32 v20, vcc, s15, v4
	v_cvt_pk_bf16_f32 v7, v7, s0
	s_nop 0
	v_addc_co_u32_e32 v21, vcc, 0, v5, vcc
	s_mov_b32 s15, 0x43a00000
	global_store_short v[20:21], v7, off offset:3840
	v_cvt_pk_bf16_f32 v20, v6, s0
	v_add_co_u32_e32 v6, vcc, s15, v4
	v_cvt_pk_bf16_f32 v1, v1, s0
	s_nop 0
	v_addc_co_u32_e32 v7, vcc, 0, v5, vcc
	v_cvt_pk_bf16_f32 v2, v2, s0
	global_store_short v[6:7], v1, off offset:2816
	v_cvt_pk_bf16_f32 v1, v11, s0
	s_mov_b32 s15, 0x43a01000
	global_store_short v[6:7], v20, off offset:768
	global_store_short v[6:7], v2, off offset:1792
	global_store_short v[6:7], v1, off offset:3840
	v_add_co_u32_e32 v6, vcc, s15, v4
	v_cvt_pk_bf16_f32 v1, v10, s0
	s_nop 0
	v_addc_co_u32_e32 v7, vcc, 0, v5, vcc
	global_store_short v[6:7], v1, off offset:768
	v_cvt_pk_bf16_f32 v1, v9, s0
	global_store_short v[6:7], v1, off offset:1792
	v_cvt_pk_bf16_f32 v1, v8, s0
	global_store_short v[6:7], v1, off offset:2816
	v_cvt_pk_bf16_f32 v1, v15, s0
	s_mov_b32 s15, 0x43a02000
	global_store_short v[6:7], v1, off offset:3840
	v_add_co_u32_e32 v6, vcc, s15, v4
	v_cvt_pk_bf16_f32 v1, v14, s0
	s_nop 0
	v_addc_co_u32_e32 v7, vcc, 0, v5, vcc
	global_store_short v[6:7], v1, off offset:768
	v_cvt_pk_bf16_f32 v1, v13, s0
	global_store_short v[6:7], v1, off offset:1792
	v_cvt_pk_bf16_f32 v1, v12, s0
	global_store_short v[6:7], v1, off offset:2816
	v_cvt_pk_bf16_f32 v1, v19, s0
	s_mov_b32 s15, 0x43a03000
	global_store_short v[6:7], v1, off offset:3840
	v_add_co_u32_e32 v6, vcc, s15, v4
	v_cvt_pk_bf16_f32 v1, v18, s0
	s_nop 0
	v_addc_co_u32_e32 v7, vcc, 0, v5, vcc
	global_store_short v[6:7], v1, off offset:768
	v_cvt_pk_bf16_f32 v1, v17, s0
	global_store_short v[6:7], v1, off offset:1792
	v_cvt_pk_bf16_f32 v1, v16, s0
	global_store_short v[6:7], v1, off offset:2816
	v_cvt_pk_bf16_f32 v1, v25, s0
	s_mov_b32 s15, 0x43a04000
	global_store_short v[6:7], v1, off offset:3840
	v_add_co_u32_e32 v6, vcc, s15, v4
	v_cvt_pk_bf16_f32 v1, v24, s0
	s_nop 0
	v_addc_co_u32_e32 v7, vcc, 0, v5, vcc
	global_store_short v[6:7], v1, off offset:768
	v_cvt_pk_bf16_f32 v1, v23, s0
	global_store_short v[6:7], v1, off offset:1792
	v_cvt_pk_bf16_f32 v1, v22, s0
	global_store_short v[6:7], v1, off offset:2816
	v_cvt_pk_bf16_f32 v1, v29, s0
	s_mov_b32 s15, 0x43a05000
	global_store_short v[6:7], v1, off offset:3840
	v_add_co_u32_e32 v6, vcc, s15, v4
	v_cvt_pk_bf16_f32 v1, v28, s0
	s_nop 0
	v_addc_co_u32_e32 v7, vcc, 0, v5, vcc
	global_store_short v[6:7], v1, off offset:768
	v_cvt_pk_bf16_f32 v1, v27, s0
	global_store_short v[6:7], v1, off offset:1792
	v_cvt_pk_bf16_f32 v1, v26, s0
	global_store_short v[6:7], v1, off offset:2816
	v_cvt_pk_bf16_f32 v1, v33, s0
	s_mov_b32 s15, 0x43a06000
	global_store_short v[6:7], v1, off offset:3840
	v_add_co_u32_e32 v6, vcc, s15, v4
	v_cvt_pk_bf16_f32 v1, v32, s0
	s_nop 0
	v_addc_co_u32_e32 v7, vcc, 0, v5, vcc
	global_store_short v[6:7], v1, off offset:768
	v_cvt_pk_bf16_f32 v1, v31, s0
	global_store_short v[6:7], v1, off offset:1792
	v_cvt_pk_bf16_f32 v1, v30, s0
	global_store_short v[6:7], v1, off offset:2816
	v_cvt_pk_bf16_f32 v1, v37, s0
	s_mov_b32 s15, 0x43a07000
	global_store_short v[6:7], v1, off offset:3840
	v_add_co_u32_e32 v6, vcc, s15, v4
	v_cvt_pk_bf16_f32 v1, v36, s0
	s_nop 0
	v_addc_co_u32_e32 v7, vcc, 0, v5, vcc
	global_store_short v[6:7], v1, off offset:768
	v_cvt_pk_bf16_f32 v1, v35, s0
	global_store_short v[6:7], v1, off offset:1792
	v_cvt_pk_bf16_f32 v1, v34, s0
	global_store_short v[6:7], v1, off offset:2816
	v_cvt_pk_bf16_f32 v1, v41, s0
	s_mov_b32 s15, 0x43a08000
	global_store_short v[6:7], v1, off offset:3840
	v_add_co_u32_e32 v6, vcc, s15, v4
	v_cvt_pk_bf16_f32 v1, v40, s0
	s_nop 0
	v_addc_co_u32_e32 v7, vcc, 0, v5, vcc
	global_store_short v[6:7], v1, off offset:768
	v_cvt_pk_bf16_f32 v1, v39, s0
	global_store_short v[6:7], v1, off offset:1792
	v_cvt_pk_bf16_f32 v1, v38, s0
	global_store_short v[6:7], v1, off offset:2816
	v_cvt_pk_bf16_f32 v1, v45, s0
	s_mov_b32 s15, 0x43a09000
	global_store_short v[6:7], v1, off offset:3840
	v_add_co_u32_e32 v6, vcc, s15, v4
	v_cvt_pk_bf16_f32 v1, v44, s0
	s_nop 0
	v_addc_co_u32_e32 v7, vcc, 0, v5, vcc
	global_store_short v[6:7], v1, off offset:768
	v_cvt_pk_bf16_f32 v1, v43, s0
	global_store_short v[6:7], v1, off offset:1792
	v_cvt_pk_bf16_f32 v1, v42, s0
	global_store_short v[6:7], v1, off offset:2816
	v_cvt_pk_bf16_f32 v1, v49, s0
	s_mov_b32 s15, 0x43a0a000
	global_store_short v[6:7], v1, off offset:3840
	v_add_co_u32_e32 v6, vcc, s15, v4
	v_cvt_pk_bf16_f32 v1, v48, s0
	s_nop 0
	v_addc_co_u32_e32 v7, vcc, 0, v5, vcc
	global_store_short v[6:7], v1, off offset:768
	v_cvt_pk_bf16_f32 v1, v47, s0
	global_store_short v[6:7], v1, off offset:1792
	v_cvt_pk_bf16_f32 v1, v46, s0
	global_store_short v[6:7], v1, off offset:2816
	v_cvt_pk_bf16_f32 v1, v53, s0
	s_mov_b32 s15, 0x43a0b000
	global_store_short v[6:7], v1, off offset:3840
	v_add_co_u32_e32 v6, vcc, s15, v4
	v_cvt_pk_bf16_f32 v1, v52, s0
	s_nop 0
	v_addc_co_u32_e32 v7, vcc, 0, v5, vcc
	global_store_short v[6:7], v1, off offset:768
	v_cvt_pk_bf16_f32 v1, v51, s0
	global_store_short v[6:7], v1, off offset:1792
	v_cvt_pk_bf16_f32 v1, v50, s0
	global_store_short v[6:7], v1, off offset:2816
	v_cvt_pk_bf16_f32 v1, v57, s0
	s_mov_b32 s15, 0x43a0c000
	global_store_short v[6:7], v1, off offset:3840
	v_add_co_u32_e32 v6, vcc, s15, v4
	v_cvt_pk_bf16_f32 v1, v56, s0
	s_nop 0
	v_addc_co_u32_e32 v7, vcc, 0, v5, vcc
	global_store_short v[6:7], v1, off offset:768
	v_cvt_pk_bf16_f32 v1, v55, s0
	global_store_short v[6:7], v1, off offset:1792
	v_cvt_pk_bf16_f32 v1, v54, s0
	global_store_short v[6:7], v1, off offset:2816
	v_cvt_pk_bf16_f32 v1, v61, s0
	s_mov_b32 s15, 0x43a0d000
	global_store_short v[6:7], v1, off offset:3840
	v_add_co_u32_e32 v6, vcc, s15, v4
	v_cvt_pk_bf16_f32 v1, v60, s0
	s_nop 0
	v_addc_co_u32_e32 v7, vcc, 0, v5, vcc
	global_store_short v[6:7], v1, off offset:768
	v_cvt_pk_bf16_f32 v1, v59, s0
	global_store_short v[6:7], v1, off offset:1792
	v_cvt_pk_bf16_f32 v1, v58, s0
	global_store_short v[6:7], v1, off offset:2816
	v_cvt_pk_bf16_f32 v1, v67, s0
	s_mov_b32 s15, 0x43a0e000
	global_store_short v[6:7], v1, off offset:3840
	v_add_co_u32_e32 v6, vcc, s15, v4
	v_cvt_pk_bf16_f32 v1, v66, s0
	s_nop 0
	v_addc_co_u32_e32 v7, vcc, 0, v5, vcc
	global_store_short v[6:7], v1, off offset:768
	v_cvt_pk_bf16_f32 v1, v63, s0
	global_store_short v[6:7], v1, off offset:1792
	v_cvt_pk_bf16_f32 v1, v62, s0
	global_store_short v[6:7], v1, off offset:2816
	v_cvt_pk_bf16_f32 v1, v69, s0
	v_add_co_u32_e32 v4, vcc, 0x43a0f000, v4
	global_store_short v[6:7], v1, off offset:3840
	v_cvt_pk_bf16_f32 v1, v68, s0
	v_addc_co_u32_e32 v5, vcc, 0, v5, vcc
	global_store_short v[4:5], v1, off offset:768
	v_cvt_pk_bf16_f32 v1, v65, s0
	global_store_short v[4:5], v1, off offset:1792
	v_cvt_pk_bf16_f32 v1, v64, s0
	global_store_short v[4:5], v1, off offset:2816
.LBB0_375:
	s_andn2_saveexec_b64 s[4:5], s[4:5]
	s_cbranch_execz .LBB0_254
	s_ashr_i32 s15, s14, 31
	s_lshl_b64 s[14:15], s[14:15], 11
	s_add_u32 s12, s12, s14
	s_addc_u32 s13, s13, s15
	s_lshl_b32 s14, s35, 2
	s_add_u32 s12, s12, s14
	s_addc_u32 s13, s13, 0
	v_ashrrev_i32_e32 v21, 31, v20
	v_lshl_add_u64 v[4:5], v[20:21], 2, s[12:13]
	s_mov_b64 s[12:13], 0x41a00000
	v_lshl_add_u64 v[20:21], v[4:5], 0, s[12:13]
	s_mov_b32 s12, 0x41a00000
	v_add_co_u32_e32 v70, vcc, s12, v4
	s_mov_b32 s12, 0x41a01000
	s_nop 0
	v_addc_co_u32_e32 v71, vcc, 0, v5, vcc
	global_store_dword v[70:71], v7, off
	global_store_dword v[20:21], v6, off offset:2048
	v_add_co_u32_e32 v6, vcc, s12, v4
	s_mov_b32 s12, 0x41a02000
	s_nop 0
	v_addc_co_u32_e32 v7, vcc, 0, v5, vcc
	global_store_dword v[6:7], v2, off
	global_store_dword v[6:7], v1, off offset:2048
	v_add_co_u32_e32 v6, vcc, s12, v4
	s_mov_b32 s12, 0x41a03000
	s_nop 0
	v_addc_co_u32_e32 v7, vcc, 0, v5, vcc
	global_store_dword v[6:7], v11, off
	global_store_dword v[6:7], v10, off offset:2048
	v_add_co_u32_e32 v6, vcc, s12, v4
	s_mov_b32 s12, 0x41a04000
	s_nop 0
	v_addc_co_u32_e32 v7, vcc, 0, v5, vcc
	global_store_dword v[6:7], v9, off
	global_store_dword v[6:7], v8, off offset:2048
	v_add_co_u32_e32 v6, vcc, s12, v4
	s_mov_b32 s12, 0x41a05000
	s_nop 0
	v_addc_co_u32_e32 v7, vcc, 0, v5, vcc
	global_store_dword v[6:7], v15, off
	global_store_dword v[6:7], v14, off offset:2048
	v_add_co_u32_e32 v6, vcc, s12, v4
	s_mov_b32 s12, 0x41a06000
	s_nop 0
	v_addc_co_u32_e32 v7, vcc, 0, v5, vcc
	global_store_dword v[6:7], v13, off
	global_store_dword v[6:7], v12, off offset:2048
	v_add_co_u32_e32 v6, vcc, s12, v4
	s_mov_b32 s12, 0x41a07000
	s_nop 0
	v_addc_co_u32_e32 v7, vcc, 0, v5, vcc
	global_store_dword v[6:7], v19, off
	global_store_dword v[6:7], v18, off offset:2048
	v_add_co_u32_e32 v6, vcc, s12, v4
	s_mov_b32 s12, 0x41a08000
	s_nop 0
	v_addc_co_u32_e32 v7, vcc, 0, v5, vcc
	global_store_dword v[6:7], v17, off
	global_store_dword v[6:7], v16, off offset:2048
	v_add_co_u32_e32 v6, vcc, s12, v4
	s_mov_b32 s12, 0x41a09000
	s_nop 0
	v_addc_co_u32_e32 v7, vcc, 0, v5, vcc
	global_store_dword v[6:7], v25, off
	global_store_dword v[6:7], v24, off offset:2048
	v_add_co_u32_e32 v6, vcc, s12, v4
	s_mov_b32 s12, 0x41a0a000
	s_nop 0
	v_addc_co_u32_e32 v7, vcc, 0, v5, vcc
	global_store_dword v[6:7], v23, off
	global_store_dword v[6:7], v22, off offset:2048
	v_add_co_u32_e32 v6, vcc, s12, v4
	s_mov_b32 s12, 0x41a0b000
	s_nop 0
	v_addc_co_u32_e32 v7, vcc, 0, v5, vcc
	global_store_dword v[6:7], v29, off
	global_store_dword v[6:7], v28, off offset:2048
	v_add_co_u32_e32 v6, vcc, s12, v4
	s_mov_b32 s12, 0x41a0c000
	s_nop 0
	v_addc_co_u32_e32 v7, vcc, 0, v5, vcc
	global_store_dword v[6:7], v27, off
	global_store_dword v[6:7], v26, off offset:2048
	v_add_co_u32_e32 v6, vcc, s12, v4
	s_mov_b32 s12, 0x41a0d000
	s_nop 0
	v_addc_co_u32_e32 v7, vcc, 0, v5, vcc
	global_store_dword v[6:7], v33, off
	global_store_dword v[6:7], v32, off offset:2048
	v_add_co_u32_e32 v6, vcc, s12, v4
	s_mov_b32 s12, 0x41a0e000
	s_nop 0
	v_addc_co_u32_e32 v7, vcc, 0, v5, vcc
	global_store_dword v[6:7], v31, off
	global_store_dword v[6:7], v30, off offset:2048
	v_add_co_u32_e32 v6, vcc, s12, v4
	s_mov_b32 s12, 0x41a0f000
	s_nop 0
	v_addc_co_u32_e32 v7, vcc, 0, v5, vcc
	global_store_dword v[6:7], v37, off
	global_store_dword v[6:7], v36, off offset:2048
	v_add_co_u32_e32 v6, vcc, s12, v4
	s_mov_b32 s12, 0x41a10000
	s_nop 0
	v_addc_co_u32_e32 v7, vcc, 0, v5, vcc
	global_store_dword v[6:7], v35, off
	global_store_dword v[6:7], v34, off offset:2048
	v_add_co_u32_e32 v6, vcc, s12, v4
	s_mov_b32 s12, 0x41a11000
	s_nop 0
	v_addc_co_u32_e32 v7, vcc, 0, v5, vcc
	global_store_dword v[6:7], v41, off
	global_store_dword v[6:7], v40, off offset:2048
	v_add_co_u32_e32 v6, vcc, s12, v4
	s_mov_b32 s12, 0x41a12000
	s_nop 0
	v_addc_co_u32_e32 v7, vcc, 0, v5, vcc
	global_store_dword v[6:7], v39, off
	global_store_dword v[6:7], v38, off offset:2048
	v_add_co_u32_e32 v6, vcc, s12, v4
	s_mov_b32 s12, 0x41a13000
	s_nop 0
	v_addc_co_u32_e32 v7, vcc, 0, v5, vcc
	global_store_dword v[6:7], v45, off
	global_store_dword v[6:7], v44, off offset:2048
	v_add_co_u32_e32 v6, vcc, s12, v4
	s_mov_b32 s12, 0x41a14000
	s_nop 0
	v_addc_co_u32_e32 v7, vcc, 0, v5, vcc
	global_store_dword v[6:7], v43, off
	global_store_dword v[6:7], v42, off offset:2048
	v_add_co_u32_e32 v6, vcc, s12, v4
	s_mov_b32 s12, 0x41a15000
	s_nop 0
	v_addc_co_u32_e32 v7, vcc, 0, v5, vcc
	global_store_dword v[6:7], v49, off
	global_store_dword v[6:7], v48, off offset:2048
	v_add_co_u32_e32 v6, vcc, s12, v4
	s_mov_b32 s12, 0x41a16000
	s_nop 0
	v_addc_co_u32_e32 v7, vcc, 0, v5, vcc
	global_store_dword v[6:7], v47, off
	global_store_dword v[6:7], v46, off offset:2048
	v_add_co_u32_e32 v6, vcc, s12, v4
	s_mov_b32 s12, 0x41a17000
	s_nop 0
	v_addc_co_u32_e32 v7, vcc, 0, v5, vcc
	global_store_dword v[6:7], v53, off
	global_store_dword v[6:7], v52, off offset:2048
	v_add_co_u32_e32 v6, vcc, s12, v4
	s_mov_b32 s12, 0x41a18000
	s_nop 0
	v_addc_co_u32_e32 v7, vcc, 0, v5, vcc
	global_store_dword v[6:7], v51, off
	global_store_dword v[6:7], v50, off offset:2048
	v_add_co_u32_e32 v6, vcc, s12, v4
	s_mov_b32 s12, 0x41a19000
	s_nop 0
	v_addc_co_u32_e32 v7, vcc, 0, v5, vcc
	global_store_dword v[6:7], v57, off
	global_store_dword v[6:7], v56, off offset:2048
	v_add_co_u32_e32 v6, vcc, s12, v4
	s_mov_b32 s12, 0x41a1a000
	s_nop 0
	v_addc_co_u32_e32 v7, vcc, 0, v5, vcc
	global_store_dword v[6:7], v55, off
	global_store_dword v[6:7], v54, off offset:2048
	v_add_co_u32_e32 v6, vcc, s12, v4
	s_mov_b32 s12, 0x41a1b000
	s_nop 0
	v_addc_co_u32_e32 v7, vcc, 0, v5, vcc
	global_store_dword v[6:7], v61, off
	global_store_dword v[6:7], v60, off offset:2048
	v_add_co_u32_e32 v6, vcc, s12, v4
	s_mov_b32 s12, 0x41a1c000
	s_nop 0
	v_addc_co_u32_e32 v7, vcc, 0, v5, vcc
	global_store_dword v[6:7], v59, off
	global_store_dword v[6:7], v58, off offset:2048
	v_add_co_u32_e32 v6, vcc, s12, v4
	s_nop 1
	v_addc_co_u32_e32 v7, vcc, 0, v5, vcc
	global_store_dword v[6:7], v67, off
	global_store_dword v[6:7], v66, off offset:2048
	v_add_co_u32_e32 v6, vcc, 0x41a1d000, v4
	s_nop 1
	v_addc_co_u32_e32 v7, vcc, 0, v5, vcc
	global_store_dword v[6:7], v63, off
	global_store_dword v[6:7], v62, off offset:2048
	v_add_co_u32_e32 v6, vcc, 0x41a1e000, v4
	s_nop 1
	v_addc_co_u32_e32 v7, vcc, 0, v5, vcc
	v_add_co_u32_e32 v4, vcc, 0x41a1f000, v4
	global_store_dword v[6:7], v69, off
	global_store_dword v[6:7], v68, off offset:2048
	v_addc_co_u32_e32 v5, vcc, 0, v5, vcc
	global_store_dword v[4:5], v65, off
	global_store_dword v[4:5], v64, off offset:2048
	s_branch .LBB0_254

.LBB0_379:
	s_waitcnt lgkmcnt(0)
	s_barrier
	s_and_saveexec_b64 s[8:9], s[0:1]
	s_cbranch_execz .LBB0_381
	v_mov_b64_e32 v[4:5], s[4:5]
	s_waitcnt vmcnt(0)
	global_atomic_add v1, v[4:5], v228, off sc0
	v_mov_b32_e32 v2, s2
	s_waitcnt vmcnt(0) lgkmcnt(0)
	ds_write_b32 v2, v1
.LBB0_381:
	s_or_b64 exec, exec, s[8:9]
	v_mov_b32_e32 v1, s2
	s_waitcnt lgkmcnt(0)
	s_barrier
	ds_read_b32 v1, v1
	s_movk_i32 s3, 0x1ff
	s_mov_b64 s[10:11], -1
	s_waitcnt lgkmcnt(0)
	v_cmp_lt_i32_e32 vcc, s3, v1
	v_readfirstlane_b32 s8, v1
	s_cbranch_vccnz .LBB0_378
	v_mov_b32_e32 v1, v0
	s_mov_b32 s3, s88
	v_readlane_b32 s9, v252, 0
	s_lshl_b32 s3, s8, 5
	s_and_b32 s9, s3, 0xfffff000
	s_lshl_b32 s3, s8, 7
	s_bfe_u32 s16, s8, 0x20005
	s_and_b32 s3, s3, 0xf80
	s_mov_b64 s[10:11], s[68:69]
	s_or_b32 s9, s9, s3
	v_cvt_f32_ubyte0_e32 v2, s16
	s_add_u32 s14, s10, 0x9000000
	v_sub_f32_e32 v34, 0xc0a00000, v2
	s_mov_b32 s6, 0xc2fc0000
	s_addc_u32 s15, s11, 0
	v_cmp_gt_f32_e32 vcc, s6, v34
	v_ashrrev_i32_e32 v11, 4, v1
	v_readlane_b32 s28, v253, 17
	s_and_b64 s[12:13], vcc, exec
	v_lshlrev_b32_e32 v12, 3, v1
	v_add_u32_e32 v2, s9, v11
	v_mov_b64_e32 v[4:5], s[14:15]
	v_readlane_b32 s29, v253, 18
	s_cselect_b32 s12, 0xffffffc0, 0
	v_and_b32_e32 v10, 0x78, v12
	v_mad_i64_i32 v[6:7], s[14:15], v2, s24, v[4:5]
	s_mov_b32 s17, s29
	s_lshl_b32 s16, s16, 8
	v_lshl_add_u64 v[6:7], v[6:7], 0, s[16:17]
	v_lshlrev_b32_e32 v2, 1, v10
	v_lshl_add_u64 v[6:7], v[6:7], 0, v[2:3]
	s_barrier
	global_load_dwordx4 v[6:9], v[6:7], off offset:2048
	v_add_u32_e32 v37, 0x200, v1
	v_mov_b32_e32 v36, s72
	v_ashrrev_i32_e32 v13, 4, v37
	v_mad_u32_u24 v14, v10, s20, v36
	v_add_u32_e32 v10, s9, v13
	v_lshl_add_u32 v15, v11, 1, v14
	v_mad_i64_i32 v[10:11], s[14:15], v10, s24, v[4:5]
	v_lshl_add_u64 v[10:11], v[10:11], 0, s[16:17]
	v_lshl_add_u64 v[10:11], v[10:11], 0, v[2:3]
	v_lshl_add_u32 v13, v13, 1, v14
	v_ashrrev_i32_e32 v38, 3, v1
	v_and_b32_e32 v39, 56, v12
	v_mov_b32_e32 v55, 0x42800000
	v_cndmask_b32_e32 v35, 0, v55, vcc
	v_add_f32_e32 v34, v34, v35
	v_exp_f32_e32 v34, v34
	v_ashrrev_i32_e32 v37, 3, v37
	v_mad_u32_u24 v36, v39, s20, v36
	v_sub_u32_e32 v40, 0x7f, v38
	v_ldexp_f32 v34, v34, s12
	v_sub_f32_e32 v34, 1.0, v34
	v_cmp_gt_f32_e32 vcc, s25, v34
	s_and_b64 s[12:13], vcc, exec
	v_cvt_f32_i32_e32 v35, v40
	v_mov_b32_e32 v40, 0x42000000
	v_cndmask_b32_e32 v40, 0, v40, vcc
	v_not_b32_e32 v56, 63
	v_and_b32_e32 v54, 31, v1
	v_readlane_b32 s30, v253, 19
	v_readlane_b32 s31, v253, 20
	s_movk_i32 s7, 0x1000
	s_waitcnt vmcnt(0) lgkmcnt(0)
	ds_write_b16 v15, v6
	ds_write_b16_d16_hi v15, v6 offset:272
	ds_write_b16 v15, v7 offset:544
	ds_write_b16_d16_hi v15, v7 offset:816
	ds_write_b16 v15, v8 offset:1088
	ds_write_b16_d16_hi v15, v8 offset:1360
	ds_write_b16 v15, v9 offset:1632
	ds_write_b16_d16_hi v15, v9 offset:1904
	global_load_dwordx4 v[6:9], v[10:11], off offset:2048
	v_add_u32_e32 v10, 0x400, v1
	v_ashrrev_i32_e32 v15, 4, v10
	v_add_u32_e32 v10, s9, v15
	v_mad_i64_i32 v[10:11], s[14:15], v10, s24, v[4:5]
	v_lshl_add_u64 v[10:11], v[10:11], 0, s[16:17]
	v_lshl_add_u64 v[10:11], v[10:11], 0, v[2:3]
	v_lshl_add_u32 v15, v15, 1, v14
	s_waitcnt vmcnt(0) lgkmcnt(0)
	ds_write_b16 v13, v6
	ds_write_b16_d16_hi v13, v6 offset:272
	ds_write_b16 v13, v7 offset:544
	ds_write_b16_d16_hi v13, v7 offset:816
	ds_write_b16 v13, v8 offset:1088
	ds_write_b16_d16_hi v13, v8 offset:1360
	ds_write_b16 v13, v9 offset:1632
	ds_write_b16_d16_hi v13, v9 offset:1904
	global_load_dwordx4 v[6:9], v[10:11], off offset:2048
	v_add_u32_e32 v10, 0x600, v1
	v_ashrrev_i32_e32 v13, 4, v10
	v_add_u32_e32 v10, s9, v13
	v_mad_i64_i32 v[10:11], s[14:15], v10, s24, v[4:5]
	v_lshl_add_u64 v[10:11], v[10:11], 0, s[16:17]
	v_lshl_add_u64 v[10:11], v[10:11], 0, v[2:3]
	v_add_u32_e32 v2, s9, v38
	v_lshl_add_u32 v12, v13, 1, v14
	s_waitcnt vmcnt(0) lgkmcnt(0)
	ds_write_b16 v15, v6
	ds_write_b16_d16_hi v15, v6 offset:272
	ds_write_b16 v15, v7 offset:544
	ds_write_b16_d16_hi v15, v7 offset:816
	ds_write_b16 v15, v8 offset:1088
	ds_write_b16_d16_hi v15, v8 offset:1360
	ds_write_b16 v15, v9 offset:1632
	ds_write_b16_d16_hi v15, v9 offset:1904
	global_load_dwordx4 v[6:9], v[10:11], off offset:2048
	v_mad_i64_i32 v[10:11], s[14:15], v2, s24, v[4:5]
	v_lshlrev_b32_e32 v2, 2, v39
	v_lshl_add_u64 v[10:11], v[10:11], 0, s[16:17]
	v_lshl_add_u64 v[26:27], s[10:11], 0, v[2:3]
	v_lshlrev_b32_e32 v2, 1, v39
	s_mov_b64 s[14:15], 0x200000
	v_lshl_add_u64 v[14:15], v[10:11], 0, v[2:3]
	v_add_u32_e32 v39, s9, v37
	s_cselect_b32 s9, 32, 0
	v_ldexp_f32 v34, v34, s9
	v_log_f32_e32 v34, v34
	v_mad_i64_i32 v[4:5], s[12:13], v39, s24, v[4:5]
	v_lshl_add_u64 v[4:5], v[4:5], 0, s[16:17]
	v_sub_f32_e32 v34, v34, v40
	v_mul_f32_e32 v39, v34, v35
	v_cmp_gt_f32_e32 vcc, s6, v39
	v_lshl_add_u64 v[4:5], v[4:5], 0, v[2:3]
	s_mov_b32 s9, s29
	v_cndmask_b32_e32 v39, 0, v55, vcc
	v_fmac_f32_e32 v39, v34, v35
	v_exp_f32_e32 v35, v39
	v_cndmask_b32_e32 v2, 0, v56, vcc
	v_writelane_b32 v253, s8, 17
	s_waitcnt vmcnt(0) lgkmcnt(0)
	ds_write_b16 v12, v6
	ds_write_b16_d16_hi v12, v6 offset:272
	ds_write_b16 v12, v7 offset:544
	ds_write_b16_d16_hi v12, v7 offset:816
	ds_write_b16 v12, v8 offset:1088
	ds_write_b16_d16_hi v12, v8 offset:1360
	ds_write_b16 v12, v9 offset:1632
	ds_write_b16_d16_hi v12, v9 offset:1904
	v_add_lshl_u32 v6, v38, s3, 6
	v_ashrrev_i32_e32 v7, 31, v6
	v_lshlrev_b64 v[28:29], 2, v[6:7]
	v_lshl_add_u64 v[6:7], v[26:27], 0, s[14:15]
	global_load_dwordx4 v[10:13], v[14:15], off offset:1024
	s_nop 0
	global_load_dwordx4 v[14:17], v[14:15], off offset:1152
	v_lshl_add_u64 v[8:9], v[6:7], 0, v[28:29]
	s_mov_b64 s[14:15], 0x100000
	global_load_dwordx4 v[18:21], v[8:9], off
	global_load_dwordx4 v[22:25], v[8:9], off offset:16
	v_lshl_add_u64 v[8:9], v[26:27], 0, s[14:15]
	v_lshl_add_u64 v[30:31], v[8:9], 0, v[28:29]
	global_load_dwordx4 v[26:29], v[30:31], off
	s_nop 0
	global_load_dwordx4 v[30:33], v[30:31], off offset:16
	v_ldexp_f32 v2, v35, v2
	v_mul_f32_e32 v2, 0x3db504f3, v2
	v_lshl_add_u32 v38, v38, 1, v36
	v_writelane_b32 v253, s9, 18
	v_writelane_b32 v253, s10, 19
	v_writelane_b32 v253, s11, 20
	s_ashr_i32 s9, s8, 31
	s_lshl_b64 s[8:9], s[8:9], 16
	s_waitcnt vmcnt(0) lgkmcnt(0)
	v_lshlrev_b32_e32 v35, 16, v10
	v_lshlrev_b32_e32 v39, 16, v14
	v_and_b32_e32 v10, 0xffff0000, v10
	v_and_b32_e32 v14, 0xffff0000, v14
	v_lshlrev_b32_e32 v40, 16, v11
	v_and_b32_e32 v11, 0xffff0000, v11
	v_lshlrev_b32_e32 v41, 16, v15
	v_and_b32_e32 v15, 0xffff0000, v15
	v_lshlrev_b32_e32 v42, 16, v12
	v_and_b32_e32 v12, 0xffff0000, v12
	v_lshlrev_b32_e32 v43, 16, v16
	v_and_b32_e32 v16, 0xffff0000, v16
	v_lshlrev_b32_e32 v44, 16, v13
	v_and_b32_e32 v13, 0xffff0000, v13
	v_lshlrev_b32_e32 v45, 16, v17
	v_and_b32_e32 v17, 0xffff0000, v17
	v_mul_f32_e32 v46, v18, v39
	v_mul_f32_e32 v47, v19, v14
	v_mul_f32_e32 v18, v18, v35
	v_mul_f32_e32 v19, v19, v10
	v_mul_f32_e32 v48, v20, v41
	v_mul_f32_e32 v49, v21, v15
	v_mul_f32_e32 v20, v20, v40
	v_mul_f32_e32 v21, v21, v11
	v_mul_f32_e32 v50, v22, v43
	v_mul_f32_e32 v51, v23, v16
	v_mul_f32_e32 v22, v22, v42
	v_mul_f32_e32 v23, v23, v12
	v_mul_f32_e32 v52, v24, v45
	v_mul_f32_e32 v53, v25, v17
	v_mul_f32_e32 v24, v24, v44
	v_mul_f32_e32 v25, v25, v13
	v_fma_f32 v35, v26, v35, -v46
	v_fma_f32 v10, v27, v10, -v47
	v_fmac_f32_e32 v18, v26, v39
	v_fmac_f32_e32 v19, v27, v14
	v_fma_f32 v14, v28, v40, -v48
	v_fma_f32 v11, v29, v11, -v49
	v_fmac_f32_e32 v20, v28, v41
	v_fmac_f32_e32 v21, v29, v15
	v_fma_f32 v15, v30, v42, -v50
	v_fma_f32 v12, v31, v12, -v51
	v_fmac_f32_e32 v22, v30, v43
	v_fmac_f32_e32 v23, v31, v16
	v_fma_f32 v16, v32, v44, -v52
	v_fma_f32 v13, v33, v13, -v53
	v_fmac_f32_e32 v24, v32, v45
	v_fmac_f32_e32 v25, v33, v17
	v_mul_f32_e32 v17, v2, v35
	v_mul_f32_e32 v10, v2, v10
	v_mul_f32_e32 v18, v2, v18
	v_mul_f32_e32 v19, v2, v19
	v_mul_f32_e32 v14, v2, v14
	v_mul_f32_e32 v11, v2, v11
	v_mul_f32_e32 v20, v2, v20
	v_mul_f32_e32 v21, v2, v21
	v_mul_f32_e32 v15, v2, v15
	v_mul_f32_e32 v12, v2, v12
	v_mul_f32_e32 v22, v2, v22
	v_mul_f32_e32 v23, v2, v23
	v_mul_f32_e32 v16, v2, v16
	v_mul_f32_e32 v13, v2, v13
	v_mul_f32_e32 v24, v2, v24
	v_mul_f32_e32 v2, v2, v25
	v_cvt_pk_bf16_f32 v17, v17, s0
	v_cvt_pk_bf16_f32 v10, v10, s0
	v_cvt_pk_bf16_f32 v18, v18, s0
	v_cvt_pk_bf16_f32 v19, v19, s0
	v_cvt_pk_bf16_f32 v14, v14, s0
	v_cvt_pk_bf16_f32 v11, v11, s0
	v_cvt_pk_bf16_f32 v20, v20, s0
	v_cvt_pk_bf16_f32 v21, v21, s0
	v_cvt_pk_bf16_f32 v15, v15, s0
	v_cvt_pk_bf16_f32 v12, v12, s0
	v_cvt_pk_bf16_f32 v22, v22, s0
	v_cvt_pk_bf16_f32 v23, v23, s0
	v_cvt_pk_bf16_f32 v16, v16, s0
	v_cvt_pk_bf16_f32 v13, v13, s0
	v_cvt_pk_bf16_f32 v24, v24, s0
	v_cvt_pk_bf16_f32 v2, v2, s0
	ds_write_b16 v38, v17 offset:34816
	ds_write_b16 v38, v10 offset:35088
	ds_write_b16 v38, v18 offset:52224
	ds_write_b16 v38, v19 offset:52496
	ds_write_b16 v38, v14 offset:35360
	ds_write_b16 v38, v11 offset:35632
	ds_write_b16 v38, v20 offset:52768
	ds_write_b16 v38, v21 offset:53040
	ds_write_b16 v38, v15 offset:35904
	ds_write_b16 v38, v12 offset:36176
	ds_write_b16 v38, v22 offset:53312
	ds_write_b16 v38, v23 offset:53584
	ds_write_b16 v38, v16 offset:36448
	ds_write_b16 v38, v13 offset:36720
	ds_write_b16 v38, v24 offset:53856
	ds_write_b16 v38, v2 offset:54128
	global_load_dwordx4 v[10:13], v[4:5], off offset:1024
	global_load_dwordx4 v[14:17], v[4:5], off offset:1152
	v_add_lshl_u32 v4, v37, s3, 6
	v_ashrrev_i32_e32 v5, 31, v4
	v_lshlrev_b64 v[22:23], 2, v[4:5]
	v_lshl_add_u64 v[18:19], v[6:7], 0, v[22:23]
	global_load_dwordx4 v[4:7], v[18:19], off
	s_nop 0
	global_load_dwordx4 v[18:21], v[18:19], off offset:16
	v_lshl_add_u64 v[8:9], v[8:9], 0, v[22:23]
	global_load_dwordx4 v[22:25], v[8:9], off
	global_load_dwordx4 v[26:29], v[8:9], off offset:16
	v_sub_u32_e32 v8, 0x7f, v37
	v_cvt_f32_i32_e32 v8, v8
	v_readfirstlane_b32 s3, v1
	v_bfe_u32 v1, v1, 5, 1
	s_ashr_i32 s14, s3, 7
	v_lshl_add_u32 v2, v1, 4, s72
	v_lshl_or_b32 v30, s14, 5, v54
	v_mad_u64_u32 v[52:53], s[12:13], v30, s20, v[2:3]
	v_mul_f32_e32 v30, v34, v8
	v_cmp_gt_f32_e32 vcc, s6, v30
	v_lshl_add_u32 v9, v37, 1, v36
	s_add_u32 s8, s10, s8
	v_cndmask_b32_e32 v30, 0, v55, vcc
	v_fmac_f32_e32 v30, v34, v8
	v_exp_f32_e32 v8, v30
	v_cndmask_b32_e32 v30, 0, v56, vcc
	s_addc_u32 s9, s11, s9
	s_add_u32 s8, s8, 0x4b900000
	v_ldexp_f32 v8, v8, v30
	v_mul_f32_e32 v8, 0x3db504f3, v8
	s_addc_u32 s9, s9, 0
	s_and_b32 s3, s3, 64
	v_or_b32_e32 v53, s3, v54
	v_mad_u32_u24 v56, v53, s20, v2
	v_lshlrev_b32_e32 v1, 9, v1
	s_lshl_b32 s10, s14, 12
	v_or3_b32 v1, s10, v1, v54
	v_or_b32_e32 v60, s3, v1
	v_ashrrev_i32_e32 v61, 31, v60
	v_lshl_add_u64 v[62:63], v[60:61], 2, s[8:9]
	v_add_co_u32_e32 v64, vcc, s7, v62
	s_movk_i32 s3, 0x2000
	s_nop 0
	v_addc_co_u32_e32 v65, vcc, 0, v63, vcc
	s_movk_i32 s6, 0x3000
	v_ashrrev_i32_e32 v61, 31, v1
	s_mov_b64 s[10:11], 0
	s_waitcnt vmcnt(0) lgkmcnt(0)
	v_and_b32_e32 v37, 0xffff0000, v13
	v_lshlrev_b32_e32 v31, 16, v14
	v_and_b32_e32 v36, 0xffff0000, v17
	v_lshlrev_b32_e32 v17, 16, v17
	v_lshlrev_b32_e32 v13, 16, v13
	v_lshlrev_b32_e32 v30, 16, v10
	v_and_b32_e32 v10, 0xffff0000, v10
	v_and_b32_e32 v14, 0xffff0000, v14
	v_lshlrev_b32_e32 v32, 16, v11
	v_and_b32_e32 v11, 0xffff0000, v11
	v_lshlrev_b32_e32 v33, 16, v15
	v_and_b32_e32 v15, 0xffff0000, v15
	v_lshlrev_b32_e32 v34, 16, v12
	v_and_b32_e32 v12, 0xffff0000, v12
	v_lshlrev_b32_e32 v35, 16, v16
	v_and_b32_e32 v16, 0xffff0000, v16
	v_mul_f32_e32 v38, v4, v31
	v_mul_f32_e32 v44, v20, v17
	v_mul_f32_e32 v20, v20, v13
	v_mul_f32_e32 v39, v5, v14
	v_mul_f32_e32 v4, v4, v30
	v_mul_f32_e32 v5, v5, v10
	v_mul_f32_e32 v40, v6, v33
	v_mul_f32_e32 v41, v7, v15
	v_mul_f32_e32 v6, v6, v32
	v_mul_f32_e32 v7, v7, v11
	v_mul_f32_e32 v42, v18, v35
	v_mul_f32_e32 v43, v19, v16
	v_mul_f32_e32 v18, v18, v34
	v_mul_f32_e32 v19, v19, v12
	v_mul_f32_e32 v45, v21, v36
	v_mul_f32_e32 v21, v21, v37
	v_fma_f32 v30, v22, v30, -v38
	v_fmac_f32_e32 v20, v28, v17
	v_fma_f32 v10, v23, v10, -v39
	v_fmac_f32_e32 v4, v22, v31
	v_fmac_f32_e32 v5, v23, v14
	v_fma_f32 v14, v24, v32, -v40
	v_fma_f32 v11, v25, v11, -v41
	v_fmac_f32_e32 v6, v24, v33
	v_fmac_f32_e32 v7, v25, v15
	v_fma_f32 v15, v26, v34, -v42
	v_fma_f32 v12, v27, v12, -v43
	v_fmac_f32_e32 v18, v26, v35
	v_fmac_f32_e32 v19, v27, v16
	v_fma_f32 v13, v28, v13, -v44
	v_fma_f32 v16, v29, v37, -v45
	v_fmac_f32_e32 v21, v29, v36
	v_mul_f32_e32 v17, v8, v30
	v_mul_f32_e32 v20, v8, v20
	v_mul_f32_e32 v10, v8, v10
	v_mul_f32_e32 v4, v8, v4
	v_mul_f32_e32 v5, v8, v5
	v_mul_f32_e32 v14, v8, v14
	v_mul_f32_e32 v11, v8, v11
	v_mul_f32_e32 v6, v8, v6
	v_mul_f32_e32 v7, v8, v7
	v_mul_f32_e32 v15, v8, v15
	v_mul_f32_e32 v12, v8, v12
	v_mul_f32_e32 v18, v8, v18
	v_mul_f32_e32 v19, v8, v19
	v_mul_f32_e32 v13, v8, v13
	v_mul_f32_e32 v16, v8, v16
	v_mul_f32_e32 v8, v8, v21
	v_cvt_pk_bf16_f32 v17, v17, s0
	v_cvt_pk_bf16_f32 v20, v20, s0
	v_cvt_pk_bf16_f32 v10, v10, s0
	v_cvt_pk_bf16_f32 v4, v4, s0
	v_cvt_pk_bf16_f32 v5, v5, s0
	v_cvt_pk_bf16_f32 v14, v14, s0
	v_cvt_pk_bf16_f32 v11, v11, s0
	v_cvt_pk_bf16_f32 v6, v6, s0
	v_cvt_pk_bf16_f32 v7, v7, s0
	v_cvt_pk_bf16_f32 v15, v15, s0
	v_cvt_pk_bf16_f32 v12, v12, s0
	v_cvt_pk_bf16_f32 v18, v18, s0
	v_cvt_pk_bf16_f32 v19, v19, s0
	v_cvt_pk_bf16_f32 v13, v13, s0
	v_cvt_pk_bf16_f32 v16, v16, s0
	v_cvt_pk_bf16_f32 v8, v8, s0
	ds_write_b16 v9, v17 offset:34816
	ds_write_b16 v9, v10 offset:35088
	ds_write_b16 v9, v4 offset:52224
	ds_write_b16 v9, v5 offset:52496
	ds_write_b16 v9, v14 offset:35360
	ds_write_b16 v9, v11 offset:35632
	ds_write_b16 v9, v6 offset:52768
	ds_write_b16 v9, v7 offset:53040
	ds_write_b16 v9, v15 offset:35904
	ds_write_b16 v9, v12 offset:36176
	ds_write_b16 v9, v18 offset:53312
	ds_write_b16 v9, v19 offset:53584
	ds_write_b16 v9, v13 offset:36448
	ds_write_b16 v9, v16 offset:36720
	ds_write_b16 v9, v20 offset:53856
	ds_write_b16 v9, v8 offset:54128
	s_waitcnt lgkmcnt(0)
	s_barrier
	ds_read_b128 v[20:23], v52
	ds_read_b128 v[4:7], v56 offset:34816
	ds_read_b128 v[24:27], v52 offset:32
	ds_read_b128 v[28:31], v56 offset:34848
	s_waitcnt lgkmcnt(2)
	v_mfma_f32_32x32x16_bf16 v[4:19], v[20:23], v[4:7], 0
	s_waitcnt lgkmcnt(0)
	v_mfma_f32_32x32x16_bf16 v[4:19], v[24:27], v[28:31], v[4:19]
	ds_read_b128 v[28:31], v52 offset:64
	ds_read_b128 v[32:35], v56 offset:34880
	ds_read_b128 v[36:39], v52 offset:96
	ds_read_b128 v[40:43], v56 offset:34912
	s_waitcnt lgkmcnt(2)
	v_mfma_f32_32x32x16_bf16 v[4:19], v[28:31], v[32:35], v[4:19]
	s_waitcnt lgkmcnt(0)
	v_mfma_f32_32x32x16_bf16 v[4:19], v[36:39], v[40:43], v[4:19]
	ds_read_b128 v[32:35], v52 offset:128
	ds_read_b128 v[40:43], v56 offset:34944
	ds_read_b128 v[44:47], v52 offset:160
	ds_read_b128 v[48:51], v56 offset:34976
	s_waitcnt lgkmcnt(2)
	v_mfma_f32_32x32x16_bf16 v[4:19], v[32:35], v[40:43], v[4:19]
	v_or_b32_e32 v40, 32, v53
	v_mad_u32_u24 v2, v40, s20, v2
	ds_read_b128 v[40:43], v52 offset:192
	s_waitcnt lgkmcnt(1)
	v_mfma_f32_32x32x16_bf16 v[4:19], v[44:47], v[48:51], v[4:19]
	ds_read_b128 v[48:51], v56 offset:35008
	ds_read_b128 v[52:55], v52 offset:224
	ds_read_b128 v[56:59], v56 offset:35040
	s_waitcnt lgkmcnt(2)
	v_mfma_f32_32x32x16_bf16 v[4:19], v[40:43], v[48:51], v[4:19]
	v_add_co_u32_e32 v48, vcc, s3, v62
	s_nop 1
	v_addc_co_u32_e32 v49, vcc, 0, v63, vcc
	v_add_co_u32_e32 v50, vcc, s6, v62
	s_waitcnt lgkmcnt(0)
	v_mfma_f32_32x32x16_bf16 v[4:19], v[52:55], v[56:59], v[4:19]
	v_addc_co_u32_e32 v51, vcc, 0, v63, vcc
	s_nop 10
	global_store_dword v[62:63], v4, off
	global_store_dword v[62:63], v5, off offset:512
	global_store_dword v[62:63], v6, off offset:1024
	global_store_dword v[62:63], v7, off offset:1536
	global_store_dword v[64:65], v8, off
	global_store_dword v[64:65], v9, off offset:512
	global_store_dword v[64:65], v10, off offset:1024
	global_store_dword v[64:65], v11, off offset:1536
	global_store_dword v[48:49], v12, off
	global_store_dword v[48:49], v13, off offset:512
	global_store_dword v[48:49], v14, off offset:1024
	global_store_dword v[48:49], v15, off offset:1536
	global_store_dword v[50:51], v16, off
	global_store_dword v[50:51], v17, off offset:512
	global_store_dword v[50:51], v18, off offset:1024
	global_store_dword v[50:51], v19, off offset:1536
	ds_read_b128 v[4:7], v2 offset:34816
	ds_read_b128 v[48:51], v2 offset:34848
	s_waitcnt lgkmcnt(0)
	v_mfma_f32_32x32x16_bf16 v[4:19], v[20:23], v[4:7], 0
	v_mfma_f32_32x32x16_bf16 v[4:19], v[24:27], v[48:51], v[4:19]
	ds_read_b128 v[20:23], v2 offset:34880
	ds_read_b128 v[24:27], v2 offset:34912
	s_waitcnt lgkmcnt(0)
	v_mfma_f32_32x32x16_bf16 v[4:19], v[28:31], v[20:23], v[4:19]
	v_lshl_add_u64 v[28:29], v[60:61], 2, s[8:9]
	v_add_co_u32_e32 v30, vcc, s7, v28
	s_nop 1
	v_addc_co_u32_e32 v31, vcc, 0, v29, vcc
	v_mfma_f32_32x32x16_bf16 v[4:19], v[36:39], v[24:27], v[4:19]
	ds_read_b128 v[20:23], v2 offset:34944
	ds_read_b128 v[24:27], v2 offset:34976
	s_waitcnt lgkmcnt(0)
	v_mfma_f32_32x32x16_bf16 v[4:19], v[32:35], v[20:23], v[4:19]
	ds_read_b128 v[20:23], v2 offset:35008
	v_add_co_u32_e32 v32, vcc, s3, v28
	s_nop 1
	v_addc_co_u32_e32 v33, vcc, 0, v29, vcc
	v_mfma_f32_32x32x16_bf16 v[4:19], v[44:47], v[24:27], v[4:19]
	ds_read_b128 v[24:27], v2 offset:35040
	s_waitcnt lgkmcnt(0)
	v_mfma_f32_32x32x16_bf16 v[4:19], v[40:43], v[20:23], v[4:19]
	v_add_co_u32_e32 v20, vcc, 0x3000, v28
	s_nop 1
	v_addc_co_u32_e32 v21, vcc, 0, v29, vcc
	v_mfma_f32_32x32x16_bf16 v[4:19], v[52:55], v[24:27], v[4:19]
	s_nop 11
	global_store_dword v[28:29], v4, off offset:128
	global_store_dword v[28:29], v5, off offset:640
	global_store_dword v[28:29], v6, off offset:1152
	global_store_dword v[28:29], v7, off offset:1664
	global_store_dword v[30:31], v8, off offset:128
	global_store_dword v[30:31], v9, off offset:640
	global_store_dword v[30:31], v10, off offset:1152
	global_store_dword v[30:31], v11, off offset:1664
	global_store_dword v[32:33], v12, off offset:128
	global_store_dword v[32:33], v13, off offset:640
	global_store_dword v[32:33], v14, off offset:1152
	global_store_dword v[32:33], v15, off offset:1664
	global_store_dword v[20:21], v16, off offset:128
	global_store_dword v[20:21], v17, off offset:640
	global_store_dword v[20:21], v18, off offset:1152
	global_store_dword v[20:21], v19, off offset:1664
	s_branch .LBB0_378

.LBB0_384:
	s_or_b64 exec, exec, s[12:13]
	v_ashrrev_i32_e32 v14, 4, v13
	v_add_u32_e32 v2, s9, v14
	v_mov_b64_e32 v[6:7], s[10:11]
	v_add_u32_e32 v16, 0x200, v13
	s_waitcnt lgkmcnt(0)
	v_mad_i64_i32 v[4:5], s[10:11], v2, s24, v[6:7]
	v_lshlrev_b32_e32 v2, 1, v24
	v_ashrrev_i32_e32 v15, 4, v16
	v_and_b32_e32 v2, 0xf0, v2
	v_add_u32_e32 v8, s9, v15
	v_lshl_add_u64 v[4:5], v[4:5], 0, v[2:3]
	v_mad_i64_i32 v[6:7], s[10:11], v8, s24, v[6:7]
	global_load_dwordx4 v[20:23], v[4:5], off offset:2048
	v_lshl_add_u64 v[6:7], v[6:7], 0, v[2:3]
	global_load_dwordx4 v[24:27], v[4:5], off offset:2304
	global_load_dwordx4 v[28:31], v[4:5], off offset:2560
	global_load_dwordx4 v[32:35], v[6:7], off offset:2048
	global_load_dwordx4 v[36:39], v[6:7], off offset:2304
	global_load_dwordx4 v[40:43], v[4:5], off offset:2816
	global_load_dwordx4 v[44:47], v[6:7], off offset:2560
	global_load_dwordx4 v[48:51], v[6:7], off offset:2816
	s_movk_i32 s6, 0x1000
	v_add_co_u32_e32 v8, vcc, s6, v4
	s_ashr_i32 s10, s3, 31
	s_nop 0
	v_addc_co_u32_e32 v9, vcc, 0, v5, vcc
	global_load_dwordx4 v[52:55], v[8:9], off offset:2048
	v_add_co_u32_e32 v10, vcc, s6, v6
	s_movk_i32 s6, 0x504
	s_nop 0
	v_addc_co_u32_e32 v11, vcc, 0, v7, vcc
	global_load_dwordx4 v[56:59], v[10:11], off offset:2048
	v_mul_lo_u32 v14, v14, s6
	s_lshr_b32 s10, s10, 26
	v_add3_u32 v17, s72, v14, v2
	v_mul_lo_u32 v14, v15, s6
	s_ashr_i32 s9, s8, 31
	v_lshlrev_b32_e32 v13, 1, v1
	v_mul_u32_u24_e32 v19, 0x504, v12
	s_add_i32 s3, s3, s10
	v_add3_u32 v18, s72, v14, v2
	s_lshl_b64 s[8:9], s[8:9], 1
	v_add3_u32 v13, s72, v13, v19
	s_lshr_b32 s3, s3, 6
	v_add_u32_e32 v2, 0x400, v17
	v_add_u32_e32 v14, 0x408, v17
	v_add_u32_e32 v15, 0x400, v18
	v_add_u32_e32 v60, 0x408, v18
	s_waitcnt lgkmcnt(0)
	s_barrier
	s_add_u32 s4, s4, s8
	s_addc_u32 s5, s5, s9
	s_add_u32 s4, s4, 0x2b800000
	s_mulk_i32 s3, 0x480
	s_addc_u32 s5, s5, 0
	s_mov_b32 s6, 0x5040100
	s_movk_i32 s7, 0x2100
	s_add_i32 s8, s3, 0x80
	s_waitcnt vmcnt(0)
	ds_write2_b32 v17, v20, v21 offset1:1
	ds_write2_b32 v17, v22, v23 offset0:2 offset1:3
	ds_write2_b32 v17, v24, v25 offset0:64 offset1:65
	ds_write2_b32 v17, v26, v27 offset0:66 offset1:67
	ds_write2_b32 v17, v28, v29 offset0:128 offset1:129
	ds_write2_b32 v17, v30, v31 offset0:130 offset1:131
	ds_write2_b32 v17, v40, v41 offset0:192 offset1:193
	ds_write2_b32 v17, v42, v43 offset0:194 offset1:195
	ds_write2_b32 v18, v32, v33 offset1:1
	ds_write2_b32 v18, v34, v35 offset0:2 offset1:3
	ds_write2_b32 v18, v36, v37 offset0:64 offset1:65
	ds_write2_b32 v18, v38, v39 offset0:66 offset1:67
	ds_write2_b32 v18, v44, v45 offset0:128 offset1:129
	ds_write2_b32 v18, v46, v47 offset0:130 offset1:131
	ds_write2_b32 v18, v48, v49 offset0:192 offset1:193
	ds_write2_b32 v18, v50, v51 offset0:194 offset1:195
	ds_write2_b32 v2, v52, v53 offset1:1
	ds_write2_b32 v14, v54, v55 offset1:1
	ds_write2_b32 v15, v56, v57 offset1:1
	ds_write2_b32 v60, v58, v59 offset1:1
	s_waitcnt lgkmcnt(0)
	s_barrier
	ds_read_u16 v2, v13
	ds_read_u16 v14, v13 offset:1284
	ds_read_u16 v15, v13 offset:2568
	ds_read_u16 v20, v13 offset:3852
	ds_read_u16 v21, v13 offset:5136
	ds_read_u16 v22, v13 offset:6420
	ds_read_u16 v23, v13 offset:7704
	ds_read_u16 v24, v13 offset:8988
	s_waitcnt lgkmcnt(2)
	v_perm_b32 v22, v22, v21, s6
	v_perm_b32 v21, v20, v15, s6
	v_perm_b32 v20, v14, v2, s6
	v_add_u32_e32 v2, s3, v1
	v_mov_b64_e32 v[14:15], s[4:5]
	s_waitcnt lgkmcnt(0)
	v_perm_b32 v23, v24, v23, s6
	v_mad_i64_i32 v[24:25], s[4:5], v2, s7, v[14:15]
	v_lshlrev_b32_e32 v2, 1, v12
	v_ashrrev_i32_e32 v12, 3, v16
	v_lshl_add_u64 v[24:25], v[24:25], 0, v[2:3]
	v_lshlrev_b32_e32 v16, 1, v12
	global_store_dwordx4 v[24:25], v[20:23], off
	v_add3_u32 v16, s72, v16, v19
	ds_read_u16 v19, v16 offset:2568
	ds_read_u16 v20, v16 offset:3852
	ds_read_u16 v21, v16 offset:5136
	ds_read_u16 v22, v16 offset:7704
	ds_read_u16 v23, v16 offset:8988
	ds_read_u16 v24, v16 offset:6420
	ds_read_u16 v25, v16
	ds_read_u16 v26, v16 offset:1284
	s_waitcnt lgkmcnt(0)
	v_perm_b32 v23, v23, v22, s6
	v_perm_b32 v22, v24, v21, s6
	v_perm_b32 v21, v20, v19, s6
	v_add_u32_e32 v19, s3, v12
	v_perm_b32 v20, v26, v25, s6
	v_mad_i64_i32 v[24:25], s[4:5], v19, s7, v[14:15]
	v_lshl_add_u64 v[24:25], v[24:25], 0, v[2:3]
	global_store_dwordx4 v[24:25], v[20:23], off
	ds_read_u16 v19, v13 offset:2824
	ds_read_u16 v20, v13 offset:4108
	ds_read_u16 v21, v13 offset:5392
	ds_read_u16 v22, v13 offset:7960
	ds_read_u16 v23, v13 offset:9244
	ds_read_u16 v24, v13 offset:6676
	ds_read_u16 v25, v13 offset:256
	ds_read_u16 v26, v13 offset:1540
	s_waitcnt lgkmcnt(0)
	v_perm_b32 v23, v23, v22, s6
	v_perm_b32 v22, v24, v21, s6
	v_perm_b32 v21, v20, v19, s6
	v_add_u32_e32 v19, s8, v1
	v_perm_b32 v20, v26, v25, s6
	v_mad_i64_i32 v[24:25], s[4:5], v19, s7, v[14:15]
	v_lshl_add_u64 v[24:25], v[24:25], 0, v[2:3]
	global_store_dwordx4 v[24:25], v[20:23], off
	ds_read_u16 v19, v16 offset:2824
	ds_read_u16 v20, v16 offset:4108
	ds_read_u16 v21, v16 offset:5392
	ds_read_u16 v22, v16 offset:7960
	ds_read_u16 v23, v16 offset:9244
	ds_read_u16 v24, v16 offset:6676
	ds_read_u16 v25, v16 offset:256
	ds_read_u16 v26, v16 offset:1540
	s_waitcnt lgkmcnt(0)
	v_perm_b32 v23, v23, v22, s6
	v_perm_b32 v22, v24, v21, s6
	v_perm_b32 v21, v20, v19, s6
	v_add_u32_e32 v19, s8, v12
	v_perm_b32 v20, v26, v25, s6
	v_mad_i64_i32 v[24:25], s[4:5], v19, s7, v[14:15]
	v_lshl_add_u64 v[24:25], v[24:25], 0, v[2:3]
	global_store_dwordx4 v[24:25], v[20:23], off
	ds_read_u16 v19, v13 offset:3080
	ds_read_u16 v20, v13 offset:4364
	ds_read_u16 v21, v13 offset:5648
	ds_read_u16 v22, v13 offset:8216
	ds_read_u16 v23, v13 offset:9500
	ds_read_u16 v24, v13 offset:6932
	ds_read_u16 v25, v13 offset:512
	ds_read_u16 v26, v13 offset:1796
	s_add_i32 s8, s3, 0x100
	s_waitcnt lgkmcnt(0)
	v_perm_b32 v23, v23, v22, s6
	v_perm_b32 v22, v24, v21, s6
	v_perm_b32 v21, v20, v19, s6
	v_add_u32_e32 v19, s8, v1
	v_perm_b32 v20, v26, v25, s6
	v_mad_i64_i32 v[24:25], s[4:5], v19, s7, v[14:15]
	v_lshl_add_u64 v[24:25], v[24:25], 0, v[2:3]
	global_store_dwordx4 v[24:25], v[20:23], off
	ds_read_u16 v19, v16 offset:3080
	ds_read_u16 v20, v16 offset:4364
	ds_read_u16 v21, v16 offset:5648
	ds_read_u16 v22, v16 offset:8216
	ds_read_u16 v23, v16 offset:9500
	ds_read_u16 v24, v16 offset:6932
	ds_read_u16 v25, v16 offset:512
	ds_read_u16 v26, v16 offset:1796
	s_waitcnt lgkmcnt(0)
	v_perm_b32 v23, v23, v22, s6
	v_perm_b32 v22, v24, v21, s6
	v_perm_b32 v21, v20, v19, s6
	v_add_u32_e32 v19, s8, v12
	v_perm_b32 v20, v26, v25, s6
	v_mad_i64_i32 v[24:25], s[4:5], v19, s7, v[14:15]
	v_lshl_add_u64 v[24:25], v[24:25], 0, v[2:3]
	global_store_dwordx4 v[24:25], v[20:23], off
	ds_read_u16 v19, v13 offset:3336
	ds_read_u16 v20, v13 offset:4620
	ds_read_u16 v21, v13 offset:5904
	ds_read_u16 v22, v13 offset:8472
	ds_read_u16 v23, v13 offset:9756
	ds_read_u16 v24, v13 offset:7188
	ds_read_u16 v25, v13 offset:768
	ds_read_u16 v26, v13 offset:2052
	s_add_i32 s8, s3, 0x180
	s_waitcnt lgkmcnt(0)
	v_perm_b32 v23, v23, v22, s6
	v_perm_b32 v22, v24, v21, s6
	v_perm_b32 v21, v20, v19, s6
	v_add_u32_e32 v19, s8, v1
	v_perm_b32 v20, v26, v25, s6
	v_mad_i64_i32 v[24:25], s[4:5], v19, s7, v[14:15]
	v_lshl_add_u64 v[24:25], v[24:25], 0, v[2:3]
	global_store_dwordx4 v[24:25], v[20:23], off
	ds_read_u16 v19, v16 offset:3336
	ds_read_u16 v20, v16 offset:4620
	ds_read_u16 v21, v16 offset:5904
	ds_read_u16 v22, v16 offset:8472
	ds_read_u16 v23, v16 offset:9756
	ds_read_u16 v24, v16 offset:7188
	ds_read_u16 v25, v16 offset:768
	ds_read_u16 v26, v16 offset:2052
	s_waitcnt lgkmcnt(0)
	v_perm_b32 v23, v23, v22, s6
	v_perm_b32 v22, v24, v21, s6
	v_perm_b32 v21, v20, v19, s6
	v_add_u32_e32 v19, s8, v12
	v_perm_b32 v20, v26, v25, s6
	v_mad_i64_i32 v[24:25], s[4:5], v19, s7, v[14:15]
	v_lshl_add_u64 v[24:25], v[24:25], 0, v[2:3]
	global_store_dwordx4 v[24:25], v[20:23], off
	ds_read_u16 v19, v13 offset:3592
	ds_read_u16 v20, v13 offset:4876
	ds_read_u16 v21, v13 offset:6160
	ds_read_u16 v22, v13 offset:8728
	ds_read_u16 v23, v13 offset:10012
	ds_read_u16 v24, v13 offset:7444
	ds_read_u16 v25, v13 offset:1024
	ds_read_u16 v26, v13 offset:2308
	s_add_i32 s8, s3, 0x200
	s_waitcnt lgkmcnt(0)
	v_perm_b32 v23, v23, v22, s6
	v_perm_b32 v22, v24, v21, s6
	v_perm_b32 v21, v20, v19, s6
	v_add_u32_e32 v19, s8, v1
	v_perm_b32 v20, v26, v25, s6
	v_mad_i64_i32 v[24:25], s[4:5], v19, s7, v[14:15]
	v_lshl_add_u64 v[24:25], v[24:25], 0, v[2:3]
	global_store_dwordx4 v[24:25], v[20:23], off
	ds_read_u16 v19, v16 offset:3592
	ds_read_u16 v20, v16 offset:4876
	ds_read_u16 v21, v16 offset:6160
	ds_read_u16 v22, v16 offset:8728
	ds_read_u16 v23, v16 offset:10012
	ds_read_u16 v24, v16 offset:7444
	ds_read_u16 v25, v16 offset:1024
	ds_read_u16 v26, v16 offset:2308
	s_waitcnt lgkmcnt(0)
	v_perm_b32 v23, v23, v22, s6
	v_perm_b32 v22, v24, v21, s6
	v_perm_b32 v21, v20, v19, s6
	v_add_u32_e32 v19, s8, v12
	v_perm_b32 v20, v26, v25, s6
	v_mad_i64_i32 v[24:25], s[4:5], v19, s7, v[14:15]
	v_lshl_add_u64 v[24:25], v[24:25], 0, v[2:3]
	global_store_dwordx4 v[24:25], v[20:23], off
	global_load_dwordx4 v[20:23], v[8:9], off offset:2304
	s_nop 0
	global_load_dwordx4 v[24:27], v[8:9], off offset:2560
	global_load_dwordx4 v[28:31], v[10:11], off offset:2304
	global_load_dwordx4 v[32:35], v[8:9], off offset:2816
	global_load_dwordx4 v[36:39], v[10:11], off offset:2560
	s_nop 0
	global_load_dwordx4 v[8:11], v[10:11], off offset:2816
	s_movk_i32 s4, 0x3000
	v_add_co_u32_e32 v4, vcc, s4, v4
	s_add_i32 s8, s3, 0x280
	s_nop 0
	v_addc_co_u32_e32 v5, vcc, 0, v5, vcc
	global_load_dwordx4 v[40:43], v[4:5], off
	v_add_co_u32_e32 v4, vcc, s4, v6
	s_nop 1
	v_addc_co_u32_e32 v5, vcc, 0, v7, vcc
	global_load_dwordx4 v[4:7], v[4:5], off
	s_waitcnt lgkmcnt(0)
	s_barrier
	s_waitcnt vmcnt(0)
	ds_write2_b32 v17, v20, v21 offset1:1
	ds_write2_b32 v17, v22, v23 offset0:2 offset1:3
	ds_write2_b32 v18, v28, v29 offset1:1
	ds_write2_b32 v18, v30, v31 offset0:2 offset1:3
	ds_write2_b32 v17, v24, v25 offset0:64 offset1:65
	ds_write2_b32 v17, v26, v27 offset0:66 offset1:67
	ds_write2_b32 v18, v36, v37 offset0:64 offset1:65
	ds_write2_b32 v18, v38, v39 offset0:66 offset1:67
	ds_write2_b32 v17, v32, v33 offset0:128 offset1:129
	ds_write2_b32 v17, v34, v35 offset0:130 offset1:131
	ds_write2_b32 v18, v8, v9 offset0:128 offset1:129
	ds_write2_b32 v18, v10, v11 offset0:130 offset1:131
	ds_write2_b32 v17, v40, v41 offset0:192 offset1:193
	ds_write2_b32 v17, v42, v43 offset0:194 offset1:195
	ds_write2_b32 v18, v4, v5 offset0:192 offset1:193
	ds_write2_b32 v18, v6, v7 offset0:194 offset1:195
	s_waitcnt lgkmcnt(0)
	s_barrier
	ds_read_u16 v4, v13 offset:2568
	ds_read_u16 v5, v13 offset:3852
	ds_read_u16 v6, v13 offset:5136
	ds_read_u16 v7, v13 offset:7704
	ds_read_u16 v8, v13 offset:8988
	ds_read_u16 v9, v13 offset:6420
	ds_read_u16 v10, v13
	ds_read_u16 v11, v13 offset:1284
	s_waitcnt lgkmcnt(6)
	v_perm_b32 v5, v5, v4, s6
	s_waitcnt lgkmcnt(3)
	v_perm_b32 v7, v8, v7, s6
	v_add_u32_e32 v8, s8, v1
	s_waitcnt lgkmcnt(2)
	v_perm_b32 v6, v9, v6, s6
	v_mad_i64_i32 v[8:9], s[4:5], v8, s7, v[14:15]
	s_waitcnt lgkmcnt(0)
	v_perm_b32 v4, v11, v10, s6
	v_lshl_add_u64 v[8:9], v[8:9], 0, v[2:3]
	global_store_dwordx4 v[8:9], v[4:7], off
	ds_read_u16 v4, v16 offset:2568
	ds_read_u16 v5, v16 offset:3852
	ds_read_u16 v6, v16 offset:5136
	ds_read_u16 v7, v16 offset:7704
	ds_read_u16 v8, v16 offset:8988
	ds_read_u16 v9, v16 offset:6420
	ds_read_u16 v10, v16
	ds_read_u16 v11, v16 offset:1284
	s_waitcnt lgkmcnt(0)
	v_perm_b32 v5, v5, v4, s6
	v_perm_b32 v7, v8, v7, s6
	v_add_u32_e32 v8, s8, v12
	v_perm_b32 v6, v9, v6, s6
	v_mad_i64_i32 v[8:9], s[4:5], v8, s7, v[14:15]
	v_perm_b32 v4, v11, v10, s6
	v_lshl_add_u64 v[8:9], v[8:9], 0, v[2:3]
	global_store_dwordx4 v[8:9], v[4:7], off
	ds_read_u16 v4, v13 offset:2824
	ds_read_u16 v5, v13 offset:4108
	ds_read_u16 v6, v13 offset:5392
	ds_read_u16 v7, v13 offset:7960
	ds_read_u16 v8, v13 offset:9244
	ds_read_u16 v9, v13 offset:6676
	ds_read_u16 v10, v13 offset:256
	ds_read_u16 v11, v13 offset:1540
	s_add_i32 s8, s3, 0x300
	s_waitcnt lgkmcnt(0)
	v_perm_b32 v7, v8, v7, s6
	v_add_u32_e32 v8, s8, v1
	v_perm_b32 v6, v9, v6, s6
	v_mad_i64_i32 v[8:9], s[4:5], v8, s7, v[14:15]
	v_perm_b32 v5, v5, v4, s6
	v_perm_b32 v4, v11, v10, s6
	v_lshl_add_u64 v[8:9], v[8:9], 0, v[2:3]
	global_store_dwordx4 v[8:9], v[4:7], off
	ds_read_u16 v4, v16 offset:2824
	ds_read_u16 v5, v16 offset:4108
	ds_read_u16 v6, v16 offset:5392
	ds_read_u16 v7, v16 offset:7960
	ds_read_u16 v8, v16 offset:9244
	ds_read_u16 v9, v16 offset:6676
	ds_read_u16 v10, v16 offset:256
	ds_read_u16 v11, v16 offset:1540
	s_waitcnt lgkmcnt(0)
	v_perm_b32 v5, v5, v4, s6
	v_perm_b32 v7, v8, v7, s6
	v_add_u32_e32 v8, s8, v12
	v_perm_b32 v6, v9, v6, s6
	v_mad_i64_i32 v[8:9], s[4:5], v8, s7, v[14:15]
	v_perm_b32 v4, v11, v10, s6
	v_lshl_add_u64 v[8:9], v[8:9], 0, v[2:3]
	global_store_dwordx4 v[8:9], v[4:7], off
	ds_read_u16 v4, v13 offset:3080
	ds_read_u16 v5, v13 offset:4364
	ds_read_u16 v6, v13 offset:5648
	ds_read_u16 v7, v13 offset:8216
	ds_read_u16 v8, v13 offset:9500
	ds_read_u16 v9, v13 offset:6932
	ds_read_u16 v10, v13 offset:512
	ds_read_u16 v11, v13 offset:1796
	s_add_i32 s8, s3, 0x380
	s_waitcnt lgkmcnt(0)
	v_perm_b32 v7, v8, v7, s6
	v_add_u32_e32 v8, s8, v1
	v_perm_b32 v6, v9, v6, s6
	v_mad_i64_i32 v[8:9], s[4:5], v8, s7, v[14:15]
	v_perm_b32 v5, v5, v4, s6
	v_perm_b32 v4, v11, v10, s6
	v_lshl_add_u64 v[8:9], v[8:9], 0, v[2:3]
	global_store_dwordx4 v[8:9], v[4:7], off
	ds_read_u16 v4, v16 offset:3080
	ds_read_u16 v5, v16 offset:4364
	ds_read_u16 v6, v16 offset:5648
	ds_read_u16 v7, v16 offset:8216
	ds_read_u16 v8, v16 offset:9500
	ds_read_u16 v9, v16 offset:6932
	ds_read_u16 v10, v16 offset:512
	ds_read_u16 v11, v16 offset:1796
	s_waitcnt lgkmcnt(0)
	v_perm_b32 v5, v5, v4, s6
	v_perm_b32 v7, v8, v7, s6
	v_add_u32_e32 v8, s8, v12
	v_perm_b32 v6, v9, v6, s6
	v_mad_i64_i32 v[8:9], s[4:5], v8, s7, v[14:15]
	v_perm_b32 v4, v11, v10, s6
	v_lshl_add_u64 v[8:9], v[8:9], 0, v[2:3]
	global_store_dwordx4 v[8:9], v[4:7], off
	ds_read_u16 v4, v13 offset:3336
	ds_read_u16 v5, v13 offset:4620
	ds_read_u16 v6, v13 offset:5904
	ds_read_u16 v7, v13 offset:8472
	ds_read_u16 v8, v13 offset:9756
	ds_read_u16 v9, v13 offset:7188
	ds_read_u16 v10, v13 offset:768
	ds_read_u16 v11, v13 offset:2052
	s_addk_i32 s3, 0x400
	v_add_u32_e32 v1, s3, v1
	s_waitcnt lgkmcnt(0)
	v_perm_b32 v7, v8, v7, s6
	v_perm_b32 v6, v9, v6, s6
	v_mad_i64_i32 v[8:9], s[4:5], v1, s7, v[14:15]
	v_perm_b32 v5, v5, v4, s6
	v_perm_b32 v4, v11, v10, s6
	v_lshl_add_u64 v[8:9], v[8:9], 0, v[2:3]
	global_store_dwordx4 v[8:9], v[4:7], off
	ds_read_u16 v1, v16 offset:3336
	ds_read_u16 v4, v16 offset:4620
	ds_read_u16 v5, v16 offset:5904
	ds_read_u16 v6, v16 offset:8472
	ds_read_u16 v7, v16 offset:9756
	ds_read_u16 v8, v16 offset:7188
	ds_read_u16 v9, v16 offset:768
	ds_read_u16 v10, v16 offset:2052
	s_waitcnt lgkmcnt(0)
	v_perm_b32 v7, v7, v6, s6
	v_perm_b32 v6, v8, v5, s6
	v_perm_b32 v5, v4, v1, s6
	v_add_u32_e32 v1, s3, v12
	v_perm_b32 v4, v10, v9, s6
	v_mad_i64_i32 v[8:9], s[4:5], v1, s7, v[14:15]
	v_lshl_add_u64 v[8:9], v[8:9], 0, v[2:3]
	s_mov_b64 s[4:5], 0
	global_store_dwordx4 v[8:9], v[4:7], off
	s_waitcnt lgkmcnt(0)
	s_barrier

.LBB0_386:
	s_waitcnt lgkmcnt(0)
	s_barrier
	s_and_saveexec_b64 s[4:5], s[36:37]
	s_cbranch_execz .LBB0_388
	v_mov_b64_e32 v[4:5], s[0:1]
	s_waitcnt vmcnt(0)
	global_atomic_add v1, v[4:5], v228, off sc0
	v_mov_b32_e32 v2, s2
	s_waitcnt vmcnt(0) lgkmcnt(0)
	ds_write_b32 v2, v1

.LBB0_390:
	v_add_u32_e32 v1, s12, v13
	v_ashrrev_i32_e32 v2, 6, v1
	v_add_u32_e32 v22, s9, v2
	v_add_lshl_u32 v26, v2, s8, 6
	v_mad_i64_i32 v[8:9], s[14:15], v22, s24, v[14:15]
	v_ashrrev_i32_e32 v27, 31, v26
	global_load_dwordx4 v[4:7], v[8:9], off
	s_nop 0
	global_load_dwordx4 v[8:11], v[8:9], off offset:128
	v_lshlrev_b64 v[34:35], 2, v[26:27]
	v_lshl_add_u64 v[30:31], v[16:17], 0, v[34:35]
	v_lshl_add_u64 v[38:39], v[18:19], 0, v[34:35]
	global_load_dwordx4 v[26:29], v[30:31], off
	s_nop 0
	global_load_dwordx4 v[30:33], v[30:31], off offset:16
	s_nop 0
	global_load_dwordx4 v[34:37], v[38:39], off
	s_nop 0
	global_load_dwordx4 v[38:41], v[38:39], off offset:16
	v_ashrrev_i32_e32 v23, 31, v22
	v_lshlrev_b64 v[22:23], 10, v[22:23]
	v_add_u32_e32 v1, 0x200, v1
	v_lshl_add_u64 v[22:23], v[20:21], 0, v[22:23]
	v_ashrrev_i32_e32 v1, 6, v1
	s_addk_i32 s12, 0x400
	s_cmpk_eq_i32 s12, 0x1000
	s_waitcnt vmcnt(0) lgkmcnt(0)
	v_lshlrev_b32_e32 v42, 16, v4
	v_and_b32_e32 v43, 0xffff0000, v4
	v_lshlrev_b32_e32 v44, 16, v8
	v_and_b32_e32 v45, 0xffff0000, v8
	v_pk_mul_f32 v[46:47], v[34:35], v[44:45]
	v_pk_mul_f32 v[34:35], v[34:35], v[42:43]
	v_pk_fma_f32 v[46:47], v[26:27], v[42:43], v[46:47] neg_lo:[0,0,1] neg_hi:[0,0,1]
	v_pk_fma_f32 v[26:27], v[26:27], v[44:45], v[34:35]
	v_lshlrev_b32_e32 v34, 16, v9
	v_and_b32_e32 v35, 0xffff0000, v9
	v_cvt_pk_bf16_f32 v8, v26, v27
	v_lshlrev_b32_e32 v26, 16, v5
	v_and_b32_e32 v27, 0xffff0000, v5
	v_pk_mul_f32 v[42:43], v[36:37], v[34:35]
	v_cvt_pk_bf16_f32 v4, v46, v47
	v_pk_fma_f32 v[42:43], v[28:29], v[26:27], v[42:43] neg_lo:[0,0,1] neg_hi:[0,0,1]
	v_pk_mul_f32 v[26:27], v[36:37], v[26:27]
	v_cvt_pk_bf16_f32 v5, v42, v43
	v_pk_fma_f32 v[26:27], v[28:29], v[34:35], v[26:27]
	v_lshlrev_b32_e32 v28, 16, v10
	v_and_b32_e32 v29, 0xffff0000, v10
	v_cvt_pk_bf16_f32 v9, v26, v27
	v_lshlrev_b32_e32 v26, 16, v6
	v_and_b32_e32 v27, 0xffff0000, v6
	v_pk_mul_f32 v[34:35], v[38:39], v[28:29]
	s_nop 0
	v_pk_fma_f32 v[34:35], v[30:31], v[26:27], v[34:35] neg_lo:[0,0,1] neg_hi:[0,0,1]
	v_pk_mul_f32 v[26:27], v[38:39], v[26:27]
	v_cvt_pk_bf16_f32 v6, v34, v35
	v_pk_fma_f32 v[26:27], v[30:31], v[28:29], v[26:27]
	v_lshlrev_b32_e32 v28, 16, v11
	v_and_b32_e32 v29, 0xffff0000, v11
	v_cvt_pk_bf16_f32 v10, v26, v27
	v_lshlrev_b32_e32 v26, 16, v7
	v_and_b32_e32 v27, 0xffff0000, v7
	v_pk_mul_f32 v[30:31], v[40:41], v[28:29]
	s_nop 0
	v_pk_fma_f32 v[30:31], v[32:33], v[26:27], v[30:31] neg_lo:[0,0,1] neg_hi:[0,0,1]
	v_pk_mul_f32 v[26:27], v[40:41], v[26:27]
	v_cvt_pk_bf16_f32 v7, v30, v31
	v_pk_fma_f32 v[26:27], v[32:33], v[28:29], v[26:27]
	s_nop 0
	v_cvt_pk_bf16_f32 v11, v26, v27
	global_store_dwordx4 v[22:23], v[4:7], off
	global_store_dwordx4 v[22:23], v[8:11], off offset:128
	v_add_u32_e32 v22, s9, v1
	v_add_lshl_u32 v26, v1, s8, 6
	v_mad_i64_i32 v[4:5], s[14:15], v22, s24, v[14:15]
	v_ashrrev_i32_e32 v27, 31, v26
	global_load_dwordx4 v[8:11], v[4:5], off
	s_nop 0
	global_load_dwordx4 v[4:7], v[4:5], off offset:128
	v_lshlrev_b64 v[34:35], 2, v[26:27]
	v_lshl_add_u64 v[30:31], v[16:17], 0, v[34:35]
	v_lshl_add_u64 v[38:39], v[18:19], 0, v[34:35]
	global_load_dwordx4 v[26:29], v[30:31], off
	s_nop 0
	global_load_dwordx4 v[30:33], v[30:31], off offset:16
	s_nop 0
	global_load_dwordx4 v[34:37], v[38:39], off
	s_nop 0
	global_load_dwordx4 v[38:41], v[38:39], off offset:16
	v_ashrrev_i32_e32 v23, 31, v22
	v_lshlrev_b64 v[22:23], 10, v[22:23]
	v_lshl_add_u64 v[22:23], v[20:21], 0, v[22:23]
	s_waitcnt vmcnt(0) lgkmcnt(0)
	v_lshlrev_b32_e32 v42, 16, v8
	v_and_b32_e32 v43, 0xffff0000, v8
	v_lshlrev_b32_e32 v44, 16, v4
	v_and_b32_e32 v45, 0xffff0000, v4
	v_pk_mul_f32 v[46:47], v[34:35], v[44:45]
	v_pk_mul_f32 v[34:35], v[34:35], v[42:43]
	v_pk_fma_f32 v[46:47], v[26:27], v[42:43], v[46:47] neg_lo:[0,0,1] neg_hi:[0,0,1]
	v_pk_fma_f32 v[26:27], v[26:27], v[44:45], v[34:35]
	v_lshlrev_b32_e32 v34, 16, v5
	v_and_b32_e32 v35, 0xffff0000, v5
	v_cvt_pk_bf16_f32 v8, v26, v27
	v_lshlrev_b32_e32 v26, 16, v9
	v_and_b32_e32 v27, 0xffff0000, v9
	v_pk_mul_f32 v[42:43], v[36:37], v[34:35]
	v_cvt_pk_bf16_f32 v4, v46, v47
	v_pk_fma_f32 v[42:43], v[28:29], v[26:27], v[42:43] neg_lo:[0,0,1] neg_hi:[0,0,1]
	v_pk_mul_f32 v[26:27], v[36:37], v[26:27]
	v_cvt_pk_bf16_f32 v5, v42, v43
	v_pk_fma_f32 v[26:27], v[28:29], v[34:35], v[26:27]
	v_lshlrev_b32_e32 v28, 16, v6
	v_and_b32_e32 v29, 0xffff0000, v6
	v_cvt_pk_bf16_f32 v9, v26, v27
	v_lshlrev_b32_e32 v26, 16, v10
	v_and_b32_e32 v27, 0xffff0000, v10
	v_pk_mul_f32 v[34:35], v[38:39], v[28:29]
	s_nop 0
	v_pk_fma_f32 v[34:35], v[30:31], v[26:27], v[34:35] neg_lo:[0,0,1] neg_hi:[0,0,1]
	v_pk_mul_f32 v[26:27], v[38:39], v[26:27]
	v_cvt_pk_bf16_f32 v6, v34, v35
	v_pk_fma_f32 v[26:27], v[30:31], v[28:29], v[26:27]
	v_lshlrev_b32_e32 v28, 16, v7
	v_and_b32_e32 v29, 0xffff0000, v7
	v_cvt_pk_bf16_f32 v10, v26, v27
	v_lshlrev_b32_e32 v26, 16, v11
	v_and_b32_e32 v27, 0xffff0000, v11
	v_pk_mul_f32 v[30:31], v[40:41], v[28:29]
	s_nop 0
	v_pk_fma_f32 v[30:31], v[32:33], v[26:27], v[30:31] neg_lo:[0,0,1] neg_hi:[0,0,1]
	v_pk_mul_f32 v[26:27], v[40:41], v[26:27]
	v_cvt_pk_bf16_f32 v7, v30, v31
	v_pk_fma_f32 v[26:27], v[32:33], v[28:29], v[26:27]
	s_nop 0
	v_cvt_pk_bf16_f32 v11, v26, v27
	global_store_dwordx4 v[22:23], v[4:7], off
	global_store_dwordx4 v[22:23], v[8:11], off offset:128
	s_cbranch_scc0 .LBB0_390
	v_ashrrev_i32_e32 v1, 3, v13
	v_and_b32_e32 v9, 7, v13
	v_add_u32_e32 v8, s9, v1
	v_mov_b64_e32 v[4:5], s[10:11]
	v_mul_u32_u24_e32 v2, 48, v9
	v_mad_i64_i32 v[4:5], s[12:13], v8, s24, v[4:5]
	v_lshlrev_b32_e32 v2, 1, v2
	v_lshl_add_u64 v[6:7], v[4:5], 0, v[2:3]
	s_mov_b64 s[12:13], 0x2c00
	v_lshl_add_u64 v[4:5], v[6:7], 0, s[12:13]
	v_add_co_u32_e32 v6, vcc, 0x2000, v6
	s_nop 1
	v_addc_co_u32_e32 v7, vcc, 0, v7, vcc
	global_load_dwordx4 v[14:17], v[6:7], off offset:3072
	s_waitcnt vmcnt(0) lgkmcnt(0)
	v_and_b32_e32 v6, 0xffff0000, v14
	v_lshlrev_b32_e32 v2, 16, v14
	v_mul_f32_e32 v6, v6, v6
	v_and_b32_e32 v7, 0xffff0000, v15
	v_fmac_f32_e32 v6, v2, v2
	v_lshlrev_b32_e32 v2, 16, v15
	v_mul_f32_e32 v7, v7, v7
	v_fmac_f32_e32 v7, v2, v2
	v_add_f32_e32 v2, v6, v7
	v_and_b32_e32 v7, 0xffff0000, v16
	v_lshlrev_b32_e32 v6, 16, v16
	v_mul_f32_e32 v7, v7, v7
	v_fmac_f32_e32 v7, v6, v6
	v_add_f32_e32 v2, v7, v2
	v_lshlrev_b32_e32 v6, 16, v17
	v_and_b32_e32 v7, 0xffff0000, v17
	global_load_dwordx4 v[14:17], v[4:5], off offset:16
	v_mul_f32_e32 v7, v7, v7
	v_fmac_f32_e32 v7, v6, v6
	v_add_f32_e32 v2, v7, v2
	s_waitcnt vmcnt(0) lgkmcnt(0)
	v_and_b32_e32 v7, 0xffff0000, v14
	v_lshlrev_b32_e32 v6, 16, v14
	v_mul_f32_e32 v7, v7, v7
	v_fmac_f32_e32 v7, v6, v6
	v_add_f32_e32 v2, v7, v2
	v_and_b32_e32 v7, 0xffff0000, v15
	v_lshlrev_b32_e32 v6, 16, v15
	v_mul_f32_e32 v7, v7, v7
	v_fmac_f32_e32 v7, v6, v6
	v_add_f32_e32 v2, v7, v2
	v_and_b32_e32 v7, 0xffff0000, v16
	v_lshlrev_b32_e32 v6, 16, v16
	v_mul_f32_e32 v7, v7, v7
	v_fmac_f32_e32 v7, v6, v6
	v_add_f32_e32 v2, v7, v2
	v_lshlrev_b32_e32 v6, 16, v17
	v_and_b32_e32 v7, 0xffff0000, v17
	global_load_dwordx4 v[14:17], v[4:5], off offset:32
	v_mul_f32_e32 v7, v7, v7
	v_fmac_f32_e32 v7, v6, v6
	v_add_f32_e32 v2, v7, v2
	s_waitcnt vmcnt(0) lgkmcnt(0)
	v_and_b32_e32 v7, 0xffff0000, v14
	v_lshlrev_b32_e32 v6, 16, v14
	v_mul_f32_e32 v7, v7, v7
	v_fmac_f32_e32 v7, v6, v6
	v_add_f32_e32 v2, v7, v2
	v_and_b32_e32 v7, 0xffff0000, v15
	v_lshlrev_b32_e32 v6, 16, v15
	v_mul_f32_e32 v7, v7, v7
	v_fmac_f32_e32 v7, v6, v6
	v_add_f32_e32 v2, v7, v2
	v_and_b32_e32 v7, 0xffff0000, v16
	v_lshlrev_b32_e32 v6, 16, v16
	v_mul_f32_e32 v7, v7, v7
	v_fmac_f32_e32 v7, v6, v6
	v_add_f32_e32 v2, v7, v2
	v_lshlrev_b32_e32 v6, 16, v17
	v_and_b32_e32 v7, 0xffff0000, v17
	global_load_dwordx4 v[14:17], v[4:5], off offset:48
	v_mul_f32_e32 v7, v7, v7
	v_fmac_f32_e32 v7, v6, v6
	v_add_f32_e32 v2, v7, v2
	s_waitcnt vmcnt(0) lgkmcnt(0)
	v_and_b32_e32 v7, 0xffff0000, v14
	v_lshlrev_b32_e32 v6, 16, v14
	v_mul_f32_e32 v7, v7, v7
	v_fmac_f32_e32 v7, v6, v6
	v_add_f32_e32 v2, v7, v2
	v_and_b32_e32 v7, 0xffff0000, v15
	v_lshlrev_b32_e32 v6, 16, v15
	v_mul_f32_e32 v7, v7, v7
	v_fmac_f32_e32 v7, v6, v6
	v_add_f32_e32 v2, v7, v2
	v_and_b32_e32 v7, 0xffff0000, v16
	v_lshlrev_b32_e32 v6, 16, v16
	v_mul_f32_e32 v7, v7, v7
	v_fmac_f32_e32 v7, v6, v6
	v_add_f32_e32 v2, v7, v2
	v_lshlrev_b32_e32 v6, 16, v17
	v_and_b32_e32 v7, 0xffff0000, v17
	global_load_dwordx4 v[14:17], v[4:5], off offset:64
	v_mul_f32_e32 v7, v7, v7
	v_fmac_f32_e32 v7, v6, v6
	v_add_f32_e32 v2, v7, v2
	s_waitcnt vmcnt(0) lgkmcnt(0)
	v_and_b32_e32 v7, 0xffff0000, v14
	v_lshlrev_b32_e32 v6, 16, v14
	v_mul_f32_e32 v7, v7, v7
	v_fmac_f32_e32 v7, v6, v6
	v_add_f32_e32 v2, v7, v2
	v_and_b32_e32 v7, 0xffff0000, v15
	v_lshlrev_b32_e32 v6, 16, v15
	v_mul_f32_e32 v7, v7, v7
	v_fmac_f32_e32 v7, v6, v6
	v_add_f32_e32 v2, v7, v2
	v_and_b32_e32 v7, 0xffff0000, v16
	v_lshlrev_b32_e32 v6, 16, v16
	v_mul_f32_e32 v7, v7, v7
	v_fmac_f32_e32 v7, v6, v6
	v_add_f32_e32 v2, v7, v2
	v_and_b32_e32 v7, 0xffff0000, v17
	v_lshlrev_b32_e32 v6, 16, v17
	v_mul_f32_e32 v7, v7, v7
	v_fmac_f32_e32 v7, v6, v6
	v_add_f32_e32 v2, v7, v2
	global_load_dwordx4 v[4:7], v[4:5], off offset:80
	s_waitcnt vmcnt(0) lgkmcnt(0)
	v_lshlrev_b32_e32 v10, 16, v4
	v_and_b32_e32 v4, 0xffff0000, v4
	v_mul_f32_e32 v4, v4, v4
	v_fmac_f32_e32 v4, v10, v10
	v_add_f32_e32 v2, v4, v2
	v_lshlrev_b32_e32 v4, 16, v5
	v_and_b32_e32 v5, 0xffff0000, v5
	v_mul_f32_e32 v5, v5, v5
	v_fmac_f32_e32 v5, v4, v4
	v_add_f32_e32 v2, v5, v2
	v_and_b32_e32 v5, 0xffff0000, v6
	v_lshlrev_b32_e32 v4, 16, v6
	v_mul_f32_e32 v5, v5, v5
	v_fmac_f32_e32 v5, v4, v4
	v_add_f32_e32 v2, v5, v2
	v_and_b32_e32 v5, 0xffff0000, v7
	v_lshlrev_b32_e32 v4, 16, v7
	v_mul_f32_e32 v5, v5, v5
	v_fmac_f32_e32 v5, v4, v4
	v_mbcnt_hi_u32_b32 v4, -1, v251
	v_and_b32_e32 v6, 64, v4
	v_add_f32_e32 v2, v5, v2
	v_xor_b32_e32 v5, 1, v4
	v_add_u32_e32 v6, 64, v6
	v_cmp_lt_i32_e32 vcc, v5, v6
	s_nop 1
	v_cndmask_b32_e32 v5, v4, v5, vcc
	v_lshlrev_b32_e32 v5, 2, v5
	ds_bpermute_b32 v5, v5, v2
	s_waitcnt lgkmcnt(0)
	v_add_f32_e32 v2, v2, v5
	v_xor_b32_e32 v5, 2, v4
	v_cmp_lt_i32_e32 vcc, v5, v6
	s_nop 1
	v_cndmask_b32_e32 v5, v4, v5, vcc
	v_lshlrev_b32_e32 v5, 2, v5
	ds_bpermute_b32 v5, v5, v2
	s_waitcnt lgkmcnt(0)
	v_add_f32_e32 v2, v2, v5
	v_xor_b32_e32 v5, 4, v4
	v_cmp_lt_i32_e32 vcc, v5, v6
	s_nop 1
	v_cndmask_b32_e32 v4, v4, v5, vcc
	v_lshlrev_b32_e32 v4, 2, v4
	ds_bpermute_b32 v4, v4, v2
	v_cmp_eq_u32_e32 vcc, 0, v9
	s_and_saveexec_b64 s[12:13], vcc
	s_cbranch_execz .LBB0_384
	s_waitcnt lgkmcnt(0)
	v_add_f32_e32 v2, v2, v4
	v_fmamk_f32 v2, v2, 0x3b2aaaab, v241
	v_mul_f32_e32 v4, 0x4b800000, v2
	v_cmp_gt_f32_e32 vcc, s25, v2
	v_ashrrev_i32_e32 v9, 31, v8
	s_nop 0
	v_cndmask_b32_e32 v2, v2, v4, vcc
	v_rsq_f32_e32 v2, v2
	v_lshl_add_u64 v[4:5], v[8:9], 2, s[4:5]
	v_mul_f32_e32 v6, 0x45800000, v2
	v_cndmask_b32_e32 v2, v2, v6, vcc
	v_add_co_u32_e32 v4, vcc, 0x49240000, v4
	s_nop 1
	v_addc_co_u32_e32 v5, vcc, 0, v5, vcc
	global_store_dword v[4:5], v2, off
	s_branch .LBB0_384

.LBB0_394:
	v_ashrrev_i32_e32 v5, 31, v4
	v_lshlrev_b64 v[4:5], 14, v[4:5]
	v_lshl_add_u64 v[4:5], s[6:7], 0, v[4:5]
	v_ashrrev_i32_e32 v7, 31, v6
	v_lshl_add_u64 v[16:17], v[6:7], 2, v[4:5]
	v_pk_add_f32 v[4:5], v[8:9], v[2:3] op_sel_hi:[1,0]
	v_add_co_u32_e32 v8, vcc, 0x49200000, v16
	s_mov_b64 s[0:1], 0x49200000
	v_pk_add_f32 v[6:7], v[10:11], v[2:3] op_sel_hi:[1,0]
	v_addc_co_u32_e32 v9, vcc, 0, v17, vcc
	v_lshl_add_u64 v[18:19], v[16:17], 0, s[0:1]
	global_store_dwordx4 v[8:9], v[4:7], off
	s_mov_b64 s[0:1], 0
	s_nop 0
	v_pk_add_f32 v[4:5], v[12:13], v[2:3] op_sel_hi:[1,0]
	v_pk_add_f32 v[6:7], v[14:15], v[2:3] op_sel_hi:[1,0]
	global_store_dwordx4 v[18:19], v[4:7], off offset:16
	s_waitcnt lgkmcnt(0)
	s_barrier

.LBB0_396:
	s_barrier
	s_and_saveexec_b64 s[0:1], s[36:37]
	s_cbranch_execz .LBB0_398
	v_mov_b64_e32 v[4:5], s[4:5]
	s_waitcnt vmcnt(0)
	global_atomic_add v1, v[4:5], v228, off sc0
	v_mov_b32_e32 v2, s2
	s_waitcnt vmcnt(0) lgkmcnt(0)
	ds_write_b32 v2, v1
.LBB0_398:
	s_or_b64 exec, exec, s[0:1]
	v_mov_b32_e32 v1, s2
	s_waitcnt lgkmcnt(0)
	s_barrier
	ds_read_b32 v4, v1
	s_mov_b64 s[0:1], -1
	s_waitcnt lgkmcnt(0)
	v_cmp_lt_i32_e32 vcc, 15, v4
	s_cbranch_vccnz .LBB0_395
	v_mov_b32_e32 v10, v0
	s_mov_b32 s1, s88
	v_readfirstlane_b32 s0, v10
	s_ashr_i32 s8, s0, 6
	v_readlane_b32 s0, v252, 0
	s_mov_b64 s[6:7], s[68:69]
	v_mov_b32_e32 v2, s3
	ds_read_b64 v[6:7], v2
	v_and_b32_e32 v11, 3, v4
	v_or_b32_e32 v2, s22, v11
	v_lshlrev_b64 v[8:9], 2, v[2:3]
	v_lshlrev_b32_e32 v2, 10, v4
	s_waitcnt lgkmcnt(0)
	v_lshl_add_u64 v[6:7], v[6:7], 0, v[8:9]
	global_load_dword v5, v[6:7], off
	v_and_b32_e32 v2, 0xfffff000, v2
	v_lshlrev_b32_e32 v6, 3, v10
	v_add_u32_e32 v7, v6, v2
	v_lshlrev_b32_e32 v2, 1, v11
	v_lshl_add_u64 v[8:9], s[6:7], 0, v[2:3]
	s_mov_b64 s[0:1], 0x90031a0
	v_lshl_add_u64 v[14:15], v[8:9], 0, s[0:1]
	v_mad_i64_i32 v[8:9], s[0:1], v7, s24, v[14:15]
	global_load_ushort v2, v[8:9], off
	s_mov_b32 s9, 0xbfb8aa3b
	s_mov_b32 s10, 0x3f317217
	s_mov_b32 s11, 0x7f800000
	v_mov_b32_e32 v18, 0x41b17218
	v_and_b32_e32 v1, 63, v10
	s_waitcnt vmcnt(0) lgkmcnt(0)
	v_lshlrev_b32_e32 v2, 16, v2
	v_add_f32_e32 v2, v5, v2
	v_min_f32_e32 v8, 0, v2
	v_mul_f32_e64 v2, |v2|, s9
	v_exp_f32_e32 v2, v2
	s_nop 0
	v_add_f32_e32 v2, 1.0, v2
	v_cmp_gt_f32_e32 vcc, s25, v2
	s_nop 1
	v_cndmask_b32_e64 v9, 0, 32, vcc
	v_ldexp_f32 v2, v2, v9
	v_log_f32_e32 v2, v2
	s_nop 0
	v_mul_f32_e32 v9, 0x3f317217, v2
	v_fma_f32 v9, v2, s10, -v9
	v_fmac_f32_e32 v9, 0x3377d1cf, v2
	v_fmac_f32_e32 v9, 0x3f317217, v2
	v_cmp_lt_f32_e64 s[0:1], |v2|, s11
	s_nop 1
	v_cndmask_b32_e64 v2, v2, v9, s[0:1]
	v_cndmask_b32_e32 v9, 0, v18, vcc
	v_sub_f32_e32 v2, v2, v9
	v_sub_f32_e32 v2, v8, v2
	v_or_b32_e32 v8, 1, v7
	v_mad_i64_i32 v[8:9], s[0:1], v8, s24, v[14:15]
	global_load_ushort v8, v[8:9], off
	s_waitcnt vmcnt(0) lgkmcnt(0)
	v_lshlrev_b32_e32 v8, 16, v8
	v_add_f32_e32 v8, v5, v8
	v_min_f32_e32 v9, 0, v8
	v_mul_f32_e64 v8, |v8|, s9
	v_exp_f32_e32 v8, v8
	s_nop 0
	v_add_f32_e32 v8, 1.0, v8
	v_cmp_gt_f32_e32 vcc, s25, v8
	s_nop 1
	v_cndmask_b32_e64 v10, 0, 32, vcc
	v_ldexp_f32 v8, v8, v10
	v_log_f32_e32 v8, v8
	s_nop 0
	v_mul_f32_e32 v10, 0x3f317217, v8
	v_fma_f32 v10, v8, s10, -v10
	v_fmac_f32_e32 v10, 0x3377d1cf, v8
	v_fmac_f32_e32 v10, 0x3f317217, v8
	v_cmp_lt_f32_e64 s[0:1], |v8|, s11
	s_nop 1
	v_cndmask_b32_e64 v8, v8, v10, s[0:1]
	v_cndmask_b32_e32 v10, 0, v18, vcc
	v_sub_f32_e32 v8, v8, v10
	v_sub_f32_e32 v9, v9, v8
	v_add_f32_e32 v8, 0, v2
	v_or_b32_e32 v2, 2, v7
	v_mad_i64_i32 v[10:11], s[0:1], v2, s24, v[14:15]
	global_load_ushort v2, v[10:11], off
	v_add_f32_e32 v9, v8, v9
	s_waitcnt vmcnt(0) lgkmcnt(0)
	v_lshlrev_b32_e32 v2, 16, v2
	v_add_f32_e32 v2, v5, v2
	v_min_f32_e32 v10, 0, v2
	v_mul_f32_e64 v2, |v2|, s9
	v_exp_f32_e32 v2, v2
	s_nop 0
	v_add_f32_e32 v2, 1.0, v2
	v_cmp_gt_f32_e32 vcc, s25, v2
	s_nop 1
	v_cndmask_b32_e64 v11, 0, 32, vcc
	v_ldexp_f32 v2, v2, v11
	v_log_f32_e32 v2, v2
	s_nop 0
	v_mul_f32_e32 v11, 0x3f317217, v2
	v_fma_f32 v11, v2, s10, -v11
	v_fmac_f32_e32 v11, 0x3377d1cf, v2
	v_fmac_f32_e32 v11, 0x3f317217, v2
	v_cmp_lt_f32_e64 s[0:1], |v2|, s11
	s_nop 1
	v_cndmask_b32_e64 v2, v2, v11, s[0:1]
	v_cndmask_b32_e32 v11, 0, v18, vcc
	v_sub_f32_e32 v2, v2, v11
	v_sub_f32_e32 v2, v10, v2
	v_or_b32_e32 v10, 3, v7
	v_mad_i64_i32 v[10:11], s[0:1], v10, s24, v[14:15]
	global_load_ushort v10, v[10:11], off
	s_waitcnt vmcnt(0) lgkmcnt(0)
	v_lshlrev_b32_e32 v10, 16, v10
	v_add_f32_e32 v10, v5, v10
	v_min_f32_e32 v11, 0, v10
	v_mul_f32_e64 v10, |v10|, s9
	v_exp_f32_e32 v10, v10
	s_nop 0
	v_add_f32_e32 v10, 1.0, v10
	v_cmp_gt_f32_e32 vcc, s25, v10
	s_nop 1
	v_cndmask_b32_e64 v12, 0, 32, vcc
	v_ldexp_f32 v10, v10, v12
	v_log_f32_e32 v10, v10
	s_nop 0
	v_mul_f32_e32 v12, 0x3f317217, v10
	v_fma_f32 v12, v10, s10, -v12
	v_fmac_f32_e32 v12, 0x3377d1cf, v10
	v_fmac_f32_e32 v12, 0x3f317217, v10
	v_cmp_lt_f32_e64 s[0:1], |v10|, s11
	s_nop 1
	v_cndmask_b32_e64 v10, v10, v12, s[0:1]
	v_cndmask_b32_e32 v12, 0, v18, vcc
	v_sub_f32_e32 v10, v10, v12
	v_sub_f32_e32 v11, v11, v10
	v_add_f32_e32 v10, v9, v2
	v_or_b32_e32 v2, 4, v7
	v_mad_i64_i32 v[12:13], s[0:1], v2, s24, v[14:15]
	global_load_ushort v2, v[12:13], off
	v_add_f32_e32 v11, v10, v11
	s_waitcnt vmcnt(0) lgkmcnt(0)
	v_lshlrev_b32_e32 v2, 16, v2
	v_add_f32_e32 v2, v5, v2
	v_min_f32_e32 v12, 0, v2
	v_mul_f32_e64 v2, |v2|, s9
	v_exp_f32_e32 v2, v2
	s_nop 0
	v_add_f32_e32 v2, 1.0, v2
	v_cmp_gt_f32_e32 vcc, s25, v2
	s_nop 1
	v_cndmask_b32_e64 v13, 0, 32, vcc
	v_ldexp_f32 v2, v2, v13
	v_log_f32_e32 v2, v2
	s_nop 0
	v_mul_f32_e32 v13, 0x3f317217, v2
	v_fma_f32 v13, v2, s10, -v13
	v_fmac_f32_e32 v13, 0x3377d1cf, v2
	v_fmac_f32_e32 v13, 0x3f317217, v2
	v_cmp_lt_f32_e64 s[0:1], |v2|, s11
	s_nop 1
	v_cndmask_b32_e64 v2, v2, v13, s[0:1]
	v_cndmask_b32_e32 v13, 0, v18, vcc
	v_sub_f32_e32 v2, v2, v13
	v_sub_f32_e32 v2, v12, v2
	v_or_b32_e32 v12, 5, v7
	v_mad_i64_i32 v[12:13], s[0:1], v12, s24, v[14:15]
	global_load_ushort v12, v[12:13], off
	s_waitcnt vmcnt(0) lgkmcnt(0)
	v_lshlrev_b32_e32 v12, 16, v12
	v_add_f32_e32 v12, v5, v12
	v_min_f32_e32 v13, 0, v12
	v_mul_f32_e64 v12, |v12|, s9
	v_exp_f32_e32 v12, v12
	s_nop 0
	v_add_f32_e32 v12, 1.0, v12
	v_cmp_gt_f32_e32 vcc, s25, v12
	s_nop 1
	v_cndmask_b32_e64 v16, 0, 32, vcc
	v_ldexp_f32 v12, v12, v16
	v_log_f32_e32 v12, v12
	s_nop 0
	v_mul_f32_e32 v16, 0x3f317217, v12
	v_fma_f32 v16, v12, s10, -v16
	v_fmac_f32_e32 v16, 0x3377d1cf, v12
	v_fmac_f32_e32 v16, 0x3f317217, v12
	v_cmp_lt_f32_e64 s[0:1], |v12|, s11
	s_nop 1
	v_cndmask_b32_e64 v12, v12, v16, s[0:1]
	v_cndmask_b32_e32 v16, 0, v18, vcc
	v_sub_f32_e32 v12, v12, v16
	v_sub_f32_e32 v13, v13, v12
	v_add_f32_e32 v12, v11, v2
	v_or_b32_e32 v2, 6, v7
	v_mad_i64_i32 v[16:17], s[0:1], v2, s24, v[14:15]
	global_load_ushort v2, v[16:17], off
	v_or_b32_e32 v7, 7, v7
	v_add_f32_e32 v13, v12, v13
	s_waitcnt vmcnt(0) lgkmcnt(0)
	v_lshlrev_b32_e32 v2, 16, v2
	v_add_f32_e32 v2, v5, v2
	v_min_f32_e32 v16, 0, v2
	v_mul_f32_e64 v2, |v2|, s9
	v_exp_f32_e32 v2, v2
	s_nop 0
	v_add_f32_e32 v2, 1.0, v2
	v_cmp_gt_f32_e32 vcc, s25, v2
	s_nop 1
	v_cndmask_b32_e64 v17, 0, 32, vcc
	v_ldexp_f32 v2, v2, v17
	v_log_f32_e32 v2, v2
	s_nop 0
	v_mul_f32_e32 v17, 0x3f317217, v2
	v_fma_f32 v17, v2, s10, -v17
	v_fmac_f32_e32 v17, 0x3377d1cf, v2
	v_fmac_f32_e32 v17, 0x3f317217, v2
	v_cmp_lt_f32_e64 s[0:1], |v2|, s11
	s_nop 1
	v_cndmask_b32_e64 v2, v2, v17, s[0:1]
	v_mad_i64_i32 v[14:15], s[0:1], v7, s24, v[14:15]
	global_load_ushort v7, v[14:15], off
	v_cndmask_b32_e32 v17, 0, v18, vcc
	v_sub_f32_e32 v2, v2, v17
	v_sub_f32_e32 v2, v16, v2
	s_waitcnt lgkmcnt(0)
	s_barrier
	s_waitcnt vmcnt(0)
	v_lshlrev_b32_e32 v7, 16, v7
	v_add_f32_e32 v5, v5, v7
	v_min_f32_e32 v7, 0, v5
	v_mul_f32_e64 v5, |v5|, s9
	v_exp_f32_e32 v5, v5
	s_nop 0
	v_add_f32_e32 v5, 1.0, v5
	v_cmp_gt_f32_e32 vcc, s25, v5
	s_nop 1
	v_cndmask_b32_e64 v14, 0, 32, vcc
	v_ldexp_f32 v5, v5, v14
	v_log_f32_e32 v5, v5
	s_nop 0
	v_mul_f32_e32 v14, 0x3f317217, v5
	v_fma_f32 v14, v5, s10, -v14
	v_fmac_f32_e32 v14, 0x3377d1cf, v5
	v_fmac_f32_e32 v14, 0x3f317217, v5
	v_cmp_lt_f32_e64 s[0:1], |v5|, s11
	s_nop 1
	v_cndmask_b32_e64 v5, v5, v14, s[0:1]
	v_cndmask_b32_e32 v14, 0, v18, vcc
	v_sub_f32_e32 v5, v5, v14
	v_sub_f32_e32 v5, v7, v5
	v_add_f32_e32 v14, v13, v2
	v_add_f32_e32 v15, v14, v5
	v_mbcnt_hi_u32_b32 v5, -1, v251
	v_and_b32_e32 v7, 64, v5
	v_add_u32_e32 v2, -1, v5
	v_cmp_lt_i32_e32 vcc, v2, v7
	v_add_u32_e32 v16, -2, v5
	s_nop 0
	v_cndmask_b32_e32 v2, v2, v5, vcc
	v_lshlrev_b32_e32 v2, 2, v2
	ds_bpermute_b32 v2, v2, v15
	v_cmp_eq_u32_e32 vcc, 0, v1
	s_waitcnt lgkmcnt(0)
	v_add_f32_e32 v2, v15, v2
	v_cndmask_b32_e32 v2, v2, v15, vcc
	v_cmp_lt_i32_e32 vcc, v16, v7
	s_nop 1
	v_cndmask_b32_e32 v16, v16, v5, vcc
	v_lshlrev_b32_e32 v16, 2, v16
	ds_bpermute_b32 v16, v16, v2
	v_cmp_gt_u32_e32 vcc, 2, v1
	s_waitcnt lgkmcnt(0)
	v_add_f32_e32 v16, v2, v16
	v_cndmask_b32_e32 v2, v16, v2, vcc
	v_add_u32_e32 v16, -4, v5
	v_cmp_lt_i32_e32 vcc, v16, v7
	s_nop 1
	v_cndmask_b32_e32 v16, v16, v5, vcc
	v_lshlrev_b32_e32 v16, 2, v16
	ds_bpermute_b32 v16, v16, v2
	v_cmp_gt_u32_e32 vcc, 4, v1
	s_waitcnt lgkmcnt(0)
	v_add_f32_e32 v16, v2, v16
	v_cndmask_b32_e32 v2, v16, v2, vcc
	v_add_u32_e32 v16, -8, v5
	v_cmp_lt_i32_e32 vcc, v16, v7
	s_nop 1
	v_cndmask_b32_e32 v16, v16, v5, vcc
	v_lshlrev_b32_e32 v16, 2, v16
	ds_bpermute_b32 v16, v16, v2
	v_cmp_gt_u32_e32 vcc, 8, v1
	s_waitcnt lgkmcnt(0)
	v_add_f32_e32 v16, v2, v16
	v_cndmask_b32_e32 v2, v16, v2, vcc
	v_add_u32_e32 v16, -16, v5
	v_cmp_lt_i32_e32 vcc, v16, v7
	s_nop 1
	v_cndmask_b32_e32 v16, v16, v5, vcc
	v_lshlrev_b32_e32 v16, 2, v16
	ds_bpermute_b32 v16, v16, v2
	v_cmp_gt_u32_e32 vcc, 16, v1
	s_waitcnt lgkmcnt(0)
	v_add_f32_e32 v16, v2, v16
	v_cndmask_b32_e32 v2, v16, v2, vcc
	v_subrev_u32_e32 v16, 32, v5
	v_cmp_lt_i32_e32 vcc, v16, v7
	s_nop 1
	v_cndmask_b32_e32 v5, v16, v5, vcc
	v_lshlrev_b32_e32 v5, 2, v5
	ds_bpermute_b32 v5, v5, v2
	v_cmp_eq_u32_e32 vcc, 63, v1
	s_waitcnt lgkmcnt(0)
	v_add_f32_e32 v5, v2, v5
	s_and_saveexec_b64 s[0:1], vcc
	s_lshl_b32 s9, s8, 2
	s_add_i32 s9, s72, s9
	v_mov_b32_e32 v7, s9
	ds_write_b32 v7, v5
	s_or_b64 exec, exec, s[0:1]
	v_cmp_gt_u32_e32 vcc, 32, v1
	s_cmp_lt_i32 s8, 1
	s_waitcnt lgkmcnt(0)
	v_cndmask_b32_e32 v1, v5, v2, vcc
	v_sub_f32_e32 v2, v1, v15
	s_barrier
	s_cbranch_scc1 .LBB0_394
	s_mov_b32 s0, s72

.LBB0_420:
	v_lshl_add_u32 v145, s46, 8, v1
	v_lshl_or_b32 v146, s49, 8, v143
	v_ashrrev_i32_e32 v147, 31, v146
	v_mov_b64_e32 v[148:149], s[8:9]
	s_movk_i32 s16, 0xc00
	v_cvt_pk_bf16_f32 v72, v72, v73
	v_cvt_pk_bf16_f32 v73, v74, v75
	v_cvt_pk_bf16_f32 v74, v68, v69
	v_add_u32_e32 v68, 0x80, v145
	v_mad_i64_i32 v[150:151], s[14:15], v145, s16, v[148:149]
	v_lshlrev_b64 v[146:147], 1, v[146:147]
	v_cvt_pk_bf16_f32 v112, v112, v113
	v_cvt_pk_bf16_f32 v113, v114, v115
	v_cvt_pk_bf16_f32 v114, v108, v109
	v_or_b32_e32 v108, 16, v145
	v_mad_i64_i32 v[68:69], s[14:15], v68, s16, v[148:149]
	v_cvt_pk_bf16_f32 v48, v48, v49
	v_cvt_pk_bf16_f32 v49, v50, v51
	v_cvt_pk_bf16_f32 v50, v44, v45
	v_add_u32_e32 v44, 0x90, v145
	v_lshl_add_u64 v[150:151], v[150:151], 0, v[146:147]
	v_cvt_pk_bf16_f32 v115, v110, v111
	v_mad_i64_i32 v[108:109], s[14:15], v108, s16, v[148:149]
	v_cvt_pk_bf16_f32 v96, v96, v97
	v_cvt_pk_bf16_f32 v97, v98, v99
	v_cvt_pk_bf16_f32 v98, v92, v93
	v_or_b32_e32 v92, 32, v145
	v_lshl_add_u64 v[68:69], v[68:69], 0, v[146:147]
	v_cvt_pk_bf16_f32 v51, v46, v47
	v_mad_i64_i32 v[44:45], s[14:15], v44, s16, v[148:149]
	v_cvt_pk_bf16_f32 v32, v32, v33
	v_cvt_pk_bf16_f32 v33, v34, v35
	v_cvt_pk_bf16_f32 v34, v28, v29
	v_add_u32_e32 v28, 0xa0, v145
	global_store_dwordx4 v[150:151], v[112:115], off offset:256
	v_cvt_pk_bf16_f32 v99, v94, v95
	v_mad_i64_i32 v[92:93], s[14:15], v92, s16, v[148:149]
	v_lshl_add_u64 v[112:113], v[108:109], 0, v[146:147]
	v_cvt_pk_bf16_f32 v80, v80, v81
	v_cvt_pk_bf16_f32 v81, v82, v83
	v_cvt_pk_bf16_f32 v82, v76, v77
	v_or_b32_e32 v76, 48, v145
	global_store_dwordx4 v[68:69], v[48:51], off offset:256
	v_cvt_pk_bf16_f32 v35, v30, v31
	v_mad_i64_i32 v[28:29], s[14:15], v28, s16, v[148:149]
	v_lshl_add_u64 v[48:49], v[44:45], 0, v[146:147]
	v_cvt_pk_bf16_f32 v16, v16, v17
	v_cvt_pk_bf16_f32 v17, v18, v19
	v_cvt_pk_bf16_f32 v18, v12, v13
	v_add_u32_e32 v12, 0xb0, v145
	global_store_dwordx4 v[112:113], v[96:99], off offset:256
	v_cvt_pk_bf16_f32 v83, v78, v79
	v_mad_i64_i32 v[76:77], s[14:15], v76, s16, v[148:149]
	v_lshl_add_u64 v[96:97], v[92:93], 0, v[146:147]
	global_store_dwordx4 v[48:49], v[32:35], off offset:256
	v_cvt_pk_bf16_f32 v19, v14, v15
	v_mad_i64_i32 v[12:13], s[14:15], v12, s16, v[148:149]
	v_lshl_add_u64 v[32:33], v[28:29], 0, v[146:147]
	v_cvt_pk_bf16_f32 v128, v128, v129
	v_cvt_pk_bf16_f32 v129, v130, v131
	v_cvt_pk_bf16_f32 v130, v124, v125
	v_cvt_pk_bf16_f32 v131, v126, v127
	v_cvt_pk_bf16_f32 v108, v120, v121
	v_cvt_pk_bf16_f32 v109, v122, v123
	v_cvt_pk_bf16_f32 v110, v116, v117
	v_cvt_pk_bf16_f32 v111, v118, v119
	v_cvt_pk_bf16_f32 v92, v104, v105
	v_cvt_pk_bf16_f32 v93, v106, v107
	v_cvt_pk_bf16_f32 v94, v100, v101
	v_cvt_pk_bf16_f32 v95, v102, v103
	global_store_dwordx4 v[96:97], v[80:83], off offset:256
	v_cvt_pk_bf16_f32 v78, v84, v85
	v_cvt_pk_bf16_f32 v79, v86, v87
	v_lshl_add_u64 v[80:81], v[76:77], 0, v[146:147]
	v_cvt_pk_bf16_f32 v76, v88, v89
	v_cvt_pk_bf16_f32 v77, v90, v91
	v_cvt_pk_bf16_f32 v75, v70, v71
	v_cvt_pk_bf16_f32 v64, v64, v65
	v_cvt_pk_bf16_f32 v65, v66, v67
	v_cvt_pk_bf16_f32 v66, v60, v61
	v_cvt_pk_bf16_f32 v67, v62, v63
	v_cvt_pk_bf16_f32 v44, v56, v57
	v_cvt_pk_bf16_f32 v45, v58, v59
	v_cvt_pk_bf16_f32 v46, v52, v53
	v_cvt_pk_bf16_f32 v47, v54, v55
	v_cvt_pk_bf16_f32 v28, v40, v41
	v_cvt_pk_bf16_f32 v29, v42, v43
	v_cvt_pk_bf16_f32 v30, v36, v37
	v_cvt_pk_bf16_f32 v31, v38, v39
	global_store_dwordx4 v[32:33], v[16:19], off offset:256
	v_cvt_pk_bf16_f32 v14, v20, v21
	v_cvt_pk_bf16_f32 v15, v22, v23
	v_lshl_add_u64 v[16:17], v[12:13], 0, v[146:147]
	v_cvt_pk_bf16_f32 v12, v24, v25
	v_cvt_pk_bf16_f32 v13, v26, v27
	v_cvt_pk_bf16_f32 v8, v8, v9
	v_cvt_pk_bf16_f32 v9, v10, v11
	v_cvt_pk_bf16_f32 v10, v4, v5
	v_cvt_pk_bf16_f32 v11, v6, v7
	s_and_b64 vcc, exec, s[0:1]
	s_mov_b64 s[0:1], -1
	s_movk_i32 s20, 0x110
	global_store_dwordx4 v[150:151], v[128:131], off
	global_store_dwordx4 v[112:113], v[108:111], off
	global_store_dwordx4 v[96:97], v[92:95], off
	global_store_dwordx4 v[80:81], v[76:79], off
	global_store_dwordx4 v[80:81], v[72:75], off offset:256
	global_store_dwordx4 v[68:69], v[64:67], off
	global_store_dwordx4 v[48:49], v[44:47], off
	global_store_dwordx4 v[32:33], v[28:31], off
	global_store_dwordx4 v[16:17], v[12:15], off
	global_store_dwordx4 v[16:17], v[8:11], off offset:256
	s_cbranch_vccnz .LBB0_409
	s_andn2_b64 vcc, exec, s[6:7]
	s_cbranch_vccnz .LBB0_408
	s_barrier
	s_branch .LBB0_408

.LBB0_483:
	s_waitcnt vmcnt(0) lgkmcnt(0)
	s_barrier
	s_and_saveexec_b64 s[6:7], s[36:37]
	s_cbranch_execz .LBB0_485
	v_mov_b64_e32 v[4:5], s[0:1]
	global_atomic_add v1, v[4:5], v228, off sc0
	v_mov_b32_e32 v2, s30
	s_waitcnt vmcnt(0) lgkmcnt(0)
	ds_write_b32 v2, v1
.LBB0_485:
	s_or_b64 exec, exec, s[6:7]
	v_mov_b32_e32 v1, s30
	s_waitcnt lgkmcnt(0)
	s_barrier
	ds_read_b32 v1, v1
	s_mov_b64 s[6:7], -1
	s_waitcnt lgkmcnt(0)
	v_cmp_lt_i32_e32 vcc, 15, v1
	v_readfirstlane_b32 s8, v1
	s_cbranch_vccnz .LBB0_482
	v_mov_b32_e32 v2, v0
	s_lshl_b32 s9, s8, 10
	v_readfirstlane_b32 s6, v2
	s_ashr_i32 s35, s6, 6
	v_readlane_b32 s6, v252, 0
	s_mov_b32 s7, s88
	s_and_b32 s26, s9, 0xfffff000
	s_lshl_b32 s9, s8, 7
	s_ashr_i32 s27, s26, 31
	s_and_b32 s38, s9, 0x180
	s_mov_b64 s[6:7], s[68:69]
	s_lshl_b64 s[10:11], s[26:27], 10
	s_lshl_b32 s9, s38, 1
	s_add_u32 s12, s6, s10
	s_addc_u32 s13, s7, s11
	s_add_u32 s9, s12, s9
	s_addc_u32 s12, s13, 0
	s_add_u32 s20, s9, 0x43a00000
	s_addc_u32 s21, s12, 0
	s_add_u32 s22, s9, 0x44a00000
	s_addc_u32 s23, s12, 0
	s_ashr_i32 s9, s8, 31
	s_lshl_b64 s[12:13], s[8:9], 19
	s_add_u32 s14, s6, s12
	s_addc_u32 s15, s7, s13
	s_add_u32 s18, s14, 0x46a00000
	s_addc_u32 s19, s15, 0
	s_lshl_b64 s[14:15], s[8:9], 20
	s_add_u32 s9, s6, s14
	s_addc_u32 s17, s7, s15
	s_add_u32 s16, s9, 0x45a00000
	s_addc_u32 s17, s17, 0
	s_cmp_lt_i32 s35, 4
	s_cselect_b64 s[24:25], -1, 0
	v_add_u32_e32 v4, 0xffffff00, v2
	v_lshlrev_b32_e32 v5, 4, v2
	v_ashrrev_i32_e32 v150, 4, v2
	v_add_u32_e32 v6, 0x100, v2
	v_add_u32_e32 v7, 0x200, v2
	s_and_b64 vcc, exec, s[24:25]
	v_lshrrev_b32_e32 v1, 3, v2
	v_and_b32_e32 v148, 0xf0, v5
	v_ashrrev_i32_e32 v152, 4, v4
	v_ashrrev_i32_e32 v151, 31, v150
	v_ashrrev_i32_e32 v154, 4, v6
	v_ashrrev_i32_e32 v156, 4, v7
	v_lshlrev_b32_e32 v158, 3, v4
	v_and_b32_e32 v212, 0x70, v5
	v_lshrrev_b32_e32 v211, 3, v4
	v_lshrrev_b32_e32 v210, 3, v6
	v_lshrrev_b32_e32 v201, 3, v7
	s_barrier
	s_cbranch_vccnz .LBB0_488
	v_mov_b32_e32 v149, v3
	v_ashrrev_i32_e32 v153, 31, v152
	v_lshl_add_u64 v[4:5], s[20:21], 0, v[148:149]
	v_lshlrev_b64 v[12:13], 10, v[152:153]
	v_lshl_add_u64 v[6:7], s[22:23], 0, v[148:149]
	v_lshl_add_u64 v[8:9], v[4:5], 0, v[12:13]
	global_load_dwordx4 v[8:11], v[8:9], off
	v_lshl_add_u64 v[12:13], v[6:7], 0, v[12:13]
	v_lshlrev_b64 v[20:21], 10, v[150:151]
	global_load_dwordx4 v[12:15], v[12:13], off
	v_lshl_add_u64 v[16:17], v[4:5], 0, v[20:21]
	v_ashrrev_i32_e32 v155, 31, v154
	global_load_dwordx4 v[16:19], v[16:17], off
	v_lshl_add_u64 v[20:21], v[6:7], 0, v[20:21]
	v_lshlrev_b64 v[28:29], 10, v[154:155]
	v_ashrrev_i32_e32 v157, 31, v156
	global_load_dwordx4 v[20:23], v[20:21], off
	v_lshl_add_u64 v[24:25], v[4:5], 0, v[28:29]
	v_lshlrev_b64 v[36:37], 10, v[156:157]
	global_load_dwordx4 v[24:27], v[24:25], off
	v_lshl_add_u64 v[28:29], v[6:7], 0, v[28:29]
	v_lshl_add_u64 v[4:5], v[4:5], 0, v[36:37]
	global_load_dwordx4 v[28:31], v[28:29], off
	v_ashrrev_i32_e32 v159, 31, v158
	global_load_dwordx4 v[32:35], v[4:5], off
	v_lshl_add_u64 v[4:5], v[6:7], 0, v[36:37]
	global_load_dwordx4 v[36:39], v[4:5], off
	v_lshlrev_b64 v[4:5], 1, v[158:159]
	v_lshl_add_u64 v[6:7], s[18:19], 0, v[4:5]
	v_lshl_add_u64 v[4:5], s[16:17], 0, v[4:5]
	global_load_dwordx4 v[40:43], v[6:7], off
	global_load_dwordx4 v[48:51], v[4:5], off
	v_add_u32_e32 v6, 0x800, v158
	v_ashrrev_i32_e32 v7, 31, v6
	v_lshlrev_b64 v[6:7], 1, v[6:7]
	v_lshl_add_u64 v[44:45], s[18:19], 0, v[6:7]
	v_lshl_add_u64 v[4:5], s[16:17], 0, v[6:7]
	global_load_dwordx4 v[44:47], v[44:45], off
	s_mov_b32 s9, s42
	global_load_dwordx4 v[52:55], v[4:5], off
	v_add_u32_e32 v4, 0x1000, v158
	v_ashrrev_i32_e32 v5, 31, v4
	v_lshl_add_u64 v[4:5], v[4:5], 1, s[16:17]
	global_load_dwordx4 v[56:59], v[4:5], off
	v_add_u32_e32 v4, 0x1800, v158
	v_ashrrev_i32_e32 v5, 31, v4
	v_lshl_add_u64 v[4:5], v[4:5], 1, s[16:17]
	global_load_dwordx4 v[4:7], v[4:5], off
	v_add_u32_e32 v60, s9, v148
	v_mad_u64_u32 v[62:63], s[28:29], v152, s57, v[60:61]
	s_waitcnt vmcnt(0) lgkmcnt(0)
	ds_write2_b64 v62, v[8:9], v[10:11] offset1:1
	v_add_u32_e32 v8, 0x4200, v62
	ds_write2_b64 v8, v[12:13], v[14:15] offset1:1
	v_mad_u64_u32 v[8:9], s[28:29], v150, s57, v[60:61]
	ds_write2_b64 v8, v[16:17], v[18:19] offset1:1
	v_add_u32_e32 v8, 0x4200, v8
	ds_write2_b64 v8, v[20:21], v[22:23] offset1:1
	v_mad_u64_u32 v[8:9], s[28:29], v154, s57, v[60:61]
	ds_write2_b64 v8, v[24:25], v[26:27] offset1:1
	v_add_u32_e32 v8, 0x4200, v8
	ds_write2_b64 v8, v[28:29], v[30:31] offset1:1
	v_mad_u64_u32 v[8:9], s[28:29], v156, s57, v[60:61]
	ds_write2_b64 v8, v[32:33], v[34:35] offset1:1
	v_add_u32_e32 v8, 0x4200, v8
	ds_write2_b64 v8, v[36:37], v[38:39] offset1:1
	v_add_u32_e32 v8, s9, v212
	s_movk_i32 s9, 0x88
	v_mad_u64_u32 v[10:11], s[28:29], v211, s9, v[8:9]
	v_add_u32_e32 v9, 0x8400, v10
	v_mad_u64_u32 v[12:13], s[28:29], v1, s9, v[8:9]
	ds_write2_b64 v9, v[40:41], v[42:43] offset1:1
	v_add_u32_e32 v9, 0x8400, v12
	ds_write2_b64 v9, v[44:45], v[46:47] offset1:1
	v_add_u32_e32 v9, 0xa600, v10
	ds_write2_b64 v9, v[48:49], v[50:51] offset1:1
	v_add_u32_e32 v9, 0xa600, v12
	ds_write2_b64 v9, v[52:53], v[54:55] offset1:1
	v_mul_lo_u32 v9, v210, s9
	v_add3_u32 v9, v8, v9, s58
	ds_write2_b64 v9, v[56:57], v[58:59] offset1:1
	v_mul_lo_u32 v9, v201, s9
	v_add3_u32 v8, v8, v9, s58
	ds_write2_b64 v8, v[4:5], v[6:7] offset1:1
.LBB0_488:
	s_mov_b64 s[28:29], -1
	s_and_b64 vcc, exec, s[24:25]
	s_waitcnt lgkmcnt(0)
	s_barrier
	s_cbranch_vccz .LBB0_492
	s_lshl_b64 s[24:25], s[26:27], 9
	s_lshl_b64 s[24:25], s[24:25], 2
	v_and_b32_e32 v18, 31, v2
	s_add_u32 s28, s6, s24
	s_addc_u32 s29, s7, s25
	s_lshl_b32 s9, s38, 2
	v_lshl_or_b32 v160, s35, 5, v18
	s_add_u32 s38, s28, s9
	v_ashrrev_i32_e32 v161, 31, v160
	v_bfe_u32 v19, v2, 5, 1
	s_addc_u32 s39, s29, 0
	v_lshlrev_b64 v[4:5], 2, v[160:161]
	v_lshl_add_u64 v[6:7], s[38:39], 0, v[4:5]
	v_lshlrev_b32_e32 v2, 13, v19
	v_lshl_add_u64 v[6:7], v[6:7], 0, v[2:3]
	s_mov_b32 s35, 0x41a00000
	v_add_co_u32_e32 v10, vcc, s35, v6
	s_mov_b64 s[38:39], 0x41a00000
	s_nop 0
	v_addc_co_u32_e32 v11, vcc, 0, v7, vcc
	v_add_co_u32_e32 v12, vcc, s43, v6
	v_lshl_add_u64 v[8:9], v[6:7], 0, s[38:39]
	s_nop 0
	v_addc_co_u32_e32 v13, vcc, 0, v7, vcc
	v_add_co_u32_e32 v14, vcc, s44, v6
	s_mov_b32 s35, 0x41a1d000
	s_nop 0
	v_addc_co_u32_e32 v15, vcc, 0, v7, vcc
	v_add_co_u32_e32 v16, vcc, s45, v6
	s_lshl_b32 s28, s8, 6
	s_nop 0
	v_addc_co_u32_e32 v17, vcc, 0, v7, vcc
	global_load_dword v166, v[10:11], off
	global_load_dword v164, v[12:13], off
	global_load_dword v165, v[12:13], off offset:2048
	global_load_dword v168, v[14:15], off
	global_load_dword v169, v[14:15], off offset:2048
	global_load_dword v170, v[16:17], off
	global_load_dword v171, v[16:17], off offset:2048
	global_load_dword v167, v[8:9], off offset:2048
	v_add_co_u32_e32 v8, vcc, s46, v6
	s_ashr_i32 s29, s28, 31
	s_nop 0
	v_addc_co_u32_e32 v9, vcc, 0, v7, vcc
	v_add_co_u32_e32 v10, vcc, s47, v6
	s_lshl_b64 s[28:29], s[28:29], 2
	s_nop 0
	v_addc_co_u32_e32 v11, vcc, 0, v7, vcc
	v_add_co_u32_e32 v12, vcc, s48, v6
	s_add_u32 s40, s6, s28
	s_nop 0
	v_addc_co_u32_e32 v13, vcc, 0, v7, vcc
	v_add_co_u32_e32 v14, vcc, s49, v6
	s_addc_u32 s41, s7, s29
	s_nop 0
	v_addc_co_u32_e32 v15, vcc, 0, v7, vcc
	global_load_dword v180, v[8:9], off
	global_load_dword v181, v[8:9], off offset:2048
	global_load_dword v194, v[10:11], off
	global_load_dword v195, v[10:11], off offset:2048
	global_load_dword v196, v[12:13], off
	global_load_dword v197, v[12:13], off offset:2048
	global_load_dword v198, v[14:15], off
	global_load_dword v199, v[14:15], off offset:2048
	v_add_co_u32_e32 v8, vcc, s50, v6
	s_add_u32 s28, s28, 0x49250004
	s_nop 0
	v_addc_co_u32_e32 v9, vcc, 0, v7, vcc
	v_add_co_u32_e32 v10, vcc, s51, v6
	s_addc_u32 s29, s29, 0
	s_nop 0
	v_addc_co_u32_e32 v11, vcc, 0, v7, vcc
	v_add_co_u32_e32 v12, vcc, s52, v6
	s_lshl_b64 s[26:27], s[26:27], 11
	s_nop 0
	v_addc_co_u32_e32 v13, vcc, 0, v7, vcc
	v_add_co_u32_e32 v14, vcc, s53, v6
	v_lshlrev_b32_e32 v149, 3, v19
	s_nop 0
	v_addc_co_u32_e32 v15, vcc, 0, v7, vcc
	global_load_dword v172, v[8:9], off
	global_load_dword v173, v[8:9], off offset:2048
	global_load_dword v174, v[10:11], off
	global_load_dword v175, v[10:11], off offset:2048
	global_load_dword v176, v[12:13], off
	global_load_dword v177, v[12:13], off offset:2048
	global_load_dword v178, v[14:15], off
	global_load_dword v179, v[14:15], off offset:2048
	v_add_co_u32_e32 v8, vcc, s54, v6
	v_mul_u32_u24_e32 v155, 0x108, v18
	s_nop 0
	v_addc_co_u32_e32 v9, vcc, 0, v7, vcc
	v_add_co_u32_e32 v10, vcc, s55, v6
	v_mul_u32_u24_e32 v153, 0x88, v18
	s_nop 0
	v_addc_co_u32_e32 v11, vcc, 0, v7, vcc
	v_add_co_u32_e32 v12, vcc, s56, v6
	v_add_u32_e32 v157, s42, v149
	s_nop 0
	v_addc_co_u32_e32 v13, vcc, 0, v7, vcc
	v_add_co_u32_e32 v6, vcc, s35, v6
	s_mov_b32 s35, 0x49250000
	s_nop 0
	v_addc_co_u32_e32 v7, vcc, 0, v7, vcc
	global_load_dword v202, v[8:9], off
	global_load_dword v203, v[8:9], off offset:2048
	global_load_dword v204, v[10:11], off
	global_load_dword v205, v[10:11], off offset:2048
	global_load_dword v206, v[12:13], off
	global_load_dword v207, v[12:13], off offset:2048
	global_load_dword v208, v[6:7], off
	global_load_dword v209, v[6:7], off offset:2048
	v_mov_b32_e32 v6, s40
	v_mov_b32_e32 v7, s41
	v_add_co_u32_e32 v6, vcc, s35, v6
	s_mov_b32 s35, 0
	s_nop 0
	v_addc_co_u32_e32 v7, vcc, 0, v7, vcc
	global_load_dword v200, v[6:7], off
	v_lshl_add_u64 v[6:7], v[2:3], 0, s[26:27]
	s_and_b32 s26, s8, 3
	v_lshl_or_b32 v6, s26, 9, v6
	v_lshl_add_u64 v[162:163], v[6:7], 0, v[4:5]
	v_mov_b32_e32 v4, 0
	v_mov_b32_e32 v5, v4
	v_mov_b32_e32 v6, v4
	v_mov_b32_e32 v7, v4
	v_mov_b32_e32 v8, v4
	v_mov_b32_e32 v9, v4
	v_mov_b32_e32 v10, v4
	v_mov_b32_e32 v11, v4
	v_mov_b32_e32 v12, v4
	v_mov_b32_e32 v13, v4
	v_mov_b32_e32 v14, v4
	v_mov_b32_e32 v15, v4
	v_mov_b32_e32 v16, v4
	v_mov_b32_e32 v17, v4
	v_mov_b32_e32 v18, v4
	v_mov_b32_e32 v19, v4
	v_mov_b32_e32 v20, v4
	v_mov_b32_e32 v21, v4
	v_mov_b32_e32 v22, v4
	v_mov_b32_e32 v23, v4
	v_mov_b32_e32 v24, v4
	v_mov_b32_e32 v25, v4
	v_mov_b32_e32 v26, v4
	v_mov_b32_e32 v27, v4
	v_mov_b32_e32 v28, v4
	v_mov_b32_e32 v29, v4
	v_mov_b32_e32 v30, v4
	v_mov_b32_e32 v31, v4
	v_mov_b32_e32 v32, v4
	v_mov_b32_e32 v33, v4
	v_mov_b32_e32 v34, v4
	v_mov_b32_e32 v35, v4
	v_mov_b32_e32 v36, v4
	v_mov_b32_e32 v37, v4
	v_mov_b32_e32 v38, v4
	v_mov_b32_e32 v39, v4
	v_mov_b32_e32 v40, v4
	v_mov_b32_e32 v41, v4
	v_mov_b32_e32 v42, v4
	v_mov_b32_e32 v43, v4
	v_mov_b32_e32 v44, v4
	v_mov_b32_e32 v45, v4
	v_mov_b32_e32 v46, v4
	v_mov_b32_e32 v47, v4
	v_mov_b32_e32 v48, v4
	v_mov_b32_e32 v49, v4
	v_mov_b32_e32 v50, v4
	v_mov_b32_e32 v51, v4
	v_mov_b32_e32 v52, v4
	v_mov_b32_e32 v53, v4
	v_mov_b32_e32 v54, v4
	v_mov_b32_e32 v55, v4
	v_mov_b32_e32 v56, v4
	v_mov_b32_e32 v57, v4
	v_mov_b32_e32 v58, v4
	v_mov_b32_e32 v59, v4
	v_mov_b32_e32 v60, v4
	v_mov_b32_e32 v61, v4
	v_mov_b32_e32 v62, v4
	v_mov_b32_e32 v63, v4
	v_mov_b32_e32 v64, v4
	v_mov_b32_e32 v65, v4
	v_mov_b32_e32 v66, v4
	v_mov_b32_e32 v67, v4
	s_mov_b64 s[38:39], 0x20000
.LBB0_490:
	s_bitcmp1_b32 s35, 0
	s_cselect_b32 s26, 0xea00, 0
	v_add_u32_e32 v159, s26, v157
	v_add_u32_e32 v190, v159, v155
	ds_read2_b64 v[68:71], v190 offset1:2
	ds_read2_b64 v[84:87], v190 offset0:4 offset1:6
	ds_read2_b64 v[88:91], v190 offset0:8 offset1:10
	ds_read2_b64 v[92:95], v190 offset0:12 offset1:14
	ds_read2_b64 v[96:99], v190 offset0:16 offset1:18
	ds_read2_b64 v[100:103], v190 offset0:20 offset1:22
	ds_read2_b64 v[104:107], v190 offset0:24 offset1:26
	ds_read2_b64 v[108:111], v190 offset0:28 offset1:30
	v_cvt_pk_bf16_f32 v116, v52, v53
	v_cvt_pk_bf16_f32 v117, v54, v55
	v_cvt_pk_bf16_f32 v118, v56, v57
	v_cvt_pk_bf16_f32 v119, v58, v59
	v_cvt_pk_bf16_f32 v120, v60, v61
	v_cvt_pk_bf16_f32 v121, v62, v63
	v_cvt_pk_bf16_f32 v122, v64, v65
	v_cvt_pk_bf16_f32 v123, v66, v67
	v_cvt_pk_bf16_f32 v124, v36, v37
	v_cvt_pk_bf16_f32 v125, v38, v39
	v_cvt_pk_bf16_f32 v126, v40, v41
	v_cvt_pk_bf16_f32 v127, v42, v43
	v_cvt_pk_bf16_f32 v128, v44, v45
	v_cvt_pk_bf16_f32 v129, v46, v47
	v_cvt_pk_bf16_f32 v130, v48, v49
	v_cvt_pk_bf16_f32 v131, v50, v51
	v_cvt_pk_bf16_f32 v132, v20, v21
	v_cvt_pk_bf16_f32 v133, v22, v23
	v_cvt_pk_bf16_f32 v134, v24, v25
	v_cvt_pk_bf16_f32 v135, v26, v27
	v_cvt_pk_bf16_f32 v136, v28, v29
	v_cvt_pk_bf16_f32 v137, v30, v31
	v_cvt_pk_bf16_f32 v138, v32, v33
	v_cvt_pk_bf16_f32 v139, v34, v35
	v_cvt_pk_bf16_f32 v140, v4, v5
	v_cvt_pk_bf16_f32 v141, v6, v7
	v_cvt_pk_bf16_f32 v142, v8, v9
	v_cvt_pk_bf16_f32 v143, v10, v11
	v_cvt_pk_bf16_f32 v144, v12, v13
	v_cvt_pk_bf16_f32 v145, v14, v15
	v_cvt_pk_bf16_f32 v146, v16, v17
	v_cvt_pk_bf16_f32 v147, v18, v19
	s_waitcnt lgkmcnt(0)
	v_mfma_f32_32x32x16_bf16 v[68:83], v[68:71], v[116:119], 0
	v_mfma_f32_32x32x16_bf16 v[68:83], v[84:87], v[120:123], v[68:83]
	v_mfma_f32_32x32x16_bf16 v[68:83], v[88:91], v[124:127], v[68:83]
	v_mfma_f32_32x32x16_bf16 v[68:83], v[92:95], v[128:131], v[68:83]
	v_mfma_f32_32x32x16_bf16 v[68:83], v[96:99], v[132:135], v[68:83]
	v_mfma_f32_32x32x16_bf16 v[68:83], v[100:103], v[136:139], v[68:83]
	v_mfma_f32_32x32x16_bf16 v[68:83], v[104:107], v[140:143], v[68:83]
	v_mfma_f32_32x32x16_bf16 v[68:83], v[108:111], v[144:147], v[68:83]
	v_add_u32_e32 v88, 0x2000, v190
	ds_read2_b64 v[84:87], v88 offset0:32 offset1:34
	ds_read2_b64 v[100:103], v88 offset0:36 offset1:38
	ds_read2_b64 v[104:107], v88 offset0:40 offset1:42
	ds_read2_b64 v[108:111], v88 offset0:44 offset1:46
	ds_read2_b64 v[112:115], v88 offset0:48 offset1:50
	ds_read2_b64 v[182:185], v88 offset0:52 offset1:54
	ds_read2_b64 v[186:189], v88 offset0:56 offset1:58
	ds_read2_b64 v[214:217], v88 offset0:60 offset1:62
	s_waitcnt lgkmcnt(0)
	v_mfma_f32_32x32x16_bf16 v[84:99], v[84:87], v[116:119], 0
	v_mfma_f32_32x32x16_bf16 v[84:99], v[100:103], v[120:123], v[84:99]
	v_mfma_f32_32x32x16_bf16 v[84:99], v[104:107], v[124:127], v[84:99]
	v_mfma_f32_32x32x16_bf16 v[84:99], v[108:111], v[128:131], v[84:99]
	v_mfma_f32_32x32x16_bf16 v[84:99], v[112:115], v[132:135], v[84:99]
	v_mfma_f32_32x32x16_bf16 v[84:99], v[182:185], v[136:139], v[84:99]
	v_mfma_f32_32x32x16_bf16 v[84:99], v[186:189], v[140:143], v[84:99]
	v_mfma_f32_32x32x16_bf16 v[84:99], v[214:217], v[144:147], v[84:99]
	s_waitcnt vmcnt(0)
	v_sub_f32_e32 v81, v197, v81
	v_sub_f32_e32 v80, v196, v80
	v_sub_f32_e32 v71, v165, v71
	v_sub_f32_e32 v70, v164, v70
	v_sub_f32_e32 v69, v167, v69
	v_sub_f32_e32 v68, v166, v68
	v_cvt_pk_bf16_f32 v106, v80, v81
	s_nop 3
	v_sub_f32_e32 v80, v175, v87
	v_sub_f32_e32 v81, v174, v86
	v_sub_f32_e32 v83, v199, v83
	v_sub_f32_e32 v82, v198, v82
	v_sub_f32_e32 v79, v195, v79
	v_sub_f32_e32 v78, v194, v78
	v_sub_f32_e32 v77, v181, v77
	v_sub_f32_e32 v76, v180, v76
	v_sub_f32_e32 v75, v171, v75
	v_sub_f32_e32 v74, v170, v74
	v_sub_f32_e32 v73, v169, v73
	v_sub_f32_e32 v72, v168, v72
	v_cvt_pk_bf16_f32 v100, v68, v69
	v_cvt_pk_bf16_f32 v101, v70, v71
	v_sub_f32_e32 v68, v179, v91
	v_sub_f32_e32 v69, v178, v90
	v_sub_f32_e32 v70, v177, v89
	v_sub_f32_e32 v71, v176, v88
	v_cvt_pk_bf16_f32 v109, v81, v80
	v_add_u32_e32 v80, 0x4000, v190
	v_cvt_pk_bf16_f32 v102, v72, v73
	v_cvt_pk_bf16_f32 v103, v74, v75
	v_cvt_pk_bf16_f32 v104, v76, v77
	v_cvt_pk_bf16_f32 v105, v78, v79
	v_cvt_pk_bf16_f32 v107, v82, v83
	v_sub_f32_e32 v72, v209, v99
	v_sub_f32_e32 v73, v208, v98
	v_sub_f32_e32 v74, v207, v97
	v_sub_f32_e32 v75, v206, v96
	v_sub_f32_e32 v76, v205, v95
	v_sub_f32_e32 v77, v204, v94
	v_sub_f32_e32 v78, v203, v93
	v_sub_f32_e32 v79, v202, v92
	v_sub_f32_e32 v82, v173, v85
	v_sub_f32_e32 v83, v172, v84
	v_cvt_pk_bf16_f32 v110, v71, v70
	v_cvt_pk_bf16_f32 v111, v69, v68
	ds_read2_b64 v[68:71], v80 offset0:64 offset1:66
	ds_read2_b64 v[84:87], v80 offset0:68 offset1:70
	ds_read2_b64 v[88:91], v80 offset0:72 offset1:74
	ds_read2_b64 v[92:95], v80 offset0:76 offset1:78
	ds_read2_b64 v[96:99], v80 offset0:80 offset1:82
	ds_read2_b64 v[164:167], v80 offset0:84 offset1:86
	ds_read2_b64 v[168:171], v80 offset0:88 offset1:90
	ds_read2_b64 v[172:175], v80 offset0:92 offset1:94
	v_cvt_pk_bf16_f32 v108, v83, v82
	v_cvt_pk_bf16_f32 v112, v79, v78
	v_cvt_pk_bf16_f32 v113, v77, v76
	v_cvt_pk_bf16_f32 v114, v75, v74
	v_cvt_pk_bf16_f32 v115, v73, v72
	s_waitcnt lgkmcnt(7)
	v_mfma_f32_32x32x16_bf16 v[68:83], v[68:71], v[116:119], 0
	s_waitcnt lgkmcnt(6)
	v_mfma_f32_32x32x16_bf16 v[68:83], v[84:87], v[120:123], v[68:83]
	s_waitcnt lgkmcnt(5)
	v_mfma_f32_32x32x16_bf16 v[68:83], v[88:91], v[124:127], v[68:83]
	s_waitcnt lgkmcnt(4)
	v_mfma_f32_32x32x16_bf16 v[68:83], v[92:95], v[128:131], v[68:83]
	s_waitcnt lgkmcnt(3)
	v_mfma_f32_32x32x16_bf16 v[68:83], v[96:99], v[132:135], v[68:83]
	s_waitcnt lgkmcnt(2)
	v_mfma_f32_32x32x16_bf16 v[68:83], v[164:167], v[136:139], v[68:83]
	s_waitcnt lgkmcnt(1)
	v_mfma_f32_32x32x16_bf16 v[68:83], v[168:171], v[140:143], v[68:83]
	s_waitcnt lgkmcnt(0)
	v_mfma_f32_32x32x16_bf16 v[68:83], v[172:175], v[144:147], v[68:83]
	v_add_u32_e32 v88, 0x6000, v190
	ds_read2_b64 v[84:87], v88 offset0:96 offset1:98
	ds_read2_b64 v[164:167], v88 offset0:100 offset1:102
	ds_read2_b64 v[168:171], v88 offset0:104 offset1:106
	ds_read2_b64 v[172:175], v88 offset0:108 offset1:110
	ds_read2_b64 v[176:179], v88 offset0:112 offset1:114
	ds_read2_b64 v[180:183], v88 offset0:116 offset1:118
	ds_read2_b64 v[184:187], v88 offset0:120 offset1:122
	ds_read2_b64 v[194:197], v88 offset0:124 offset1:126
	s_waitcnt lgkmcnt(7)
	v_mfma_f32_32x32x16_bf16 v[84:99], v[84:87], v[116:119], 0
	s_waitcnt lgkmcnt(6)
	v_mfma_f32_32x32x16_bf16 v[84:99], v[164:167], v[120:123], v[84:99]
	s_waitcnt lgkmcnt(5)
	v_mfma_f32_32x32x16_bf16 v[84:99], v[168:171], v[124:127], v[84:99]
	s_waitcnt lgkmcnt(4)
	v_mfma_f32_32x32x16_bf16 v[84:99], v[172:175], v[128:131], v[84:99]
	s_waitcnt lgkmcnt(3)
	v_mfma_f32_32x32x16_bf16 v[84:99], v[176:179], v[132:135], v[84:99]
	s_waitcnt lgkmcnt(2)
	v_mfma_f32_32x32x16_bf16 v[84:99], v[180:183], v[136:139], v[84:99]
	s_waitcnt lgkmcnt(1)
	v_mfma_f32_32x32x16_bf16 v[84:99], v[184:187], v[140:143], v[84:99]
	s_waitcnt lgkmcnt(0)
	v_mfma_f32_32x32x16_bf16 v[84:99], v[194:197], v[144:147], v[84:99]
	v_add_u32_e32 v159, v159, v153
	v_add_u32_e32 v128, 0x8000, v159
	v_add_u32_e32 v144, 0x9000, v159
	ds_read2_b64 v[116:119], v128 offset0:128 offset1:130
	ds_read2_b64 v[120:123], v128 offset0:132 offset1:134
	ds_read2_b64 v[124:127], v128 offset0:136 offset1:138
	ds_read2_b64 v[128:131], v128 offset0:140 offset1:142
	ds_read2_b64 v[132:135], v144 offset0:160 offset1:162
	ds_read2_b64 v[136:139], v144 offset0:164 offset1:166
	ds_read2_b64 v[140:143], v144 offset0:168 offset1:170
	ds_read2_b64 v[144:147], v144 offset0:172 offset1:174
	s_waitcnt lgkmcnt(7)
	v_mfma_f32_32x32x16_bf16 v[68:83], v[116:119], v[100:103], v[68:83]
	s_waitcnt lgkmcnt(3)
	v_mfma_f32_32x32x16_bf16 v[84:99], v[132:135], v[100:103], v[84:99]
	v_mfma_f32_32x32x16_bf16 v[68:83], v[120:123], v[104:107], v[68:83]
	s_waitcnt lgkmcnt(2)
	v_mfma_f32_32x32x16_bf16 v[84:99], v[136:139], v[104:107], v[84:99]
	v_mfma_f32_32x32x16_bf16 v[68:83], v[124:127], v[108:111], v[68:83]
	s_waitcnt lgkmcnt(1)
	v_mfma_f32_32x32x16_bf16 v[84:99], v[140:143], v[108:111], v[84:99]
	v_mfma_f32_32x32x16_bf16 v[68:83], v[128:131], v[112:115], v[68:83]
	s_waitcnt lgkmcnt(0)
	v_mfma_f32_32x32x16_bf16 v[84:99], v[144:147], v[112:115], v[84:99]
	v_lshl_add_u64 v[116:117], s[6:7], 0, v[162:163]
	s_mov_b32 s26, 0x47200000
	v_add_co_u32_e32 v118, vcc, s26, v116
	s_mov_b32 s26, 0x47201000
	s_nop 0
	v_addc_co_u32_e32 v119, vcc, 0, v117, vcc
	s_nop 3
	global_store_dword v[118:119], v68, off
	global_store_dword v[118:119], v69, off offset:2048
	v_add_co_u32_e32 v68, vcc, s26, v116
	s_mov_b32 s26, 0x47204000
	s_nop 0
	v_addc_co_u32_e32 v69, vcc, 0, v117, vcc
	global_store_dword v[68:69], v70, off
	global_store_dword v[68:69], v71, off offset:2048
	v_add_co_u32_e32 v68, vcc, s26, v116
	s_mov_b32 s26, 0x47205000
	s_nop 0
	v_addc_co_u32_e32 v69, vcc, 0, v117, vcc
	global_store_dword v[68:69], v72, off
	global_store_dword v[68:69], v73, off offset:2048
	v_add_co_u32_e32 v68, vcc, s26, v116
	s_mov_b32 s26, 0x47208000
	s_nop 0
	v_addc_co_u32_e32 v69, vcc, 0, v117, vcc
	global_store_dword v[68:69], v74, off
	global_store_dword v[68:69], v75, off offset:2048
	v_add_co_u32_e32 v68, vcc, s26, v116
	s_mov_b32 s26, 0x47209000
	s_nop 0
	v_addc_co_u32_e32 v69, vcc, 0, v117, vcc
	global_store_dword v[68:69], v76, off
	global_store_dword v[68:69], v77, off offset:2048
	v_add_co_u32_e32 v68, vcc, s26, v116
	s_mov_b32 s26, 0x4720c000
	s_nop 0
	v_addc_co_u32_e32 v69, vcc, 0, v117, vcc
	global_store_dword v[68:69], v78, off
	global_store_dword v[68:69], v79, off offset:2048
	v_add_co_u32_e32 v68, vcc, s26, v116
	s_mov_b32 s26, 0x4720d000
	s_nop 0
	v_addc_co_u32_e32 v69, vcc, 0, v117, vcc
	global_store_dword v[68:69], v80, off
	global_store_dword v[68:69], v81, off offset:2048
	v_add_co_u32_e32 v68, vcc, s26, v116
	s_mov_b32 s26, 0x47210000
	s_nop 0
	v_addc_co_u32_e32 v69, vcc, 0, v117, vcc
	global_store_dword v[68:69], v82, off
	global_store_dword v[68:69], v83, off offset:2048
	v_add_co_u32_e32 v68, vcc, s26, v116
	s_mov_b32 s26, 0x47211000
	s_nop 0
	v_addc_co_u32_e32 v69, vcc, 0, v117, vcc
	global_store_dword v[68:69], v84, off
	global_store_dword v[68:69], v85, off offset:2048
	v_add_co_u32_e32 v68, vcc, s26, v116
	s_mov_b32 s26, 0x47214000
	s_nop 0
	v_addc_co_u32_e32 v69, vcc, 0, v117, vcc
	global_store_dword v[68:69], v86, off
	global_store_dword v[68:69], v87, off offset:2048
	v_add_co_u32_e32 v68, vcc, s26, v116
	s_mov_b32 s26, 0x47215000
	s_nop 0
	v_addc_co_u32_e32 v69, vcc, 0, v117, vcc
	global_store_dword v[68:69], v88, off
	global_store_dword v[68:69], v89, off offset:2048
	v_add_co_u32_e32 v68, vcc, s26, v116
	s_mov_b32 s26, 0x47218000
	s_nop 0
	v_addc_co_u32_e32 v69, vcc, 0, v117, vcc
	global_store_dword v[68:69], v90, off
	global_store_dword v[68:69], v91, off offset:2048
	v_add_co_u32_e32 v68, vcc, s26, v116
	s_mov_b32 s26, 0x47219000
	s_nop 0
	v_addc_co_u32_e32 v69, vcc, 0, v117, vcc
	global_store_dword v[68:69], v92, off
	global_store_dword v[68:69], v93, off offset:2048
	v_add_co_u32_e32 v68, vcc, s26, v116
	s_mov_b32 s26, 0x4721c000
	s_nop 0
	v_addc_co_u32_e32 v69, vcc, 0, v117, vcc
	global_store_dword v[68:69], v94, off
	global_store_dword v[68:69], v95, off offset:2048
	v_add_co_u32_e32 v68, vcc, s26, v116
	s_mov_b32 s26, 0x4721d000
	s_nop 0
	v_addc_co_u32_e32 v69, vcc, 0, v117, vcc
	global_store_dword v[68:69], v96, off
	global_store_dword v[68:69], v97, off offset:2048
	v_add_co_u32_e32 v68, vcc, s26, v116
	s_mov_b32 s26, 0x41a20000
	s_nop 0
	v_addc_co_u32_e32 v69, vcc, 0, v117, vcc
	global_store_dword v[68:69], v98, off
	global_store_dword v[68:69], v99, off offset:2048
	v_add_co_u32_e32 v68, vcc, s26, v116
	s_mov_b32 s26, 0x41a21000
	s_nop 0
	v_addc_co_u32_e32 v69, vcc, 0, v117, vcc
	v_add_co_u32_e32 v70, vcc, s26, v116
	s_mov_b32 s26, 0x41a24000
	s_nop 0
	v_addc_co_u32_e32 v71, vcc, 0, v117, vcc
	v_add_co_u32_e32 v72, vcc, s26, v116
	s_mov_b32 s26, 0x41a25000
	s_nop 0
	v_addc_co_u32_e32 v73, vcc, 0, v117, vcc
	v_add_co_u32_e32 v74, vcc, s26, v116
	s_mov_b32 s26, 0x41a28000
	s_nop 0
	v_addc_co_u32_e32 v75, vcc, 0, v117, vcc
	global_load_dword v166, v[68:69], off
	global_load_dword v167, v[68:69], off offset:2048
	global_load_dword v164, v[70:71], off
	global_load_dword v165, v[70:71], off offset:2048
	global_load_dword v168, v[72:73], off
	global_load_dword v169, v[72:73], off offset:2048
	global_load_dword v170, v[74:75], off
	global_load_dword v171, v[74:75], off offset:2048
	v_add_co_u32_e32 v68, vcc, s26, v116
	s_mov_b32 s26, 0x41a29000
	s_nop 0
	v_addc_co_u32_e32 v69, vcc, 0, v117, vcc
	v_add_co_u32_e32 v70, vcc, s26, v116
	s_mov_b32 s26, 0x41a2c000
	s_nop 0
	v_addc_co_u32_e32 v71, vcc, 0, v117, vcc
	v_add_co_u32_e32 v72, vcc, s26, v116
	s_mov_b32 s26, 0x41a2d000
	s_nop 0
	v_addc_co_u32_e32 v73, vcc, 0, v117, vcc
	v_add_co_u32_e32 v74, vcc, s26, v116
	s_mov_b32 s26, 0x41a30000
	s_nop 0
	v_addc_co_u32_e32 v75, vcc, 0, v117, vcc
	global_load_dword v180, v[68:69], off
	global_load_dword v181, v[68:69], off offset:2048
	global_load_dword v194, v[70:71], off
	global_load_dword v195, v[70:71], off offset:2048
	global_load_dword v196, v[72:73], off
	global_load_dword v197, v[72:73], off offset:2048
	global_load_dword v198, v[74:75], off
	global_load_dword v199, v[74:75], off offset:2048
	v_add_co_u32_e32 v68, vcc, s26, v116
	s_mov_b32 s26, 0x41a31000
	s_nop 0
	v_addc_co_u32_e32 v69, vcc, 0, v117, vcc
	v_add_co_u32_e32 v70, vcc, s26, v116
	s_mov_b32 s26, 0x41a34000
	s_nop 0
	v_addc_co_u32_e32 v71, vcc, 0, v117, vcc
	v_add_co_u32_e32 v72, vcc, s26, v116
	s_mov_b32 s26, 0x41a35000
	s_nop 0
	v_addc_co_u32_e32 v73, vcc, 0, v117, vcc
	v_add_co_u32_e32 v74, vcc, s26, v116
	s_mov_b32 s26, 0x41a38000
	s_nop 0
	v_addc_co_u32_e32 v75, vcc, 0, v117, vcc
	global_load_dword v172, v[68:69], off
	global_load_dword v173, v[68:69], off offset:2048
	global_load_dword v174, v[70:71], off
	global_load_dword v175, v[70:71], off offset:2048
	global_load_dword v176, v[72:73], off
	global_load_dword v177, v[72:73], off offset:2048
	global_load_dword v178, v[74:75], off
	global_load_dword v179, v[74:75], off offset:2048
	v_add_co_u32_e32 v68, vcc, s26, v116
	s_mov_b32 s26, 0x41a39000
	s_nop 0
	v_addc_co_u32_e32 v69, vcc, 0, v117, vcc
	v_add_co_u32_e32 v70, vcc, s26, v116
	s_mov_b32 s26, 0x41a3c000
	s_nop 0
	v_addc_co_u32_e32 v71, vcc, 0, v117, vcc
	v_add_co_u32_e32 v72, vcc, s26, v116
	s_mov_b32 s26, 0x41a3d000
	s_nop 0
	v_addc_co_u32_e32 v73, vcc, 0, v117, vcc
	v_add_co_u32_e32 v74, vcc, s26, v116
	s_add_i32 s35, s35, 1
	s_nop 0
	v_addc_co_u32_e32 v75, vcc, 0, v117, vcc
	global_load_dword v202, v[68:69], off
	global_load_dword v203, v[68:69], off offset:2048
	global_load_dword v204, v[70:71], off
	global_load_dword v205, v[70:71], off offset:2048
	global_load_dword v206, v[72:73], off
	global_load_dword v207, v[72:73], off offset:2048
	global_load_dword v208, v[74:75], off
	global_load_dword v209, v[74:75], off offset:2048
	s_add_u32 s26, s6, s28
	s_addc_u32 s27, s7, s29
	v_mov_b64_e32 v[68:69], s[26:27]
	global_load_dword v116, v[68:69], off
	v_add_u32_e32 v80, 0xa000, v159
	v_add_u32_e32 v96, 0xb000, v159
	ds_read2_b64 v[68:71], v80 offset0:192 offset1:194
	ds_read2_b64 v[72:75], v80 offset0:196 offset1:198
	ds_read2_b64 v[76:79], v80 offset0:200 offset1:202
	ds_read2_b64 v[80:83], v80 offset0:204 offset1:206
	ds_read2_b64 v[84:87], v96 offset0:224 offset1:226
	ds_read2_b64 v[88:91], v96 offset0:228 offset1:230
	ds_read2_b64 v[92:95], v96 offset0:232 offset1:234
	ds_read2_b64 v[96:99], v96 offset0:236 offset1:238
	v_pk_mul_f32 v[66:67], v[66:67], v[200:201] op_sel_hi:[1,0]
	v_pk_mul_f32 v[64:65], v[64:65], v[200:201] op_sel_hi:[1,0]
	v_pk_mul_f32 v[62:63], v[62:63], v[200:201] op_sel_hi:[1,0]
	v_pk_mul_f32 v[60:61], v[60:61], v[200:201] op_sel_hi:[1,0]
	v_pk_mul_f32 v[58:59], v[58:59], v[200:201] op_sel_hi:[1,0]
	v_pk_mul_f32 v[56:57], v[56:57], v[200:201] op_sel_hi:[1,0]
	v_pk_mul_f32 v[54:55], v[54:55], v[200:201] op_sel_hi:[1,0]
	v_pk_mul_f32 v[52:53], v[52:53], v[200:201] op_sel_hi:[1,0]
	v_pk_mul_f32 v[50:51], v[50:51], v[200:201] op_sel_hi:[1,0]
	v_pk_mul_f32 v[48:49], v[48:49], v[200:201] op_sel_hi:[1,0]
	v_pk_mul_f32 v[46:47], v[46:47], v[200:201] op_sel_hi:[1,0]
	v_pk_mul_f32 v[44:45], v[44:45], v[200:201] op_sel_hi:[1,0]
	v_pk_mul_f32 v[42:43], v[42:43], v[200:201] op_sel_hi:[1,0]
	v_pk_mul_f32 v[40:41], v[40:41], v[200:201] op_sel_hi:[1,0]
	v_pk_mul_f32 v[38:39], v[38:39], v[200:201] op_sel_hi:[1,0]
	v_pk_mul_f32 v[36:37], v[36:37], v[200:201] op_sel_hi:[1,0]
	s_waitcnt lgkmcnt(0)
	v_mfma_f32_32x32x16_bf16 v[52:67], v[68:71], v[100:103], v[52:67]
	v_mfma_f32_32x32x16_bf16 v[36:51], v[84:87], v[100:103], v[36:51]
	v_mfma_f32_32x32x16_bf16 v[52:67], v[72:75], v[104:107], v[52:67]
	v_mfma_f32_32x32x16_bf16 v[36:51], v[88:91], v[104:107], v[36:51]
	v_mfma_f32_32x32x16_bf16 v[52:67], v[76:79], v[108:111], v[52:67]
	v_mfma_f32_32x32x16_bf16 v[36:51], v[92:95], v[108:111], v[36:51]
	v_mfma_f32_32x32x16_bf16 v[52:67], v[80:83], v[112:115], v[52:67]
	v_mfma_f32_32x32x16_bf16 v[36:51], v[96:99], v[112:115], v[36:51]
	v_add_u32_e32 v80, 0xc800, v159
	v_add_u32_e32 v96, 0xd800, v159
	ds_read2_b64 v[68:71], v80 offset1:2
	ds_read2_b64 v[72:75], v80 offset0:4 offset1:6
	ds_read2_b64 v[76:79], v80 offset0:8 offset1:10
	ds_read2_b64 v[80:83], v80 offset0:12 offset1:14
	ds_read2_b64 v[84:87], v96 offset0:32 offset1:34
	ds_read2_b64 v[88:91], v96 offset0:36 offset1:38
	ds_read2_b64 v[92:95], v96 offset0:40 offset1:42
	ds_read2_b64 v[96:99], v96 offset0:44 offset1:46
	v_pk_mul_f32 v[34:35], v[34:35], v[200:201] op_sel_hi:[1,0]
	v_pk_mul_f32 v[32:33], v[32:33], v[200:201] op_sel_hi:[1,0]
	v_pk_mul_f32 v[30:31], v[30:31], v[200:201] op_sel_hi:[1,0]
	v_pk_mul_f32 v[28:29], v[28:29], v[200:201] op_sel_hi:[1,0]
	v_pk_mul_f32 v[26:27], v[26:27], v[200:201] op_sel_hi:[1,0]
	v_pk_mul_f32 v[24:25], v[24:25], v[200:201] op_sel_hi:[1,0]
	v_pk_mul_f32 v[22:23], v[22:23], v[200:201] op_sel_hi:[1,0]
	v_pk_mul_f32 v[20:21], v[20:21], v[200:201] op_sel_hi:[1,0]
	v_pk_mul_f32 v[18:19], v[18:19], v[200:201] op_sel_hi:[1,0]
	v_pk_mul_f32 v[16:17], v[16:17], v[200:201] op_sel_hi:[1,0]
	v_pk_mul_f32 v[14:15], v[14:15], v[200:201] op_sel_hi:[1,0]
	v_pk_mul_f32 v[12:13], v[12:13], v[200:201] op_sel_hi:[1,0]
	v_pk_mul_f32 v[10:11], v[10:11], v[200:201] op_sel_hi:[1,0]
	v_pk_mul_f32 v[8:9], v[8:9], v[200:201] op_sel_hi:[1,0]
	v_pk_mul_f32 v[6:7], v[6:7], v[200:201] op_sel_hi:[1,0]
	v_pk_mul_f32 v[4:5], v[4:5], v[200:201] op_sel_hi:[1,0]
	s_waitcnt lgkmcnt(0)
	v_mfma_f32_32x32x16_bf16 v[20:35], v[68:71], v[100:103], v[20:35]
	v_mfma_f32_32x32x16_bf16 v[4:19], v[84:87], v[100:103], v[4:19]
	v_mfma_f32_32x32x16_bf16 v[20:35], v[72:75], v[104:107], v[20:35]
	v_mfma_f32_32x32x16_bf16 v[4:19], v[88:91], v[104:107], v[4:19]
	v_mfma_f32_32x32x16_bf16 v[20:35], v[76:79], v[108:111], v[20:35]
	v_mfma_f32_32x32x16_bf16 v[4:19], v[92:95], v[108:111], v[4:19]
	v_mfma_f32_32x32x16_bf16 v[20:35], v[80:83], v[112:115], v[20:35]
	v_mfma_f32_32x32x16_bf16 v[4:19], v[96:99], v[112:115], v[4:19]
	s_add_u32 s28, s28, 4
	s_addc_u32 s29, s29, 0
	v_lshl_add_u64 v[162:163], v[162:163], 0, s[38:39]
	s_cmp_eq_u32 s35, 63
	s_waitcnt vmcnt(0)
	v_mov_b32_e32 v200, v116
	s_barrier
	s_cbranch_scc0 .LBB0_490
	v_add_u32_e32 v82, v157, v155
	v_cvt_pk_bf16_f32 v52, v52, v53
	v_cvt_pk_bf16_f32 v53, v54, v55
	v_cvt_pk_bf16_f32 v54, v56, v57
	v_cvt_pk_bf16_f32 v57, v62, v63
	v_cvt_pk_bf16_f32 v62, v8, v9
	v_add_u32_e32 v8, 0xe800, v82
	v_cvt_pk_bf16_f32 v56, v60, v61
	v_cvt_pk_bf16_f32 v36, v36, v37
	v_cvt_pk_bf16_f32 v37, v38, v39
	v_cvt_pk_bf16_f32 v38, v40, v41
	v_cvt_pk_bf16_f32 v39, v42, v43
	v_cvt_pk_bf16_f32 v40, v44, v45
	v_cvt_pk_bf16_f32 v41, v46, v47
	v_cvt_pk_bf16_f32 v42, v48, v49
	v_cvt_pk_bf16_f32 v43, v50, v51
	v_cvt_pk_bf16_f32 v44, v20, v21
	v_cvt_pk_bf16_f32 v45, v22, v23
	v_cvt_pk_bf16_f32 v46, v24, v25
	v_cvt_pk_bf16_f32 v47, v26, v27
	v_cvt_pk_bf16_f32 v48, v28, v29
	v_cvt_pk_bf16_f32 v49, v30, v31
	v_cvt_pk_bf16_f32 v50, v32, v33
	v_cvt_pk_bf16_f32 v51, v34, v35
	v_cvt_pk_bf16_f32 v60, v4, v5
	v_cvt_pk_bf16_f32 v61, v6, v7
	ds_read2_b64 v[4:7], v8 offset0:64 offset1:66
	ds_read2_b64 v[20:23], v8 offset0:68 offset1:70
	ds_read2_b64 v[24:27], v8 offset0:72 offset1:74
	ds_read2_b64 v[28:31], v8 offset0:76 offset1:78
	ds_read2_b64 v[32:35], v8 offset0:80 offset1:82
	ds_read2_b64 v[68:71], v8 offset0:84 offset1:86
	ds_read2_b64 v[72:75], v8 offset0:88 offset1:90
	ds_read2_b64 v[78:81], v8 offset0:92 offset1:94
	s_add_u32 s24, s6, s24
	s_addc_u32 s25, s7, s25
	s_add_u32 s24, s24, s9
	s_addc_u32 s25, s25, 0
	v_lshl_add_u64 v[76:77], v[160:161], 2, s[24:25]
	v_cvt_pk_bf16_f32 v55, v58, v59
	v_cvt_pk_bf16_f32 v58, v64, v65
	v_cvt_pk_bf16_f32 v59, v66, v67
	v_cvt_pk_bf16_f32 v63, v10, v11
	v_cvt_pk_bf16_f32 v64, v12, v13
	v_cvt_pk_bf16_f32 v65, v14, v15
	v_cvt_pk_bf16_f32 v66, v16, v17
	v_cvt_pk_bf16_f32 v67, v18, v19
	s_waitcnt lgkmcnt(7)
	v_mfma_f32_32x32x16_bf16 v[4:19], v[4:7], v[52:55], 0
	s_waitcnt lgkmcnt(6)
	v_mfma_f32_32x32x16_bf16 v[4:19], v[20:23], v[56:59], v[4:19]
	s_waitcnt lgkmcnt(5)
	v_mfma_f32_32x32x16_bf16 v[4:19], v[24:27], v[36:39], v[4:19]
	s_waitcnt lgkmcnt(4)
	v_mfma_f32_32x32x16_bf16 v[4:19], v[28:31], v[40:43], v[4:19]
	s_waitcnt lgkmcnt(3)
	v_mfma_f32_32x32x16_bf16 v[4:19], v[32:35], v[44:47], v[4:19]
	s_waitcnt lgkmcnt(2)
	v_mfma_f32_32x32x16_bf16 v[4:19], v[68:71], v[48:51], v[4:19]
	s_waitcnt lgkmcnt(1)
	v_mfma_f32_32x32x16_bf16 v[4:19], v[72:75], v[60:63], v[4:19]
	s_waitcnt lgkmcnt(0)
	v_mfma_f32_32x32x16_bf16 v[4:19], v[78:81], v[64:67], v[4:19]
	v_add_u32_e32 v20, 0x2100, v82
	v_add_u32_e32 v24, 0xe800, v20
	ds_read2_b64 v[20:23], v24 offset0:64 offset1:66
	ds_read2_b64 v[68:71], v24 offset0:68 offset1:70
	ds_read2_b64 v[72:75], v24 offset0:72 offset1:74
	ds_read2_b64 v[78:81], v24 offset0:76 offset1:78
	ds_read2_b64 v[82:85], v24 offset0:80 offset1:82
	ds_read2_b64 v[86:89], v24 offset0:84 offset1:86
	ds_read2_b64 v[90:93], v24 offset0:88 offset1:90
	ds_read2_b64 v[94:97], v24 offset0:92 offset1:94
	s_waitcnt lgkmcnt(7)
	v_mfma_f32_32x32x16_bf16 v[20:35], v[20:23], v[52:55], 0
	s_waitcnt lgkmcnt(6)
	v_mfma_f32_32x32x16_bf16 v[20:35], v[68:71], v[56:59], v[20:35]
	s_waitcnt lgkmcnt(5)
	v_mfma_f32_32x32x16_bf16 v[20:35], v[72:75], v[36:39], v[20:35]
	s_waitcnt lgkmcnt(4)
	v_mfma_f32_32x32x16_bf16 v[20:35], v[78:81], v[40:43], v[20:35]
	s_waitcnt lgkmcnt(3)
	v_mfma_f32_32x32x16_bf16 v[20:35], v[82:85], v[44:47], v[20:35]
	s_waitcnt lgkmcnt(2)
	v_mfma_f32_32x32x16_bf16 v[20:35], v[86:89], v[48:51], v[20:35]
	s_waitcnt lgkmcnt(1)
	v_mfma_f32_32x32x16_bf16 v[20:35], v[90:93], v[60:63], v[20:35]
	s_waitcnt lgkmcnt(0)
	v_mfma_f32_32x32x16_bf16 v[20:35], v[94:97], v[64:67], v[20:35]
	v_add_f32_e64 v4, v166, -v4
	v_add_f32_e64 v5, v167, -v5
	v_add_f32_e64 v6, v164, -v6
	v_add_f32_e64 v7, v165, -v7
	v_add_f32_e64 v8, v168, -v8
	v_add_f32_e64 v9, v169, -v9
	v_pk_add_f32 v[10:11], v[170:171], v[10:11] neg_lo:[0,1] neg_hi:[0,1]
	v_pk_add_f32 v[12:13], v[180:181], v[12:13] neg_lo:[0,1] neg_hi:[0,1]
	v_pk_add_f32 v[14:15], v[194:195], v[14:15] neg_lo:[0,1] neg_hi:[0,1]
	v_pk_add_f32 v[16:17], v[196:197], v[16:17] neg_lo:[0,1] neg_hi:[0,1]
	v_pk_add_f32 v[18:19], v[198:199], v[18:19] neg_lo:[0,1] neg_hi:[0,1]
	v_cvt_pk_bf16_f32 v68, v4, v5
	v_cvt_pk_bf16_f32 v69, v6, v7
	v_pk_add_f32 v[4:5], v[172:173], v[20:21] neg_lo:[0,1] neg_hi:[0,1]
	v_pk_add_f32 v[6:7], v[174:175], v[22:23] neg_lo:[0,1] neg_hi:[0,1]
	v_add3_u32 v98, s31, v149, v155
	v_cvt_pk_bf16_f32 v70, v8, v9
	v_cvt_pk_bf16_f32 v71, v10, v11
	v_cvt_pk_bf16_f32 v72, v12, v13
	v_cvt_pk_bf16_f32 v73, v14, v15
	v_cvt_pk_bf16_f32 v74, v16, v17
	v_cvt_pk_bf16_f32 v75, v18, v19
	v_pk_add_f32 v[8:9], v[176:177], v[24:25] neg_lo:[0,1] neg_hi:[0,1]
	v_pk_add_f32 v[10:11], v[178:179], v[26:27] neg_lo:[0,1] neg_hi:[0,1]
	v_pk_add_f32 v[12:13], v[202:203], v[28:29] neg_lo:[0,1] neg_hi:[0,1]
	v_pk_add_f32 v[14:15], v[204:205], v[30:31] neg_lo:[0,1] neg_hi:[0,1]
	v_pk_add_f32 v[16:17], v[206:207], v[32:33] neg_lo:[0,1] neg_hi:[0,1]
	v_pk_add_f32 v[18:19], v[208:209], v[34:35] neg_lo:[0,1] neg_hi:[0,1]
	v_cvt_pk_bf16_f32 v78, v4, v5
	v_cvt_pk_bf16_f32 v79, v6, v7
	ds_read2_b64 v[4:7], v98 offset1:2
	ds_read2_b64 v[20:23], v98 offset0:4 offset1:6
	ds_read2_b64 v[24:27], v98 offset0:8 offset1:10
	ds_read2_b64 v[28:31], v98 offset0:12 offset1:14
	ds_read2_b64 v[32:35], v98 offset0:16 offset1:18
	ds_read2_b64 v[82:85], v98 offset0:20 offset1:22
	ds_read2_b64 v[86:89], v98 offset0:24 offset1:26
	ds_read2_b64 v[90:93], v98 offset0:28 offset1:30
	v_cvt_pk_bf16_f32 v80, v8, v9
	v_cvt_pk_bf16_f32 v81, v10, v11
	v_cvt_pk_bf16_f32 v94, v12, v13
	v_cvt_pk_bf16_f32 v95, v14, v15
	v_cvt_pk_bf16_f32 v96, v16, v17
	v_cvt_pk_bf16_f32 v97, v18, v19
	s_waitcnt lgkmcnt(7)
	v_mfma_f32_32x32x16_bf16 v[4:19], v[4:7], v[52:55], 0
	s_waitcnt lgkmcnt(6)
	v_mfma_f32_32x32x16_bf16 v[4:19], v[20:23], v[56:59], v[4:19]
	s_waitcnt lgkmcnt(5)
	v_mfma_f32_32x32x16_bf16 v[4:19], v[24:27], v[36:39], v[4:19]
	s_waitcnt lgkmcnt(4)
	v_mfma_f32_32x32x16_bf16 v[4:19], v[28:31], v[40:43], v[4:19]
	s_waitcnt lgkmcnt(3)
	v_mfma_f32_32x32x16_bf16 v[4:19], v[32:35], v[44:47], v[4:19]
	s_waitcnt lgkmcnt(2)
	v_mfma_f32_32x32x16_bf16 v[4:19], v[82:85], v[48:51], v[4:19]
	s_waitcnt lgkmcnt(1)
	v_mfma_f32_32x32x16_bf16 v[4:19], v[86:89], v[60:63], v[4:19]
	s_waitcnt lgkmcnt(0)
	v_mfma_f32_32x32x16_bf16 v[4:19], v[90:93], v[64:67], v[4:19]
	v_add_u32_e32 v24, 0x2000, v98
	ds_read2_b64 v[20:23], v24 offset0:32 offset1:34
	ds_read2_b64 v[82:85], v24 offset0:36 offset1:38
	ds_read2_b64 v[86:89], v24 offset0:40 offset1:42
	ds_read2_b64 v[90:93], v24 offset0:44 offset1:46
	ds_read2_b64 v[98:101], v24 offset0:48 offset1:50
	ds_read2_b64 v[102:105], v24 offset0:52 offset1:54
	ds_read2_b64 v[106:109], v24 offset0:56 offset1:58
	ds_read2_b64 v[110:113], v24 offset0:60 offset1:62
	s_waitcnt lgkmcnt(7)
	v_mfma_f32_32x32x16_bf16 v[20:35], v[20:23], v[52:55], 0
	s_waitcnt lgkmcnt(6)
	v_mfma_f32_32x32x16_bf16 v[20:35], v[82:85], v[56:59], v[20:35]
	s_waitcnt lgkmcnt(5)
	v_mfma_f32_32x32x16_bf16 v[20:35], v[86:89], v[36:39], v[20:35]
	s_waitcnt lgkmcnt(4)
	v_mfma_f32_32x32x16_bf16 v[20:35], v[90:93], v[40:43], v[20:35]
	s_waitcnt lgkmcnt(3)
	v_mfma_f32_32x32x16_bf16 v[20:35], v[98:101], v[44:47], v[20:35]
	s_waitcnt lgkmcnt(2)
	v_mfma_f32_32x32x16_bf16 v[20:35], v[102:105], v[48:51], v[20:35]
	s_waitcnt lgkmcnt(1)
	v_mfma_f32_32x32x16_bf16 v[20:35], v[106:109], v[60:63], v[20:35]
	s_waitcnt lgkmcnt(0)
	v_mfma_f32_32x32x16_bf16 v[20:35], v[110:113], v[64:67], v[20:35]
	v_add3_u32 v52, s33, v149, v153
	v_add_u32_e32 v64, 0x1000, v52
	ds_read2_b64 v[36:39], v52 offset1:2
	ds_read2_b64 v[40:43], v52 offset0:4 offset1:6
	ds_read2_b64 v[44:47], v52 offset0:8 offset1:10
	ds_read2_b64 v[48:51], v52 offset0:12 offset1:14
	ds_read2_b64 v[52:55], v64 offset0:32 offset1:34
	ds_read2_b64 v[56:59], v64 offset0:36 offset1:38
	ds_read2_b64 v[60:63], v64 offset0:40 offset1:42
	ds_read2_b64 v[64:67], v64 offset0:44 offset1:46
	s_waitcnt lgkmcnt(7)
	v_mfma_f32_32x32x16_bf16 v[4:19], v[36:39], v[68:71], v[4:19]
	s_waitcnt lgkmcnt(3)
	v_mfma_f32_32x32x16_bf16 v[20:35], v[52:55], v[68:71], v[20:35]
	v_mfma_f32_32x32x16_bf16 v[4:19], v[40:43], v[72:75], v[4:19]
	s_waitcnt lgkmcnt(2)
	v_mfma_f32_32x32x16_bf16 v[20:35], v[56:59], v[72:75], v[20:35]
	v_mfma_f32_32x32x16_bf16 v[4:19], v[44:47], v[78:81], v[4:19]
	s_waitcnt lgkmcnt(1)
	v_mfma_f32_32x32x16_bf16 v[20:35], v[60:63], v[78:81], v[20:35]
	v_mfma_f32_32x32x16_bf16 v[4:19], v[48:51], v[94:97], v[4:19]
	s_waitcnt lgkmcnt(0)
	v_mfma_f32_32x32x16_bf16 v[20:35], v[64:67], v[94:97], v[20:35]
	v_lshl_add_u64 v[36:37], v[76:77], 0, v[2:3]
	s_mov_b32 s9, 0x479e0000
	v_add_co_u32_e32 v38, vcc, s9, v36
	s_mov_b32 s9, 0x479e1000
	s_nop 0
	v_addc_co_u32_e32 v39, vcc, 0, v37, vcc
	s_nop 3
	global_store_dword v[38:39], v4, off
	global_store_dword v[38:39], v5, off offset:2048
	v_add_co_u32_e32 v4, vcc, s9, v36
	s_mov_b32 s9, 0x479e4000
	s_nop 0
	v_addc_co_u32_e32 v5, vcc, 0, v37, vcc
	global_store_dword v[4:5], v6, off
	global_store_dword v[4:5], v7, off offset:2048
	v_add_co_u32_e32 v4, vcc, s9, v36
	s_mov_b32 s9, 0x479e5000
	s_nop 0
	v_addc_co_u32_e32 v5, vcc, 0, v37, vcc
	global_store_dword v[4:5], v8, off
	global_store_dword v[4:5], v9, off offset:2048
	v_add_co_u32_e32 v4, vcc, s9, v36
	s_mov_b32 s9, 0x479e8000
	s_nop 0
	v_addc_co_u32_e32 v5, vcc, 0, v37, vcc
	global_store_dword v[4:5], v10, off
	global_store_dword v[4:5], v11, off offset:2048
	v_add_co_u32_e32 v4, vcc, s9, v36
	s_mov_b32 s9, 0x479e9000
	s_nop 0
	v_addc_co_u32_e32 v5, vcc, 0, v37, vcc
	global_store_dword v[4:5], v12, off
	global_store_dword v[4:5], v13, off offset:2048
	v_add_co_u32_e32 v4, vcc, s9, v36
	s_mov_b32 s9, 0x479ec000
	s_nop 0
	v_addc_co_u32_e32 v5, vcc, 0, v37, vcc
	global_store_dword v[4:5], v14, off
	global_store_dword v[4:5], v15, off offset:2048
	v_add_co_u32_e32 v4, vcc, s9, v36
	s_mov_b32 s9, 0x479ed000
	s_nop 0
	v_addc_co_u32_e32 v5, vcc, 0, v37, vcc
	global_store_dword v[4:5], v16, off
	global_store_dword v[4:5], v17, off offset:2048
	v_add_co_u32_e32 v4, vcc, s9, v36
	s_mov_b32 s9, 0x479f0000
	s_nop 0
	v_addc_co_u32_e32 v5, vcc, 0, v37, vcc
	global_store_dword v[4:5], v18, off
	global_store_dword v[4:5], v19, off offset:2048
	v_add_co_u32_e32 v4, vcc, s9, v36
	s_mov_b32 s9, 0x479f1000
	s_nop 0
	v_addc_co_u32_e32 v5, vcc, 0, v37, vcc
	global_store_dword v[4:5], v20, off
	global_store_dword v[4:5], v21, off offset:2048
	v_add_co_u32_e32 v4, vcc, s9, v36
	s_mov_b32 s9, 0x479f4000
	s_nop 0
	v_addc_co_u32_e32 v5, vcc, 0, v37, vcc
	global_store_dword v[4:5], v22, off
	global_store_dword v[4:5], v23, off offset:2048
	v_add_co_u32_e32 v4, vcc, s9, v36
	s_mov_b32 s9, 0x479f5000
	s_nop 0
	v_addc_co_u32_e32 v5, vcc, 0, v37, vcc
	global_store_dword v[4:5], v24, off
	global_store_dword v[4:5], v25, off offset:2048
	v_add_co_u32_e32 v4, vcc, s9, v36
	s_mov_b32 s9, 0x479f8000
	s_nop 0
	v_addc_co_u32_e32 v5, vcc, 0, v37, vcc
	global_store_dword v[4:5], v26, off
	global_store_dword v[4:5], v27, off offset:2048
	v_add_co_u32_e32 v4, vcc, s9, v36
	s_mov_b32 s9, 0x479f9000
	s_nop 0
	v_addc_co_u32_e32 v5, vcc, 0, v37, vcc
	global_store_dword v[4:5], v28, off
	global_store_dword v[4:5], v29, off offset:2048
	v_add_co_u32_e32 v4, vcc, s9, v36
	s_mov_b32 s9, 0x479fc000
	s_nop 0
	v_addc_co_u32_e32 v5, vcc, 0, v37, vcc
	global_store_dword v[4:5], v30, off
	global_store_dword v[4:5], v31, off offset:2048
	v_add_co_u32_e32 v4, vcc, s9, v36
	s_nop 1
	v_addc_co_u32_e32 v5, vcc, 0, v37, vcc
	global_store_dword v[4:5], v32, off
	global_store_dword v[4:5], v33, off offset:2048
	v_add_co_u32_e32 v4, vcc, 0x479fd000, v36
	s_nop 1
	v_addc_co_u32_e32 v5, vcc, 0, v37, vcc
	global_store_dword v[4:5], v34, off
	global_store_dword v[4:5], v35, off offset:2048
	s_mov_b64 s[28:29], 0
	s_waitcnt lgkmcnt(0)
	s_barrier
.LBB0_492:
	s_and_b64 vcc, exec, s[28:29]
	s_mov_b32 s25, 0x800000
	s_movk_i32 s24, 0x7200
	s_cbranch_vccz .LBB0_481
	s_add_u32 s18, s18, 0x2000
	v_mov_b32_e32 v149, v3
	v_ashrrev_i32_e32 v153, 31, v152
	v_ashrrev_i32_e32 v155, 31, v154
	v_ashrrev_i32_e32 v157, 31, v156
	s_addc_u32 s19, s19, 0
	v_add_u32_e32 v38, 0x800, v158
	v_add_u32_e32 v64, 0x1000, v158
	v_lshl_add_u64 v[28:29], s[20:21], 0, v[148:149]
	v_lshlrev_b64 v[44:45], 10, v[152:153]
	s_mov_b64 s[20:21], 0x10000
	v_lshlrev_b64 v[46:47], 10, v[150:151]
	v_lshlrev_b64 v[48:49], 10, v[154:155]
	v_lshlrev_b64 v[50:51], 10, v[156:157]
	v_ashrrev_i32_e32 v159, 31, v158
	v_ashrrev_i32_e32 v39, 31, v38
	s_add_u32 s16, s16, 0x4000
	v_ashrrev_i32_e32 v65, 31, v64
	v_add_u32_e32 v68, 0x1800, v158
	v_lshl_add_u64 v[30:31], s[22:23], 0, v[148:149]
	v_lshl_add_u64 v[4:5], v[44:45], 0, s[20:21]
	v_lshl_add_u64 v[12:13], v[46:47], 0, s[20:21]
	v_lshl_add_u64 v[20:21], v[48:49], 0, s[20:21]
	v_lshl_add_u64 v[32:33], v[50:51], 0, s[20:21]
	v_lshlrev_b64 v[60:61], 1, v[158:159]
	v_lshlrev_b64 v[62:63], 1, v[38:39]
	s_addc_u32 s17, s17, 0
	v_lshlrev_b64 v[64:65], 1, v[64:65]
	v_ashrrev_i32_e32 v69, 31, v68
	v_lshl_add_u64 v[6:7], v[28:29], 0, v[4:5]
	v_lshl_add_u64 v[8:9], v[30:31], 0, v[4:5]
	v_lshl_add_u64 v[14:15], v[28:29], 0, v[12:13]
	v_lshl_add_u64 v[16:17], v[30:31], 0, v[12:13]
	v_lshl_add_u64 v[22:23], v[28:29], 0, v[20:21]
	v_lshl_add_u64 v[24:25], v[30:31], 0, v[20:21]
	v_lshl_add_u64 v[28:29], v[28:29], 0, v[32:33]
	v_lshl_add_u64 v[32:33], v[30:31], 0, v[32:33]
	v_lshl_add_u64 v[36:37], s[18:19], 0, v[60:61]
	v_lshl_add_u64 v[40:41], s[18:19], 0, v[62:63]
	v_lshl_add_u64 v[52:53], s[16:17], 0, v[60:61]
	v_lshl_add_u64 v[56:57], s[16:17], 0, v[62:63]
	v_lshl_add_u64 v[66:67], s[16:17], 0, v[64:65]
	v_lshlrev_b64 v[68:69], 1, v[68:69]
	global_load_dwordx4 v[4:7], v[6:7], off
	s_nop 0
	global_load_dwordx4 v[8:11], v[8:9], off
	s_nop 0
	global_load_dwordx4 v[12:15], v[14:15], off
	s_nop 0
	global_load_dwordx4 v[16:19], v[16:17], off
	s_nop 0
	global_load_dwordx4 v[20:23], v[22:23], off
	s_nop 0
	global_load_dwordx4 v[24:27], v[24:25], off
	s_nop 0
	global_load_dwordx4 v[28:31], v[28:29], off
	s_nop 0
	global_load_dwordx4 v[32:35], v[32:33], off
	s_nop 0
	global_load_dwordx4 v[36:39], v[36:37], off
	s_nop 0
	global_load_dwordx4 v[40:43], v[40:41], off
	s_nop 0
	global_load_dwordx4 v[52:55], v[52:53], off
	s_nop 0
	global_load_dwordx4 v[56:59], v[56:57], off
	v_lshl_add_u64 v[70:71], s[16:17], 0, v[68:69]
	global_load_dwordx4 v[76:79], v[66:67], off
	global_load_dwordx4 v[80:83], v[70:71], off
	s_mov_b32 s9, s42
	s_lshl_b32 s8, s8, 8
	v_add_u32_e32 v2, s9, v148
	v_add_u32_e32 v160, s9, v212
	s_movk_i32 s9, 0x88
	v_lshl_add_u64 v[128:129], v[50:51], 0, s[10:11]
	s_and_b32 s8, s8, 0x300
	v_lshl_add_u64 v[130:131], v[48:49], 0, s[10:11]
	v_lshl_add_u64 v[132:133], v[46:47], 0, s[10:11]
	v_lshl_add_u64 v[134:135], v[44:45], 0, s[10:11]
	v_add_u32_e32 v157, s31, v148
	v_add_u32_e32 v158, s33, v212
	v_add_u32_e32 v159, s34, v212
	v_mul_lo_u32 v161, v152, s57
	v_mul_lo_u32 v162, v150, s57
	v_mul_lo_u32 v163, v154, s57
	v_mul_lo_u32 v156, v156, s57
	v_mul_lo_u32 v164, v211, s9
	v_mul_lo_u32 v1, v1, s9
	v_mul_lo_u32 v165, v210, s9
	v_mul_lo_u32 v166, v201, s9
	v_lshl_add_u64 v[116:117], s[14:15], 0, v[68:69]
	v_lshl_add_u64 v[118:119], s[14:15], 0, v[64:65]
	v_lshl_add_u64 v[120:121], s[14:15], 0, v[62:63]
	v_lshl_add_u64 v[122:123], s[14:15], 0, v[60:61]
	v_lshl_add_u64 v[124:125], s[12:13], 0, v[62:63]
	v_lshl_add_u64 v[126:127], s[12:13], 0, v[60:61]
	v_or3_b32 v128, v128, s8, v148
	v_or3_b32 v130, v130, s8, v148
	v_or3_b32 v132, v132, s8, v148
	v_or3_b32 v134, v134, s8, v148
	s_mov_b32 s12, 0
	s_branch .LBB0_495

.LBB0_495:
	s_cmp_lt_u32 s12, 62
	s_cselect_b64 s[10:11], -1, 0
	s_cmp_gt_u32 s12, 61
	s_cselect_b64 s[8:9], -1, 0
	s_and_b64 vcc, exec, s[8:9]
	v_lshl_add_u64 v[154:155], s[6:7], 0, v[134:135]
	v_lshl_add_u64 v[152:153], s[6:7], 0, v[132:133]
	v_lshl_add_u64 v[150:151], s[6:7], 0, v[130:131]
	v_lshl_add_u64 v[148:149], s[6:7], 0, v[128:129]
	v_lshl_add_u64 v[146:147], s[6:7], 0, v[126:127]
	v_lshl_add_u64 v[144:145], s[6:7], 0, v[124:125]
	v_lshl_add_u64 v[142:143], s[6:7], 0, v[122:123]
	v_lshl_add_u64 v[140:141], s[6:7], 0, v[120:121]
	v_lshl_add_u64 v[138:139], s[6:7], 0, v[118:119]
	v_lshl_add_u64 v[136:137], s[6:7], 0, v[116:117]
	s_cbranch_vccnz .LBB0_497
	v_add_co_u32_e32 v44, vcc, 0x43a20000, v154
	s_nop 1
	v_addc_co_u32_e32 v45, vcc, 0, v155, vcc
	v_add_co_u32_e32 v46, vcc, 0x44a20000, v154
	s_nop 1
	v_addc_co_u32_e32 v47, vcc, 0, v155, vcc
	v_add_co_u32_e32 v60, vcc, 0x43a20000, v152
	global_load_dwordx4 v[48:51], v[44:45], off
	s_nop 0
	global_load_dwordx4 v[44:47], v[46:47], off
	v_addc_co_u32_e32 v61, vcc, 0, v153, vcc
	v_add_co_u32_e32 v62, vcc, 0x44a20000, v152
	s_nop 1
	v_addc_co_u32_e32 v63, vcc, 0, v153, vcc
	v_add_co_u32_e32 v68, vcc, 0x43a20000, v150
	global_load_dwordx4 v[64:67], v[60:61], off
	s_nop 0
	global_load_dwordx4 v[60:63], v[62:63], off
	v_addc_co_u32_e32 v69, vcc, 0, v151, vcc
	v_add_co_u32_e32 v70, vcc, 0x44a20000, v150
	s_nop 1
	v_addc_co_u32_e32 v71, vcc, 0, v151, vcc
	v_add_co_u32_e32 v84, vcc, 0x43a20000, v148
	global_load_dwordx4 v[72:75], v[68:69], off
	s_nop 0
	global_load_dwordx4 v[68:71], v[70:71], off
	v_addc_co_u32_e32 v85, vcc, 0, v149, vcc
	v_add_co_u32_e32 v86, vcc, 0x44a20000, v148
	s_nop 1
	v_addc_co_u32_e32 v87, vcc, 0, v149, vcc
	v_add_co_u32_e32 v92, vcc, 0x46a04000, v146
	global_load_dwordx4 v[88:91], v[84:85], off
	s_nop 0
	global_load_dwordx4 v[84:87], v[86:87], off
	v_addc_co_u32_e32 v93, vcc, 0, v147, vcc
	v_add_co_u32_e32 v96, vcc, 0x46a04000, v144
	s_nop 1
	v_addc_co_u32_e32 v97, vcc, 0, v145, vcc
	v_add_co_u32_e32 v100, vcc, 0x45a08000, v142
	global_load_dwordx4 v[92:95], v[92:93], off
	s_nop 0
	global_load_dwordx4 v[96:99], v[96:97], off
	v_addc_co_u32_e32 v101, vcc, 0, v143, vcc
	v_add_co_u32_e32 v104, vcc, 0x45a08000, v140
	s_nop 1
	v_addc_co_u32_e32 v105, vcc, 0, v141, vcc
	v_add_co_u32_e32 v108, vcc, 0x45a08000, v138
	global_load_dwordx4 v[100:103], v[100:101], off
	s_nop 0
	global_load_dwordx4 v[104:107], v[104:105], off
	v_addc_co_u32_e32 v109, vcc, 0, v139, vcc
	v_add_co_u32_e32 v112, vcc, 0x45a08000, v136
	s_nop 1
	v_addc_co_u32_e32 v113, vcc, 0, v137, vcc
	global_load_dwordx4 v[108:111], v[108:109], off
	s_nop 0
	global_load_dwordx4 v[112:115], v[112:113], off
.LBB0_497:
	v_add3_u32 v167, v2, v161, s59
	s_waitcnt vmcnt(0) lgkmcnt(0)
	ds_write2_b64 v167, v[4:5], v[6:7] offset1:1
	v_add_u32_e32 v167, v157, v161
	ds_write2_b64 v167, v[8:9], v[10:11] offset1:1
	v_add3_u32 v167, v2, v162, s59
	ds_write2_b64 v167, v[12:13], v[14:15] offset1:1
	v_add_u32_e32 v167, v157, v162
	ds_write2_b64 v167, v[16:17], v[18:19] offset1:1
	v_add3_u32 v167, v2, v163, s59
	ds_write2_b64 v167, v[20:21], v[22:23] offset1:1
	v_add_u32_e32 v167, v157, v163
	ds_write2_b64 v167, v[24:25], v[26:27] offset1:1
	v_add3_u32 v167, v2, v156, s59
	ds_write2_b64 v167, v[28:29], v[30:31] offset1:1
	v_add_u32_e32 v167, v157, v156
	ds_write2_b64 v167, v[32:33], v[34:35] offset1:1
	v_add_u32_e32 v167, v158, v164
	ds_write2_b64 v167, v[36:37], v[38:39] offset1:1
	v_add_u32_e32 v167, v158, v1
	ds_write2_b64 v167, v[40:41], v[42:43] offset1:1
	v_add_u32_e32 v167, v159, v164
	ds_write2_b64 v167, v[52:53], v[54:55] offset1:1
	v_add_u32_e32 v167, v159, v1
	ds_write2_b64 v167, v[56:57], v[58:59] offset1:1
	v_add_u32_e32 v167, v159, v165
	ds_write2_b64 v167, v[76:77], v[78:79] offset1:1
	v_add_u32_e32 v167, v159, v166
	s_cmp_gt_u32 s12, 60
	ds_write2_b64 v167, v[80:81], v[82:83] offset1:1
	s_waitcnt lgkmcnt(0)
	s_barrier
	s_cbranch_scc1 .LBB0_499
	v_add_co_u32_e32 v4, vcc, 0x43a30000, v154
	s_nop 1
	v_addc_co_u32_e32 v5, vcc, 0, v155, vcc
	v_add_co_u32_e32 v8, vcc, 0x44a30000, v154
	s_nop 1
	v_addc_co_u32_e32 v9, vcc, 0, v155, vcc
	v_add_co_u32_e32 v12, vcc, 0x43a30000, v152
	global_load_dwordx4 v[4:7], v[4:5], off
	s_nop 0
	global_load_dwordx4 v[8:11], v[8:9], off
	v_addc_co_u32_e32 v13, vcc, 0, v153, vcc
	v_add_co_u32_e32 v16, vcc, 0x44a30000, v152
	s_nop 1
	v_addc_co_u32_e32 v17, vcc, 0, v153, vcc
	v_add_co_u32_e32 v20, vcc, 0x43a30000, v150
	global_load_dwordx4 v[12:15], v[12:13], off
	s_nop 0
	global_load_dwordx4 v[16:19], v[16:17], off
	v_addc_co_u32_e32 v21, vcc, 0, v151, vcc
	v_add_co_u32_e32 v24, vcc, 0x44a30000, v150
	s_nop 1
	v_addc_co_u32_e32 v25, vcc, 0, v151, vcc
	v_add_co_u32_e32 v28, vcc, 0x43a30000, v148
	global_load_dwordx4 v[20:23], v[20:21], off
	s_nop 0
	global_load_dwordx4 v[24:27], v[24:25], off
	v_addc_co_u32_e32 v29, vcc, 0, v149, vcc
	v_add_co_u32_e32 v32, vcc, 0x44a30000, v148
	s_nop 1
	v_addc_co_u32_e32 v33, vcc, 0, v149, vcc
	v_add_co_u32_e32 v36, vcc, 0x46a06000, v146
	global_load_dwordx4 v[28:31], v[28:29], off
	s_nop 0
	global_load_dwordx4 v[32:35], v[32:33], off
	v_addc_co_u32_e32 v37, vcc, 0, v147, vcc
	v_add_co_u32_e32 v40, vcc, 0x46a06000, v144
	s_nop 1
	v_addc_co_u32_e32 v41, vcc, 0, v145, vcc
	v_add_co_u32_e32 v52, vcc, 0x45a0c000, v142
	global_load_dwordx4 v[36:39], v[36:37], off
	s_nop 0
	global_load_dwordx4 v[40:43], v[40:41], off
	v_addc_co_u32_e32 v53, vcc, 0, v143, vcc
	v_add_co_u32_e32 v56, vcc, 0x45a0c000, v140
	s_nop 1
	v_addc_co_u32_e32 v57, vcc, 0, v141, vcc
	v_add_co_u32_e32 v76, vcc, 0x45a0c000, v138
	global_load_dwordx4 v[52:55], v[52:53], off
	s_nop 0
	global_load_dwordx4 v[56:59], v[56:57], off
	v_addc_co_u32_e32 v77, vcc, 0, v139, vcc
	v_add_co_u32_e32 v80, vcc, 0x45a0c000, v136
	s_nop 1
	v_addc_co_u32_e32 v81, vcc, 0, v137, vcc
	global_load_dwordx4 v[76:79], v[76:77], off
	s_nop 0
	global_load_dwordx4 v[80:83], v[80:81], off

.Lmix1_s1:
	s_mov_b32 s72, s42
	s_mov_b64 s[100:101], s[4:5]
	s_branch .LBB0_538
.Lmix1_s2:
	s_mov_b64 s[4:5], s[100:101]
	s_branch .LBB0_512

.LBB0_504:
	s_barrier
	s_and_saveexec_b64 s[8:9], s[0:1]
	s_cbranch_execz .LBB0_506
	s_waitcnt vmcnt(0)
	v_mov_b64_e32 v[4:5], s[6:7]
	global_atomic_add v1, v[4:5], v228, off sc0
	v_mov_b32_e32 v2, s12
	s_waitcnt vmcnt(0) lgkmcnt(0)
	ds_write_b32 v2, v1
.LBB0_506:
	s_or_b64 exec, exec, s[8:9]
	v_mov_b32_e32 v1, s12
	s_waitcnt lgkmcnt(0)
	s_barrier
	ds_read_b32 v1, v1
	s_movk_i32 s8, 0x1ff
	s_waitcnt lgkmcnt(0)
	v_cmp_lt_i32_e32 vcc, s8, v1
	v_readfirstlane_b32 s16, v1
	s_mov_b64 s[8:9], -1
	s_cbranch_vccnz .LBB0_503
	v_mov_b32_e32 v1, v0
	s_lshl_b32 s15, s16, 3
	v_readlane_b32 s8, v252, 0
	v_readfirstlane_b32 s17, v1
	s_mov_b32 s9, s88
	s_andn2_b32 s15, s15, 31
	s_ashr_i32 s14, s17, 6
	s_mov_b64 s[10:11], s[68:69]
	s_add_u32 s8, s10, 0x9000000
	s_addc_u32 s9, s11, 0
	s_lshl_b32 s16, s16, 12
	s_and_b32 s18, s16, 0x3000
	s_sub_i32 s16, s18, s15
	s_addk_i32 s16, 0xfe0
	s_waitcnt vmcnt(0)
	v_ashrrev_i32_e32 v9, 7, v1
	v_lshlrev_b32_e32 v2, 4, v1
	v_add_u32_e32 v4, s16, v9
	v_mov_b64_e32 v[10:11], s[10:11]
	s_movk_i32 s19, 0xc00
	v_and_b32_e32 v2, 0x7f0, v2
	v_mad_i64_i32 v[4:5], s[20:21], v4, s19, v[10:11]
	v_lshl_add_u64 v[4:5], v[4:5], 0, v[2:3]
	s_mov_b32 s22, 0x2de00000
	v_add_co_u32_e32 v4, vcc, s22, v4
	s_nop 1
	v_addc_co_u32_e32 v5, vcc, 0, v5, vcc
	s_barrier
	global_load_dwordx4 v[4:7], v[4:5], off offset:1024
	v_add_u32_e32 v8, s72, v2
	s_movk_i32 s23, 0x810
	v_mad_u64_u32 v[12:13], s[20:21], v9, s23, v[8:9]
	s_sub_i32 s15, 0x1020, s15
	s_lshr_b32 s15, s15, 6
	s_cmp_ge_i32 s14, s15
	s_waitcnt vmcnt(0) lgkmcnt(0)
	ds_write_b128 v12, v[4:7]
	v_add_u32_e32 v4, 0x200, v1
	v_ashrrev_i32_e32 v9, 7, v4
	v_add_u32_e32 v4, s16, v9
	v_mad_i64_i32 v[4:5], s[20:21], v4, s19, v[10:11]
	v_lshl_add_u64 v[4:5], v[4:5], 0, v[2:3]
	v_add_co_u32_e32 v4, vcc, s22, v4
	v_mad_u64_u32 v[12:13], s[20:21], v9, s23, v[8:9]
	s_nop 0
	v_addc_co_u32_e32 v5, vcc, 0, v5, vcc
	global_load_dwordx4 v[4:7], v[4:5], off offset:1024
	s_waitcnt vmcnt(0) lgkmcnt(0)
	ds_write_b128 v12, v[4:7]
	v_add_u32_e32 v4, 0x400, v1
	v_ashrrev_i32_e32 v9, 7, v4
	v_add_u32_e32 v4, s16, v9
	v_mad_i64_i32 v[4:5], s[20:21], v4, s19, v[10:11]
	v_lshl_add_u64 v[4:5], v[4:5], 0, v[2:3]
	v_add_co_u32_e32 v4, vcc, s22, v4
	v_mad_u64_u32 v[12:13], s[20:21], v9, s23, v[8:9]
	s_nop 0
	v_addc_co_u32_e32 v5, vcc, 0, v5, vcc
	global_load_dwordx4 v[4:7], v[4:5], off offset:1024
	s_waitcnt vmcnt(0) lgkmcnt(0)
	ds_write_b128 v12, v[4:7]
	v_add_u32_e32 v4, 0x600, v1
	v_ashrrev_i32_e32 v9, 7, v4
	v_add_u32_e32 v4, s16, v9
	v_mad_i64_i32 v[4:5], s[20:21], v4, s19, v[10:11]
	v_lshl_add_u64 v[4:5], v[4:5], 0, v[2:3]
	v_add_co_u32_e32 v4, vcc, s22, v4
	v_mad_u64_u32 v[12:13], s[20:21], v9, s23, v[8:9]
	s_nop 0
	v_addc_co_u32_e32 v5, vcc, 0, v5, vcc
	global_load_dwordx4 v[4:7], v[4:5], off offset:1024
	s_waitcnt vmcnt(0) lgkmcnt(0)
	ds_write_b128 v12, v[4:7]
	v_add_u32_e32 v4, 0x800, v1
	v_ashrrev_i32_e32 v9, 7, v4
	v_add_u32_e32 v4, s16, v9
	v_mad_i64_i32 v[4:5], s[20:21], v4, s19, v[10:11]
	v_lshl_add_u64 v[4:5], v[4:5], 0, v[2:3]
	v_add_co_u32_e32 v4, vcc, s22, v4
	v_mad_u64_u32 v[12:13], s[20:21], v9, s23, v[8:9]
	s_nop 0
	v_addc_co_u32_e32 v5, vcc, 0, v5, vcc
	global_load_dwordx4 v[4:7], v[4:5], off offset:1024
	s_waitcnt vmcnt(0) lgkmcnt(0)
	ds_write_b128 v12, v[4:7]
	v_add_u32_e32 v4, 0xa00, v1
	v_ashrrev_i32_e32 v9, 7, v4
	v_add_u32_e32 v4, s16, v9
	v_mad_i64_i32 v[4:5], s[20:21], v4, s19, v[10:11]
	v_lshl_add_u64 v[4:5], v[4:5], 0, v[2:3]
	v_add_co_u32_e32 v4, vcc, s22, v4
	v_mad_u64_u32 v[12:13], s[20:21], v9, s23, v[8:9]
	s_nop 0
	v_addc_co_u32_e32 v5, vcc, 0, v5, vcc
	global_load_dwordx4 v[4:7], v[4:5], off offset:1024
	s_waitcnt vmcnt(0) lgkmcnt(0)
	ds_write_b128 v12, v[4:7]
	v_add_u32_e32 v4, 0xc00, v1
	v_ashrrev_i32_e32 v9, 7, v4
	v_add_u32_e32 v4, s16, v9
	v_mad_i64_i32 v[4:5], s[20:21], v4, s19, v[10:11]
	v_lshl_add_u64 v[4:5], v[4:5], 0, v[2:3]
	v_add_co_u32_e32 v4, vcc, s22, v4
	v_mad_u64_u32 v[12:13], s[20:21], v9, s23, v[8:9]
	s_nop 0
	v_addc_co_u32_e32 v5, vcc, 0, v5, vcc
	global_load_dwordx4 v[4:7], v[4:5], off offset:1024
	s_waitcnt vmcnt(0) lgkmcnt(0)
	ds_write_b128 v12, v[4:7]
	v_add_u32_e32 v4, 0xe00, v1
	v_ashrrev_i32_e32 v9, 7, v4
	v_add_u32_e32 v4, s16, v9
	v_mad_i64_i32 v[4:5], s[20:21], v4, s19, v[10:11]
	v_lshl_add_u64 v[4:5], v[4:5], 0, v[2:3]
	v_add_co_u32_e32 v4, vcc, s22, v4
	v_mad_u64_u32 v[8:9], s[20:21], v9, s23, v[8:9]
	s_nop 0
	v_addc_co_u32_e32 v5, vcc, 0, v5, vcc
	global_load_dwordx4 v[4:7], v[4:5], off offset:1024
	s_movk_i32 s19, 0x3000
	s_waitcnt vmcnt(0) lgkmcnt(0)
	ds_write_b128 v8, v[4:7]
	v_ashrrev_i32_e32 v6, 4, v1
	v_and_b32_e32 v7, 15, v1
	v_add_u32_e32 v2, s16, v6
	v_mov_b64_e32 v[4:5], s[8:9]
	v_mad_i64_i32 v[4:5], s[20:21], v2, s24, v[4:5]
	v_lshlrev_b32_e32 v2, 1, v7
	v_lshl_add_u64 v[4:5], v[4:5], 0, v[2:3]
	v_add_co_u32_e32 v4, vcc, s19, v4
	s_mov_b64 s[20:21], 0x3100
	s_nop 0
	v_addc_co_u32_e32 v5, vcc, 0, v5, vcc
	global_load_ushort v2, v[4:5], off offset:384
	v_lshlrev_b32_e32 v4, 7, v7
	v_lshlrev_b32_e32 v5, 2, v6
	v_add3_u32 v4, s13, v4, v5
	s_waitcnt vmcnt(0) lgkmcnt(0)
	v_lshlrev_b32_e32 v2, 16, v2
	v_mul_f32_e32 v2, 0x3d000000, v2
	ds_write_b32 v4, v2
	s_waitcnt lgkmcnt(0)
	s_barrier
	s_cbranch_scc1 .LBB0_502
	s_andn2_b32 s17, s17, 63
	v_and_b32_e32 v5, 31, v1
	s_add_i32 s17, s17, s18
	v_or_b32_e32 v12, s17, v5
	v_bfe_u32 v2, v1, 5, 1
	v_or_b32_e32 v8, 32, v12
	v_mov_b64_e32 v[6:7], s[8:9]
	v_lshlrev_b32_e32 v4, 3, v2
	v_or_b32_e32 v1, s18, v5
	v_mad_i64_i32 v[8:9], s[18:19], v8, s24, v[6:7]
	v_lshlrev_b32_e32 v2, 4, v2
	v_lshl_add_u64 v[8:9], v[8:9], 0, v[2:3]
	s_movk_i32 s17, 0x3000
	v_lshl_add_u64 v[10:11], v[8:9], 0, s[20:21]
	v_add_co_u32_e32 v8, vcc, s17, v8
	v_mad_i64_i32 v[6:7], s[18:19], v12, s24, v[6:7]
	s_nop 0
	v_addc_co_u32_e32 v9, vcc, 0, v9, vcc
	v_lshl_add_u64 v[6:7], v[6:7], 0, v[2:3]
	global_load_dwordx4 v[36:39], v[10:11], off offset:96
	global_load_dwordx4 v[44:47], v[10:11], off offset:64
	global_load_dwordx4 v[40:43], v[10:11], off offset:32
	global_load_dwordx4 v[48:51], v[8:9], off offset:256
	v_lshl_add_u64 v[8:9], v[6:7], 0, s[20:21]
	v_add_co_u32_e32 v6, vcc, s17, v6
	global_load_dwordx4 v[52:55], v[8:9], off offset:96
	global_load_dwordx4 v[60:63], v[8:9], off offset:64
	global_load_dwordx4 v[56:59], v[8:9], off offset:32
	v_addc_co_u32_e32 v7, vcc, 0, v7, vcc
	global_load_dwordx4 v[64:67], v[6:7], off offset:256
	v_mul_u32_u24_e32 v6, 0x810, v5
	v_lshl_add_u32 v134, v5, 2, s13
	v_add3_u32 v135, s72, v6, v2
	v_or_b32_e32 v5, s16, v5
	v_mov_b64_e32 v[6:7], s[10:11]
	s_movk_i32 s10, 0x4100
	v_mad_u64_u32 v[6:7], s[10:11], v5, s10, v[6:7]
	v_lshl_add_u64 v[6:7], v[6:7], 0, v[2:3]
	s_mov_b64 s[10:11], 0x30e00000
	v_lshl_add_u64 v[132:133], v[6:7], 0, s[10:11]
	v_lshlrev_b32_e32 v2, 1, v4
.LBB0_509:
	s_add_i32 s16, s14, 8
	s_cmp_ge_i32 s16, s15
	s_cselect_b64 s[10:11], -1, 0
	s_cmp_lt_i32 s16, s15
	s_cselect_b32 s17, s16, s14
	v_lshl_add_u32 v10, s17, 6, v1
	v_mov_b64_e32 v[4:5], s[8:9]
	v_mad_i64_i32 v[6:7], s[18:19], v10, s24, v[4:5]
	v_lshl_add_u64 v[6:7], v[6:7], 0, v[2:3]
	s_movk_i32 s17, 0x3000
	v_lshl_add_u64 v[8:9], v[6:7], 0, s[20:21]
	v_add_co_u32_e32 v6, vcc, s17, v6
	v_mov_b32_e32 v102, 0
	s_nop 0
	v_addc_co_u32_e32 v7, vcc, 0, v7, vcc
	global_load_dwordx4 v[68:71], v[8:9], off offset:32
	global_load_dwordx4 v[72:75], v[8:9], off offset:64
	global_load_dwordx4 v[80:83], v[6:7], off offset:256
	global_load_dwordx4 v[76:79], v[8:9], off offset:96
	v_or_b32_e32 v6, 32, v10
	v_mad_i64_i32 v[4:5], s[18:19], v6, s24, v[4:5]
	v_lshl_add_u64 v[4:5], v[4:5], 0, v[2:3]
	v_lshl_add_u64 v[6:7], v[4:5], 0, s[20:21]
	v_add_co_u32_e32 v4, vcc, 0x3000, v4
	s_mov_b32 s17, 0
	s_nop 0
	v_addc_co_u32_e32 v5, vcc, 0, v5, vcc
	global_load_dwordx4 v[84:87], v[6:7], off offset:32
	global_load_dwordx4 v[88:91], v[6:7], off offset:64
	global_load_dwordx4 v[96:99], v[4:5], off offset:256
	global_load_dwordx4 v[92:95], v[6:7], off offset:96
	v_mov_b32_e32 v103, v102
	v_mov_b32_e32 v116, v102
	v_mov_b32_e32 v117, v102
	v_mov_b32_e32 v118, v102
	v_mov_b32_e32 v119, v102
	v_mov_b32_e32 v112, v102
	v_mov_b32_e32 v113, v102
	v_mov_b32_e32 v114, v102
	v_mov_b32_e32 v115, v102
	v_mov_b32_e32 v104, v102
	v_mov_b32_e32 v105, v102
	v_mov_b32_e32 v106, v102
	v_mov_b32_e32 v107, v102
	v_mov_b32_e32 v100, v102
	v_mov_b32_e32 v101, v102
	v_mov_b32_e32 v110, v102
	v_mov_b32_e32 v111, v102
	v_mov_b32_e32 v128, v102
	v_mov_b32_e32 v129, v102
	v_mov_b32_e32 v130, v102
	v_mov_b32_e32 v131, v102
	v_mov_b32_e32 v124, v102
	v_mov_b32_e32 v125, v102
	v_mov_b32_e32 v126, v102
	v_mov_b32_e32 v127, v102
	v_mov_b32_e32 v120, v102
	v_mov_b32_e32 v121, v102
	v_mov_b32_e32 v122, v102
	v_mov_b32_e32 v123, v102
	v_mov_b32_e32 v108, v102
	v_mov_b32_e32 v109, v102
.LBB0_510:
	v_add_u32_e32 v4, s17, v134
	v_add_u32_e32 v141, s17, v135
	ds_read_b32 v140, v4
	ds_read_b128 v[4:7], v141
	ds_read_b128 v[136:139], v141 offset:32
	s_addk_i32 s17, 0x80
	s_waitcnt vmcnt(0) lgkmcnt(0)
	v_mfma_f32_32x32x16_bf16 v[20:35], v[64:67], v[4:7], 0
	s_cmpk_lg_i32 s17, 0x800
	v_mfma_f32_32x32x16_bf16 v[4:19], v[48:51], v[4:7], 0
	v_mfma_f32_32x32x16_bf16 v[4:19], v[40:43], v[136:139], v[4:19]
	v_mfma_f32_32x32x16_bf16 v[20:35], v[56:59], v[136:139], v[20:35]
	ds_read_b128 v[136:139], v141 offset:64
	s_waitcnt lgkmcnt(0)
	v_mfma_f32_32x32x16_bf16 v[4:19], v[44:47], v[136:139], v[4:19]
	v_mfma_f32_32x32x16_bf16 v[20:35], v[60:63], v[136:139], v[20:35]
	ds_read_b128 v[136:139], v141 offset:96
	s_waitcnt lgkmcnt(0)
	v_mfma_f32_32x32x16_bf16 v[4:19], v[36:39], v[136:139], v[4:19]
	v_mfma_f32_32x32x16_bf16 v[20:35], v[52:55], v[136:139], v[20:35]
	s_nop 10
	v_max_i32_e32 v5, 0, v5
	v_max_i32_e32 v4, 0, v4
	v_fma_f32 v116, v140, v4, v116
	v_fma_f32 v117, v140, v5, v117
	v_max_i32_e32 v5, 0, v23
	v_max_i32_e32 v4, 0, v22
	v_pk_fma_f32 v[130:131], v[140:141], v[4:5], v[130:131] op_sel_hi:[0,1,1]
	v_max_i32_e32 v5, 0, v7
	v_max_i32_e32 v4, 0, v6
	v_pk_fma_f32 v[118:119], v[140:141], v[4:5], v[118:119] op_sel_hi:[0,1,1]
	v_max_i32_e32 v5, 0, v25
	v_max_i32_e32 v4, 0, v24
	v_pk_fma_f32 v[124:125], v[140:141], v[4:5], v[124:125] op_sel_hi:[0,1,1]
	v_max_i32_e32 v5, 0, v9
	v_max_i32_e32 v4, 0, v8
	v_pk_fma_f32 v[112:113], v[140:141], v[4:5], v[112:113] op_sel_hi:[0,1,1]
	v_max_i32_e32 v5, 0, v27
	v_max_i32_e32 v4, 0, v26
	v_pk_fma_f32 v[126:127], v[140:141], v[4:5], v[126:127] op_sel_hi:[0,1,1]
	v_max_i32_e32 v5, 0, v11
	v_max_i32_e32 v4, 0, v10
	v_pk_fma_f32 v[114:115], v[140:141], v[4:5], v[114:115] op_sel_hi:[0,1,1]
	v_max_i32_e32 v5, 0, v29
	v_max_i32_e32 v4, 0, v28
	v_pk_fma_f32 v[120:121], v[140:141], v[4:5], v[120:121] op_sel_hi:[0,1,1]
	v_max_i32_e32 v5, 0, v13
	v_max_i32_e32 v4, 0, v12
	v_pk_fma_f32 v[104:105], v[140:141], v[4:5], v[104:105] op_sel_hi:[0,1,1]
	v_max_i32_e32 v5, 0, v31
	v_max_i32_e32 v4, 0, v30
	v_pk_fma_f32 v[122:123], v[140:141], v[4:5], v[122:123] op_sel_hi:[0,1,1]
	v_max_i32_e32 v5, 0, v15
	v_max_i32_e32 v4, 0, v14
	v_pk_fma_f32 v[106:107], v[140:141], v[4:5], v[106:107] op_sel_hi:[0,1,1]
	v_max_i32_e32 v5, 0, v33
	v_max_i32_e32 v4, 0, v32
	v_pk_fma_f32 v[108:109], v[140:141], v[4:5], v[108:109] op_sel_hi:[0,1,1]
	v_max_i32_e32 v5, 0, v17
	v_max_i32_e32 v4, 0, v16
	v_pk_fma_f32 v[100:101], v[140:141], v[4:5], v[100:101] op_sel_hi:[0,1,1]
	v_max_i32_e32 v5, 0, v35
	v_max_i32_e32 v4, 0, v34
	v_max_i32_e32 v21, 0, v21
	v_max_i32_e32 v20, 0, v20
	v_pk_fma_f32 v[110:111], v[140:141], v[4:5], v[110:111] op_sel_hi:[0,1,1]
	v_max_i32_e32 v5, 0, v19
	v_max_i32_e32 v4, 0, v18
	v_pk_fma_f32 v[128:129], v[140:141], v[20:21], v[128:129] op_sel_hi:[0,1,1]
	v_pk_fma_f32 v[102:103], v[140:141], v[4:5], v[102:103] op_sel_hi:[0,1,1]
	s_cbranch_scc1 .LBB0_510
	s_lshl_b32 s18, s14, 6
	s_ashr_i32 s19, s18, 31
	v_mov_b64_e32 v[64:65], v[80:81]
	v_mov_b64_e32 v[56:57], v[68:69]
	v_mov_b64_e32 v[60:61], v[72:73]
	v_mov_b64_e32 v[52:53], v[76:77]
	v_mov_b64_e32 v[48:49], v[96:97]
	v_mov_b64_e32 v[40:41], v[84:85]
	v_mov_b64_e32 v[44:45], v[88:89]
	v_mov_b64_e32 v[36:37], v[92:93]
	v_lshl_add_u64 v[4:5], s[18:19], 2, v[132:133]
	s_and_b64 vcc, exec, s[10:11]
	v_mov_b64_e32 v[66:67], v[82:83]
	v_mov_b64_e32 v[58:59], v[70:71]
	v_mov_b64_e32 v[62:63], v[74:75]
	v_mov_b64_e32 v[54:55], v[78:79]
	v_mov_b64_e32 v[50:51], v[98:99]
	v_mov_b64_e32 v[42:43], v[86:87]
	v_mov_b64_e32 v[46:47], v[90:91]
	v_mov_b64_e32 v[38:39], v[94:95]
	s_mov_b32 s14, s16
	global_store_dwordx4 v[4:5], v[128:131], off
	global_store_dwordx4 v[4:5], v[116:119], off offset:128
	global_store_dwordx4 v[4:5], v[124:127], off offset:32
	global_store_dwordx4 v[4:5], v[112:115], off offset:160
	global_store_dwordx4 v[4:5], v[120:123], off offset:64
	global_store_dwordx4 v[4:5], v[104:107], off offset:192
	global_store_dwordx4 v[4:5], v[108:111], off offset:96
	global_store_dwordx4 v[4:5], v[100:103], off offset:224
	s_cbranch_vccz .LBB0_509
	s_branch .LBB0_502

.LBB0_513:
	v_cmp_lt_i32_e32 vcc, v213, v215
	v_lshlrev_b64 v[4:5], 12, v[194:195]
	v_lshl_add_u64 v[4:5], s[8:9], 0, v[4:5]
	v_cndmask_b32_e32 v6, v214, v213, vcc
	v_lshlrev_b32_e32 v6, 2, v6
	v_readlane_b32 s8, v253, 17
	ds_bpermute_b32 v6, v6, v2
	v_readlane_b32 s9, v253, 18
	s_mov_b32 s1, s9
	v_readlane_b32 s10, v253, 19
	v_readlane_b32 s11, v253, 20
	v_writelane_b32 v253, s0, 17
	s_waitcnt lgkmcnt(0)
	v_add_f32_e32 v2, v2, v6
	s_lshl_b32 s8, s17, 1
	v_writelane_b32 v253, s1, 18
	v_writelane_b32 v253, s2, 19
	v_writelane_b32 v253, s3, 20
	v_div_scale_f32 v6, s[0:1], v2, v2, 1.0
	v_rcp_f32_e32 v7, v6
	v_lshl_add_u64 v[4:5], v[4:5], 0, s[8:9]
	s_mov_b64 s[0:1], 0x25800800
	v_fma_f32 v8, -v6, v7, 1.0
	v_fmac_f32_e32 v7, v8, v7
	v_div_scale_f32 v8, vcc, 1.0, v2, 1.0
	v_mul_f32_e32 v9, v8, v7
	v_fma_f32 v10, -v6, v9, v8
	v_fmac_f32_e32 v9, v10, v7
	v_fma_f32 v6, -v6, v9, v8
	v_div_fmas_f32 v6, v6, v7, v9
	v_div_fixup_f32 v6, v6, v2, 1.0
	v_lshlrev_b32_e32 v2, 1, v1
	v_pk_mul_f32 v[8:9], v[130:131], v[6:7] op_sel_hi:[1,0]
	v_pk_mul_f32 v[10:11], v[132:133], v[6:7] op_sel_hi:[1,0]
	v_lshl_add_u64 v[4:5], v[4:5], 0, v[2:3]
	v_cvt_pk_bf16_f32 v8, v8, v9
	v_cvt_pk_bf16_f32 v9, v10, v11
	v_lshl_add_u64 v[10:11], v[4:5], 0, s[0:1]
	s_mov_b32 s0, 0x25800000
	v_add_co_u32_e32 v4, vcc, s0, v4
	s_barrier
	s_nop 0
	v_addc_co_u32_e32 v5, vcc, 0, v5, vcc
	global_store_dwordx2 v[4:5], v[8:9], off offset:2048
	v_pk_mul_f32 v[4:5], v[134:135], v[6:7] op_sel_hi:[1,0]
	v_pk_mul_f32 v[8:9], v[136:137], v[6:7] op_sel_hi:[1,0]
	v_cvt_pk_bf16_f32 v4, v4, v5
	v_cvt_pk_bf16_f32 v5, v8, v9
	global_store_dwordx2 v[10:11], v[4:5], off offset:16
	v_pk_mul_f32 v[4:5], v[138:139], v[6:7] op_sel_hi:[1,0]
	v_pk_mul_f32 v[8:9], v[140:141], v[6:7] op_sel_hi:[1,0]
	v_cvt_pk_bf16_f32 v4, v4, v5
	v_cvt_pk_bf16_f32 v5, v8, v9
	global_store_dwordx2 v[10:11], v[4:5], off offset:32
	v_pk_mul_f32 v[4:5], v[142:143], v[6:7] op_sel_hi:[1,0]
	v_pk_mul_f32 v[8:9], v[144:145], v[6:7] op_sel_hi:[1,0]
	v_cvt_pk_bf16_f32 v4, v4, v5
	v_cvt_pk_bf16_f32 v5, v8, v9
	global_store_dwordx2 v[10:11], v[4:5], off offset:48
	v_pk_mul_f32 v[4:5], v[114:115], v[6:7] op_sel_hi:[1,0]
	v_pk_mul_f32 v[8:9], v[116:117], v[6:7] op_sel_hi:[1,0]
	v_cvt_pk_bf16_f32 v4, v4, v5
	v_cvt_pk_bf16_f32 v5, v8, v9
	global_store_dwordx2 v[10:11], v[4:5], off offset:64
	v_pk_mul_f32 v[4:5], v[118:119], v[6:7] op_sel_hi:[1,0]
	v_pk_mul_f32 v[8:9], v[120:121], v[6:7] op_sel_hi:[1,0]
	v_cvt_pk_bf16_f32 v4, v4, v5
	v_cvt_pk_bf16_f32 v5, v8, v9
	global_store_dwordx2 v[10:11], v[4:5], off offset:80
	v_pk_mul_f32 v[4:5], v[122:123], v[6:7] op_sel_hi:[1,0]
	v_pk_mul_f32 v[8:9], v[124:125], v[6:7] op_sel_hi:[1,0]
	v_cvt_pk_bf16_f32 v4, v4, v5
	v_cvt_pk_bf16_f32 v5, v8, v9
	global_store_dwordx2 v[10:11], v[4:5], off offset:96
	v_pk_mul_f32 v[4:5], v[126:127], v[6:7] op_sel_hi:[1,0]
	v_pk_mul_f32 v[8:9], v[128:129], v[6:7] op_sel_hi:[1,0]
	v_cvt_pk_bf16_f32 v4, v4, v5
	v_cvt_pk_bf16_f32 v5, v8, v9
	global_store_dwordx2 v[10:11], v[4:5], off offset:112
	v_pk_mul_f32 v[4:5], v[98:99], v[6:7] op_sel_hi:[1,0]
	v_pk_mul_f32 v[8:9], v[100:101], v[6:7] op_sel_hi:[1,0]
	v_cvt_pk_bf16_f32 v4, v4, v5
	v_cvt_pk_bf16_f32 v5, v8, v9
	global_store_dwordx2 v[10:11], v[4:5], off offset:128
	v_pk_mul_f32 v[4:5], v[102:103], v[6:7] op_sel_hi:[1,0]
	v_pk_mul_f32 v[8:9], v[104:105], v[6:7] op_sel_hi:[1,0]
	v_cvt_pk_bf16_f32 v4, v4, v5
	v_cvt_pk_bf16_f32 v5, v8, v9
	global_store_dwordx2 v[10:11], v[4:5], off offset:144
	v_pk_mul_f32 v[4:5], v[106:107], v[6:7] op_sel_hi:[1,0]
	v_pk_mul_f32 v[8:9], v[108:109], v[6:7] op_sel_hi:[1,0]
	v_cvt_pk_bf16_f32 v4, v4, v5
	v_cvt_pk_bf16_f32 v5, v8, v9
	global_store_dwordx2 v[10:11], v[4:5], off offset:160
	v_pk_mul_f32 v[4:5], v[110:111], v[6:7] op_sel_hi:[1,0]
	v_pk_mul_f32 v[8:9], v[112:113], v[6:7] op_sel_hi:[1,0]
	v_cvt_pk_bf16_f32 v4, v4, v5
	v_cvt_pk_bf16_f32 v5, v8, v9
	global_store_dwordx2 v[10:11], v[4:5], off offset:176
	v_pk_mul_f32 v[4:5], v[82:83], v[6:7] op_sel_hi:[1,0]
	v_pk_mul_f32 v[8:9], v[84:85], v[6:7] op_sel_hi:[1,0]
	v_cvt_pk_bf16_f32 v4, v4, v5
	v_cvt_pk_bf16_f32 v5, v8, v9
	global_store_dwordx2 v[10:11], v[4:5], off offset:192
	v_pk_mul_f32 v[4:5], v[86:87], v[6:7] op_sel_hi:[1,0]
	v_pk_mul_f32 v[8:9], v[88:89], v[6:7] op_sel_hi:[1,0]
	v_cvt_pk_bf16_f32 v4, v4, v5
	v_cvt_pk_bf16_f32 v5, v8, v9
	global_store_dwordx2 v[10:11], v[4:5], off offset:208
	v_pk_mul_f32 v[4:5], v[90:91], v[6:7] op_sel_hi:[1,0]
	v_pk_mul_f32 v[8:9], v[92:93], v[6:7] op_sel_hi:[1,0]
	v_cvt_pk_bf16_f32 v4, v4, v5
	v_cvt_pk_bf16_f32 v5, v8, v9
	global_store_dwordx2 v[10:11], v[4:5], off offset:224
	v_pk_mul_f32 v[4:5], v[94:95], v[6:7] op_sel_hi:[1,0]
	v_pk_mul_f32 v[6:7], v[96:97], v[6:7] op_sel_hi:[1,0]
	v_cvt_pk_bf16_f32 v4, v4, v5
	v_cvt_pk_bf16_f32 v5, v6, v7
	s_mov_b64 s[0:1], 0
	s_movk_i32 s20, 0x110
	global_store_dwordx2 v[10:11], v[4:5], off offset:240

.LBB0_515:
	s_waitcnt lgkmcnt(0)
	s_barrier
	s_and_saveexec_b64 s[0:1], s[36:37]
	s_cbranch_execz .LBB0_517
	s_waitcnt vmcnt(0)
	v_mov_b64_e32 v[4:5], s[6:7]
	global_atomic_add v1, v[4:5], v228, off sc0
	v_mov_b32_e32 v2, s16
	s_waitcnt vmcnt(0) lgkmcnt(0)
	ds_write_b32 v2, v1
.LBB0_517:
	s_or_b64 exec, exec, s[0:1]
	v_mov_b32_e32 v1, s16
	s_waitcnt lgkmcnt(0)
	s_barrier
	ds_read_b32 v1, v1
	s_mov_b64 s[0:1], -1
	s_waitcnt lgkmcnt(0)
	v_cmp_lt_i32_e32 vcc, s75, v1
	v_readfirstlane_b32 s8, v1
	s_cbranch_vccnz .LBB0_514
	s_lshl_b32 s0, s8, 4
	v_mov_b32_e32 v208, v0
	s_and_b32 s19, s0, 0xffffff00
	s_bfe_u32 s10, s8, 0x20002
	v_readfirstlane_b32 s0, v208
	s_ashr_i32 s0, s0, 1
	s_and_b32 s11, s8, 3
	s_mov_b32 s1, s88
	v_readlane_b32 s8, v252, 0
	s_andn2_b32 s0, s0, 31
	s_sub_i32 s21, s0, s19
	s_mov_b64 s[8:9], s[68:69]
	s_add_i32 s18, s21, 0xf00
	s_lshl_b32 s17, s11, 7
	s_lshl_b32 s0, s11, 8
	s_add_u32 s12, s8, s0
	s_addc_u32 s13, s9, 0
	s_add_u32 s0, s12, 0x9001000
	s_mul_i32 s14, s10, 0x480
	s_addc_u32 s1, s13, 0
	s_add_i32 s14, s14, s17
	s_mul_i32 s22, s14, 0x2100
	s_add_i32 s22, s22, 0x420000
	s_add_u32 s14, s8, s22
	s_addc_u32 s15, s9, 0
	s_add_u32 s14, s14, 0x2b800000
	v_and_b32_e32 v1, 31, v208
	s_addc_u32 s15, s15, 0
	s_lshl_b32 s20, s10, 16
	s_lshl_b32 s11, s11, 14
	v_or_b32_e32 v211, s18, v1
	s_or_b32 s11, s20, s11
	s_lshl_b32 s23, s10, 12
	s_waitcnt vmcnt(0)
	v_bfe_u32 v5, v208, 5, 1
	v_add_u32_e32 v194, s23, v211
	v_mov_b64_e32 v[6:7], s[0:1]
	s_add_u32 s12, s12, 0x9001400
	v_mad_i64_i32 v[6:7], s[0:1], v194, s24, v[6:7]
	v_lshlrev_b32_e32 v196, 4, v5
	v_mov_b32_e32 v197, v3
	s_addc_u32 s13, s13, 0
	v_lshl_add_u64 v[6:7], v[6:7], 0, v[196:197]
	s_add_u32 s0, s8, s11
	global_load_dwordx4 v[174:177], v[6:7], off
	global_load_dwordx4 v[170:173], v[6:7], off offset:32
	global_load_dwordx4 v[166:169], v[6:7], off offset:64
	global_load_dwordx4 v[162:165], v[6:7], off offset:96
	global_load_dwordx4 v[158:161], v[6:7], off offset:128
	global_load_dwordx4 v[154:157], v[6:7], off offset:160
	global_load_dwordx4 v[150:153], v[6:7], off offset:192
	global_load_dwordx4 v[146:149], v[6:7], off offset:224
	s_addc_u32 s1, s9, 0
	v_ashrrev_i32_e32 v6, 4, v208
	s_add_u32 s10, s0, 0x49200000
	v_add_u32_e32 v2, s23, v6
	v_mov_b64_e32 v[10:11], s[12:13]
	s_addc_u32 s11, s1, 0
	v_mad_i64_i32 v[8:9], s[0:1], v2, s24, v[10:11]
	v_lshlrev_b32_e32 v2, 3, v208
	v_and_b32_e32 v2, 0x78, v2
	v_lshlrev_b32_e32 v2, 1, v2
	v_lshl_add_u64 v[8:9], v[8:9], 0, v[2:3]
	s_waitcnt lgkmcnt(0)
	s_barrier
	global_load_dwordx4 v[12:15], v[8:9], off
	v_add_u32_e32 v9, 0x200, v208
	v_ashrrev_i32_e32 v7, 4, v9
	v_ashrrev_i32_e32 v8, 3, v208
	v_mov_b64_e32 v[24:25], s[14:15]
	s_movk_i32 s14, 0x2100
	v_lshlrev_b32_e32 v28, 4, v208
	v_add_u32_e32 v20, s23, v7
	v_mad_i64_i32 v[16:17], s[0:1], v8, s14, v[24:25]
	v_and_b32_e32 v198, 0x70, v28
	v_mov_b32_e32 v199, v3
	v_mad_i64_i32 v[10:11], s[0:1], v20, s24, v[10:11]
	v_lshl_add_u64 v[16:17], v[16:17], 0, v[198:199]
	v_lshl_add_u64 v[10:11], v[10:11], 0, v[2:3]
	v_ashrrev_i32_e32 v9, 3, v9
	global_load_dwordx4 v[16:19], v[16:17], off
	v_and_b32_e32 v4, 63, v208
	global_load_dwordx4 v[20:23], v[10:11], off
	v_mad_i64_i32 v[10:11], s[0:1], v9, s14, v[24:25]
	v_lshl_add_u64 v[10:11], v[10:11], 0, v[198:199]
	global_load_dwordx4 v[24:27], v[10:11], off
	v_lshlrev_b32_e32 v10, 2, v4
	v_mov_b32_e32 v11, v3
	v_lshl_add_u64 v[10:11], s[10:11], 0, v[10:11]
	global_load_dword v10, v[10:11], off
	s_movk_i32 s25, 0x110
	v_mul_lo_u32 v209, v6, s25
	v_and_b32_e32 v213, 0xf0, v28
	s_movk_i32 s0, 0x88
	v_add3_u32 v11, s72, v209, v213
	v_mul_lo_u32 v214, v8, s0
	s_movk_i32 s1, 0x4400
	v_mul_lo_u32 v215, v7, s25
	v_mul_lo_u32 v216, v9, s0
	s_waitcnt vmcnt(0) lgkmcnt(0)
	ds_write_b128 v11, v[12:15]
	v_add_u32_e32 v11, s72, v214
	v_add3_u32 v11, v11, v198, s1
	ds_write2_b64 v11, v[16:17], v[18:19] offset1:1
	v_add3_u32 v11, s72, v215, v213
	ds_write_b128 v11, v[20:23]
	v_add_u32_e32 v11, s72, v216
	v_add3_u32 v11, v11, v198, s1
	v_cmp_gt_i32_e64 s[0:1], 64, v208
	ds_write2_b64 v11, v[24:25], v[26:27] offset1:1
	s_and_saveexec_b64 s[14:15], s[0:1]
	v_mul_f32_e32 v10, 0x3fb8aa3b, v10
	v_lshl_add_u32 v11, v208, 2, s72
	ds_write_b32 v11, v10 offset:34816
	s_or_b64 exec, exec, s[14:15]
	s_movk_i32 s20, 0x2100
	v_mad_i64_i32 v[10:11], s[14:15], v8, s20, 0
	v_mad_i64_i32 v[8:9], s[14:15], v9, s20, 0
	s_sub_i32 s14, 0x1000, s19
	s_lshr_b32 s15, s14, 6
	s_add_i32 s19, s21, 0xf1f
	v_lshl_add_u64 v[200:201], s[12:13], 0, v[2:3]
	s_add_u32 s12, s8, s22
	v_and_b32_e32 v2, 7, v208
	s_addc_u32 s13, s9, 0
	v_lshlrev_b32_e32 v2, 4, v2
	s_add_u32 s12, s12, 0x2b800080
	v_lshlrev_b32_e32 v197, 3, v5
	v_mul_u32_u24_e32 v217, 0x110, v1
	v_mul_u32_u24_e32 v199, 0x88, v1
	v_lshlrev_b32_e32 v1, 2, v5
	v_or_b32_e32 v218, 64, v4
	v_lshl_add_u64 v[4:5], v[8:9], 0, v[2:3]
	s_addc_u32 s13, s13, 0
	v_lshl_add_u64 v[202:203], s[12:13], 0, v[4:5]
	v_lshl_add_u64 v[4:5], v[10:11], 0, v[2:3]
	v_mov_b32_e32 v16, v3
	v_mov_b32_e32 v17, v3
	v_add3_u32 v219, v7, s23, 64
	v_add3_u32 v220, v6, s23, 64
	v_lshl_add_u64 v[204:205], s[12:13], 0, v[4:5]
	v_mov_b32_e32 v2, v3
	v_mov_b32_e32 v4, v3
	v_mov_b32_e32 v5, v3
	v_mov_b32_e32 v6, v3
	v_mov_b32_e32 v7, v3
	v_mov_b32_e32 v8, v3
	v_mov_b32_e32 v9, v3
	v_mov_b32_e32 v10, v3
	v_mov_b32_e32 v11, v3
	v_mov_b32_e32 v12, v3
	v_mov_b32_e32 v13, v3
	v_mov_b32_e32 v14, v3
	v_mov_b32_e32 v15, v3
	v_mov_b64_e32 v[32:33], v[16:17]
	v_mov_b64_e32 v[48:49], v[16:17]
	v_mov_b64_e32 v[64:65], v[16:17]
	v_mov_b64_e32 v[80:81], v[16:17]
	v_ashrrev_i32_e32 v195, 31, v194
	s_mov_b32 s20, 1
	s_mov_b32 s14, 0
	v_mov_b32_e32 v212, 0xf149f2ca
	v_mov_b32_e32 v210, 0
	v_mov_b64_e32 v[30:31], v[14:15]
	v_mov_b64_e32 v[28:29], v[12:13]
	v_mov_b64_e32 v[26:27], v[10:11]
	v_mov_b64_e32 v[24:25], v[8:9]
	v_mov_b64_e32 v[22:23], v[6:7]
	v_mov_b64_e32 v[20:21], v[4:5]
	v_mov_b64_e32 v[18:19], v[2:3]
	v_mov_b64_e32 v[46:47], v[14:15]
	v_mov_b64_e32 v[44:45], v[12:13]
	v_mov_b64_e32 v[42:43], v[10:11]
	v_mov_b64_e32 v[40:41], v[8:9]
	v_mov_b64_e32 v[38:39], v[6:7]
	v_mov_b64_e32 v[36:37], v[4:5]
	v_mov_b64_e32 v[34:35], v[2:3]
	v_mov_b64_e32 v[62:63], v[14:15]
	v_mov_b64_e32 v[60:61], v[12:13]
	v_mov_b64_e32 v[58:59], v[10:11]
	v_mov_b64_e32 v[56:57], v[8:9]
	v_mov_b64_e32 v[54:55], v[6:7]
	v_mov_b64_e32 v[52:53], v[4:5]
	v_mov_b64_e32 v[50:51], v[2:3]
	v_mov_b64_e32 v[78:79], v[14:15]
	v_mov_b64_e32 v[76:77], v[12:13]
	v_mov_b64_e32 v[74:75], v[10:11]
	v_mov_b64_e32 v[72:73], v[8:9]
	v_mov_b64_e32 v[70:71], v[6:7]
	v_mov_b64_e32 v[68:69], v[4:5]
	v_mov_b64_e32 v[66:67], v[2:3]
	s_mov_b32 s25, 0x800000
	s_movk_i32 s24, 0x7200
	s_waitcnt lgkmcnt(0)
	s_barrier
	s_branch .LBB0_522

.LBB0_522:
	v_add_u32_e32 v2, s14, v220
	v_mad_i64_i32 v[4:5], s[12:13], v2, s24, v[200:201]
	v_add_u32_e32 v2, s14, v219
	v_mad_i64_i32 v[6:7], s[12:13], v2, s24, v[200:201]
	v_add_u32_e32 v2, s14, v218
	global_load_dwordx4 v[8:11], v[204:205], off
	global_load_dwordx4 v[114:117], v[4:5], off
	global_load_dwordx4 v[12:15], v[6:7], off
	s_nop 0
	global_load_dwordx4 v[4:7], v[202:203], off
	v_lshl_add_u64 v[16:17], v[2:3], 2, s[10:11]
	global_load_dword v2, v[16:17], off
	s_cmp_gt_i32 s14, s19
	s_cbranch_scc1 .LBB0_528
	s_bitcmp1_b32 s20, 0
	s_cselect_b32 s12, 0, 0x8900
	s_add_i32 s12, s72, s12
	v_add3_u32 v16, s12, v217, v196
	ds_read_b128 v[82:85], v16
	ds_read_b128 v[118:121], v16 offset:32
	ds_read_b128 v[86:89], v16 offset:8704
	ds_read_b128 v[122:125], v16 offset:8736
	ds_read_b128 v[126:129], v16 offset:64
	ds_read_b128 v[130:133], v16 offset:96
	ds_read_b128 v[134:137], v16 offset:8768
	ds_read_b128 v[138:141], v16 offset:8800
	s_waitcnt lgkmcnt(0)
	v_mfma_f32_32x32x16_bf16 v[98:113], v[82:85], v[174:177], 0
	v_mfma_f32_32x32x16_bf16 v[82:97], v[86:89], v[174:177], 0
	v_mfma_f32_32x32x16_bf16 v[98:113], v[118:121], v[170:173], v[98:113]
	v_mfma_f32_32x32x16_bf16 v[82:97], v[122:125], v[170:173], v[82:97]
	v_mfma_f32_32x32x16_bf16 v[98:113], v[126:129], v[166:169], v[98:113]
	v_mfma_f32_32x32x16_bf16 v[82:97], v[134:137], v[166:169], v[82:97]
	v_mfma_f32_32x32x16_bf16 v[98:113], v[130:133], v[162:165], v[98:113]
	v_mfma_f32_32x32x16_bf16 v[82:97], v[138:141], v[162:165], v[82:97]
	ds_read_b128 v[118:121], v16 offset:128
	ds_read_b128 v[122:125], v16 offset:160
	ds_read_b128 v[126:129], v16 offset:8832
	ds_read_b128 v[130:133], v16 offset:8864
	ds_read_b128 v[134:137], v16 offset:192
	ds_read_b128 v[142:145], v16 offset:224
	ds_read_b128 v[138:141], v16 offset:8896
	ds_read_b128 v[182:185], v16 offset:8928
	s_waitcnt lgkmcnt(0)
	v_mfma_f32_32x32x16_bf16 v[98:113], v[118:121], v[158:161], v[98:113]
	v_add_u32_e32 v16, s12, v199
	v_add_u32_e32 v221, v16, v197
	v_add_u32_e32 v16, 0x4000, v221
	v_mfma_f32_32x32x16_bf16 v[82:97], v[126:129], v[158:161], v[82:97]
	v_mfma_f32_32x32x16_bf16 v[98:113], v[122:125], v[154:157], v[98:113]
	v_mfma_f32_32x32x16_bf16 v[82:97], v[130:133], v[154:157], v[82:97]
	v_mfma_f32_32x32x16_bf16 v[98:113], v[134:137], v[150:153], v[98:113]
	v_mfma_f32_32x32x16_bf16 v[82:97], v[138:141], v[150:153], v[82:97]
	ds_read2_b64 v[178:181], v16 offset0:128 offset1:130
	ds_read2_b64 v[138:141], v16 offset0:132 offset1:134
	v_mfma_f32_32x32x16_bf16 v[98:113], v[142:145], v[146:149], v[98:113]
	ds_read2_b64 v[142:145], v16 offset0:136 offset1:138
	ds_read2_b64 v[134:137], v16 offset0:140 offset1:142
	v_add_u32_e32 v16, 0x5000, v221
	ds_read2_b64 v[130:133], v16 offset0:160 offset1:162
	ds_read2_b64 v[126:129], v16 offset0:164 offset1:166
	ds_read2_b64 v[122:125], v16 offset0:168 offset1:170
	ds_read2_b64 v[118:121], v16 offset0:172 offset1:174
	v_mfma_f32_32x32x16_bf16 v[82:97], v[182:185], v[146:149], v[82:97]
	v_lshl_add_u32 v16, v1, 2, s12
	ds_read_b128 v[182:185], v16 offset:34816
	ds_read_b128 v[186:189], v16 offset:34848
	ds_read_b128 v[222:225], v16 offset:34944
	ds_read_b128 v[232:235], v16 offset:34976
	ds_read_b128 v[236:239], v16 offset:34880
	ds_read_b128 v[242:245], v16 offset:34912
	ds_read_b128 v[246:249], v16 offset:35008
	ds_read_b128 v[190:193], v16 offset:35040
	s_add_i32 s13, s14, 63
	s_waitcnt lgkmcnt(0)
	v_xor_b32_e32 v185, 0x80000000, v185
	v_xor_b32_e32 v184, 0x80000000, v184
	v_xor_b32_e32 v17, 0x80000000, v245
	v_xor_b32_e32 v16, 0x80000000, v244
	s_mov_b32 s12, 0x3e0293ee
	v_xor_b32_e32 v189, 0x80000000, v189
	v_xor_b32_e32 v188, 0x80000000, v188
	v_xor_b32_e32 v239, 0x80000000, v239
	v_xor_b32_e32 v238, 0x80000000, v238
	v_pk_fma_f32 v[206:207], v[102:103], s[12:13], v[186:187] op_sel_hi:[1,0,1] neg_lo:[0,0,1] neg_hi:[0,0,1]
	v_pk_fma_f32 v[16:17], v[112:113], s[12:13], v[16:17] op_sel_hi:[1,0,1]
	v_pk_fma_f32 v[100:101], v[100:101], s[12:13], v[184:185] op_sel_hi:[1,0,1]
	v_pk_fma_f32 v[98:99], v[98:99], s[12:13], v[182:183] op_sel_hi:[1,0,1] neg_lo:[0,0,1] neg_hi:[0,0,1]
	v_xor_b32_e32 v113, 0x80000000, v225
	v_xor_b32_e32 v112, 0x80000000, v224
	v_xor_b32_e32 v183, 0x80000000, v235
	v_xor_b32_e32 v182, 0x80000000, v234
	v_xor_b32_e32 v185, 0x80000000, v249
	v_xor_b32_e32 v184, 0x80000000, v248
	v_xor_b32_e32 v187, 0x80000000, v193
	v_xor_b32_e32 v186, 0x80000000, v192
	v_pk_fma_f32 v[110:111], v[110:111], s[12:13], v[242:243] op_sel_hi:[1,0,1] neg_lo:[0,0,1] neg_hi:[0,0,1]
	v_pk_fma_f32 v[106:107], v[106:107], s[12:13], v[236:237] op_sel_hi:[1,0,1] neg_lo:[0,0,1] neg_hi:[0,0,1]
	v_pk_fma_f32 v[102:103], v[108:109], s[12:13], v[238:239] op_sel_hi:[1,0,1]
	v_pk_fma_f32 v[104:105], v[104:105], s[12:13], v[188:189] op_sel_hi:[1,0,1]
	v_pk_fma_f32 v[94:95], v[94:95], s[12:13], v[190:191] op_sel_hi:[1,0,1] neg_lo:[0,0,1] neg_hi:[0,0,1]
	v_pk_fma_f32 v[90:91], v[90:91], s[12:13], v[246:247] op_sel_hi:[1,0,1] neg_lo:[0,0,1] neg_hi:[0,0,1]
	v_pk_fma_f32 v[108:109], v[86:87], s[12:13], v[232:233] op_sel_hi:[1,0,1] neg_lo:[0,0,1] neg_hi:[0,0,1]
	v_pk_fma_f32 v[86:87], v[96:97], s[12:13], v[186:187] op_sel_hi:[1,0,1]
	v_pk_fma_f32 v[92:93], v[92:93], s[12:13], v[184:185] op_sel_hi:[1,0,1]
	v_pk_fma_f32 v[88:89], v[88:89], s[12:13], v[182:183] op_sel_hi:[1,0,1]
	v_pk_fma_f32 v[84:85], v[84:85], s[12:13], v[112:113] op_sel_hi:[1,0,1]
	s_cmp_le_i32 s13, s18
	v_pk_fma_f32 v[82:83], v[82:83], s[12:13], v[222:223] op_sel_hi:[1,0,1] neg_lo:[0,0,1] neg_hi:[0,0,1]
	s_cbranch_scc1 .LBB0_525
	v_add_u32_e32 v96, s14, v1
	v_add_u32_e32 v97, 32, v96
	v_cmp_le_i32_e32 vcc, v97, v211
	v_add_u32_e32 v97, 33, v96
	s_nop 0
	v_cndmask_b32_e32 v82, v229, v82, vcc
	v_cmp_lt_i32_e32 vcc, v96, v211
	s_nop 1
	v_cndmask_b32_e32 v99, v229, v99, vcc
	v_cmp_le_i32_e32 vcc, v96, v211
	s_nop 1
	v_cndmask_b32_e32 v98, v229, v98, vcc
	v_cmp_le_i32_e32 vcc, v97, v211
	v_add_u32_e32 v97, 2, v96
	s_nop 0
	v_cndmask_b32_e32 v83, v229, v83, vcc
	v_cmp_le_i32_e32 vcc, v97, v211
	v_add_u32_e32 v97, 34, v96
	s_nop 0
	v_cndmask_b32_e32 v100, v229, v100, vcc
	v_cmp_le_i32_e32 vcc, v97, v211
	v_add_u32_e32 v97, 3, v96
	s_nop 0
	v_cndmask_b32_e32 v84, v229, v84, vcc
	v_cmp_le_i32_e32 vcc, v97, v211
	v_add_u32_e32 v97, 35, v96
	s_nop 0
	v_cndmask_b32_e32 v101, v229, v101, vcc
	v_cmp_le_i32_e32 vcc, v97, v211
	v_add_u32_e32 v97, 8, v96
	s_nop 0
	v_cndmask_b32_e32 v85, v229, v85, vcc
	v_cmp_le_i32_e32 vcc, v97, v211
	v_add_u32_e32 v97, 40, v96
	s_nop 0
	v_cndmask_b32_e32 v206, v229, v206, vcc
	v_cmp_le_i32_e32 vcc, v97, v211
	v_add_u32_e32 v97, 9, v96
	s_nop 0
	v_cndmask_b32_e32 v108, v229, v108, vcc
	v_cmp_le_i32_e32 vcc, v97, v211
	v_add_u32_e32 v97, 41, v96
	s_nop 0
	v_cndmask_b32_e32 v207, v229, v207, vcc
	v_cmp_le_i32_e32 vcc, v97, v211
	v_add_u32_e32 v97, 10, v96
	s_nop 0
	v_cndmask_b32_e32 v109, v229, v109, vcc
	v_cmp_le_i32_e32 vcc, v97, v211
	v_add_u32_e32 v97, 42, v96
	s_nop 0
	v_cndmask_b32_e32 v104, v229, v104, vcc
	v_cmp_le_i32_e32 vcc, v97, v211
	v_add_u32_e32 v97, 11, v96
	s_nop 0
	v_cndmask_b32_e32 v88, v229, v88, vcc
	v_cmp_le_i32_e32 vcc, v97, v211
	v_add_u32_e32 v97, 43, v96
	s_nop 0
	v_cndmask_b32_e32 v105, v229, v105, vcc
	v_cmp_le_i32_e32 vcc, v97, v211
	v_add_u32_e32 v97, 16, v96
	s_nop 0
	v_cndmask_b32_e32 v89, v229, v89, vcc
	v_cmp_le_i32_e32 vcc, v97, v211
	v_add_u32_e32 v97, 48, v96
	s_nop 0
	v_cndmask_b32_e32 v106, v229, v106, vcc
	v_cmp_le_i32_e32 vcc, v97, v211
	v_add_u32_e32 v97, 17, v96
	s_nop 0
	v_cndmask_b32_e32 v90, v229, v90, vcc
	v_cmp_le_i32_e32 vcc, v97, v211
	v_add_u32_e32 v97, 49, v96
	s_nop 0
	v_cndmask_b32_e32 v107, v229, v107, vcc
	v_cmp_le_i32_e32 vcc, v97, v211
	v_add_u32_e32 v97, 18, v96
	s_nop 0
	v_cndmask_b32_e32 v91, v229, v91, vcc
	v_cmp_le_i32_e32 vcc, v97, v211
	v_add_u32_e32 v97, 50, v96
	s_nop 0
	v_cndmask_b32_e32 v102, v229, v102, vcc
	v_cmp_le_i32_e32 vcc, v97, v211
	v_add_u32_e32 v97, 19, v96
	s_nop 0
	v_cndmask_b32_e32 v92, v229, v92, vcc
	v_cmp_le_i32_e32 vcc, v97, v211
	v_add_u32_e32 v97, 51, v96
	s_nop 0
	v_cndmask_b32_e32 v103, v229, v103, vcc
	v_cmp_le_i32_e32 vcc, v97, v211
	v_add_u32_e32 v97, 24, v96
	s_nop 0
	v_cndmask_b32_e32 v93, v229, v93, vcc
	v_cmp_le_i32_e32 vcc, v97, v211
	v_add_u32_e32 v97, 56, v96
	s_nop 0
	v_cndmask_b32_e32 v110, v229, v110, vcc
	v_cmp_le_i32_e32 vcc, v97, v211
	v_add_u32_e32 v97, 25, v96
	s_nop 0
	v_cndmask_b32_e32 v94, v229, v94, vcc
	v_cmp_le_i32_e32 vcc, v97, v211
	v_add_u32_e32 v97, 57, v96
	s_nop 0
	v_cndmask_b32_e32 v111, v229, v111, vcc
	v_cmp_le_i32_e32 vcc, v97, v211
	v_add_u32_e32 v97, 26, v96
	s_nop 0
	v_cndmask_b32_e32 v95, v229, v95, vcc
	v_cmp_le_i32_e32 vcc, v97, v211
	v_add_u32_e32 v97, 58, v96
	s_nop 0
	v_cndmask_b32_e32 v16, v229, v16, vcc
	v_cmp_le_i32_e32 vcc, v97, v211
	v_add_u32_e32 v97, 27, v96
	v_add_u32_e32 v96, 59, v96
	v_cndmask_b32_e32 v86, v229, v86, vcc
	v_cmp_le_i32_e32 vcc, v97, v211
	s_nop 1
	v_cndmask_b32_e32 v17, v229, v17, vcc
	v_cmp_le_i32_e32 vcc, v96, v211
	s_nop 1
	v_cndmask_b32_e32 v87, v229, v87, vcc

.LBB0_540:
	s_waitcnt lgkmcnt(0)
	s_barrier
	s_and_saveexec_b64 s[6:7], s[0:1]
	s_cbranch_execz .LBB0_542
	s_waitcnt vmcnt(0)
	v_mov_b64_e32 v[4:5], s[4:5]
	global_atomic_add v1, v[4:5], v228, off sc0
	v_mov_b32_e32 v2, s8
	s_waitcnt vmcnt(0) lgkmcnt(0)
	ds_write_b32 v2, v1

.LBB0_544:
	v_lshl_add_u64 v[4:5], v[38:39], 0, s[6:7]
	v_add_co_u32_e32 v6, vcc, s10, v4
	s_mov_b32 s9, 0x4b908000
	s_nop 0
	v_addc_co_u32_e32 v7, vcc, 0, v5, vcc
	global_load_dwordx4 v[76:79], v[6:7], off
	v_add_co_u32_e32 v6, vcc, s11, v4
	v_lshl_add_u64 v[72:73], v[40:41], 0, s[6:7]
	s_nop 0
	v_addc_co_u32_e32 v7, vcc, 0, v5, vcc
	global_load_dwordx4 v[28:31], v[6:7], off
	v_add_co_u32_e32 v6, vcc, s12, v4
	v_mov_b32_e32 v35, v34
	s_nop 0
	v_addc_co_u32_e32 v7, vcc, 0, v5, vcc
	global_load_dwordx4 v[24:27], v[6:7], off
	v_add_co_u32_e32 v6, vcc, s13, v4
	v_cvt_pk_bf16_f32 v81, v46, v47
	s_nop 0
	v_addc_co_u32_e32 v7, vcc, 0, v5, vcc
	global_load_dwordx4 v[20:23], v[6:7], off
	v_add_co_u32_e32 v6, vcc, s9, v4
	s_mov_b32 s9, 0x4b90a000
	s_nop 0
	v_addc_co_u32_e32 v7, vcc, 0, v5, vcc
	global_load_dwordx4 v[16:19], v[6:7], off
	v_add_co_u32_e32 v6, vcc, s9, v4
	s_mov_b32 s9, 0x4b90c000
	s_nop 0
	v_addc_co_u32_e32 v7, vcc, 0, v5, vcc
	global_load_dwordx4 v[12:15], v[6:7], off
	v_add_co_u32_e32 v6, vcc, s9, v4
	s_mov_b32 s9, 0x4b90e000
	s_nop 0
	v_addc_co_u32_e32 v7, vcc, 0, v5, vcc
	v_add_co_u32_e32 v4, vcc, s9, v4
	global_load_dwordx4 v[8:11], v[6:7], off
	s_nop 0
	v_addc_co_u32_e32 v5, vcc, 0, v5, vcc
	global_load_dwordx4 v[4:7], v[4:5], off
	v_add_co_u32_e32 v82, vcc, s10, v72
	s_mov_b32 s9, 0x4b901000
	s_nop 0
	v_addc_co_u32_e32 v83, vcc, 0, v73, vcc
	v_cvt_pk_bf16_f32 v80, v44, v45
	s_waitcnt vmcnt(0)
	s_add_u32 s6, s6, 0x10000
	s_addc_u32 s7, s7, 0
	s_cmp_eq_u32 s6, 0x200000
	s_waitcnt lgkmcnt(0)
	s_barrier
	global_store_dwordx2 v[82:83], v[80:81], off
	s_waitcnt vmcnt(0)
	v_pk_fma_f32 v[46:47], v[34:35], v[46:47], v[78:79]
	v_add_co_u32_e32 v78, vcc, s9, v72
	v_pk_fma_f32 v[44:45], v[36:37], v[44:45], v[76:77]
	s_nop 0
	v_addc_co_u32_e32 v79, vcc, 0, v73, vcc
	v_cvt_pk_bf16_f32 v77, v50, v51
	v_pk_fma_f32 v[50:51], v[34:35], v[50:51], v[30:31]
	v_add_co_u32_e32 v30, vcc, s11, v72
	s_mov_b32 s9, 0x4b903000
	s_nop 0
	v_addc_co_u32_e32 v31, vcc, 0, v73, vcc
	v_cvt_pk_bf16_f32 v76, v48, v49
	v_pk_fma_f32 v[48:49], v[36:37], v[48:49], v[28:29]
	v_cvt_pk_bf16_f32 v29, v54, v55
	v_pk_fma_f32 v[54:55], v[34:35], v[54:55], v[26:27]
	v_add_co_u32_e32 v26, vcc, s9, v72
	v_cvt_pk_bf16_f32 v28, v52, v53
	s_nop 0
	v_addc_co_u32_e32 v27, vcc, 0, v73, vcc
	v_pk_fma_f32 v[52:53], v[36:37], v[52:53], v[24:25]
	v_cvt_pk_bf16_f32 v25, v58, v59
	v_pk_fma_f32 v[58:59], v[34:35], v[58:59], v[22:23]
	v_add_co_u32_e32 v22, vcc, s12, v72
	s_mov_b32 s9, 0x4b905000
	s_nop 0
	v_addc_co_u32_e32 v23, vcc, 0, v73, vcc
	v_cvt_pk_bf16_f32 v24, v56, v57
	v_pk_fma_f32 v[56:57], v[36:37], v[56:57], v[20:21]
	v_cvt_pk_bf16_f32 v21, v62, v63
	v_pk_fma_f32 v[62:63], v[34:35], v[62:63], v[18:19]
	v_add_co_u32_e32 v18, vcc, s9, v72
	v_cvt_pk_bf16_f32 v20, v60, v61
	s_nop 0
	v_addc_co_u32_e32 v19, vcc, 0, v73, vcc
	v_pk_fma_f32 v[60:61], v[36:37], v[60:61], v[16:17]
	v_cvt_pk_bf16_f32 v17, v66, v67
	v_pk_fma_f32 v[66:67], v[34:35], v[66:67], v[14:15]
	v_add_co_u32_e32 v14, vcc, s13, v72
	s_mov_b32 s9, 0x4b907000
	s_nop 0
	v_addc_co_u32_e32 v15, vcc, 0, v73, vcc
	v_cvt_pk_bf16_f32 v16, v64, v65
	v_pk_fma_f32 v[64:65], v[36:37], v[64:65], v[12:13]
	v_cvt_pk_bf16_f32 v12, v68, v69
	v_cvt_pk_bf16_f32 v13, v70, v71
	v_pk_fma_f32 v[70:71], v[34:35], v[70:71], v[10:11]
	v_pk_fma_f32 v[68:69], v[36:37], v[68:69], v[8:9]
	v_cvt_pk_bf16_f32 v8, v32, v1
	v_add_co_u32_e32 v10, vcc, s9, v72
	v_pk_fma_f32 v[42:43], v[34:35], v[42:43], v[6:7]
	v_pk_fma_f32 v[32:33], v[36:37], v[32:33], v[4:5]
	v_cvt_pk_bf16_f32 v9, v2, v74
	v_addc_co_u32_e32 v11, vcc, 0, v73, vcc
	v_mov_b32_e32 v1, v33
	v_mov_b32_e32 v2, v42
	v_mov_b32_e32 v74, v43
	global_store_dwordx2 v[78:79], v[76:77], off
	global_store_dwordx2 v[30:31], v[28:29], off
	global_store_dwordx2 v[26:27], v[24:25], off
	global_store_dwordx2 v[22:23], v[20:21], off
	global_store_dwordx2 v[18:19], v[16:17], off
	global_store_dwordx2 v[14:15], v[12:13], off
	global_store_dwordx2 v[10:11], v[8:9], off
	s_cbranch_scc0 .LBB0_544
	s_mov_b64 s[6:7], 0
	s_branch .LBB0_539

.LBB0_603:
	s_lshl_b64 s[0:1], s[4:5], 9
	v_readlane_b32 s2, v253, 60
	s_add_u32 s0, s2, s0
	v_readlane_b32 s2, v253, 61
	s_addc_u32 s1, s2, s1
	v_lshl_add_u64 v[6:7], v[74:75], 3, s[0:1]
	v_readlane_b32 s0, v253, 57
	s_add_i32 s4, s4, s0
	v_readlane_b32 s72, v254, 2
	s_cmpk_lt_i32 s4, 0x4000
	global_store_dwordx2 v[6:7], v[4:5], off
	s_cbranch_scc0 .LBB0_1133
.LBB0_604:
	s_mov_b32 s2, s4
	v_writelane_b32 v254, s2, 3
	s_and_b32 s33, s4, 0xfff
	s_mul_i32 s1, s4, 0x4100
	v_writelane_b32 v254, s3, 4
	v_readlane_b32 s2, v253, 58
	s_mul_hi_i32 s0, s4, 0x4100
	s_add_u32 s4, s2, s1
	v_readlane_b32 s1, v253, 59
	s_addc_u32 s5, s1, s0
	s_cmpk_lt_u32 s33, 0x200
	s_cselect_b64 s[0:1], -1, 0
	v_mov_b32_e32 v74, v76
	s_mov_b64 s[2:3], -1
	s_and_b64 vcc, exec, s[0:1]
	s_cbranch_vccz .LBB0_606
	v_min_i32_e32 v4, s33, v74
	s_waitcnt lgkmcnt(0)
	v_ashrrev_i32_e32 v5, 31, v4
	v_lshl_add_u64 v[4:5], v[4:5], 2, s[4:5]
	v_add_u32_e32 v11, 64, v74
	global_load_dword v1, v[4:5], off
	v_min_i32_e32 v4, s33, v11
	v_ashrrev_i32_e32 v5, 31, v4
	v_add_u32_e32 v10, 0x80, v74
	v_lshl_add_u64 v[4:5], v[4:5], 2, s[4:5]
	global_load_dword v12, v[4:5], off
	v_min_i32_e32 v4, s33, v10
	v_ashrrev_i32_e32 v5, 31, v4
	v_add_u32_e32 v9, 0xc0, v74
	v_lshl_add_u64 v[4:5], v[4:5], 2, s[4:5]
	global_load_dword v13, v[4:5], off
	v_min_i32_e32 v4, s33, v9
	v_ashrrev_i32_e32 v5, 31, v4
	v_add_u32_e32 v8, 0x100, v74
	v_lshl_add_u64 v[4:5], v[4:5], 2, s[4:5]
	global_load_dword v14, v[4:5], off
	v_min_i32_e32 v4, s33, v8
	v_ashrrev_i32_e32 v5, 31, v4
	v_add_u32_e32 v7, 0x140, v74
	v_lshl_add_u64 v[4:5], v[4:5], 2, s[4:5]
	global_load_dword v15, v[4:5], off
	v_min_i32_e32 v4, s33, v7
	v_ashrrev_i32_e32 v5, 31, v4
	v_add_u32_e32 v6, 0x180, v74
	v_lshl_add_u64 v[4:5], v[4:5], 2, s[4:5]
	global_load_dword v16, v[4:5], off
	v_min_i32_e32 v4, s33, v6
	v_ashrrev_i32_e32 v5, 31, v4
	v_add_u32_e32 v2, 0x1c0, v74
	v_lshl_add_u64 v[4:5], v[4:5], 2, s[4:5]
	global_load_dword v17, v[4:5], off
	v_min_i32_e32 v4, s33, v2
	v_ashrrev_i32_e32 v5, 31, v4
	v_lshl_add_u64 v[4:5], v[4:5], 2, s[4:5]
	global_load_dword v4, v[4:5], off
	v_cmp_ge_i32_e32 vcc, s33, v74
	s_mov_b64 s[2:3], 0
	s_waitcnt vmcnt(0) lgkmcnt(0)
	v_cndmask_b32_e32 v18, v229, v1, vcc
	v_cmp_ge_i32_e32 vcc, s33, v2
	s_nop 1
	v_cndmask_b32_e32 v25, v229, v4, vcc
	v_cmp_ge_i32_e32 vcc, s33, v6
	s_nop 1
	v_cndmask_b32_e32 v24, v229, v17, vcc
	v_cmp_ge_i32_e32 vcc, s33, v7
	s_nop 1
	v_cndmask_b32_e32 v23, v229, v16, vcc
	v_cmp_ge_i32_e32 vcc, s33, v8
	s_nop 1
	v_cndmask_b32_e32 v22, v229, v15, vcc
	v_cmp_ge_i32_e32 vcc, s33, v9
	s_nop 1
	v_cndmask_b32_e32 v21, v229, v14, vcc
	v_cmp_ge_i32_e32 vcc, s33, v10
	s_nop 1
	v_cndmask_b32_e32 v20, v229, v13, vcc
	v_cmp_ge_i32_e32 vcc, s33, v11
	s_nop 1
	v_cndmask_b32_e32 v19, v229, v12, vcc
.LBB0_606:
	s_andn2_b64 vcc, exec, s[2:3]
	v_ashrrev_i32_e32 v75, 31, v74
	s_cbranch_vccnz .LBB0_608
	s_waitcnt lgkmcnt(0)
	v_lshl_add_u64 v[4:5], v[74:75], 2, s[4:5]
	global_load_dword v18, v[4:5], off
	global_load_dword v19, v[4:5], off offset:256
	global_load_dword v20, v[4:5], off offset:512
	global_load_dword v21, v[4:5], off offset:768
	global_load_dword v22, v[4:5], off offset:1024
	global_load_dword v23, v[4:5], off offset:1280
	global_load_dword v24, v[4:5], off offset:1536
	global_load_dword v25, v[4:5], off offset:1792
.LBB0_608:
	s_cmpk_lt_u32 s33, 0x400
	s_cselect_b64 s[2:3], -1, 0
	s_cmpk_gt_u32 s33, 0x3ff
	s_mov_b64 s[6:7], -1
	s_cbranch_scc1 .LBB0_612
	v_mov_b32_e32 v77, 0xff800000
	s_cmpk_lt_u32 s33, 0x200
	v_mov_b32_e32 v78, 0xff800000
	v_mov_b32_e32 v79, 0xff800000
	v_mov_b32_e32 v80, 0xff800000
	v_mov_b32_e32 v81, 0xff800000
	v_mov_b32_e32 v82, 0xff800000
	v_mov_b32_e32 v83, 0xff800000
	v_mov_b32_e32 v84, 0xff800000
	s_cbranch_scc1 .LBB0_611
	v_add_u32_e32 v11, 0x200, v74
	v_min_i32_e32 v4, s33, v11
	s_waitcnt lgkmcnt(0)
	v_ashrrev_i32_e32 v5, 31, v4
	v_add_u32_e32 v10, 0x240, v74
	v_lshl_add_u64 v[4:5], v[4:5], 2, s[4:5]
	global_load_dword v12, v[4:5], off
	v_min_i32_e32 v4, s33, v10
	v_ashrrev_i32_e32 v5, 31, v4
	v_add_u32_e32 v9, 0x280, v74
	v_lshl_add_u64 v[4:5], v[4:5], 2, s[4:5]
	global_load_dword v13, v[4:5], off
	v_min_i32_e32 v4, s33, v9
	v_ashrrev_i32_e32 v5, 31, v4
	v_add_u32_e32 v8, 0x2c0, v74
	v_lshl_add_u64 v[4:5], v[4:5], 2, s[4:5]
	global_load_dword v14, v[4:5], off
	v_min_i32_e32 v4, s33, v8
	v_ashrrev_i32_e32 v5, 31, v4
	v_add_u32_e32 v7, 0x300, v74
	v_lshl_add_u64 v[4:5], v[4:5], 2, s[4:5]
	global_load_dword v15, v[4:5], off
	v_min_i32_e32 v4, s33, v7
	v_ashrrev_i32_e32 v5, 31, v4
	v_add_u32_e32 v6, 0x340, v74
	v_lshl_add_u64 v[4:5], v[4:5], 2, s[4:5]
	global_load_dword v16, v[4:5], off
	v_min_i32_e32 v4, s33, v6
	v_ashrrev_i32_e32 v5, 31, v4
	v_add_u32_e32 v2, 0x380, v74
	v_lshl_add_u64 v[4:5], v[4:5], 2, s[4:5]
	global_load_dword v17, v[4:5], off
	v_min_i32_e32 v4, s33, v2
	v_ashrrev_i32_e32 v5, 31, v4
	v_add_u32_e32 v1, 0x3c0, v74
	v_lshl_add_u64 v[4:5], v[4:5], 2, s[4:5]
	global_load_dword v26, v[4:5], off
	v_min_i32_e32 v4, s33, v1
	v_ashrrev_i32_e32 v5, 31, v4
	v_lshl_add_u64 v[4:5], v[4:5], 2, s[4:5]
	global_load_dword v4, v[4:5], off
	v_cmp_ge_i32_e32 vcc, s33, v11
	s_waitcnt vmcnt(0) lgkmcnt(0)
	s_nop 0
	v_cndmask_b32_e32 v84, v229, v12, vcc
	v_cmp_ge_i32_e32 vcc, s33, v10
	s_nop 1
	v_cndmask_b32_e32 v83, v229, v13, vcc
	v_cmp_ge_i32_e32 vcc, s33, v9
	s_nop 1
	v_cndmask_b32_e32 v82, v229, v14, vcc
	v_cmp_ge_i32_e32 vcc, s33, v8
	s_nop 1
	v_cndmask_b32_e32 v81, v229, v15, vcc
	v_cmp_ge_i32_e32 vcc, s33, v7
	s_nop 1
	v_cndmask_b32_e32 v80, v229, v16, vcc
	v_cmp_ge_i32_e32 vcc, s33, v6
	s_nop 1
	v_cndmask_b32_e32 v79, v229, v17, vcc
	v_cmp_ge_i32_e32 vcc, s33, v2
	s_nop 1
	v_cndmask_b32_e32 v78, v229, v26, vcc
	v_cmp_ge_i32_e32 vcc, s33, v1
	s_nop 1
	v_cndmask_b32_e32 v77, v229, v4, vcc

.LBB0_612:
	s_andn2_b64 vcc, exec, s[6:7]
	s_cbranch_vccnz .LBB0_614
	s_waitcnt lgkmcnt(0)
	v_lshl_add_u64 v[4:5], v[74:75], 2, s[4:5]
	global_load_dword v84, v[4:5], off offset:2048
	global_load_dword v83, v[4:5], off offset:2304
	global_load_dword v82, v[4:5], off offset:2560
	global_load_dword v81, v[4:5], off offset:2816
	global_load_dword v80, v[4:5], off offset:3072
	global_load_dword v79, v[4:5], off offset:3328
	global_load_dword v78, v[4:5], off offset:3584
	global_load_dword v77, v[4:5], off offset:3840
.LBB0_614:
	s_cmpk_lt_u32 s33, 0x600
	s_cselect_b64 s[18:19], -1, 0
	s_cmpk_gt_u32 s33, 0x5ff
	s_mov_b64 s[6:7], -1
	s_cbranch_scc1 .LBB0_618
	v_mov_b32_e32 v85, 0xff800000
	s_cmpk_lt_u32 s33, 0x400
	v_mov_b32_e32 v86, 0xff800000
	v_mov_b32_e32 v87, 0xff800000
	v_mov_b32_e32 v88, 0xff800000
	v_mov_b32_e32 v89, 0xff800000
	v_mov_b32_e32 v90, 0xff800000
	v_mov_b32_e32 v91, 0xff800000
	v_mov_b32_e32 v92, 0xff800000
	s_cbranch_scc1 .LBB0_617
	v_add_u32_e32 v11, 0x400, v74
	v_min_i32_e32 v4, s33, v11
	s_waitcnt lgkmcnt(0)
	v_ashrrev_i32_e32 v5, 31, v4
	v_add_u32_e32 v10, 0x440, v74
	v_lshl_add_u64 v[4:5], v[4:5], 2, s[4:5]
	global_load_dword v12, v[4:5], off
	v_min_i32_e32 v4, s33, v10
	v_ashrrev_i32_e32 v5, 31, v4
	v_add_u32_e32 v9, 0x480, v74
	v_lshl_add_u64 v[4:5], v[4:5], 2, s[4:5]
	global_load_dword v13, v[4:5], off
	v_min_i32_e32 v4, s33, v9
	v_ashrrev_i32_e32 v5, 31, v4
	v_add_u32_e32 v8, 0x4c0, v74
	v_lshl_add_u64 v[4:5], v[4:5], 2, s[4:5]
	global_load_dword v14, v[4:5], off
	v_min_i32_e32 v4, s33, v8
	v_ashrrev_i32_e32 v5, 31, v4
	v_add_u32_e32 v7, 0x500, v74
	v_lshl_add_u64 v[4:5], v[4:5], 2, s[4:5]
	global_load_dword v15, v[4:5], off
	v_min_i32_e32 v4, s33, v7
	v_ashrrev_i32_e32 v5, 31, v4
	v_add_u32_e32 v6, 0x540, v74
	v_lshl_add_u64 v[4:5], v[4:5], 2, s[4:5]
	global_load_dword v16, v[4:5], off
	v_min_i32_e32 v4, s33, v6
	v_ashrrev_i32_e32 v5, 31, v4
	v_add_u32_e32 v2, 0x580, v74
	v_lshl_add_u64 v[4:5], v[4:5], 2, s[4:5]
	global_load_dword v17, v[4:5], off
	v_min_i32_e32 v4, s33, v2
	v_ashrrev_i32_e32 v5, 31, v4
	v_add_u32_e32 v1, 0x5c0, v74
	v_lshl_add_u64 v[4:5], v[4:5], 2, s[4:5]
	global_load_dword v26, v[4:5], off
	v_min_i32_e32 v4, s33, v1
	v_ashrrev_i32_e32 v5, 31, v4
	v_lshl_add_u64 v[4:5], v[4:5], 2, s[4:5]
	global_load_dword v4, v[4:5], off
	v_cmp_ge_i32_e32 vcc, s33, v11
	s_waitcnt vmcnt(0) lgkmcnt(0)
	s_nop 0
	v_cndmask_b32_e32 v92, v229, v12, vcc
	v_cmp_ge_i32_e32 vcc, s33, v10
	s_nop 1
	v_cndmask_b32_e32 v91, v229, v13, vcc
	v_cmp_ge_i32_e32 vcc, s33, v9
	s_nop 1
	v_cndmask_b32_e32 v90, v229, v14, vcc
	v_cmp_ge_i32_e32 vcc, s33, v8
	s_nop 1
	v_cndmask_b32_e32 v89, v229, v15, vcc
	v_cmp_ge_i32_e32 vcc, s33, v7
	s_nop 1
	v_cndmask_b32_e32 v88, v229, v16, vcc
	v_cmp_ge_i32_e32 vcc, s33, v6
	s_nop 1
	v_cndmask_b32_e32 v87, v229, v17, vcc
	v_cmp_ge_i32_e32 vcc, s33, v2
	s_nop 1
	v_cndmask_b32_e32 v86, v229, v26, vcc
	v_cmp_ge_i32_e32 vcc, s33, v1
	s_nop 1
	v_cndmask_b32_e32 v85, v229, v4, vcc

.LBB0_618:
	s_andn2_b64 vcc, exec, s[6:7]
	s_cbranch_vccnz .LBB0_620
	s_waitcnt lgkmcnt(0)
	v_lshl_add_u64 v[4:5], v[74:75], 2, s[4:5]
	v_add_co_u32_e32 v4, vcc, 0x1000, v4
	s_nop 1
	v_addc_co_u32_e32 v5, vcc, 0, v5, vcc
	global_load_dword v92, v[4:5], off
	global_load_dword v91, v[4:5], off offset:256
	global_load_dword v90, v[4:5], off offset:512
	global_load_dword v89, v[4:5], off offset:768
	global_load_dword v88, v[4:5], off offset:1024
	global_load_dword v87, v[4:5], off offset:1280
	global_load_dword v86, v[4:5], off offset:1536
	global_load_dword v85, v[4:5], off offset:1792
.LBB0_620:
	s_cmpk_lt_u32 s33, 0x800
	s_cselect_b64 s[20:21], -1, 0
	s_cmpk_gt_u32 s33, 0x7ff
	s_mov_b64 s[6:7], -1
	s_cbranch_scc1 .LBB0_624
	v_mov_b32_e32 v93, 0xff800000
	s_cmpk_lt_u32 s33, 0x600
	v_mov_b32_e32 v94, 0xff800000
	v_mov_b32_e32 v95, 0xff800000
	v_mov_b32_e32 v96, 0xff800000
	v_mov_b32_e32 v97, 0xff800000
	v_mov_b32_e32 v98, 0xff800000
	v_mov_b32_e32 v99, 0xff800000
	v_mov_b32_e32 v100, 0xff800000
	s_cbranch_scc1 .LBB0_623
	v_add_u32_e32 v11, 0x600, v74
	v_min_i32_e32 v4, s33, v11
	s_waitcnt lgkmcnt(0)
	v_ashrrev_i32_e32 v5, 31, v4
	v_add_u32_e32 v10, 0x640, v74
	v_lshl_add_u64 v[4:5], v[4:5], 2, s[4:5]
	global_load_dword v12, v[4:5], off
	v_min_i32_e32 v4, s33, v10
	v_ashrrev_i32_e32 v5, 31, v4
	v_add_u32_e32 v9, 0x680, v74
	v_lshl_add_u64 v[4:5], v[4:5], 2, s[4:5]
	global_load_dword v13, v[4:5], off
	v_min_i32_e32 v4, s33, v9
	v_ashrrev_i32_e32 v5, 31, v4
	v_add_u32_e32 v8, 0x6c0, v74
	v_lshl_add_u64 v[4:5], v[4:5], 2, s[4:5]
	global_load_dword v14, v[4:5], off
	v_min_i32_e32 v4, s33, v8
	v_ashrrev_i32_e32 v5, 31, v4
	v_add_u32_e32 v7, 0x700, v74
	v_lshl_add_u64 v[4:5], v[4:5], 2, s[4:5]
	global_load_dword v15, v[4:5], off
	v_min_i32_e32 v4, s33, v7
	v_ashrrev_i32_e32 v5, 31, v4
	v_add_u32_e32 v6, 0x740, v74
	v_lshl_add_u64 v[4:5], v[4:5], 2, s[4:5]
	global_load_dword v16, v[4:5], off
	v_min_i32_e32 v4, s33, v6
	v_ashrrev_i32_e32 v5, 31, v4
	v_add_u32_e32 v2, 0x780, v74
	v_lshl_add_u64 v[4:5], v[4:5], 2, s[4:5]
	global_load_dword v17, v[4:5], off
	v_min_i32_e32 v4, s33, v2
	v_ashrrev_i32_e32 v5, 31, v4
	v_add_u32_e32 v1, 0x7c0, v74
	v_lshl_add_u64 v[4:5], v[4:5], 2, s[4:5]
	global_load_dword v26, v[4:5], off
	v_min_i32_e32 v4, s33, v1
	v_ashrrev_i32_e32 v5, 31, v4
	v_lshl_add_u64 v[4:5], v[4:5], 2, s[4:5]
	global_load_dword v4, v[4:5], off
	v_cmp_ge_i32_e32 vcc, s33, v11
	s_waitcnt vmcnt(0) lgkmcnt(0)
	s_nop 0
	v_cndmask_b32_e32 v100, v229, v12, vcc
	v_cmp_ge_i32_e32 vcc, s33, v10
	s_nop 1
	v_cndmask_b32_e32 v99, v229, v13, vcc
	v_cmp_ge_i32_e32 vcc, s33, v9
	s_nop 1
	v_cndmask_b32_e32 v98, v229, v14, vcc
	v_cmp_ge_i32_e32 vcc, s33, v8
	s_nop 1
	v_cndmask_b32_e32 v97, v229, v15, vcc
	v_cmp_ge_i32_e32 vcc, s33, v7
	s_nop 1
	v_cndmask_b32_e32 v96, v229, v16, vcc
	v_cmp_ge_i32_e32 vcc, s33, v6
	s_nop 1
	v_cndmask_b32_e32 v95, v229, v17, vcc
	v_cmp_ge_i32_e32 vcc, s33, v2
	s_nop 1
	v_cndmask_b32_e32 v94, v229, v26, vcc
	v_cmp_ge_i32_e32 vcc, s33, v1
	s_nop 1
	v_cndmask_b32_e32 v93, v229, v4, vcc

.LBB0_624:
	s_andn2_b64 vcc, exec, s[6:7]
	s_cbranch_vccnz .LBB0_626
	s_waitcnt lgkmcnt(0)
	v_lshl_add_u64 v[4:5], v[74:75], 2, s[4:5]
	v_add_co_u32_e32 v4, vcc, 0x1000, v4
	s_nop 1
	v_addc_co_u32_e32 v5, vcc, 0, v5, vcc
	global_load_dword v100, v[4:5], off offset:2048
	global_load_dword v99, v[4:5], off offset:2304
	global_load_dword v98, v[4:5], off offset:2560
	global_load_dword v97, v[4:5], off offset:2816
	global_load_dword v96, v[4:5], off offset:3072
	global_load_dword v95, v[4:5], off offset:3328
	global_load_dword v94, v[4:5], off offset:3584
	global_load_dword v93, v[4:5], off offset:3840
.LBB0_626:
	s_cmpk_lt_u32 s33, 0xa00
	s_cselect_b64 s[22:23], -1, 0
	s_cmpk_gt_u32 s33, 0x9ff
	s_mov_b64 s[6:7], -1
	s_cbranch_scc1 .LBB0_630
	v_mov_b32_e32 v101, 0xff800000
	s_cmpk_lt_u32 s33, 0x800
	v_mov_b32_e32 v102, 0xff800000
	v_mov_b32_e32 v103, 0xff800000
	v_mov_b32_e32 v104, 0xff800000
	v_mov_b32_e32 v105, 0xff800000
	v_mov_b32_e32 v106, 0xff800000
	v_mov_b32_e32 v107, 0xff800000
	v_mov_b32_e32 v108, 0xff800000
	s_cbranch_scc1 .LBB0_629
	v_add_u32_e32 v11, 0x800, v74
	v_min_i32_e32 v4, s33, v11
	s_waitcnt lgkmcnt(0)
	v_ashrrev_i32_e32 v5, 31, v4
	v_add_u32_e32 v10, 0x840, v74
	v_lshl_add_u64 v[4:5], v[4:5], 2, s[4:5]
	global_load_dword v12, v[4:5], off
	v_min_i32_e32 v4, s33, v10
	v_ashrrev_i32_e32 v5, 31, v4
	v_add_u32_e32 v9, 0x880, v74
	v_lshl_add_u64 v[4:5], v[4:5], 2, s[4:5]
	global_load_dword v13, v[4:5], off
	v_min_i32_e32 v4, s33, v9
	v_ashrrev_i32_e32 v5, 31, v4
	v_add_u32_e32 v8, 0x8c0, v74
	v_lshl_add_u64 v[4:5], v[4:5], 2, s[4:5]
	global_load_dword v14, v[4:5], off
	v_min_i32_e32 v4, s33, v8
	v_ashrrev_i32_e32 v5, 31, v4
	v_add_u32_e32 v7, 0x900, v74
	v_lshl_add_u64 v[4:5], v[4:5], 2, s[4:5]
	global_load_dword v15, v[4:5], off
	v_min_i32_e32 v4, s33, v7
	v_ashrrev_i32_e32 v5, 31, v4
	v_add_u32_e32 v6, 0x940, v74
	v_lshl_add_u64 v[4:5], v[4:5], 2, s[4:5]
	global_load_dword v16, v[4:5], off
	v_min_i32_e32 v4, s33, v6
	v_ashrrev_i32_e32 v5, 31, v4
	v_add_u32_e32 v2, 0x980, v74
	v_lshl_add_u64 v[4:5], v[4:5], 2, s[4:5]
	global_load_dword v17, v[4:5], off
	v_min_i32_e32 v4, s33, v2
	v_ashrrev_i32_e32 v5, 31, v4
	v_add_u32_e32 v1, 0x9c0, v74
	v_lshl_add_u64 v[4:5], v[4:5], 2, s[4:5]
	global_load_dword v26, v[4:5], off
	v_min_i32_e32 v4, s33, v1
	v_ashrrev_i32_e32 v5, 31, v4
	v_lshl_add_u64 v[4:5], v[4:5], 2, s[4:5]
	global_load_dword v4, v[4:5], off
	v_cmp_ge_i32_e32 vcc, s33, v11
	s_waitcnt vmcnt(0) lgkmcnt(0)
	s_nop 0
	v_cndmask_b32_e32 v108, v229, v12, vcc
	v_cmp_ge_i32_e32 vcc, s33, v10
	s_nop 1
	v_cndmask_b32_e32 v107, v229, v13, vcc
	v_cmp_ge_i32_e32 vcc, s33, v9
	s_nop 1
	v_cndmask_b32_e32 v106, v229, v14, vcc
	v_cmp_ge_i32_e32 vcc, s33, v8
	s_nop 1
	v_cndmask_b32_e32 v105, v229, v15, vcc
	v_cmp_ge_i32_e32 vcc, s33, v7
	s_nop 1
	v_cndmask_b32_e32 v104, v229, v16, vcc
	v_cmp_ge_i32_e32 vcc, s33, v6
	s_nop 1
	v_cndmask_b32_e32 v103, v229, v17, vcc
	v_cmp_ge_i32_e32 vcc, s33, v2
	s_nop 1
	v_cndmask_b32_e32 v102, v229, v26, vcc
	v_cmp_ge_i32_e32 vcc, s33, v1
	s_nop 1
	v_cndmask_b32_e32 v101, v229, v4, vcc

.LBB0_630:
	s_andn2_b64 vcc, exec, s[6:7]
	s_cbranch_vccnz .LBB0_632
	s_waitcnt lgkmcnt(0)
	v_lshl_add_u64 v[4:5], v[74:75], 2, s[4:5]
	v_add_co_u32_e32 v4, vcc, 0x2000, v4
	s_nop 1
	v_addc_co_u32_e32 v5, vcc, 0, v5, vcc
	global_load_dword v108, v[4:5], off
	global_load_dword v107, v[4:5], off offset:256
	global_load_dword v106, v[4:5], off offset:512
	global_load_dword v105, v[4:5], off offset:768
	global_load_dword v104, v[4:5], off offset:1024
	global_load_dword v103, v[4:5], off offset:1280
	global_load_dword v102, v[4:5], off offset:1536
	global_load_dword v101, v[4:5], off offset:1792
.LBB0_632:
	s_cmpk_lt_u32 s33, 0xc00
	s_cselect_b64 s[24:25], -1, 0
	s_cmpk_gt_u32 s33, 0xbff
	s_mov_b64 s[6:7], -1
	s_cbranch_scc1 .LBB0_636
	v_mov_b32_e32 v109, 0xff800000
	s_cmpk_lt_u32 s33, 0xa00
	v_mov_b32_e32 v110, 0xff800000
	v_mov_b32_e32 v111, 0xff800000
	v_mov_b32_e32 v112, 0xff800000
	v_mov_b32_e32 v113, 0xff800000
	v_mov_b32_e32 v114, 0xff800000
	v_mov_b32_e32 v115, 0xff800000
	v_mov_b32_e32 v116, 0xff800000
	s_cbranch_scc1 .LBB0_635
	v_add_u32_e32 v11, 0xa00, v74
	v_min_i32_e32 v4, s33, v11
	s_waitcnt lgkmcnt(0)
	v_ashrrev_i32_e32 v5, 31, v4
	v_add_u32_e32 v10, 0xa40, v74
	v_lshl_add_u64 v[4:5], v[4:5], 2, s[4:5]
	global_load_dword v12, v[4:5], off
	v_min_i32_e32 v4, s33, v10
	v_ashrrev_i32_e32 v5, 31, v4
	v_add_u32_e32 v9, 0xa80, v74
	v_lshl_add_u64 v[4:5], v[4:5], 2, s[4:5]
	global_load_dword v13, v[4:5], off
	v_min_i32_e32 v4, s33, v9
	v_ashrrev_i32_e32 v5, 31, v4
	v_add_u32_e32 v8, 0xac0, v74
	v_lshl_add_u64 v[4:5], v[4:5], 2, s[4:5]
	global_load_dword v14, v[4:5], off
	v_min_i32_e32 v4, s33, v8
	v_ashrrev_i32_e32 v5, 31, v4
	v_add_u32_e32 v7, 0xb00, v74
	v_lshl_add_u64 v[4:5], v[4:5], 2, s[4:5]
	global_load_dword v15, v[4:5], off
	v_min_i32_e32 v4, s33, v7
	v_ashrrev_i32_e32 v5, 31, v4
	v_add_u32_e32 v6, 0xb40, v74
	v_lshl_add_u64 v[4:5], v[4:5], 2, s[4:5]
	global_load_dword v16, v[4:5], off
	v_min_i32_e32 v4, s33, v6
	v_ashrrev_i32_e32 v5, 31, v4
	v_add_u32_e32 v2, 0xb80, v74
	v_lshl_add_u64 v[4:5], v[4:5], 2, s[4:5]
	global_load_dword v17, v[4:5], off
	v_min_i32_e32 v4, s33, v2
	v_ashrrev_i32_e32 v5, 31, v4
	v_add_u32_e32 v1, 0xbc0, v74
	v_lshl_add_u64 v[4:5], v[4:5], 2, s[4:5]
	global_load_dword v26, v[4:5], off
	v_min_i32_e32 v4, s33, v1
	v_ashrrev_i32_e32 v5, 31, v4
	v_lshl_add_u64 v[4:5], v[4:5], 2, s[4:5]
	global_load_dword v4, v[4:5], off
	v_cmp_ge_i32_e32 vcc, s33, v11
	s_waitcnt vmcnt(0) lgkmcnt(0)
	s_nop 0
	v_cndmask_b32_e32 v116, v229, v12, vcc
	v_cmp_ge_i32_e32 vcc, s33, v10
	s_nop 1
	v_cndmask_b32_e32 v115, v229, v13, vcc
	v_cmp_ge_i32_e32 vcc, s33, v9
	s_nop 1
	v_cndmask_b32_e32 v114, v229, v14, vcc
	v_cmp_ge_i32_e32 vcc, s33, v8
	s_nop 1
	v_cndmask_b32_e32 v113, v229, v15, vcc
	v_cmp_ge_i32_e32 vcc, s33, v7
	s_nop 1
	v_cndmask_b32_e32 v112, v229, v16, vcc
	v_cmp_ge_i32_e32 vcc, s33, v6
	s_nop 1
	v_cndmask_b32_e32 v111, v229, v17, vcc
	v_cmp_ge_i32_e32 vcc, s33, v2
	s_nop 1
	v_cndmask_b32_e32 v110, v229, v26, vcc
	v_cmp_ge_i32_e32 vcc, s33, v1
	s_nop 1
	v_cndmask_b32_e32 v109, v229, v4, vcc

.LBB0_636:
	s_andn2_b64 vcc, exec, s[6:7]
	s_cbranch_vccnz .LBB0_638
	s_waitcnt lgkmcnt(0)
	v_lshl_add_u64 v[4:5], v[74:75], 2, s[4:5]
	v_add_co_u32_e32 v4, vcc, 0x2000, v4
	s_nop 1
	v_addc_co_u32_e32 v5, vcc, 0, v5, vcc
	global_load_dword v116, v[4:5], off offset:2048
	global_load_dword v115, v[4:5], off offset:2304
	global_load_dword v114, v[4:5], off offset:2560
	global_load_dword v113, v[4:5], off offset:2816
	global_load_dword v112, v[4:5], off offset:3072
	global_load_dword v111, v[4:5], off offset:3328
	global_load_dword v110, v[4:5], off offset:3584
	global_load_dword v109, v[4:5], off offset:3840
.LBB0_638:
	s_cmpk_lt_u32 s33, 0xe00
	s_cselect_b64 s[26:27], -1, 0
	s_cmpk_gt_u32 s33, 0xdff
	s_mov_b64 s[6:7], -1
	s_cbranch_scc1 .LBB0_642
	v_mov_b32_e32 v117, 0xff800000
	s_cmpk_lt_u32 s33, 0xc00
	v_mov_b32_e32 v118, 0xff800000
	v_mov_b32_e32 v119, 0xff800000
	v_mov_b32_e32 v120, 0xff800000
	v_mov_b32_e32 v121, 0xff800000
	v_mov_b32_e32 v122, 0xff800000
	v_mov_b32_e32 v123, 0xff800000
	v_mov_b32_e32 v124, 0xff800000
	s_cbranch_scc1 .LBB0_641
	v_add_u32_e32 v11, 0xc00, v74
	v_min_i32_e32 v4, s33, v11
	s_waitcnt lgkmcnt(0)
	v_ashrrev_i32_e32 v5, 31, v4
	v_add_u32_e32 v10, 0xc40, v74
	v_lshl_add_u64 v[4:5], v[4:5], 2, s[4:5]
	global_load_dword v12, v[4:5], off
	v_min_i32_e32 v4, s33, v10
	v_ashrrev_i32_e32 v5, 31, v4
	v_add_u32_e32 v9, 0xc80, v74
	v_lshl_add_u64 v[4:5], v[4:5], 2, s[4:5]
	global_load_dword v13, v[4:5], off
	v_min_i32_e32 v4, s33, v9
	v_ashrrev_i32_e32 v5, 31, v4
	v_add_u32_e32 v8, 0xcc0, v74
	v_lshl_add_u64 v[4:5], v[4:5], 2, s[4:5]
	global_load_dword v14, v[4:5], off
	v_min_i32_e32 v4, s33, v8
	v_ashrrev_i32_e32 v5, 31, v4
	v_add_u32_e32 v7, 0xd00, v74
	v_lshl_add_u64 v[4:5], v[4:5], 2, s[4:5]
	global_load_dword v15, v[4:5], off
	v_min_i32_e32 v4, s33, v7
	v_ashrrev_i32_e32 v5, 31, v4
	v_add_u32_e32 v6, 0xd40, v74
	v_lshl_add_u64 v[4:5], v[4:5], 2, s[4:5]
	global_load_dword v16, v[4:5], off
	v_min_i32_e32 v4, s33, v6
	v_ashrrev_i32_e32 v5, 31, v4
	v_add_u32_e32 v2, 0xd80, v74
	v_lshl_add_u64 v[4:5], v[4:5], 2, s[4:5]
	global_load_dword v17, v[4:5], off
	v_min_i32_e32 v4, s33, v2
	v_ashrrev_i32_e32 v5, 31, v4
	v_add_u32_e32 v1, 0xdc0, v74
	v_lshl_add_u64 v[4:5], v[4:5], 2, s[4:5]
	global_load_dword v26, v[4:5], off
	v_min_i32_e32 v4, s33, v1
	v_ashrrev_i32_e32 v5, 31, v4
	v_lshl_add_u64 v[4:5], v[4:5], 2, s[4:5]
	global_load_dword v4, v[4:5], off
	v_cmp_ge_i32_e32 vcc, s33, v11
	s_waitcnt vmcnt(0) lgkmcnt(0)
	s_nop 0
	v_cndmask_b32_e32 v124, v229, v12, vcc
	v_cmp_ge_i32_e32 vcc, s33, v10
	s_nop 1
	v_cndmask_b32_e32 v123, v229, v13, vcc
	v_cmp_ge_i32_e32 vcc, s33, v9
	s_nop 1
	v_cndmask_b32_e32 v122, v229, v14, vcc
	v_cmp_ge_i32_e32 vcc, s33, v8
	s_nop 1
	v_cndmask_b32_e32 v121, v229, v15, vcc
	v_cmp_ge_i32_e32 vcc, s33, v7
	s_nop 1
	v_cndmask_b32_e32 v120, v229, v16, vcc
	v_cmp_ge_i32_e32 vcc, s33, v6
	s_nop 1
	v_cndmask_b32_e32 v119, v229, v17, vcc
	v_cmp_ge_i32_e32 vcc, s33, v2
	s_nop 1
	v_cndmask_b32_e32 v118, v229, v26, vcc
	v_cmp_ge_i32_e32 vcc, s33, v1
	s_nop 1
	v_cndmask_b32_e32 v117, v229, v4, vcc

.LBB0_642:
	s_andn2_b64 vcc, exec, s[6:7]
	s_cbranch_vccnz .LBB0_644
	s_waitcnt lgkmcnt(0)
	v_lshl_add_u64 v[4:5], v[74:75], 2, s[4:5]
	v_add_co_u32_e32 v4, vcc, 0x3000, v4
	s_nop 1
	v_addc_co_u32_e32 v5, vcc, 0, v5, vcc
	global_load_dword v124, v[4:5], off
	global_load_dword v123, v[4:5], off offset:256
	global_load_dword v122, v[4:5], off offset:512
	global_load_dword v121, v[4:5], off offset:768
	global_load_dword v120, v[4:5], off offset:1024
	global_load_dword v119, v[4:5], off offset:1280
	global_load_dword v118, v[4:5], off offset:1536
	global_load_dword v117, v[4:5], off offset:1792
.LBB0_644:
	s_cmpk_gt_u32 s33, 0xdff
	s_cselect_b64 s[6:7], -1, 0
	v_writelane_b32 v254, s6, 5
	v_mov_b32_e32 v125, 0xff800000
	s_cmpk_lt_u32 s33, 0xe00
	v_writelane_b32 v254, s7, 6
	v_mov_b32_e32 v126, 0xff800000
	v_mov_b32_e32 v127, 0xff800000
	v_mov_b32_e32 v128, 0xff800000
	v_mov_b32_e32 v129, 0xff800000
	v_mov_b32_e32 v130, 0xff800000
	v_mov_b32_e32 v131, 0xff800000
	s_waitcnt vmcnt(0)
	v_mov_b32_e32 v132, 0xff800000
	s_cbranch_scc1 .LBB0_647
	v_add_u32_e32 v11, 0xe00, v74
	v_min_i32_e32 v4, s33, v11
	s_waitcnt lgkmcnt(0)
	v_ashrrev_i32_e32 v5, 31, v4
	v_add_u32_e32 v10, 0xe40, v74
	v_lshl_add_u64 v[4:5], v[4:5], 2, s[4:5]
	global_load_dword v12, v[4:5], off
	v_min_i32_e32 v4, s33, v10
	v_ashrrev_i32_e32 v5, 31, v4
	v_add_u32_e32 v9, 0xe80, v74
	v_lshl_add_u64 v[4:5], v[4:5], 2, s[4:5]
	global_load_dword v13, v[4:5], off
	v_min_i32_e32 v4, s33, v9
	v_ashrrev_i32_e32 v5, 31, v4
	v_add_u32_e32 v8, 0xec0, v74
	v_lshl_add_u64 v[4:5], v[4:5], 2, s[4:5]
	global_load_dword v14, v[4:5], off
	v_min_i32_e32 v4, s33, v8
	v_ashrrev_i32_e32 v5, 31, v4
	v_add_u32_e32 v7, 0xf00, v74
	v_lshl_add_u64 v[4:5], v[4:5], 2, s[4:5]
	global_load_dword v15, v[4:5], off
	v_min_i32_e32 v4, s33, v7
	v_ashrrev_i32_e32 v5, 31, v4
	v_add_u32_e32 v6, 0xf40, v74
	v_lshl_add_u64 v[4:5], v[4:5], 2, s[4:5]
	global_load_dword v16, v[4:5], off
	v_min_i32_e32 v4, s33, v6
	v_ashrrev_i32_e32 v5, 31, v4
	v_add_u32_e32 v2, 0xf80, v74
	v_lshl_add_u64 v[4:5], v[4:5], 2, s[4:5]
	global_load_dword v17, v[4:5], off
	v_min_i32_e32 v4, s33, v2
	v_ashrrev_i32_e32 v5, 31, v4
	v_add_u32_e32 v1, 0xfc0, v74
	v_lshl_add_u64 v[4:5], v[4:5], 2, s[4:5]
	global_load_dword v26, v[4:5], off
	v_min_i32_e32 v4, s33, v1
	v_ashrrev_i32_e32 v5, 31, v4
	v_lshl_add_u64 v[4:5], v[4:5], 2, s[4:5]
	global_load_dword v4, v[4:5], off
	v_cmp_ge_i32_e32 vcc, s33, v1
	s_waitcnt vmcnt(0) lgkmcnt(0)
	s_nop 0
	v_cndmask_b32_e32 v125, v229, v4, vcc
	v_cmp_ge_i32_e32 vcc, s33, v2
	s_nop 1
	v_cndmask_b32_e32 v126, v229, v26, vcc
	v_cmp_ge_i32_e32 vcc, s33, v6
	s_nop 1
	v_cndmask_b32_e32 v127, v229, v17, vcc
	v_cmp_ge_i32_e32 vcc, s33, v7
	s_nop 1
	v_cndmask_b32_e32 v128, v229, v16, vcc
	v_cmp_ge_i32_e32 vcc, s33, v8
	s_nop 1
	v_cndmask_b32_e32 v129, v229, v15, vcc
	v_cmp_ge_i32_e32 vcc, s33, v9
	s_nop 1
	v_cndmask_b32_e32 v130, v229, v14, vcc
	v_cmp_ge_i32_e32 vcc, s33, v10
	s_nop 1
	v_cndmask_b32_e32 v131, v229, v13, vcc
	v_cmp_ge_i32_e32 vcc, s33, v11
	s_nop 1
	v_cndmask_b32_e32 v132, v229, v12, vcc
	s_cmpk_gt_u32 s33, 0xff
	s_mov_b64 s[4:5], -1
	s_cbranch_scc0 .LBB0_648

.LBB0_1134:
	s_lshl_b32 s5, s14, 7
	s_lshl_b32 s6, s15, 5
	s_ashr_i32 s4, s4, 7
	s_or_b32 s5, s5, s6
	s_add_i32 s4, s5, s4
	s_ashr_i32 s5, s4, 31
	s_lshl_b64 s[4:5], s[4:5], 16
	s_add_u32 s4, s2, s4
	s_addc_u32 s5, s3, s5
	v_ashrrev_i32_e32 v76, 11, v209
	s_add_u32 s4, s4, 0x4b900000
	v_ashrrev_i32_e32 v77, 31, v76
	s_addc_u32 s5, s5, 0
	v_bfe_u32 v78, v209, 4, 7
	v_lshlrev_b64 v[68:69], 16, v[76:77]
	v_lshl_add_u64 v[70:71], s[4:5], 0, v[68:69]
	v_lshlrev_b32_e32 v68, 8, v78
	v_mov_b32_e32 v69, v3
	v_lshl_add_u64 v[70:71], v[70:71], 0, v[68:69]
	v_mov_b32_e32 v195, v3
	v_lshl_add_u64 v[70:71], v[70:71], 0, v[194:195]
	global_load_dwordx4 v[72:75], v[70:71], off
	v_mov_b32_e32 v70, s72
	s_mov_b32 s6, 0x8900
	v_mad_i32_i24 v71, v76, s6, v70
	v_mul_u32_u24_e32 v78, 0x110, v78
	v_ashrrev_i32_e32 v76, 11, v210
	v_add3_u32 v71, v71, v78, v194
	v_ashrrev_i32_e32 v77, 31, v76
	v_and_b32_e32 v79, 0xffff0000, v127
	v_lshlrev_b32_e32 v80, 16, v122
	v_and_b32_e32 v81, 0xffff0000, v122
	v_lshlrev_b32_e32 v82, 16, v123
	v_and_b32_e32 v83, 0xffff0000, v123
	v_lshlrev_b32_e32 v84, 16, v118
	v_and_b32_e32 v85, 0xffff0000, v118
	v_lshlrev_b32_e32 v86, 16, v119
	v_and_b32_e32 v87, 0xffff0000, v119
	v_lshlrev_b32_e32 v88, 16, v114
	v_and_b32_e32 v89, 0xffff0000, v114
	v_lshlrev_b32_e32 v90, 16, v115
	v_and_b32_e32 v91, 0xffff0000, v115
	v_lshlrev_b32_e32 v92, 16, v110
	v_and_b32_e32 v93, 0xffff0000, v110
	v_lshlrev_b32_e32 v94, 16, v111
	v_and_b32_e32 v95, 0xffff0000, v111
	v_lshlrev_b32_e32 v98, 16, v106
	v_and_b32_e32 v99, 0xffff0000, v106
	s_mul_i32 s13, s13, 0x8900
	s_waitcnt vmcnt(0) lgkmcnt(0)
	ds_write_b128 v71, v[72:75]
	v_bfe_u32 v71, v210, 4, 7
	v_lshlrev_b64 v[72:73], 16, v[76:77]
	v_lshl_add_u64 v[72:73], s[4:5], 0, v[72:73]
	v_lshlrev_b32_e32 v74, 8, v71
	v_mov_b32_e32 v75, v3
	v_lshl_add_u64 v[72:73], v[72:73], 0, v[74:75]
	v_lshl_add_u64 v[72:73], v[72:73], 0, v[194:195]
	global_load_dwordx4 v[72:75], v[72:73], off
	v_mad_i32_i24 v76, v76, s6, v70
	v_mul_u32_u24_e32 v71, 0x110, v71
	v_add3_u32 v71, v76, v71, v194
	s_waitcnt vmcnt(0) lgkmcnt(0)
	ds_write_b128 v71, v[72:75]
	v_add_u32_e32 v71, 0x400, v209
	v_ashrrev_i32_e32 v76, 11, v71
	v_ashrrev_i32_e32 v77, 31, v76
	v_bfe_u32 v71, v71, 4, 7
	v_lshlrev_b64 v[72:73], 16, v[76:77]
	v_lshl_add_u64 v[72:73], s[4:5], 0, v[72:73]
	v_lshlrev_b32_e32 v74, 8, v71
	v_mov_b32_e32 v75, v3
	v_lshl_add_u64 v[72:73], v[72:73], 0, v[74:75]
	v_lshl_add_u64 v[72:73], v[72:73], 0, v[194:195]
	global_load_dwordx4 v[72:75], v[72:73], off
	v_mad_i32_i24 v76, v76, s6, v70
	v_mul_u32_u24_e32 v71, 0x110, v71
	v_add3_u32 v71, v76, v71, v194
	s_waitcnt vmcnt(0) lgkmcnt(0)
	ds_write_b128 v71, v[72:75]
	v_add_u32_e32 v71, 0x600, v209
	v_ashrrev_i32_e32 v76, 11, v71
	v_ashrrev_i32_e32 v77, 31, v76
	v_bfe_u32 v71, v71, 4, 7
	v_lshlrev_b64 v[72:73], 16, v[76:77]
	v_lshl_add_u64 v[72:73], s[4:5], 0, v[72:73]
	v_lshlrev_b32_e32 v74, 8, v71
	v_mov_b32_e32 v75, v3
	v_lshl_add_u64 v[72:73], v[72:73], 0, v[74:75]
	v_lshl_add_u64 v[72:73], v[72:73], 0, v[194:195]
	global_load_dwordx4 v[72:75], v[72:73], off
	v_mad_i32_i24 v76, v76, s6, v70
	v_mul_u32_u24_e32 v71, 0x110, v71
	v_add3_u32 v71, v76, v71, v194
	s_waitcnt vmcnt(0) lgkmcnt(0)
	ds_write_b128 v71, v[72:75]
	v_add_u32_e32 v71, 0x800, v209
	v_ashrrev_i32_e32 v76, 11, v71
	v_ashrrev_i32_e32 v77, 31, v76
	v_lshlrev_b64 v[72:73], 16, v[76:77]
	v_lshl_add_u64 v[72:73], s[4:5], 0, v[72:73]
	v_lshl_add_u64 v[68:69], v[72:73], 0, v[68:69]
	v_lshl_add_u64 v[68:69], v[68:69], 0, v[194:195]
	global_load_dwordx4 v[72:75], v[68:69], off
	v_mad_i32_i24 v68, v76, s6, v70
	v_add3_u32 v68, v68, v78, v194
	v_add_u32_e32 v69, 0xa00, v209
	v_bfe_u32 v71, v69, 4, 7
	v_lshlrev_b32_e32 v76, 16, v126
	v_and_b32_e32 v77, 0xffff0000, v126
	v_lshlrev_b32_e32 v78, 16, v127
	s_waitcnt vmcnt(0) lgkmcnt(0)
	ds_write_b128 v68, v[72:75]
	v_ashrrev_i32_e32 v68, 11, v69
	v_ashrrev_i32_e32 v69, 31, v68
	v_lshlrev_b64 v[72:73], 16, v[68:69]
	v_lshl_add_u64 v[72:73], s[4:5], 0, v[72:73]
	v_lshlrev_b32_e32 v74, 8, v71
	v_mov_b32_e32 v75, v3
	v_lshl_add_u64 v[72:73], v[72:73], 0, v[74:75]
	v_lshl_add_u64 v[72:73], v[72:73], 0, v[194:195]
	global_load_dwordx4 v[72:75], v[72:73], off
	v_mad_i32_i24 v68, v68, s6, v70
	v_mul_u32_u24_e32 v69, 0x110, v71
	v_add3_u32 v68, v68, v69, v194
	v_add_u32_e32 v69, 0xc00, v209
	v_bfe_u32 v71, v69, 4, 7
	s_waitcnt vmcnt(0) lgkmcnt(0)
	ds_write_b128 v68, v[72:75]
	v_ashrrev_i32_e32 v68, 11, v69
	v_ashrrev_i32_e32 v69, 31, v68
	v_lshlrev_b64 v[72:73], 16, v[68:69]
	v_lshl_add_u64 v[72:73], s[4:5], 0, v[72:73]
	v_lshlrev_b32_e32 v74, 8, v71
	v_mov_b32_e32 v75, v3
	v_lshl_add_u64 v[72:73], v[72:73], 0, v[74:75]
	v_lshl_add_u64 v[72:73], v[72:73], 0, v[194:195]
	global_load_dwordx4 v[72:75], v[72:73], off
	v_mad_i32_i24 v68, v68, s6, v70
	v_mul_u32_u24_e32 v69, 0x110, v71
	v_add3_u32 v68, v68, v69, v194
	v_add_u32_e32 v69, 0xe00, v209
	v_bfe_u32 v71, v69, 4, 7
	s_waitcnt vmcnt(0) lgkmcnt(0)
	ds_write_b128 v68, v[72:75]
	v_ashrrev_i32_e32 v68, 11, v69
	v_ashrrev_i32_e32 v69, 31, v68
	v_lshlrev_b64 v[72:73], 16, v[68:69]
	v_lshl_add_u64 v[72:73], s[4:5], 0, v[72:73]
	v_lshlrev_b32_e32 v74, 8, v71
	v_mov_b32_e32 v75, v3
	v_lshl_add_u64 v[72:73], v[72:73], 0, v[74:75]
	v_lshl_add_u64 v[72:73], v[72:73], 0, v[194:195]
	global_load_dwordx4 v[72:75], v[72:73], off
	v_mad_i32_i24 v68, v68, s6, v70
	v_mul_u32_u24_e32 v69, 0x110, v71
	v_add3_u32 v68, v68, v69, v194
	s_mov_b32 s4, 0xc2fc0000
	v_lshlrev_b32_e32 v70, 16, v129
	v_and_b32_e32 v71, 0xffff0000, v129
	s_waitcnt vmcnt(0) lgkmcnt(0)
	ds_write_b128 v68, v[72:75]
	v_and_b32_e32 v68, 0x7f, v207
	v_add_u32_e32 v68, 1, v68
	v_cvt_f32_ubyte0_e32 v68, v68
	v_mul_f32_e32 v69, v208, v68
	v_cmp_gt_f32_e32 vcc, s4, v69
	v_mov_b32_e32 v69, 0x42800000
	v_lshlrev_b32_e32 v72, 16, v130
	v_cndmask_b32_e32 v69, 0, v69, vcc
	v_fmac_f32_e32 v69, v208, v68
	v_exp_f32_e32 v68, v69
	v_not_b32_e32 v69, 63
	v_cndmask_b32_e32 v69, 0, v69, vcc
	v_and_b32_e32 v73, 0xffff0000, v130
	v_ldexp_f32 v96, v68, v69
	v_lshlrev_b32_e32 v68, 16, v128
	v_and_b32_e32 v69, 0xffff0000, v128
	v_lshlrev_b32_e32 v74, 16, v131
	v_and_b32_e32 v75, 0xffff0000, v131
	v_pk_mul_f32 v[68:69], v[96:97], v[68:69] op_sel_hi:[0,1]
	v_pk_mul_f32 v[70:71], v[96:97], v[70:71] op_sel_hi:[0,1]
	v_pk_mul_f32 v[72:73], v[96:97], v[72:73] op_sel_hi:[0,1]
	v_pk_mul_f32 v[74:75], v[96:97], v[74:75] op_sel_hi:[0,1]
	v_cvt_pk_bf16_f32 v68, v68, v69
	v_cvt_pk_bf16_f32 v69, v70, v71
	v_cvt_pk_bf16_f32 v70, v72, v73
	v_cvt_pk_bf16_f32 v71, v74, v75
	v_lshlrev_b32_e32 v72, 16, v124
	v_and_b32_e32 v73, 0xffff0000, v124
	v_lshlrev_b32_e32 v74, 16, v125
	v_and_b32_e32 v75, 0xffff0000, v125
	v_pk_mul_f32 v[72:73], v[96:97], v[72:73] op_sel_hi:[0,1]
	v_pk_mul_f32 v[74:75], v[96:97], v[74:75] op_sel_hi:[0,1]
	v_pk_mul_f32 v[76:77], v[96:97], v[76:77] op_sel_hi:[0,1]
	v_pk_mul_f32 v[78:79], v[96:97], v[78:79] op_sel_hi:[0,1]
	v_cvt_pk_bf16_f32 v72, v72, v73
	v_cvt_pk_bf16_f32 v73, v74, v75
	v_cvt_pk_bf16_f32 v74, v76, v77
	v_cvt_pk_bf16_f32 v75, v78, v79
	v_lshlrev_b32_e32 v76, 16, v120
	v_and_b32_e32 v77, 0xffff0000, v120
	v_lshlrev_b32_e32 v78, 16, v121
	v_and_b32_e32 v79, 0xffff0000, v121
	v_pk_mul_f32 v[76:77], v[96:97], v[76:77] op_sel_hi:[0,1]
	v_pk_mul_f32 v[78:79], v[96:97], v[78:79] op_sel_hi:[0,1]
	v_pk_mul_f32 v[80:81], v[96:97], v[80:81] op_sel_hi:[0,1]
	v_pk_mul_f32 v[82:83], v[96:97], v[82:83] op_sel_hi:[0,1]
	v_cvt_pk_bf16_f32 v76, v76, v77
	v_cvt_pk_bf16_f32 v77, v78, v79
	v_cvt_pk_bf16_f32 v78, v80, v81
	v_cvt_pk_bf16_f32 v79, v82, v83
	v_lshlrev_b32_e32 v80, 16, v116
	v_and_b32_e32 v81, 0xffff0000, v116
	v_lshlrev_b32_e32 v82, 16, v117
	v_and_b32_e32 v83, 0xffff0000, v117
	v_pk_mul_f32 v[80:81], v[96:97], v[80:81] op_sel_hi:[0,1]
	v_pk_mul_f32 v[82:83], v[96:97], v[82:83] op_sel_hi:[0,1]
	v_pk_mul_f32 v[84:85], v[96:97], v[84:85] op_sel_hi:[0,1]
	v_pk_mul_f32 v[86:87], v[96:97], v[86:87] op_sel_hi:[0,1]
	v_cvt_pk_bf16_f32 v80, v80, v81
	v_cvt_pk_bf16_f32 v81, v82, v83
	v_cvt_pk_bf16_f32 v82, v84, v85
	v_cvt_pk_bf16_f32 v83, v86, v87
	v_lshlrev_b32_e32 v84, 16, v112
	v_and_b32_e32 v85, 0xffff0000, v112
	v_lshlrev_b32_e32 v86, 16, v113
	v_and_b32_e32 v87, 0xffff0000, v113
	v_pk_mul_f32 v[84:85], v[96:97], v[84:85] op_sel_hi:[0,1]
	v_pk_mul_f32 v[86:87], v[96:97], v[86:87] op_sel_hi:[0,1]
	v_pk_mul_f32 v[88:89], v[96:97], v[88:89] op_sel_hi:[0,1]
	v_pk_mul_f32 v[90:91], v[96:97], v[90:91] op_sel_hi:[0,1]
	v_cvt_pk_bf16_f32 v84, v84, v85
	v_cvt_pk_bf16_f32 v85, v86, v87
	v_cvt_pk_bf16_f32 v86, v88, v89
	v_cvt_pk_bf16_f32 v87, v90, v91
	v_lshlrev_b32_e32 v88, 16, v108
	v_and_b32_e32 v89, 0xffff0000, v108
	v_lshlrev_b32_e32 v90, 16, v109
	v_and_b32_e32 v91, 0xffff0000, v109
	v_pk_mul_f32 v[88:89], v[96:97], v[88:89] op_sel_hi:[0,1]
	v_pk_mul_f32 v[90:91], v[96:97], v[90:91] op_sel_hi:[0,1]
	v_pk_mul_f32 v[92:93], v[96:97], v[92:93] op_sel_hi:[0,1]
	v_pk_mul_f32 v[94:95], v[96:97], v[94:95] op_sel_hi:[0,1]
	v_cvt_pk_bf16_f32 v88, v88, v89
	v_cvt_pk_bf16_f32 v89, v90, v91
	v_cvt_pk_bf16_f32 v90, v92, v93
	v_cvt_pk_bf16_f32 v91, v94, v95
	v_lshlrev_b32_e32 v92, 16, v104
	v_and_b32_e32 v93, 0xffff0000, v104
	v_lshlrev_b32_e32 v94, 16, v105
	v_and_b32_e32 v95, 0xffff0000, v105
	v_lshlrev_b32_e32 v104, 16, v107
	v_and_b32_e32 v105, 0xffff0000, v107
	v_pk_mul_f32 v[92:93], v[96:97], v[92:93] op_sel_hi:[0,1]
	v_pk_mul_f32 v[94:95], v[96:97], v[94:95] op_sel_hi:[0,1]
	v_pk_mul_f32 v[98:99], v[96:97], v[98:99] op_sel_hi:[0,1]
	v_pk_mul_f32 v[104:105], v[96:97], v[104:105] op_sel_hi:[0,1]
	v_cvt_pk_bf16_f32 v92, v92, v93
	v_cvt_pk_bf16_f32 v93, v94, v95
	v_cvt_pk_bf16_f32 v94, v98, v99
	v_cvt_pk_bf16_f32 v95, v104, v105
	v_lshlrev_b32_e32 v98, 16, v100
	v_and_b32_e32 v99, 0xffff0000, v100
	v_lshlrev_b32_e32 v100, 16, v101
	v_and_b32_e32 v101, 0xffff0000, v101
	v_lshlrev_b32_e32 v104, 16, v102
	v_and_b32_e32 v105, 0xffff0000, v102
	v_lshlrev_b32_e32 v102, 16, v103
	v_and_b32_e32 v103, 0xffff0000, v103
	s_add_i32 s4, s72, s13
	v_pk_mul_f32 v[98:99], v[96:97], v[98:99] op_sel_hi:[0,1]
	v_pk_mul_f32 v[100:101], v[96:97], v[100:101] op_sel_hi:[0,1]
	v_pk_mul_f32 v[104:105], v[96:97], v[104:105] op_sel_hi:[0,1]
	v_pk_mul_f32 v[102:103], v[96:97], v[102:103] op_sel_hi:[0,1]
	v_add3_u32 v1, s4, v1, v2
	v_cvt_pk_bf16_f32 v96, v98, v99
	v_cvt_pk_bf16_f32 v97, v100, v101
	v_cvt_pk_bf16_f32 v98, v104, v105
	v_cvt_pk_bf16_f32 v99, v102, v103
	s_waitcnt lgkmcnt(0)
	s_barrier
	ds_read_b128 v[100:103], v1
	ds_read_b128 v[104:107], v1 offset:32
	ds_read_b128 v[108:111], v1 offset:64
	ds_read_b128 v[112:115], v1 offset:96
	ds_read_b128 v[116:119], v1 offset:128
	ds_read_b128 v[120:123], v1 offset:160
	ds_read_b128 v[124:127], v1 offset:192
	ds_read_b128 v[128:131], v1 offset:224
	s_waitcnt lgkmcnt(7)
	v_mfma_f32_32x32x16_bf16 v[52:67], v[100:103], v[68:71], v[52:67]
	s_waitcnt lgkmcnt(6)
	v_mfma_f32_32x32x16_bf16 v[52:67], v[104:107], v[72:75], v[52:67]
	s_waitcnt lgkmcnt(5)
	v_mfma_f32_32x32x16_bf16 v[52:67], v[108:111], v[76:79], v[52:67]
	s_waitcnt lgkmcnt(4)
	v_mfma_f32_32x32x16_bf16 v[52:67], v[112:115], v[80:83], v[52:67]
	s_waitcnt lgkmcnt(3)
	v_mfma_f32_32x32x16_bf16 v[52:67], v[116:119], v[84:87], v[52:67]
	s_waitcnt lgkmcnt(2)
	v_mfma_f32_32x32x16_bf16 v[52:67], v[120:123], v[88:91], v[52:67]
	s_waitcnt lgkmcnt(1)
	v_mfma_f32_32x32x16_bf16 v[52:67], v[124:127], v[92:95], v[52:67]
	s_waitcnt lgkmcnt(0)
	v_mfma_f32_32x32x16_bf16 v[52:67], v[128:131], v[96:99], v[52:67]
	ds_read_b128 v[100:103], v1 offset:8704
	ds_read_b128 v[104:107], v1 offset:8736
	ds_read_b128 v[108:111], v1 offset:8768
	ds_read_b128 v[112:115], v1 offset:8800
	ds_read_b128 v[116:119], v1 offset:8832
	ds_read_b128 v[120:123], v1 offset:8864
	ds_read_b128 v[124:127], v1 offset:8896
	ds_read_b128 v[128:131], v1 offset:8928
	s_waitcnt lgkmcnt(7)
	v_mfma_f32_32x32x16_bf16 v[36:51], v[100:103], v[68:71], v[36:51]
	s_waitcnt lgkmcnt(6)
	v_mfma_f32_32x32x16_bf16 v[36:51], v[104:107], v[72:75], v[36:51]
	s_waitcnt lgkmcnt(5)
	v_mfma_f32_32x32x16_bf16 v[36:51], v[108:111], v[76:79], v[36:51]
	s_waitcnt lgkmcnt(4)
	v_mfma_f32_32x32x16_bf16 v[36:51], v[112:115], v[80:83], v[36:51]
	s_waitcnt lgkmcnt(3)
	v_mfma_f32_32x32x16_bf16 v[36:51], v[116:119], v[84:87], v[36:51]
	s_waitcnt lgkmcnt(2)
	v_mfma_f32_32x32x16_bf16 v[36:51], v[120:123], v[88:91], v[36:51]
	s_waitcnt lgkmcnt(1)
	v_mfma_f32_32x32x16_bf16 v[36:51], v[124:127], v[92:95], v[36:51]
	s_waitcnt lgkmcnt(0)
	v_mfma_f32_32x32x16_bf16 v[36:51], v[128:131], v[96:99], v[36:51]
	ds_read_b128 v[100:103], v1 offset:17408
	ds_read_b128 v[104:107], v1 offset:17440
	ds_read_b128 v[108:111], v1 offset:17472
	ds_read_b128 v[112:115], v1 offset:17504
	ds_read_b128 v[116:119], v1 offset:17536
	ds_read_b128 v[120:123], v1 offset:17568
	ds_read_b128 v[124:127], v1 offset:17600
	ds_read_b128 v[128:131], v1 offset:17632
	s_waitcnt lgkmcnt(7)
	v_mfma_f32_32x32x16_bf16 v[20:35], v[100:103], v[68:71], v[20:35]
	s_waitcnt lgkmcnt(6)
	v_mfma_f32_32x32x16_bf16 v[20:35], v[104:107], v[72:75], v[20:35]
	s_waitcnt lgkmcnt(5)
	v_mfma_f32_32x32x16_bf16 v[20:35], v[108:111], v[76:79], v[20:35]
	s_waitcnt lgkmcnt(4)
	v_mfma_f32_32x32x16_bf16 v[20:35], v[112:115], v[80:83], v[20:35]
	s_waitcnt lgkmcnt(3)
	v_mfma_f32_32x32x16_bf16 v[20:35], v[116:119], v[84:87], v[20:35]
	s_waitcnt lgkmcnt(2)
	v_mfma_f32_32x32x16_bf16 v[20:35], v[120:123], v[88:91], v[20:35]
	s_waitcnt lgkmcnt(1)
	v_mfma_f32_32x32x16_bf16 v[20:35], v[124:127], v[92:95], v[20:35]
	s_waitcnt lgkmcnt(0)
	v_mfma_f32_32x32x16_bf16 v[20:35], v[128:131], v[96:99], v[20:35]
	ds_read_b128 v[100:103], v1 offset:26112
	ds_read_b128 v[104:107], v1 offset:26144
	ds_read_b128 v[108:111], v1 offset:26176
	ds_read_b128 v[112:115], v1 offset:26208
	ds_read_b128 v[116:119], v1 offset:26240
	ds_read_b128 v[120:123], v1 offset:26272
	ds_read_b128 v[124:127], v1 offset:26304
	ds_read_b128 v[128:131], v1 offset:26336
	s_waitcnt lgkmcnt(7)
	v_mfma_f32_32x32x16_bf16 v[4:19], v[100:103], v[68:71], v[4:19]
	s_waitcnt lgkmcnt(6)
	v_mfma_f32_32x32x16_bf16 v[4:19], v[104:107], v[72:75], v[4:19]
	s_waitcnt lgkmcnt(5)
	v_mfma_f32_32x32x16_bf16 v[4:19], v[108:111], v[76:79], v[4:19]
	s_waitcnt lgkmcnt(4)
	v_mfma_f32_32x32x16_bf16 v[4:19], v[112:115], v[80:83], v[4:19]
	s_waitcnt lgkmcnt(3)
	v_mfma_f32_32x32x16_bf16 v[4:19], v[116:119], v[84:87], v[4:19]
	s_waitcnt lgkmcnt(2)
	v_mfma_f32_32x32x16_bf16 v[4:19], v[120:123], v[88:91], v[4:19]
	s_waitcnt lgkmcnt(1)
	v_mfma_f32_32x32x16_bf16 v[4:19], v[124:127], v[92:95], v[4:19]
	s_waitcnt lgkmcnt(0)
	v_mfma_f32_32x32x16_bf16 v[4:19], v[128:131], v[96:99], v[4:19]
	v_add_f32_e32 v1, 0, v52
	v_add_f32_e32 v1, v53, v1
	v_add_f32_e32 v1, v54, v1
	v_add_f32_e32 v1, v55, v1
	v_add_f32_e32 v1, v56, v1
	v_add_f32_e32 v1, v57, v1
	v_add_f32_e32 v1, v58, v1
	v_add_f32_e32 v1, v59, v1
	v_add_f32_e32 v1, v60, v1
	v_add_f32_e32 v1, v61, v1
	v_add_f32_e32 v1, v62, v1
	v_add_f32_e32 v1, v63, v1
	v_add_f32_e32 v1, v64, v1
	v_add_f32_e32 v1, v65, v1
	v_add_f32_e32 v1, v66, v1
	v_add_f32_e32 v1, v67, v1
	v_add_f32_e32 v1, v1, v36
	v_add_f32_e32 v1, v37, v1
	v_add_f32_e32 v1, v38, v1
	v_add_f32_e32 v1, v39, v1
	v_add_f32_e32 v1, v40, v1
	v_add_f32_e32 v1, v41, v1
	v_add_f32_e32 v1, v42, v1
	v_add_f32_e32 v1, v43, v1
	v_add_f32_e32 v1, v44, v1
	v_add_f32_e32 v1, v45, v1
	v_add_f32_e32 v1, v46, v1
	v_add_f32_e32 v1, v47, v1
	v_add_f32_e32 v1, v48, v1
	v_add_f32_e32 v1, v49, v1
	v_add_f32_e32 v1, v50, v1
	v_add_f32_e32 v1, v51, v1
	v_add_f32_e32 v1, v1, v20
	v_add_f32_e32 v1, v21, v1
	v_add_f32_e32 v1, v22, v1
	v_add_f32_e32 v1, v23, v1
	v_add_f32_e32 v1, v24, v1
	v_add_f32_e32 v1, v25, v1
	v_add_f32_e32 v1, v26, v1
	v_add_f32_e32 v1, v27, v1
	v_add_f32_e32 v1, v28, v1
	v_add_f32_e32 v1, v29, v1
	v_add_f32_e32 v1, v30, v1
	v_add_f32_e32 v1, v31, v1
	v_add_f32_e32 v1, v32, v1
	v_add_f32_e32 v1, v33, v1
	v_add_f32_e32 v1, v34, v1
	v_add_f32_e32 v1, v35, v1
	v_add_f32_e32 v1, v1, v4
	v_add_f32_e32 v1, v5, v1
	v_add_f32_e32 v1, v6, v1
	v_add_f32_e32 v1, v7, v1
	v_add_f32_e32 v1, v8, v1
	v_add_f32_e32 v1, v9, v1
	v_add_f32_e32 v1, v10, v1
	v_add_f32_e32 v1, v11, v1
	v_add_f32_e32 v1, v12, v1
	v_add_f32_e32 v1, v13, v1
	v_add_f32_e32 v1, v14, v1
	v_add_f32_e32 v1, v15, v1
	v_add_f32_e32 v1, v16, v1
	v_add_f32_e32 v1, v17, v1
	v_add_f32_e32 v1, v18, v1
	v_add_f32_e32 v2, v19, v1
	v_xor_b32_e32 v1, 32, v230
	v_cmp_lt_i32_e32 vcc, v1, v231
	v_lshlrev_b64 v[68:69], 12, v[180:181]
	v_readlane_b32 s4, v253, 17
	v_cndmask_b32_e32 v1, v230, v1, vcc
	v_lshlrev_b32_e32 v1, 2, v1
	ds_bpermute_b32 v70, v1, v2
	v_lshl_add_u64 v[68:69], s[2:3], 0, v[68:69]
	v_readlane_b32 s5, v253, 18
	s_movk_i32 s20, 0x110
	v_readlane_b32 s6, v253, 19
	s_waitcnt lgkmcnt(0)
	v_add_f32_e32 v2, v2, v70
	v_mul_f32_e32 v78, 0x3c000000, v2
	v_pk_add_f32 v[70:71], v[14:15], v[78:79] op_sel_hi:[1,0] neg_lo:[0,1] neg_hi:[0,1]
	v_pk_add_f32 v[14:15], v[18:19], v[78:79] op_sel_hi:[1,0] neg_lo:[0,1] neg_hi:[0,1]
	v_lshl_add_u64 v[18:19], v[68:69], 0, s[4:5]
	v_mov_b64_e32 v[68:69], s[2:3]
	v_mad_i64_i32 v[68:69], s[2:3], v180, s24, v[68:69]
	v_lshl_add_u64 v[68:69], v[68:69], 0, s[4:5]
	v_lshlrev_b32_e32 v2, 1, v206
	v_lshl_add_u64 v[80:81], v[68:69], 0, v[2:3]
	s_mov_b64 s[2:3], 0x9000c00
	v_lshl_add_u64 v[68:69], v[80:81], 0, s[2:3]
	s_mov_b32 s2, 0x9000000
	v_add_co_u32_e32 v80, vcc, s2, v80
	global_load_dwordx2 v[92:93], v[68:69], off offset:16
	global_load_dwordx2 v[100:101], v[68:69], off offset:32
	global_load_dwordx2 v[104:105], v[68:69], off offset:48
	global_load_dwordx2 v[108:109], v[68:69], off offset:64
	v_addc_co_u32_e32 v81, vcc, 0, v81, vcc
	global_load_dwordx2 v[82:83], v[80:81], off offset:3072
	v_pk_add_f32 v[16:17], v[16:17], v[78:79] op_sel_hi:[1,0] neg_lo:[0,1] neg_hi:[0,1]
	v_pk_add_f32 v[54:55], v[54:55], v[78:79] op_sel_hi:[1,0] neg_lo:[0,1] neg_hi:[0,1]
	v_pk_add_f32 v[52:53], v[52:53], v[78:79] op_sel_hi:[1,0] neg_lo:[0,1] neg_hi:[0,1]
	global_load_dwordx2 v[114:115], v[68:69], off offset:80
	global_load_dwordx2 v[120:121], v[68:69], off offset:96
	global_load_dwordx2 v[128:129], v[68:69], off offset:112
	global_load_dwordx2 v[136:137], v[68:69], off offset:128
	global_load_dwordx2 v[144:145], v[68:69], off offset:144
	global_load_dwordx2 v[152:153], v[68:69], off offset:160
	global_load_dwordx2 v[160:161], v[68:69], off offset:176
	global_load_dwordx2 v[166:167], v[68:69], off offset:192
	v_pk_mul_f32 v[88:89], v[52:53], v[52:53]
	v_pk_mul_f32 v[86:87], v[54:55], v[54:55]
	v_pk_mul_f32 v[72:73], v[70:71], v[70:71]
	v_pk_mul_f32 v[74:75], v[16:17], v[16:17]
	v_pk_mul_f32 v[76:77], v[14:15], v[14:15]
	s_mov_b64 s[2:3], 0x25800000
	v_readlane_b32 s7, v253, 20
	s_waitcnt vmcnt(0) lgkmcnt(0)
	v_lshlrev_b32_e32 v90, 16, v92
	v_and_b32_e32 v91, 0xffff0000, v92
	v_lshlrev_b32_e32 v92, 16, v93
	v_and_b32_e32 v93, 0xffff0000, v93
	v_lshlrev_b32_e32 v80, 16, v82
	v_mul_f32_e32 v79, 0xbfb8aa3b, v80
	v_exp_f32_e32 v79, v79
	v_and_b32_e32 v81, 0xffff0000, v82
	v_lshlrev_b32_e32 v82, 16, v83
	v_and_b32_e32 v83, 0xffff0000, v83
	v_add_f32_e32 v79, 1.0, v79
	v_rcp_f32_e32 v84, v79
	v_mul_f32_e32 v79, 0xbfb8aa3b, v81
	v_exp_f32_e32 v79, v79
	s_nop 0
	v_add_f32_e32 v79, 1.0, v79
	v_rcp_f32_e32 v85, v79
	v_mul_f32_e32 v79, 0xbfb8aa3b, v82
	v_exp_f32_e32 v79, v79
	v_pk_mul_f32 v[80:81], v[84:85], v[80:81]
	v_add_f32_e32 v79, 1.0, v79
	v_rcp_f32_e32 v84, v79
	v_mul_f32_e32 v79, 0xbfb8aa3b, v83
	v_exp_f32_e32 v79, v79
	s_nop 0
	v_add_f32_e32 v79, 1.0, v79
	v_rcp_f32_e32 v85, v79
	v_pk_add_f32 v[56:57], v[56:57], v[78:79] op_sel_hi:[1,0] neg_lo:[0,1] neg_hi:[0,1]
	v_pk_add_f32 v[58:59], v[58:59], v[78:79] op_sel_hi:[1,0] neg_lo:[0,1] neg_hi:[0,1]
	v_pk_mul_f32 v[96:97], v[56:57], v[56:57]
	v_pk_mul_f32 v[84:85], v[84:85], v[82:83]
	v_lshl_add_u64 v[82:83], v[18:19], 0, v[2:3]
	v_mul_f32_e32 v2, 0xbfb8aa3b, v90
	v_exp_f32_e32 v2, v2
	v_pk_mul_f32 v[94:95], v[58:59], v[58:59]
	v_pk_add_f32 v[60:61], v[60:61], v[78:79] op_sel_hi:[1,0] neg_lo:[0,1] neg_hi:[0,1]
	v_pk_add_f32 v[62:63], v[62:63], v[78:79] op_sel_hi:[1,0] neg_lo:[0,1] neg_hi:[0,1]
	v_add_f32_e32 v2, 1.0, v2
	v_rcp_f32_e32 v98, v2
	v_mul_f32_e32 v2, 0xbfb8aa3b, v91
	v_exp_f32_e32 v2, v2
	v_pk_mul_f32 v[116:117], v[60:61], v[60:61]
	v_pk_mul_f32 v[112:113], v[62:63], v[62:63]
	v_pk_add_f32 v[64:65], v[64:65], v[78:79] op_sel_hi:[1,0] neg_lo:[0,1] neg_hi:[0,1]
	v_add_f32_e32 v2, 1.0, v2
	v_rcp_f32_e32 v99, v2
	v_mul_f32_e32 v2, 0xbfb8aa3b, v92
	v_exp_f32_e32 v2, v2
	v_pk_mul_f32 v[124:125], v[64:65], v[64:65]
	v_pk_mul_f32 v[90:91], v[98:99], v[90:91]
	v_pk_add_f32 v[66:67], v[66:67], v[78:79] op_sel_hi:[1,0] neg_lo:[0,1] neg_hi:[0,1]
	v_add_f32_e32 v2, 1.0, v2
	v_rcp_f32_e32 v98, v2
	v_mul_f32_e32 v2, 0xbfb8aa3b, v93
	v_exp_f32_e32 v2, v2
	v_pk_mul_f32 v[122:123], v[66:67], v[66:67]
	v_pk_add_f32 v[36:37], v[36:37], v[78:79] op_sel_hi:[1,0] neg_lo:[0,1] neg_hi:[0,1]
	v_pk_add_f32 v[38:39], v[38:39], v[78:79] op_sel_hi:[1,0] neg_lo:[0,1] neg_hi:[0,1]
	v_add_f32_e32 v2, 1.0, v2
	v_rcp_f32_e32 v99, v2
	v_pk_mul_f32 v[132:133], v[36:37], v[36:37]
	v_pk_mul_f32 v[130:131], v[38:39], v[38:39]
	v_pk_add_f32 v[40:41], v[40:41], v[78:79] op_sel_hi:[1,0] neg_lo:[0,1] neg_hi:[0,1]
	v_pk_mul_f32 v[92:93], v[98:99], v[92:93]
	v_lshlrev_b32_e32 v98, 16, v100
	v_mul_f32_e32 v2, 0xbfb8aa3b, v98
	v_exp_f32_e32 v2, v2
	v_and_b32_e32 v99, 0xffff0000, v100
	v_lshlrev_b32_e32 v100, 16, v101
	v_and_b32_e32 v101, 0xffff0000, v101
	v_add_f32_e32 v2, 1.0, v2
	v_rcp_f32_e32 v102, v2
	v_mul_f32_e32 v2, 0xbfb8aa3b, v99
	v_exp_f32_e32 v2, v2
	v_pk_mul_f32 v[140:141], v[40:41], v[40:41]
	v_pk_add_f32 v[42:43], v[42:43], v[78:79] op_sel_hi:[1,0] neg_lo:[0,1] neg_hi:[0,1]
	v_pk_add_f32 v[44:45], v[44:45], v[78:79] op_sel_hi:[1,0] neg_lo:[0,1] neg_hi:[0,1]
	v_add_f32_e32 v2, 1.0, v2
	v_rcp_f32_e32 v103, v2
	v_mul_f32_e32 v2, 0xbfb8aa3b, v100
	v_exp_f32_e32 v2, v2
	v_pk_mul_f32 v[138:139], v[42:43], v[42:43]
	v_pk_mul_f32 v[98:99], v[102:103], v[98:99]
	v_pk_mul_f32 v[150:151], v[44:45], v[44:45]
	v_add_f32_e32 v2, 1.0, v2
	v_rcp_f32_e32 v102, v2
	v_mul_f32_e32 v2, 0xbfb8aa3b, v101
	v_exp_f32_e32 v2, v2
	v_pk_add_f32 v[46:47], v[46:47], v[78:79] op_sel_hi:[1,0] neg_lo:[0,1] neg_hi:[0,1]
	v_pk_add_f32 v[48:49], v[48:49], v[78:79] op_sel_hi:[1,0] neg_lo:[0,1] neg_hi:[0,1]
	v_pk_mul_f32 v[146:147], v[46:47], v[46:47]
	v_add_f32_e32 v2, 1.0, v2
	v_rcp_f32_e32 v103, v2
	v_pk_mul_f32 v[158:159], v[48:49], v[48:49]
	v_pk_add_f32 v[50:51], v[50:51], v[78:79] op_sel_hi:[1,0] neg_lo:[0,1] neg_hi:[0,1]
	v_pk_add_f32 v[20:21], v[20:21], v[78:79] op_sel_hi:[1,0] neg_lo:[0,1] neg_hi:[0,1]
	v_pk_mul_f32 v[100:101], v[102:103], v[100:101]
	v_lshlrev_b32_e32 v102, 16, v104
	v_mul_f32_e32 v2, 0xbfb8aa3b, v102
	v_exp_f32_e32 v2, v2
	v_and_b32_e32 v103, 0xffff0000, v104
	v_lshlrev_b32_e32 v104, 16, v105
	v_and_b32_e32 v105, 0xffff0000, v105
	v_add_f32_e32 v2, 1.0, v2
	v_rcp_f32_e32 v106, v2
	v_mul_f32_e32 v2, 0xbfb8aa3b, v103
	v_exp_f32_e32 v2, v2
	v_pk_mul_f32 v[156:157], v[50:51], v[50:51]
	v_pk_mul_f32 v[168:169], v[20:21], v[20:21]
	v_pk_add_f32 v[22:23], v[22:23], v[78:79] op_sel_hi:[1,0] neg_lo:[0,1] neg_hi:[0,1]
	v_add_f32_e32 v2, 1.0, v2
	v_rcp_f32_e32 v107, v2
	v_mul_f32_e32 v2, 0xbfb8aa3b, v104
	v_exp_f32_e32 v2, v2
	v_pk_mul_f32 v[164:165], v[22:23], v[22:23]
	v_pk_mul_f32 v[102:103], v[106:107], v[102:103]
	v_pk_add_f32 v[24:25], v[24:25], v[78:79] op_sel_hi:[1,0] neg_lo:[0,1] neg_hi:[0,1]
	v_add_f32_e32 v2, 1.0, v2
	v_rcp_f32_e32 v106, v2
	v_mul_f32_e32 v2, 0xbfb8aa3b, v105
	v_exp_f32_e32 v2, v2
	v_pk_mul_f32 v[172:173], v[24:25], v[24:25]
	v_pk_add_f32 v[26:27], v[26:27], v[78:79] op_sel_hi:[1,0] neg_lo:[0,1] neg_hi:[0,1]
	v_pk_add_f32 v[28:29], v[28:29], v[78:79] op_sel_hi:[1,0] neg_lo:[0,1] neg_hi:[0,1]
	v_add_f32_e32 v2, 1.0, v2
	v_rcp_f32_e32 v107, v2
	v_pk_mul_f32 v[170:171], v[26:27], v[26:27]
	v_pk_mul_f32 v[176:177], v[28:29], v[28:29]
	v_pk_add_f32 v[30:31], v[30:31], v[78:79] op_sel_hi:[1,0] neg_lo:[0,1] neg_hi:[0,1]
	v_pk_mul_f32 v[104:105], v[106:107], v[104:105]
	v_lshlrev_b32_e32 v106, 16, v108
	v_mul_f32_e32 v2, 0xbfb8aa3b, v106
	v_exp_f32_e32 v2, v2
	v_and_b32_e32 v107, 0xffff0000, v108
	v_lshlrev_b32_e32 v108, 16, v109
	v_and_b32_e32 v109, 0xffff0000, v109
	v_add_f32_e32 v2, 1.0, v2
	v_rcp_f32_e32 v110, v2
	v_mul_f32_e32 v2, 0xbfb8aa3b, v107
	v_exp_f32_e32 v2, v2
	v_pk_mul_f32 v[174:175], v[30:31], v[30:31]
	v_pk_add_f32 v[32:33], v[32:33], v[78:79] op_sel_hi:[1,0] neg_lo:[0,1] neg_hi:[0,1]
	v_pk_add_f32 v[34:35], v[34:35], v[78:79] op_sel_hi:[1,0] neg_lo:[0,1] neg_hi:[0,1]
	v_add_f32_e32 v2, 1.0, v2
	v_rcp_f32_e32 v111, v2
	v_mul_f32_e32 v2, 0xbfb8aa3b, v108
	v_exp_f32_e32 v2, v2
	v_pk_mul_f32 v[180:181], v[32:33], v[32:33]
	v_pk_mul_f32 v[106:107], v[110:111], v[106:107]
	v_pk_mul_f32 v[178:179], v[34:35], v[34:35]
	v_add_f32_e32 v2, 1.0, v2
	v_rcp_f32_e32 v110, v2
	v_mul_f32_e32 v2, 0xbfb8aa3b, v109
	v_exp_f32_e32 v2, v2
	v_pk_add_f32 v[4:5], v[4:5], v[78:79] op_sel_hi:[1,0] neg_lo:[0,1] neg_hi:[0,1]
	v_pk_add_f32 v[6:7], v[6:7], v[78:79] op_sel_hi:[1,0] neg_lo:[0,1] neg_hi:[0,1]
	v_pk_mul_f32 v[196:197], v[4:5], v[4:5]
	v_add_f32_e32 v2, 1.0, v2
	v_rcp_f32_e32 v111, v2
	v_pk_mul_f32 v[194:195], v[6:7], v[6:7]
	v_pk_add_f32 v[8:9], v[8:9], v[78:79] op_sel_hi:[1,0] neg_lo:[0,1] neg_hi:[0,1]
	v_pk_add_f32 v[10:11], v[10:11], v[78:79] op_sel_hi:[1,0] neg_lo:[0,1] neg_hi:[0,1]
	v_pk_mul_f32 v[108:109], v[110:111], v[108:109]
	v_lshlrev_b32_e32 v110, 16, v114
	v_mul_f32_e32 v2, 0xbfb8aa3b, v110
	v_exp_f32_e32 v2, v2
	v_and_b32_e32 v111, 0xffff0000, v114
	v_lshlrev_b32_e32 v114, 16, v115
	v_and_b32_e32 v115, 0xffff0000, v115
	v_add_f32_e32 v2, 1.0, v2
	v_rcp_f32_e32 v118, v2
	v_mul_f32_e32 v2, 0xbfb8aa3b, v111
	v_exp_f32_e32 v2, v2
	v_pk_mul_f32 v[186:187], v[8:9], v[8:9]
	v_pk_mul_f32 v[184:185], v[10:11], v[10:11]
	v_pk_add_f32 v[12:13], v[12:13], v[78:79] op_sel_hi:[1,0] neg_lo:[0,1] neg_hi:[0,1]
	v_add_f32_e32 v2, 1.0, v2
	v_rcp_f32_e32 v119, v2
	v_mul_f32_e32 v2, 0xbfb8aa3b, v114
	v_exp_f32_e32 v2, v2
	v_pk_mul_f32 v[78:79], v[12:13], v[12:13]
	v_pk_mul_f32 v[110:111], v[118:119], v[110:111]
	v_lshl_add_u64 v[18:19], v[82:83], 0, s[2:3]
	v_add_f32_e32 v2, 1.0, v2
	v_rcp_f32_e32 v118, v2
	v_mul_f32_e32 v2, 0xbfb8aa3b, v115
	v_exp_f32_e32 v2, v2
	s_mov_b32 s2, 0x25800000
	v_add_f32_e32 v2, 1.0, v2
	v_rcp_f32_e32 v119, v2
	s_nop 0
	v_pk_mul_f32 v[114:115], v[118:119], v[114:115]
	v_lshlrev_b32_e32 v118, 16, v120
	v_mul_f32_e32 v2, 0xbfb8aa3b, v118
	v_exp_f32_e32 v2, v2
	v_and_b32_e32 v119, 0xffff0000, v120
	v_lshlrev_b32_e32 v120, 16, v121
	v_and_b32_e32 v121, 0xffff0000, v121
	v_add_f32_e32 v2, 1.0, v2
	v_rcp_f32_e32 v126, v2
	v_mul_f32_e32 v2, 0xbfb8aa3b, v119
	v_exp_f32_e32 v2, v2
	s_nop 0
	v_add_f32_e32 v2, 1.0, v2
	v_rcp_f32_e32 v127, v2
	v_mul_f32_e32 v2, 0xbfb8aa3b, v120
	v_exp_f32_e32 v2, v2
	v_pk_mul_f32 v[118:119], v[126:127], v[118:119]
	v_add_f32_e32 v2, 1.0, v2
	v_rcp_f32_e32 v126, v2
	v_mul_f32_e32 v2, 0xbfb8aa3b, v121
	v_exp_f32_e32 v2, v2
	s_nop 0
	v_add_f32_e32 v2, 1.0, v2
	v_rcp_f32_e32 v127, v2
	s_nop 0
	v_pk_mul_f32 v[120:121], v[126:127], v[120:121]
	v_lshlrev_b32_e32 v126, 16, v128
	v_mul_f32_e32 v2, 0xbfb8aa3b, v126
	v_exp_f32_e32 v2, v2
	v_and_b32_e32 v127, 0xffff0000, v128
	v_lshlrev_b32_e32 v128, 16, v129
	v_and_b32_e32 v129, 0xffff0000, v129
	v_add_f32_e32 v2, 1.0, v2
	v_rcp_f32_e32 v134, v2
	v_mul_f32_e32 v2, 0xbfb8aa3b, v127
	v_exp_f32_e32 v2, v2
	s_nop 0
	v_add_f32_e32 v2, 1.0, v2
	v_rcp_f32_e32 v135, v2
	v_mul_f32_e32 v2, 0xbfb8aa3b, v128
	v_exp_f32_e32 v2, v2
	v_pk_mul_f32 v[126:127], v[134:135], v[126:127]
	v_add_f32_e32 v2, 1.0, v2
	v_rcp_f32_e32 v134, v2
	v_mul_f32_e32 v2, 0xbfb8aa3b, v129
	v_exp_f32_e32 v2, v2
	s_nop 0
	v_add_f32_e32 v2, 1.0, v2
	v_rcp_f32_e32 v135, v2
	s_nop 0
	v_pk_mul_f32 v[128:129], v[134:135], v[128:129]
	v_lshlrev_b32_e32 v134, 16, v136
	v_mul_f32_e32 v2, 0xbfb8aa3b, v134
	v_exp_f32_e32 v2, v2
	v_and_b32_e32 v135, 0xffff0000, v136
	v_lshlrev_b32_e32 v136, 16, v137
	v_and_b32_e32 v137, 0xffff0000, v137
	v_add_f32_e32 v2, 1.0, v2
	v_rcp_f32_e32 v142, v2
	v_mul_f32_e32 v2, 0xbfb8aa3b, v135
	v_exp_f32_e32 v2, v2
	s_nop 0
	v_add_f32_e32 v2, 1.0, v2
	v_rcp_f32_e32 v143, v2
	v_mul_f32_e32 v2, 0xbfb8aa3b, v136
	v_exp_f32_e32 v2, v2
	v_pk_mul_f32 v[134:135], v[142:143], v[134:135]
	v_add_f32_e32 v2, 1.0, v2
	v_rcp_f32_e32 v142, v2
	v_mul_f32_e32 v2, 0xbfb8aa3b, v137
	v_exp_f32_e32 v2, v2
	s_nop 0
	v_add_f32_e32 v2, 1.0, v2
	v_rcp_f32_e32 v143, v2
	s_nop 0
	v_pk_mul_f32 v[136:137], v[142:143], v[136:137]
	v_lshlrev_b32_e32 v142, 16, v144
	v_mul_f32_e32 v2, 0xbfb8aa3b, v142
	v_exp_f32_e32 v2, v2
	v_and_b32_e32 v143, 0xffff0000, v144
	v_lshlrev_b32_e32 v144, 16, v145
	v_and_b32_e32 v145, 0xffff0000, v145
	v_add_f32_e32 v2, 1.0, v2
	v_rcp_f32_e32 v148, v2
	v_mul_f32_e32 v2, 0xbfb8aa3b, v143
	v_exp_f32_e32 v2, v2
	s_nop 0
	v_add_f32_e32 v2, 1.0, v2
	v_rcp_f32_e32 v149, v2
	v_mul_f32_e32 v2, 0xbfb8aa3b, v144
	v_exp_f32_e32 v2, v2
	v_pk_mul_f32 v[142:143], v[148:149], v[142:143]
	v_add_f32_e32 v2, 1.0, v2
	v_rcp_f32_e32 v148, v2
	v_mul_f32_e32 v2, 0xbfb8aa3b, v145
	v_exp_f32_e32 v2, v2
	s_nop 0
	v_add_f32_e32 v2, 1.0, v2
	v_rcp_f32_e32 v149, v2
	s_nop 0
	v_pk_mul_f32 v[144:145], v[148:149], v[144:145]
	v_lshlrev_b32_e32 v148, 16, v152
	v_mul_f32_e32 v2, 0xbfb8aa3b, v148
	v_exp_f32_e32 v2, v2
	v_and_b32_e32 v149, 0xffff0000, v152
	v_lshlrev_b32_e32 v152, 16, v153
	v_and_b32_e32 v153, 0xffff0000, v153
	v_add_f32_e32 v2, 1.0, v2
	v_rcp_f32_e32 v154, v2
	v_mul_f32_e32 v2, 0xbfb8aa3b, v149
	v_exp_f32_e32 v2, v2
	s_nop 0
	v_add_f32_e32 v2, 1.0, v2
	v_rcp_f32_e32 v155, v2
	v_mul_f32_e32 v2, 0xbfb8aa3b, v152
	v_exp_f32_e32 v2, v2
	v_pk_mul_f32 v[148:149], v[154:155], v[148:149]
	v_add_f32_e32 v2, 1.0, v2
	v_rcp_f32_e32 v154, v2
	v_mul_f32_e32 v2, 0xbfb8aa3b, v153
	v_exp_f32_e32 v2, v2
	s_nop 0
	v_add_f32_e32 v2, 1.0, v2
	v_rcp_f32_e32 v155, v2
	s_nop 0
	v_pk_mul_f32 v[152:153], v[154:155], v[152:153]
	v_lshlrev_b32_e32 v154, 16, v160
	v_mul_f32_e32 v2, 0xbfb8aa3b, v154
	v_exp_f32_e32 v2, v2
	v_and_b32_e32 v155, 0xffff0000, v160
	v_lshlrev_b32_e32 v160, 16, v161
	v_and_b32_e32 v161, 0xffff0000, v161
	v_add_f32_e32 v2, 1.0, v2
	v_rcp_f32_e32 v162, v2
	v_mul_f32_e32 v2, 0xbfb8aa3b, v155
	v_exp_f32_e32 v2, v2
	s_nop 0
	v_add_f32_e32 v2, 1.0, v2
	v_rcp_f32_e32 v163, v2
	v_mul_f32_e32 v2, 0xbfb8aa3b, v160
	v_exp_f32_e32 v2, v2
	v_pk_mul_f32 v[154:155], v[162:163], v[154:155]
	v_add_f32_e32 v2, 1.0, v2
	v_rcp_f32_e32 v162, v2
	v_mul_f32_e32 v2, 0xbfb8aa3b, v161
	v_exp_f32_e32 v2, v2
	s_nop 0
	v_add_f32_e32 v2, 1.0, v2
	v_rcp_f32_e32 v163, v2
	s_nop 0
	v_pk_mul_f32 v[160:161], v[162:163], v[160:161]
	v_lshlrev_b32_e32 v162, 16, v166
	v_mul_f32_e32 v2, 0xbfb8aa3b, v162
	v_exp_f32_e32 v2, v2
	v_and_b32_e32 v163, 0xffff0000, v166
	v_lshlrev_b32_e32 v166, 16, v167
	v_and_b32_e32 v167, 0xffff0000, v167
	v_add_f32_e32 v2, 1.0, v2
	v_rcp_f32_e32 v182, v2
	v_mul_f32_e32 v2, 0xbfb8aa3b, v163
	v_exp_f32_e32 v2, v2
	s_nop 0
	v_add_f32_e32 v2, 1.0, v2
	v_rcp_f32_e32 v183, v2
	v_mul_f32_e32 v2, 0xbfb8aa3b, v166
	v_exp_f32_e32 v2, v2
	v_pk_mul_f32 v[162:163], v[182:183], v[162:163]
	v_add_f32_e32 v2, 1.0, v2
	v_rcp_f32_e32 v182, v2
	v_mul_f32_e32 v2, 0xbfb8aa3b, v167
	v_exp_f32_e32 v2, v2
	s_nop 0
	v_add_f32_e32 v2, 1.0, v2
	v_rcp_f32_e32 v183, v2
	s_nop 0
	v_pk_mul_f32 v[166:167], v[182:183], v[166:167]
	global_load_dwordx2 v[182:183], v[68:69], off offset:208
	s_waitcnt vmcnt(0) lgkmcnt(0)
	v_lshlrev_b32_e32 v188, 16, v182
	v_mul_f32_e32 v2, 0xbfb8aa3b, v188
	v_exp_f32_e32 v2, v2
	v_and_b32_e32 v189, 0xffff0000, v182
	v_lshlrev_b32_e32 v182, 16, v183
	v_and_b32_e32 v183, 0xffff0000, v183
	v_add_f32_e32 v2, 1.0, v2
	v_rcp_f32_e32 v190, v2
	v_mul_f32_e32 v2, 0xbfb8aa3b, v189
	v_exp_f32_e32 v2, v2
	s_nop 0
	v_add_f32_e32 v2, 1.0, v2
	v_rcp_f32_e32 v191, v2
	v_mul_f32_e32 v2, 0xbfb8aa3b, v182
	v_exp_f32_e32 v2, v2
	v_pk_mul_f32 v[198:199], v[190:191], v[188:189]
	v_add_f32_e32 v2, 1.0, v2
	v_rcp_f32_e32 v188, v2
	v_mul_f32_e32 v2, 0xbfb8aa3b, v183
	v_exp_f32_e32 v2, v2
	s_nop 0
	v_add_f32_e32 v2, 1.0, v2
	v_rcp_f32_e32 v189, v2
	v_add_f32_e32 v2, v88, v89
	v_add_f32_e32 v2, v86, v2
	v_add_f32_e32 v2, v87, v2
	v_add_f32_e32 v2, v96, v2
	v_pk_mul_f32 v[200:201], v[188:189], v[182:183]
	global_load_dwordx2 v[182:183], v[68:69], off offset:224
	v_add_f32_e32 v2, v97, v2
	v_add_f32_e32 v2, v94, v2
	v_add_f32_e32 v2, v95, v2
	v_add_f32_e32 v2, v116, v2
	v_add_f32_e32 v2, v117, v2
	v_add_f32_e32 v2, v112, v2
	v_add_f32_e32 v2, v113, v2
	v_add_f32_e32 v2, v124, v2
	v_add_f32_e32 v2, v125, v2
	v_add_f32_e32 v2, v122, v2
	v_add_f32_e32 v2, v123, v2
	v_add_f32_e32 v2, v132, v2
	v_add_f32_e32 v2, v133, v2
	v_add_f32_e32 v2, v130, v2
	v_add_f32_e32 v2, v131, v2
	v_add_f32_e32 v2, v140, v2
	v_add_f32_e32 v2, v141, v2
	v_add_f32_e32 v2, v138, v2
	v_add_f32_e32 v2, v139, v2
	v_add_f32_e32 v2, v150, v2
	v_add_f32_e32 v2, v151, v2
	v_add_f32_e32 v2, v146, v2
	v_add_f32_e32 v2, v147, v2
	v_add_f32_e32 v2, v158, v2
	v_add_f32_e32 v2, v159, v2
	v_add_f32_e32 v2, v156, v2
	v_add_f32_e32 v2, v157, v2
	v_add_f32_e32 v2, v168, v2
	v_add_f32_e32 v2, v169, v2
	v_add_f32_e32 v2, v164, v2
	v_add_f32_e32 v2, v165, v2
	v_add_f32_e32 v2, v172, v2
	v_add_f32_e32 v2, v173, v2
	v_add_f32_e32 v2, v170, v2
	v_add_f32_e32 v2, v171, v2
	v_add_f32_e32 v2, v176, v2
	v_add_f32_e32 v2, v177, v2
	v_add_f32_e32 v2, v174, v2
	v_add_f32_e32 v2, v175, v2
	v_add_f32_e32 v2, v180, v2
	v_add_f32_e32 v2, v181, v2
	v_add_f32_e32 v2, v178, v2
	v_add_f32_e32 v2, v179, v2
	v_add_f32_e32 v2, v196, v2
	v_add_f32_e32 v2, v197, v2
	v_add_f32_e32 v2, v194, v2
	v_add_f32_e32 v2, v195, v2
	v_add_f32_e32 v2, v186, v2
	v_add_f32_e32 v2, v187, v2
	v_add_f32_e32 v2, v184, v2
	v_add_f32_e32 v2, v185, v2
	v_add_f32_e32 v2, v78, v2
	v_add_f32_e32 v2, v79, v2
	v_add_f32_e32 v2, v72, v2
	v_add_f32_e32 v2, v73, v2
	v_add_f32_e32 v2, v74, v2
	v_add_f32_e32 v2, v75, v2
	v_add_f32_e32 v2, v76, v2
	v_add_f32_e32 v2, v77, v2
	ds_bpermute_b32 v1, v1, v2
	s_waitcnt lgkmcnt(0)
	v_add_f32_e32 v1, v2, v1
	v_fmamk_f32 v1, v1, 0x3c000000, v241
	v_cmp_gt_f32_e32 vcc, s25, v1
	v_mul_f32_e32 v2, 0x4b800000, v1
	s_nop 0
	v_cndmask_b32_e32 v1, v1, v2, vcc
	v_rsq_f32_e32 v1, v1
	s_nop 0
	v_mul_f32_e32 v2, 0x45800000, v1
	v_cndmask_b32_e32 v2, v1, v2, vcc
	v_pk_mul_f32 v[4:5], v[4:5], v[2:3] op_sel_hi:[1,0]
	v_pk_mul_f32 v[6:7], v[6:7], v[2:3] op_sel_hi:[1,0]
	v_pk_mul_f32 v[4:5], v[162:163], v[4:5]
	v_pk_mul_f32 v[6:7], v[166:167], v[6:7]
	v_cvt_pk_bf16_f32 v4, v4, v5
	v_cvt_pk_bf16_f32 v5, v6, v7
	global_store_dwordx2 v[18:19], v[4:5], off offset:192
	v_pk_mul_f32 v[4:5], v[8:9], v[2:3] op_sel_hi:[1,0]
	v_pk_mul_f32 v[6:7], v[10:11], v[2:3] op_sel_hi:[1,0]
	v_pk_mul_f32 v[4:5], v[198:199], v[4:5]
	v_pk_mul_f32 v[6:7], v[200:201], v[6:7]
	v_cvt_pk_bf16_f32 v4, v4, v5
	v_cvt_pk_bf16_f32 v5, v6, v7
	global_store_dwordx2 v[18:19], v[4:5], off offset:208
	s_waitcnt vmcnt(0)
	v_lshlrev_b32_e32 v4, 16, v182
	v_mul_f32_e32 v1, 0xbfb8aa3b, v4
	v_exp_f32_e32 v1, v1
	v_and_b32_e32 v5, 0xffff0000, v182
	v_pk_mul_f32 v[8:9], v[12:13], v[2:3] op_sel_hi:[1,0]
	v_pk_mul_f32 v[10:11], v[70:71], v[2:3] op_sel_hi:[1,0]
	v_add_f32_e32 v1, 1.0, v1
	v_rcp_f32_e32 v6, v1
	v_mul_f32_e32 v1, 0xbfb8aa3b, v5
	v_exp_f32_e32 v1, v1
	v_pk_mul_f32 v[52:53], v[52:53], v[2:3] op_sel_hi:[1,0]
	v_pk_mul_f32 v[54:55], v[54:55], v[2:3] op_sel_hi:[1,0]
	v_pk_mul_f32 v[52:53], v[80:81], v[52:53]
	v_add_f32_e32 v1, 1.0, v1
	v_rcp_f32_e32 v7, v1
	v_pk_mul_f32 v[54:55], v[84:85], v[54:55]
	v_pk_mul_f32 v[36:37], v[36:37], v[2:3] op_sel_hi:[1,0]
	v_pk_mul_f32 v[38:39], v[38:39], v[2:3] op_sel_hi:[1,0]
	v_pk_mul_f32 v[4:5], v[6:7], v[4:5]
	v_lshlrev_b32_e32 v6, 16, v183
	v_mul_f32_e32 v1, 0xbfb8aa3b, v6
	v_exp_f32_e32 v1, v1
	v_and_b32_e32 v7, 0xffff0000, v183
	v_pk_mul_f32 v[4:5], v[4:5], v[8:9]
	v_pk_mul_f32 v[20:21], v[20:21], v[2:3] op_sel_hi:[1,0]
	v_add_f32_e32 v1, 1.0, v1
	v_rcp_f32_e32 v8, v1
	v_mul_f32_e32 v1, 0xbfb8aa3b, v7
	v_exp_f32_e32 v1, v1
	v_cvt_pk_bf16_f32 v4, v4, v5
	v_pk_mul_f32 v[22:23], v[22:23], v[2:3] op_sel_hi:[1,0]
	v_cvt_pk_bf16_f32 v52, v52, v53
	v_add_f32_e32 v1, 1.0, v1
	v_rcp_f32_e32 v9, v1
	v_cvt_pk_bf16_f32 v53, v54, v55
	v_add_co_u32_e32 v54, vcc, s2, v82
	v_pk_mul_f32 v[6:7], v[8:9], v[6:7]
	v_pk_mul_f32 v[36:37], v[106:107], v[36:37]
	v_pk_mul_f32 v[6:7], v[6:7], v[10:11]
	v_pk_mul_f32 v[10:11], v[16:17], v[2:3] op_sel_hi:[1,0]
	v_cvt_pk_bf16_f32 v5, v6, v7
	global_store_dwordx2 v[18:19], v[4:5], off offset:224
	global_load_dwordx2 v[4:5], v[68:69], off offset:240
	v_pk_mul_f32 v[38:39], v[108:109], v[38:39]
	v_pk_mul_f32 v[20:21], v[134:135], v[20:21]
	v_pk_mul_f32 v[22:23], v[136:137], v[22:23]
	v_addc_co_u32_e32 v55, vcc, 0, v83, vcc
	v_cvt_pk_bf16_f32 v36, v36, v37
	v_cvt_pk_bf16_f32 v37, v38, v39
	v_cvt_pk_bf16_f32 v20, v20, v21
	v_cvt_pk_bf16_f32 v21, v22, v23
	global_store_dwordx2 v[54:55], v[52:53], off
	v_pk_mul_f32 v[52:53], v[56:57], v[2:3] op_sel_hi:[1,0]
	v_pk_mul_f32 v[54:55], v[58:59], v[2:3] op_sel_hi:[1,0]
	global_store_dwordx2 v[18:19], v[36:37], off offset:64
	v_pk_mul_f32 v[36:37], v[40:41], v[2:3] op_sel_hi:[1,0]
	v_pk_mul_f32 v[38:39], v[42:43], v[2:3] op_sel_hi:[1,0]
	global_store_dwordx2 v[18:19], v[20:21], off offset:128
	v_pk_mul_f32 v[20:21], v[24:25], v[2:3] op_sel_hi:[1,0]
	v_pk_mul_f32 v[22:23], v[26:27], v[2:3] op_sel_hi:[1,0]
	v_pk_mul_f32 v[52:53], v[90:91], v[52:53]
	v_pk_mul_f32 v[54:55], v[92:93], v[54:55]
	v_pk_mul_f32 v[36:37], v[110:111], v[36:37]
	v_pk_mul_f32 v[38:39], v[114:115], v[38:39]
	v_pk_mul_f32 v[20:21], v[142:143], v[20:21]
	v_pk_mul_f32 v[22:23], v[144:145], v[22:23]
	v_cvt_pk_bf16_f32 v52, v52, v53
	v_cvt_pk_bf16_f32 v53, v54, v55
	v_cvt_pk_bf16_f32 v36, v36, v37
	v_cvt_pk_bf16_f32 v37, v38, v39
	v_cvt_pk_bf16_f32 v20, v20, v21
	v_cvt_pk_bf16_f32 v21, v22, v23
	global_store_dwordx2 v[18:19], v[52:53], off offset:16
	v_pk_mul_f32 v[52:53], v[60:61], v[2:3] op_sel_hi:[1,0]
	v_pk_mul_f32 v[54:55], v[62:63], v[2:3] op_sel_hi:[1,0]
	global_store_dwordx2 v[18:19], v[36:37], off offset:80
	v_pk_mul_f32 v[36:37], v[44:45], v[2:3] op_sel_hi:[1,0]
	v_pk_mul_f32 v[38:39], v[46:47], v[2:3] op_sel_hi:[1,0]
	global_store_dwordx2 v[18:19], v[20:21], off offset:144
	v_pk_mul_f32 v[20:21], v[28:29], v[2:3] op_sel_hi:[1,0]
	v_pk_mul_f32 v[22:23], v[30:31], v[2:3] op_sel_hi:[1,0]
	v_pk_mul_f32 v[52:53], v[98:99], v[52:53]
	v_pk_mul_f32 v[54:55], v[100:101], v[54:55]
	v_pk_mul_f32 v[36:37], v[118:119], v[36:37]
	v_pk_mul_f32 v[38:39], v[120:121], v[38:39]
	v_pk_mul_f32 v[20:21], v[148:149], v[20:21]
	v_pk_mul_f32 v[22:23], v[152:153], v[22:23]
	v_cvt_pk_bf16_f32 v52, v52, v53
	v_cvt_pk_bf16_f32 v53, v54, v55
	v_cvt_pk_bf16_f32 v36, v36, v37
	v_cvt_pk_bf16_f32 v37, v38, v39
	v_cvt_pk_bf16_f32 v20, v20, v21
	v_cvt_pk_bf16_f32 v21, v22, v23
	global_store_dwordx2 v[18:19], v[52:53], off offset:32
	v_pk_mul_f32 v[52:53], v[64:65], v[2:3] op_sel_hi:[1,0]
	v_pk_mul_f32 v[54:55], v[66:67], v[2:3] op_sel_hi:[1,0]
	global_store_dwordx2 v[18:19], v[36:37], off offset:96
	v_pk_mul_f32 v[36:37], v[48:49], v[2:3] op_sel_hi:[1,0]
	v_pk_mul_f32 v[38:39], v[50:51], v[2:3] op_sel_hi:[1,0]
	global_store_dwordx2 v[18:19], v[20:21], off offset:160
	v_pk_mul_f32 v[20:21], v[32:33], v[2:3] op_sel_hi:[1,0]
	v_pk_mul_f32 v[22:23], v[34:35], v[2:3] op_sel_hi:[1,0]
	v_pk_mul_f32 v[52:53], v[102:103], v[52:53]
	v_pk_mul_f32 v[54:55], v[104:105], v[54:55]
	v_pk_mul_f32 v[36:37], v[126:127], v[36:37]
	v_pk_mul_f32 v[38:39], v[128:129], v[38:39]
	v_pk_mul_f32 v[20:21], v[154:155], v[20:21]
	v_pk_mul_f32 v[22:23], v[160:161], v[22:23]
	v_cvt_pk_bf16_f32 v52, v52, v53
	v_cvt_pk_bf16_f32 v53, v54, v55
	v_cvt_pk_bf16_f32 v36, v36, v37
	v_cvt_pk_bf16_f32 v37, v38, v39
	v_cvt_pk_bf16_f32 v20, v20, v21
	v_cvt_pk_bf16_f32 v21, v22, v23
	s_mov_b64 s[2:3], 0
	global_store_dwordx2 v[18:19], v[52:53], off offset:48
	global_store_dwordx2 v[18:19], v[36:37], off offset:112
	global_store_dwordx2 v[18:19], v[20:21], off offset:176
	s_waitcnt vmcnt(0) lgkmcnt(0)
	v_lshlrev_b32_e32 v6, 16, v4
	v_mul_f32_e32 v1, 0xbfb8aa3b, v6
	v_exp_f32_e32 v1, v1
	v_and_b32_e32 v7, 0xffff0000, v4
	v_add_f32_e32 v1, 1.0, v1
	v_rcp_f32_e32 v8, v1
	v_mul_f32_e32 v1, 0xbfb8aa3b, v7
	v_exp_f32_e32 v1, v1
	s_nop 0
	v_add_f32_e32 v1, 1.0, v1
	v_rcp_f32_e32 v9, v1
	s_nop 0
	v_pk_mul_f32 v[6:7], v[8:9], v[6:7]
	s_nop 0
	v_pk_mul_f32 v[6:7], v[6:7], v[10:11]
	v_pk_mul_f32 v[10:11], v[14:15], v[2:3] op_sel_hi:[1,0]
	v_cvt_pk_bf16_f32 v4, v6, v7
	v_lshlrev_b32_e32 v6, 16, v5
	v_mul_f32_e32 v1, 0xbfb8aa3b, v6
	v_exp_f32_e32 v1, v1
	v_and_b32_e32 v7, 0xffff0000, v5
	v_add_f32_e32 v1, 1.0, v1
	v_rcp_f32_e32 v8, v1
	v_mul_f32_e32 v1, 0xbfb8aa3b, v7
	v_exp_f32_e32 v1, v1
	s_nop 0
	v_add_f32_e32 v1, 1.0, v1
	v_rcp_f32_e32 v9, v1
	s_nop 0
	v_pk_mul_f32 v[6:7], v[8:9], v[6:7]
	s_nop 0
	v_pk_mul_f32 v[6:7], v[6:7], v[10:11]
	s_nop 0
	v_cvt_pk_bf16_f32 v5, v6, v7
	global_store_dwordx2 v[18:19], v[4:5], off offset:240

.LBB0_1136:
	s_waitcnt vmcnt(0) lgkmcnt(0)
	s_barrier
	s_and_saveexec_b64 s[2:3], s[36:37]
	s_cbranch_execz .LBB0_1138
	v_mov_b64_e32 v[4:5], s[0:1]
	global_atomic_add v1, v[4:5], v228, off sc0
	v_mov_b32_e32 v2, s10
	s_waitcnt vmcnt(0) lgkmcnt(0)
	ds_write_b32 v2, v1
.LBB0_1138:
	s_or_b64 exec, exec, s[2:3]
	v_mov_b32_e32 v1, s10
	s_waitcnt lgkmcnt(0)
	s_barrier
	ds_read_b32 v1, v1
	s_mov_b64 s[2:3], -1
	s_waitcnt lgkmcnt(0)
	v_cmp_lt_i32_e32 vcc, s75, v1
	v_readfirstlane_b32 s4, v1
	s_cbranch_vccnz .LBB0_1135
	v_mov_b32_e32 v209, v0
	s_lshl_b32 s2, s4, 4
	s_bfe_u32 s14, s4, 0x20002
	v_readfirstlane_b32 s8, v209
	s_and_b32 s15, s4, 3
	s_and_b32 s4, s2, 0xffffff00
	v_readlane_b32 s2, v252, 0
	s_mov_b32 s3, s88
	s_ashr_i32 s5, s8, 1
	s_and_b32 s16, s5, 0xffffffe0
	s_mov_b64 s[2:3], s[68:69]
	s_add_i32 s16, s16, s4
	s_lshl_b32 s5, s15, 7
	s_lshl_b32 s6, s15, 8
	v_and_b32_e32 v4, 31, v209
	s_add_u32 s6, s2, s6
	v_or_b32_e32 v207, s16, v4
	s_addc_u32 s7, s3, 0
	s_lshl_b32 s9, s14, 12
	v_add_u32_e32 v180, s9, v207
	v_ashrrev_i32_e32 v181, 31, v180
	v_bfe_u32 v5, v209, 5, 1
	v_lshlrev_b64 v[6:7], 10, v[180:181]
	v_lshl_add_u64 v[6:7], s[6:7], 0, v[6:7]
	v_lshlrev_b32_e32 v2, 4, v5
	v_lshl_add_u64 v[6:7], v[6:7], 0, v[2:3]
	s_mov_b64 s[6:7], 0x29800000
	v_lshl_add_u64 v[8:9], v[6:7], 0, s[6:7]
	s_mov_b32 s6, 0x29800000
	v_add_co_u32_e32 v6, vcc, s6, v6
	v_cvt_f32_ubyte0_e32 v1, s15
	s_nop 0
	v_addc_co_u32_e32 v7, vcc, 0, v7, vcc
	global_load_dwordx4 v[124:127], v[8:9], off offset:32
	global_load_dwordx4 v[120:123], v[8:9], off offset:64
	global_load_dwordx4 v[116:119], v[8:9], off offset:96
	global_load_dwordx4 v[112:115], v[8:9], off offset:128
	global_load_dwordx4 v[108:111], v[8:9], off offset:160
	global_load_dwordx4 v[104:107], v[8:9], off offset:192
	global_load_dwordx4 v[128:131], v[6:7], off
	global_load_dwordx4 v[100:103], v[8:9], off offset:224
	v_sub_f32_e32 v1, 0xc0a00000, v1
	s_mov_b32 s6, 0xc2fc0000
	v_cmp_gt_f32_e32 vcc, s6, v1
	v_mov_b32_e32 v6, 0x42800000
	s_and_b64 s[6:7], vcc, exec
	v_cndmask_b32_e32 v6, 0, v6, vcc
	v_add_f32_e32 v1, v1, v6
	v_exp_f32_e32 v1, v1
	s_cselect_b32 s6, 0xffffffc0, 0
	v_mov_b32_e32 v6, 0x42000000
	s_waitcnt lgkmcnt(0)
	v_ldexp_f32 v1, v1, s6
	v_sub_f32_e32 v1, 1.0, v1
	v_cmp_gt_f32_e32 vcc, s25, v1
	s_and_b64 s[6:7], vcc, exec
	s_cselect_b32 s6, 32, 0
	v_ldexp_f32 v1, v1, s6
	v_log_f32_e32 v1, v1
	v_cndmask_b32_e32 v6, 0, v6, vcc
	v_cmp_gt_i32_e32 vcc, 64, v209
	s_barrier
	v_sub_f32_e32 v208, v1, v6
	s_and_saveexec_b64 s[6:7], vcc
	s_cbranch_execz .LBB0_1141
	v_sub_u32_e32 v1, 63, v209
	v_cvt_f32_u32_e32 v1, v1
	s_mov_b32 s13, 0xc2fc0000
	v_not_b32_e32 v7, 63
	v_mul_f32_e32 v6, v208, v1
	v_cmp_gt_f32_e32 vcc, s13, v6
	v_mov_b32_e32 v6, 0x42800000
	s_nop 0
	v_cndmask_b32_e32 v6, 0, v6, vcc
	v_fmac_f32_e32 v6, v208, v1
	v_exp_f32_e32 v1, v6
	v_cndmask_b32_e32 v7, 0, v7, vcc
	v_lshl_add_u32 v6, v209, 2, s11
	v_ldexp_f32 v1, v1, v7
	ds_write_b32 v6, v1
.LBB0_1141:
	s_or_b64 exec, exec, s[6:7]
	s_add_i32 s13, s4, 0x100
	s_lshl_b32 s24, s5, 1
	s_add_u32 s6, s2, s24
	s_addc_u32 s7, s3, 0
	s_add_u32 s6, s6, 0x2a800000
	s_mul_i32 s17, s14, 0x480
	v_readlane_b32 s20, v253, 17
	s_addc_u32 s7, s7, 0
	s_add_i32 s5, s17, s5
	v_readlane_b32 s21, v253, 18
	s_mulk_i32 s5, 0x2100
	s_ashr_i32 s17, s13, 6
	s_mov_b32 s25, s21
	s_add_u32 s5, s2, s5
	v_readlane_b32 s22, v253, 19
	v_readlane_b32 s23, v253, 20
	s_mov_b64 s[20:21], s[24:25]
	s_addc_u32 s13, s3, 0
	v_writelane_b32 v253, s20, 17
	s_add_u32 s18, s5, 0x2b800000
	s_addc_u32 s19, s13, 0
	v_writelane_b32 v253, s21, 18
	v_ashrrev_i32_e32 v14, 4, v209
	s_add_i32 s13, s9, s4
	v_writelane_b32 v253, s22, 19
	v_add_u32_e32 v6, s13, v14
	v_writelane_b32 v253, s23, 20
	v_ashrrev_i32_e32 v7, 31, v6
	v_ashrrev_i32_e32 v15, 3, v209
	v_mov_b64_e32 v[8:9], s[18:19]
	s_movk_i32 s20, 0x2100
	s_ashr_i32 s5, s4, 31
	v_lshlrev_b64 v[6:7], 10, v[6:7]
	v_lshlrev_b32_e32 v1, 4, v209
	v_mad_i64_i32 v[10:11], s[18:19], v15, s20, v[8:9]
	v_lshl_add_u64 v[6:7], s[6:7], 0, v[6:7]
	v_and_b32_e32 v194, 0xf0, v1
	v_mov_b32_e32 v195, v3
	s_lshl_b64 s[18:19], s[4:5], 1
	v_add_u32_e32 v210, 0x200, v209
	v_lshl_add_u64 v[6:7], v[6:7], 0, v[194:195]
	v_lshl_add_u64 v[12:13], v[10:11], 0, s[18:19]
	v_and_b32_e32 v196, 0x70, v1
	v_mov_b32_e32 v197, v3
	v_ashrrev_i32_e32 v16, 4, v210
	v_lshl_add_u64 v[12:13], v[12:13], 0, v[196:197]
	global_load_dwordx4 v[132:135], v[6:7], off
	global_load_dwordx4 v[136:139], v[12:13], off
	v_add_u32_e32 v6, s13, v16
	v_ashrrev_i32_e32 v7, 31, v6
	v_lshlrev_b64 v[6:7], 10, v[6:7]
	v_ashrrev_i32_e32 v17, 3, v210
	v_lshl_add_u64 v[6:7], s[6:7], 0, v[6:7]
	v_mad_i64_i32 v[8:9], s[20:21], v17, s20, v[8:9]
	v_lshl_add_u64 v[6:7], v[6:7], 0, v[194:195]
	v_lshl_add_u64 v[12:13], v[8:9], 0, s[18:19]
	v_lshl_add_u64 v[12:13], v[12:13], 0, v[196:197]
	global_load_dwordx4 v[140:143], v[6:7], off
	global_load_dwordx4 v[144:147], v[12:13], off
	s_movk_i32 s13, 0x88
	s_movk_i32 s5, 0x110
	v_mul_lo_u32 v216, v15, s13
	v_mul_lo_u32 v219, v17, s13
	v_mul_lo_u32 v215, v14, s5
	v_add_u32_e32 v6, s72, v216
	v_mul_lo_u32 v218, v16, s5
	s_movk_i32 s5, 0x4400
	v_add_u32_e32 v12, s72, v219
	v_lshl_add_u64 v[198:199], s[6:7], 0, v[194:195]
	s_sub_i32 s6, s16, 63
	v_lshlrev_b32_e32 v211, 3, v5
	v_mul_u32_u24_e32 v1, 0x110, v4
	v_mul_u32_u24_e32 v212, 0x88, v4
	v_lshlrev_b32_e32 v206, 2, v5
	v_mov_b32_e32 v52, v3
	v_mov_b32_e32 v53, v3
	v_add3_u32 v5, s72, v215, v194
	v_add3_u32 v6, v6, v196, s5
	v_add3_u32 v7, s72, v218, v194
	v_add3_u32 v12, v12, v196, s5
	s_ashr_i32 s13, s8, 8
	v_add_u32_e32 v4, s6, v4
	v_mov_b32_e32 v54, v3
	v_mov_b32_e32 v55, v3
	v_mov_b32_e32 v56, v3
	v_mov_b32_e32 v57, v3
	v_mov_b32_e32 v58, v3
	v_mov_b32_e32 v59, v3
	v_mov_b32_e32 v60, v3
	v_mov_b32_e32 v61, v3
	v_add3_u32 v217, v14, s9, 64
	v_add3_u32 v220, v16, s9, 64
	s_lshl_b32 s18, s13, 7
	v_subrev_u32_e32 v195, s4, v4
	v_lshl_add_u64 v[200:201], v[10:11], 0, v[196:197]
	v_lshl_add_u64 v[202:203], v[8:9], 0, v[196:197]
	v_mov_b32_e32 v62, v3
	v_mov_b32_e32 v63, v3
	v_mov_b32_e32 v64, v3
	v_mov_b32_e32 v65, v3
	s_waitcnt vmcnt(0) lgkmcnt(0)
	ds_write_b128 v5, v[132:135]
	ds_write2_b64 v6, v[136:137], v[138:139] offset1:1
	ds_write_b128 v7, v[140:143]
	ds_write2_b64 v12, v[144:145], v[146:147] offset1:1
	v_mov_b32_e32 v66, v3
	v_mov_b32_e32 v67, v3
	v_mov_b64_e32 v[36:37], v[52:53]
	v_mov_b64_e32 v[20:21], v[52:53]
	v_mov_b64_e32 v[4:5], v[52:53]
	v_add_u32_e32 v213, s11, v2
	v_add_u32_e32 v214, s12, v2
	s_ashr_i32 s21, s4, 6
	s_or_b32 s5, s16, 31
	s_add_i32 s18, s18, s4
	s_mov_b32 s19, s4
	v_mov_b64_e32 v[38:39], v[54:55]
	v_mov_b64_e32 v[40:41], v[56:57]
	v_mov_b64_e32 v[42:43], v[58:59]
	v_mov_b64_e32 v[44:45], v[60:61]
	v_mov_b64_e32 v[46:47], v[62:63]
	v_mov_b64_e32 v[48:49], v[64:65]
	v_mov_b64_e32 v[50:51], v[66:67]
	v_mov_b64_e32 v[22:23], v[54:55]
	v_mov_b64_e32 v[24:25], v[56:57]
	v_mov_b64_e32 v[26:27], v[58:59]
	v_mov_b64_e32 v[28:29], v[60:61]
	v_mov_b64_e32 v[30:31], v[62:63]
	v_mov_b64_e32 v[32:33], v[64:65]
	v_mov_b64_e32 v[34:35], v[66:67]
	v_mov_b64_e32 v[6:7], v[54:55]
	v_mov_b64_e32 v[8:9], v[56:57]
	v_mov_b64_e32 v[10:11], v[58:59]
	v_mov_b64_e32 v[12:13], v[60:61]
	v_mov_b64_e32 v[14:15], v[62:63]
	v_mov_b64_e32 v[16:17], v[64:65]
	v_mov_b64_e32 v[18:19], v[66:67]
	s_waitcnt lgkmcnt(0)
	s_barrier
.LBB0_1142:
	s_add_i32 s20, s21, 1
	s_cmp_lt_i32 s20, s17
	s_cselect_b64 s[8:9], -1, 0
	s_cmp_ge_i32 s20, s17
	s_cselect_b64 s[6:7], -1, 0
	s_and_b64 vcc, exec, s[6:7]
	s_cbranch_vccnz .LBB0_1144
	v_add_u32_e32 v68, s19, v217
	s_add_i32 s22, s19, 64
	v_ashrrev_i32_e32 v69, 31, v68
	s_ashr_i32 s23, s22, 31
	v_lshlrev_b64 v[68:69], 10, v[68:69]
	v_lshl_add_u64 v[68:69], v[198:199], 0, v[68:69]
	s_lshl_b64 s[22:23], s[22:23], 1
	v_lshl_add_u64 v[70:71], v[200:201], 0, s[22:23]
	s_waitcnt vmcnt(0)
	global_load_dwordx4 v[132:135], v[68:69], off
	global_load_dwordx4 v[136:139], v[70:71], off
	v_add_u32_e32 v68, s19, v220
	v_ashrrev_i32_e32 v69, 31, v68
	v_lshlrev_b64 v[68:69], 10, v[68:69]
	v_lshl_add_u64 v[68:69], v[198:199], 0, v[68:69]
	v_lshl_add_u64 v[70:71], v[202:203], 0, s[22:23]
	global_load_dwordx4 v[140:143], v[68:69], off
	global_load_dwordx4 v[144:147], v[70:71], off

.LBB0_1209:
	v_xor_b32_e32 v1, 32, v230
	v_cmp_lt_i32_e32 vcc, v1, v231
	v_lshlrev_b64 v[68:69], 12, v[2:3]
	v_lshl_add_u64 v[68:69], s[8:9], 0, v[68:69]
	v_cndmask_b32_e32 v1, v230, v1, vcc
	v_lshlrev_b32_e32 v1, 2, v1
	ds_bpermute_b32 v1, v1, v151
	v_lshl_add_u64 v[68:69], s[10:11], 1, v[68:69]
	s_movk_i32 s24, 0x7200
	s_waitcnt lgkmcnt(0)
	v_add_f32_e32 v1, v151, v1
	v_div_scale_f32 v2, s[0:1], v1, v1, 1.0
	v_rcp_f32_e32 v70, v2
	s_mov_b64 s[0:1], 0x25800400
	v_fma_f32 v71, -v2, v70, 1.0
	v_fmac_f32_e32 v70, v71, v70
	v_div_scale_f32 v71, vcc, 1.0, v1, 1.0
	v_mul_f32_e32 v72, v71, v70
	v_fma_f32 v73, -v2, v72, v71
	v_fmac_f32_e32 v72, v73, v70
	v_fma_f32 v2, -v2, v72, v71
	v_div_fmas_f32 v2, v2, v70, v72
	v_div_fixup_f32 v70, v2, v1, 1.0
	v_pk_mul_f32 v[52:53], v[52:53], v[70:71] op_sel_hi:[1,0]
	v_pk_mul_f32 v[54:55], v[54:55], v[70:71] op_sel_hi:[1,0]
	v_lshlrev_b32_e32 v2, 1, v149
	v_cvt_pk_bf16_f32 v52, v52, v53
	v_cvt_pk_bf16_f32 v53, v54, v55
	v_lshl_add_u64 v[54:55], v[68:69], 0, v[2:3]
	v_lshl_add_u64 v[68:69], v[54:55], 0, s[0:1]
	s_mov_b32 s0, 0x25800000
	v_add_co_u32_e32 v54, vcc, s0, v54
	v_pk_mul_f32 v[36:37], v[36:37], v[70:71] op_sel_hi:[1,0]
	v_pk_mul_f32 v[38:39], v[38:39], v[70:71] op_sel_hi:[1,0]
	v_pk_mul_f32 v[20:21], v[20:21], v[70:71] op_sel_hi:[1,0]
	v_pk_mul_f32 v[22:23], v[22:23], v[70:71] op_sel_hi:[1,0]
	v_pk_mul_f32 v[4:5], v[4:5], v[70:71] op_sel_hi:[1,0]
	v_pk_mul_f32 v[6:7], v[6:7], v[70:71] op_sel_hi:[1,0]
	v_addc_co_u32_e32 v55, vcc, 0, v55, vcc
	v_cvt_pk_bf16_f32 v36, v36, v37
	v_cvt_pk_bf16_f32 v37, v38, v39
	v_cvt_pk_bf16_f32 v20, v20, v21
	v_cvt_pk_bf16_f32 v21, v22, v23
	v_cvt_pk_bf16_f32 v4, v4, v5
	v_cvt_pk_bf16_f32 v5, v6, v7
	global_store_dwordx2 v[54:55], v[52:53], off offset:1024
	v_pk_mul_f32 v[52:53], v[56:57], v[70:71] op_sel_hi:[1,0]
	v_pk_mul_f32 v[54:55], v[58:59], v[70:71] op_sel_hi:[1,0]
	global_store_dwordx2 v[68:69], v[36:37], off offset:64
	v_pk_mul_f32 v[36:37], v[40:41], v[70:71] op_sel_hi:[1,0]
	v_pk_mul_f32 v[38:39], v[42:43], v[70:71] op_sel_hi:[1,0]
	global_store_dwordx2 v[68:69], v[20:21], off offset:128
	v_pk_mul_f32 v[20:21], v[24:25], v[70:71] op_sel_hi:[1,0]
	v_pk_mul_f32 v[22:23], v[26:27], v[70:71] op_sel_hi:[1,0]
	global_store_dwordx2 v[68:69], v[4:5], off offset:192
	v_pk_mul_f32 v[4:5], v[8:9], v[70:71] op_sel_hi:[1,0]
	v_pk_mul_f32 v[6:7], v[10:11], v[70:71] op_sel_hi:[1,0]
	v_cvt_pk_bf16_f32 v52, v52, v53
	v_cvt_pk_bf16_f32 v53, v54, v55
	v_cvt_pk_bf16_f32 v36, v36, v37
	v_cvt_pk_bf16_f32 v37, v38, v39
	v_cvt_pk_bf16_f32 v20, v20, v21
	v_cvt_pk_bf16_f32 v21, v22, v23
	v_cvt_pk_bf16_f32 v4, v4, v5
	v_cvt_pk_bf16_f32 v5, v6, v7
	global_store_dwordx2 v[68:69], v[52:53], off offset:16
	v_pk_mul_f32 v[52:53], v[60:61], v[70:71] op_sel_hi:[1,0]
	v_pk_mul_f32 v[54:55], v[62:63], v[70:71] op_sel_hi:[1,0]
	global_store_dwordx2 v[68:69], v[36:37], off offset:80
	v_pk_mul_f32 v[36:37], v[44:45], v[70:71] op_sel_hi:[1,0]
	v_pk_mul_f32 v[38:39], v[46:47], v[70:71] op_sel_hi:[1,0]
	global_store_dwordx2 v[68:69], v[20:21], off offset:144
	v_pk_mul_f32 v[20:21], v[28:29], v[70:71] op_sel_hi:[1,0]
	v_pk_mul_f32 v[22:23], v[30:31], v[70:71] op_sel_hi:[1,0]
	global_store_dwordx2 v[68:69], v[4:5], off offset:208
	v_pk_mul_f32 v[4:5], v[12:13], v[70:71] op_sel_hi:[1,0]
	v_pk_mul_f32 v[6:7], v[14:15], v[70:71] op_sel_hi:[1,0]
	v_cvt_pk_bf16_f32 v52, v52, v53
	v_cvt_pk_bf16_f32 v53, v54, v55
	v_cvt_pk_bf16_f32 v36, v36, v37
	v_cvt_pk_bf16_f32 v37, v38, v39
	v_cvt_pk_bf16_f32 v20, v20, v21
	v_cvt_pk_bf16_f32 v21, v22, v23
	v_cvt_pk_bf16_f32 v4, v4, v5
	v_cvt_pk_bf16_f32 v5, v6, v7
	global_store_dwordx2 v[68:69], v[52:53], off offset:32
	v_pk_mul_f32 v[52:53], v[64:65], v[70:71] op_sel_hi:[1,0]
	v_pk_mul_f32 v[54:55], v[66:67], v[70:71] op_sel_hi:[1,0]
	global_store_dwordx2 v[68:69], v[36:37], off offset:96
	v_pk_mul_f32 v[36:37], v[48:49], v[70:71] op_sel_hi:[1,0]
	v_pk_mul_f32 v[38:39], v[50:51], v[70:71] op_sel_hi:[1,0]
	global_store_dwordx2 v[68:69], v[20:21], off offset:160
	v_pk_mul_f32 v[20:21], v[32:33], v[70:71] op_sel_hi:[1,0]
	v_pk_mul_f32 v[22:23], v[34:35], v[70:71] op_sel_hi:[1,0]
	global_store_dwordx2 v[68:69], v[4:5], off offset:224
	v_pk_mul_f32 v[4:5], v[16:17], v[70:71] op_sel_hi:[1,0]
	v_pk_mul_f32 v[6:7], v[18:19], v[70:71] op_sel_hi:[1,0]
	v_cvt_pk_bf16_f32 v52, v52, v53
	v_cvt_pk_bf16_f32 v53, v54, v55
	v_cvt_pk_bf16_f32 v36, v36, v37
	v_cvt_pk_bf16_f32 v37, v38, v39
	v_cvt_pk_bf16_f32 v20, v20, v21
	v_cvt_pk_bf16_f32 v21, v22, v23
	v_cvt_pk_bf16_f32 v4, v4, v5
	v_cvt_pk_bf16_f32 v5, v6, v7
	s_mov_b64 s[0:1], 0
	global_store_dwordx2 v[68:69], v[52:53], off offset:48
	global_store_dwordx2 v[68:69], v[36:37], off offset:112
	global_store_dwordx2 v[68:69], v[20:21], off offset:176
	global_store_dwordx2 v[68:69], v[4:5], off offset:240

.LBB0_1211:
	s_waitcnt vmcnt(0) lgkmcnt(0)
	s_barrier
	s_and_saveexec_b64 s[0:1], s[36:37]
	s_cbranch_execz .LBB0_1213
	v_mov_b64_e32 v[4:5], s[6:7]
	global_atomic_add v1, v[4:5], v228, off sc0
	v_mov_b32_e32 v2, s16
	s_waitcnt vmcnt(0) lgkmcnt(0)
	ds_write_b32 v2, v1
.LBB0_1213:
	s_or_b64 exec, exec, s[0:1]
	v_mov_b32_e32 v1, s16
	s_waitcnt lgkmcnt(0)
	s_barrier
	ds_read_b32 v1, v1
	s_mov_b64 s[0:1], -1
	s_waitcnt lgkmcnt(0)
	v_cmp_lt_i32_e32 vcc, s75, v1
	v_readfirstlane_b32 s8, v1
	s_cbranch_vccnz .LBB0_1210
	v_mov_b32_e32 v4, v0
	v_readlane_b32 s0, v252, 0
	s_mov_b32 s1, s88
	s_lshl_b32 s20, s8, 4
	v_readfirstlane_b32 s21, v4
	s_lshr_b32 s0, s21, 1
	s_andn2_b32 s20, s20, 63
	s_and_b32 s0, s0, 32
	s_and_b32 s10, s21, 0xffffff80
	s_sub_i32 s14, s0, s20
	s_ashr_i32 s11, s10, 31
	s_and_b32 s18, s8, 3
	s_mov_b64 s[8:9], s[68:69]
	s_add_i32 s15, s14, 0xfc0
	s_lshl_b64 s[0:1], s[10:11], 1
	s_add_u32 s0, s8, s0
	s_addc_u32 s1, s9, s1
	v_and_b32_e32 v8, 31, v4
	s_add_u32 s0, s0, 0x2de00000
	v_or_b32_e32 v1, s15, v8
	s_addc_u32 s1, s1, 0
	s_lshl_b32 s19, s18, 12
	v_bfe_u32 v9, v4, 5, 1
	v_add_u32_e32 v2, s19, v1
	v_mov_b64_e32 v[6:7], s[0:1]
	s_movk_i32 s0, 0xc00
	v_mad_u64_u32 v[6:7], s[0:1], v2, s0, v[6:7]
	v_lshlrev_b32_e32 v148, 4, v9
	v_mov_b32_e32 v149, v3
	v_lshl_add_u64 v[6:7], v[6:7], 0, v[148:149]
	global_load_dwordx4 v[100:103], v[6:7], off
	global_load_dwordx4 v[104:107], v[6:7], off offset:32
	global_load_dwordx4 v[108:111], v[6:7], off offset:64
	global_load_dwordx4 v[112:115], v[6:7], off offset:96
	global_load_dwordx4 v[116:119], v[6:7], off offset:128
	global_load_dwordx4 v[120:123], v[6:7], off offset:160
	global_load_dwordx4 v[124:127], v[6:7], off offset:192
	global_load_dwordx4 v[128:131], v[6:7], off offset:224
	v_lshl_add_u64 v[6:7], v[2:3], 2, s[8:9]
	v_add_co_u32_e32 v6, vcc, 0x49240000, v6
	s_movk_i32 s0, 0x204
	s_nop 0
	v_addc_co_u32_e32 v7, vcc, 0, v7, vcc
	global_load_dword v10, v[6:7], off
	v_cmp_gt_i32_e32 vcc, s0, v4
	s_waitcnt lgkmcnt(0)
	s_barrier
	s_and_saveexec_b64 s[0:1], vcc
	s_cbranch_execz .LBB0_1217
	v_ashrrev_i32_e32 v5, 31, v4
	v_lshl_add_u64 v[6:7], v[4:5], 2, s[8:9]
	s_mov_b64 s[12:13], 0x300000
	v_add_u32_e32 v1, 0xfffffe00, v4
	v_lshl_add_u32 v11, v4, 2, s17
	v_lshl_add_u64 v[6:7], v[6:7], 0, s[12:13]
	s_mov_b64 s[12:13], 0
.LBB0_1216:
	global_load_dword v5, v[6:7], off
	v_add_u32_e32 v1, 0x200, v1
	s_mov_b64 s[22:23], 0x800
	v_cmp_lt_i32_e32 vcc, 3, v1
	v_lshl_add_u64 v[6:7], v[6:7], 0, s[22:23]
	s_or_b64 s[12:13], vcc, s[12:13]
	s_waitcnt vmcnt(0) lgkmcnt(0)
	v_mul_f32_e32 v5, 0x3fb8aa3b, v5
	ds_write_b32 v11, v5
	v_add_u32_e32 v11, 0x800, v11
	s_andn2_b64 exec, exec, s[12:13]
	s_cbranch_execnz .LBB0_1216
.LBB0_1217:
	s_or_b64 exec, exec, s[0:1]
	s_ashr_i32 s22, s21, 7
	s_sub_i32 s0, 0x1000, s20
	s_mul_i32 s18, s18, 0x948000
	s_add_u32 s12, s8, s18
	s_addc_u32 s13, s9, 0
	s_lshr_b32 s18, s0, 6
	s_add_u32 s0, s8, 0x9002f00
	s_addc_u32 s1, s9, 0
	v_ashrrev_i32_e32 v11, 4, v4
	s_add_u32 s12, s12, 0x2c040000
	v_add_u32_e32 v166, s19, v11
	v_mov_b64_e32 v[6:7], s[0:1]
	s_addc_u32 s13, s13, 0
	v_mad_i64_i32 v[12:13], s[20:21], v166, s24, v[6:7]
	v_lshlrev_b32_e32 v5, 4, v4
	v_ashrrev_i32_e32 v18, 3, v4
	v_mov_b64_e32 v[14:15], s[12:13]
	s_movk_i32 s20, 0x2100
	v_mad_i64_i32 v[16:17], s[12:13], v18, s20, v[14:15]
	v_and_b32_e32 v152, 0x70, v5
	v_mov_b32_e32 v153, v3
	v_lshl_add_u64 v[154:155], v[16:17], 0, v[152:153]
	v_add_u32_e32 v16, 0x200, v4
	v_ashrrev_i32_e32 v17, 4, v16
	v_and_b32_e32 v150, 0xf0, v5
	v_mov_b32_e32 v151, v3
	v_add_u32_e32 v167, s19, v17
	v_lshl_add_u64 v[12:13], v[12:13], 0, v[150:151]
	v_mad_i64_i32 v[4:5], s[12:13], v167, s24, v[6:7]
	global_load_dwordx4 v[132:135], v[154:155], off
	v_lshl_add_u64 v[4:5], v[4:5], 0, v[150:151]
	global_load_dwordx4 v[136:139], v[12:13], off
	global_load_dwordx4 v[140:143], v[4:5], off
	v_ashrrev_i32_e32 v12, 3, v16
	v_mad_i64_i32 v[4:5], s[12:13], v12, s20, v[14:15]
	v_lshl_add_u64 v[156:157], v[4:5], 0, v[152:153]
	v_lshlrev_b64 v[4:5], 9, v[2:3]
	v_lshl_add_u64 v[4:5], s[8:9], 0, v[4:5]
	s_mov_b32 s12, 0x41200000
	v_add_co_u32_e32 v6, vcc, s12, v4
	global_load_dwordx4 v[144:147], v[156:157], off
	s_nop 0
	v_addc_co_u32_e32 v7, vcc, 0, v5, vcc
	global_load_dwordx2 v[158:159], v[6:7], off
	s_movk_i32 s13, 0x88
	s_movk_i32 s12, 0x110
	v_mul_lo_u32 v171, v18, s13
	v_mul_lo_u32 v200, v12, s13
	s_waitcnt vmcnt(0)
	v_mul_f32_e32 v153, 0x3e0293ee, v10
	v_mul_lo_u32 v170, v11, s12
	v_add_u32_e32 v7, s72, v171
	v_mul_lo_u32 v199, v17, s12
	s_movk_i32 s12, 0x4400
	v_add_u32_e32 v10, s72, v200
	v_lshl_add_u64 v[160:161], s[0:1], 0, v[150:151]
	s_lshl_b32 s0, s22, 2
	s_lshl_b32 s1, s10, 2
	v_lshlrev_b32_e32 v1, 3, v9
	v_lshlrev_b32_e32 v149, 2, v9
	v_add3_u32 v6, s72, v170, v150
	v_add3_u32 v7, v7, v152, s12
	v_add3_u32 v9, s72, v199, v150
	v_add3_u32 v10, v10, v152, s12
	s_add_i32 s21, s17, s0
	s_add_i32 s22, s17, s1
	s_mov_b64 s[0:1], 0x41200008
	v_mov_b32_e32 v52, v3
	v_mov_b32_e32 v53, v3
	v_mul_u32_u24_e32 v168, 0x110, v8
	v_mul_u32_u24_e32 v169, 0x88, v8
	v_lshl_add_u64 v[162:163], v[4:5], 0, s[0:1]
	v_sub_u32_e32 v201, v8, v149
	v_mov_b32_e32 v54, v3
	v_mov_b32_e32 v55, v3
	v_mov_b32_e32 v56, v3
	v_mov_b32_e32 v57, v3
	v_mov_b32_e32 v58, v3
	v_mov_b32_e32 v59, v3
	v_mov_b32_e32 v60, v3
	v_mov_b32_e32 v61, v3
	v_mov_b32_e32 v62, v3
	v_mov_b32_e32 v63, v3
	v_mov_b32_e32 v64, v3
	v_mov_b32_e32 v65, v3
	v_mov_b32_e32 v66, v3
	v_mov_b32_e32 v67, v3
	v_mov_b64_e32 v[36:37], v[52:53]
	v_mov_b64_e32 v[20:21], v[52:53]
	s_mov_b32 s24, 0
	s_waitcnt lgkmcnt(0)
	ds_write_b128 v6, v[136:139]
	ds_write2_b64 v7, v[132:133], v[134:135] offset1:1
	ds_write_b128 v9, v[140:143]
	ds_write2_b64 v10, v[144:145], v[146:147] offset1:1
	v_mov_b64_e32 v[4:5], v[52:53]
	v_or_b32_e32 v172, 1, v149
	v_or_b32_e32 v173, 2, v149
	v_or_b32_e32 v174, 3, v149
	v_or_b32_e32 v175, 8, v149
	v_or_b32_e32 v176, 9, v149
	v_or_b32_e32 v177, 10, v149
	v_or_b32_e32 v178, 11, v149
	v_or_b32_e32 v179, 16, v149
	v_or_b32_e32 v180, 17, v149
	v_or_b32_e32 v181, 18, v149
	v_or_b32_e32 v194, 19, v149
	v_or_b32_e32 v195, 24, v149
	v_or_b32_e32 v196, 25, v149
	v_or_b32_e32 v197, 26, v149
	v_or_b32_e32 v198, 27, v149
	s_or_b32 s19, s15, 31
	s_add_i32 s20, s14, 0xf81
	v_mov_b32_e32 v202, 0xf149f2ca
	v_mov_b32_e32 v151, 0
	s_mov_b32 s28, 64
	v_mov_b64_e32 v[38:39], v[54:55]
	v_mov_b64_e32 v[40:41], v[56:57]
	v_mov_b64_e32 v[42:43], v[58:59]
	v_mov_b64_e32 v[44:45], v[60:61]
	v_mov_b64_e32 v[46:47], v[62:63]
	v_mov_b64_e32 v[48:49], v[64:65]
	v_mov_b64_e32 v[50:51], v[66:67]
	v_mov_b64_e32 v[22:23], v[54:55]
	v_mov_b64_e32 v[24:25], v[56:57]
	v_mov_b64_e32 v[26:27], v[58:59]
	v_mov_b64_e32 v[28:29], v[60:61]
	v_mov_b64_e32 v[30:31], v[62:63]
	v_mov_b64_e32 v[32:33], v[64:65]
	v_mov_b64_e32 v[34:35], v[66:67]
	v_mov_b64_e32 v[6:7], v[54:55]
	v_mov_b64_e32 v[8:9], v[56:57]
	v_mov_b64_e32 v[10:11], v[58:59]
	v_mov_b64_e32 v[12:13], v[60:61]
	v_mov_b64_e32 v[14:15], v[62:63]
	v_mov_b64_e32 v[16:17], v[64:65]
	v_mov_b64_e32 v[18:19], v[66:67]
	v_mov_b64_e32 v[164:165], v[158:159]
	s_waitcnt lgkmcnt(0)
	s_barrier
.LBB0_1218:
	s_add_i32 s23, s24, 1
	s_cmp_lt_u32 s23, s18
	s_cselect_b64 s[12:13], -1, 0
	s_cmp_ge_u32 s23, s18
	s_cbranch_scc1 .LBB0_1224
	s_mov_b64 s[40:41], s[28:29]
	v_add_u32_e32 v68, s40, v166
	s_movk_i32 s14, 0x7200
	v_mad_i64_i32 v[68:69], s[0:1], v68, s14, v[160:161]
	s_lshl_b64 s[0:1], s[28:29], 1
	s_nop 0
	v_lshl_add_u64 v[70:71], v[154:155], 0, s[0:1]
	s_waitcnt vmcnt(0)
	global_load_dwordx4 v[136:139], v[68:69], off
	global_load_dwordx4 v[132:135], v[70:71], off
	v_add_u32_e32 v68, s40, v167
	v_mad_i64_i32 v[68:69], s[14:15], v68, s14, v[160:161]
	v_lshl_add_u64 v[70:71], v[156:157], 0, s[0:1]
	global_load_dwordx4 v[140:143], v[68:69], off
	global_load_dwordx4 v[144:147], v[70:71], off
	global_load_dwordx2 v[164:165], v[162:163], off
	s_sub_i32 s0, s28, 64
	s_cmp_gt_u32 s0, s19
	s_cbranch_scc0 .LBB0_1225

.LBB0_1328:
	s_waitcnt lgkmcnt(0)
	s_barrier
	s_and_saveexec_b64 s[0:1], s[36:37]
	s_cbranch_execz .LBB0_1330
	v_mov_b64_e32 v[4:5], s[4:5]
	global_atomic_add v1, v[4:5], v228, off sc0
	v_mov_b32_e32 v2, s33
	s_waitcnt vmcnt(0) lgkmcnt(0)
	ds_write_b32 v2, v1

.LBB0_1332:
	v_ashrrev_i32_e32 v5, 31, v4
	v_lshlrev_b64 v[4:5], 12, v[4:5]
	v_cndmask_b32_e64 v2, 0, 1.0, s[0:1]
	v_lshl_add_u64 v[4:5], s[42:43], 0, v[4:5]
	v_lshl_add_u64 v[74:75], s[38:39], 1, v[4:5]
	s_waitcnt vmcnt(0) lgkmcnt(0)
	v_pk_mul_f32 v[4:5], v[2:3], v[16:17] op_sel_hi:[0,1]
	v_cvt_pk_bf16_f32 v8, v4, v5
	v_pk_mul_f32 v[4:5], v[2:3], v[14:15] op_sel_hi:[0,1]
	v_cvt_pk_bf16_f32 v9, v4, v5
	v_pk_mul_f32 v[4:5], v[2:3], v[12:13] op_sel_hi:[0,1]
	v_cvt_pk_bf16_f32 v10, v4, v5
	v_pk_mul_f32 v[4:5], v[2:3], v[6:7] op_sel_hi:[0,1]
	v_cvt_pk_bf16_f32 v11, v4, v5
	v_pk_mul_f32 v[4:5], v[2:3], v[24:25] op_sel_hi:[0,1]
	v_pk_mul_f32 v[6:7], v[2:3], v[22:23] op_sel_hi:[0,1]
	global_store_dwordx4 v[74:75], v[8:11], off
	v_cvt_pk_bf16_f32 v4, v4, v5
	v_cvt_pk_bf16_f32 v5, v6, v7
	v_pk_mul_f32 v[6:7], v[2:3], v[20:21] op_sel_hi:[0,1]
	v_pk_mul_f32 v[8:9], v[2:3], v[18:19] op_sel_hi:[0,1]
	v_cvt_pk_bf16_f32 v6, v6, v7
	v_cvt_pk_bf16_f32 v7, v8, v9
	global_store_dwordx4 v[74:75], v[4:7], off offset:16
	v_pk_mul_f32 v[8:9], v[2:3], v[26:27] op_sel_hi:[0,1]
	s_nop 0
	v_pk_mul_f32 v[4:5], v[2:3], v[32:33] op_sel_hi:[0,1]
	v_pk_mul_f32 v[6:7], v[2:3], v[30:31] op_sel_hi:[0,1]
	v_cvt_pk_bf16_f32 v4, v4, v5
	v_cvt_pk_bf16_f32 v5, v6, v7
	v_pk_mul_f32 v[6:7], v[2:3], v[28:29] op_sel_hi:[0,1]
	v_cvt_pk_bf16_f32 v6, v6, v7
	v_cvt_pk_bf16_f32 v7, v8, v9
	global_store_dwordx4 v[74:75], v[4:7], off offset:32
	v_pk_mul_f32 v[8:9], v[2:3], v[34:35] op_sel_hi:[0,1]
	s_nop 0
	v_pk_mul_f32 v[4:5], v[2:3], v[40:41] op_sel_hi:[0,1]
	v_pk_mul_f32 v[6:7], v[2:3], v[38:39] op_sel_hi:[0,1]
	v_cvt_pk_bf16_f32 v4, v4, v5
	v_cvt_pk_bf16_f32 v5, v6, v7
	v_pk_mul_f32 v[6:7], v[2:3], v[36:37] op_sel_hi:[0,1]
	v_cvt_pk_bf16_f32 v6, v6, v7
	v_cvt_pk_bf16_f32 v7, v8, v9
	global_store_dwordx4 v[74:75], v[4:7], off offset:48
	v_pk_mul_f32 v[8:9], v[2:3], v[42:43] op_sel_hi:[0,1]
	s_nop 0
	v_pk_mul_f32 v[4:5], v[2:3], v[48:49] op_sel_hi:[0,1]
	v_pk_mul_f32 v[6:7], v[2:3], v[46:47] op_sel_hi:[0,1]
	v_cvt_pk_bf16_f32 v4, v4, v5
	v_cvt_pk_bf16_f32 v5, v6, v7
	v_pk_mul_f32 v[6:7], v[2:3], v[44:45] op_sel_hi:[0,1]
	v_cvt_pk_bf16_f32 v6, v6, v7
	v_cvt_pk_bf16_f32 v7, v8, v9
	global_store_dwordx4 v[74:75], v[4:7], off offset:64
	v_pk_mul_f32 v[8:9], v[2:3], v[50:51] op_sel_hi:[0,1]
	s_nop 0
	v_pk_mul_f32 v[4:5], v[2:3], v[56:57] op_sel_hi:[0,1]
	v_pk_mul_f32 v[6:7], v[2:3], v[54:55] op_sel_hi:[0,1]
	v_cvt_pk_bf16_f32 v4, v4, v5
	v_cvt_pk_bf16_f32 v5, v6, v7
	v_pk_mul_f32 v[6:7], v[2:3], v[52:53] op_sel_hi:[0,1]
	v_cvt_pk_bf16_f32 v6, v6, v7
	v_cvt_pk_bf16_f32 v7, v8, v9
	global_store_dwordx4 v[74:75], v[4:7], off offset:80
	v_pk_mul_f32 v[8:9], v[2:3], v[58:59] op_sel_hi:[0,1]
	v_pk_mul_f32 v[52:53], v[2:3], v[66:67] op_sel_hi:[0,1]
	v_pk_mul_f32 v[4:5], v[2:3], v[64:65] op_sel_hi:[0,1]
	v_pk_mul_f32 v[6:7], v[2:3], v[62:63] op_sel_hi:[0,1]
	v_cvt_pk_bf16_f32 v4, v4, v5
	v_cvt_pk_bf16_f32 v5, v6, v7
	v_pk_mul_f32 v[6:7], v[2:3], v[60:61] op_sel_hi:[0,1]
	v_cvt_pk_bf16_f32 v6, v6, v7
	v_cvt_pk_bf16_f32 v7, v8, v9
	global_store_dwordx4 v[74:75], v[4:7], off offset:96
	s_nop 1
	v_pk_mul_f32 v[4:5], v[2:3], v[72:73] op_sel_hi:[0,1]
	v_pk_mul_f32 v[6:7], v[2:3], v[70:71] op_sel_hi:[0,1]
	v_cvt_pk_bf16_f32 v4, v4, v5
	v_cvt_pk_bf16_f32 v5, v6, v7
	v_pk_mul_f32 v[6:7], v[2:3], v[68:69] op_sel_hi:[0,1]
	v_cvt_pk_bf16_f32 v6, v6, v7
.LBB0_1333:
	v_cvt_pk_bf16_f32 v7, v52, v53
	global_store_dwordx4 v[74:75], v[4:7], off offset:112

.LBB0_1336:
	s_add_i32 s58, s53, s57
	s_cmp_ge_i32 s58, s45
	s_mov_b64 s[0:1], -1
	s_cbranch_scc1 .LBB0_1335
	s_cmpk_gt_i32 s58, 0x20ff
	s_cbranch_scc0 .LBB0_1373
	v_mov_b32_e32 v2, s46
	s_waitcnt lgkmcnt(0)
	ds_read2_b64 v[6:9], v2 offset1:1
	s_add_i32 s59, s58, 0xffffdf00
	s_cmpk_gt_u32 s59, 0xc7f
	s_waitcnt lgkmcnt(0)
	v_lshl_add_u64 v[10:11], v[6:7], 0, s[8:9]
	s_cbranch_scc0 .LBB0_1351
	s_cmpk_gt_u32 s59, 0x1c7f
	s_cbranch_scc0 .LBB0_1348
	v_mov_b32_e32 v2, s47
	ds_read2_b64 v[4:7], v2 offset1:1
	s_add_i32 s60, s54, 0xfff7c000
	v_lshl_add_u64 v[12:13], v[8:9], 0, s[14:15]
	s_cmpk_gt_u32 s59, 0x1caf
	v_cmp_eq_u64_e64 s[38:39], 0, v[8:9]
	s_cbranch_scc0 .LBB0_1344
	s_and_b32 s0, s55, 0x3c0
	s_and_b32 s1, s60, 0x3c0
	v_readlane_b32 s76, v253, 17
	s_waitcnt lgkmcnt(0)
	v_lshl_add_u64 v[6:7], v[6:7], 0, s[12:13]
	v_or_b32_e32 v76, s1, v1
	v_readlane_b32 s77, v253, 18
	s_lshl_b32 s76, s0, 12
	v_lshlrev_b32_e32 v2, 2, v76
	v_lshl_add_u64 v[6:7], v[6:7], 0, s[76:77]
	v_lshl_add_u64 v[58:59], v[6:7], 0, v[2:3]
	v_add_co_u32_e32 v8, vcc, 0x1000, v58
	s_movk_i32 s1, 0x2000
	s_nop 0
	v_addc_co_u32_e32 v9, vcc, 0, v59, vcc
	global_load_dword v6, v[58:59], off
	global_load_dword v7, v[8:9], off
	v_add_co_u32_e32 v8, vcc, s1, v58
	s_movk_i32 s1, 0x3000
	s_nop 0
	v_addc_co_u32_e32 v9, vcc, 0, v59, vcc
	v_add_co_u32_e32 v14, vcc, s1, v58
	s_movk_i32 s1, 0x4000
	s_nop 0
	v_addc_co_u32_e32 v15, vcc, 0, v59, vcc
	global_load_dword v8, v[8:9], off
	v_readlane_b32 s78, v253, 19
	global_load_dword v9, v[14:15], off
	v_add_co_u32_e32 v14, vcc, s1, v58
	s_movk_i32 s1, 0x6000
	s_nop 0
	v_addc_co_u32_e32 v15, vcc, 0, v59, vcc
	v_add_co_u32_e32 v16, vcc, s66, v58
	global_load_dword v14, v[14:15], off
	s_nop 0
	v_addc_co_u32_e32 v17, vcc, 0, v59, vcc
	global_load_dword v15, v[16:17], off
	v_add_co_u32_e32 v16, vcc, s1, v58
	s_movk_i32 s1, 0x7000
	s_nop 0
	v_addc_co_u32_e32 v17, vcc, 0, v59, vcc
	v_add_co_u32_e32 v18, vcc, s1, v58
	s_mov_b32 s1, 0x8000
	s_nop 0
	v_addc_co_u32_e32 v19, vcc, 0, v59, vcc
	global_load_dword v16, v[16:17], off
	v_readlane_b32 s79, v253, 20
	global_load_dword v17, v[18:19], off
	v_add_co_u32_e32 v18, vcc, s1, v58
	s_mov_b32 s1, 0x9000
	s_nop 0
	v_addc_co_u32_e32 v19, vcc, 0, v59, vcc
	v_add_co_u32_e32 v20, vcc, s1, v58
	s_mov_b32 s1, 0xa000
	s_nop 0
	v_addc_co_u32_e32 v21, vcc, 0, v59, vcc
	global_load_dword v18, v[18:19], off
	s_nop 0
	global_load_dword v19, v[20:21], off
	v_add_co_u32_e32 v20, vcc, s1, v58
	s_mov_b32 s1, 0xb000
	s_nop 0
	v_addc_co_u32_e32 v21, vcc, 0, v59, vcc
	v_add_co_u32_e32 v22, vcc, s1, v58
	s_mov_b32 s1, 0xc000
	s_nop 0
	v_addc_co_u32_e32 v23, vcc, 0, v59, vcc
	global_load_dword v20, v[20:21], off
	s_nop 0
	global_load_dword v21, v[22:23], off
	v_add_co_u32_e32 v22, vcc, s1, v58
	s_mov_b32 s1, 0xd000
	s_nop 0
	v_addc_co_u32_e32 v23, vcc, 0, v59, vcc
	v_add_co_u32_e32 v24, vcc, s1, v58
	s_mov_b32 s1, 0xe000
	s_nop 0
	v_addc_co_u32_e32 v25, vcc, 0, v59, vcc
	global_load_dword v22, v[22:23], off
	s_nop 0
	global_load_dword v23, v[24:25], off
	v_add_co_u32_e32 v24, vcc, s1, v58
	s_mov_b32 s1, 0xf000
	s_nop 0
	v_addc_co_u32_e32 v25, vcc, 0, v59, vcc
	v_add_co_u32_e32 v26, vcc, s1, v58
	s_mov_b32 s1, 0x10000
	s_nop 0
	v_addc_co_u32_e32 v27, vcc, 0, v59, vcc
	global_load_dword v24, v[24:25], off
	s_nop 0
	global_load_dword v25, v[26:27], off
	v_add_co_u32_e32 v26, vcc, s1, v58
	s_mov_b32 s1, 0x11000
	s_nop 0
	v_addc_co_u32_e32 v27, vcc, 0, v59, vcc
	v_add_co_u32_e32 v28, vcc, s1, v58
	s_mov_b32 s1, 0x12000
	s_nop 0
	v_addc_co_u32_e32 v29, vcc, 0, v59, vcc
	global_load_dword v26, v[26:27], off
	s_nop 0
	global_load_dword v27, v[28:29], off
	v_add_co_u32_e32 v28, vcc, s1, v58
	s_mov_b32 s1, 0x13000
	s_nop 0
	v_addc_co_u32_e32 v29, vcc, 0, v59, vcc
	v_add_co_u32_e32 v30, vcc, s1, v58
	s_mov_b32 s1, 0x14000
	s_nop 0
	v_addc_co_u32_e32 v31, vcc, 0, v59, vcc
	global_load_dword v28, v[28:29], off
	s_nop 0
	global_load_dword v29, v[30:31], off
	v_add_co_u32_e32 v30, vcc, s1, v58
	s_mov_b32 s1, 0x15000
	s_nop 0
	v_addc_co_u32_e32 v31, vcc, 0, v59, vcc
	v_add_co_u32_e32 v32, vcc, s1, v58
	s_mov_b32 s1, 0x16000
	s_nop 0
	v_addc_co_u32_e32 v33, vcc, 0, v59, vcc
	global_load_dword v30, v[30:31], off
	s_nop 0
	global_load_dword v31, v[32:33], off
	v_add_co_u32_e32 v32, vcc, s1, v58
	s_mov_b32 s1, 0x17000
	s_nop 0
	v_addc_co_u32_e32 v33, vcc, 0, v59, vcc
	v_add_co_u32_e32 v34, vcc, s1, v58
	s_mov_b32 s1, 0x18000
	s_nop 0
	v_addc_co_u32_e32 v35, vcc, 0, v59, vcc
	global_load_dword v32, v[32:33], off
	s_nop 0
	global_load_dword v33, v[34:35], off
	v_add_co_u32_e32 v34, vcc, s1, v58
	s_mov_b32 s1, 0x19000
	s_nop 0
	v_addc_co_u32_e32 v35, vcc, 0, v59, vcc
	v_add_co_u32_e32 v36, vcc, s1, v58
	s_mov_b32 s1, 0x1a000
	s_nop 0
	v_addc_co_u32_e32 v37, vcc, 0, v59, vcc
	global_load_dword v34, v[34:35], off
	s_nop 0
	global_load_dword v35, v[36:37], off
	v_add_co_u32_e32 v36, vcc, s1, v58
	s_mov_b32 s1, 0x1b000
	s_nop 0
	v_addc_co_u32_e32 v37, vcc, 0, v59, vcc
	v_add_co_u32_e32 v38, vcc, s1, v58
	s_mov_b32 s1, 0x1c000
	s_nop 0
	v_addc_co_u32_e32 v39, vcc, 0, v59, vcc
	global_load_dword v36, v[36:37], off
	s_nop 0
	global_load_dword v37, v[38:39], off
	v_add_co_u32_e32 v38, vcc, s1, v58
	s_mov_b32 s1, 0x1d000
	s_nop 0
	v_addc_co_u32_e32 v39, vcc, 0, v59, vcc
	v_add_co_u32_e32 v40, vcc, s1, v58
	s_mov_b32 s1, 0x1e000
	s_nop 0
	v_addc_co_u32_e32 v41, vcc, 0, v59, vcc
	global_load_dword v38, v[38:39], off
	s_nop 0
	global_load_dword v39, v[40:41], off
	v_add_co_u32_e32 v40, vcc, s1, v58
	s_mov_b32 s1, 0x1f000
	s_nop 0
	v_addc_co_u32_e32 v41, vcc, 0, v59, vcc
	v_add_co_u32_e32 v42, vcc, s1, v58
	s_mov_b32 s1, 0x20000
	s_nop 0
	v_addc_co_u32_e32 v43, vcc, 0, v59, vcc
	global_load_dword v40, v[40:41], off
	s_nop 0
	global_load_dword v41, v[42:43], off
	v_add_co_u32_e32 v42, vcc, s1, v58
	s_mov_b32 s1, 0x22000
	s_nop 0
	v_addc_co_u32_e32 v43, vcc, 0, v59, vcc
	v_add_co_u32_e32 v44, vcc, s65, v58
	global_load_dword v42, v[42:43], off
	s_nop 0
	v_addc_co_u32_e32 v45, vcc, 0, v59, vcc
	global_load_dword v43, v[44:45], off
	v_add_co_u32_e32 v44, vcc, s1, v58
	s_mov_b32 s1, 0x23000
	s_nop 0
	v_addc_co_u32_e32 v45, vcc, 0, v59, vcc
	v_add_co_u32_e32 v46, vcc, s1, v58
	s_mov_b32 s1, 0x24000
	s_nop 0
	v_addc_co_u32_e32 v47, vcc, 0, v59, vcc
	global_load_dword v44, v[44:45], off
	s_nop 0
	global_load_dword v45, v[46:47], off
	v_add_co_u32_e32 v46, vcc, s1, v58
	s_mov_b32 s1, 0x25000
	s_nop 0
	v_addc_co_u32_e32 v47, vcc, 0, v59, vcc
	v_add_co_u32_e32 v48, vcc, s1, v58
	s_mov_b32 s1, 0x26000
	s_nop 0
	v_addc_co_u32_e32 v49, vcc, 0, v59, vcc
	global_load_dword v46, v[46:47], off
	s_nop 0
	global_load_dword v47, v[48:49], off
	v_add_co_u32_e32 v48, vcc, s1, v58
	s_mov_b32 s1, 0x27000
	s_nop 0
	v_addc_co_u32_e32 v49, vcc, 0, v59, vcc
	v_add_co_u32_e32 v50, vcc, s1, v58
	s_mov_b32 s1, 0x28000
	s_nop 0
	v_addc_co_u32_e32 v51, vcc, 0, v59, vcc
	global_load_dword v48, v[48:49], off
	s_nop 0
	global_load_dword v49, v[50:51], off
	v_add_co_u32_e32 v50, vcc, s1, v58
	s_mov_b32 s1, 0x29000
	s_nop 0
	v_addc_co_u32_e32 v51, vcc, 0, v59, vcc
	v_add_co_u32_e32 v52, vcc, s1, v58
	s_mov_b32 s1, 0x2a000
	s_nop 0
	v_addc_co_u32_e32 v53, vcc, 0, v59, vcc
	global_load_dword v50, v[50:51], off
	s_nop 0
	global_load_dword v51, v[52:53], off
	v_add_co_u32_e32 v52, vcc, s1, v58
	s_mov_b32 s1, 0x2b000
	s_nop 0
	v_addc_co_u32_e32 v53, vcc, 0, v59, vcc
	v_add_co_u32_e32 v54, vcc, s1, v58
	s_mov_b32 s1, 0x2c000
	s_nop 0
	v_addc_co_u32_e32 v55, vcc, 0, v59, vcc
	global_load_dword v52, v[52:53], off
	s_nop 0
	global_load_dword v53, v[54:55], off
	v_add_co_u32_e32 v54, vcc, s1, v58
	s_mov_b32 s1, 0x2d000
	s_nop 0
	v_addc_co_u32_e32 v55, vcc, 0, v59, vcc
	v_add_co_u32_e32 v56, vcc, s1, v58
	s_mov_b32 s1, 0x2e000
	s_nop 0
	v_addc_co_u32_e32 v57, vcc, 0, v59, vcc
	global_load_dword v54, v[54:55], off
	s_nop 0
	global_load_dword v55, v[56:57], off
	v_add_co_u32_e32 v56, vcc, s1, v58
	s_mov_b32 s1, 0x2f000
	s_nop 0
	v_addc_co_u32_e32 v57, vcc, 0, v59, vcc
	v_add_co_u32_e32 v60, vcc, s1, v58
	global_load_dword v56, v[56:57], off
	s_nop 0
	v_addc_co_u32_e32 v61, vcc, 0, v59, vcc
	global_load_dword v57, v[60:61], off
	v_add_co_u32_e32 v60, vcc, s67, v58
	s_mov_b32 s1, 0x31000
	s_nop 0
	v_addc_co_u32_e32 v61, vcc, 0, v59, vcc
	v_add_co_u32_e32 v62, vcc, s1, v58
	s_mov_b32 s1, 0x32000
	s_nop 0
	v_addc_co_u32_e32 v63, vcc, 0, v59, vcc
	global_load_dword v60, v[60:61], off
	s_nop 0
	global_load_dword v61, v[62:63], off
	v_add_co_u32_e32 v62, vcc, s1, v58
	s_mov_b32 s1, 0x33000
	s_nop 0
	v_addc_co_u32_e32 v63, vcc, 0, v59, vcc
	v_add_co_u32_e32 v64, vcc, s1, v58
	s_mov_b32 s1, 0x34000
	s_nop 0
	v_addc_co_u32_e32 v65, vcc, 0, v59, vcc
	global_load_dword v62, v[62:63], off
	s_nop 0
	global_load_dword v63, v[64:65], off
	v_add_co_u32_e32 v64, vcc, s1, v58
	s_mov_b32 s1, 0x35000
	s_nop 0
	v_addc_co_u32_e32 v65, vcc, 0, v59, vcc
	v_add_co_u32_e32 v66, vcc, s1, v58
	s_mov_b32 s1, 0x36000
	s_nop 0
	v_addc_co_u32_e32 v67, vcc, 0, v59, vcc
	global_load_dword v64, v[64:65], off
	s_nop 0
	global_load_dword v65, v[66:67], off
	v_add_co_u32_e32 v66, vcc, s1, v58
	s_mov_b32 s1, 0x37000
	s_nop 0
	v_addc_co_u32_e32 v67, vcc, 0, v59, vcc
	v_add_co_u32_e32 v68, vcc, s1, v58
	s_mov_b32 s1, 0x38000
	s_nop 0
	v_addc_co_u32_e32 v69, vcc, 0, v59, vcc
	global_load_dword v66, v[66:67], off
	s_nop 0
	global_load_dword v67, v[68:69], off
	v_add_co_u32_e32 v68, vcc, s1, v58
	s_mov_b32 s1, 0x3a000
	s_nop 0
	v_addc_co_u32_e32 v69, vcc, 0, v59, vcc
	v_add_co_u32_e32 v70, vcc, s72, v58
	global_load_dword v68, v[68:69], off
	s_nop 0
	v_addc_co_u32_e32 v71, vcc, 0, v59, vcc
	global_load_dword v69, v[70:71], off
	v_add_co_u32_e32 v70, vcc, s1, v58
	s_mov_b32 s1, 0x3b000
	s_nop 0
	v_addc_co_u32_e32 v71, vcc, 0, v59, vcc
	v_add_co_u32_e32 v72, vcc, s1, v58
	s_mov_b32 s1, 0x3c000
	s_nop 0
	v_addc_co_u32_e32 v73, vcc, 0, v59, vcc
	global_load_dword v70, v[70:71], off
	s_nop 0
	global_load_dword v71, v[72:73], off
	v_add_co_u32_e32 v72, vcc, s1, v58
	s_mov_b32 s1, 0x3d000
	s_nop 0
	v_addc_co_u32_e32 v73, vcc, 0, v59, vcc
	v_add_co_u32_e32 v74, vcc, s1, v58
	s_mov_b32 s1, 0x3e000
	s_nop 0
	v_addc_co_u32_e32 v75, vcc, 0, v59, vcc
	global_load_dword v72, v[72:73], off
	s_nop 0
	global_load_dword v73, v[74:75], off
	v_add_co_u32_e32 v74, vcc, s1, v58
	s_mov_b32 s1, 0x3f000
	s_nop 0
	v_addc_co_u32_e32 v75, vcc, 0, v59, vcc
	v_add_co_u32_e32 v58, vcc, s1, v58
	global_load_dword v74, v[74:75], off
	s_nop 0
	v_addc_co_u32_e32 v59, vcc, 0, v59, vcc
	global_load_dword v75, v[58:59], off
	s_and_b64 vcc, exec, s[38:39]
	s_cbranch_vccnz .LBB0_1343
	s_lshl_b32 s76, s0, 2
	v_lshl_add_u64 v[58:59], v[12:13], 0, s[76:77]
	global_load_dwordx4 v[86:89], v[58:59], off
	global_load_dwordx4 v[90:93], v[58:59], off offset:16
	global_load_dwordx4 v[94:97], v[58:59], off offset:32
	global_load_dwordx4 v[98:101], v[58:59], off offset:48
	global_load_dwordx4 v[102:105], v[58:59], off offset:64
	global_load_dwordx4 v[106:109], v[58:59], off offset:80
	global_load_dwordx4 v[110:113], v[58:59], off offset:96
	global_load_dwordx4 v[114:117], v[58:59], off offset:112
	global_load_dwordx4 v[118:121], v[58:59], off offset:128
	global_load_dwordx4 v[122:125], v[58:59], off offset:144
	global_load_dwordx4 v[126:129], v[58:59], off offset:160
	global_load_dwordx4 v[130:133], v[58:59], off offset:176
	global_load_dwordx4 v[134:137], v[58:59], off offset:192
	global_load_dwordx4 v[138:141], v[58:59], off offset:208
	global_load_dwordx4 v[142:145], v[58:59], off offset:224
	global_load_dwordx4 v[78:81], v[58:59], off offset:240
	s_waitcnt vmcnt(0) lgkmcnt(0)
	v_pk_mul_f32 v[6:7], v[6:7], v[86:87]
	v_pk_mul_f32 v[8:9], v[8:9], v[88:89]
	v_pk_mul_f32 v[14:15], v[14:15], v[90:91]
	v_pk_mul_f32 v[16:17], v[16:17], v[92:93]
	v_pk_mul_f32 v[18:19], v[18:19], v[94:95]
	v_pk_mul_f32 v[20:21], v[20:21], v[96:97]
	v_pk_mul_f32 v[22:23], v[22:23], v[98:99]
	v_pk_mul_f32 v[24:25], v[24:25], v[100:101]
	v_pk_mul_f32 v[26:27], v[26:27], v[102:103]
	v_pk_mul_f32 v[28:29], v[28:29], v[104:105]
	v_pk_mul_f32 v[30:31], v[30:31], v[106:107]
	v_pk_mul_f32 v[32:33], v[32:33], v[108:109]
	v_pk_mul_f32 v[34:35], v[34:35], v[110:111]
	v_pk_mul_f32 v[36:37], v[36:37], v[112:113]
	v_pk_mul_f32 v[38:39], v[38:39], v[114:115]
	v_pk_mul_f32 v[40:41], v[40:41], v[116:117]
	v_pk_mul_f32 v[42:43], v[42:43], v[118:119]
	v_pk_mul_f32 v[44:45], v[44:45], v[120:121]
	v_pk_mul_f32 v[46:47], v[46:47], v[122:123]
	v_pk_mul_f32 v[48:49], v[48:49], v[124:125]
	v_pk_mul_f32 v[50:51], v[50:51], v[126:127]
	v_pk_mul_f32 v[52:53], v[52:53], v[128:129]
	v_pk_mul_f32 v[54:55], v[54:55], v[130:131]
	v_pk_mul_f32 v[56:57], v[56:57], v[132:133]
	v_pk_mul_f32 v[60:61], v[60:61], v[134:135]
	v_pk_mul_f32 v[62:63], v[62:63], v[136:137]
	v_pk_mul_f32 v[64:65], v[64:65], v[138:139]
	v_pk_mul_f32 v[66:67], v[66:67], v[140:141]
	v_pk_mul_f32 v[68:69], v[68:69], v[142:143]
	v_pk_mul_f32 v[70:71], v[70:71], v[144:145]
	v_pk_mul_f32 v[72:73], v[72:73], v[78:79]
	v_pk_mul_f32 v[74:75], v[74:75], v[80:81]
.LBB0_1343:
	v_mul_u32_u24_e32 v2, 0x300, v76
	v_lshl_add_u64 v[58:59], s[22:23], 0, v[2:3]
	s_lshl_b32 s76, s0, 1
	v_lshl_add_u64 v[58:59], v[58:59], 0, s[76:77]
	s_waitcnt vmcnt(0) lgkmcnt(0)
	v_cvt_pk_bf16_f32 v6, v6, v7
	v_cvt_pk_bf16_f32 v7, v8, v9
	v_cvt_pk_bf16_f32 v8, v14, v15
	v_cvt_pk_bf16_f32 v9, v16, v17
	global_store_dwordx4 v[58:59], v[6:9], off
	s_mov_b32 s1, s77
	v_writelane_b32 v253, s0, 17
	v_cvt_pk_bf16_f32 v6, v18, v19
	v_cvt_pk_bf16_f32 v7, v20, v21
	v_cvt_pk_bf16_f32 v8, v22, v23
	v_cvt_pk_bf16_f32 v9, v24, v25
	global_store_dwordx4 v[58:59], v[6:9], off offset:16
	v_writelane_b32 v253, s1, 18
	v_writelane_b32 v253, s2, 19
	v_cvt_pk_bf16_f32 v6, v26, v27
	v_cvt_pk_bf16_f32 v7, v28, v29
	v_cvt_pk_bf16_f32 v8, v30, v31
	v_cvt_pk_bf16_f32 v9, v32, v33
	global_store_dwordx4 v[58:59], v[6:9], off offset:32
	v_writelane_b32 v253, s3, 20
	s_mov_b64 s[0:1], 0
	v_cvt_pk_bf16_f32 v6, v34, v35
	v_cvt_pk_bf16_f32 v7, v36, v37
	v_cvt_pk_bf16_f32 v8, v38, v39
	v_cvt_pk_bf16_f32 v9, v40, v41
	global_store_dwordx4 v[58:59], v[6:9], off offset:48
	s_nop 1
	v_cvt_pk_bf16_f32 v6, v42, v43
	v_cvt_pk_bf16_f32 v7, v44, v45
	v_cvt_pk_bf16_f32 v8, v46, v47
	v_cvt_pk_bf16_f32 v9, v48, v49
	global_store_dwordx4 v[58:59], v[6:9], off offset:64
	s_nop 1
	v_cvt_pk_bf16_f32 v6, v50, v51
	v_cvt_pk_bf16_f32 v7, v52, v53
	v_cvt_pk_bf16_f32 v8, v54, v55
	v_cvt_pk_bf16_f32 v9, v56, v57
	global_store_dwordx4 v[58:59], v[6:9], off offset:80
	s_nop 1
	v_cvt_pk_bf16_f32 v6, v60, v61
	v_cvt_pk_bf16_f32 v7, v62, v63
	v_cvt_pk_bf16_f32 v8, v64, v65
	v_cvt_pk_bf16_f32 v9, v66, v67
	global_store_dwordx4 v[58:59], v[6:9], off offset:96
	s_nop 1
	v_cvt_pk_bf16_f32 v6, v68, v69
	v_cvt_pk_bf16_f32 v7, v70, v71
	v_cvt_pk_bf16_f32 v8, v72, v73
	v_cvt_pk_bf16_f32 v9, v74, v75
	global_store_dwordx4 v[58:59], v[6:9], off offset:112
.LBB0_1344:
	s_and_b64 vcc, exec, s[0:1]
	s_cbranch_vccz .LBB0_1385
	s_and_b32 s0, s56, 0x7c0
	s_xor_b32 s0, s0, 0x400
	s_and_b32 s1, s60, 0x1c0
	v_readlane_b32 s60, v253, 17
	s_waitcnt lgkmcnt(0)
	v_lshl_add_u64 v[4:5], v[4:5], 0, s[10:11]
	v_or_b32_e32 v72, s1, v1
	v_readlane_b32 s61, v253, 18
	s_lshl_b32 s60, s0, 11
	v_lshlrev_b32_e32 v2, 2, v72
	v_lshl_add_u64 v[4:5], v[4:5], 0, s[60:61]
	v_lshl_add_u64 v[64:65], v[4:5], 0, v[2:3]
	v_add_co_u32_e32 v8, vcc, 0x1000, v64
	s_movk_i32 s1, 0x2000
	s_nop 0
	v_addc_co_u32_e32 v9, vcc, 0, v65, vcc
	v_add_co_u32_e32 v14, vcc, s1, v64
	s_movk_i32 s1, 0x3000
	s_nop 0
	v_addc_co_u32_e32 v15, vcc, 0, v65, vcc
	v_add_co_u32_e32 v16, vcc, s1, v64
	s_movk_i32 s1, 0x4000
	s_nop 0
	v_addc_co_u32_e32 v17, vcc, 0, v65, vcc
	v_add_co_u32_e32 v18, vcc, s1, v64
	s_movk_i32 s1, 0x6000
	s_nop 0
	v_addc_co_u32_e32 v19, vcc, 0, v65, vcc
	v_add_co_u32_e32 v20, vcc, s66, v64
	global_load_dword v4, v[64:65], off
	global_load_dword v5, v[64:65], off offset:2048
	global_load_dword v6, v[8:9], off
	global_load_dword v7, v[8:9], off offset:2048
	s_nop 0
	global_load_dword v8, v[14:15], off
	global_load_dword v9, v[14:15], off offset:2048
	s_nop 0
	global_load_dword v14, v[16:17], off
	global_load_dword v15, v[16:17], off offset:2048
	v_addc_co_u32_e32 v21, vcc, 0, v65, vcc
	v_add_co_u32_e32 v22, vcc, s1, v64
	s_movk_i32 s1, 0x7000
	s_nop 0
	v_addc_co_u32_e32 v23, vcc, 0, v65, vcc
	v_add_co_u32_e32 v24, vcc, s1, v64
	s_mov_b32 s1, 0x8000
	s_nop 0
	v_addc_co_u32_e32 v25, vcc, 0, v65, vcc
	v_add_co_u32_e32 v26, vcc, s1, v64
	s_mov_b32 s1, 0x9000
	s_nop 0
	v_addc_co_u32_e32 v27, vcc, 0, v65, vcc
	v_add_co_u32_e32 v28, vcc, s1, v64
	s_mov_b32 s1, 0xa000
	s_nop 0
	v_addc_co_u32_e32 v29, vcc, 0, v65, vcc
	v_add_co_u32_e32 v30, vcc, s1, v64
	s_mov_b32 s1, 0xb000
	s_nop 0
	v_addc_co_u32_e32 v31, vcc, 0, v65, vcc
	v_add_co_u32_e32 v32, vcc, s1, v64
	s_mov_b32 s1, 0xc000
	s_nop 0
	v_addc_co_u32_e32 v33, vcc, 0, v65, vcc
	v_add_co_u32_e32 v34, vcc, s1, v64
	s_mov_b32 s1, 0xd000
	s_nop 0
	v_addc_co_u32_e32 v35, vcc, 0, v65, vcc
	v_add_co_u32_e32 v36, vcc, s1, v64
	s_mov_b32 s1, 0xe000
	s_nop 0
	v_addc_co_u32_e32 v37, vcc, 0, v65, vcc
	v_add_co_u32_e32 v38, vcc, s1, v64
	s_mov_b32 s1, 0xf000
	s_nop 0
	v_addc_co_u32_e32 v39, vcc, 0, v65, vcc
	v_add_co_u32_e32 v40, vcc, s1, v64
	s_mov_b32 s1, 0x10000
	s_nop 0
	v_addc_co_u32_e32 v41, vcc, 0, v65, vcc
	v_add_co_u32_e32 v42, vcc, s1, v64
	s_mov_b32 s1, 0x11000
	s_nop 0
	v_addc_co_u32_e32 v43, vcc, 0, v65, vcc
	v_add_co_u32_e32 v44, vcc, s1, v64
	s_mov_b32 s1, 0x12000
	s_nop 0
	v_addc_co_u32_e32 v45, vcc, 0, v65, vcc
	v_add_co_u32_e32 v46, vcc, s1, v64
	s_mov_b32 s1, 0x13000
	s_nop 0
	v_addc_co_u32_e32 v47, vcc, 0, v65, vcc
	v_add_co_u32_e32 v48, vcc, s1, v64
	s_mov_b32 s1, 0x14000
	s_nop 0
	v_addc_co_u32_e32 v49, vcc, 0, v65, vcc
	v_add_co_u32_e32 v50, vcc, s1, v64
	s_mov_b32 s1, 0x15000
	s_nop 0
	v_addc_co_u32_e32 v51, vcc, 0, v65, vcc
	v_add_co_u32_e32 v52, vcc, s1, v64
	s_mov_b32 s1, 0x16000
	s_nop 0
	v_addc_co_u32_e32 v53, vcc, 0, v65, vcc
	v_add_co_u32_e32 v54, vcc, s1, v64
	s_mov_b32 s1, 0x17000
	s_nop 0
	v_addc_co_u32_e32 v55, vcc, 0, v65, vcc
	v_add_co_u32_e32 v56, vcc, s1, v64
	s_mov_b32 s1, 0x18000
	s_nop 0
	v_addc_co_u32_e32 v57, vcc, 0, v65, vcc
	v_add_co_u32_e32 v58, vcc, s1, v64
	s_mov_b32 s1, 0x19000
	s_nop 0
	v_addc_co_u32_e32 v59, vcc, 0, v65, vcc
	v_add_co_u32_e32 v60, vcc, s1, v64
	s_mov_b32 s1, 0x1a000
	s_nop 0
	v_addc_co_u32_e32 v61, vcc, 0, v65, vcc
	v_add_co_u32_e32 v62, vcc, s1, v64
	s_mov_b32 s1, 0x1b000
	s_nop 0
	v_addc_co_u32_e32 v63, vcc, 0, v65, vcc
	v_add_co_u32_e32 v66, vcc, s1, v64
	s_mov_b32 s1, 0x1c000
	s_nop 0
	v_addc_co_u32_e32 v67, vcc, 0, v65, vcc
	global_load_dword v16, v[18:19], off
	global_load_dword v17, v[18:19], off offset:2048
	s_nop 0
	global_load_dword v18, v[20:21], off
	global_load_dword v19, v[20:21], off offset:2048
	s_nop 0
	global_load_dword v20, v[22:23], off
	global_load_dword v21, v[22:23], off offset:2048
	s_nop 0
	global_load_dword v22, v[24:25], off
	global_load_dword v23, v[24:25], off offset:2048
	s_nop 0
	global_load_dword v24, v[26:27], off
	global_load_dword v25, v[26:27], off offset:2048
	s_nop 0
	global_load_dword v26, v[28:29], off
	global_load_dword v27, v[28:29], off offset:2048
	s_nop 0
	global_load_dword v28, v[30:31], off
	global_load_dword v29, v[30:31], off offset:2048
	s_nop 0
	global_load_dword v30, v[32:33], off
	global_load_dword v31, v[32:33], off offset:2048
	s_nop 0
	global_load_dword v32, v[34:35], off
	global_load_dword v33, v[34:35], off offset:2048
	s_nop 0
	global_load_dword v34, v[36:37], off
	global_load_dword v35, v[36:37], off offset:2048
	s_nop 0
	global_load_dword v36, v[38:39], off
	global_load_dword v37, v[38:39], off offset:2048
	s_nop 0
	global_load_dword v38, v[40:41], off
	global_load_dword v39, v[40:41], off offset:2048
	s_nop 0
	global_load_dword v40, v[42:43], off
	global_load_dword v41, v[42:43], off offset:2048
	s_nop 0
	global_load_dword v42, v[44:45], off
	global_load_dword v43, v[44:45], off offset:2048
	s_nop 0
	global_load_dword v44, v[46:47], off
	global_load_dword v45, v[46:47], off offset:2048
	s_nop 0
	global_load_dword v46, v[48:49], off
	global_load_dword v47, v[48:49], off offset:2048
	s_nop 0
	global_load_dword v48, v[50:51], off
	global_load_dword v49, v[50:51], off offset:2048
	s_nop 0
	global_load_dword v50, v[52:53], off
	global_load_dword v51, v[52:53], off offset:2048
	s_nop 0
	global_load_dword v52, v[54:55], off
	global_load_dword v53, v[54:55], off offset:2048
	s_nop 0
	global_load_dword v54, v[56:57], off
	global_load_dword v55, v[56:57], off offset:2048
	s_nop 0
	global_load_dword v56, v[58:59], off
	global_load_dword v57, v[58:59], off offset:2048
	s_nop 0
	global_load_dword v58, v[60:61], off
	global_load_dword v59, v[60:61], off offset:2048
	s_nop 0
	global_load_dword v60, v[62:63], off
	global_load_dword v61, v[62:63], off offset:2048
	s_nop 0
	global_load_dword v62, v[66:67], off
	global_load_dword v63, v[66:67], off offset:2048
	v_add_co_u32_e32 v66, vcc, s1, v64
	s_mov_b32 s1, 0x1d000
	s_nop 0
	v_addc_co_u32_e32 v67, vcc, 0, v65, vcc
	v_add_co_u32_e32 v68, vcc, s1, v64
	s_mov_b32 s1, 0x1e000
	s_nop 0
	v_addc_co_u32_e32 v69, vcc, 0, v65, vcc
	v_add_co_u32_e32 v70, vcc, s1, v64
	s_mov_b32 s1, 0x1f000
	s_nop 0
	v_addc_co_u32_e32 v71, vcc, 0, v65, vcc
	v_add_co_u32_e32 v74, vcc, s1, v64
	v_readlane_b32 s62, v253, 19
	s_nop 0
	v_addc_co_u32_e32 v75, vcc, 0, v65, vcc
	global_load_dword v64, v[66:67], off
	global_load_dword v65, v[66:67], off offset:2048
	s_nop 0
	global_load_dword v66, v[68:69], off
	global_load_dword v67, v[68:69], off offset:2048
	s_nop 0
	global_load_dword v68, v[70:71], off
	global_load_dword v69, v[70:71], off offset:2048
	s_nop 0
	global_load_dword v70, v[74:75], off
	global_load_dword v71, v[74:75], off offset:2048
	s_and_b64 vcc, exec, s[38:39]
	v_readlane_b32 s63, v253, 20
	s_cbranch_vccnz .LBB0_1347
	s_lshl_b32 s60, s0, 2
	v_lshl_add_u64 v[12:13], v[12:13], 0, s[60:61]
	global_load_dwordx4 v[86:89], v[12:13], off
	global_load_dwordx4 v[90:93], v[12:13], off offset:16
	global_load_dwordx4 v[94:97], v[12:13], off offset:32
	global_load_dwordx4 v[98:101], v[12:13], off offset:48
	global_load_dwordx4 v[102:105], v[12:13], off offset:64
	global_load_dwordx4 v[106:109], v[12:13], off offset:80
	global_load_dwordx4 v[110:113], v[12:13], off offset:96
	global_load_dwordx4 v[114:117], v[12:13], off offset:112
	global_load_dwordx4 v[118:121], v[12:13], off offset:128
	global_load_dwordx4 v[122:125], v[12:13], off offset:144
	global_load_dwordx4 v[126:129], v[12:13], off offset:160
	global_load_dwordx4 v[130:133], v[12:13], off offset:176
	global_load_dwordx4 v[134:137], v[12:13], off offset:192
	global_load_dwordx4 v[138:141], v[12:13], off offset:208
	global_load_dwordx4 v[142:145], v[12:13], off offset:224
	global_load_dwordx4 v[74:77], v[12:13], off offset:240
	s_waitcnt vmcnt(0) lgkmcnt(0)
	v_pk_mul_f32 v[4:5], v[4:5], v[86:87]
	v_pk_mul_f32 v[6:7], v[6:7], v[88:89]
	v_pk_mul_f32 v[8:9], v[8:9], v[90:91]
	v_pk_mul_f32 v[14:15], v[14:15], v[92:93]
	v_pk_mul_f32 v[16:17], v[16:17], v[94:95]
	v_pk_mul_f32 v[18:19], v[18:19], v[96:97]
	v_pk_mul_f32 v[20:21], v[20:21], v[98:99]
	v_pk_mul_f32 v[22:23], v[22:23], v[100:101]
	v_pk_mul_f32 v[24:25], v[24:25], v[102:103]
	v_pk_mul_f32 v[26:27], v[26:27], v[104:105]
	v_pk_mul_f32 v[28:29], v[28:29], v[106:107]
	v_pk_mul_f32 v[30:31], v[30:31], v[108:109]
	v_pk_mul_f32 v[32:33], v[32:33], v[110:111]
	v_pk_mul_f32 v[34:35], v[34:35], v[112:113]
	v_pk_mul_f32 v[36:37], v[36:37], v[114:115]
	v_pk_mul_f32 v[38:39], v[38:39], v[116:117]
	v_pk_mul_f32 v[40:41], v[40:41], v[118:119]
	v_pk_mul_f32 v[42:43], v[42:43], v[120:121]
	v_pk_mul_f32 v[44:45], v[44:45], v[122:123]
	v_pk_mul_f32 v[46:47], v[46:47], v[124:125]
	v_pk_mul_f32 v[48:49], v[48:49], v[126:127]
	v_pk_mul_f32 v[50:51], v[50:51], v[128:129]
	v_pk_mul_f32 v[52:53], v[52:53], v[130:131]
	v_pk_mul_f32 v[54:55], v[54:55], v[132:133]
	v_pk_mul_f32 v[56:57], v[56:57], v[134:135]
	v_pk_mul_f32 v[58:59], v[58:59], v[136:137]
	v_pk_mul_f32 v[60:61], v[60:61], v[138:139]
	v_pk_mul_f32 v[62:63], v[62:63], v[140:141]
	v_pk_mul_f32 v[64:65], v[64:65], v[142:143]
	v_pk_mul_f32 v[66:67], v[66:67], v[144:145]
	v_pk_mul_f32 v[68:69], v[68:69], v[74:75]
	v_pk_mul_f32 v[70:71], v[70:71], v[76:77]
.LBB0_1347:
	v_mul_u32_u24_e32 v2, 0x300, v72
	v_lshl_add_u64 v[12:13], s[24:25], 0, v[2:3]
	s_lshl_b32 s60, s0, 1
	v_lshl_add_u64 v[12:13], v[12:13], 0, s[60:61]
	s_waitcnt vmcnt(0) lgkmcnt(0)
	v_cvt_pk_bf16_f32 v4, v4, v5
	v_cvt_pk_bf16_f32 v5, v6, v7
	v_cvt_pk_bf16_f32 v6, v8, v9
	v_cvt_pk_bf16_f32 v7, v14, v15
	global_store_dwordx4 v[12:13], v[4:7], off
	s_mov_b32 s1, s61
	v_writelane_b32 v253, s0, 17
	v_cvt_pk_bf16_f32 v4, v16, v17
	v_cvt_pk_bf16_f32 v5, v18, v19
	v_cvt_pk_bf16_f32 v6, v20, v21
	v_cvt_pk_bf16_f32 v7, v22, v23
	global_store_dwordx4 v[12:13], v[4:7], off offset:16
	v_writelane_b32 v253, s1, 18
	v_writelane_b32 v253, s2, 19
	v_cvt_pk_bf16_f32 v4, v24, v25
	v_cvt_pk_bf16_f32 v5, v26, v27
	v_cvt_pk_bf16_f32 v6, v28, v29
	v_cvt_pk_bf16_f32 v7, v30, v31
	global_store_dwordx4 v[12:13], v[4:7], off offset:32
	v_writelane_b32 v253, s3, 20
	s_mov_b64 s[0:1], 0
	v_cvt_pk_bf16_f32 v4, v32, v33
	v_cvt_pk_bf16_f32 v5, v34, v35
	v_cvt_pk_bf16_f32 v6, v36, v37
	v_cvt_pk_bf16_f32 v7, v38, v39
	global_store_dwordx4 v[12:13], v[4:7], off offset:48
	s_nop 1
	v_cvt_pk_bf16_f32 v4, v40, v41
	v_cvt_pk_bf16_f32 v5, v42, v43
	v_cvt_pk_bf16_f32 v6, v44, v45
	v_cvt_pk_bf16_f32 v7, v46, v47
	global_store_dwordx4 v[12:13], v[4:7], off offset:64
	s_nop 1
	v_cvt_pk_bf16_f32 v4, v48, v49
	v_cvt_pk_bf16_f32 v5, v50, v51
	v_cvt_pk_bf16_f32 v6, v52, v53
	v_cvt_pk_bf16_f32 v7, v54, v55
	global_store_dwordx4 v[12:13], v[4:7], off offset:80
	s_nop 1
	v_cvt_pk_bf16_f32 v4, v56, v57
	v_cvt_pk_bf16_f32 v5, v58, v59
	v_cvt_pk_bf16_f32 v6, v60, v61
	v_cvt_pk_bf16_f32 v7, v62, v63
	global_store_dwordx4 v[12:13], v[4:7], off offset:96
	s_nop 1
	v_cvt_pk_bf16_f32 v4, v64, v65
	v_cvt_pk_bf16_f32 v5, v66, v67
	v_cvt_pk_bf16_f32 v6, v68, v69
	v_cvt_pk_bf16_f32 v7, v70, v71
	global_store_dwordx4 v[12:13], v[4:7], off offset:112

.LBB0_1349:
	v_mov_b32_e32 v2, s48
	s_waitcnt lgkmcnt(0)
	ds_read_b64 v[4:5], v2
	s_add_i32 s38, s58, 0xffffd280
	s_lshl_b64 s[0:1], s[6:7], 2
	v_readlane_b32 s60, v253, 17
	v_readlane_b32 s61, v253, 18
	s_waitcnt lgkmcnt(0)
	v_lshl_add_u64 v[4:5], v[4:5], 0, s[0:1]
	s_lshr_b32 s0, s38, 1
	s_add_i32 s1, s54, 0xfff4a000
	s_and_b32 s60, s0, 0x7c0
	s_and_b32 s1, s1, 0x1fc0
	v_or_b32_e32 v8, s1, v1
	s_mul_i32 s38, s60, 0xe370
	s_mov_b32 s39, s61
	v_lshl_add_u64 v[6:7], v[10:11], 0, s[38:39]
	v_lshlrev_b32_e32 v2, 2, v8
	v_lshl_add_u64 v[6:7], v[6:7], 0, v[2:3]
	s_movk_i32 s1, 0x6000
	v_add_co_u32_e32 v12, vcc, s1, v6
	s_mov_b32 s1, 0x14000
	s_nop 0
	v_addc_co_u32_e32 v13, vcc, 0, v7, vcc
	global_load_dword v9, v[12:13], off offset:880
	v_add_co_u32_e32 v12, vcc, s1, v6
	s_mov_b32 s1, 0x22000
	s_nop 0
	v_addc_co_u32_e32 v13, vcc, 0, v7, vcc
	v_add_co_u32_e32 v14, vcc, s1, v6
	global_load_dword v12, v[12:13], off offset:1760
	s_nop 0
	v_addc_co_u32_e32 v15, vcc, 0, v7, vcc
	global_load_dword v13, v[14:15], off offset:2640
	v_add_co_u32_e32 v14, vcc, s67, v6
	s_mov_b32 s1, 0x3f000
	s_nop 0
	v_addc_co_u32_e32 v15, vcc, 0, v7, vcc
	v_add_co_u32_e32 v16, vcc, s1, v6
	s_mov_b32 s1, 0x4d000
	s_nop 0
	v_addc_co_u32_e32 v17, vcc, 0, v7, vcc
	global_load_dword v14, v[14:15], off offset:3520
	s_lshl_b32 s38, s60, 2
	global_load_dword v15, v[16:17], off offset:304
	v_add_co_u32_e32 v16, vcc, s1, v6
	s_mov_b32 s1, 0x5b000
	s_nop 0
	v_addc_co_u32_e32 v17, vcc, 0, v7, vcc
	v_add_co_u32_e32 v18, vcc, s1, v6
	s_mov_b32 s1, 0x69000
	s_nop 0
	v_addc_co_u32_e32 v19, vcc, 0, v7, vcc
	global_load_dword v16, v[16:17], off offset:1184
	s_or_b32 s0, s0, 63
	global_load_dword v17, v[18:19], off offset:2064
	v_add_co_u32_e32 v18, vcc, s1, v6
	s_mov_b32 s1, 0x77000
	s_nop 0
	v_addc_co_u32_e32 v19, vcc, 0, v7, vcc
	v_add_co_u32_e32 v20, vcc, s1, v6
	s_mov_b32 s1, 0x86000
	s_nop 0
	v_addc_co_u32_e32 v21, vcc, 0, v7, vcc
	global_load_dword v18, v[18:19], off offset:2944
	v_readlane_b32 s62, v253, 19
	global_load_dword v19, v[20:21], off offset:3824
	v_add_co_u32_e32 v20, vcc, s1, v6
	s_mov_b32 s1, 0x94000
	s_nop 0
	v_addc_co_u32_e32 v21, vcc, 0, v7, vcc
	v_add_co_u32_e32 v22, vcc, s1, v6
	s_mov_b32 s1, 0xa2000
	s_nop 0
	v_addc_co_u32_e32 v23, vcc, 0, v7, vcc
	global_load_dword v20, v[20:21], off offset:608
	v_readlane_b32 s63, v253, 20
	global_load_dword v21, v[22:23], off offset:1488
	v_add_co_u32_e32 v22, vcc, s1, v6
	s_mov_b32 s1, 0xb0000
	s_nop 0
	v_addc_co_u32_e32 v23, vcc, 0, v7, vcc
	v_add_co_u32_e32 v24, vcc, s1, v6
	s_mov_b32 s1, 0xbf000
	s_nop 0
	v_addc_co_u32_e32 v25, vcc, 0, v7, vcc
	global_load_dword v22, v[22:23], off offset:2368
	s_nop 0
	global_load_dword v23, v[24:25], off offset:3248
	v_add_co_u32_e32 v24, vcc, s1, v6
	s_mov_b32 s1, 0xcd000
	s_nop 0
	v_addc_co_u32_e32 v25, vcc, 0, v7, vcc
	v_add_co_u32_e32 v26, vcc, s1, v6
	s_mov_b32 s1, 0xdb000
	s_nop 0
	v_addc_co_u32_e32 v27, vcc, 0, v7, vcc
	global_load_dword v24, v[24:25], off offset:32
	s_nop 0
	global_load_dword v25, v[26:27], off offset:912
	v_add_co_u32_e32 v26, vcc, s1, v6
	s_mov_b32 s1, 0xe9000
	s_nop 0
	v_addc_co_u32_e32 v27, vcc, 0, v7, vcc
	v_add_co_u32_e32 v28, vcc, s1, v6
	s_mov_b32 s1, 0xf7000
	s_nop 0
	v_addc_co_u32_e32 v29, vcc, 0, v7, vcc
	global_load_dword v30, v[28:29], off offset:2672
	v_add_co_u32_e32 v28, vcc, s1, v6
	s_mov_b32 s1, 0x106000
	s_nop 0
	v_addc_co_u32_e32 v29, vcc, 0, v7, vcc
	global_load_dword v31, v[28:29], off offset:3552
	v_add_co_u32_e32 v28, vcc, s1, v6
	s_mov_b32 s1, 0x114000
	s_nop 0
	v_addc_co_u32_e32 v29, vcc, 0, v7, vcc
	global_load_dword v32, v[28:29], off offset:336
	v_add_co_u32_e32 v28, vcc, s1, v6
	s_mov_b32 s1, 0x122000
	s_nop 0
	v_addc_co_u32_e32 v29, vcc, 0, v7, vcc
	global_load_dword v33, v[28:29], off offset:1216
	v_add_co_u32_e32 v28, vcc, s1, v6
	s_mov_b32 s1, 0x130000
	s_nop 0
	v_addc_co_u32_e32 v29, vcc, 0, v7, vcc
	global_load_dword v38, v[28:29], off offset:2096
	v_add_co_u32_e32 v28, vcc, s1, v6
	s_mov_b32 s1, 0x13e000
	s_nop 0
	v_addc_co_u32_e32 v29, vcc, 0, v7, vcc
	global_load_dword v39, v[28:29], off offset:2976
	v_add_co_u32_e32 v28, vcc, s1, v6
	s_mov_b32 s1, 0x14d000
	s_nop 0
	v_addc_co_u32_e32 v29, vcc, 0, v7, vcc
	global_load_dword v40, v[28:29], off offset:3856
	v_add_co_u32_e32 v28, vcc, s1, v6
	s_mov_b32 s1, 0x15b000
	s_nop 0
	v_addc_co_u32_e32 v29, vcc, 0, v7, vcc
	global_load_dword v41, v[28:29], off offset:640
	v_add_co_u32_e32 v28, vcc, s1, v6
	s_mov_b32 s1, 0x169000
	s_nop 0
	v_addc_co_u32_e32 v29, vcc, 0, v7, vcc
	global_load_dword v42, v[28:29], off offset:1520
	v_add_co_u32_e32 v28, vcc, s1, v6
	s_mov_b32 s1, 0x177000
	s_nop 0
	v_addc_co_u32_e32 v29, vcc, 0, v7, vcc
	global_load_dword v43, v[28:29], off offset:2400
	v_add_co_u32_e32 v28, vcc, s1, v6
	s_mov_b32 s1, 0x186000
	s_nop 0
	v_addc_co_u32_e32 v29, vcc, 0, v7, vcc
	global_load_dword v44, v[28:29], off offset:3280
	v_add_co_u32_e32 v28, vcc, s1, v6
	s_mov_b32 s1, 0x194000
	s_nop 0
	v_addc_co_u32_e32 v29, vcc, 0, v7, vcc
	global_load_dword v26, v[26:27], off offset:1792
	s_nop 0
	global_load_dword v45, v[28:29], off offset:64
	v_add_co_u32_e32 v28, vcc, s1, v6
	s_mov_b32 s1, 0x1a2000
	s_nop 0
	v_addc_co_u32_e32 v29, vcc, 0, v7, vcc
	global_load_dword v50, v[28:29], off offset:944
	v_add_co_u32_e32 v28, vcc, s1, v6
	s_mov_b32 s1, 0x1b0000
	s_nop 0
	v_addc_co_u32_e32 v29, vcc, 0, v7, vcc
	global_load_dword v51, v[28:29], off offset:1824
	v_add_co_u32_e32 v28, vcc, s1, v6
	s_mov_b32 s1, 0x1be000
	s_nop 0
	v_addc_co_u32_e32 v29, vcc, 0, v7, vcc
	global_load_dword v52, v[28:29], off offset:2704
	v_add_co_u32_e32 v28, vcc, s1, v6
	s_mov_b32 s1, 0x1cd000
	s_nop 0
	v_addc_co_u32_e32 v29, vcc, 0, v7, vcc
	global_load_dword v53, v[28:29], off offset:3584
	v_add_co_u32_e32 v28, vcc, s1, v6
	s_mov_b32 s1, 0x1db000
	s_nop 0
	v_addc_co_u32_e32 v29, vcc, 0, v7, vcc
	global_load_dword v56, v[28:29], off offset:368
	v_add_co_u32_e32 v28, vcc, s1, v6
	s_mov_b32 s1, 0x1e9000
	s_nop 0
	v_addc_co_u32_e32 v29, vcc, 0, v7, vcc
	global_load_dword v57, v[28:29], off offset:1248
	v_add_co_u32_e32 v28, vcc, s1, v6
	s_mov_b32 s1, 0x1f7000
	s_nop 0
	v_addc_co_u32_e32 v29, vcc, 0, v7, vcc
	global_load_dword v59, v[28:29], off offset:2128
	v_add_co_u32_e32 v28, vcc, s1, v6
	s_mov_b32 s1, 0x205000
	s_nop 0
	v_addc_co_u32_e32 v29, vcc, 0, v7, vcc
	global_load_dword v60, v[28:29], off offset:3008
	v_add_co_u32_e32 v28, vcc, s1, v6
	s_mov_b32 s1, 0x214000
	s_nop 0
	v_addc_co_u32_e32 v29, vcc, 0, v7, vcc
	global_load_dword v69, v[28:29], off offset:3888
	v_add_co_u32_e32 v28, vcc, s1, v6
	s_mov_b32 s1, 0x222000
	s_nop 0
	v_addc_co_u32_e32 v29, vcc, 0, v7, vcc
	global_load_dword v71, v[28:29], off offset:672
	v_add_co_u32_e32 v28, vcc, s1, v6
	s_mov_b32 s1, 0x230000
	s_nop 0
	v_addc_co_u32_e32 v29, vcc, 0, v7, vcc
	global_load_dword v72, v[28:29], off offset:1552
	v_add_co_u32_e32 v28, vcc, s1, v6
	s_mov_b32 s1, 0x23e000
	s_nop 0
	v_addc_co_u32_e32 v29, vcc, 0, v7, vcc
	global_load_dword v73, v[28:29], off offset:2432
	v_add_co_u32_e32 v28, vcc, s1, v6
	s_mov_b32 s1, 0x24d000
	s_nop 0
	v_addc_co_u32_e32 v29, vcc, 0, v7, vcc
	global_load_dword v65, v[28:29], off offset:3312
	v_add_co_u32_e32 v28, vcc, s1, v6
	s_mov_b32 s1, 0x25b000
	s_nop 0
	v_addc_co_u32_e32 v29, vcc, 0, v7, vcc
	global_load_dword v66, v[28:29], off offset:96
	v_add_co_u32_e32 v28, vcc, s1, v6
	s_mov_b32 s1, 0x269000
	s_nop 0
	v_addc_co_u32_e32 v29, vcc, 0, v7, vcc
	global_load_dword v68, v[28:29], off offset:976
	v_add_co_u32_e32 v28, vcc, s1, v6
	s_mov_b32 s1, 0x277000
	s_nop 0
	v_addc_co_u32_e32 v29, vcc, 0, v7, vcc
	global_load_dword v70, v[28:29], off offset:1856
	v_add_co_u32_e32 v28, vcc, s1, v6
	s_mov_b32 s1, 0x285000
	s_nop 0
	v_addc_co_u32_e32 v29, vcc, 0, v7, vcc
	global_load_dword v62, v[28:29], off offset:2736
	v_add_co_u32_e32 v28, vcc, s1, v6
	s_mov_b32 s1, 0x294000
	s_nop 0
	v_addc_co_u32_e32 v29, vcc, 0, v7, vcc
	global_load_dword v63, v[28:29], off offset:3616
	v_add_co_u32_e32 v28, vcc, s1, v6
	s_mov_b32 s1, 0x2a2000
	s_nop 0
	v_addc_co_u32_e32 v29, vcc, 0, v7, vcc
	global_load_dword v64, v[28:29], off offset:400
	v_add_co_u32_e32 v28, vcc, s1, v6
	s_mov_b32 s1, 0x2b0000
	s_nop 0
	v_addc_co_u32_e32 v29, vcc, 0, v7, vcc
	global_load_dword v67, v[28:29], off offset:1280
	v_add_co_u32_e32 v28, vcc, s1, v6
	s_mov_b32 s1, 0x2be000
	s_nop 0
	v_addc_co_u32_e32 v29, vcc, 0, v7, vcc
	global_load_dword v54, v[28:29], off offset:2160
	v_add_co_u32_e32 v28, vcc, s1, v6
	s_mov_b32 s1, 0x2cc000
	s_nop 0
	v_addc_co_u32_e32 v29, vcc, 0, v7, vcc
	global_load_dword v55, v[28:29], off offset:3040
	v_add_co_u32_e32 v28, vcc, s1, v6
	s_mov_b32 s1, 0x2db000
	s_nop 0
	v_addc_co_u32_e32 v29, vcc, 0, v7, vcc
	global_load_dword v58, v[28:29], off offset:3920
	v_add_co_u32_e32 v28, vcc, s1, v6
	s_mov_b32 s1, 0x2e9000
	s_nop 0
	v_addc_co_u32_e32 v29, vcc, 0, v7, vcc
	global_load_dword v61, v[28:29], off offset:704
	v_add_co_u32_e32 v28, vcc, s1, v6
	s_mov_b32 s1, 0x2f7000
	s_nop 0
	v_addc_co_u32_e32 v29, vcc, 0, v7, vcc
	global_load_dword v46, v[28:29], off offset:1584
	v_add_co_u32_e32 v28, vcc, s1, v6
	s_mov_b32 s1, 0x305000
	s_nop 0
	v_addc_co_u32_e32 v29, vcc, 0, v7, vcc
	global_load_dword v47, v[28:29], off offset:2464
	v_add_co_u32_e32 v28, vcc, s1, v6
	s_mov_b32 s1, 0x314000
	s_nop 0
	v_addc_co_u32_e32 v29, vcc, 0, v7, vcc
	global_load_dword v48, v[28:29], off offset:3344
	v_add_co_u32_e32 v28, vcc, s1, v6
	s_mov_b32 s1, 0x322000
	s_nop 0
	v_addc_co_u32_e32 v29, vcc, 0, v7, vcc
	global_load_dword v49, v[28:29], off offset:128
	v_add_co_u32_e32 v28, vcc, s1, v6
	s_mov_b32 s1, 0x330000
	s_nop 0
	v_addc_co_u32_e32 v29, vcc, 0, v7, vcc
	global_load_dword v34, v[28:29], off offset:1008
	v_add_co_u32_e32 v28, vcc, s1, v6
	s_mov_b32 s1, 0x33e000
	s_nop 0
	v_addc_co_u32_e32 v29, vcc, 0, v7, vcc
	global_load_dword v35, v[28:29], off offset:1888
	v_add_co_u32_e32 v28, vcc, s1, v6
	s_mov_b32 s1, 0x34c000
	s_nop 0
	v_addc_co_u32_e32 v29, vcc, 0, v7, vcc
	global_load_dword v36, v[28:29], off offset:2768
	v_add_co_u32_e32 v28, vcc, s1, v6
	s_mov_b32 s1, 0x35b000
	s_nop 0
	v_addc_co_u32_e32 v29, vcc, 0, v7, vcc
	global_load_dword v37, v[28:29], off offset:3648
	v_add_co_u32_e32 v28, vcc, s1, v6
	s_mov_b32 s1, 0x369000
	s_nop 0
	v_addc_co_u32_e32 v29, vcc, 0, v7, vcc
	global_load_dword v27, v[28:29], off offset:432
	v_add_co_u32_e32 v28, vcc, s1, v6
	s_mov_b32 s1, 0x377000
	s_nop 0
	v_addc_co_u32_e32 v29, vcc, 0, v7, vcc
	v_add_co_u32_e32 v74, vcc, s1, v6
	s_mov_b32 s1, 0x385000
	s_nop 0
	v_addc_co_u32_e32 v75, vcc, 0, v7, vcc
	v_add_co_u32_e32 v6, vcc, s1, v6
	global_load_dword v28, v[28:29], off offset:1312
	s_nop 0
	v_addc_co_u32_e32 v7, vcc, 0, v7, vcc
	global_load_dword v2, v[6:7], off offset:3072
	v_lshl_add_u64 v[6:7], v[4:5], 0, s[38:39]
	global_load_dword v29, v[74:75], off offset:2192
	s_mov_b32 s1, s61
	global_load_dwordx4 v[74:77], v[6:7], off
	global_load_dwordx4 v[86:89], v[6:7], off offset:16
	global_load_dwordx4 v[90:93], v[6:7], off offset:32
	global_load_dwordx4 v[94:97], v[6:7], off offset:48
	global_load_dwordx4 v[98:101], v[6:7], off offset:64
	global_load_dwordx4 v[102:105], v[6:7], off offset:80
	global_load_dwordx4 v[106:109], v[6:7], off offset:96
	global_load_dwordx4 v[110:113], v[6:7], off offset:112
	global_load_dwordx4 v[114:117], v[6:7], off offset:128
	global_load_dwordx4 v[118:121], v[6:7], off offset:144
	global_load_dwordx4 v[122:125], v[6:7], off offset:160
	global_load_dwordx4 v[126:129], v[6:7], off offset:176
	global_load_dwordx4 v[130:133], v[6:7], off offset:192
	global_load_dwordx4 v[134:137], v[6:7], off offset:208
	global_load_dwordx4 v[138:141], v[6:7], off offset:224
	global_load_dwordx3 v[142:144], v[6:7], off offset:240
	s_lshl_b64 s[0:1], s[0:1], 2
	v_lshl_add_u64 v[4:5], v[4:5], 0, s[0:1]
	global_load_dword v4, v[4:5], off
	s_mov_b32 s1, s61
	v_writelane_b32 v253, s0, 17
	s_waitcnt vmcnt(0) lgkmcnt(0)
	v_mul_f32_e32 v74, 0x43000000, v74
	v_mul_f32_e32 v9, v9, v74
	v_mul_f32_e32 v74, 0x43000000, v75
	v_mul_f32_e32 v12, v12, v74
	v_mul_f32_e32 v74, 0x43000000, v76
	v_mul_f32_e32 v13, v13, v74
	v_mul_f32_e32 v74, 0x43000000, v77
	v_mul_f32_e32 v14, v14, v74
	v_writelane_b32 v253, s1, 18
	v_mul_f32_e32 v4, 0x43000000, v4
	v_writelane_b32 v253, s2, 19
	v_writelane_b32 v253, s3, 20
	s_mov_b32 s0, 0xc3e00000
	v_mul_f32_e32 v74, 0x43000000, v86
	v_mul_f32_e32 v15, v15, v74
	v_mul_f32_e32 v74, 0x43000000, v87
	v_mul_f32_e32 v16, v16, v74
	v_mul_f32_e32 v74, 0x43000000, v88
	v_mul_f32_e32 v17, v17, v74
	v_mul_f32_e32 v74, 0x43000000, v89
	v_mul_f32_e32 v18, v18, v74
	v_mul_f32_e32 v74, 0x43000000, v90
	v_mul_f32_e32 v19, v19, v74
	v_mul_f32_e32 v74, 0x43000000, v91
	v_mul_f32_e32 v20, v20, v74
	v_mul_f32_e32 v74, 0x43000000, v92
	v_mul_f32_e32 v21, v21, v74
	v_mul_f32_e32 v74, 0x43000000, v93
	v_mul_f32_e32 v22, v22, v74
	v_mul_f32_e32 v74, 0x43000000, v94
	v_mul_f32_e32 v23, v23, v74
	v_mul_f32_e32 v74, 0x43000000, v95
	v_mul_f32_e32 v24, v24, v74
	v_mul_f32_e32 v74, 0x43000000, v96
	v_mul_f32_e32 v25, v25, v74
	v_mul_f32_e32 v74, 0x43000000, v97
	v_mul_f32_e32 v26, v26, v74
	v_mul_f32_e32 v74, 0x43000000, v98
	v_mul_f32_e32 v30, v30, v74
	v_mul_f32_e32 v74, 0x43000000, v99
	v_mul_f32_e32 v31, v31, v74
	v_mul_f32_e32 v74, 0x43000000, v100
	v_mul_f32_e32 v32, v32, v74
	v_mul_f32_e32 v74, 0x43000000, v101
	v_mul_f32_e32 v33, v33, v74
	v_mul_f32_e32 v74, 0x43000000, v102
	v_mul_f32_e32 v38, v38, v74
	v_mul_f32_e32 v74, 0x43000000, v103
	v_mul_f32_e32 v39, v39, v74
	v_mul_f32_e32 v74, 0x43000000, v104
	v_mul_f32_e32 v40, v40, v74
	v_mul_f32_e32 v74, 0x43000000, v105
	v_mul_f32_e32 v41, v41, v74
	v_mul_f32_e32 v74, 0x43000000, v106
	v_mul_f32_e32 v42, v42, v74
	v_mul_f32_e32 v74, 0x43000000, v107
	v_mul_f32_e32 v43, v43, v74
	v_mul_f32_e32 v74, 0x43000000, v108
	v_mul_f32_e32 v44, v44, v74
	v_mul_f32_e32 v74, 0x43000000, v109
	v_mul_f32_e32 v45, v45, v74
	v_mul_f32_e32 v74, 0x43000000, v110
	v_mul_f32_e32 v50, v50, v74
	v_mul_f32_e32 v74, 0x43000000, v111
	v_mul_f32_e32 v51, v51, v74
	v_mul_f32_e32 v74, 0x43000000, v112
	v_mul_f32_e32 v52, v52, v74
	v_mul_f32_e32 v74, 0x43000000, v113
	v_mul_f32_e32 v53, v53, v74
	v_mul_f32_e32 v74, 0x43000000, v114
	v_mul_f32_e32 v56, v56, v74
	v_mul_f32_e32 v74, 0x43000000, v115
	v_mul_f32_e32 v57, v57, v74
	v_mul_f32_e32 v74, 0x43000000, v116
	v_mul_f32_e32 v59, v59, v74
	v_mul_f32_e32 v74, 0x43000000, v117
	v_mul_f32_e32 v60, v60, v74
	v_mul_f32_e32 v74, 0x43000000, v118
	v_mul_f32_e32 v69, v69, v74
	v_mul_f32_e32 v74, 0x43000000, v119
	v_mul_f32_e32 v71, v71, v74
	v_mul_f32_e32 v74, 0x43000000, v120
	v_mul_f32_e32 v72, v72, v74
	v_mul_f32_e32 v74, 0x43000000, v121
	v_mul_f32_e32 v73, v73, v74
	v_mul_f32_e32 v74, 0x43000000, v122
	v_mul_f32_e32 v65, v65, v74
	v_mul_f32_e32 v74, 0x43000000, v123
	v_mul_f32_e32 v66, v66, v74
	v_mul_f32_e32 v74, 0x43000000, v124
	v_mul_f32_e32 v68, v68, v74
	v_mul_f32_e32 v74, 0x43000000, v125
	v_mul_f32_e32 v70, v70, v74
	v_mul_f32_e32 v74, 0x43000000, v126
	v_mul_f32_e32 v62, v62, v74
	v_mul_f32_e32 v74, 0x43000000, v127
	v_mul_f32_e32 v63, v63, v74
	v_mul_f32_e32 v74, 0x43000000, v128
	v_mul_f32_e32 v64, v64, v74
	v_mul_f32_e32 v74, 0x43000000, v129
	v_mul_f32_e32 v67, v67, v74
	v_mul_f32_e32 v74, 0x43000000, v130
	v_mul_f32_e32 v54, v54, v74
	v_mul_f32_e32 v74, 0x43000000, v131
	v_mul_f32_e32 v55, v55, v74
	v_mul_f32_e32 v74, 0x43000000, v132
	v_mul_f32_e32 v58, v58, v74
	v_mul_f32_e32 v74, 0x43000000, v133
	v_mul_f32_e32 v61, v61, v74
	v_mul_f32_e32 v74, 0x43000000, v134
	v_mul_f32_e32 v46, v46, v74
	v_mul_f32_e32 v74, 0x43000000, v135
	v_mul_f32_e32 v47, v47, v74
	v_mul_f32_e32 v74, 0x43000000, v136
	v_mul_f32_e32 v48, v48, v74
	v_mul_f32_e32 v74, 0x43000000, v137
	v_mul_f32_e32 v49, v49, v74
	v_mul_f32_e32 v74, 0x43000000, v138
	v_mul_f32_e32 v34, v34, v74
	v_mul_f32_e32 v74, 0x43000000, v139
	v_mul_f32_e32 v35, v35, v74
	v_mul_f32_e32 v74, 0x43000000, v140
	v_mul_f32_e32 v36, v36, v74
	v_mul_f32_e32 v74, 0x43000000, v141
	v_mul_f32_e32 v37, v37, v74
	v_mov_b32_e32 v74, v142
	v_mov_b32_e32 v75, v143
	v_mov_b32_e32 v76, v144
	v_mul_f32_e32 v7, 0x43000000, v75
	v_mul_f32_e32 v7, v28, v7
	v_mul_f32_e32 v28, v2, v4
	v_lshlrev_b32_e32 v2, 11, v8
	v_lshl_add_u64 v[4:5], s[26:27], 0, v[2:3]
	v_med3_f32 v2, v9, s0, v240
	v_med3_f32 v8, v12, s0, v240
	v_mov_b32_e32 v12, v3
	v_cvt_pk_fp8_f32 v12, v2, v8
	v_med3_f32 v9, v13, s0, v240
	v_med3_f32 v13, v14, s0, v240
	v_med3_f32 v2, v15, s0, v240
	v_cvt_pk_fp8_f32 v12, v9, v13 op_sel:[0,0,1]
	v_med3_f32 v8, v16, s0, v240
	v_mov_b32_e32 v13, v3
	v_cvt_pk_fp8_f32 v13, v2, v8
	v_med3_f32 v9, v17, s0, v240
	v_med3_f32 v14, v18, s0, v240
	v_med3_f32 v2, v19, s0, v240
	v_cvt_pk_fp8_f32 v13, v9, v14 op_sel:[0,0,1]
	v_med3_f32 v8, v20, s0, v240
	v_mov_b32_e32 v14, v3
	v_cvt_pk_fp8_f32 v14, v2, v8
	v_med3_f32 v9, v21, s0, v240
	v_med3_f32 v15, v22, s0, v240
	v_med3_f32 v2, v23, s0, v240
	v_cvt_pk_fp8_f32 v14, v9, v15 op_sel:[0,0,1]
	v_med3_f32 v8, v24, s0, v240
	v_mov_b32_e32 v15, v3
	v_cvt_pk_fp8_f32 v15, v2, v8
	v_med3_f32 v9, v25, s0, v240
	v_med3_f32 v16, v26, s0, v240
	v_lshl_add_u64 v[4:5], v[4:5], 0, s[60:61]
	v_cvt_pk_fp8_f32 v15, v9, v16 op_sel:[0,0,1]
	v_med3_f32 v2, v30, s0, v240
	v_med3_f32 v8, v31, s0, v240
	v_med3_f32 v9, v32, s0, v240
	global_store_dwordx4 v[4:5], v[12:15], off
	v_med3_f32 v16, v53, s0, v240
	v_mul_f32_e32 v6, 0x43000000, v74
	v_mov_b32_e32 v12, v3
	v_cvt_pk_fp8_f32 v12, v2, v8
	v_med3_f32 v13, v33, s0, v240
	v_med3_f32 v2, v38, s0, v240
	v_med3_f32 v8, v39, s0, v240
	v_cvt_pk_fp8_f32 v12, v9, v13 op_sel:[0,0,1]
	v_mov_b32_e32 v13, v3
	v_cvt_pk_fp8_f32 v13, v2, v8
	v_med3_f32 v9, v40, s0, v240
	v_med3_f32 v14, v41, s0, v240
	v_med3_f32 v2, v42, s0, v240
	v_cvt_pk_fp8_f32 v13, v9, v14 op_sel:[0,0,1]
	v_med3_f32 v8, v43, s0, v240
	v_mov_b32_e32 v14, v3
	v_cvt_pk_fp8_f32 v14, v2, v8
	v_med3_f32 v9, v44, s0, v240
	v_med3_f32 v15, v45, s0, v240
	v_med3_f32 v2, v50, s0, v240
	v_cvt_pk_fp8_f32 v14, v9, v15 op_sel:[0,0,1]
	v_med3_f32 v8, v51, s0, v240
	v_mov_b32_e32 v15, v3
	v_cvt_pk_fp8_f32 v15, v2, v8
	v_med3_f32 v9, v52, s0, v240
	v_med3_f32 v2, v56, s0, v240
	v_med3_f32 v8, v57, s0, v240
	v_cvt_pk_fp8_f32 v15, v9, v16 op_sel:[0,0,1]
	v_med3_f32 v9, v59, s0, v240
	v_med3_f32 v16, v67, s0, v240
	v_mul_f32_e32 v6, v27, v6
	global_store_dwordx4 v[4:5], v[12:15], off offset:16
	v_mul_f32_e32 v27, 0x43000000, v76
	v_mul_f32_e32 v27, v29, v27
	v_mov_b32_e32 v12, v3
	v_cvt_pk_fp8_f32 v12, v2, v8
	v_med3_f32 v13, v60, s0, v240
	v_med3_f32 v2, v69, s0, v240
	v_med3_f32 v8, v71, s0, v240
	v_cvt_pk_fp8_f32 v12, v9, v13 op_sel:[0,0,1]
	v_mov_b32_e32 v13, v3
	v_cvt_pk_fp8_f32 v13, v2, v8
	v_med3_f32 v9, v72, s0, v240
	v_med3_f32 v14, v73, s0, v240
	v_med3_f32 v2, v65, s0, v240
	v_cvt_pk_fp8_f32 v13, v9, v14 op_sel:[0,0,1]
	v_med3_f32 v8, v66, s0, v240
	v_mov_b32_e32 v14, v3
	v_cvt_pk_fp8_f32 v14, v2, v8
	v_med3_f32 v9, v68, s0, v240
	v_med3_f32 v15, v70, s0, v240
	v_med3_f32 v2, v62, s0, v240
	v_cvt_pk_fp8_f32 v14, v9, v15 op_sel:[0,0,1]
	v_med3_f32 v8, v63, s0, v240
	v_mov_b32_e32 v15, v3
	v_cvt_pk_fp8_f32 v15, v2, v8
	v_med3_f32 v9, v64, s0, v240
	v_med3_f32 v2, v54, s0, v240
	v_med3_f32 v8, v55, s0, v240
	v_cvt_pk_fp8_f32 v15, v9, v16 op_sel:[0,0,1]
	v_med3_f32 v9, v58, s0, v240
	global_store_dwordx4 v[4:5], v[12:15], off offset:32
	s_nop 1
	v_mov_b32_e32 v12, v3
	v_cvt_pk_fp8_f32 v12, v2, v8
	v_med3_f32 v13, v61, s0, v240
	v_med3_f32 v2, v46, s0, v240
	v_med3_f32 v8, v47, s0, v240
	v_cvt_pk_fp8_f32 v12, v9, v13 op_sel:[0,0,1]
	v_mov_b32_e32 v13, v3
	v_cvt_pk_fp8_f32 v13, v2, v8
	v_med3_f32 v9, v48, s0, v240
	v_med3_f32 v14, v49, s0, v240
	v_med3_f32 v2, v34, s0, v240
	v_cvt_pk_fp8_f32 v13, v9, v14 op_sel:[0,0,1]
	v_med3_f32 v8, v35, s0, v240
	v_mov_b32_e32 v14, v3
	v_cvt_pk_fp8_f32 v14, v2, v8
	v_med3_f32 v9, v36, s0, v240
	v_med3_f32 v15, v37, s0, v240
	v_med3_f32 v2, v6, s0, v240
	v_cvt_pk_fp8_f32 v14, v9, v15 op_sel:[0,0,1]
	v_med3_f32 v6, v7, s0, v240
	v_mov_b32_e32 v15, v3
	v_cvt_pk_fp8_f32 v15, v2, v6
	v_med3_f32 v7, v27, s0, v240
	v_med3_f32 v8, v28, s0, v240
	v_cvt_pk_fp8_f32 v15, v7, v8 op_sel:[0,0,1]
	global_store_dwordx4 v[4:5], v[12:15], off offset:48

.LBB0_1369:
	s_lshl_b32 s38, s60, 6
	s_and_b32 s38, s38, 0xffc0
	v_readlane_b32 s76, v253, 17
	v_cmp_lt_i32_e64 s[0:1], -1, v2
	v_readlane_b32 s77, v253, 18
	s_mul_i32 s76, s38, 0xe370
	v_cndmask_b32_e64 v2, 0, v2, s[0:1]
	s_waitcnt lgkmcnt(0)
	v_lshl_add_u64 v[4:5], v[10:11], 0, s[76:77]
	v_lshl_add_u64 v[62:63], v[2:3], 2, v[4:5]
	v_add_co_u32_e32 v6, vcc, 0xe000, v62
	s_mov_b32 s39, 0x1c000
	s_nop 0
	v_addc_co_u32_e32 v7, vcc, 0, v63, vcc
	global_load_dword v4, v[62:63], off
	global_load_dword v5, v[6:7], off offset:880
	v_add_co_u32_e32 v6, vcc, s39, v62
	v_readlane_b32 s78, v253, 19
	s_nop 0
	v_addc_co_u32_e32 v7, vcc, 0, v63, vcc
	v_add_co_u32_e32 v8, vcc, 0x2a000, v62
	global_load_dword v6, v[6:7], off offset:1760
	s_nop 0
	v_addc_co_u32_e32 v9, vcc, 0, v63, vcc
	global_load_dword v7, v[8:9], off offset:2640
	v_add_co_u32_e32 v8, vcc, 0x38000, v62
	v_readlane_b32 s79, v253, 20
	s_nop 0
	v_addc_co_u32_e32 v9, vcc, 0, v63, vcc
	v_add_co_u32_e32 v10, vcc, 0x47000, v62
	global_load_dword v8, v[8:9], off offset:3520
	s_nop 0
	v_addc_co_u32_e32 v11, vcc, 0, v63, vcc
	global_load_dword v9, v[10:11], off offset:304
	v_add_co_u32_e32 v10, vcc, 0x55000, v62
	s_nop 1
	v_addc_co_u32_e32 v11, vcc, 0, v63, vcc
	v_add_co_u32_e32 v12, vcc, 0x63000, v62
	global_load_dword v10, v[10:11], off offset:1184
	s_nop 0
	v_addc_co_u32_e32 v13, vcc, 0, v63, vcc
	global_load_dword v11, v[12:13], off offset:2064
	v_add_co_u32_e32 v12, vcc, 0x71000, v62
	s_nop 1
	v_addc_co_u32_e32 v13, vcc, 0, v63, vcc
	v_add_co_u32_e32 v14, vcc, 0x7f000, v62
	global_load_dword v12, v[12:13], off offset:2944
	s_nop 0
	v_addc_co_u32_e32 v15, vcc, 0, v63, vcc
	global_load_dword v13, v[14:15], off offset:3824
	v_add_co_u32_e32 v14, vcc, 0x8e000, v62
	s_nop 1
	v_addc_co_u32_e32 v15, vcc, 0, v63, vcc
	v_add_co_u32_e32 v16, vcc, 0x9c000, v62
	global_load_dword v14, v[14:15], off offset:608
	s_nop 0
	v_addc_co_u32_e32 v17, vcc, 0, v63, vcc
	global_load_dword v15, v[16:17], off offset:1488
	v_add_co_u32_e32 v16, vcc, 0xaa000, v62
	s_nop 1
	v_addc_co_u32_e32 v17, vcc, 0, v63, vcc
	v_add_co_u32_e32 v18, vcc, 0xb8000, v62
	global_load_dword v16, v[16:17], off offset:2368
	s_nop 0
	v_addc_co_u32_e32 v19, vcc, 0, v63, vcc
	global_load_dword v17, v[18:19], off offset:3248
	v_add_co_u32_e32 v18, vcc, 0xc7000, v62
	s_nop 1
	v_addc_co_u32_e32 v19, vcc, 0, v63, vcc
	v_add_co_u32_e32 v20, vcc, 0xd5000, v62
	global_load_dword v18, v[18:19], off offset:32
	s_nop 0
	v_addc_co_u32_e32 v21, vcc, 0, v63, vcc
	global_load_dword v19, v[20:21], off offset:912
	v_add_co_u32_e32 v20, vcc, 0xe3000, v62
	s_nop 1
	v_addc_co_u32_e32 v21, vcc, 0, v63, vcc
	v_add_co_u32_e32 v22, vcc, 0xf1000, v62
	global_load_dword v20, v[20:21], off offset:1792
	s_nop 0
	v_addc_co_u32_e32 v23, vcc, 0, v63, vcc
	global_load_dword v21, v[22:23], off offset:2672
	v_add_co_u32_e32 v22, vcc, 0xff000, v62
	s_nop 1
	v_addc_co_u32_e32 v23, vcc, 0, v63, vcc
	v_add_co_u32_e32 v24, vcc, 0x10e000, v62
	global_load_dword v22, v[22:23], off offset:3552
	s_nop 0
	v_addc_co_u32_e32 v25, vcc, 0, v63, vcc
	global_load_dword v23, v[24:25], off offset:336
	v_add_co_u32_e32 v24, vcc, 0x11c000, v62
	s_nop 1
	v_addc_co_u32_e32 v25, vcc, 0, v63, vcc
	v_add_co_u32_e32 v26, vcc, 0x12a000, v62
	global_load_dword v24, v[24:25], off offset:1216
	s_nop 0
	v_addc_co_u32_e32 v27, vcc, 0, v63, vcc
	global_load_dword v25, v[26:27], off offset:2096
	v_add_co_u32_e32 v26, vcc, 0x138000, v62
	s_nop 1
	v_addc_co_u32_e32 v27, vcc, 0, v63, vcc
	v_add_co_u32_e32 v28, vcc, 0x146000, v62
	global_load_dword v26, v[26:27], off offset:2976
	s_nop 0
	v_addc_co_u32_e32 v29, vcc, 0, v63, vcc
	global_load_dword v27, v[28:29], off offset:3856
	v_add_co_u32_e32 v28, vcc, 0x155000, v62
	s_nop 1
	v_addc_co_u32_e32 v29, vcc, 0, v63, vcc
	v_add_co_u32_e32 v30, vcc, 0x163000, v62
	global_load_dword v28, v[28:29], off offset:640
	s_nop 0
	v_addc_co_u32_e32 v31, vcc, 0, v63, vcc
	global_load_dword v29, v[30:31], off offset:1520
	v_add_co_u32_e32 v30, vcc, 0x171000, v62
	s_nop 1
	v_addc_co_u32_e32 v31, vcc, 0, v63, vcc
	v_add_co_u32_e32 v32, vcc, 0x17f000, v62
	global_load_dword v30, v[30:31], off offset:2400
	s_nop 0
	v_addc_co_u32_e32 v33, vcc, 0, v63, vcc
	global_load_dword v31, v[32:33], off offset:3280
	v_add_co_u32_e32 v32, vcc, 0x18e000, v62
	s_nop 1
	v_addc_co_u32_e32 v33, vcc, 0, v63, vcc
	v_add_co_u32_e32 v34, vcc, 0x19c000, v62
	global_load_dword v32, v[32:33], off offset:64
	s_nop 0
	v_addc_co_u32_e32 v35, vcc, 0, v63, vcc
	global_load_dword v33, v[34:35], off offset:944
	v_add_co_u32_e32 v34, vcc, 0x1aa000, v62
	s_nop 1
	v_addc_co_u32_e32 v35, vcc, 0, v63, vcc
	v_add_co_u32_e32 v38, vcc, 0x1b8000, v62
	global_load_dword v34, v[34:35], off offset:1824
	s_nop 0
	v_addc_co_u32_e32 v39, vcc, 0, v63, vcc
	global_load_dword v35, v[38:39], off offset:2704
	v_add_co_u32_e32 v38, vcc, 0x1c6000, v62
	s_nop 1
	v_addc_co_u32_e32 v39, vcc, 0, v63, vcc
	v_add_co_u32_e32 v40, vcc, 0x1d5000, v62
	global_load_dword v38, v[38:39], off offset:3584
	s_nop 0
	v_addc_co_u32_e32 v41, vcc, 0, v63, vcc
	global_load_dword v39, v[40:41], off offset:368
	v_add_co_u32_e32 v40, vcc, 0x1e3000, v62
	s_nop 1
	v_addc_co_u32_e32 v41, vcc, 0, v63, vcc
	v_add_co_u32_e32 v42, vcc, 0x1f1000, v62
	global_load_dword v40, v[40:41], off offset:1248
	s_nop 0
	v_addc_co_u32_e32 v43, vcc, 0, v63, vcc
	global_load_dword v41, v[42:43], off offset:2128
	v_add_co_u32_e32 v42, vcc, 0x1ff000, v62
	s_nop 1
	v_addc_co_u32_e32 v43, vcc, 0, v63, vcc
	v_add_co_u32_e32 v44, vcc, 0x20d000, v62
	global_load_dword v42, v[42:43], off offset:3008
	s_nop 0
	v_addc_co_u32_e32 v45, vcc, 0, v63, vcc
	global_load_dword v43, v[44:45], off offset:3888
	v_add_co_u32_e32 v44, vcc, 0x21c000, v62
	s_nop 1
	v_addc_co_u32_e32 v45, vcc, 0, v63, vcc
	v_add_co_u32_e32 v46, vcc, 0x22a000, v62
	global_load_dword v44, v[44:45], off offset:672
	s_nop 0
	v_addc_co_u32_e32 v47, vcc, 0, v63, vcc
	global_load_dword v45, v[46:47], off offset:1552
	v_add_co_u32_e32 v46, vcc, 0x238000, v62
	s_nop 1
	v_addc_co_u32_e32 v47, vcc, 0, v63, vcc
	v_add_co_u32_e32 v48, vcc, 0x246000, v62
	global_load_dword v46, v[46:47], off offset:2432
	s_nop 0
	v_addc_co_u32_e32 v49, vcc, 0, v63, vcc
	global_load_dword v47, v[48:49], off offset:3312
	v_add_co_u32_e32 v48, vcc, 0x255000, v62
	s_nop 1
	v_addc_co_u32_e32 v49, vcc, 0, v63, vcc
	v_add_co_u32_e32 v50, vcc, 0x263000, v62
	global_load_dword v48, v[48:49], off offset:96
	s_nop 0
	v_addc_co_u32_e32 v51, vcc, 0, v63, vcc
	global_load_dword v49, v[50:51], off offset:976
	v_add_co_u32_e32 v50, vcc, 0x271000, v62
	s_nop 1
	v_addc_co_u32_e32 v51, vcc, 0, v63, vcc
	v_add_co_u32_e32 v52, vcc, 0x27f000, v62
	global_load_dword v50, v[50:51], off offset:1856
	s_nop 0
	v_addc_co_u32_e32 v53, vcc, 0, v63, vcc
	global_load_dword v51, v[52:53], off offset:2736
	v_add_co_u32_e32 v52, vcc, 0x28d000, v62
	s_nop 1
	v_addc_co_u32_e32 v53, vcc, 0, v63, vcc
	v_add_co_u32_e32 v54, vcc, 0x29c000, v62
	global_load_dword v52, v[52:53], off offset:3616
	s_nop 0
	v_addc_co_u32_e32 v55, vcc, 0, v63, vcc
	global_load_dword v53, v[54:55], off offset:400
	v_add_co_u32_e32 v54, vcc, 0x2aa000, v62
	s_nop 1
	v_addc_co_u32_e32 v55, vcc, 0, v63, vcc
	v_add_co_u32_e32 v56, vcc, 0x2b8000, v62
	global_load_dword v54, v[54:55], off offset:1280
	s_nop 0
	v_addc_co_u32_e32 v57, vcc, 0, v63, vcc
	global_load_dword v55, v[56:57], off offset:2160
	v_add_co_u32_e32 v56, vcc, 0x2c6000, v62
	s_nop 1
	v_addc_co_u32_e32 v57, vcc, 0, v63, vcc
	v_add_co_u32_e32 v58, vcc, 0x2d4000, v62
	global_load_dword v56, v[56:57], off offset:3040
	s_nop 0
	v_addc_co_u32_e32 v59, vcc, 0, v63, vcc
	global_load_dword v57, v[58:59], off offset:3920
	v_add_co_u32_e32 v58, vcc, 0x2e3000, v62
	s_nop 1
	v_addc_co_u32_e32 v59, vcc, 0, v63, vcc
	v_add_co_u32_e32 v60, vcc, 0x2f1000, v62
	global_load_dword v58, v[58:59], off offset:704
	s_nop 0
	v_addc_co_u32_e32 v61, vcc, 0, v63, vcc
	global_load_dword v59, v[60:61], off offset:1584
	v_add_co_u32_e32 v60, vcc, 0x2ff000, v62
	s_nop 1
	v_addc_co_u32_e32 v61, vcc, 0, v63, vcc
	v_add_co_u32_e32 v64, vcc, 0x30d000, v62
	global_load_dword v60, v[60:61], off offset:2464
	s_nop 0
	v_addc_co_u32_e32 v65, vcc, 0, v63, vcc
	global_load_dword v61, v[64:65], off offset:3344
	v_add_co_u32_e32 v64, vcc, 0x31c000, v62
	s_nop 1
	v_addc_co_u32_e32 v65, vcc, 0, v63, vcc
	v_add_co_u32_e32 v66, vcc, 0x32a000, v62
	global_load_dword v64, v[64:65], off offset:128
	s_nop 0
	v_addc_co_u32_e32 v67, vcc, 0, v63, vcc
	global_load_dword v65, v[66:67], off offset:1008
	v_add_co_u32_e32 v66, vcc, 0x338000, v62
	s_nop 1
	v_addc_co_u32_e32 v67, vcc, 0, v63, vcc
	v_add_co_u32_e32 v68, vcc, 0x346000, v62
	global_load_dword v66, v[66:67], off offset:1888
	s_nop 0
	v_addc_co_u32_e32 v69, vcc, 0, v63, vcc
	global_load_dword v67, v[68:69], off offset:2768
	v_add_co_u32_e32 v68, vcc, 0x354000, v62
	s_nop 1
	v_addc_co_u32_e32 v69, vcc, 0, v63, vcc
	v_add_co_u32_e32 v70, vcc, 0x363000, v62
	global_load_dword v68, v[68:69], off offset:3648
	s_nop 0
	v_addc_co_u32_e32 v71, vcc, 0, v63, vcc
	global_load_dword v69, v[70:71], off offset:432
	v_add_co_u32_e32 v70, vcc, 0x371000, v62
	s_nop 1
	v_addc_co_u32_e32 v71, vcc, 0, v63, vcc
	v_add_co_u32_e32 v62, vcc, 0x37f000, v62
	global_load_dword v70, v[70:71], off offset:1312
	s_nop 0
	v_addc_co_u32_e32 v63, vcc, 0, v63, vcc
	global_load_dword v71, v[62:63], off offset:2192
	v_cmp_eq_u64_e32 vcc, 0, v[36:37]
	s_cbranch_vccnz .LBB0_1371
	s_lshl_b64 s[60:61], s[6:7], 2
	v_lshl_add_u64 v[36:37], v[36:37], 0, s[60:61]
	s_lshl_b32 s76, s38, 2
	v_lshl_add_u64 v[36:37], v[36:37], 0, s[76:77]
	global_load_dwordx4 v[86:89], v[36:37], off
	global_load_dwordx4 v[90:93], v[36:37], off offset:16
	global_load_dwordx4 v[94:97], v[36:37], off offset:32
	global_load_dwordx4 v[98:101], v[36:37], off offset:48
	global_load_dwordx4 v[102:105], v[36:37], off offset:64
	global_load_dwordx4 v[106:109], v[36:37], off offset:80
	global_load_dwordx4 v[110:113], v[36:37], off offset:96
	global_load_dwordx4 v[114:117], v[36:37], off offset:112
	global_load_dwordx4 v[118:121], v[36:37], off offset:128
	global_load_dwordx4 v[122:125], v[36:37], off offset:144
	global_load_dwordx4 v[126:129], v[36:37], off offset:160
	global_load_dwordx4 v[130:133], v[36:37], off offset:176
	global_load_dwordx4 v[134:137], v[36:37], off offset:192
	global_load_dwordx4 v[138:141], v[36:37], off offset:208
	global_load_dwordx4 v[142:145], v[36:37], off offset:224
	global_load_dwordx4 v[74:77], v[36:37], off offset:240
	s_waitcnt vmcnt(0) lgkmcnt(0)
	v_pk_mul_f32 v[4:5], v[4:5], v[86:87]
	v_pk_mul_f32 v[6:7], v[6:7], v[88:89]
	v_pk_mul_f32 v[8:9], v[8:9], v[90:91]
	v_pk_mul_f32 v[10:11], v[10:11], v[92:93]
	v_pk_mul_f32 v[12:13], v[12:13], v[94:95]
	v_pk_mul_f32 v[14:15], v[14:15], v[96:97]
	v_pk_mul_f32 v[16:17], v[16:17], v[98:99]
	v_pk_mul_f32 v[18:19], v[18:19], v[100:101]
	v_pk_mul_f32 v[20:21], v[20:21], v[102:103]
	v_pk_mul_f32 v[22:23], v[22:23], v[104:105]
	v_pk_mul_f32 v[24:25], v[24:25], v[106:107]
	v_pk_mul_f32 v[26:27], v[26:27], v[108:109]
	v_pk_mul_f32 v[28:29], v[28:29], v[110:111]
	v_pk_mul_f32 v[30:31], v[30:31], v[112:113]
	v_pk_mul_f32 v[32:33], v[32:33], v[114:115]
	v_pk_mul_f32 v[34:35], v[34:35], v[116:117]
	v_pk_mul_f32 v[38:39], v[38:39], v[118:119]
	v_pk_mul_f32 v[40:41], v[40:41], v[120:121]
	v_pk_mul_f32 v[42:43], v[42:43], v[122:123]
	v_pk_mul_f32 v[44:45], v[44:45], v[124:125]
	v_pk_mul_f32 v[46:47], v[46:47], v[126:127]
	v_pk_mul_f32 v[48:49], v[48:49], v[128:129]
	v_pk_mul_f32 v[50:51], v[50:51], v[130:131]
	v_pk_mul_f32 v[52:53], v[52:53], v[132:133]
	v_pk_mul_f32 v[54:55], v[54:55], v[134:135]
	v_pk_mul_f32 v[56:57], v[56:57], v[136:137]
	v_pk_mul_f32 v[58:59], v[58:59], v[138:139]
	v_pk_mul_f32 v[60:61], v[60:61], v[140:141]
	v_pk_mul_f32 v[64:65], v[64:65], v[142:143]
	v_pk_mul_f32 v[66:67], v[66:67], v[144:145]
	v_pk_mul_f32 v[68:69], v[68:69], v[74:75]
	v_pk_mul_f32 v[70:71], v[70:71], v[76:77]
.LBB0_1371:
	v_cndmask_b32_e64 v36, 0, 1.0, s[0:1]
	v_lshlrev_b32_e32 v2, 12, v72
	s_waitcnt vmcnt(0) lgkmcnt(0)
	v_pk_mul_f32 v[4:5], v[36:37], v[4:5] op_sel_hi:[0,1]
	v_pk_mul_f32 v[6:7], v[36:37], v[6:7] op_sel_hi:[0,1]
	v_lshl_add_u64 v[62:63], s[28:29], 0, v[2:3]
	s_lshl_b32 s76, s38, 1
	v_cvt_pk_bf16_f32 v4, v4, v5
	v_cvt_pk_bf16_f32 v5, v6, v7
	v_pk_mul_f32 v[6:7], v[36:37], v[8:9] op_sel_hi:[0,1]
	v_pk_mul_f32 v[8:9], v[36:37], v[10:11] op_sel_hi:[0,1]
	v_lshl_add_u64 v[62:63], v[62:63], 0, s[76:77]
	v_cvt_pk_bf16_f32 v6, v6, v7
	v_cvt_pk_bf16_f32 v7, v8, v9
	global_store_dwordx4 v[62:63], v[4:7], off
	v_pk_mul_f32 v[8:9], v[36:37], v[18:19] op_sel_hi:[0,1]
	s_mov_b32 s1, s77
	v_pk_mul_f32 v[4:5], v[36:37], v[12:13] op_sel_hi:[0,1]
	v_pk_mul_f32 v[6:7], v[36:37], v[14:15] op_sel_hi:[0,1]
	v_cvt_pk_bf16_f32 v4, v4, v5
	v_cvt_pk_bf16_f32 v5, v6, v7
	v_pk_mul_f32 v[6:7], v[36:37], v[16:17] op_sel_hi:[0,1]
	v_cvt_pk_bf16_f32 v6, v6, v7
	v_cvt_pk_bf16_f32 v7, v8, v9
	global_store_dwordx4 v[62:63], v[4:7], off offset:16
	v_pk_mul_f32 v[8:9], v[36:37], v[26:27] op_sel_hi:[0,1]
	v_writelane_b32 v253, s0, 17
	v_pk_mul_f32 v[4:5], v[36:37], v[20:21] op_sel_hi:[0,1]
	v_pk_mul_f32 v[6:7], v[36:37], v[22:23] op_sel_hi:[0,1]
	v_cvt_pk_bf16_f32 v4, v4, v5
	v_cvt_pk_bf16_f32 v5, v6, v7
	v_pk_mul_f32 v[6:7], v[36:37], v[24:25] op_sel_hi:[0,1]
	v_cvt_pk_bf16_f32 v6, v6, v7
	v_cvt_pk_bf16_f32 v7, v8, v9
	global_store_dwordx4 v[62:63], v[4:7], off offset:32
	v_pk_mul_f32 v[8:9], v[36:37], v[34:35] op_sel_hi:[0,1]
	v_writelane_b32 v253, s1, 18
	v_pk_mul_f32 v[4:5], v[36:37], v[28:29] op_sel_hi:[0,1]
	v_pk_mul_f32 v[6:7], v[36:37], v[30:31] op_sel_hi:[0,1]
	v_cvt_pk_bf16_f32 v4, v4, v5
	v_cvt_pk_bf16_f32 v5, v6, v7
	v_pk_mul_f32 v[6:7], v[36:37], v[32:33] op_sel_hi:[0,1]
	v_cvt_pk_bf16_f32 v6, v6, v7
	v_cvt_pk_bf16_f32 v7, v8, v9
	global_store_dwordx4 v[62:63], v[4:7], off offset:48
	v_pk_mul_f32 v[8:9], v[36:37], v[44:45] op_sel_hi:[0,1]
	v_writelane_b32 v253, s2, 19
	v_pk_mul_f32 v[4:5], v[36:37], v[38:39] op_sel_hi:[0,1]
	v_pk_mul_f32 v[6:7], v[36:37], v[40:41] op_sel_hi:[0,1]
	v_cvt_pk_bf16_f32 v4, v4, v5
	v_cvt_pk_bf16_f32 v5, v6, v7
	v_pk_mul_f32 v[6:7], v[36:37], v[42:43] op_sel_hi:[0,1]
	v_cvt_pk_bf16_f32 v6, v6, v7
	v_cvt_pk_bf16_f32 v7, v8, v9
	global_store_dwordx4 v[62:63], v[4:7], off offset:64
	v_pk_mul_f32 v[8:9], v[36:37], v[52:53] op_sel_hi:[0,1]
	v_writelane_b32 v253, s3, 20
	v_pk_mul_f32 v[4:5], v[36:37], v[46:47] op_sel_hi:[0,1]
	v_pk_mul_f32 v[6:7], v[36:37], v[48:49] op_sel_hi:[0,1]
	v_cvt_pk_bf16_f32 v4, v4, v5
	v_cvt_pk_bf16_f32 v5, v6, v7
	v_pk_mul_f32 v[6:7], v[36:37], v[50:51] op_sel_hi:[0,1]
	v_cvt_pk_bf16_f32 v6, v6, v7
	v_cvt_pk_bf16_f32 v7, v8, v9
	global_store_dwordx4 v[62:63], v[4:7], off offset:80
	v_pk_mul_f32 v[8:9], v[36:37], v[60:61] op_sel_hi:[0,1]
	s_nop 0
	v_pk_mul_f32 v[4:5], v[36:37], v[54:55] op_sel_hi:[0,1]
	v_pk_mul_f32 v[6:7], v[36:37], v[56:57] op_sel_hi:[0,1]
	v_cvt_pk_bf16_f32 v4, v4, v5
	v_cvt_pk_bf16_f32 v5, v6, v7
	v_pk_mul_f32 v[6:7], v[36:37], v[58:59] op_sel_hi:[0,1]
	v_cvt_pk_bf16_f32 v6, v6, v7
	v_cvt_pk_bf16_f32 v7, v8, v9
	global_store_dwordx4 v[62:63], v[4:7], off offset:96
	v_pk_mul_f32 v[8:9], v[36:37], v[70:71] op_sel_hi:[0,1]
	s_nop 0
	v_pk_mul_f32 v[4:5], v[36:37], v[64:65] op_sel_hi:[0,1]
	v_pk_mul_f32 v[6:7], v[36:37], v[66:67] op_sel_hi:[0,1]
	v_cvt_pk_bf16_f32 v4, v4, v5
	v_cvt_pk_bf16_f32 v5, v6, v7
	v_pk_mul_f32 v[6:7], v[36:37], v[68:69] op_sel_hi:[0,1]
	v_cvt_pk_bf16_f32 v6, v6, v7
	v_cvt_pk_bf16_f32 v7, v8, v9
	global_store_dwordx4 v[62:63], v[4:7], off offset:112

.LBB0_1373:
	s_andn2_b64 vcc, exec, s[0:1]
	s_cbranch_vccnz .LBB0_1334
	v_mov_b32_e32 v2, s51
	ds_read_b64 v[10:11], v2
	s_cmpk_gt_i32 s58, 0xaff
	s_mov_b64 s[0:1], -1
	s_waitcnt lgkmcnt(0)
	v_lshl_add_u64 v[8:9], v[10:11], 0, s[20:21]
	s_cbranch_scc0 .LBB0_1382
	s_cmpk_gt_u32 s58, 0x15ff
	s_cbranch_scc0 .LBB0_1377
	v_mov_b32_e32 v2, s50
	ds_read_b64 v[4:5], v2
	s_and_b32 s0, s54, 0x7c0
	v_or_b32_e32 v6, s0, v1
	v_lshlrev_b32_e32 v2, 2, v6
	s_mov_b32 s0, 0x10000
	s_waitcnt lgkmcnt(0)
	v_lshl_add_u64 v[4:5], v[4:5], 0, s[18:19]
	v_lshl_add_u64 v[4:5], v[4:5], 0, s[30:31]
	v_lshl_add_u64 v[4:5], v[4:5], 0, v[2:3]
	v_add_co_u32_e32 v12, vcc, 0x2000, v4
	global_load_dword v7, v[4:5], off
	s_nop 0
	v_addc_co_u32_e32 v13, vcc, 0, v5, vcc
	v_add_co_u32_e32 v14, vcc, 0x4000, v4
	global_load_dword v12, v[12:13], off
	s_nop 0
	v_addc_co_u32_e32 v15, vcc, 0, v5, vcc
	global_load_dword v13, v[14:15], off
	v_add_co_u32_e32 v14, vcc, 0x6000, v4
	v_mul_u32_u24_e32 v2, 0x2c00, v6
	s_nop 0
	v_addc_co_u32_e32 v15, vcc, 0, v5, vcc
	v_add_co_u32_e32 v16, vcc, 0x8000, v4
	global_load_dword v14, v[14:15], off
	s_nop 0
	v_addc_co_u32_e32 v17, vcc, 0, v5, vcc
	global_load_dword v15, v[16:17], off
	v_add_co_u32_e32 v16, vcc, 0xa000, v4
	v_lshl_add_u64 v[74:75], s[34:35], 0, v[2:3]
	s_nop 0
	v_addc_co_u32_e32 v17, vcc, 0, v5, vcc
	v_add_co_u32_e32 v18, vcc, 0xc000, v4
	global_load_dword v16, v[16:17], off
	s_nop 0
	v_addc_co_u32_e32 v19, vcc, 0, v5, vcc
	global_load_dword v17, v[18:19], off
	v_add_co_u32_e32 v18, vcc, 0xe000, v4
	s_waitcnt vmcnt(0) lgkmcnt(0)
	v_cvt_pk_bf16_f32 v6, v15, v16
	v_addc_co_u32_e32 v19, vcc, 0, v5, vcc
	v_add_co_u32_e32 v20, vcc, s0, v4
	global_load_dword v18, v[18:19], off
	s_nop 0
	v_addc_co_u32_e32 v21, vcc, 0, v5, vcc
	global_load_dword v19, v[20:21], off
	v_add_co_u32_e32 v20, vcc, 0x12000, v4
	s_mov_b32 s0, 0x14000
	s_nop 0
	v_addc_co_u32_e32 v21, vcc, 0, v5, vcc
	v_add_co_u32_e32 v22, vcc, s0, v4
	global_load_dword v20, v[20:21], off
	s_nop 0
	v_addc_co_u32_e32 v23, vcc, 0, v5, vcc
	global_load_dword v21, v[22:23], off
	v_add_co_u32_e32 v22, vcc, 0x16000, v4
	s_mov_b32 s0, 0x18000
	s_nop 0
	v_addc_co_u32_e32 v23, vcc, 0, v5, vcc
	v_add_co_u32_e32 v24, vcc, s0, v4
	global_load_dword v22, v[22:23], off
	s_nop 0
	v_addc_co_u32_e32 v25, vcc, 0, v5, vcc
	global_load_dword v23, v[24:25], off
	v_add_co_u32_e32 v24, vcc, 0x1a000, v4
	s_mov_b32 s0, 0x1c000
	s_nop 0
	v_addc_co_u32_e32 v25, vcc, 0, v5, vcc
	v_add_co_u32_e32 v26, vcc, s0, v4
	global_load_dword v24, v[24:25], off
	s_nop 0
	v_addc_co_u32_e32 v27, vcc, 0, v5, vcc
	global_load_dword v25, v[26:27], off
	v_add_co_u32_e32 v26, vcc, 0x1e000, v4
	s_mov_b64 s[0:1], 0
	s_nop 0
	v_addc_co_u32_e32 v27, vcc, 0, v5, vcc
	v_add_co_u32_e32 v28, vcc, 0x20000, v4
	global_load_dword v27, v[26:27], off
	s_nop 0
	v_addc_co_u32_e32 v29, vcc, 0, v5, vcc
	global_load_dword v26, v[28:29], off
	v_add_co_u32_e32 v28, vcc, 0x22000, v4
	s_nop 1
	v_addc_co_u32_e32 v29, vcc, 0, v5, vcc
	v_add_co_u32_e32 v30, vcc, 0x24000, v4
	global_load_dword v28, v[28:29], off
	s_nop 0
	v_addc_co_u32_e32 v31, vcc, 0, v5, vcc
	global_load_dword v29, v[30:31], off
	v_add_co_u32_e32 v30, vcc, 0x26000, v4
	s_nop 1
	v_addc_co_u32_e32 v31, vcc, 0, v5, vcc
	v_add_co_u32_e32 v32, vcc, 0x28000, v4
	global_load_dword v30, v[30:31], off
	s_nop 0
	v_addc_co_u32_e32 v33, vcc, 0, v5, vcc
	global_load_dword v31, v[32:33], off
	v_add_co_u32_e32 v32, vcc, 0x2a000, v4
	s_nop 1
	v_addc_co_u32_e32 v33, vcc, 0, v5, vcc
	v_add_co_u32_e32 v34, vcc, 0x2c000, v4
	global_load_dword v32, v[32:33], off
	s_nop 0
	v_addc_co_u32_e32 v35, vcc, 0, v5, vcc
	global_load_dword v33, v[34:35], off
	v_add_co_u32_e32 v34, vcc, 0x2e000, v4
	s_nop 1
	v_addc_co_u32_e32 v35, vcc, 0, v5, vcc
	v_add_co_u32_e32 v36, vcc, s67, v4
	global_load_dword v35, v[34:35], off
	s_nop 0
	v_addc_co_u32_e32 v37, vcc, 0, v5, vcc
	global_load_dword v34, v[36:37], off
	v_add_co_u32_e32 v36, vcc, 0x32000, v4
	s_nop 1
	v_addc_co_u32_e32 v37, vcc, 0, v5, vcc
	v_add_co_u32_e32 v38, vcc, 0x34000, v4
	global_load_dword v36, v[36:37], off
	s_nop 0
	v_addc_co_u32_e32 v39, vcc, 0, v5, vcc
	global_load_dword v37, v[38:39], off
	v_add_co_u32_e32 v38, vcc, 0x36000, v4
	s_nop 1
	v_addc_co_u32_e32 v39, vcc, 0, v5, vcc
	global_load_dword v40, v[38:39], off
	v_add_co_u32_e32 v38, vcc, 0x38000, v4
	s_nop 1
	v_addc_co_u32_e32 v39, vcc, 0, v5, vcc
	global_load_dword v41, v[38:39], off
	v_add_co_u32_e32 v38, vcc, 0x3a000, v4
	s_nop 1
	v_addc_co_u32_e32 v39, vcc, 0, v5, vcc
	global_load_dword v42, v[38:39], off
	v_add_co_u32_e32 v38, vcc, 0x3c000, v4
	s_nop 1
	v_addc_co_u32_e32 v39, vcc, 0, v5, vcc
	global_load_dword v43, v[38:39], off
	v_add_co_u32_e32 v38, vcc, 0x3e000, v4
	s_nop 1
	v_addc_co_u32_e32 v39, vcc, 0, v5, vcc
	global_load_dword v44, v[38:39], off
	v_add_co_u32_e32 v38, vcc, 0x40000, v4
	s_nop 1
	v_addc_co_u32_e32 v39, vcc, 0, v5, vcc
	global_load_dword v45, v[38:39], off
	v_add_co_u32_e32 v38, vcc, 0x42000, v4
	s_nop 1
	v_addc_co_u32_e32 v39, vcc, 0, v5, vcc
	global_load_dword v46, v[38:39], off
	v_add_co_u32_e32 v38, vcc, 0x44000, v4
	s_nop 1
	v_addc_co_u32_e32 v39, vcc, 0, v5, vcc
	global_load_dword v47, v[38:39], off
	v_add_co_u32_e32 v38, vcc, 0x46000, v4
	s_nop 1
	v_addc_co_u32_e32 v39, vcc, 0, v5, vcc
	global_load_dword v48, v[38:39], off
	v_add_co_u32_e32 v38, vcc, 0x48000, v4
	s_nop 1
	v_addc_co_u32_e32 v39, vcc, 0, v5, vcc
	global_load_dword v49, v[38:39], off
	v_add_co_u32_e32 v38, vcc, 0x4a000, v4
	s_nop 1
	v_addc_co_u32_e32 v39, vcc, 0, v5, vcc
	global_load_dword v50, v[38:39], off
	v_add_co_u32_e32 v38, vcc, 0x4c000, v4
	s_nop 1
	v_addc_co_u32_e32 v39, vcc, 0, v5, vcc
	global_load_dword v51, v[38:39], off
	v_add_co_u32_e32 v38, vcc, 0x4e000, v4
	s_nop 1
	v_addc_co_u32_e32 v39, vcc, 0, v5, vcc
	global_load_dword v54, v[38:39], off
	v_add_co_u32_e32 v38, vcc, 0x50000, v4
	s_nop 1
	v_addc_co_u32_e32 v39, vcc, 0, v5, vcc
	global_load_dword v55, v[38:39], off
	v_add_co_u32_e32 v38, vcc, 0x52000, v4
	s_nop 1
	v_addc_co_u32_e32 v39, vcc, 0, v5, vcc
	global_load_dword v56, v[38:39], off
	v_add_co_u32_e32 v38, vcc, 0x54000, v4
	s_nop 1
	v_addc_co_u32_e32 v39, vcc, 0, v5, vcc
	global_load_dword v57, v[38:39], off
	v_add_co_u32_e32 v38, vcc, 0x56000, v4
	s_nop 1
	v_addc_co_u32_e32 v39, vcc, 0, v5, vcc
	global_load_dword v58, v[38:39], off
	v_add_co_u32_e32 v38, vcc, 0x58000, v4
	s_nop 1
	v_addc_co_u32_e32 v39, vcc, 0, v5, vcc
	global_load_dword v59, v[38:39], off
	v_add_co_u32_e32 v38, vcc, 0x5a000, v4
	s_nop 1
	v_addc_co_u32_e32 v39, vcc, 0, v5, vcc
	global_load_dword v60, v[38:39], off
	v_add_co_u32_e32 v38, vcc, 0x5c000, v4
	s_nop 1
	v_addc_co_u32_e32 v39, vcc, 0, v5, vcc
	global_load_dword v61, v[38:39], off
	v_add_co_u32_e32 v38, vcc, 0x5e000, v4
	s_nop 1
	v_addc_co_u32_e32 v39, vcc, 0, v5, vcc
	global_load_dword v62, v[38:39], off
	v_add_co_u32_e32 v38, vcc, 0x60000, v4
	s_nop 1
	v_addc_co_u32_e32 v39, vcc, 0, v5, vcc
	global_load_dword v63, v[38:39], off
	v_add_co_u32_e32 v38, vcc, 0x62000, v4
	s_nop 1
	v_addc_co_u32_e32 v39, vcc, 0, v5, vcc
	global_load_dword v64, v[38:39], off
	v_add_co_u32_e32 v38, vcc, 0x64000, v4
	s_nop 1
	v_addc_co_u32_e32 v39, vcc, 0, v5, vcc
	global_load_dword v65, v[38:39], off
	v_add_co_u32_e32 v38, vcc, 0x66000, v4
	s_nop 1
	v_addc_co_u32_e32 v39, vcc, 0, v5, vcc
	global_load_dword v66, v[38:39], off
	v_add_co_u32_e32 v38, vcc, 0x68000, v4
	s_nop 1
	v_addc_co_u32_e32 v39, vcc, 0, v5, vcc
	global_load_dword v67, v[38:39], off
	v_add_co_u32_e32 v38, vcc, 0x6a000, v4
	s_nop 1
	v_addc_co_u32_e32 v39, vcc, 0, v5, vcc
	global_load_dword v68, v[38:39], off
	v_add_co_u32_e32 v38, vcc, 0x6c000, v4
	s_nop 1
	v_addc_co_u32_e32 v39, vcc, 0, v5, vcc
	global_load_dword v69, v[38:39], off
	v_add_co_u32_e32 v38, vcc, 0x6e000, v4
	s_nop 1
	v_addc_co_u32_e32 v39, vcc, 0, v5, vcc
	global_load_dword v70, v[38:39], off
	v_add_co_u32_e32 v38, vcc, 0x70000, v4
	s_nop 1
	v_addc_co_u32_e32 v39, vcc, 0, v5, vcc
	global_load_dword v71, v[38:39], off
	v_add_co_u32_e32 v38, vcc, 0x72000, v4
	s_nop 1
	v_addc_co_u32_e32 v39, vcc, 0, v5, vcc
	global_load_dword v72, v[38:39], off
	v_add_co_u32_e32 v38, vcc, 0x74000, v4
	s_nop 1
	v_addc_co_u32_e32 v39, vcc, 0, v5, vcc
	global_load_dword v73, v[38:39], off
	v_add_co_u32_e32 v38, vcc, 0x76000, v4
	s_nop 1
	v_addc_co_u32_e32 v39, vcc, 0, v5, vcc
	global_load_dword v76, v[38:39], off
	v_add_co_u32_e32 v38, vcc, 0x78000, v4
	s_nop 1
	v_addc_co_u32_e32 v39, vcc, 0, v5, vcc
	global_load_dword v77, v[38:39], off
	v_add_co_u32_e32 v38, vcc, 0x7a000, v4
	s_nop 1
	v_addc_co_u32_e32 v39, vcc, 0, v5, vcc
	global_load_dword v78, v[38:39], off
	v_add_co_u32_e32 v38, vcc, 0x7c000, v4
	s_nop 1
	v_addc_co_u32_e32 v39, vcc, 0, v5, vcc
	v_add_co_u32_e32 v4, vcc, 0x7e000, v4
	global_load_dword v52, v[38:39], off
	s_nop 0
	v_addc_co_u32_e32 v5, vcc, 0, v5, vcc
	global_load_dword v53, v[4:5], off
	v_cvt_pk_bf16_f32 v4, v7, v12
	v_cvt_pk_bf16_f32 v5, v13, v14
	s_waitcnt vmcnt(0) lgkmcnt(0)
	v_cvt_pk_bf16_f32 v7, v17, v18
	global_store_dwordx4 v[74:75], v[4:7], off
	s_nop 1
	v_cvt_pk_bf16_f32 v4, v19, v20
	v_cvt_pk_bf16_f32 v5, v21, v22
	v_cvt_pk_bf16_f32 v6, v23, v24
	v_cvt_pk_bf16_f32 v7, v25, v27
	global_store_dwordx4 v[74:75], v[4:7], off offset:16
	s_nop 1
	v_cvt_pk_bf16_f32 v4, v26, v28
	v_cvt_pk_bf16_f32 v5, v29, v30
	v_cvt_pk_bf16_f32 v6, v31, v32
	v_cvt_pk_bf16_f32 v7, v33, v35
	global_store_dwordx4 v[74:75], v[4:7], off offset:32
	s_nop 1
	v_cvt_pk_bf16_f32 v4, v34, v36
	v_cvt_pk_bf16_f32 v5, v37, v40
	v_cvt_pk_bf16_f32 v6, v41, v42
	v_cvt_pk_bf16_f32 v7, v43, v44
	global_store_dwordx4 v[74:75], v[4:7], off offset:48
	s_nop 1
	v_cvt_pk_bf16_f32 v4, v45, v46
	v_cvt_pk_bf16_f32 v5, v47, v48
	v_cvt_pk_bf16_f32 v6, v49, v50
	v_cvt_pk_bf16_f32 v7, v51, v54
	global_store_dwordx4 v[74:75], v[4:7], off offset:64
	s_nop 1
	v_cvt_pk_bf16_f32 v4, v55, v56
	v_cvt_pk_bf16_f32 v5, v57, v58
	v_cvt_pk_bf16_f32 v6, v59, v60
	v_cvt_pk_bf16_f32 v7, v61, v62
	global_store_dwordx4 v[74:75], v[4:7], off offset:80
	s_nop 1
	v_cvt_pk_bf16_f32 v4, v63, v64
	v_cvt_pk_bf16_f32 v5, v65, v66
	v_cvt_pk_bf16_f32 v6, v67, v68
	v_cvt_pk_bf16_f32 v7, v69, v70
	global_store_dwordx4 v[74:75], v[4:7], off offset:96
	s_nop 1
	v_cvt_pk_bf16_f32 v4, v71, v72
	v_cvt_pk_bf16_f32 v5, v73, v76
	v_cvt_pk_bf16_f32 v6, v77, v78
.LBB0_1377:
	s_andn2_b64 vcc, exec, s[0:1]
	s_cbranch_vccnz .LBB0_1381
	v_mov_b32_e32 v2, s49
	ds_read_b64 v[4:5], v2
	s_lshl_b64 s[0:1], s[16:17], 2
	v_readlane_b32 s60, v253, 17
	v_readlane_b32 s61, v253, 18
	v_readlane_b32 s62, v253, 19
	s_waitcnt lgkmcnt(0)
	v_lshl_add_u64 v[4:5], v[4:5], 0, s[0:1]
	s_add_i32 s0, s58, 0xf500
	s_and_b32 s1, s0, 0xffff
	s_mul_i32 s1, s1, 0xba2f
	s_lshr_b32 s38, s1, 16
	s_lshr_b32 s1, s1, 22
	s_mulk_i32 s1, 0x58
	s_sub_i32 s0, s0, s1
	s_lshl_b32 s0, s0, 6
	s_and_b32 s0, s0, 0xffc0
	v_or_b32_e32 v74, s0, v1
	s_and_b32 s0, s38, 0xffc0
	s_mul_i32 s60, s0, 0x5800
	v_lshl_add_u64 v[4:5], v[4:5], 0, s[60:61]
	v_lshlrev_b32_e32 v2, 2, v74
	v_lshl_add_u64 v[66:67], v[4:5], 0, v[2:3]
	v_add_co_u32_e32 v6, vcc, s66, v66
	s_mov_b32 s1, 0xb000
	s_nop 0
	v_addc_co_u32_e32 v7, vcc, 0, v67, vcc
	global_load_dword v5, v[6:7], off offset:2048
	v_add_co_u32_e32 v6, vcc, s1, v66
	s_mov_b32 s1, 0x10000
	s_nop 0
	v_addc_co_u32_e32 v7, vcc, 0, v67, vcc
	v_add_co_u32_e32 v12, vcc, s1, v66
	s_mov_b32 s1, 0x16000
	s_nop 0
	v_addc_co_u32_e32 v13, vcc, 0, v67, vcc
	global_load_dword v4, v[66:67], off
	v_readlane_b32 s63, v253, 20
	global_load_dword v6, v[6:7], off
	s_nop 0
	global_load_dword v7, v[12:13], off offset:2048
	v_add_co_u32_e32 v12, vcc, s1, v66
	s_mov_b32 s1, 0x1b000
	s_nop 0
	v_addc_co_u32_e32 v13, vcc, 0, v67, vcc
	v_add_co_u32_e32 v14, vcc, s1, v66
	global_load_dword v12, v[12:13], off
	s_nop 0
	v_addc_co_u32_e32 v15, vcc, 0, v67, vcc
	global_load_dword v13, v[14:15], off offset:2048
	v_add_co_u32_e32 v14, vcc, s65, v66
	s_mov_b32 s1, 0x26000
	s_nop 0
	v_addc_co_u32_e32 v15, vcc, 0, v67, vcc
	v_add_co_u32_e32 v16, vcc, s1, v66
	s_mov_b32 s1, 0x2c000
	s_nop 0
	v_addc_co_u32_e32 v17, vcc, 0, v67, vcc
	global_load_dword v14, v[14:15], off
	s_nop 0
	global_load_dword v15, v[16:17], off offset:2048
	v_add_co_u32_e32 v16, vcc, s1, v66
	s_mov_b32 s1, 0x31000
	s_nop 0
	v_addc_co_u32_e32 v17, vcc, 0, v67, vcc
	v_add_co_u32_e32 v18, vcc, s1, v66
	s_mov_b32 s1, 0x37000
	s_nop 0
	v_addc_co_u32_e32 v19, vcc, 0, v67, vcc
	global_load_dword v16, v[16:17], off
	s_nop 0
	global_load_dword v17, v[18:19], off offset:2048
	v_add_co_u32_e32 v18, vcc, s1, v66
	s_mov_b32 s1, 0x3c000
	s_nop 0
	v_addc_co_u32_e32 v19, vcc, 0, v67, vcc
	v_add_co_u32_e32 v20, vcc, s1, v66
	s_mov_b32 s1, 0x42000
	s_nop 0
	v_addc_co_u32_e32 v21, vcc, 0, v67, vcc
	global_load_dword v18, v[18:19], off
	s_nop 0
	global_load_dword v19, v[20:21], off offset:2048
	v_add_co_u32_e32 v20, vcc, s1, v66
	s_mov_b32 s1, 0x47000
	s_nop 0
	v_addc_co_u32_e32 v21, vcc, 0, v67, vcc
	v_add_co_u32_e32 v22, vcc, s1, v66
	s_mov_b32 s1, 0x4d000
	s_nop 0
	v_addc_co_u32_e32 v23, vcc, 0, v67, vcc
	global_load_dword v20, v[20:21], off
	s_nop 0
	global_load_dword v21, v[22:23], off offset:2048
	v_add_co_u32_e32 v22, vcc, s1, v66
	s_mov_b32 s1, 0x52000
	s_nop 0
	v_addc_co_u32_e32 v23, vcc, 0, v67, vcc
	v_add_co_u32_e32 v24, vcc, s1, v66
	s_mov_b32 s1, 0x58000
	s_nop 0
	v_addc_co_u32_e32 v25, vcc, 0, v67, vcc
	global_load_dword v22, v[22:23], off
	s_nop 0
	global_load_dword v23, v[24:25], off offset:2048
	v_add_co_u32_e32 v24, vcc, s1, v66
	s_mov_b32 s1, 0x5d000
	s_nop 0
	v_addc_co_u32_e32 v25, vcc, 0, v67, vcc
	v_add_co_u32_e32 v26, vcc, s1, v66
	s_mov_b32 s1, 0x63000
	s_nop 0
	v_addc_co_u32_e32 v27, vcc, 0, v67, vcc
	global_load_dword v24, v[24:25], off
	s_nop 0
	global_load_dword v25, v[26:27], off offset:2048
	v_add_co_u32_e32 v26, vcc, s1, v66
	s_mov_b32 s1, 0x68000
	s_nop 0
	v_addc_co_u32_e32 v27, vcc, 0, v67, vcc
	v_add_co_u32_e32 v28, vcc, s1, v66
	s_mov_b32 s1, 0x6e000
	s_nop 0
	v_addc_co_u32_e32 v29, vcc, 0, v67, vcc
	global_load_dword v26, v[26:27], off
	s_nop 0
	global_load_dword v27, v[28:29], off offset:2048
	v_add_co_u32_e32 v28, vcc, s1, v66
	s_mov_b32 s1, 0x73000
	s_nop 0
	v_addc_co_u32_e32 v29, vcc, 0, v67, vcc
	v_add_co_u32_e32 v30, vcc, s1, v66
	s_mov_b32 s1, 0x79000
	s_nop 0
	v_addc_co_u32_e32 v31, vcc, 0, v67, vcc
	global_load_dword v28, v[28:29], off
	s_nop 0
	global_load_dword v29, v[30:31], off offset:2048
	v_add_co_u32_e32 v30, vcc, s1, v66
	s_mov_b32 s1, 0x7e000
	s_nop 0
	v_addc_co_u32_e32 v31, vcc, 0, v67, vcc
	v_add_co_u32_e32 v32, vcc, s1, v66
	s_mov_b32 s1, 0x84000
	s_nop 0
	v_addc_co_u32_e32 v33, vcc, 0, v67, vcc
	global_load_dword v30, v[30:31], off
	s_nop 0
	global_load_dword v31, v[32:33], off offset:2048
	v_add_co_u32_e32 v32, vcc, s1, v66
	s_mov_b32 s1, 0x89000
	s_nop 0
	v_addc_co_u32_e32 v33, vcc, 0, v67, vcc
	v_add_co_u32_e32 v34, vcc, s1, v66
	s_mov_b32 s1, 0x8f000
	s_nop 0
	v_addc_co_u32_e32 v35, vcc, 0, v67, vcc
	global_load_dword v32, v[32:33], off
	s_nop 0
	global_load_dword v33, v[34:35], off offset:2048
	v_add_co_u32_e32 v34, vcc, s1, v66
	s_mov_b32 s1, 0x94000
	s_nop 0
	v_addc_co_u32_e32 v35, vcc, 0, v67, vcc
	v_add_co_u32_e32 v36, vcc, s1, v66
	s_mov_b32 s1, 0x9a000
	s_nop 0
	v_addc_co_u32_e32 v37, vcc, 0, v67, vcc
	global_load_dword v34, v[34:35], off
	s_nop 0
	global_load_dword v35, v[36:37], off offset:2048
	v_add_co_u32_e32 v36, vcc, s1, v66
	s_mov_b32 s1, 0x9f000
	s_nop 0
	v_addc_co_u32_e32 v37, vcc, 0, v67, vcc
	v_add_co_u32_e32 v38, vcc, s1, v66
	s_mov_b32 s1, 0xa5000
	s_nop 0
	v_addc_co_u32_e32 v39, vcc, 0, v67, vcc
	global_load_dword v36, v[36:37], off
	s_nop 0
	global_load_dword v37, v[38:39], off offset:2048
	v_add_co_u32_e32 v38, vcc, s1, v66
	s_mov_b32 s1, 0xaa000
	s_nop 0
	v_addc_co_u32_e32 v39, vcc, 0, v67, vcc
	v_add_co_u32_e32 v40, vcc, s1, v66
	s_mov_b32 s1, 0xb0000
	s_nop 0
	v_addc_co_u32_e32 v41, vcc, 0, v67, vcc
	global_load_dword v38, v[38:39], off
	s_nop 0
	global_load_dword v39, v[40:41], off offset:2048
	v_add_co_u32_e32 v40, vcc, s1, v66
	s_mov_b32 s1, 0xb5000
	s_nop 0
	v_addc_co_u32_e32 v41, vcc, 0, v67, vcc
	v_add_co_u32_e32 v42, vcc, s1, v66
	s_mov_b32 s1, 0xbb000
	s_nop 0
	v_addc_co_u32_e32 v43, vcc, 0, v67, vcc
	global_load_dword v40, v[40:41], off
	s_nop 0
	global_load_dword v41, v[42:43], off offset:2048
	v_add_co_u32_e32 v42, vcc, s1, v66
	s_mov_b32 s1, 0xc0000
	s_nop 0
	v_addc_co_u32_e32 v43, vcc, 0, v67, vcc
	v_add_co_u32_e32 v44, vcc, s1, v66
	s_mov_b32 s1, 0xc6000
	s_nop 0
	v_addc_co_u32_e32 v45, vcc, 0, v67, vcc
	global_load_dword v42, v[42:43], off
	s_nop 0
	global_load_dword v43, v[44:45], off offset:2048
	v_add_co_u32_e32 v44, vcc, s1, v66
	s_mov_b32 s1, 0xcb000
	s_nop 0
	v_addc_co_u32_e32 v45, vcc, 0, v67, vcc
	v_add_co_u32_e32 v46, vcc, s1, v66
	s_mov_b32 s1, 0xd1000
	s_nop 0
	v_addc_co_u32_e32 v47, vcc, 0, v67, vcc
	global_load_dword v44, v[44:45], off
	s_nop 0
	global_load_dword v45, v[46:47], off offset:2048
	v_add_co_u32_e32 v46, vcc, s1, v66
	s_mov_b32 s1, 0xd6000
	s_nop 0
	v_addc_co_u32_e32 v47, vcc, 0, v67, vcc
	v_add_co_u32_e32 v48, vcc, s1, v66
	s_mov_b32 s1, 0xdc000
	s_nop 0
	v_addc_co_u32_e32 v49, vcc, 0, v67, vcc
	global_load_dword v46, v[46:47], off
	s_nop 0
	global_load_dword v47, v[48:49], off offset:2048
	v_add_co_u32_e32 v48, vcc, s1, v66
	s_mov_b32 s1, 0xe1000
	s_nop 0
	v_addc_co_u32_e32 v49, vcc, 0, v67, vcc
	v_add_co_u32_e32 v50, vcc, s1, v66
	s_mov_b32 s1, 0xe7000
	s_nop 0
	v_addc_co_u32_e32 v51, vcc, 0, v67, vcc
	global_load_dword v48, v[48:49], off
	s_nop 0
	global_load_dword v49, v[50:51], off offset:2048
	v_add_co_u32_e32 v50, vcc, s1, v66
	s_mov_b32 s1, 0xec000
	s_nop 0
	v_addc_co_u32_e32 v51, vcc, 0, v67, vcc
	v_add_co_u32_e32 v52, vcc, s1, v66
	s_mov_b32 s1, 0xf2000
	s_nop 0
	v_addc_co_u32_e32 v53, vcc, 0, v67, vcc
	global_load_dword v50, v[50:51], off
	s_nop 0
	global_load_dword v51, v[52:53], off offset:2048
	v_add_co_u32_e32 v52, vcc, s1, v66
	s_mov_b32 s1, 0xf7000
	s_nop 0
	v_addc_co_u32_e32 v53, vcc, 0, v67, vcc
	global_load_dword v54, v[52:53], off
	v_add_co_u32_e32 v52, vcc, s1, v66
	s_mov_b32 s1, 0xfd000
	s_nop 0
	v_addc_co_u32_e32 v53, vcc, 0, v67, vcc
	global_load_dword v55, v[52:53], off offset:2048
	v_add_co_u32_e32 v52, vcc, s1, v66
	s_mov_b32 s1, 0x102000
	s_nop 0
	v_addc_co_u32_e32 v53, vcc, 0, v67, vcc
	global_load_dword v56, v[52:53], off
	v_add_co_u32_e32 v52, vcc, s1, v66
	s_mov_b32 s1, 0x108000
	s_nop 0
	v_addc_co_u32_e32 v53, vcc, 0, v67, vcc
	global_load_dword v57, v[52:53], off offset:2048
	v_add_co_u32_e32 v52, vcc, s1, v66
	s_mov_b32 s1, 0x10d000
	s_nop 0
	v_addc_co_u32_e32 v53, vcc, 0, v67, vcc
	global_load_dword v58, v[52:53], off
	v_add_co_u32_e32 v52, vcc, s1, v66
	s_mov_b32 s1, 0x113000
	s_nop 0
	v_addc_co_u32_e32 v53, vcc, 0, v67, vcc
	global_load_dword v59, v[52:53], off offset:2048
	v_add_co_u32_e32 v52, vcc, s1, v66
	s_mov_b32 s1, 0x118000
	s_nop 0
	v_addc_co_u32_e32 v53, vcc, 0, v67, vcc
	global_load_dword v60, v[52:53], off
	v_add_co_u32_e32 v52, vcc, s1, v66
	s_mov_b32 s1, 0x11e000
	s_nop 0
	v_addc_co_u32_e32 v53, vcc, 0, v67, vcc
	global_load_dword v61, v[52:53], off offset:2048
	v_add_co_u32_e32 v52, vcc, s1, v66
	s_mov_b32 s1, 0x123000
	s_nop 0
	v_addc_co_u32_e32 v53, vcc, 0, v67, vcc
	global_load_dword v62, v[52:53], off
	v_add_co_u32_e32 v52, vcc, s1, v66
	s_mov_b32 s1, 0x129000
	s_nop 0
	v_addc_co_u32_e32 v53, vcc, 0, v67, vcc
	global_load_dword v63, v[52:53], off offset:2048
	v_add_co_u32_e32 v52, vcc, s1, v66
	s_mov_b32 s1, 0x12e000
	s_nop 0
	v_addc_co_u32_e32 v53, vcc, 0, v67, vcc
	global_load_dword v64, v[52:53], off
	v_add_co_u32_e32 v52, vcc, s1, v66
	s_mov_b32 s1, 0x134000
	s_nop 0
	v_addc_co_u32_e32 v53, vcc, 0, v67, vcc
	global_load_dword v65, v[52:53], off offset:2048
	v_add_co_u32_e32 v52, vcc, s1, v66
	s_mov_b32 s1, 0x139000
	s_nop 0
	v_addc_co_u32_e32 v53, vcc, 0, v67, vcc
	global_load_dword v68, v[52:53], off
	v_add_co_u32_e32 v52, vcc, s1, v66
	s_mov_b32 s1, 0x13f000
	s_nop 0
	v_addc_co_u32_e32 v53, vcc, 0, v67, vcc
	global_load_dword v69, v[52:53], off offset:2048
	v_add_co_u32_e32 v52, vcc, s1, v66
	s_mov_b32 s1, 0x144000
	s_nop 0
	v_addc_co_u32_e32 v53, vcc, 0, v67, vcc
	global_load_dword v70, v[52:53], off
	v_add_co_u32_e32 v52, vcc, s1, v66
	s_mov_b32 s1, 0x14a000
	s_nop 0
	v_addc_co_u32_e32 v53, vcc, 0, v67, vcc
	global_load_dword v71, v[52:53], off offset:2048
	v_add_co_u32_e32 v52, vcc, s1, v66
	s_mov_b32 s1, 0x14f000
	s_nop 0
	v_addc_co_u32_e32 v53, vcc, 0, v67, vcc
	global_load_dword v72, v[52:53], off
	v_add_co_u32_e32 v52, vcc, s1, v66
	s_mov_b32 s1, 0x155000
	s_nop 0
	v_addc_co_u32_e32 v53, vcc, 0, v67, vcc
	global_load_dword v73, v[52:53], off offset:2048
	v_add_co_u32_e32 v52, vcc, s1, v66
	s_mov_b32 s1, 0x15a000
	s_nop 0
	v_addc_co_u32_e32 v53, vcc, 0, v67, vcc
	v_add_co_u32_e32 v66, vcc, s1, v66
	global_load_dword v52, v[52:53], off
	s_nop 0
	v_addc_co_u32_e32 v67, vcc, 0, v67, vcc
	global_load_dword v53, v[66:67], off offset:2048
	v_cmp_eq_u64_e32 vcc, 0, v[10:11]
	s_cbranch_vccnz .LBB0_1380
	s_lshl_b32 s60, s0, 2
	v_lshl_add_u64 v[66:67], v[8:9], 0, s[60:61]
	global_load_dwordx4 v[86:89], v[66:67], off
	global_load_dwordx4 v[90:93], v[66:67], off offset:16
	global_load_dwordx4 v[94:97], v[66:67], off offset:32
	global_load_dwordx4 v[98:101], v[66:67], off offset:48
	global_load_dwordx4 v[102:105], v[66:67], off offset:64
	global_load_dwordx4 v[106:109], v[66:67], off offset:80
	global_load_dwordx4 v[110:113], v[66:67], off offset:96
	global_load_dwordx4 v[114:117], v[66:67], off offset:112
	global_load_dwordx4 v[118:121], v[66:67], off offset:128
	global_load_dwordx4 v[122:125], v[66:67], off offset:144
	global_load_dwordx4 v[126:129], v[66:67], off offset:160
	global_load_dwordx4 v[130:133], v[66:67], off offset:176
	global_load_dwordx4 v[134:137], v[66:67], off offset:192
	global_load_dwordx4 v[138:141], v[66:67], off offset:208
	global_load_dwordx4 v[142:145], v[66:67], off offset:224
	global_load_dwordx4 v[76:79], v[66:67], off offset:240
	s_waitcnt vmcnt(0) lgkmcnt(0)
	v_pk_mul_f32 v[4:5], v[4:5], v[86:87]
	v_pk_mul_f32 v[6:7], v[6:7], v[88:89]
	v_pk_mul_f32 v[12:13], v[12:13], v[90:91]
	v_pk_mul_f32 v[14:15], v[14:15], v[92:93]
	v_pk_mul_f32 v[16:17], v[16:17], v[94:95]
	v_pk_mul_f32 v[18:19], v[18:19], v[96:97]
	v_pk_mul_f32 v[20:21], v[20:21], v[98:99]
	v_pk_mul_f32 v[22:23], v[22:23], v[100:101]
	v_pk_mul_f32 v[24:25], v[24:25], v[102:103]
	v_pk_mul_f32 v[26:27], v[26:27], v[104:105]
	v_pk_mul_f32 v[28:29], v[28:29], v[106:107]
	v_pk_mul_f32 v[30:31], v[30:31], v[108:109]
	v_pk_mul_f32 v[32:33], v[32:33], v[110:111]
	v_pk_mul_f32 v[34:35], v[34:35], v[112:113]
	v_pk_mul_f32 v[36:37], v[36:37], v[114:115]
	v_pk_mul_f32 v[38:39], v[38:39], v[116:117]
	v_pk_mul_f32 v[40:41], v[40:41], v[118:119]
	v_pk_mul_f32 v[42:43], v[42:43], v[120:121]
	v_pk_mul_f32 v[44:45], v[44:45], v[122:123]
	v_pk_mul_f32 v[46:47], v[46:47], v[124:125]
	v_pk_mul_f32 v[48:49], v[48:49], v[126:127]
	v_pk_mul_f32 v[50:51], v[50:51], v[128:129]
	v_pk_mul_f32 v[54:55], v[54:55], v[130:131]
	v_pk_mul_f32 v[56:57], v[56:57], v[132:133]
	v_pk_mul_f32 v[58:59], v[58:59], v[134:135]
	v_pk_mul_f32 v[60:61], v[60:61], v[136:137]
	v_pk_mul_f32 v[62:63], v[62:63], v[138:139]
	v_pk_mul_f32 v[64:65], v[64:65], v[140:141]
	v_pk_mul_f32 v[68:69], v[68:69], v[142:143]
	v_pk_mul_f32 v[70:71], v[70:71], v[144:145]
	v_pk_mul_f32 v[72:73], v[72:73], v[76:77]
	v_pk_mul_f32 v[52:53], v[52:53], v[78:79]
.LBB0_1380:
	v_lshlrev_b32_e32 v2, 12, v74
	v_lshl_add_u64 v[66:67], s[40:41], 0, v[2:3]
	s_lshl_b32 s60, s0, 1
	v_lshl_add_u64 v[74:75], v[66:67], 0, s[60:61]
	s_waitcnt vmcnt(0) lgkmcnt(0)
	v_cvt_pk_bf16_f32 v4, v4, v5
	v_cvt_pk_bf16_f32 v5, v6, v7
	v_cvt_pk_bf16_f32 v6, v12, v13
	v_cvt_pk_bf16_f32 v7, v14, v15
	global_store_dwordx4 v[74:75], v[4:7], off
	s_mov_b32 s1, s61
	v_writelane_b32 v253, s0, 17
	v_cvt_pk_bf16_f32 v4, v16, v17
	v_cvt_pk_bf16_f32 v5, v18, v19
	v_cvt_pk_bf16_f32 v6, v20, v21
	v_cvt_pk_bf16_f32 v7, v22, v23
	global_store_dwordx4 v[74:75], v[4:7], off offset:16
	v_writelane_b32 v253, s1, 18
	v_writelane_b32 v253, s2, 19
	v_cvt_pk_bf16_f32 v4, v24, v25
	v_cvt_pk_bf16_f32 v5, v26, v27
	v_cvt_pk_bf16_f32 v6, v28, v29
	v_cvt_pk_bf16_f32 v7, v30, v31
	global_store_dwordx4 v[74:75], v[4:7], off offset:32
	v_writelane_b32 v253, s3, 20
	s_nop 0
	v_cvt_pk_bf16_f32 v4, v32, v33
	v_cvt_pk_bf16_f32 v5, v34, v35
	v_cvt_pk_bf16_f32 v6, v36, v37
	v_cvt_pk_bf16_f32 v7, v38, v39
	global_store_dwordx4 v[74:75], v[4:7], off offset:48
	s_nop 1
	v_cvt_pk_bf16_f32 v4, v40, v41
	v_cvt_pk_bf16_f32 v5, v42, v43
	v_cvt_pk_bf16_f32 v6, v44, v45
	v_cvt_pk_bf16_f32 v7, v46, v47
	global_store_dwordx4 v[74:75], v[4:7], off offset:64
	s_nop 1
	v_cvt_pk_bf16_f32 v4, v48, v49
	v_cvt_pk_bf16_f32 v5, v50, v51
	v_cvt_pk_bf16_f32 v6, v54, v55
	v_cvt_pk_bf16_f32 v7, v56, v57
	global_store_dwordx4 v[74:75], v[4:7], off offset:80
	s_nop 1
	v_cvt_pk_bf16_f32 v4, v58, v59
	v_cvt_pk_bf16_f32 v5, v60, v61
	v_cvt_pk_bf16_f32 v6, v62, v63
	v_cvt_pk_bf16_f32 v7, v64, v65
	global_store_dwordx4 v[74:75], v[4:7], off offset:96
	s_nop 1
	v_cvt_pk_bf16_f32 v4, v68, v69
	v_cvt_pk_bf16_f32 v5, v70, v71
	v_cvt_pk_bf16_f32 v6, v72, v73

.LBB0_1382:
	s_andn2_b64 vcc, exec, s[0:1]
	s_cbranch_vccnz .LBB0_1333
	v_mov_b32_e32 v2, s52
	ds_read_b64 v[4:5], v2
	s_mul_hi_i32 s38, s58, 0x2e8ba2e9
	s_lshr_b32 s39, s38, 31
	s_ashr_i32 s38, s38, 4
	s_lshl_b64 s[0:1], s[16:17], 2
	s_add_i32 s39, s38, s39
	s_waitcnt lgkmcnt(0)
	v_lshl_add_u64 v[6:7], v[4:5], 0, s[0:1]
	s_mul_i32 s0, s39, 0x58
	s_sub_i32 s0, s58, s0
	s_lshl_b32 s38, s39, 6
	s_cmp_gt_i32 s0, -1
	v_lshl_or_b32 v4, s0, 6, v1
	s_cselect_b64 s[0:1], -1, 0
	s_mul_i32 s58, s39, 0x160000
	s_mul_hi_i32 s59, s38, 0x5800
	v_cndmask_b32_e64 v2, 0, v4, s[0:1]
	v_lshl_add_u64 v[6:7], v[6:7], 0, s[58:59]
	v_lshl_add_u64 v[66:67], v[2:3], 2, v[6:7]
	v_add_co_u32_e32 v6, vcc, s66, v66
	s_mov_b32 s39, 0xb000
	s_nop 0
	v_addc_co_u32_e32 v7, vcc, 0, v67, vcc
	v_add_co_u32_e32 v12, vcc, s39, v66
	s_mov_b32 s39, 0x10000
	s_nop 0
	v_addc_co_u32_e32 v13, vcc, 0, v67, vcc
	v_add_co_u32_e32 v18, vcc, s39, v66
	s_mov_b32 s39, 0x16000
	s_nop 0
	v_addc_co_u32_e32 v19, vcc, 0, v67, vcc
	v_add_co_u32_e32 v20, vcc, s39, v66
	s_mov_b32 s39, 0x1b000
	s_nop 0
	v_addc_co_u32_e32 v21, vcc, 0, v67, vcc
	v_add_co_u32_e32 v22, vcc, s39, v66
	s_mov_b32 s39, 0x26000
	s_nop 0
	v_addc_co_u32_e32 v23, vcc, 0, v67, vcc
	v_add_co_u32_e32 v24, vcc, s65, v66
	s_nop 1
	v_addc_co_u32_e32 v25, vcc, 0, v67, vcc
	v_add_co_u32_e32 v26, vcc, s39, v66
	s_mov_b32 s39, 0x2c000
	s_nop 0
	v_addc_co_u32_e32 v27, vcc, 0, v67, vcc
	global_load_dword v16, v[66:67], off
	global_load_dword v17, v[6:7], off offset:2048
	global_load_dword v14, v[12:13], off
	global_load_dword v15, v[18:19], off offset:2048
	s_nop 0
	global_load_dword v12, v[20:21], off
	global_load_dword v13, v[22:23], off offset:2048
	global_load_dword v6, v[24:25], off
	global_load_dword v7, v[26:27], off offset:2048
	v_add_co_u32_e32 v18, vcc, s39, v66
	s_mov_b32 s39, 0x31000
	s_nop 0
	v_addc_co_u32_e32 v19, vcc, 0, v67, vcc
	v_add_co_u32_e32 v20, vcc, s39, v66
	s_mov_b32 s39, 0x37000
	s_nop 0
	v_addc_co_u32_e32 v21, vcc, 0, v67, vcc
	v_add_co_u32_e32 v22, vcc, s39, v66
	s_mov_b32 s39, 0x3c000
	s_nop 0
	v_addc_co_u32_e32 v23, vcc, 0, v67, vcc
	v_add_co_u32_e32 v26, vcc, s39, v66
	s_mov_b32 s39, 0x42000
	s_nop 0
	v_addc_co_u32_e32 v27, vcc, 0, v67, vcc
	v_add_co_u32_e32 v28, vcc, s39, v66
	s_mov_b32 s39, 0x47000
	s_nop 0
	v_addc_co_u32_e32 v29, vcc, 0, v67, vcc
	v_add_co_u32_e32 v30, vcc, s39, v66
	s_mov_b32 s39, 0x4d000
	s_nop 0
	v_addc_co_u32_e32 v31, vcc, 0, v67, vcc
	v_add_co_u32_e32 v32, vcc, s39, v66
	s_mov_b32 s39, 0x52000
	s_nop 0
	v_addc_co_u32_e32 v33, vcc, 0, v67, vcc
	v_add_co_u32_e32 v34, vcc, s39, v66
	s_mov_b32 s39, 0x58000
	s_nop 0
	v_addc_co_u32_e32 v35, vcc, 0, v67, vcc
	global_load_dword v24, v[18:19], off
	global_load_dword v25, v[20:21], off offset:2048
	s_nop 0
	global_load_dword v22, v[22:23], off
	s_nop 0
	global_load_dword v23, v[26:27], off offset:2048
	global_load_dword v20, v[28:29], off
	global_load_dword v21, v[30:31], off offset:2048
	global_load_dword v18, v[32:33], off
	global_load_dword v19, v[34:35], off offset:2048
	v_add_co_u32_e32 v26, vcc, s39, v66
	s_mov_b32 s39, 0x5d000
	s_nop 0
	v_addc_co_u32_e32 v27, vcc, 0, v67, vcc
	v_add_co_u32_e32 v28, vcc, s39, v66
	s_mov_b32 s39, 0x63000
	s_nop 0
	v_addc_co_u32_e32 v29, vcc, 0, v67, vcc
	v_add_co_u32_e32 v30, vcc, s39, v66
	s_mov_b32 s39, 0x68000
	s_nop 0
	v_addc_co_u32_e32 v31, vcc, 0, v67, vcc
	v_add_co_u32_e32 v34, vcc, s39, v66
	s_mov_b32 s39, 0x6e000
	s_nop 0
	v_addc_co_u32_e32 v35, vcc, 0, v67, vcc
	v_add_co_u32_e32 v36, vcc, s39, v66
	s_mov_b32 s39, 0x73000
	s_nop 0
	v_addc_co_u32_e32 v37, vcc, 0, v67, vcc
	v_add_co_u32_e32 v38, vcc, s39, v66
	s_mov_b32 s39, 0x79000
	s_nop 0
	v_addc_co_u32_e32 v39, vcc, 0, v67, vcc
	v_add_co_u32_e32 v40, vcc, s39, v66
	s_mov_b32 s39, 0x7e000
	s_nop 0
	v_addc_co_u32_e32 v41, vcc, 0, v67, vcc
	v_add_co_u32_e32 v42, vcc, s39, v66
	s_mov_b32 s39, 0x84000
	s_nop 0
	v_addc_co_u32_e32 v43, vcc, 0, v67, vcc
	global_load_dword v32, v[26:27], off
	global_load_dword v33, v[28:29], off offset:2048
	s_nop 0
	global_load_dword v30, v[30:31], off
	s_nop 0
	global_load_dword v31, v[34:35], off offset:2048
	global_load_dword v28, v[36:37], off
	global_load_dword v29, v[38:39], off offset:2048
	global_load_dword v26, v[40:41], off
	global_load_dword v27, v[42:43], off offset:2048
	v_add_co_u32_e32 v34, vcc, s39, v66
	s_mov_b32 s39, 0x89000
	s_nop 0
	v_addc_co_u32_e32 v35, vcc, 0, v67, vcc
	v_add_co_u32_e32 v36, vcc, s39, v66
	s_mov_b32 s39, 0x8f000
	s_nop 0
	v_addc_co_u32_e32 v37, vcc, 0, v67, vcc
	v_add_co_u32_e32 v38, vcc, s39, v66
	s_mov_b32 s39, 0x94000
	s_nop 0
	v_addc_co_u32_e32 v39, vcc, 0, v67, vcc
	v_add_co_u32_e32 v42, vcc, s39, v66
	s_mov_b32 s39, 0x9a000
	s_nop 0
	v_addc_co_u32_e32 v43, vcc, 0, v67, vcc
	v_add_co_u32_e32 v44, vcc, s39, v66
	s_mov_b32 s39, 0x9f000
	s_nop 0
	v_addc_co_u32_e32 v45, vcc, 0, v67, vcc
	v_add_co_u32_e32 v46, vcc, s39, v66
	s_mov_b32 s39, 0xa5000
	s_nop 0
	v_addc_co_u32_e32 v47, vcc, 0, v67, vcc
	v_add_co_u32_e32 v48, vcc, s39, v66
	s_mov_b32 s39, 0xaa000
	s_nop 0
	v_addc_co_u32_e32 v49, vcc, 0, v67, vcc
	v_add_co_u32_e32 v50, vcc, s39, v66
	s_mov_b32 s39, 0xb0000
	s_nop 0
	v_addc_co_u32_e32 v51, vcc, 0, v67, vcc
	global_load_dword v40, v[34:35], off
	global_load_dword v41, v[36:37], off offset:2048
	s_nop 0
	global_load_dword v38, v[38:39], off
	s_nop 0
	global_load_dword v39, v[42:43], off offset:2048
	global_load_dword v36, v[44:45], off
	global_load_dword v37, v[46:47], off offset:2048
	global_load_dword v34, v[48:49], off
	global_load_dword v35, v[50:51], off offset:2048
	v_add_co_u32_e32 v42, vcc, s39, v66
	s_mov_b32 s39, 0xb5000
	s_nop 0
	v_addc_co_u32_e32 v43, vcc, 0, v67, vcc
	v_add_co_u32_e32 v44, vcc, s39, v66
	s_mov_b32 s39, 0xbb000
	s_nop 0
	v_addc_co_u32_e32 v45, vcc, 0, v67, vcc
	v_add_co_u32_e32 v46, vcc, s39, v66
	s_mov_b32 s39, 0xc0000
	s_nop 0
	v_addc_co_u32_e32 v47, vcc, 0, v67, vcc
	v_add_co_u32_e32 v50, vcc, s39, v66
	s_mov_b32 s39, 0xc6000
	s_nop 0
	v_addc_co_u32_e32 v51, vcc, 0, v67, vcc
	v_add_co_u32_e32 v52, vcc, s39, v66
	s_mov_b32 s39, 0xcb000
	s_nop 0
	v_addc_co_u32_e32 v53, vcc, 0, v67, vcc
	v_add_co_u32_e32 v54, vcc, s39, v66
	s_mov_b32 s39, 0xd1000
	s_nop 0
	v_addc_co_u32_e32 v55, vcc, 0, v67, vcc
	v_add_co_u32_e32 v56, vcc, s39, v66
	s_mov_b32 s39, 0xd6000
	s_nop 0
	v_addc_co_u32_e32 v57, vcc, 0, v67, vcc
	v_add_co_u32_e32 v58, vcc, s39, v66
	s_mov_b32 s39, 0xdc000
	s_nop 0
	v_addc_co_u32_e32 v59, vcc, 0, v67, vcc
	global_load_dword v48, v[42:43], off
	global_load_dword v49, v[44:45], off offset:2048
	s_nop 0
	global_load_dword v46, v[46:47], off
	s_nop 0
	global_load_dword v47, v[50:51], off offset:2048
	global_load_dword v44, v[52:53], off
	global_load_dword v45, v[54:55], off offset:2048
	global_load_dword v42, v[56:57], off
	global_load_dword v43, v[58:59], off offset:2048
	v_add_co_u32_e32 v50, vcc, s39, v66
	s_mov_b32 s39, 0xe1000
	s_nop 0
	v_addc_co_u32_e32 v51, vcc, 0, v67, vcc
	v_add_co_u32_e32 v52, vcc, s39, v66
	s_mov_b32 s39, 0xe7000
	s_nop 0
	v_addc_co_u32_e32 v53, vcc, 0, v67, vcc
	v_add_co_u32_e32 v54, vcc, s39, v66
	s_mov_b32 s39, 0xec000
	s_nop 0
	v_addc_co_u32_e32 v55, vcc, 0, v67, vcc
	v_add_co_u32_e32 v58, vcc, s39, v66
	s_mov_b32 s39, 0xf2000
	s_nop 0
	v_addc_co_u32_e32 v59, vcc, 0, v67, vcc
	v_add_co_u32_e32 v60, vcc, s39, v66
	s_mov_b32 s39, 0xf7000
	s_nop 0
	v_addc_co_u32_e32 v61, vcc, 0, v67, vcc
	v_add_co_u32_e32 v62, vcc, s39, v66
	s_mov_b32 s39, 0xfd000
	s_nop 0
	v_addc_co_u32_e32 v63, vcc, 0, v67, vcc
	v_add_co_u32_e32 v64, vcc, s39, v66
	s_mov_b32 s39, 0x102000
	s_nop 0
	v_addc_co_u32_e32 v65, vcc, 0, v67, vcc
	v_add_co_u32_e32 v68, vcc, s39, v66
	s_mov_b32 s39, 0x108000
	s_nop 0
	v_addc_co_u32_e32 v69, vcc, 0, v67, vcc
	global_load_dword v56, v[50:51], off
	global_load_dword v57, v[52:53], off offset:2048
	s_nop 0
	global_load_dword v54, v[54:55], off
	s_nop 0
	global_load_dword v55, v[58:59], off offset:2048
	global_load_dword v52, v[60:61], off
	global_load_dword v53, v[62:63], off offset:2048
	global_load_dword v50, v[64:65], off
	global_load_dword v51, v[68:69], off offset:2048
	v_add_co_u32_e32 v58, vcc, s39, v66
	s_mov_b32 s39, 0x10d000
	s_nop 0
	v_addc_co_u32_e32 v59, vcc, 0, v67, vcc
	v_add_co_u32_e32 v60, vcc, s39, v66
	s_mov_b32 s39, 0x113000
	s_nop 0
	v_addc_co_u32_e32 v61, vcc, 0, v67, vcc
	v_add_co_u32_e32 v62, vcc, s39, v66
	s_mov_b32 s39, 0x118000
	s_nop 0
	v_addc_co_u32_e32 v63, vcc, 0, v67, vcc
	v_add_co_u32_e32 v68, vcc, s39, v66
	s_mov_b32 s39, 0x11e000
	s_nop 0
	v_addc_co_u32_e32 v69, vcc, 0, v67, vcc
	v_add_co_u32_e32 v70, vcc, s39, v66
	s_mov_b32 s39, 0x123000
	s_nop 0
	v_addc_co_u32_e32 v71, vcc, 0, v67, vcc
	v_add_co_u32_e32 v72, vcc, s39, v66
	s_mov_b32 s39, 0x129000
	s_nop 0
	v_addc_co_u32_e32 v73, vcc, 0, v67, vcc
	v_add_co_u32_e32 v74, vcc, s39, v66
	s_mov_b32 s39, 0x12e000
	s_nop 0
	v_addc_co_u32_e32 v75, vcc, 0, v67, vcc
	v_add_co_u32_e32 v76, vcc, s39, v66
	s_mov_b32 s39, 0x134000
	s_nop 0
	v_addc_co_u32_e32 v77, vcc, 0, v67, vcc
	global_load_dword v64, v[58:59], off
	global_load_dword v65, v[60:61], off offset:2048
	s_nop 0
	global_load_dword v62, v[62:63], off
	s_nop 0
	global_load_dword v63, v[68:69], off offset:2048
	global_load_dword v60, v[70:71], off
	global_load_dword v61, v[72:73], off offset:2048
	global_load_dword v58, v[74:75], off
	global_load_dword v59, v[76:77], off offset:2048
	v_add_co_u32_e32 v68, vcc, s39, v66
	s_mov_b32 s39, 0x139000
	s_nop 0
	v_addc_co_u32_e32 v69, vcc, 0, v67, vcc
	v_add_co_u32_e32 v70, vcc, s39, v66
	s_mov_b32 s39, 0x13f000
	s_nop 0
	v_addc_co_u32_e32 v71, vcc, 0, v67, vcc
	v_add_co_u32_e32 v74, vcc, s39, v66
	s_mov_b32 s39, 0x144000
	s_nop 0
	v_addc_co_u32_e32 v75, vcc, 0, v67, vcc
	v_add_co_u32_e32 v76, vcc, s39, v66
	s_mov_b32 s39, 0x14a000
	s_nop 0
	v_addc_co_u32_e32 v77, vcc, 0, v67, vcc
	v_add_co_u32_e32 v78, vcc, s39, v66
	s_mov_b32 s39, 0x14f000
	s_nop 0
	v_addc_co_u32_e32 v79, vcc, 0, v67, vcc
	v_add_co_u32_e32 v80, vcc, s39, v66
	s_mov_b32 s39, 0x155000
	s_nop 0
	v_addc_co_u32_e32 v81, vcc, 0, v67, vcc
	v_add_co_u32_e32 v82, vcc, s39, v66
	s_mov_b32 s39, 0x15a000
	s_nop 0
	v_addc_co_u32_e32 v83, vcc, 0, v67, vcc
	v_add_co_u32_e32 v84, vcc, s39, v66
	s_ashr_i32 s39, s38, 31
	s_nop 0
	v_addc_co_u32_e32 v85, vcc, 0, v67, vcc
	global_load_dword v72, v[68:69], off
	global_load_dword v73, v[70:71], off offset:2048
	s_nop 0
	global_load_dword v70, v[74:75], off
	global_load_dword v71, v[76:77], off offset:2048
	global_load_dword v68, v[78:79], off
	global_load_dword v69, v[80:81], off offset:2048
	global_load_dword v66, v[82:83], off
	global_load_dword v67, v[84:85], off offset:2048
	v_cmp_eq_u64_e32 vcc, 0, v[10:11]
	s_cbranch_vccnz .LBB0_1332
	s_lshl_b64 s[58:59], s[38:39], 2
	v_lshl_add_u64 v[74:75], v[8:9], 0, s[58:59]
	global_load_dwordx4 v[86:89], v[74:75], off
	global_load_dwordx4 v[90:93], v[74:75], off offset:16
	global_load_dwordx4 v[94:97], v[74:75], off offset:32
	global_load_dwordx4 v[98:101], v[74:75], off offset:48
	global_load_dwordx4 v[102:105], v[74:75], off offset:64
	global_load_dwordx4 v[106:109], v[74:75], off offset:80
	global_load_dwordx4 v[110:113], v[74:75], off offset:96
	global_load_dwordx4 v[114:117], v[74:75], off offset:112
	global_load_dwordx4 v[118:121], v[74:75], off offset:128
	global_load_dwordx4 v[122:125], v[74:75], off offset:144
	global_load_dwordx4 v[126:129], v[74:75], off offset:160
	global_load_dwordx4 v[130:133], v[74:75], off offset:176
	global_load_dwordx4 v[134:137], v[74:75], off offset:192
	global_load_dwordx4 v[138:141], v[74:75], off offset:208
	global_load_dwordx4 v[142:145], v[74:75], off offset:224
	global_load_dwordx4 v[8:11], v[74:75], off offset:240
	s_waitcnt vmcnt(0) lgkmcnt(0)
	v_pk_mul_f32 v[16:17], v[16:17], v[86:87]
	v_pk_mul_f32 v[14:15], v[14:15], v[88:89]
	v_pk_mul_f32 v[12:13], v[12:13], v[90:91]
	v_pk_mul_f32 v[6:7], v[6:7], v[92:93]
	v_pk_mul_f32 v[24:25], v[24:25], v[94:95]
	v_pk_mul_f32 v[22:23], v[22:23], v[96:97]
	v_pk_mul_f32 v[20:21], v[20:21], v[98:99]
	v_pk_mul_f32 v[18:19], v[18:19], v[100:101]
	v_pk_mul_f32 v[32:33], v[32:33], v[102:103]
	v_pk_mul_f32 v[30:31], v[30:31], v[104:105]
	v_pk_mul_f32 v[28:29], v[28:29], v[106:107]
	v_pk_mul_f32 v[26:27], v[26:27], v[108:109]
	v_pk_mul_f32 v[40:41], v[40:41], v[110:111]
	v_pk_mul_f32 v[38:39], v[38:39], v[112:113]
	v_pk_mul_f32 v[36:37], v[36:37], v[114:115]
	v_pk_mul_f32 v[34:35], v[34:35], v[116:117]
	v_pk_mul_f32 v[48:49], v[48:49], v[118:119]
	v_pk_mul_f32 v[46:47], v[46:47], v[120:121]
	v_pk_mul_f32 v[44:45], v[44:45], v[122:123]
	v_pk_mul_f32 v[42:43], v[42:43], v[124:125]
	v_pk_mul_f32 v[56:57], v[56:57], v[126:127]
	v_pk_mul_f32 v[54:55], v[54:55], v[128:129]
	v_pk_mul_f32 v[52:53], v[52:53], v[130:131]
	v_pk_mul_f32 v[50:51], v[50:51], v[132:133]
	v_pk_mul_f32 v[64:65], v[64:65], v[134:135]
	v_pk_mul_f32 v[62:63], v[62:63], v[136:137]
	v_pk_mul_f32 v[60:61], v[60:61], v[138:139]
	v_pk_mul_f32 v[58:59], v[58:59], v[140:141]
	v_pk_mul_f32 v[72:73], v[72:73], v[142:143]
	v_pk_mul_f32 v[70:71], v[70:71], v[144:145]
	v_pk_mul_f32 v[68:69], v[68:69], v[8:9]
	v_pk_mul_f32 v[66:67], v[66:67], v[10:11]
	s_branch .LBB0_1332

.LBB0_1386:
	s_mov_b32 s72, s64
	v_mov_b32_e32 v1, v0
	v_mov_b32_e32 v12, v0
	v_readlane_b32 s10, v252, 0
	s_mov_b32 s5, s88
	s_lshl_b32 s5, s5, 3
	v_readfirstlane_b32 s0, v12
	s_ashr_i32 s4, s0, 6
	s_add_i32 s4, s5, s4
	s_mov_b64 s[0:1], s[68:69]
	s_cmpk_gt_i32 s4, 0x3fff
	s_cbranch_scc1 .LBB0_1389
	s_add_i32 s5, s72, 0x21090
	v_readlane_b32 s12, v253, 17
	v_mov_b32_e32 v1, s5
	v_readlane_b32 s13, v253, 18
	v_readlane_b32 s6, v253, 24
	ds_read_b64 v[4:5], v1
	v_readlane_b32 s7, v253, 25
	s_mov_b32 s5, s13
	v_readlane_b32 s14, v253, 19
	v_readlane_b32 s15, v253, 20
	s_lshl_b32 s8, s6, 7
	v_writelane_b32 v253, s4, 17
	s_mov_b32 s9, s13
	v_lshlrev_b32_e32 v1, 5, v12
	v_writelane_b32 v253, s5, 18
	v_writelane_b32 v253, s6, 19
	v_writelane_b32 v253, s7, 20
	s_lshl_b64 s[6:7], s[8:9], 2
	v_and_b32_e32 v2, 0x1e0, v1
	s_waitcnt lgkmcnt(0)
	v_lshl_add_u64 v[4:5], v[4:5], 0, s[6:7]
	v_lshl_add_u64 v[8:9], v[4:5], 0, v[2:3]
	global_load_dwordx4 v[4:7], v[8:9], off offset:16
	s_nop 0
	global_load_dwordx4 v[8:11], v[8:9], off
	v_xor_b32_e32 v1, 1, v230
	v_cmp_lt_i32_e32 vcc, v1, v231
	v_xor_b32_e32 v2, 2, v230
	s_ashr_i32 s5, s4, 31
	v_cndmask_b32_e32 v1, v230, v1, vcc
	v_cmp_lt_i32_e32 vcc, v2, v231
	s_lshl_b32 s6, s10, 3
	s_lshl_b64 s[8:9], s[4:5], 12
	v_cndmask_b32_e32 v2, v230, v2, vcc
	v_lshlrev_b32_e32 v22, 2, v2
	v_xor_b32_e32 v2, 4, v230
	v_cmp_lt_i32_e32 vcc, v2, v231
	v_and_b32_e32 v12, 63, v12
	s_add_u32 s7, s8, 0x25800c00
	v_cndmask_b32_e32 v2, v230, v2, vcc
	v_lshlrev_b32_e32 v23, 2, v2
	v_xor_b32_e32 v2, 8, v230
	v_cmp_lt_i32_e32 vcc, v2, v231
	s_addc_u32 s8, s9, 0
	v_mov_b32_e32 v17, s8
	v_cndmask_b32_e32 v2, v230, v2, vcc
	v_lshlrev_b32_e32 v24, 2, v2
	v_lshlrev_b32_e32 v2, 4, v12
	v_or_b32_e32 v16, s7, v2
	s_ashr_i32 s7, s6, 31
	s_lshl_b64 s[8:9], s[6:7], 12
	s_mul_i32 s12, s4, 0x7200
	s_mul_hi_i32 s13, s4, 0x7200
	s_add_u32 s12, s12, 0x9002800
	s_addc_u32 s13, s13, 0
	v_lshl_add_u64 v[18:19], s[12:13], 0, v[2:3]
	s_lshl_b64 s[12:13], s[4:5], 11
	v_lshlrev_b32_e32 v1, 2, v1
	s_mul_i32 s10, s10, 0x39000
	s_mul_hi_i32 s11, s6, 0x7200
	v_lshl_or_b32 v20, v12, 5, s12
	v_mov_b32_e32 v21, s13
	s_lshl_b64 s[12:13], s[6:7], 11
	s_movk_i32 s20, 0x110
.LBB0_1388:
	v_lshl_add_u64 v[12:13], s[0:1], 0, v[20:21]
	v_add_co_u32_e32 v26, vcc, 0x47200000, v12
	s_add_i32 s4, s4, s6
	s_nop 0
	v_addc_co_u32_e32 v27, vcc, 0, v13, vcc
	global_load_dwordx4 v[12:15], v[26:27], off
	s_nop 0
	global_load_dwordx4 v[26:29], v[26:27], off offset:16
	v_lshl_add_u64 v[20:21], v[20:21], 0, s[12:13]
	s_cmpk_lt_i32 s4, 0x4000
	s_waitcnt vmcnt(0) lgkmcnt(0)
	v_pk_mul_f32 v[30:31], v[14:15], v[14:15]
	v_pk_mul_f32 v[32:33], v[12:13], v[12:13]
	s_nop 0
	v_pk_mov_b32 v[34:35], v[32:33], v[30:31] op_sel:[1,0]
	v_mov_b32_e32 v33, v31
	v_pk_add_f32 v[30:31], v[34:35], v[32:33]
	v_pk_mul_f32 v[32:33], v[28:29], v[28:29]
	v_pk_mul_f32 v[34:35], v[26:27], v[26:27]
	v_mov_b32_e32 v36, v32
	v_mov_b32_e32 v37, v34
	v_mov_b32_e32 v34, v33
	v_pk_add_f32 v[32:33], v[36:37], v[34:35]
	v_add_f32_e32 v2, v30, v31
	v_add_f32_e32 v2, v2, v33
	v_lshl_add_u64 v[30:31], s[0:1], 0, v[18:19]
	v_add_f32_e32 v2, v32, v2
	global_load_dwordx4 v[30:33], v[30:31], off
	ds_bpermute_b32 v25, v1, v2
	v_lshl_add_u64 v[18:19], v[18:19], 0, s[10:11]
	s_waitcnt lgkmcnt(0)
	v_add_f32_e32 v2, v2, v25
	ds_bpermute_b32 v25, v22, v2
	s_waitcnt lgkmcnt(0)
	v_add_f32_e32 v2, v2, v25
	ds_bpermute_b32 v25, v23, v2
	s_waitcnt lgkmcnt(0)
	v_add_f32_e32 v2, v2, v25
	ds_bpermute_b32 v25, v24, v2
	s_waitcnt lgkmcnt(0)
	v_add_f32_e32 v2, v2, v25
	v_fmamk_f32 v2, v2, 0x3c000000, v241
	v_cmp_gt_f32_e32 vcc, s25, v2
	v_mul_f32_e32 v25, 0x4b800000, v2
	s_waitcnt vmcnt(0)
	v_lshlrev_b32_e32 v34, 16, v30
	v_cndmask_b32_e32 v2, v2, v25, vcc
	v_rsq_f32_e32 v2, v2
	v_and_b32_e32 v35, 0xffff0000, v30
	v_lshlrev_b32_e32 v30, 16, v31
	v_and_b32_e32 v31, 0xffff0000, v31
	v_mul_f32_e32 v25, 0x45800000, v2
	v_cndmask_b32_e32 v2, v2, v25, vcc
	v_mul_f32_e32 v25, 0xbfb8aa3b, v34
	v_exp_f32_e32 v25, v25
	v_pk_mul_f32 v[12:13], v[12:13], v[2:3] op_sel_hi:[1,0]
	v_pk_mul_f32 v[14:15], v[14:15], v[2:3] op_sel_hi:[1,0]
	v_pk_mul_f32 v[12:13], v[8:9], v[12:13]
	v_add_f32_e32 v25, 1.0, v25
	v_rcp_f32_e32 v36, v25
	v_mul_f32_e32 v25, 0xbfb8aa3b, v35
	v_exp_f32_e32 v25, v25
	v_pk_mul_f32 v[14:15], v[10:11], v[14:15]
	v_pk_mul_f32 v[26:27], v[26:27], v[2:3] op_sel_hi:[1,0]
	v_pk_mul_f32 v[28:29], v[28:29], v[2:3] op_sel_hi:[1,0]
	v_add_f32_e32 v25, 1.0, v25
	v_rcp_f32_e32 v37, v25
	v_pk_mul_f32 v[26:27], v[4:5], v[26:27]
	v_pk_mul_f32 v[28:29], v[6:7], v[28:29]
	v_pk_mul_f32 v[34:35], v[36:37], v[34:35]
	s_nop 0
	v_pk_mul_f32 v[12:13], v[34:35], v[12:13]
	s_nop 0
	v_cvt_pk_bf16_f32 v12, v12, v13
	v_mul_f32_e32 v13, 0xbfb8aa3b, v30
	v_exp_f32_e32 v13, v13
	s_nop 0
	v_add_f32_e32 v13, 1.0, v13
	v_rcp_f32_e32 v34, v13
	v_mul_f32_e32 v13, 0xbfb8aa3b, v31
	v_exp_f32_e32 v13, v13
	s_nop 0
	v_add_f32_e32 v13, 1.0, v13
	v_rcp_f32_e32 v35, v13
	s_nop 0
	v_pk_mul_f32 v[30:31], v[34:35], v[30:31]
	s_nop 0
	v_pk_mul_f32 v[14:15], v[30:31], v[14:15]
	s_nop 0
	v_cvt_pk_bf16_f32 v13, v14, v15
	v_lshlrev_b32_e32 v14, 16, v32
	v_mul_f32_e32 v25, 0xbfb8aa3b, v14
	v_exp_f32_e32 v25, v25
	v_and_b32_e32 v15, 0xffff0000, v32
	v_add_f32_e32 v25, 1.0, v25
	v_rcp_f32_e32 v30, v25
	v_mul_f32_e32 v25, 0xbfb8aa3b, v15
	v_exp_f32_e32 v25, v25
	s_nop 0
	v_add_f32_e32 v25, 1.0, v25
	v_rcp_f32_e32 v31, v25
	s_nop 0
	v_pk_mul_f32 v[14:15], v[30:31], v[14:15]
	s_nop 0
	v_pk_mul_f32 v[14:15], v[14:15], v[26:27]
	v_lshlrev_b32_e32 v26, 16, v33
	v_and_b32_e32 v27, 0xffff0000, v33
	v_cvt_pk_bf16_f32 v14, v14, v15
	v_mul_f32_e32 v15, 0xbfb8aa3b, v26
	v_mul_f32_e32 v2, 0xbfb8aa3b, v27
	v_exp_f32_e32 v15, v15
	v_exp_f32_e32 v2, v2
	v_add_f32_e32 v15, 1.0, v15
	v_add_f32_e32 v2, 1.0, v2
	v_rcp_f32_e32 v30, v15
	v_rcp_f32_e32 v31, v2
	s_nop 0
	v_pk_mul_f32 v[26:27], v[30:31], v[26:27]
	s_nop 0
	v_pk_mul_f32 v[26:27], v[26:27], v[28:29]
	s_nop 0
	v_cvt_pk_bf16_f32 v15, v26, v27
	v_lshl_add_u64 v[26:27], s[0:1], 0, v[16:17]
	v_lshl_add_u64 v[16:17], v[16:17], 0, s[8:9]
	global_store_dwordx4 v[26:27], v[12:15], off
	s_cbranch_scc1 .LBB0_1388
	s_branch .LBB0_1390

.LBB0_1469:
	v_readlane_b32 s20, v253, 17
	s_lshl_b32 s60, s1, 11
	v_lshl_add_u32 v178, s0, 8, v1
	v_readlane_b32 s21, v253, 18
	v_readlane_b32 s22, v253, 19
	v_readlane_b32 s23, v253, 20
	s_cmp_lg_u32 s1, 3
	v_mov_b64_e32 v[34:35], s[6:7]
	s_movk_i32 s24, 0x7200
	v_lshl_or_b32 v4, s18, 8, v211
	s_mov_b32 s61, s21
	s_cselect_b64 s[18:19], -1, 0
	s_cmp_eq_u32 s1, 3
	v_mad_i64_i32 v[30:31], s[22:23], v178, s24, v[34:35]
	v_ashrrev_i32_e32 v5, 31, v4
	s_cselect_b64 s[0:1], -1, 0
	v_lshl_add_u64 v[30:31], v[30:31], 0, s[60:61]
	s_and_b64 s[0:1], s[0:1], exec
	v_lshl_add_u64 v[30:31], v[30:31], 0, v[4:5]
	s_mov_b64 s[56:57], 0x3200
	s_movk_i32 s11, 0x3000
	s_cselect_b32 s20, 0, 0x800
	v_lshl_add_u64 v[36:37], v[30:31], 0, s[56:57]
	v_add_co_u32_e32 v30, vcc, s11, v30
	v_lshl_add_u64 v[62:63], v[36:37], 0, s[20:21]
	s_nop 0
	v_addc_co_u32_e32 v31, vcc, 0, v31, vcc
	v_or_b32_e32 v200, 16, v178
	global_load_dwordx2 v[32:33], v[30:31], off offset:512
	s_nop 0
	global_load_dwordx2 v[30:31], v[62:63], off
	global_load_dwordx2 v[68:69], v[36:37], off offset:128
	global_load_dwordx2 v[66:67], v[62:63], off offset:128
	v_mad_i64_i32 v[36:37], s[22:23], v200, s24, v[34:35]
	v_lshl_add_u64 v[36:37], v[36:37], 0, s[60:61]
	v_lshl_add_u64 v[36:37], v[36:37], 0, v[4:5]
	v_lshl_add_u64 v[94:95], v[36:37], 0, s[56:57]
	v_add_co_u32_e32 v36, vcc, s11, v36
	v_or_b32_e32 v198, 32, v178
	s_nop 0
	v_addc_co_u32_e32 v37, vcc, 0, v37, vcc
	global_load_dwordx2 v[64:65], v[36:37], off offset:512
	v_lshl_add_u64 v[36:37], v[94:95], 0, s[20:21]
	global_load_dwordx2 v[62:63], v[36:37], off
	global_load_dwordx2 v[100:101], v[94:95], off offset:128
	global_load_dwordx2 v[98:99], v[36:37], off offset:128
	v_mad_i64_i32 v[36:37], s[22:23], v198, s24, v[34:35]
	v_lshl_add_u64 v[36:37], v[36:37], 0, s[60:61]
	v_lshl_add_u64 v[36:37], v[36:37], 0, v[4:5]
	v_or_b32_e32 v196, 48, v178
	v_lshl_add_u64 v[126:127], v[36:37], 0, s[56:57]
	v_add_co_u32_e32 v36, vcc, s11, v36
	v_mad_i64_i32 v[34:35], s[22:23], v196, s24, v[34:35]
	s_nop 0
	v_addc_co_u32_e32 v37, vcc, 0, v37, vcc
	v_lshl_add_u64 v[34:35], v[34:35], 0, s[60:61]
	global_load_dwordx2 v[96:97], v[36:37], off offset:512
	v_lshl_add_u64 v[36:37], v[126:127], 0, s[20:21]
	v_lshl_add_u64 v[34:35], v[34:35], 0, v[4:5]
	global_load_dwordx2 v[94:95], v[36:37], off
	global_load_dwordx2 v[132:133], v[126:127], off offset:128
	global_load_dwordx2 v[130:131], v[36:37], off offset:128
	v_lshl_add_u64 v[36:37], v[34:35], 0, s[56:57]
	v_add_co_u32_e32 v34, vcc, s11, v34
	s_mov_b64 s[64:65], s[60:61]
	s_nop 0
	v_addc_co_u32_e32 v35, vcc, 0, v35, vcc
	global_load_dwordx2 v[128:129], v[34:35], off offset:512
	v_lshl_add_u64 v[34:35], v[36:37], 0, s[20:21]
	global_load_dwordx2 v[126:127], v[34:35], off
	global_load_dwordx2 v[194:195], v[36:37], off offset:128
	global_load_dwordx2 v[180:181], v[34:35], off offset:128
	v_writelane_b32 v253, s64, 17
	s_mov_b64 s[22:23], -1
	s_mov_b64 vcc, s[0:1]
	v_writelane_b32 v253, s65, 18
	v_writelane_b32 v253, s66, 19
	v_writelane_b32 v253, s67, 20
	s_mov_b32 s25, 0x800000
	s_waitcnt vmcnt(0) lgkmcnt(0)
	v_cvt_f32_ubyte1_e32 v205, v32
	v_cvt_f32_ubyte0_e32 v204, v32
	v_cvt_f32_ubyte3_e32 v203, v32
	v_cvt_f32_ubyte2_e32 v202, v32
	s_cbranch_vccnz .LBB0_1471
	v_cvt_f32_ubyte0_e32 v2, v30
	v_rcp_iflag_f32_e32 v34, v2
	v_cvt_f32_ubyte1_e32 v2, v30
	v_rcp_iflag_f32_e32 v35, v2
	v_cvt_f32_ubyte2_e32 v2, v30
	v_rcp_iflag_f32_e32 v182, v2
	v_cvt_f32_ubyte3_e32 v2, v30
	v_rcp_iflag_f32_e32 v183, v2
	v_pk_mul_f32 v[36:37], v[34:35], v[204:205]
	s_mov_b64 s[22:23], 0
	v_pk_mul_f32 v[34:35], v[182:183], v[202:203]

.LBB0_1479:
	v_ashrrev_i32_e32 v179, 31, v178
	v_lshlrev_b64 v[182:183], 12, v[178:179]
	v_lshl_add_u64 v[182:183], s[4:5], 0, v[182:183]
	s_andn2_b64 vcc, exec, s[0:1]
	v_lshl_add_u64 v[202:203], v[4:5], 1, v[182:183]
	s_cbranch_vccnz .LBB0_1481
	v_cvt_pk_bf16_f32 v30, v30, v31
	v_cvt_pk_bf16_f32 v31, v32, v33
	v_cvt_pk_bf16_f32 v32, v34, v35
	v_cvt_pk_bf16_f32 v33, v36, v37
	global_store_dwordx4 v[202:203], v[30:33], off
	v_mov_b64_e32 v[34:35], v[46:47]
	v_mov_b64_e32 v[36:37], v[48:49]
	v_mov_b64_e32 v[30:31], v[58:59]
	v_mov_b64_e32 v[32:33], v[60:61]

.LBB0_1491:
	s_andn2_b64 vcc, exec, s[0:1]
	s_cbranch_vccnz .LBB0_1493
	v_cvt_pk_bf16_f32 v46, v46, v47
	v_cvt_pk_bf16_f32 v47, v48, v49
	v_cvt_pk_bf16_f32 v48, v58, v59
	v_cvt_pk_bf16_f32 v49, v60, v61
	global_store_dwordx4 v[202:203], v[46:49], off offset:256
	v_mov_b64_e32 v[58:59], v[158:159]
	v_mov_b64_e32 v[60:61], v[160:161]
	v_mov_b64_e32 v[46:47], v[162:163]
	v_mov_b64_e32 v[48:49], v[164:165]

.LBB0_1503:
	v_ashrrev_i32_e32 v201, 31, v200
	v_lshlrev_b64 v[158:159], 12, v[200:201]
	v_lshl_add_u64 v[158:159], s[4:5], 0, v[158:159]
	s_andn2_b64 vcc, exec, s[0:1]
	v_lshl_add_u64 v[158:159], v[4:5], 1, v[158:159]
	s_cbranch_vccnz .LBB0_1505
	v_cvt_pk_bf16_f32 v62, v62, v63
	v_cvt_pk_bf16_f32 v63, v64, v65
	v_cvt_pk_bf16_f32 v64, v66, v67
	v_cvt_pk_bf16_f32 v65, v68, v69
	global_store_dwordx4 v[158:159], v[62:65], off
	v_mov_b64_e32 v[66:67], v[78:79]
	v_mov_b64_e32 v[68:69], v[80:81]
	v_mov_b64_e32 v[62:63], v[86:87]
	v_mov_b64_e32 v[64:65], v[88:89]

.LBB0_1515:
	s_andn2_b64 vcc, exec, s[0:1]
	s_cbranch_vccnz .LBB0_1517
	v_cvt_pk_bf16_f32 v78, v78, v79
	v_cvt_pk_bf16_f32 v79, v80, v81
	v_cvt_pk_bf16_f32 v80, v86, v87
	v_cvt_pk_bf16_f32 v81, v88, v89
	global_store_dwordx4 v[158:159], v[78:81], off offset:256
	v_mov_b64_e32 v[86:87], v[150:151]
	v_mov_b64_e32 v[88:89], v[152:153]
	v_mov_b64_e32 v[78:79], v[154:155]
	v_mov_b64_e32 v[80:81], v[156:157]

.LBB0_1527:
	v_ashrrev_i32_e32 v199, 31, v198
	v_lshlrev_b64 v[150:151], 12, v[198:199]
	v_lshl_add_u64 v[150:151], s[4:5], 0, v[150:151]
	s_andn2_b64 vcc, exec, s[0:1]
	v_lshl_add_u64 v[150:151], v[4:5], 1, v[150:151]
	s_cbranch_vccnz .LBB0_1529
	v_cvt_pk_bf16_f32 v94, v94, v95
	v_cvt_pk_bf16_f32 v95, v96, v97
	v_cvt_pk_bf16_f32 v96, v98, v99
	v_cvt_pk_bf16_f32 v97, v100, v101
	global_store_dwordx4 v[150:151], v[94:97], off
	v_mov_b64_e32 v[98:99], v[110:111]
	v_mov_b64_e32 v[100:101], v[112:113]
	v_mov_b64_e32 v[94:95], v[114:115]
	v_mov_b64_e32 v[96:97], v[116:117]

.LBB0_1539:
	s_andn2_b64 vcc, exec, s[0:1]
	s_cbranch_vccnz .LBB0_1541
	v_cvt_pk_bf16_f32 v110, v110, v111
	v_cvt_pk_bf16_f32 v111, v112, v113
	v_cvt_pk_bf16_f32 v112, v114, v115
	v_cvt_pk_bf16_f32 v113, v116, v117
	global_store_dwordx4 v[150:151], v[110:113], off offset:256
	v_mov_b64_e32 v[114:115], v[142:143]
	v_mov_b64_e32 v[116:117], v[144:145]
	v_mov_b64_e32 v[110:111], v[146:147]
	v_mov_b64_e32 v[112:113], v[148:149]

.LBB0_1551:
	v_ashrrev_i32_e32 v197, 31, v196
	v_lshlrev_b64 v[142:143], 12, v[196:197]
	v_lshl_add_u64 v[142:143], s[4:5], 0, v[142:143]
	s_andn2_b64 vcc, exec, s[0:1]
	v_lshl_add_u64 v[142:143], v[4:5], 1, v[142:143]
	s_cbranch_vccnz .LBB0_1553
	v_cvt_pk_bf16_f32 v126, v126, v127
	v_cvt_pk_bf16_f32 v127, v128, v129
	v_cvt_pk_bf16_f32 v128, v130, v131
	v_cvt_pk_bf16_f32 v129, v132, v133
	global_store_dwordx4 v[142:143], v[126:129], off
	v_mov_b64_e32 v[130:131], v[134:135]
	v_mov_b64_e32 v[132:133], v[136:137]
	v_mov_b64_e32 v[126:127], v[138:139]
	v_mov_b64_e32 v[128:129], v[140:141]

.LBB0_1563:
	s_andn2_b64 vcc, exec, s[0:1]
	s_cbranch_vccnz .LBB0_1565
	v_cvt_pk_bf16_f32 v134, v134, v135
	v_cvt_pk_bf16_f32 v135, v136, v137
	v_cvt_pk_bf16_f32 v136, v138, v139
	v_cvt_pk_bf16_f32 v137, v140, v141
	global_store_dwordx4 v[142:143], v[134:137], off offset:256
	v_mov_b64_e32 v[140:141], v[120:121]
	v_mov_b64_e32 v[138:139], v[118:119]
	v_mov_b64_e32 v[136:137], v[124:125]
	v_mov_b64_e32 v[134:135], v[122:123]
.LBB0_1565:
	v_add_u32_e32 v200, 0x80, v178
	v_mov_b64_e32 v[122:123], s[6:7]
	v_readlane_b32 s56, v253, 17
	v_mad_i64_i32 v[118:119], s[0:1], v200, s24, v[122:123]
	v_readlane_b32 s57, v253, 18
	s_mov_b64 s[22:23], 0x3200
	v_add_u32_e32 v198, 0x90, v178
	v_lshl_add_u64 v[118:119], v[118:119], 0, s[56:57]
	v_lshl_add_u64 v[118:119], v[118:119], 0, v[4:5]
	v_lshl_add_u64 v[124:125], v[118:119], 0, s[22:23]
	v_add_co_u32_e32 v118, vcc, 0x3000, v118
	v_lshl_add_u64 v[142:143], v[124:125], 0, s[20:21]
	s_nop 0
	v_addc_co_u32_e32 v119, vcc, 0, v119, vcc
	global_load_dwordx2 v[120:121], v[118:119], off offset:512
	s_nop 0
	global_load_dwordx2 v[118:119], v[142:143], off
	global_load_dwordx2 v[146:147], v[142:143], off offset:128
	global_load_dwordx2 v[148:149], v[124:125], off offset:128
	v_mad_i64_i32 v[124:125], s[0:1], v198, s24, v[122:123]
	v_lshl_add_u64 v[124:125], v[124:125], 0, s[56:57]
	v_lshl_add_u64 v[124:125], v[124:125], 0, v[4:5]
	v_lshl_add_u64 v[150:151], v[124:125], 0, s[22:23]
	v_add_co_u32_e32 v124, vcc, s11, v124
	v_add_u32_e32 v196, 0xa0, v178
	s_nop 0
	v_addc_co_u32_e32 v125, vcc, 0, v125, vcc
	v_lshl_add_u64 v[152:153], v[150:151], 0, s[20:21]
	global_load_dwordx2 v[144:145], v[124:125], off offset:512
	global_load_dwordx2 v[142:143], v[152:153], off
	global_load_dwordx2 v[154:155], v[152:153], off offset:128
	global_load_dwordx2 v[156:157], v[150:151], off offset:128
	v_mad_i64_i32 v[124:125], s[0:1], v196, s24, v[122:123]
	v_lshl_add_u64 v[124:125], v[124:125], 0, s[56:57]
	v_add_u32_e32 v194, 0xb0, v178
	v_lshl_add_u64 v[124:125], v[124:125], 0, v[4:5]
	v_mad_i64_i32 v[122:123], s[0:1], v194, s24, v[122:123]
	v_lshl_add_u64 v[158:159], v[124:125], 0, s[22:23]
	v_add_co_u32_e32 v124, vcc, s11, v124
	v_lshl_add_u64 v[122:123], v[122:123], 0, s[56:57]
	s_nop 0
	v_addc_co_u32_e32 v125, vcc, 0, v125, vcc
	v_lshl_add_u64 v[122:123], v[122:123], 0, v[4:5]
	v_lshl_add_u64 v[160:161], v[158:159], 0, s[20:21]
	global_load_dwordx2 v[152:153], v[124:125], off offset:512
	global_load_dwordx2 v[150:151], v[160:161], off
	global_load_dwordx2 v[162:163], v[160:161], off offset:128
	global_load_dwordx2 v[164:165], v[158:159], off offset:128
	v_lshl_add_u64 v[124:125], v[122:123], 0, s[22:23]
	v_add_co_u32_e32 v122, vcc, s11, v122
	v_lshl_add_u64 v[178:179], v[124:125], 0, s[20:21]
	s_nop 0
	v_addc_co_u32_e32 v123, vcc, 0, v123, vcc
	global_load_dwordx2 v[160:161], v[122:123], off offset:512
	global_load_dwordx2 v[158:159], v[178:179], off
	s_nop 0
	global_load_dwordx2 v[178:179], v[178:179], off offset:128
	s_nop 0
	global_load_dwordx2 v[180:181], v[124:125], off offset:128
	s_mov_b64 s[0:1], -1
	s_and_b64 vcc, exec, s[18:19]
	v_readlane_b32 s58, v253, 19
	v_readlane_b32 s59, v253, 20
	s_waitcnt vmcnt(0) lgkmcnt(0)
	v_cvt_f32_ubyte1_e32 v205, v120
	v_cvt_f32_ubyte0_e32 v204, v120
	v_cvt_f32_ubyte3_e32 v203, v120
	v_cvt_f32_ubyte2_e32 v202, v120
	s_cbranch_vccz .LBB0_1567
	v_cvt_f32_ubyte0_e32 v2, v118
	v_rcp_iflag_f32_e32 v122, v2
	v_cvt_f32_ubyte1_e32 v2, v118
	v_rcp_iflag_f32_e32 v123, v2
	v_cvt_f32_ubyte2_e32 v2, v118
	v_rcp_iflag_f32_e32 v182, v2
	v_cvt_f32_ubyte3_e32 v2, v118
	v_rcp_iflag_f32_e32 v183, v2
	v_pk_mul_f32 v[124:125], v[122:123], v[204:205]
	s_mov_b64 s[0:1], 0
	v_pk_mul_f32 v[122:123], v[182:183], v[202:203]

.LBB0_1575:
	v_ashrrev_i32_e32 v201, 31, v200
	v_lshlrev_b64 v[182:183], 12, v[200:201]
	v_lshl_add_u64 v[182:183], s[4:5], 0, v[182:183]
	s_andn2_b64 vcc, exec, s[0:1]
	v_lshl_add_u64 v[200:201], v[4:5], 1, v[182:183]
	s_cbranch_vccnz .LBB0_1577
	v_cvt_pk_bf16_f32 v118, v118, v119
	v_cvt_pk_bf16_f32 v119, v120, v121
	v_cvt_pk_bf16_f32 v120, v122, v123
	v_cvt_pk_bf16_f32 v121, v124, v125
	global_store_dwordx4 v[200:201], v[118:121], off
	v_mov_b64_e32 v[124:125], v[104:105]
	v_mov_b64_e32 v[122:123], v[102:103]
	v_mov_b64_e32 v[120:121], v[108:109]
	v_mov_b64_e32 v[118:119], v[106:107]

.LBB0_1587:
	s_andn2_b64 vcc, exec, s[0:1]
	s_cbranch_vccnz .LBB0_1589
	v_cvt_pk_bf16_f32 v102, v102, v103
	v_cvt_pk_bf16_f32 v103, v104, v105
	v_cvt_pk_bf16_f32 v104, v106, v107
	v_cvt_pk_bf16_f32 v105, v108, v109
	global_store_dwordx4 v[200:201], v[102:105], off offset:256
	v_mov_b64_e32 v[108:109], v[84:85]
	v_mov_b64_e32 v[106:107], v[82:83]
	v_mov_b64_e32 v[104:105], v[92:93]
	v_mov_b64_e32 v[102:103], v[90:91]

.LBB0_1599:
	v_ashrrev_i32_e32 v199, 31, v198
	v_lshlrev_b64 v[82:83], 12, v[198:199]
	v_lshl_add_u64 v[82:83], s[4:5], 0, v[82:83]
	s_andn2_b64 vcc, exec, s[0:1]
	v_lshl_add_u64 v[82:83], v[4:5], 1, v[82:83]
	s_cbranch_vccnz .LBB0_1601
	v_cvt_pk_bf16_f32 v90, v142, v143
	v_cvt_pk_bf16_f32 v91, v144, v145
	v_cvt_pk_bf16_f32 v92, v146, v147
	v_cvt_pk_bf16_f32 v93, v148, v149
	v_mov_b64_e32 v[148:149], v[72:73]
	v_mov_b64_e32 v[144:145], v[76:77]
	v_mov_b64_e32 v[146:147], v[70:71]
	v_mov_b64_e32 v[142:143], v[74:75]
	global_store_dwordx4 v[82:83], v[90:93], off

.LBB0_1611:
	s_andn2_b64 vcc, exec, s[0:1]
	s_cbranch_vccnz .LBB0_1613
	v_cvt_pk_bf16_f32 v70, v70, v71
	v_cvt_pk_bf16_f32 v71, v72, v73
	v_cvt_pk_bf16_f32 v72, v74, v75
	v_cvt_pk_bf16_f32 v73, v76, v77
	global_store_dwordx4 v[82:83], v[70:73], off offset:256
	v_mov_b64_e32 v[76:77], v[52:53]
	v_mov_b64_e32 v[74:75], v[50:51]
	v_mov_b64_e32 v[72:73], v[56:57]
	v_mov_b64_e32 v[70:71], v[54:55]

.LBB0_1623:
	v_ashrrev_i32_e32 v197, 31, v196
	v_lshlrev_b64 v[50:51], 12, v[196:197]
	v_lshl_add_u64 v[50:51], s[4:5], 0, v[50:51]
	s_andn2_b64 vcc, exec, s[0:1]
	v_lshl_add_u64 v[50:51], v[4:5], 1, v[50:51]
	s_cbranch_vccnz .LBB0_1625
	v_cvt_pk_bf16_f32 v52, v150, v151
	v_cvt_pk_bf16_f32 v53, v152, v153
	v_cvt_pk_bf16_f32 v54, v154, v155
	v_cvt_pk_bf16_f32 v55, v156, v157
	v_mov_b64_e32 v[156:157], v[40:41]
	v_mov_b64_e32 v[152:153], v[44:45]
	v_mov_b64_e32 v[154:155], v[38:39]
	v_mov_b64_e32 v[150:151], v[42:43]
	global_store_dwordx4 v[50:51], v[52:55], off

.LBB0_1635:
	s_andn2_b64 vcc, exec, s[0:1]
	s_cbranch_vccnz .LBB0_1637
	v_cvt_pk_bf16_f32 v38, v38, v39
	v_cvt_pk_bf16_f32 v39, v40, v41
	v_cvt_pk_bf16_f32 v40, v42, v43
	v_cvt_pk_bf16_f32 v41, v44, v45
	global_store_dwordx4 v[50:51], v[38:41], off offset:256
	v_mov_b64_e32 v[44:45], v[24:25]
	v_mov_b64_e32 v[42:43], v[22:23]
	v_mov_b64_e32 v[40:41], v[28:29]
	v_mov_b64_e32 v[38:39], v[26:27]

.LBB0_1647:
	v_ashrrev_i32_e32 v195, 31, v194
	v_lshlrev_b64 v[22:23], 12, v[194:195]
	v_lshl_add_u64 v[22:23], s[4:5], 0, v[22:23]
	s_andn2_b64 vcc, exec, s[0:1]
	v_lshl_add_u64 v[4:5], v[4:5], 1, v[22:23]
	s_cbranch_vccnz .LBB0_1649
	v_cvt_pk_bf16_f32 v22, v158, v159
	v_cvt_pk_bf16_f32 v23, v160, v161
	v_cvt_pk_bf16_f32 v24, v162, v163
	v_cvt_pk_bf16_f32 v25, v164, v165
	v_mov_b64_e32 v[164:165], v[16:17]
	v_mov_b64_e32 v[160:161], v[20:21]
	v_mov_b64_e32 v[162:163], v[14:15]
	v_mov_b64_e32 v[158:159], v[18:19]
	global_store_dwordx4 v[4:5], v[22:25], off

.LBB0_1661:
	v_cvt_pk_bf16_f32 v14, v14, v15
	v_cvt_pk_bf16_f32 v15, v16, v17
	v_cvt_pk_bf16_f32 v16, v18, v19
	v_cvt_pk_bf16_f32 v17, v20, v21
	global_store_dwordx4 v[4:5], v[14:17], off offset:256
	v_mov_b64_e32 v[20:21], v[8:9]
	v_mov_b64_e32 v[18:19], v[6:7]
	v_mov_b64_e32 v[16:17], v[12:13]
	v_mov_b64_e32 v[14:15], v[10:11]
	s_andn2_b64 vcc, exec, s[36:37]
	s_mov_b64 s[0:1], -1
	s_cbranch_vccnz .LBB0_1458

.LBB0_1744:
	v_lshl_or_b32 v166, s16, 8, v179
	v_lshl_add_u32 v170, s18, 8, v1
	v_ashrrev_i32_e32 v167, 31, v166
	v_lshlrev_b64 v[190:191], 1, v[166:167]
	v_ashrrev_i32_e32 v171, 31, v170
	v_lshl_add_u64 v[168:169], s[2:3], 0, v[190:191]
	v_lshlrev_b64 v[192:193], 12, v[170:171]
	v_lshl_add_u64 v[116:117], v[168:169], 0, v[192:193]
	global_load_dwordx4 v[182:185], v[116:117], off
	global_load_dwordx4 v[186:189], v[116:117], off offset:256
	v_or_b32_e32 v176, 16, v170
	v_ashrrev_i32_e32 v177, 31, v176
	v_lshlrev_b64 v[116:117], 12, v[176:177]
	v_or_b32_e32 v174, 32, v170
	v_lshl_add_u64 v[116:117], v[168:169], 0, v[116:117]
	v_ashrrev_i32_e32 v175, 31, v174
	global_load_dwordx4 v[152:155], v[116:117], off
	global_load_dwordx4 v[148:151], v[116:117], off offset:256
	v_lshlrev_b64 v[116:117], 12, v[174:175]
	v_or_b32_e32 v172, 48, v170
	v_lshl_add_u64 v[116:117], v[168:169], 0, v[116:117]
	v_ashrrev_i32_e32 v173, 31, v172
	global_load_dwordx4 v[136:139], v[116:117], off
	global_load_dwordx4 v[124:127], v[116:117], off offset:256
	v_lshlrev_b64 v[116:117], 12, v[172:173]
	v_lshl_add_u64 v[116:117], v[168:169], 0, v[116:117]
	global_load_dwordx4 v[120:123], v[116:117], off
	s_nop 0
	global_load_dwordx4 v[116:119], v[116:117], off offset:256
	v_lshl_add_u64 v[192:193], s[2:3], 0, v[192:193]
	v_lshl_add_u64 v[190:191], v[192:193], 0, v[190:191]
	s_lshl_b32 s16, s16, 2
	s_ashr_i32 s17, s16, 31
	s_waitcnt vmcnt(0) lgkmcnt(0)
	v_lshlrev_b32_e32 v194, 16, v182
	v_and_b32_e32 v195, 0xffff0000, v182
	v_lshlrev_b32_e32 v182, 16, v183
	v_and_b32_e32 v183, 0xffff0000, v183
	v_pk_add_f32 v[146:147], v[146:147], v[182:183]
	v_lshlrev_b32_e32 v182, 16, v184
	v_and_b32_e32 v183, 0xffff0000, v184
	v_lshlrev_b32_e32 v184, 16, v185
	v_and_b32_e32 v185, 0xffff0000, v185
	v_pk_add_f32 v[144:145], v[144:145], v[194:195]
	v_pk_add_f32 v[184:185], v[142:143], v[184:185]
	v_pk_add_f32 v[182:183], v[140:141], v[182:183]
	v_cvt_pk_bf16_f32 v140, v144, v145
	v_cvt_pk_bf16_f32 v141, v146, v147
	v_cvt_pk_bf16_f32 v142, v182, v183
	v_cvt_pk_bf16_f32 v143, v184, v185
	global_store_dwordx4 v[190:191], v[140:143], off
	s_nop 1
	v_mul_f32_e32 v140, v145, v145
	v_mul_f32_e32 v141, v147, v147
	v_fmac_f32_e32 v140, v144, v144
	v_fmac_f32_e32 v141, v146, v146
	v_add_f32_e32 v140, v140, v141
	v_mul_f32_e32 v141, v183, v183
	v_mul_f32_e32 v142, v185, v185
	v_fmac_f32_e32 v141, v182, v182
	v_fmac_f32_e32 v142, v184, v184
	v_add_f32_e32 v141, v141, v142
	v_add_f32_e32 v144, v140, v141
	v_lshlrev_b32_e32 v140, 16, v186
	v_and_b32_e32 v141, 0xffff0000, v186
	v_lshlrev_b32_e32 v142, 16, v187
	v_and_b32_e32 v143, 0xffff0000, v187
	v_pk_add_f32 v[134:135], v[134:135], v[142:143]
	v_pk_add_f32 v[132:133], v[132:133], v[140:141]
	v_lshlrev_b32_e32 v140, 16, v188
	v_and_b32_e32 v141, 0xffff0000, v188
	v_lshlrev_b32_e32 v142, 16, v189
	v_and_b32_e32 v143, 0xffff0000, v189
	v_pk_add_f32 v[142:143], v[130:131], v[142:143]
	v_pk_add_f32 v[140:141], v[128:129], v[140:141]
	v_cvt_pk_bf16_f32 v128, v132, v133
	v_cvt_pk_bf16_f32 v129, v134, v135
	v_cvt_pk_bf16_f32 v130, v140, v141
	v_cvt_pk_bf16_f32 v131, v142, v143
	global_store_dwordx4 v[190:191], v[128:131], off offset:256
	s_nop 1
	v_mul_f32_e32 v128, v133, v133
	v_mul_f32_e32 v129, v135, v135
	v_fmac_f32_e32 v128, v132, v132
	v_fmac_f32_e32 v129, v134, v134
	v_add_f32_e32 v128, v128, v129
	v_mul_f32_e32 v129, v141, v141
	v_mul_f32_e32 v130, v143, v143
	v_fmac_f32_e32 v129, v140, v140
	v_fmac_f32_e32 v130, v142, v142
	v_add_f32_e32 v129, v129, v130
	v_add_f32_e32 v128, v128, v129
	v_add_f32_e32 v129, v144, v128
	v_xor_b32_e32 v128, 16, v230
	v_cmp_lt_i32_e32 vcc, v128, v231
	s_nop 1
	v_cndmask_b32_e32 v128, v230, v128, vcc
	v_lshlrev_b32_e32 v128, 2, v128
	ds_bpermute_b32 v130, v128, v129
	s_waitcnt lgkmcnt(0)
	v_add_f32_e32 v130, v129, v130
	v_xor_b32_e32 v129, 32, v230
	v_cmp_lt_i32_e32 vcc, v129, v231
	s_nop 1
	v_cndmask_b32_e32 v129, v230, v129, vcc
	v_lshlrev_b32_e32 v129, 2, v129
	ds_bpermute_b32 v131, v129, v130
	s_and_saveexec_b64 s[18:19], s[36:37]
	s_mov_b32 s25, 0x800000
	s_movk_i32 s24, 0x7200
	s_cbranch_execz .LBB0_1746
	v_readlane_b32 s20, v253, 17
	v_readlane_b32 s21, v253, 18
	s_mov_b32 s9, s21
	v_lshlrev_b64 v[132:133], 7, v[170:171]
	v_readlane_b32 s22, v253, 19
	v_readlane_b32 s23, v253, 20
	v_writelane_b32 v253, s8, 17
	v_lshl_add_u64 v[132:133], s[4:5], 0, v[132:133]
	v_lshl_add_u64 v[132:133], s[16:17], 2, v[132:133]
	v_writelane_b32 v253, s9, 18
	s_lshl_b32 s20, s47, 2
	v_writelane_b32 v253, s10, 19
	v_writelane_b32 v253, s11, 20
	v_lshl_add_u64 v[132:133], v[132:133], 0, s[20:21]
	s_waitcnt lgkmcnt(0)
	v_add_f32_e32 v130, v130, v131
	global_store_dword v[132:133], v130, off
.LBB0_1746:
	s_or_b64 exec, exec, s[18:19]
	v_lshlrev_b32_e32 v132, 16, v152
	v_and_b32_e32 v133, 0xffff0000, v152
	v_lshlrev_b32_e32 v134, 16, v153
	v_and_b32_e32 v135, 0xffff0000, v153
	v_pk_add_f32 v[112:113], v[112:113], v[132:133]
	v_lshlrev_b32_e32 v132, 16, v154
	v_and_b32_e32 v133, 0xffff0000, v154
	v_pk_add_f32 v[114:115], v[114:115], v[134:135]
	v_pk_add_f32 v[132:133], v[108:109], v[132:133]
	v_cvt_pk_bf16_f32 v108, v112, v113
	v_mul_f32_e32 v113, v113, v113
	v_lshlrev_b32_e32 v134, 16, v155
	v_and_b32_e32 v135, 0xffff0000, v155
	v_fmac_f32_e32 v113, v112, v112
	v_mul_f32_e32 v112, v115, v115
	v_pk_add_f32 v[134:135], v[110:111], v[134:135]
	v_fmac_f32_e32 v112, v114, v114
	v_cvt_pk_bf16_f32 v109, v114, v115
	v_add_f32_e32 v112, v113, v112
	v_mul_f32_e32 v113, v133, v133
	v_mul_f32_e32 v114, v135, v135
	v_fmac_f32_e32 v113, v132, v132
	v_fmac_f32_e32 v114, v134, v134
	v_add_f32_e32 v113, v113, v114
	v_cvt_pk_bf16_f32 v110, v132, v133
	v_add_f32_e32 v132, v112, v113
	v_lshlrev_b32_e32 v112, 16, v148
	v_and_b32_e32 v113, 0xffff0000, v148
	v_lshlrev_b32_e32 v114, 16, v149
	v_and_b32_e32 v115, 0xffff0000, v149
	v_pk_add_f32 v[106:107], v[106:107], v[114:115]
	v_pk_add_f32 v[104:105], v[104:105], v[112:113]
	v_lshlrev_b32_e32 v112, 16, v150
	v_and_b32_e32 v113, 0xffff0000, v150
	v_lshlrev_b32_e32 v114, 16, v151
	v_and_b32_e32 v115, 0xffff0000, v151
	v_pk_add_f32 v[112:113], v[100:101], v[112:113]
	v_mul_f32_e32 v100, v105, v105
	v_mul_f32_e32 v101, v107, v107
	v_pk_add_f32 v[114:115], v[102:103], v[114:115]
	v_fmac_f32_e32 v100, v104, v104
	v_fmac_f32_e32 v101, v106, v106
	v_add_f32_e32 v100, v100, v101
	v_mul_f32_e32 v101, v113, v113
	v_mul_f32_e32 v102, v115, v115
	v_fmac_f32_e32 v101, v112, v112
	v_fmac_f32_e32 v102, v114, v114
	v_add_f32_e32 v101, v101, v102
	v_add_f32_e32 v100, v100, v101
	v_add_f32_e32 v103, v132, v100
	ds_bpermute_b32 v132, v128, v103
	s_waitcnt lgkmcnt(0)
	v_lshlrev_b64 v[130:131], 11, v[176:177]
	v_lshl_add_u64 v[100:101], v[130:131], 1, s[2:3]
	v_lshl_add_u64 v[130:131], v[166:167], 1, v[100:101]
	v_cvt_pk_bf16_f32 v111, v134, v135
	v_add_f32_e32 v100, v103, v132
	ds_bpermute_b32 v101, v129, v100
	v_cvt_pk_bf16_f32 v102, v104, v105
	v_cvt_pk_bf16_f32 v103, v106, v107
	v_cvt_pk_bf16_f32 v104, v112, v113
	v_cvt_pk_bf16_f32 v105, v114, v115
	global_store_dwordx4 v[130:131], v[108:111], off
	global_store_dwordx4 v[130:131], v[102:105], off offset:256
	s_and_saveexec_b64 s[18:19], s[36:37]
	s_cbranch_execz .LBB0_1748
	v_readlane_b32 s20, v253, 17
	v_readlane_b32 s21, v253, 18
	s_mov_b32 s9, s21
	v_lshlrev_b64 v[102:103], 7, v[176:177]
	v_readlane_b32 s22, v253, 19
	v_readlane_b32 s23, v253, 20
	v_writelane_b32 v253, s8, 17
	v_lshl_add_u64 v[102:103], s[4:5], 0, v[102:103]
	v_lshl_add_u64 v[102:103], s[16:17], 2, v[102:103]
	v_writelane_b32 v253, s9, 18
	s_lshl_b32 s20, s47, 2
	v_writelane_b32 v253, s10, 19
	v_writelane_b32 v253, s11, 20
	v_lshl_add_u64 v[102:103], v[102:103], 0, s[20:21]
	s_waitcnt lgkmcnt(0)
	v_add_f32_e32 v100, v100, v101
	global_store_dword v[102:103], v100, off
.LBB0_1748:
	s_or_b64 exec, exec, s[18:19]
	v_lshlrev_b32_e32 v102, 16, v136
	v_and_b32_e32 v103, 0xffff0000, v136
	v_lshlrev_b32_e32 v104, 16, v137
	v_and_b32_e32 v105, 0xffff0000, v137
	v_pk_add_f32 v[96:97], v[96:97], v[102:103]
	v_lshlrev_b32_e32 v102, 16, v138
	v_and_b32_e32 v103, 0xffff0000, v138
	v_pk_add_f32 v[98:99], v[98:99], v[104:105]
	v_pk_add_f32 v[102:103], v[92:93], v[102:103]
	v_cvt_pk_bf16_f32 v92, v96, v97
	v_mul_f32_e32 v97, v97, v97
	v_lshlrev_b32_e32 v104, 16, v139
	v_and_b32_e32 v105, 0xffff0000, v139
	v_fmac_f32_e32 v97, v96, v96
	v_mul_f32_e32 v96, v99, v99
	v_pk_add_f32 v[104:105], v[94:95], v[104:105]
	v_fmac_f32_e32 v96, v98, v98
	v_cvt_pk_bf16_f32 v93, v98, v99
	v_add_f32_e32 v96, v97, v96
	v_mul_f32_e32 v97, v103, v103
	v_mul_f32_e32 v98, v105, v105
	v_fmac_f32_e32 v97, v102, v102
	v_fmac_f32_e32 v98, v104, v104
	v_add_f32_e32 v97, v97, v98
	v_cvt_pk_bf16_f32 v94, v102, v103
	v_add_f32_e32 v102, v96, v97
	v_lshlrev_b32_e32 v96, 16, v124
	v_and_b32_e32 v97, 0xffff0000, v124
	v_lshlrev_b32_e32 v98, 16, v125
	v_and_b32_e32 v99, 0xffff0000, v125
	v_pk_add_f32 v[90:91], v[90:91], v[98:99]
	v_pk_add_f32 v[88:89], v[88:89], v[96:97]
	v_lshlrev_b32_e32 v96, 16, v126
	v_and_b32_e32 v97, 0xffff0000, v126
	v_lshlrev_b32_e32 v98, 16, v127
	v_and_b32_e32 v99, 0xffff0000, v127
	v_pk_add_f32 v[96:97], v[84:85], v[96:97]
	v_mul_f32_e32 v84, v89, v89
	v_mul_f32_e32 v85, v91, v91
	v_pk_add_f32 v[98:99], v[86:87], v[98:99]
	v_fmac_f32_e32 v84, v88, v88
	v_fmac_f32_e32 v85, v90, v90
	v_add_f32_e32 v84, v84, v85
	v_mul_f32_e32 v85, v97, v97
	v_mul_f32_e32 v86, v99, v99
	v_fmac_f32_e32 v85, v96, v96
	v_fmac_f32_e32 v86, v98, v98
	v_add_f32_e32 v85, v85, v86
	v_add_f32_e32 v84, v84, v85
	v_add_f32_e32 v87, v102, v84
	ds_bpermute_b32 v102, v128, v87
	s_waitcnt lgkmcnt(0)
	v_lshlrev_b64 v[100:101], 11, v[174:175]
	v_lshl_add_u64 v[84:85], v[100:101], 1, s[2:3]
	v_lshl_add_u64 v[100:101], v[166:167], 1, v[84:85]
	v_cvt_pk_bf16_f32 v95, v104, v105
	v_add_f32_e32 v84, v87, v102
	ds_bpermute_b32 v85, v129, v84
	v_cvt_pk_bf16_f32 v86, v88, v89
	v_cvt_pk_bf16_f32 v87, v90, v91
	v_cvt_pk_bf16_f32 v88, v96, v97
	v_cvt_pk_bf16_f32 v89, v98, v99
	global_store_dwordx4 v[100:101], v[92:95], off
	global_store_dwordx4 v[100:101], v[86:89], off offset:256
	s_and_saveexec_b64 s[18:19], s[36:37]
	s_cbranch_execz .LBB0_1750
	v_readlane_b32 s20, v253, 17
	v_readlane_b32 s21, v253, 18
	s_mov_b32 s9, s21
	v_lshlrev_b64 v[86:87], 7, v[174:175]
	v_readlane_b32 s22, v253, 19
	v_readlane_b32 s23, v253, 20
	v_writelane_b32 v253, s8, 17
	v_lshl_add_u64 v[86:87], s[4:5], 0, v[86:87]
	v_lshl_add_u64 v[86:87], s[16:17], 2, v[86:87]
	v_writelane_b32 v253, s9, 18
	s_lshl_b32 s20, s47, 2
	v_writelane_b32 v253, s10, 19
	v_writelane_b32 v253, s11, 20
	v_lshl_add_u64 v[86:87], v[86:87], 0, s[20:21]
	s_waitcnt lgkmcnt(0)
	v_add_f32_e32 v84, v84, v85
	global_store_dword v[86:87], v84, off
.LBB0_1750:
	s_or_b64 exec, exec, s[18:19]
	v_lshlrev_b32_e32 v86, 16, v120
	v_and_b32_e32 v87, 0xffff0000, v120
	v_lshlrev_b32_e32 v88, 16, v121
	v_and_b32_e32 v89, 0xffff0000, v121
	v_pk_add_f32 v[80:81], v[80:81], v[86:87]
	v_lshlrev_b32_e32 v86, 16, v122
	v_and_b32_e32 v87, 0xffff0000, v122
	v_pk_add_f32 v[82:83], v[82:83], v[88:89]
	v_pk_add_f32 v[86:87], v[76:77], v[86:87]
	v_cvt_pk_bf16_f32 v76, v80, v81
	v_mul_f32_e32 v81, v81, v81
	v_lshlrev_b32_e32 v88, 16, v123
	v_and_b32_e32 v89, 0xffff0000, v123
	v_fmac_f32_e32 v81, v80, v80
	v_mul_f32_e32 v80, v83, v83
	v_pk_add_f32 v[88:89], v[78:79], v[88:89]
	v_fmac_f32_e32 v80, v82, v82
	v_cvt_pk_bf16_f32 v77, v82, v83
	v_add_f32_e32 v80, v81, v80
	v_mul_f32_e32 v81, v87, v87
	v_mul_f32_e32 v82, v89, v89
	v_fmac_f32_e32 v81, v86, v86
	v_fmac_f32_e32 v82, v88, v88
	v_add_f32_e32 v81, v81, v82
	v_cvt_pk_bf16_f32 v78, v86, v87
	v_add_f32_e32 v86, v80, v81
	v_lshlrev_b32_e32 v80, 16, v116
	v_and_b32_e32 v81, 0xffff0000, v116
	v_lshlrev_b32_e32 v82, 16, v117
	v_and_b32_e32 v83, 0xffff0000, v117
	v_pk_add_f32 v[74:75], v[74:75], v[82:83]
	v_pk_add_f32 v[72:73], v[72:73], v[80:81]
	v_lshlrev_b32_e32 v80, 16, v118
	v_and_b32_e32 v81, 0xffff0000, v118
	v_lshlrev_b32_e32 v82, 16, v119
	v_and_b32_e32 v83, 0xffff0000, v119
	v_pk_add_f32 v[80:81], v[68:69], v[80:81]
	v_mul_f32_e32 v68, v73, v73
	v_mul_f32_e32 v69, v75, v75
	v_pk_add_f32 v[82:83], v[70:71], v[82:83]
	v_fmac_f32_e32 v68, v72, v72
	v_fmac_f32_e32 v69, v74, v74
	v_add_f32_e32 v68, v68, v69
	v_mul_f32_e32 v69, v81, v81
	v_mul_f32_e32 v70, v83, v83
	v_fmac_f32_e32 v69, v80, v80
	v_fmac_f32_e32 v70, v82, v82
	v_add_f32_e32 v69, v69, v70
	v_add_f32_e32 v68, v68, v69
	v_add_f32_e32 v71, v86, v68
	ds_bpermute_b32 v86, v128, v71
	s_waitcnt lgkmcnt(0)
	v_lshlrev_b64 v[84:85], 11, v[172:173]
	v_lshl_add_u64 v[68:69], v[84:85], 1, s[2:3]
	v_lshl_add_u64 v[84:85], v[166:167], 1, v[68:69]
	v_cvt_pk_bf16_f32 v79, v88, v89
	v_add_f32_e32 v68, v71, v86
	ds_bpermute_b32 v69, v129, v68
	v_cvt_pk_bf16_f32 v70, v72, v73
	v_cvt_pk_bf16_f32 v71, v74, v75
	v_cvt_pk_bf16_f32 v72, v80, v81
	v_cvt_pk_bf16_f32 v73, v82, v83
	global_store_dwordx4 v[84:85], v[76:79], off
	global_store_dwordx4 v[84:85], v[70:73], off offset:256
	s_and_saveexec_b64 s[18:19], s[36:37]
	s_cbranch_execz .LBB0_1752
	v_readlane_b32 s20, v253, 17
	v_readlane_b32 s21, v253, 18
	s_mov_b32 s9, s21
	v_lshlrev_b64 v[70:71], 7, v[172:173]
	v_readlane_b32 s22, v253, 19
	v_readlane_b32 s23, v253, 20
	v_writelane_b32 v253, s8, 17
	v_lshl_add_u64 v[70:71], s[4:5], 0, v[70:71]
	v_lshl_add_u64 v[70:71], s[16:17], 2, v[70:71]
	v_writelane_b32 v253, s9, 18
	s_lshl_b32 s20, s47, 2
	v_writelane_b32 v253, s10, 19
	v_writelane_b32 v253, s11, 20
	v_lshl_add_u64 v[70:71], v[70:71], 0, s[20:21]
	s_waitcnt lgkmcnt(0)
	v_add_f32_e32 v68, v68, v69
	global_store_dword v[70:71], v68, off
.LBB0_1752:
	s_or_b64 exec, exec, s[18:19]
	v_add_u32_e32 v102, 0x80, v170
	v_ashrrev_i32_e32 v103, 31, v102
	v_lshlrev_b64 v[108:109], 12, v[102:103]
	s_waitcnt lgkmcnt(0)
	v_lshl_add_u64 v[68:69], v[168:169], 0, v[108:109]
	global_load_dwordx4 v[104:107], v[68:69], off
	global_load_dwordx4 v[92:95], v[68:69], off offset:256
	v_add_u32_e32 v100, 0x90, v170
	v_ashrrev_i32_e32 v101, 31, v100
	v_lshlrev_b64 v[68:69], 12, v[100:101]
	v_add_u32_e32 v98, 0xa0, v170
	v_lshl_add_u64 v[68:69], v[168:169], 0, v[68:69]
	v_ashrrev_i32_e32 v99, 31, v98
	global_load_dwordx4 v[88:91], v[68:69], off
	global_load_dwordx4 v[84:87], v[68:69], off offset:256
	v_lshlrev_b64 v[68:69], 12, v[98:99]
	v_add_u32_e32 v96, 0xb0, v170
	v_lshl_add_u64 v[68:69], v[168:169], 0, v[68:69]
	v_ashrrev_i32_e32 v97, 31, v96
	global_load_dwordx4 v[80:83], v[68:69], off
	global_load_dwordx4 v[76:79], v[68:69], off offset:256
	v_lshlrev_b64 v[68:69], 12, v[96:97]
	v_lshl_add_u64 v[68:69], v[168:169], 0, v[68:69]
	global_load_dwordx4 v[72:75], v[68:69], off
	s_nop 0
	global_load_dwordx4 v[68:71], v[68:69], off offset:256
	v_lshl_add_u64 v[108:109], s[2:3], 0, v[108:109]
	v_lshl_add_u64 v[108:109], v[166:167], 1, v[108:109]
	s_waitcnt vmcnt(0) lgkmcnt(0)
	v_lshlrev_b32_e32 v110, 16, v104
	v_and_b32_e32 v111, 0xffff0000, v104
	v_lshlrev_b32_e32 v104, 16, v105
	v_and_b32_e32 v105, 0xffff0000, v105
	v_pk_add_f32 v[66:67], v[66:67], v[104:105]
	v_lshlrev_b32_e32 v104, 16, v106
	v_and_b32_e32 v105, 0xffff0000, v106
	v_lshlrev_b32_e32 v106, 16, v107
	v_and_b32_e32 v107, 0xffff0000, v107
	v_pk_add_f32 v[64:65], v[64:65], v[110:111]
	v_pk_add_f32 v[106:107], v[62:63], v[106:107]
	v_pk_add_f32 v[104:105], v[60:61], v[104:105]
	v_cvt_pk_bf16_f32 v60, v64, v65
	v_cvt_pk_bf16_f32 v61, v66, v67
	v_cvt_pk_bf16_f32 v62, v104, v105
	v_cvt_pk_bf16_f32 v63, v106, v107
	global_store_dwordx4 v[108:109], v[60:63], off
	s_nop 1
	v_mul_f32_e32 v60, v65, v65
	v_mul_f32_e32 v61, v67, v67
	v_fmac_f32_e32 v60, v64, v64
	v_fmac_f32_e32 v61, v66, v66
	v_add_f32_e32 v60, v60, v61
	v_mul_f32_e32 v61, v105, v105
	v_mul_f32_e32 v62, v107, v107
	v_fmac_f32_e32 v61, v104, v104
	v_fmac_f32_e32 v62, v106, v106
	v_add_f32_e32 v61, v61, v62
	v_add_f32_e32 v64, v60, v61
	v_lshlrev_b32_e32 v60, 16, v92
	v_and_b32_e32 v61, 0xffff0000, v92
	v_lshlrev_b32_e32 v62, 16, v93
	v_and_b32_e32 v63, 0xffff0000, v93
	v_pk_add_f32 v[58:59], v[58:59], v[62:63]
	v_pk_add_f32 v[56:57], v[56:57], v[60:61]
	v_lshlrev_b32_e32 v60, 16, v94
	v_and_b32_e32 v61, 0xffff0000, v94
	v_lshlrev_b32_e32 v62, 16, v95
	v_and_b32_e32 v63, 0xffff0000, v95
	v_pk_add_f32 v[62:63], v[54:55], v[62:63]
	v_pk_add_f32 v[60:61], v[52:53], v[60:61]
	v_cvt_pk_bf16_f32 v52, v56, v57
	v_cvt_pk_bf16_f32 v53, v58, v59
	v_cvt_pk_bf16_f32 v54, v60, v61
	v_cvt_pk_bf16_f32 v55, v62, v63
	global_store_dwordx4 v[108:109], v[52:55], off offset:256
	s_nop 1
	v_mul_f32_e32 v52, v57, v57
	v_mul_f32_e32 v53, v59, v59
	v_fmac_f32_e32 v52, v56, v56
	v_fmac_f32_e32 v53, v58, v58
	v_add_f32_e32 v52, v52, v53
	v_mul_f32_e32 v53, v61, v61
	v_mul_f32_e32 v54, v63, v63
	v_fmac_f32_e32 v53, v60, v60
	v_fmac_f32_e32 v54, v62, v62
	v_add_f32_e32 v53, v53, v54
	v_add_f32_e32 v52, v52, v53
	v_add_f32_e32 v52, v64, v52
	ds_bpermute_b32 v53, v128, v52
	s_waitcnt lgkmcnt(0)
	v_add_f32_e32 v52, v52, v53
	ds_bpermute_b32 v53, v129, v52
	s_and_saveexec_b64 s[18:19], s[36:37]
	s_cbranch_execz .LBB0_1754
	v_readlane_b32 s20, v253, 17
	v_readlane_b32 s21, v253, 18
	s_mov_b32 s9, s21
	v_lshlrev_b64 v[54:55], 7, v[102:103]
	v_readlane_b32 s22, v253, 19
	v_readlane_b32 s23, v253, 20
	v_writelane_b32 v253, s8, 17
	v_lshl_add_u64 v[54:55], s[4:5], 0, v[54:55]
	v_lshl_add_u64 v[54:55], s[16:17], 2, v[54:55]
	v_writelane_b32 v253, s9, 18
	s_lshl_b32 s20, s47, 2
	v_writelane_b32 v253, s10, 19
	v_writelane_b32 v253, s11, 20
	v_lshl_add_u64 v[54:55], v[54:55], 0, s[20:21]
	s_waitcnt lgkmcnt(0)
	v_add_f32_e32 v52, v52, v53
	global_store_dword v[54:55], v52, off
.LBB0_1754:
	s_or_b64 exec, exec, s[18:19]
	v_lshlrev_b32_e32 v54, 16, v88
	v_and_b32_e32 v55, 0xffff0000, v88
	v_lshlrev_b32_e32 v56, 16, v89
	v_and_b32_e32 v57, 0xffff0000, v89
	v_pk_add_f32 v[48:49], v[48:49], v[54:55]
	v_lshlrev_b32_e32 v54, 16, v90
	v_and_b32_e32 v55, 0xffff0000, v90
	v_pk_add_f32 v[50:51], v[50:51], v[56:57]
	v_pk_add_f32 v[54:55], v[44:45], v[54:55]
	v_cvt_pk_bf16_f32 v44, v48, v49
	v_mul_f32_e32 v49, v49, v49
	v_lshlrev_b32_e32 v56, 16, v91
	v_and_b32_e32 v57, 0xffff0000, v91
	v_fmac_f32_e32 v49, v48, v48
	v_mul_f32_e32 v48, v51, v51
	v_pk_add_f32 v[56:57], v[46:47], v[56:57]
	v_fmac_f32_e32 v48, v50, v50
	v_cvt_pk_bf16_f32 v45, v50, v51
	v_add_f32_e32 v48, v49, v48
	v_mul_f32_e32 v49, v55, v55
	v_mul_f32_e32 v50, v57, v57
	v_fmac_f32_e32 v49, v54, v54
	v_fmac_f32_e32 v50, v56, v56
	v_add_f32_e32 v49, v49, v50
	v_cvt_pk_bf16_f32 v46, v54, v55
	v_add_f32_e32 v54, v48, v49
	v_lshlrev_b32_e32 v48, 16, v84
	v_and_b32_e32 v49, 0xffff0000, v84
	v_lshlrev_b32_e32 v50, 16, v85
	v_and_b32_e32 v51, 0xffff0000, v85
	v_pk_add_f32 v[42:43], v[42:43], v[50:51]
	v_pk_add_f32 v[40:41], v[40:41], v[48:49]
	v_lshlrev_b32_e32 v48, 16, v86
	v_and_b32_e32 v49, 0xffff0000, v86
	v_lshlrev_b32_e32 v50, 16, v87
	v_and_b32_e32 v51, 0xffff0000, v87
	v_pk_add_f32 v[48:49], v[36:37], v[48:49]
	v_mul_f32_e32 v36, v41, v41
	v_mul_f32_e32 v37, v43, v43
	v_pk_add_f32 v[50:51], v[38:39], v[50:51]
	v_fmac_f32_e32 v36, v40, v40
	v_fmac_f32_e32 v37, v42, v42
	v_add_f32_e32 v36, v36, v37
	v_mul_f32_e32 v37, v49, v49
	v_mul_f32_e32 v38, v51, v51
	v_fmac_f32_e32 v37, v48, v48
	v_fmac_f32_e32 v38, v50, v50
	v_add_f32_e32 v37, v37, v38
	v_add_f32_e32 v36, v36, v37
	v_add_f32_e32 v39, v54, v36
	ds_bpermute_b32 v54, v128, v39
	s_waitcnt lgkmcnt(0)
	v_lshlrev_b64 v[52:53], 11, v[100:101]
	v_lshl_add_u64 v[36:37], v[52:53], 1, s[2:3]
	v_lshl_add_u64 v[52:53], v[166:167], 1, v[36:37]
	v_cvt_pk_bf16_f32 v47, v56, v57
	v_add_f32_e32 v36, v39, v54
	ds_bpermute_b32 v37, v129, v36
	v_cvt_pk_bf16_f32 v38, v40, v41
	v_cvt_pk_bf16_f32 v39, v42, v43
	v_cvt_pk_bf16_f32 v40, v48, v49
	v_cvt_pk_bf16_f32 v41, v50, v51
	global_store_dwordx4 v[52:53], v[44:47], off
	global_store_dwordx4 v[52:53], v[38:41], off offset:256
	s_and_saveexec_b64 s[18:19], s[36:37]
	s_cbranch_execz .LBB0_1756
	v_readlane_b32 s20, v253, 17
	v_readlane_b32 s21, v253, 18
	s_mov_b32 s9, s21
	v_lshlrev_b64 v[38:39], 7, v[100:101]
	v_readlane_b32 s22, v253, 19
	v_readlane_b32 s23, v253, 20
	v_writelane_b32 v253, s8, 17
	v_lshl_add_u64 v[38:39], s[4:5], 0, v[38:39]
	v_lshl_add_u64 v[38:39], s[16:17], 2, v[38:39]
	v_writelane_b32 v253, s9, 18
	s_lshl_b32 s20, s47, 2
	v_writelane_b32 v253, s10, 19
	v_writelane_b32 v253, s11, 20
	v_lshl_add_u64 v[38:39], v[38:39], 0, s[20:21]
	s_waitcnt lgkmcnt(0)
	v_add_f32_e32 v36, v36, v37
	global_store_dword v[38:39], v36, off
.LBB0_1756:
	s_or_b64 exec, exec, s[18:19]
	v_lshlrev_b32_e32 v38, 16, v80
	v_and_b32_e32 v39, 0xffff0000, v80
	v_lshlrev_b32_e32 v40, 16, v81
	v_and_b32_e32 v41, 0xffff0000, v81
	v_pk_add_f32 v[32:33], v[32:33], v[38:39]
	v_lshlrev_b32_e32 v38, 16, v82
	v_and_b32_e32 v39, 0xffff0000, v82
	v_pk_add_f32 v[34:35], v[34:35], v[40:41]
	v_pk_add_f32 v[38:39], v[28:29], v[38:39]
	v_cvt_pk_bf16_f32 v28, v32, v33
	v_mul_f32_e32 v33, v33, v33
	v_lshlrev_b32_e32 v40, 16, v83
	v_and_b32_e32 v41, 0xffff0000, v83
	v_fmac_f32_e32 v33, v32, v32
	v_mul_f32_e32 v32, v35, v35
	v_pk_add_f32 v[40:41], v[30:31], v[40:41]
	v_fmac_f32_e32 v32, v34, v34
	v_cvt_pk_bf16_f32 v29, v34, v35
	v_add_f32_e32 v32, v33, v32
	v_mul_f32_e32 v33, v39, v39
	v_mul_f32_e32 v34, v41, v41
	v_fmac_f32_e32 v33, v38, v38
	v_fmac_f32_e32 v34, v40, v40
	v_add_f32_e32 v33, v33, v34
	v_cvt_pk_bf16_f32 v30, v38, v39
	v_add_f32_e32 v38, v32, v33
	v_lshlrev_b32_e32 v32, 16, v76
	v_and_b32_e32 v33, 0xffff0000, v76
	v_lshlrev_b32_e32 v34, 16, v77
	v_and_b32_e32 v35, 0xffff0000, v77
	v_pk_add_f32 v[26:27], v[26:27], v[34:35]
	v_pk_add_f32 v[24:25], v[24:25], v[32:33]
	v_lshlrev_b32_e32 v32, 16, v78
	v_and_b32_e32 v33, 0xffff0000, v78
	v_lshlrev_b32_e32 v34, 16, v79
	v_and_b32_e32 v35, 0xffff0000, v79
	v_pk_add_f32 v[32:33], v[20:21], v[32:33]
	v_mul_f32_e32 v20, v25, v25
	v_mul_f32_e32 v21, v27, v27
	v_pk_add_f32 v[34:35], v[22:23], v[34:35]
	v_fmac_f32_e32 v20, v24, v24
	v_fmac_f32_e32 v21, v26, v26
	v_add_f32_e32 v20, v20, v21
	v_mul_f32_e32 v21, v33, v33
	v_mul_f32_e32 v22, v35, v35
	v_fmac_f32_e32 v21, v32, v32
	v_fmac_f32_e32 v22, v34, v34
	v_add_f32_e32 v21, v21, v22
	v_add_f32_e32 v20, v20, v21
	v_add_f32_e32 v23, v38, v20
	ds_bpermute_b32 v38, v128, v23
	s_waitcnt lgkmcnt(0)
	v_lshlrev_b64 v[36:37], 11, v[98:99]
	v_lshl_add_u64 v[20:21], v[36:37], 1, s[2:3]
	v_lshl_add_u64 v[36:37], v[166:167], 1, v[20:21]
	v_cvt_pk_bf16_f32 v31, v40, v41
	v_add_f32_e32 v20, v23, v38
	ds_bpermute_b32 v21, v129, v20
	v_cvt_pk_bf16_f32 v22, v24, v25
	v_cvt_pk_bf16_f32 v23, v26, v27
	v_cvt_pk_bf16_f32 v24, v32, v33
	v_cvt_pk_bf16_f32 v25, v34, v35
	global_store_dwordx4 v[36:37], v[28:31], off
	global_store_dwordx4 v[36:37], v[22:25], off offset:256
	s_and_saveexec_b64 s[18:19], s[36:37]
	s_cbranch_execz .LBB0_1758
	v_readlane_b32 s20, v253, 17
	v_readlane_b32 s21, v253, 18
	s_mov_b32 s9, s21
	v_lshlrev_b64 v[22:23], 7, v[98:99]
	v_readlane_b32 s22, v253, 19
	v_readlane_b32 s23, v253, 20
	v_writelane_b32 v253, s8, 17
	v_lshl_add_u64 v[22:23], s[4:5], 0, v[22:23]
	v_lshl_add_u64 v[22:23], s[16:17], 2, v[22:23]
	v_writelane_b32 v253, s9, 18
	s_lshl_b32 s20, s47, 2
	v_writelane_b32 v253, s10, 19
	v_writelane_b32 v253, s11, 20
	v_lshl_add_u64 v[22:23], v[22:23], 0, s[20:21]
	s_waitcnt lgkmcnt(0)
	v_add_f32_e32 v20, v20, v21
	global_store_dword v[22:23], v20, off
.LBB0_1758:
	s_or_b64 exec, exec, s[18:19]
	v_lshlrev_b32_e32 v22, 16, v72
	v_and_b32_e32 v23, 0xffff0000, v72
	v_lshlrev_b32_e32 v24, 16, v73
	v_and_b32_e32 v25, 0xffff0000, v73
	v_pk_add_f32 v[16:17], v[16:17], v[22:23]
	v_lshlrev_b32_e32 v22, 16, v74
	v_and_b32_e32 v23, 0xffff0000, v74
	v_pk_add_f32 v[18:19], v[18:19], v[24:25]
	v_pk_add_f32 v[22:23], v[12:13], v[22:23]
	v_cvt_pk_bf16_f32 v12, v16, v17
	v_mul_f32_e32 v17, v17, v17
	v_lshlrev_b32_e32 v24, 16, v75
	v_and_b32_e32 v25, 0xffff0000, v75
	v_fmac_f32_e32 v17, v16, v16
	v_mul_f32_e32 v16, v19, v19
	v_pk_add_f32 v[24:25], v[14:15], v[24:25]
	v_fmac_f32_e32 v16, v18, v18
	v_cvt_pk_bf16_f32 v13, v18, v19
	v_add_f32_e32 v16, v17, v16
	v_mul_f32_e32 v17, v23, v23
	v_mul_f32_e32 v18, v25, v25
	v_fmac_f32_e32 v17, v22, v22
	v_fmac_f32_e32 v18, v24, v24
	v_add_f32_e32 v17, v17, v18
	v_cvt_pk_bf16_f32 v14, v22, v23
	v_add_f32_e32 v22, v16, v17
	v_lshlrev_b32_e32 v16, 16, v68
	v_and_b32_e32 v17, 0xffff0000, v68
	v_lshlrev_b32_e32 v18, 16, v69
	v_and_b32_e32 v19, 0xffff0000, v69
	v_pk_add_f32 v[10:11], v[10:11], v[18:19]
	v_pk_add_f32 v[8:9], v[8:9], v[16:17]
	v_lshlrev_b32_e32 v16, 16, v70
	v_and_b32_e32 v17, 0xffff0000, v70
	v_lshlrev_b32_e32 v18, 16, v71
	v_and_b32_e32 v19, 0xffff0000, v71
	v_pk_add_f32 v[16:17], v[4:5], v[16:17]
	v_mul_f32_e32 v4, v9, v9
	v_mul_f32_e32 v5, v11, v11
	v_pk_add_f32 v[18:19], v[6:7], v[18:19]
	v_fmac_f32_e32 v4, v8, v8
	v_fmac_f32_e32 v5, v10, v10
	v_add_f32_e32 v4, v4, v5
	v_mul_f32_e32 v5, v17, v17
	v_mul_f32_e32 v6, v19, v19
	v_fmac_f32_e32 v5, v16, v16
	v_fmac_f32_e32 v6, v18, v18
	v_add_f32_e32 v5, v5, v6
	v_add_f32_e32 v4, v4, v5
	v_add_f32_e32 v7, v22, v4
	ds_bpermute_b32 v22, v128, v7
	s_waitcnt lgkmcnt(0)
	v_lshlrev_b64 v[20:21], 11, v[96:97]
	v_lshl_add_u64 v[4:5], v[20:21], 1, s[2:3]
	v_lshl_add_u64 v[20:21], v[166:167], 1, v[4:5]
	v_cvt_pk_bf16_f32 v15, v24, v25
	v_add_f32_e32 v4, v7, v22
	ds_bpermute_b32 v5, v129, v4
	v_cvt_pk_bf16_f32 v6, v8, v9
	v_cvt_pk_bf16_f32 v7, v10, v11
	v_cvt_pk_bf16_f32 v8, v16, v17
	v_cvt_pk_bf16_f32 v9, v18, v19
	global_store_dwordx4 v[20:21], v[12:15], off
	global_store_dwordx4 v[20:21], v[6:9], off offset:256
	s_and_saveexec_b64 s[18:19], s[36:37]
	s_cbranch_execz .LBB0_1760
	v_readlane_b32 s20, v253, 17
	v_readlane_b32 s21, v253, 18
	s_mov_b32 s9, s21
	v_lshlrev_b64 v[6:7], 7, v[96:97]
	v_readlane_b32 s22, v253, 19
	v_readlane_b32 s23, v253, 20
	v_writelane_b32 v253, s8, 17
	v_lshl_add_u64 v[6:7], s[4:5], 0, v[6:7]
	v_lshl_add_u64 v[6:7], s[16:17], 2, v[6:7]
	v_writelane_b32 v253, s9, 18
	s_mov_b32 s17, s21
	s_lshl_b32 s16, s47, 2
	v_writelane_b32 v253, s10, 19
	v_writelane_b32 v253, s11, 20
	v_lshl_add_u64 v[6:7], v[6:7], 0, s[16:17]
	s_waitcnt lgkmcnt(0)
	v_add_f32_e32 v4, v4, v5
	global_store_dword v[6:7], v4, off

.LBB0_1825:
	v_mov_b64_e32 v[6:7], 0x57f
	v_cmp_gt_i64_e32 vcc, s[8:9], v[6:7]
	s_mov_b64 s[10:11], -1
	s_cbranch_vccnz .LBB0_1824
	s_ashr_i32 s10, s8, 31
	s_lshr_b32 s10, s10, 29
	s_add_i32 s10, s8, s10
	s_ashr_i32 s11, s10, 3
	s_and_b32 s10, s10, -8
	s_sub_i32 s10, s8, s10
	s_cmp_lt_i32 s10, 0
	s_movk_i32 s12, 0xb1
	s_cselect_b32 s12, s12, 0xb0
	s_mul_i32 s10, s12, s10
	s_add_i32 s10, s10, s11
	s_mul_hi_i32 s11, s10, 0x2e8ba2e9
	s_lshr_b32 s12, s11, 31
	s_ashr_i32 s11, s11, 5
	s_add_i32 s11, s11, s12
	s_lshl_b32 s12, s11, 3
	s_sub_i32 s14, 64, s12
	s_min_i32 s14, s14, 8
	s_abs_i32 s14, s14
	v_cvt_f32_u32_e32 v2, s14
	s_sub_i32 s15, 0, s14
	s_mulk_i32 s11, 0xb0
	s_sub_i32 s10, s10, s11
	v_rcp_iflag_f32_e32 v2, v2
	s_ashr_i32 s11, s10, 31
	s_abs_i32 s10, s10
	v_mul_f32_e32 v2, 0x4f7ffffe, v2
	v_cvt_u32_f32_e32 v2, v2
	s_nop 0
	v_readfirstlane_b32 s16, v2
	s_mul_i32 s15, s15, s16
	s_mul_hi_u32 s15, s16, s15
	s_add_i32 s16, s16, s15
	s_mul_hi_u32 s15, s10, s16
	s_mul_i32 s15, s15, s14
	s_sub_i32 s10, s10, s15
	s_sub_i32 s15, s10, s14
	s_cmp_ge_u32 s10, s14
	s_cselect_b32 s10, s15, s10
	s_sub_i32 s15, s10, s14
	s_cmp_ge_u32 s10, s14
	s_cselect_b32 s10, s15, s10
	s_xor_b32 s10, s10, s11
	s_sub_i32 s10, s10, s11
	s_add_i32 s12, s10, s12
	s_cmp_eq_u32 s12, s13
	s_cbranch_scc1 .LBB0_1823
	v_lshl_add_u32 v6, s12, 8, v9
	v_ashrrev_i32_e32 v7, 31, v6
	s_waitcnt lgkmcnt(0)
	v_lshlrev_b64 v[10:11], 7, v[6:7]
	v_lshl_add_u64 v[14:15], v[4:5], 0, v[10:11]
	global_load_dwordx4 v[10:13], v[14:15], off
	s_waitcnt vmcnt(0) lgkmcnt(0)
	v_add_f32_e32 v2, v10, v11
	v_add_f32_e32 v10, v12, v13
	v_add_f32_e32 v2, v2, v10
	global_load_dwordx4 v[10:13], v[14:15], off offset:16
	v_add_f32_e32 v2, 0, v2
	s_waitcnt vmcnt(0) lgkmcnt(0)
	v_add_f32_e32 v10, v10, v11
	v_add_f32_e32 v11, v12, v13
	v_add_f32_e32 v10, v10, v11
	v_add_f32_e32 v2, v2, v10
	global_load_dwordx4 v[10:13], v[14:15], off offset:32
	s_waitcnt vmcnt(0) lgkmcnt(0)
	v_add_f32_e32 v10, v10, v11
	v_add_f32_e32 v11, v12, v13
	v_add_f32_e32 v10, v10, v11
	v_add_f32_e32 v2, v2, v10
	global_load_dwordx4 v[10:13], v[14:15], off offset:48
	s_waitcnt vmcnt(0) lgkmcnt(0)
	v_add_f32_e32 v10, v10, v11
	v_add_f32_e32 v11, v12, v13
	v_add_f32_e32 v10, v10, v11
	v_add_f32_e32 v2, v2, v10
	v_xor_b32_e32 v10, 1, v230
	v_cmp_lt_i32_e32 vcc, v10, v231
	s_nop 1
	v_cndmask_b32_e32 v10, v230, v10, vcc
	v_lshlrev_b32_e32 v10, 2, v10
	ds_bpermute_b32 v10, v10, v2
	s_and_saveexec_b64 s[10:11], s[0:1]
	s_cbranch_execz .LBB0_1822
	s_waitcnt lgkmcnt(0)
	v_add_f32_e32 v2, v2, v10
	v_fmamk_f32 v2, v2, 0x3a000000, v241
	v_mul_f32_e32 v10, 0x4b800000, v2
	v_cmp_gt_f32_e32 vcc, s25, v2
	v_lshl_add_u64 v[6:7], v[6:7], 2, s[6:7]
	s_nop 0
	v_cndmask_b32_e32 v2, v2, v10, vcc
	v_rsq_f32_e32 v2, v2
	s_nop 0
	v_mul_f32_e32 v10, 0x45800000, v2
	v_cndmask_b32_e32 v2, v2, v10, vcc
	global_store_dword v[6:7], v2, off
	s_branch .LBB0_1822

.LBB0_1841:
	v_lshl_add_u32 v146, s20, 8, v151
	v_ashrrev_i32_e32 v147, 31, v146
	v_lshl_add_u64 v[148:149], v[146:147], 2, s[6:7]
	global_load_dword v156, v[148:149], off offset:64
	global_load_dword v152, v[148:149], off offset:128
	global_load_dword v150, v[148:149], off offset:192
	global_load_dword v160, v[148:149], off
	v_lshl_or_b32 v144, s21, 8, v154
	v_ashrrev_i32_e32 v145, 31, v144
	v_mov_b64_e32 v[142:143], s[8:9]
	s_movk_i32 s13, 0x2c00
	v_mad_i64_i32 v[158:159], s[20:21], v146, s13, v[142:143]
	v_lshlrev_b64 v[144:145], 1, v[144:145]
	v_lshl_add_u64 v[158:159], v[158:159], 0, v[144:145]
	s_andn2_b64 vcc, exec, s[36:37]
	s_waitcnt vmcnt(0) lgkmcnt(0)
	v_pk_mul_f32 v[114:115], v[114:115], v[156:157] op_sel_hi:[1,0]
	v_pk_mul_f32 v[106:107], v[106:107], v[156:157] op_sel_hi:[1,0]
	v_pk_mul_f32 v[98:99], v[98:99], v[152:153] op_sel_hi:[1,0]
	v_pk_mul_f32 v[162:163], v[126:127], v[160:161] op_sel_hi:[1,0]
	v_pk_mul_f32 v[126:127], v[124:125], v[160:161] op_sel_hi:[1,0]
	v_pk_mul_f32 v[130:131], v[130:131], v[160:161] op_sel_hi:[1,0]
	v_pk_mul_f32 v[124:125], v[128:129], v[160:161] op_sel_hi:[1,0]
	v_cvt_pk_bf16_f32 v126, v126, v127
	v_cvt_pk_bf16_f32 v124, v124, v125
	v_cvt_pk_bf16_f32 v125, v130, v131
	v_cvt_pk_bf16_f32 v127, v162, v163
	global_store_dwordx4 v[158:159], v[124:127], off
	v_pk_mul_f32 v[122:123], v[122:123], v[160:161] op_sel_hi:[1,0]
	v_pk_mul_f32 v[90:91], v[90:91], v[152:153] op_sel_hi:[1,0]
	v_pk_mul_f32 v[124:125], v[118:119], v[160:161] op_sel_hi:[1,0]
	v_pk_mul_f32 v[118:119], v[116:117], v[160:161] op_sel_hi:[1,0]
	v_pk_mul_f32 v[116:117], v[120:121], v[160:161] op_sel_hi:[1,0]
	v_cvt_pk_bf16_f32 v118, v118, v119
	v_cvt_pk_bf16_f32 v116, v116, v117
	v_cvt_pk_bf16_f32 v117, v122, v123
	v_cvt_pk_bf16_f32 v119, v124, v125
	global_store_dwordx4 v[158:159], v[116:119], off offset:256
	v_pk_mul_f32 v[82:83], v[82:83], v[150:151] op_sel_hi:[1,0]
	v_pk_mul_f32 v[74:75], v[74:75], v[150:151] op_sel_hi:[1,0]
	v_or_b32_e32 v116, 16, v146
	v_mad_i64_i32 v[116:117], s[20:21], v116, s13, v[142:143]
	v_pk_mul_f32 v[118:119], v[110:111], v[156:157] op_sel_hi:[1,0]
	v_pk_mul_f32 v[110:111], v[108:109], v[156:157] op_sel_hi:[1,0]
	v_pk_mul_f32 v[108:109], v[112:113], v[156:157] op_sel_hi:[1,0]
	v_lshl_add_u64 v[116:117], v[116:117], 0, v[144:145]
	v_cvt_pk_bf16_f32 v108, v108, v109
	v_cvt_pk_bf16_f32 v109, v114, v115
	v_cvt_pk_bf16_f32 v110, v110, v111
	v_cvt_pk_bf16_f32 v111, v118, v119
	global_store_dwordx4 v[116:117], v[108:111], off
	s_nop 1
	v_pk_mul_f32 v[108:109], v[102:103], v[156:157] op_sel_hi:[1,0]
	v_pk_mul_f32 v[102:103], v[100:101], v[156:157] op_sel_hi:[1,0]
	v_pk_mul_f32 v[100:101], v[104:105], v[156:157] op_sel_hi:[1,0]
	v_cvt_pk_bf16_f32 v102, v102, v103
	v_cvt_pk_bf16_f32 v100, v100, v101
	v_cvt_pk_bf16_f32 v101, v106, v107
	v_cvt_pk_bf16_f32 v103, v108, v109
	global_store_dwordx4 v[116:117], v[100:103], off offset:256
	s_nop 1
	v_or_b32_e32 v100, 32, v146
	v_mad_i64_i32 v[100:101], s[20:21], v100, s13, v[142:143]
	v_pk_mul_f32 v[102:103], v[94:95], v[152:153] op_sel_hi:[1,0]
	v_pk_mul_f32 v[94:95], v[92:93], v[152:153] op_sel_hi:[1,0]
	v_pk_mul_f32 v[92:93], v[96:97], v[152:153] op_sel_hi:[1,0]
	v_lshl_add_u64 v[100:101], v[100:101], 0, v[144:145]
	v_cvt_pk_bf16_f32 v92, v92, v93
	v_cvt_pk_bf16_f32 v93, v98, v99
	v_cvt_pk_bf16_f32 v94, v94, v95
	v_cvt_pk_bf16_f32 v95, v102, v103
	global_store_dwordx4 v[100:101], v[92:95], off
	s_nop 1
	v_pk_mul_f32 v[92:93], v[86:87], v[152:153] op_sel_hi:[1,0]
	v_pk_mul_f32 v[86:87], v[84:85], v[152:153] op_sel_hi:[1,0]
	v_pk_mul_f32 v[84:85], v[88:89], v[152:153] op_sel_hi:[1,0]
	v_cvt_pk_bf16_f32 v86, v86, v87
	v_cvt_pk_bf16_f32 v84, v84, v85
	v_cvt_pk_bf16_f32 v85, v90, v91
	v_cvt_pk_bf16_f32 v87, v92, v93
	global_store_dwordx4 v[100:101], v[84:87], off offset:256
	s_nop 1
	v_or_b32_e32 v84, 48, v146
	v_mad_i64_i32 v[84:85], s[20:21], v84, s13, v[142:143]
	v_pk_mul_f32 v[86:87], v[78:79], v[150:151] op_sel_hi:[1,0]
	v_pk_mul_f32 v[78:79], v[76:77], v[150:151] op_sel_hi:[1,0]
	v_pk_mul_f32 v[76:77], v[80:81], v[150:151] op_sel_hi:[1,0]
	v_lshl_add_u64 v[84:85], v[84:85], 0, v[144:145]
	v_cvt_pk_bf16_f32 v76, v76, v77
	v_cvt_pk_bf16_f32 v77, v82, v83
	v_cvt_pk_bf16_f32 v78, v78, v79
	v_cvt_pk_bf16_f32 v79, v86, v87
	global_store_dwordx4 v[84:85], v[76:79], off
	s_nop 1
	v_pk_mul_f32 v[76:77], v[70:71], v[150:151] op_sel_hi:[1,0]
	v_pk_mul_f32 v[70:71], v[68:69], v[150:151] op_sel_hi:[1,0]
	v_pk_mul_f32 v[68:69], v[72:73], v[150:151] op_sel_hi:[1,0]
	v_cvt_pk_bf16_f32 v70, v70, v71
	v_cvt_pk_bf16_f32 v68, v68, v69
	v_cvt_pk_bf16_f32 v69, v74, v75
	v_cvt_pk_bf16_f32 v71, v76, v77
	global_store_dwordx4 v[84:85], v[68:71], off offset:256
	global_load_dword v72, v[148:149], off offset:576
	s_nop 0
	global_load_dword v70, v[148:149], off offset:640
	global_load_dword v68, v[148:149], off offset:704
	global_load_dword v76, v[148:149], off offset:512
	v_add_u32_e32 v69, 0x80, v146
	v_mad_i64_i32 v[74:75], s[20:21], v69, s13, v[142:143]
	v_lshl_add_u64 v[74:75], v[74:75], 0, v[144:145]
	s_waitcnt vmcnt(0) lgkmcnt(0)
	v_pk_mul_f32 v[50:51], v[50:51], v[72:73] op_sel_hi:[1,0]
	v_pk_mul_f32 v[42:43], v[42:43], v[72:73] op_sel_hi:[1,0]
	v_pk_mul_f32 v[34:35], v[34:35], v[70:71] op_sel_hi:[1,0]
	v_pk_mul_f32 v[78:79], v[62:63], v[76:77] op_sel_hi:[1,0]
	v_pk_mul_f32 v[62:63], v[60:61], v[76:77] op_sel_hi:[1,0]
	v_pk_mul_f32 v[66:67], v[66:67], v[76:77] op_sel_hi:[1,0]
	v_pk_mul_f32 v[60:61], v[64:65], v[76:77] op_sel_hi:[1,0]
	v_cvt_pk_bf16_f32 v62, v62, v63
	v_cvt_pk_bf16_f32 v60, v60, v61
	v_cvt_pk_bf16_f32 v61, v66, v67
	v_cvt_pk_bf16_f32 v63, v78, v79
	global_store_dwordx4 v[74:75], v[60:63], off
	v_pk_mul_f32 v[58:59], v[58:59], v[76:77] op_sel_hi:[1,0]
	v_pk_mul_f32 v[26:27], v[26:27], v[70:71] op_sel_hi:[1,0]
	v_pk_mul_f32 v[60:61], v[54:55], v[76:77] op_sel_hi:[1,0]
	v_pk_mul_f32 v[54:55], v[52:53], v[76:77] op_sel_hi:[1,0]
	v_pk_mul_f32 v[52:53], v[56:57], v[76:77] op_sel_hi:[1,0]
	v_cvt_pk_bf16_f32 v54, v54, v55
	v_cvt_pk_bf16_f32 v52, v52, v53
	v_cvt_pk_bf16_f32 v53, v58, v59
	v_cvt_pk_bf16_f32 v55, v60, v61
	global_store_dwordx4 v[74:75], v[52:55], off offset:256
	v_pk_mul_f32 v[18:19], v[18:19], v[68:69] op_sel_hi:[1,0]
	v_pk_mul_f32 v[10:11], v[10:11], v[68:69] op_sel_hi:[1,0]
	v_add_u32_e32 v52, 0x90, v146
	v_mad_i64_i32 v[52:53], s[20:21], v52, s13, v[142:143]
	v_pk_mul_f32 v[54:55], v[46:47], v[72:73] op_sel_hi:[1,0]
	v_pk_mul_f32 v[46:47], v[44:45], v[72:73] op_sel_hi:[1,0]
	v_pk_mul_f32 v[44:45], v[48:49], v[72:73] op_sel_hi:[1,0]
	v_lshl_add_u64 v[52:53], v[52:53], 0, v[144:145]
	v_cvt_pk_bf16_f32 v44, v44, v45
	v_cvt_pk_bf16_f32 v45, v50, v51
	v_cvt_pk_bf16_f32 v46, v46, v47
	v_cvt_pk_bf16_f32 v47, v54, v55
	global_store_dwordx4 v[52:53], v[44:47], off
	s_nop 1
	v_pk_mul_f32 v[44:45], v[38:39], v[72:73] op_sel_hi:[1,0]
	v_pk_mul_f32 v[38:39], v[36:37], v[72:73] op_sel_hi:[1,0]
	v_pk_mul_f32 v[36:37], v[40:41], v[72:73] op_sel_hi:[1,0]
	v_cvt_pk_bf16_f32 v38, v38, v39
	v_cvt_pk_bf16_f32 v36, v36, v37
	v_cvt_pk_bf16_f32 v37, v42, v43
	v_cvt_pk_bf16_f32 v39, v44, v45
	global_store_dwordx4 v[52:53], v[36:39], off offset:256
	s_nop 1
	v_add_u32_e32 v36, 0xa0, v146
	v_mad_i64_i32 v[36:37], s[20:21], v36, s13, v[142:143]
	v_pk_mul_f32 v[38:39], v[30:31], v[70:71] op_sel_hi:[1,0]
	v_pk_mul_f32 v[30:31], v[28:29], v[70:71] op_sel_hi:[1,0]
	v_pk_mul_f32 v[28:29], v[32:33], v[70:71] op_sel_hi:[1,0]
	v_lshl_add_u64 v[36:37], v[36:37], 0, v[144:145]
	v_cvt_pk_bf16_f32 v28, v28, v29
	v_cvt_pk_bf16_f32 v29, v34, v35
	v_cvt_pk_bf16_f32 v30, v30, v31
	v_cvt_pk_bf16_f32 v31, v38, v39
	global_store_dwordx4 v[36:37], v[28:31], off
	s_nop 1
	v_pk_mul_f32 v[28:29], v[22:23], v[70:71] op_sel_hi:[1,0]
	v_pk_mul_f32 v[22:23], v[20:21], v[70:71] op_sel_hi:[1,0]
	v_pk_mul_f32 v[20:21], v[24:25], v[70:71] op_sel_hi:[1,0]
	v_cvt_pk_bf16_f32 v22, v22, v23
	v_cvt_pk_bf16_f32 v20, v20, v21
	v_cvt_pk_bf16_f32 v21, v26, v27
	v_cvt_pk_bf16_f32 v23, v28, v29
	global_store_dwordx4 v[36:37], v[20:23], off offset:256
	s_nop 1
	v_add_u32_e32 v20, 0xb0, v146
	v_mad_i64_i32 v[20:21], s[20:21], v20, s13, v[142:143]
	v_pk_mul_f32 v[22:23], v[14:15], v[68:69] op_sel_hi:[1,0]
	v_pk_mul_f32 v[14:15], v[12:13], v[68:69] op_sel_hi:[1,0]
	v_pk_mul_f32 v[12:13], v[16:17], v[68:69] op_sel_hi:[1,0]
	v_lshl_add_u64 v[20:21], v[20:21], 0, v[144:145]
	v_cvt_pk_bf16_f32 v12, v12, v13
	v_cvt_pk_bf16_f32 v13, v18, v19
	v_cvt_pk_bf16_f32 v14, v14, v15
	v_cvt_pk_bf16_f32 v15, v22, v23
	global_store_dwordx4 v[20:21], v[12:15], off
	s_mov_b64 s[20:21], -1
	s_nop 0
	v_pk_mul_f32 v[12:13], v[6:7], v[68:69] op_sel_hi:[1,0]
	v_pk_mul_f32 v[6:7], v[4:5], v[68:69] op_sel_hi:[1,0]
	v_pk_mul_f32 v[4:5], v[8:9], v[68:69] op_sel_hi:[1,0]
	v_cvt_pk_bf16_f32 v6, v6, v7
	v_cvt_pk_bf16_f32 v4, v4, v5
	v_cvt_pk_bf16_f32 v5, v10, v11
	v_cvt_pk_bf16_f32 v7, v12, v13
	global_store_dwordx4 v[20:21], v[4:7], off offset:256
	s_cbranch_vccnz .LBB0_1834
	s_andn2_b64 vcc, exec, s[0:1]
	s_cbranch_vccnz .LBB0_1833
	s_barrier
	s_branch .LBB0_1833

.LBB0_1849:
	s_lshl_b64 s[20:21], s[2:3], 13
	v_lshl_add_u64 v[8:9], v[8:9], 0, s[20:21]
	v_lshl_add_u64 v[14:15], v[2:3], 2, v[8:9]
	v_add_co_u32_e32 v10, vcc, 0x2000, v14
	global_load_dword v8, v[14:15], off
	s_nop 0
	v_addc_co_u32_e32 v11, vcc, 0, v15, vcc
	global_load_dword v9, v[10:11], off
	v_add_co_u32_e32 v10, vcc, 0x4000, v14
	s_mov_b32 s9, 0x10000
	s_nop 0
	v_addc_co_u32_e32 v11, vcc, 0, v15, vcc
	v_add_co_u32_e32 v12, vcc, 0x6000, v14
	global_load_dword v10, v[10:11], off
	s_nop 0
	v_addc_co_u32_e32 v13, vcc, 0, v15, vcc
	global_load_dword v11, v[12:13], off
	v_add_co_u32_e32 v12, vcc, 0x8000, v14
	v_ashrrev_i32_e32 v7, 31, v6
	s_nop 0
	v_addc_co_u32_e32 v13, vcc, 0, v15, vcc
	v_add_co_u32_e32 v16, vcc, 0xa000, v14
	global_load_dword v12, v[12:13], off
	s_nop 0
	v_addc_co_u32_e32 v17, vcc, 0, v15, vcc
	global_load_dword v13, v[16:17], off
	v_add_co_u32_e32 v16, vcc, 0xc000, v14
	v_lshlrev_b64 v[6:7], s8, v[6:7]
	s_nop 0
	v_addc_co_u32_e32 v17, vcc, 0, v15, vcc
	v_add_co_u32_e32 v18, vcc, 0xe000, v14
	global_load_dword v16, v[16:17], off
	s_nop 0
	v_addc_co_u32_e32 v19, vcc, 0, v15, vcc
	global_load_dword v17, v[18:19], off
	v_add_co_u32_e32 v18, vcc, s9, v14
	s_mov_b32 s9, 0x14000
	s_nop 0
	v_addc_co_u32_e32 v19, vcc, 0, v15, vcc
	v_add_co_u32_e32 v20, vcc, 0x12000, v14
	global_load_dword v18, v[18:19], off
	s_nop 0
	v_addc_co_u32_e32 v21, vcc, 0, v15, vcc
	global_load_dword v19, v[20:21], off
	v_add_co_u32_e32 v20, vcc, s9, v14
	s_mov_b32 s9, 0x18000
	s_nop 0
	v_addc_co_u32_e32 v21, vcc, 0, v15, vcc
	v_add_co_u32_e32 v22, vcc, 0x16000, v14
	global_load_dword v20, v[20:21], off
	s_nop 0
	v_addc_co_u32_e32 v23, vcc, 0, v15, vcc
	global_load_dword v21, v[22:23], off
	v_add_co_u32_e32 v22, vcc, s9, v14
	s_mov_b32 s9, 0x1c000
	s_nop 0
	v_addc_co_u32_e32 v23, vcc, 0, v15, vcc
	v_add_co_u32_e32 v24, vcc, 0x1a000, v14
	global_load_dword v22, v[22:23], off
	s_nop 0
	v_addc_co_u32_e32 v25, vcc, 0, v15, vcc
	global_load_dword v23, v[24:25], off
	v_add_co_u32_e32 v24, vcc, s9, v14
	s_mov_b32 s9, 0x30000
	s_nop 0
	v_addc_co_u32_e32 v25, vcc, 0, v15, vcc
	v_add_co_u32_e32 v26, vcc, 0x1e000, v14
	global_load_dword v24, v[24:25], off
	s_nop 0
	v_addc_co_u32_e32 v27, vcc, 0, v15, vcc
	global_load_dword v25, v[26:27], off
	v_add_co_u32_e32 v26, vcc, 0x20000, v14
	v_lshl_add_u64 v[6:7], s[6:7], 0, v[6:7]
	s_nop 0
	v_addc_co_u32_e32 v27, vcc, 0, v15, vcc
	v_add_co_u32_e32 v28, vcc, 0x22000, v14
	global_load_dword v26, v[26:27], off
	s_nop 0
	v_addc_co_u32_e32 v29, vcc, 0, v15, vcc
	global_load_dword v27, v[28:29], off
	v_add_co_u32_e32 v28, vcc, 0x24000, v14
	s_add_i32 s10, s10, s11
	s_nop 0
	v_addc_co_u32_e32 v29, vcc, 0, v15, vcc
	v_add_co_u32_e32 v30, vcc, 0x26000, v14
	global_load_dword v28, v[28:29], off
	s_nop 0
	v_addc_co_u32_e32 v31, vcc, 0, v15, vcc
	global_load_dword v29, v[30:31], off
	v_add_co_u32_e32 v30, vcc, 0x28000, v14
	s_add_i32 s16, s16, s17
	s_nop 0
	v_addc_co_u32_e32 v31, vcc, 0, v15, vcc
	v_add_co_u32_e32 v32, vcc, 0x2a000, v14
	global_load_dword v30, v[30:31], off
	s_nop 0
	v_addc_co_u32_e32 v33, vcc, 0, v15, vcc
	global_load_dword v31, v[32:33], off
	v_add_co_u32_e32 v32, vcc, 0x2c000, v14
	s_add_i32 s18, s18, s19
	s_nop 0
	v_addc_co_u32_e32 v33, vcc, 0, v15, vcc
	v_add_co_u32_e32 v34, vcc, 0x2e000, v14
	global_load_dword v32, v[32:33], off
	s_nop 0
	v_addc_co_u32_e32 v35, vcc, 0, v15, vcc
	global_load_dword v33, v[34:35], off
	v_add_co_u32_e32 v34, vcc, s9, v14
	s_cmpk_lt_i32 s10, 0x800
	s_nop 0
	v_addc_co_u32_e32 v35, vcc, 0, v15, vcc
	v_add_co_u32_e32 v36, vcc, 0x32000, v14
	global_load_dword v34, v[34:35], off
	s_nop 0
	v_addc_co_u32_e32 v37, vcc, 0, v15, vcc
	global_load_dword v35, v[36:37], off
	v_add_co_u32_e32 v36, vcc, 0x34000, v14
	s_movk_i32 s20, 0x110
	s_nop 0
	v_addc_co_u32_e32 v37, vcc, 0, v15, vcc
	v_add_co_u32_e32 v38, vcc, 0x36000, v14
	global_load_dword v36, v[36:37], off
	s_nop 0
	v_addc_co_u32_e32 v39, vcc, 0, v15, vcc
	global_load_dword v37, v[38:39], off
	v_add_co_u32_e32 v38, vcc, 0x38000, v14
	s_nop 1
	v_addc_co_u32_e32 v39, vcc, 0, v15, vcc
	v_add_co_u32_e32 v40, vcc, 0x3a000, v14
	global_load_dword v38, v[38:39], off
	s_nop 0
	v_addc_co_u32_e32 v41, vcc, 0, v15, vcc
	global_load_dword v39, v[40:41], off
	v_add_co_u32_e32 v40, vcc, 0x3c000, v14
	s_nop 1
	v_addc_co_u32_e32 v41, vcc, 0, v15, vcc
	v_add_co_u32_e32 v42, vcc, 0x3e000, v14
	global_load_dword v40, v[40:41], off
	s_nop 0
	v_addc_co_u32_e32 v43, vcc, 0, v15, vcc
	global_load_dword v41, v[42:43], off
	v_add_co_u32_e32 v42, vcc, 0x40000, v14
	s_nop 1
	v_addc_co_u32_e32 v43, vcc, 0, v15, vcc
	v_add_co_u32_e32 v44, vcc, 0x42000, v14
	global_load_dword v42, v[42:43], off
	s_nop 0
	v_addc_co_u32_e32 v45, vcc, 0, v15, vcc
	global_load_dword v43, v[44:45], off
	v_add_co_u32_e32 v44, vcc, 0x44000, v14
	s_nop 1
	v_addc_co_u32_e32 v45, vcc, 0, v15, vcc
	v_add_co_u32_e32 v46, vcc, 0x46000, v14
	global_load_dword v44, v[44:45], off
	s_nop 0
	v_addc_co_u32_e32 v47, vcc, 0, v15, vcc
	global_load_dword v45, v[46:47], off
	v_add_co_u32_e32 v46, vcc, 0x48000, v14
	s_nop 1
	v_addc_co_u32_e32 v47, vcc, 0, v15, vcc
	v_add_co_u32_e32 v48, vcc, 0x4a000, v14
	global_load_dword v46, v[46:47], off
	s_nop 0
	v_addc_co_u32_e32 v49, vcc, 0, v15, vcc
	global_load_dword v47, v[48:49], off
	v_add_co_u32_e32 v48, vcc, 0x4c000, v14
	s_nop 1
	v_addc_co_u32_e32 v49, vcc, 0, v15, vcc
	v_add_co_u32_e32 v50, vcc, 0x4e000, v14
	global_load_dword v48, v[48:49], off
	s_nop 0
	v_addc_co_u32_e32 v51, vcc, 0, v15, vcc
	global_load_dword v49, v[50:51], off
	v_add_co_u32_e32 v50, vcc, 0x50000, v14
	s_nop 1
	v_addc_co_u32_e32 v51, vcc, 0, v15, vcc
	v_add_co_u32_e32 v52, vcc, 0x52000, v14
	global_load_dword v50, v[50:51], off
	s_nop 0
	v_addc_co_u32_e32 v53, vcc, 0, v15, vcc
	global_load_dword v51, v[52:53], off
	v_add_co_u32_e32 v52, vcc, 0x54000, v14
	s_nop 1
	v_addc_co_u32_e32 v53, vcc, 0, v15, vcc
	v_add_co_u32_e32 v54, vcc, 0x56000, v14
	global_load_dword v52, v[52:53], off
	s_nop 0
	v_addc_co_u32_e32 v55, vcc, 0, v15, vcc
	global_load_dword v53, v[54:55], off
	v_add_co_u32_e32 v54, vcc, 0x58000, v14
	s_nop 1
	v_addc_co_u32_e32 v55, vcc, 0, v15, vcc
	v_add_co_u32_e32 v56, vcc, 0x5a000, v14
	global_load_dword v54, v[54:55], off
	s_nop 0
	v_addc_co_u32_e32 v57, vcc, 0, v15, vcc
	global_load_dword v55, v[56:57], off
	v_add_co_u32_e32 v56, vcc, 0x5c000, v14
	s_nop 1
	v_addc_co_u32_e32 v57, vcc, 0, v15, vcc
	v_add_co_u32_e32 v58, vcc, 0x5e000, v14
	global_load_dword v56, v[56:57], off
	s_nop 0
	v_addc_co_u32_e32 v59, vcc, 0, v15, vcc
	global_load_dword v57, v[58:59], off
	v_add_co_u32_e32 v58, vcc, 0x60000, v14
	s_nop 1
	v_addc_co_u32_e32 v59, vcc, 0, v15, vcc
	v_add_co_u32_e32 v60, vcc, 0x62000, v14
	global_load_dword v58, v[58:59], off
	s_nop 0
	v_addc_co_u32_e32 v61, vcc, 0, v15, vcc
	global_load_dword v59, v[60:61], off
	v_add_co_u32_e32 v60, vcc, 0x64000, v14
	s_nop 1
	v_addc_co_u32_e32 v61, vcc, 0, v15, vcc
	v_add_co_u32_e32 v62, vcc, 0x66000, v14
	global_load_dword v60, v[60:61], off
	s_nop 0
	v_addc_co_u32_e32 v63, vcc, 0, v15, vcc
	global_load_dword v61, v[62:63], off
	v_add_co_u32_e32 v62, vcc, 0x68000, v14
	s_nop 1
	v_addc_co_u32_e32 v63, vcc, 0, v15, vcc
	v_add_co_u32_e32 v64, vcc, 0x6a000, v14
	global_load_dword v62, v[62:63], off
	s_nop 0
	v_addc_co_u32_e32 v65, vcc, 0, v15, vcc
	global_load_dword v63, v[64:65], off
	v_add_co_u32_e32 v64, vcc, 0x6c000, v14
	s_nop 1
	v_addc_co_u32_e32 v65, vcc, 0, v15, vcc
	v_add_co_u32_e32 v66, vcc, 0x6e000, v14
	global_load_dword v64, v[64:65], off
	s_nop 0
	v_addc_co_u32_e32 v67, vcc, 0, v15, vcc
	global_load_dword v65, v[66:67], off
	v_add_co_u32_e32 v66, vcc, 0x70000, v14
	s_nop 1
	v_addc_co_u32_e32 v67, vcc, 0, v15, vcc
	v_add_co_u32_e32 v68, vcc, 0x72000, v14
	global_load_dword v66, v[66:67], off
	s_nop 0
	v_addc_co_u32_e32 v69, vcc, 0, v15, vcc
	global_load_dword v67, v[68:69], off
	v_add_co_u32_e32 v68, vcc, 0x74000, v14
	s_nop 1
	v_addc_co_u32_e32 v69, vcc, 0, v15, vcc
	v_add_co_u32_e32 v70, vcc, 0x76000, v14
	global_load_dword v68, v[68:69], off
	s_nop 0
	v_addc_co_u32_e32 v71, vcc, 0, v15, vcc
	global_load_dword v69, v[70:71], off
	v_add_co_u32_e32 v70, vcc, 0x78000, v14
	s_nop 1
	v_addc_co_u32_e32 v71, vcc, 0, v15, vcc
	v_add_co_u32_e32 v72, vcc, 0x7a000, v14
	global_load_dword v70, v[70:71], off
	s_nop 0
	v_addc_co_u32_e32 v73, vcc, 0, v15, vcc
	global_load_dword v71, v[72:73], off
	v_add_co_u32_e32 v72, vcc, 0x7c000, v14
	s_nop 1
	v_addc_co_u32_e32 v73, vcc, 0, v15, vcc
	v_add_co_u32_e32 v14, vcc, 0x7e000, v14
	global_load_dword v72, v[72:73], off
	s_nop 0
	v_addc_co_u32_e32 v15, vcc, 0, v15, vcc
	global_load_dword v73, v[14:15], off
	v_lshl_add_u64 v[14:15], s[2:3], 1, v[6:7]
	s_waitcnt vmcnt(0) lgkmcnt(0)
	v_pk_mul_f32 v[6:7], v[4:5], v[8:9] op_sel_hi:[0,1]
	v_pk_mul_f32 v[8:9], v[4:5], v[10:11] op_sel_hi:[0,1]
	v_cvt_pk_bf16_f32 v6, v6, v7
	v_cvt_pk_bf16_f32 v7, v8, v9
	v_pk_mul_f32 v[8:9], v[4:5], v[12:13] op_sel_hi:[0,1]
	v_pk_mul_f32 v[10:11], v[4:5], v[16:17] op_sel_hi:[0,1]
	v_cvt_pk_bf16_f32 v8, v8, v9
	v_cvt_pk_bf16_f32 v9, v10, v11
	global_store_dwordx4 v[14:15], v[6:9], off
	v_pk_mul_f32 v[10:11], v[4:5], v[24:25] op_sel_hi:[0,1]
	s_nop 0
	v_pk_mul_f32 v[6:7], v[4:5], v[18:19] op_sel_hi:[0,1]
	v_pk_mul_f32 v[8:9], v[4:5], v[20:21] op_sel_hi:[0,1]
	v_cvt_pk_bf16_f32 v6, v6, v7
	v_cvt_pk_bf16_f32 v7, v8, v9
	v_pk_mul_f32 v[8:9], v[4:5], v[22:23] op_sel_hi:[0,1]
	v_cvt_pk_bf16_f32 v8, v8, v9
	v_cvt_pk_bf16_f32 v9, v10, v11
	global_store_dwordx4 v[14:15], v[6:9], off offset:16
	v_pk_mul_f32 v[10:11], v[4:5], v[32:33] op_sel_hi:[0,1]
	s_nop 0
	v_pk_mul_f32 v[6:7], v[4:5], v[26:27] op_sel_hi:[0,1]
	v_pk_mul_f32 v[8:9], v[4:5], v[28:29] op_sel_hi:[0,1]
	v_cvt_pk_bf16_f32 v6, v6, v7
	v_cvt_pk_bf16_f32 v7, v8, v9
	v_pk_mul_f32 v[8:9], v[4:5], v[30:31] op_sel_hi:[0,1]
	v_cvt_pk_bf16_f32 v8, v8, v9
	v_cvt_pk_bf16_f32 v9, v10, v11
	global_store_dwordx4 v[14:15], v[6:9], off offset:32
	v_pk_mul_f32 v[10:11], v[4:5], v[40:41] op_sel_hi:[0,1]
	s_nop 0
	v_pk_mul_f32 v[6:7], v[4:5], v[34:35] op_sel_hi:[0,1]
	v_pk_mul_f32 v[8:9], v[4:5], v[36:37] op_sel_hi:[0,1]
	v_cvt_pk_bf16_f32 v6, v6, v7
	v_cvt_pk_bf16_f32 v7, v8, v9
	v_pk_mul_f32 v[8:9], v[4:5], v[38:39] op_sel_hi:[0,1]
	v_cvt_pk_bf16_f32 v8, v8, v9
	v_cvt_pk_bf16_f32 v9, v10, v11
	global_store_dwordx4 v[14:15], v[6:9], off offset:48
	v_pk_mul_f32 v[10:11], v[4:5], v[48:49] op_sel_hi:[0,1]
	s_nop 0
	v_pk_mul_f32 v[6:7], v[4:5], v[42:43] op_sel_hi:[0,1]
	v_pk_mul_f32 v[8:9], v[4:5], v[44:45] op_sel_hi:[0,1]
	v_cvt_pk_bf16_f32 v6, v6, v7
	v_cvt_pk_bf16_f32 v7, v8, v9
	v_pk_mul_f32 v[8:9], v[4:5], v[46:47] op_sel_hi:[0,1]
	v_cvt_pk_bf16_f32 v8, v8, v9
	v_cvt_pk_bf16_f32 v9, v10, v11
	global_store_dwordx4 v[14:15], v[6:9], off offset:64
	v_pk_mul_f32 v[10:11], v[4:5], v[56:57] op_sel_hi:[0,1]
	s_nop 0
	v_pk_mul_f32 v[6:7], v[4:5], v[50:51] op_sel_hi:[0,1]
	v_pk_mul_f32 v[8:9], v[4:5], v[52:53] op_sel_hi:[0,1]
	v_cvt_pk_bf16_f32 v6, v6, v7
	v_cvt_pk_bf16_f32 v7, v8, v9
	v_pk_mul_f32 v[8:9], v[4:5], v[54:55] op_sel_hi:[0,1]
	v_cvt_pk_bf16_f32 v8, v8, v9
	v_cvt_pk_bf16_f32 v9, v10, v11
	global_store_dwordx4 v[14:15], v[6:9], off offset:80
	v_pk_mul_f32 v[10:11], v[4:5], v[64:65] op_sel_hi:[0,1]
	s_nop 0
	v_pk_mul_f32 v[6:7], v[4:5], v[58:59] op_sel_hi:[0,1]
	v_pk_mul_f32 v[8:9], v[4:5], v[60:61] op_sel_hi:[0,1]
	v_cvt_pk_bf16_f32 v6, v6, v7
	v_cvt_pk_bf16_f32 v7, v8, v9
	v_pk_mul_f32 v[8:9], v[4:5], v[62:63] op_sel_hi:[0,1]
	v_cvt_pk_bf16_f32 v8, v8, v9
	v_cvt_pk_bf16_f32 v9, v10, v11
	global_store_dwordx4 v[14:15], v[6:9], off offset:96
	s_nop 1
	v_pk_mul_f32 v[6:7], v[4:5], v[66:67] op_sel_hi:[0,1]
	v_pk_mul_f32 v[8:9], v[4:5], v[68:69] op_sel_hi:[0,1]
	v_cvt_pk_bf16_f32 v6, v6, v7
	v_cvt_pk_bf16_f32 v7, v8, v9
	v_pk_mul_f32 v[8:9], v[4:5], v[70:71] op_sel_hi:[0,1]
	v_cvt_pk_bf16_f32 v8, v8, v9
	v_pk_mul_f32 v[4:5], v[4:5], v[72:73] op_sel_hi:[0,1]
	v_cvt_pk_bf16_f32 v9, v4, v5
	global_store_dwordx4 v[14:15], v[6:9], off offset:112
	s_cbranch_scc0 .LBB0_1854

.LBB0_1923:
	s_lshl_b32 s11, s18, 8
	v_lshl_or_b32 v222, s19, 8, v243
	s_add_i32 s11, s11, s51
	v_ashrrev_i32_e32 v223, 31, v222
	v_or_b32_e32 v220, s11, v1
	v_lshlrev_b64 v[206:207], 1, v[222:223]
	s_and_b32 s13, s11, 0xfc0
	v_lshl_add_u64 v[224:225], s[4:5], 0, v[206:207]
	s_movk_i32 s21, 0x2c00
	s_cmp_lg_u32 s13, 0
	v_ashrrev_i32_e32 v221, 31, v220
	v_mad_i64_i32 v[36:37], s[18:19], v220, s21, v[224:225]
	v_lshl_add_u64 v[202:203], v[220:221], 2, s[6:7]
	s_cselect_b64 vcc, -1, 0
	global_load_dwordx4 v[164:167], v[36:37], off
	global_load_dword v186, v[202:203], off
	v_cndmask_b32_e32 v36, 0, v242, vcc
	v_add_u32_e32 v36, s11, v36
	v_mov_b64_e32 v[204:205], s[4:5]
	v_mad_i64_i32 v[36:37], s[18:19], v36, s21, v[204:205]
	v_lshl_add_u64 v[216:217], v[36:37], 0, v[206:207]
	global_load_dwordx4 v[182:185], v[216:217], off
	v_lshlrev_b64 v[36:37], 2, v[222:223]
	v_lshl_add_u64 v[208:209], v[178:179], 0, v[36:37]
	v_lshl_add_u64 v[38:39], v[194:195], 0, v[36:37]
	global_load_dwordx4 v[116:119], v[208:209], off
	global_load_dwordx4 v[128:131], v[38:39], off
	v_lshl_add_u64 v[40:41], v[196:197], 0, v[36:37]
	v_lshl_add_u64 v[210:211], v[180:181], 0, v[36:37]
	global_load_dwordx4 v[120:123], v[40:41], off
	global_load_dwordx4 v[124:127], v[210:211], off
	global_load_dwordx4 v[44:47], v[208:209], off offset:16
	global_load_dwordx4 v[48:51], v[38:39], off offset:16
	s_nop 0
	global_load_dwordx4 v[36:39], v[40:41], off offset:16
	s_nop 0
	global_load_dwordx4 v[40:43], v[210:211], off offset:16
	v_sub_u32_e32 v170, v220, v1
	v_and_b32_e32 v187, 0xfff, v170
	v_cmp_ne_u32_e32 vcc, 0, v187
	s_mov_b32 s20, 0xffff0000
	v_or_b32_e32 v212, 16, v220
	v_cndmask_b32_e64 v187, 0, -1, vcc
	v_cndmask_b32_e64 v223, 0, v187, s[38:39]
	v_cndmask_b32_e64 v245, 0, v187, s[36:37]
	v_mad_i64_i32 v[168:169], s[18:19], v212, s21, v[224:225]
	v_ashrrev_i32_e32 v213, 31, v212
	global_load_dwordx4 v[168:171], v[168:169], off
	s_addk_i32 s11, 0x80
	s_and_b32 s13, s11, 0xfc0
	s_cmp_lg_u32 s13, 0
	s_mov_b32 s25, 0x800000
	s_movk_i32 s24, 0x7200
	s_waitcnt vmcnt(0) lgkmcnt(0)
	v_mov_b32_dpp v193, v164 row_shr:2 row_mask:0xf bank_mask:0xf bound_ctrl:1
	v_mov_b32_dpp v191, v164 row_shr:1 row_mask:0xf bank_mask:0xf bound_ctrl:1
	v_mov_b32_dpp v219, v165 row_shr:2 row_mask:0xf bank_mask:0xf bound_ctrl:1
	v_pk_mul_f32 v[188:189], v[158:159], v[186:187] op_sel_hi:[1,0]
	v_pk_mul_f32 v[158:159], v[156:157], v[186:187] op_sel_hi:[1,0]
	v_lshlrev_b32_e32 v156, 16, v164
	v_and_b32_e32 v157, 0xffff0000, v164
	v_mov_b32_dpp v215, v165 row_shr:1 row_mask:0xf bank_mask:0xf bound_ctrl:1
	v_and_b32_dpp v238, v182, v223 row_ror:2 row_mask:0xf bank_mask:0xf bound_ctrl:1
	v_and_b32_dpp v237, v182, v245 row_ror:1 row_mask:0xf bank_mask:0xf bound_ctrl:1
	v_and_b32_dpp v247, v184, v245 row_ror:1 row_mask:0xf bank_mask:0xf bound_ctrl:1
	v_and_b32_dpp v248, v184, v223 row_ror:2 row_mask:0xf bank_mask:0xf bound_ctrl:1
	v_and_b32_dpp v249, v185, v245 row_ror:1 row_mask:0xf bank_mask:0xf bound_ctrl:1
	v_and_b32_dpp v250, v185, v223 row_ror:2 row_mask:0xf bank_mask:0xf bound_ctrl:1
	v_or_b32_sdwa v184, v238, v193 dst_sel:WORD_1 dst_unused:UNUSED_PAD src0_sel:DWORD src1_sel:DWORD
	v_bitop3_b32 v185, v238, s20, v193 bitop3:0xc8
	v_and_b32_dpp v239, v183, v245 row_ror:1 row_mask:0xf bank_mask:0xf bound_ctrl:1
	v_and_b32_dpp v246, v183, v223 row_ror:2 row_mask:0xf bank_mask:0xf bound_ctrl:1
	v_or_b32_sdwa v182, v237, v191 dst_sel:WORD_1 dst_unused:UNUSED_PAD src0_sel:DWORD src1_sel:DWORD
	v_bitop3_b32 v183, v237, s20, v191 bitop3:0xc8
	v_pk_mul_f32 v[184:185], v[116:117], v[184:185]
	v_or_b32_sdwa v192, v246, v219 dst_sel:WORD_1 dst_unused:UNUSED_PAD src0_sel:DWORD src1_sel:DWORD
	v_pk_fma_f32 v[182:183], v[128:129], v[182:183], v[184:185]
	v_bitop3_b32 v193, v246, s20, v219 bitop3:0xc8
	v_pk_fma_f32 v[156:157], v[120:121], v[156:157], v[182:183]
	v_or_b32_sdwa v190, v239, v215 dst_sel:WORD_1 dst_unused:UNUSED_PAD src0_sel:DWORD src1_sel:DWORD
	v_bitop3_b32 v191, v239, s20, v215 bitop3:0xc8
	v_pk_mul_f32 v[192:193], v[118:119], v[192:193]
	v_pk_add_f32 v[156:157], v[124:125], v[156:157]
	v_pk_mul_f32 v[162:163], v[162:163], v[186:187] op_sel_hi:[1,0]
	v_pk_mul_f32 v[160:161], v[160:161], v[186:187] op_sel_hi:[1,0]
	v_lshlrev_b32_e32 v186, 16, v165
	v_and_b32_e32 v187, 0xffff0000, v165
	v_pk_fma_f32 v[184:185], v[130:131], v[190:191], v[192:193]
	v_mul_f32_e32 v182, 0xbfb8aa3b, v156
	v_mul_f32_e32 v183, 0xbfb8aa3b, v157
	v_exp_f32_e32 v190, v182
	v_exp_f32_e32 v191, v183
	v_pk_fma_f32 v[182:183], v[122:123], v[186:187], v[184:185]
	v_mov_b32_dpp v233, v166 row_shr:2 row_mask:0xf bank_mask:0xf bound_ctrl:1
	v_pk_add_f32 v[182:183], v[126:127], v[182:183]
	v_add_f32_e32 v184, 1.0, v190
	v_mul_f32_e32 v186, 0xbfb8aa3b, v182
	v_mul_f32_e32 v187, 0xbfb8aa3b, v183
	v_exp_f32_e32 v186, v186
	v_exp_f32_e32 v187, v187
	v_add_f32_e32 v185, 1.0, v191
	v_rcp_f32_e32 v184, v184
	v_rcp_f32_e32 v185, v185
	v_add_f32_e32 v186, 1.0, v186
	v_add_f32_e32 v187, 1.0, v187
	v_rcp_f32_e32 v186, v186
	v_rcp_f32_e32 v187, v187
	v_pk_mul_f32 v[156:157], v[156:157], v[184:185]
	v_mov_b32_dpp v221, v166 row_shr:1 row_mask:0xf bank_mask:0xf bound_ctrl:1
	v_or_b32_sdwa v218, v248, v233 dst_sel:WORD_1 dst_unused:UNUSED_PAD src0_sel:DWORD src1_sel:DWORD
	v_bitop3_b32 v219, v248, s20, v233 bitop3:0xc8
	v_pk_mul_f32 v[156:157], v[156:157], v[160:161]
	v_pk_mul_f32 v[160:161], v[182:183], v[186:187]
	v_or_b32_sdwa v214, v247, v221 dst_sel:WORD_1 dst_unused:UNUSED_PAD src0_sel:DWORD src1_sel:DWORD
	v_bitop3_b32 v215, v247, s20, v221 bitop3:0xc8
	v_pk_mul_f32 v[160:161], v[160:161], v[162:163]
	v_pk_mul_f32 v[162:163], v[44:45], v[218:219]
	v_lshlrev_b32_e32 v182, 16, v166
	v_pk_fma_f32 v[162:163], v[48:49], v[214:215], v[162:163]
	v_and_b32_e32 v183, 0xffff0000, v166
	v_pk_fma_f32 v[162:163], v[36:37], v[182:183], v[162:163]
	v_cvt_pk_bf16_f32 v156, v156, v157
	v_pk_add_f32 v[162:163], v[40:41], v[162:163]
	v_mov_b32_dpp v235, v167 row_shr:2 row_mask:0xf bank_mask:0xf bound_ctrl:1
	v_mul_f32_e32 v157, 0xbfb8aa3b, v162
	v_exp_f32_e32 v182, v157
	v_mul_f32_e32 v157, 0xbfb8aa3b, v163
	v_exp_f32_e32 v183, v157
	v_mov_b32_dpp v236, v167 row_shr:1 row_mask:0xf bank_mask:0xf bound_ctrl:1
	v_or_b32_sdwa v234, v250, v235 dst_sel:WORD_1 dst_unused:UNUSED_PAD src0_sel:DWORD src1_sel:DWORD
	v_bitop3_b32 v235, v250, s20, v235 bitop3:0xc8
	v_or_b32_sdwa v232, v249, v236 dst_sel:WORD_1 dst_unused:UNUSED_PAD src0_sel:DWORD src1_sel:DWORD
	v_bitop3_b32 v233, v249, s20, v236 bitop3:0xc8
	v_cvt_pk_bf16_f32 v157, v160, v161
	v_add_f32_e32 v160, 1.0, v182
	v_add_f32_e32 v161, 1.0, v183
	v_pk_mul_f32 v[182:183], v[46:47], v[234:235]
	v_lshlrev_b32_e32 v184, 16, v167
	v_pk_fma_f32 v[182:183], v[50:51], v[232:233], v[182:183]
	v_and_b32_e32 v185, 0xffff0000, v167
	v_pk_fma_f32 v[182:183], v[38:39], v[184:185], v[182:183]
	v_rcp_f32_e32 v160, v160
	v_pk_add_f32 v[182:183], v[42:43], v[182:183]
	v_rcp_f32_e32 v161, v161
	v_mul_f32_e32 v184, 0xbfb8aa3b, v182
	v_mul_f32_e32 v185, 0xbfb8aa3b, v183
	v_exp_f32_e32 v184, v184
	v_exp_f32_e32 v185, v185
	v_pk_mul_f32 v[160:161], v[162:163], v[160:161]
	v_mov_b64_e32 v[218:219], s[2:3]
	v_add_f32_e32 v184, 1.0, v184
	v_add_f32_e32 v185, 1.0, v185
	v_rcp_f32_e32 v184, v184
	v_rcp_f32_e32 v185, v185
	v_pk_mul_f32 v[158:159], v[158:159], v[160:161]
	v_lshl_add_u64 v[214:215], v[212:213], 2, s[6:7]
	v_cvt_pk_bf16_f32 v158, v158, v159
	v_pk_mul_f32 v[160:161], v[182:183], v[184:185]
	v_sub_u32_e32 v183, v212, v1
	v_pk_mul_f32 v[160:161], v[188:189], v[160:161]
	v_and_b32_e32 v183, 0xfdf, v183
	v_cvt_pk_bf16_f32 v159, v160, v161
	v_mad_i64_i32 v[160:161], s[18:19], v220, s21, v[218:219]
	v_lshl_add_u64 v[162:163], v[160:161], 0, v[206:207]
	global_store_dwordx4 v[162:163], v[156:159], off
	global_load_dword v182, v[214:215], off
	v_cmp_ne_u32_e32 vcc, 0, v183
	v_mov_b32_dpp v185, v168 row_shr:2 row_mask:0xf bank_mask:0xf bound_ctrl:1
	v_mov_b32_dpp v191, v169 row_shr:1 row_mask:0xf bank_mask:0xf bound_ctrl:1
	v_cndmask_b32_e64 v183, 0, -1, vcc
	v_cndmask_b32_e64 v213, 0, v183, s[38:39]
	v_cndmask_b32_e64 v221, 0, v183, s[36:37]
	v_mov_b32_dpp v183, v168 row_shr:1 row_mask:0xf bank_mask:0xf bound_ctrl:1
	v_and_b32_dpp v189, v164, v213 row_ror:2 row_mask:0xf bank_mask:0xf bound_ctrl:1
	v_and_b32_dpp v187, v164, v221 row_ror:1 row_mask:0xf bank_mask:0xf bound_ctrl:1
	v_or_b32_sdwa v164, v189, v185 dst_sel:WORD_1 dst_unused:UNUSED_PAD src0_sel:DWORD src1_sel:DWORD
	v_mov_b32_dpp v193, v169 row_shr:2 row_mask:0xf bank_mask:0xf bound_ctrl:1
	v_and_b32_dpp v233, v165, v221 row_ror:1 row_mask:0xf bank_mask:0xf bound_ctrl:1
	v_and_b32_dpp v234, v165, v213 row_ror:2 row_mask:0xf bank_mask:0xf bound_ctrl:1
	v_mov_b32_dpp v235, v170 row_shr:1 row_mask:0xf bank_mask:0xf bound_ctrl:1
	v_and_b32_dpp v237, v166, v221 row_ror:1 row_mask:0xf bank_mask:0xf bound_ctrl:1
	v_bitop3_b32 v165, v189, s20, v185 bitop3:0xc8
	v_or_b32_sdwa v184, v187, v183 dst_sel:WORD_1 dst_unused:UNUSED_PAD src0_sel:DWORD src1_sel:DWORD
	v_or_b32_sdwa v186, v233, v191 dst_sel:WORD_1 dst_unused:UNUSED_PAD src0_sel:DWORD src1_sel:DWORD
	v_or_b32_sdwa v188, v234, v193 dst_sel:WORD_1 dst_unused:UNUSED_PAD src0_sel:DWORD src1_sel:DWORD
	v_or_b32_sdwa v190, v237, v235 dst_sel:WORD_1 dst_unused:UNUSED_PAD src0_sel:DWORD src1_sel:DWORD
	v_bitop3_b32 v185, v187, s20, v183 bitop3:0xc8
	v_bitop3_b32 v189, v234, s20, v193 bitop3:0xc8
	v_bitop3_b32 v187, v233, s20, v191 bitop3:0xc8
	v_bitop3_b32 v191, v237, s20, v235 bitop3:0xc8
	v_mov_b32_dpp v236, v170 row_shr:2 row_mask:0xf bank_mask:0xf bound_ctrl:1
	v_and_b32_dpp v238, v166, v213 row_ror:2 row_mask:0xf bank_mask:0xf bound_ctrl:1
	v_or_b32_sdwa v166, v238, v236 dst_sel:WORD_1 dst_unused:UNUSED_PAD src0_sel:DWORD src1_sel:DWORD
	v_and_b32_dpp v247, v167, v221 row_ror:1 row_mask:0xf bank_mask:0xf bound_ctrl:1
	v_and_b32_dpp v248, v167, v213 row_ror:2 row_mask:0xf bank_mask:0xf bound_ctrl:1
	v_bitop3_b32 v167, v238, s20, v236 bitop3:0xc8
	v_mov_b32_dpp v246, v171 row_shr:2 row_mask:0xf bank_mask:0xf bound_ctrl:1
	v_mov_b32_dpp v239, v171 row_shr:1 row_mask:0xf bank_mask:0xf bound_ctrl:1
	v_or_b32_sdwa v232, v248, v246 dst_sel:WORD_1 dst_unused:UNUSED_PAD src0_sel:DWORD src1_sel:DWORD
	v_bitop3_b32 v233, v248, s20, v246 bitop3:0xc8
	v_or_b32_sdwa v192, v247, v239 dst_sel:WORD_1 dst_unused:UNUSED_PAD src0_sel:DWORD src1_sel:DWORD
	v_bitop3_b32 v193, v247, s20, v239 bitop3:0xc8
	v_or_b32_e32 v160, 32, v220
	v_mad_i64_i32 v[156:157], s[18:19], v160, s21, v[224:225]
	global_load_dwordx4 v[156:159], v[156:157], off
	v_ashrrev_i32_e32 v161, 31, v160
	s_waitcnt vmcnt(0) lgkmcnt(0)
	v_pk_mul_f32 v[234:235], v[150:151], v[182:183] op_sel_hi:[1,0]
	v_pk_mul_f32 v[150:151], v[116:117], v[164:165]
	v_pk_mul_f32 v[154:155], v[154:155], v[182:183] op_sel_hi:[1,0]
	v_pk_mul_f32 v[152:153], v[152:153], v[182:183] op_sel_hi:[1,0]
	v_pk_fma_f32 v[150:151], v[128:129], v[184:185], v[150:151]
	v_lshlrev_b32_e32 v164, 16, v168
	v_and_b32_e32 v165, 0xffff0000, v168
	v_pk_mul_f32 v[148:149], v[148:149], v[182:183] op_sel_hi:[1,0]
	v_pk_mul_f32 v[182:183], v[118:119], v[188:189]
	v_pk_fma_f32 v[150:151], v[120:121], v[164:165], v[150:151]
	v_pk_fma_f32 v[182:183], v[130:131], v[186:187], v[182:183]
	v_lshlrev_b32_e32 v184, 16, v169
	v_and_b32_e32 v185, 0xffff0000, v169
	v_pk_add_f32 v[150:151], v[124:125], v[150:151]
	v_pk_fma_f32 v[182:183], v[122:123], v[184:185], v[182:183]
	v_mul_f32_e32 v164, 0xbfb8aa3b, v150
	v_mul_f32_e32 v165, 0xbfb8aa3b, v151
	v_pk_add_f32 v[182:183], v[126:127], v[182:183]
	v_exp_f32_e32 v164, v164
	v_exp_f32_e32 v165, v165
	v_mul_f32_e32 v184, 0xbfb8aa3b, v182
	v_mul_f32_e32 v185, 0xbfb8aa3b, v183
	v_exp_f32_e32 v184, v184
	v_exp_f32_e32 v185, v185
	v_add_f32_e32 v164, 1.0, v164
	v_add_f32_e32 v165, 1.0, v165
	v_rcp_f32_e32 v164, v164
	v_rcp_f32_e32 v165, v165
	v_add_f32_e32 v184, 1.0, v184
	v_add_f32_e32 v185, 1.0, v185
	v_rcp_f32_e32 v184, v184
	v_rcp_f32_e32 v185, v185
	v_pk_mul_f32 v[150:151], v[150:151], v[164:165]
	v_lshlrev_b32_e32 v164, 16, v170
	v_pk_mul_f32 v[150:151], v[150:151], v[152:153]
	v_pk_mul_f32 v[152:153], v[182:183], v[184:185]
	v_and_b32_e32 v165, 0xffff0000, v170
	v_pk_mul_f32 v[152:153], v[152:153], v[154:155]
	v_pk_mul_f32 v[154:155], v[44:45], v[166:167]
	v_cvt_pk_bf16_f32 v150, v150, v151
	v_pk_fma_f32 v[154:155], v[48:49], v[190:191], v[154:155]
	v_lshlrev_b32_e32 v166, 16, v171
	v_pk_fma_f32 v[154:155], v[36:37], v[164:165], v[154:155]
	v_and_b32_e32 v167, 0xffff0000, v171
	v_pk_add_f32 v[154:155], v[40:41], v[154:155]
	s_nop 0
	v_mul_f32_e32 v151, 0xbfb8aa3b, v154
	v_exp_f32_e32 v164, v151
	v_mul_f32_e32 v151, 0xbfb8aa3b, v155
	v_exp_f32_e32 v165, v151
	v_cvt_pk_bf16_f32 v151, v152, v153
	v_add_f32_e32 v152, 1.0, v164
	v_rcp_f32_e32 v152, v152
	v_add_f32_e32 v153, 1.0, v165
	v_pk_mul_f32 v[164:165], v[46:47], v[232:233]
	v_rcp_f32_e32 v153, v153
	v_pk_fma_f32 v[164:165], v[50:51], v[192:193], v[164:165]
	v_pk_mul_f32 v[152:153], v[154:155], v[152:153]
	v_pk_fma_f32 v[164:165], v[38:39], v[166:167], v[164:165]
	v_pk_mul_f32 v[148:149], v[148:149], v[152:153]
	v_pk_add_f32 v[164:165], v[42:43], v[164:165]
	v_cvt_pk_bf16_f32 v152, v148, v149
	v_mul_f32_e32 v166, 0xbfb8aa3b, v164
	v_mul_f32_e32 v167, 0xbfb8aa3b, v165
	v_exp_f32_e32 v166, v166
	v_exp_f32_e32 v167, v167
	v_sub_u32_e32 v155, v160, v1
	v_and_b32_e32 v155, 0xfff, v155
	v_add_f32_e32 v166, 1.0, v166
	v_add_f32_e32 v167, 1.0, v167
	v_rcp_f32_e32 v166, v166
	v_rcp_f32_e32 v167, v167
	v_cmp_ne_u32_e32 vcc, 0, v155
	v_pk_mul_f32 v[148:149], v[164:165], v[166:167]
	s_nop 0
	v_pk_mul_f32 v[148:149], v[234:235], v[148:149]
	v_cndmask_b32_e64 v155, 0, -1, vcc
	v_cvt_pk_bf16_f32 v153, v148, v149
	v_mad_i64_i32 v[148:149], s[18:19], v212, s21, v[218:219]
	v_lshl_add_u64 v[148:149], v[148:149], 0, v[206:207]
	global_store_dwordx4 v[148:149], v[150:153], off
	s_cselect_b64 vcc, -1, 0
	s_nop 0
	v_lshl_add_u64 v[150:151], v[160:161], 2, s[6:7]
	global_load_dword v154, v[150:151], off
	v_or_b32_e32 v152, 48, v220
	v_mad_i64_i32 v[164:165], s[18:19], v152, s21, v[224:225]
	v_cndmask_b32_e64 v161, 0, v155, s[38:39]
	global_load_dwordx4 v[182:185], v[164:165], off
	v_cndmask_b32_e64 v164, 0, v155, s[36:37]
	v_mov_b32_dpp v165, v156 row_shr:2 row_mask:0xf bank_mask:0xf bound_ctrl:1
	v_and_b32_dpp v187, v168, v161 row_ror:2 row_mask:0xf bank_mask:0xf bound_ctrl:1
	v_mov_b32_dpp v155, v156 row_shr:1 row_mask:0xf bank_mask:0xf bound_ctrl:1
	v_and_b32_dpp v167, v168, v164 row_ror:1 row_mask:0xf bank_mask:0xf bound_ctrl:1
	v_or_b32_sdwa v168, v187, v165 dst_sel:WORD_1 dst_unused:UNUSED_PAD src0_sel:DWORD src1_sel:DWORD
	v_and_b32_dpp v193, v169, v164 row_ror:1 row_mask:0xf bank_mask:0xf bound_ctrl:1
	v_and_b32_dpp v233, v169, v161 row_ror:2 row_mask:0xf bank_mask:0xf bound_ctrl:1
	v_bitop3_b32 v169, v187, s20, v165 bitop3:0xc8
	v_or_b32_sdwa v166, v167, v155 dst_sel:WORD_1 dst_unused:UNUSED_PAD src0_sel:DWORD src1_sel:DWORD
	v_bitop3_b32 v167, v167, s20, v155 bitop3:0xc8
	v_pk_mul_f32 v[168:169], v[116:117], v[168:169]
	v_mov_b32_dpp v189, v157 row_shr:2 row_mask:0xf bank_mask:0xf bound_ctrl:1
	v_pk_fma_f32 v[166:167], v[128:129], v[166:167], v[168:169]
	v_lshlrev_b32_e32 v168, 16, v156
	v_and_b32_e32 v169, 0xffff0000, v156
	v_pk_fma_f32 v[166:167], v[120:121], v[168:169], v[166:167]
	v_mov_b32_dpp v191, v157 row_shr:1 row_mask:0xf bank_mask:0xf bound_ctrl:1
	v_pk_add_f32 v[166:167], v[124:125], v[166:167]
	v_or_b32_sdwa v188, v233, v189 dst_sel:WORD_1 dst_unused:UNUSED_PAD src0_sel:DWORD src1_sel:DWORD
	v_bitop3_b32 v189, v233, s20, v189 bitop3:0xc8
	v_mul_f32_e32 v165, 0xbfb8aa3b, v167
	v_or_b32_sdwa v186, v193, v191 dst_sel:WORD_1 dst_unused:UNUSED_PAD src0_sel:DWORD src1_sel:DWORD
	v_bitop3_b32 v187, v193, s20, v191 bitop3:0xc8
	v_exp_f32_e32 v165, v165
	v_pk_mul_f32 v[168:169], v[118:119], v[188:189]
	v_mov_b32_dpp v235, v158 row_shr:2 row_mask:0xf bank_mask:0xf bound_ctrl:1
	v_pk_fma_f32 v[168:169], v[130:131], v[186:187], v[168:169]
	v_lshlrev_b32_e32 v186, 16, v157
	v_and_b32_e32 v187, 0xffff0000, v157
	v_pk_fma_f32 v[168:169], v[122:123], v[186:187], v[168:169]
	v_and_b32_dpp v237, v170, v161 row_ror:2 row_mask:0xf bank_mask:0xf bound_ctrl:1
	v_pk_add_f32 v[168:169], v[126:127], v[168:169]
	v_mov_b32_dpp v234, v158 row_shr:1 row_mask:0xf bank_mask:0xf bound_ctrl:1
	v_mul_f32_e32 v186, 0xbfb8aa3b, v169
	v_exp_f32_e32 v187, v186
	v_and_b32_dpp v236, v170, v164 row_ror:1 row_mask:0xf bank_mask:0xf bound_ctrl:1
	v_or_b32_sdwa v170, v237, v235 dst_sel:WORD_1 dst_unused:UNUSED_PAD src0_sel:DWORD src1_sel:DWORD
	v_and_b32_dpp v246, v171, v164 row_ror:1 row_mask:0xf bank_mask:0xf bound_ctrl:1
	v_and_b32_dpp v247, v171, v161 row_ror:2 row_mask:0xf bank_mask:0xf bound_ctrl:1
	v_bitop3_b32 v171, v237, s20, v235 bitop3:0xc8
	v_or_b32_sdwa v190, v236, v234 dst_sel:WORD_1 dst_unused:UNUSED_PAD src0_sel:DWORD src1_sel:DWORD
	v_bitop3_b32 v191, v236, s20, v234 bitop3:0xc8
	v_mov_b32_dpp v239, v159 row_shr:2 row_mask:0xf bank_mask:0xf bound_ctrl:1
	v_mov_b32_dpp v238, v159 row_shr:1 row_mask:0xf bank_mask:0xf bound_ctrl:1
	v_or_b32_sdwa v232, v247, v239 dst_sel:WORD_1 dst_unused:UNUSED_PAD src0_sel:DWORD src1_sel:DWORD
	v_bitop3_b32 v233, v247, s20, v239 bitop3:0xc8
	v_or_b32_sdwa v192, v246, v238 dst_sel:WORD_1 dst_unused:UNUSED_PAD src0_sel:DWORD src1_sel:DWORD
	v_bitop3_b32 v193, v246, s20, v238 bitop3:0xc8
	v_ashrrev_i32_e32 v153, 31, v152
	s_waitcnt vmcnt(0) lgkmcnt(0)
	v_pk_mul_f32 v[146:147], v[146:147], v[154:155] op_sel_hi:[1,0]
	v_pk_mul_f32 v[144:145], v[144:145], v[154:155] op_sel_hi:[1,0]
	v_pk_mul_f32 v[142:143], v[142:143], v[154:155] op_sel_hi:[1,0]
	v_mul_f32_e32 v155, 0xbfb8aa3b, v166
	v_exp_f32_e32 v155, v155
	v_mov_b32_dpp v188, v184 row_shr:2 row_mask:0xf bank_mask:0xf bound_ctrl:1
	v_pk_mul_f32 v[140:141], v[140:141], v[154:155] op_sel_hi:[1,0]
	v_add_f32_e32 v154, 1.0, v155
	v_add_f32_e32 v155, 1.0, v165
	v_mul_f32_e32 v165, 0xbfb8aa3b, v168
	v_exp_f32_e32 v165, v165
	v_rcp_f32_e32 v154, v154
	v_rcp_f32_e32 v155, v155
	v_add_f32_e32 v165, 1.0, v165
	v_rcp_f32_e32 v186, v165
	v_add_f32_e32 v165, 1.0, v187
	v_rcp_f32_e32 v187, v165
	v_pk_mul_f32 v[154:155], v[166:167], v[154:155]
	v_lshlrev_b32_e32 v166, 16, v158
	v_pk_mul_f32 v[144:145], v[154:155], v[144:145]
	v_pk_mul_f32 v[154:155], v[168:169], v[186:187]
	v_and_b32_e32 v167, 0xffff0000, v158
	v_pk_mul_f32 v[146:147], v[154:155], v[146:147]
	v_pk_mul_f32 v[154:155], v[44:45], v[170:171]
	v_cvt_pk_bf16_f32 v144, v144, v145
	v_pk_fma_f32 v[154:155], v[48:49], v[190:191], v[154:155]
	v_lshlrev_b32_e32 v168, 16, v159
	v_pk_fma_f32 v[154:155], v[36:37], v[166:167], v[154:155]
	v_and_b32_e32 v169, 0xffff0000, v159
	v_pk_add_f32 v[154:155], v[40:41], v[154:155]
	v_mov_b32_dpp v187, v184 row_shr:1 row_mask:0xf bank_mask:0xf bound_ctrl:1
	v_mul_f32_e32 v145, 0xbfb8aa3b, v154
	v_exp_f32_e32 v165, v145
	v_mul_f32_e32 v145, 0xbfb8aa3b, v155
	v_exp_f32_e32 v166, v145
	v_cvt_pk_bf16_f32 v145, v146, v147
	v_add_f32_e32 v146, 1.0, v165
	v_rcp_f32_e32 v146, v146
	v_add_f32_e32 v147, 1.0, v166
	v_pk_mul_f32 v[166:167], v[46:47], v[232:233]
	v_rcp_f32_e32 v147, v147
	v_pk_fma_f32 v[166:167], v[50:51], v[192:193], v[166:167]
	v_mov_b32_dpp v192, v185 row_shr:2 row_mask:0xf bank_mask:0xf bound_ctrl:1
	v_pk_fma_f32 v[166:167], v[38:39], v[168:169], v[166:167]
	v_pk_mul_f32 v[146:147], v[154:155], v[146:147]
	v_pk_add_f32 v[166:167], v[42:43], v[166:167]
	v_pk_mul_f32 v[140:141], v[140:141], v[146:147]
	v_mul_f32_e32 v165, 0xbfb8aa3b, v166
	v_exp_f32_e32 v165, v165
	v_mul_f32_e32 v168, 0xbfb8aa3b, v167
	v_exp_f32_e32 v169, v168
	v_cvt_pk_bf16_f32 v146, v140, v141
	v_add_f32_e32 v165, 1.0, v165
	v_rcp_f32_e32 v168, v165
	v_add_f32_e32 v165, 1.0, v169
	v_rcp_f32_e32 v169, v165
	v_mov_b32_dpp v155, v157 row_ror:1 row_mask:0xf bank_mask:0xf bound_ctrl:1
	v_cndmask_b32_e64 v171, 0, v155, s[36:37]
	v_mov_b32_dpp v157, v157 row_ror:2 row_mask:0xf bank_mask:0xf bound_ctrl:1
	v_pk_mul_f32 v[140:141], v[166:167], v[168:169]
	v_mov_b32_dpp v155, v158 row_ror:1 row_mask:0xf bank_mask:0xf bound_ctrl:1
	v_pk_mul_f32 v[140:141], v[142:143], v[140:141]
	v_mov_b32_dpp v168, v158 row_ror:2 row_mask:0xf bank_mask:0xf bound_ctrl:1
	v_cvt_pk_bf16_f32 v147, v140, v141
	v_mad_i64_i32 v[140:141], s[18:19], v160, s21, v[218:219]
	v_lshl_add_u64 v[142:143], v[140:141], 0, v[206:207]
	global_store_dwordx4 v[142:143], v[144:147], off
	v_cndmask_b32_e64 v189, 0, v155, s[36:37]
	v_mov_b32_dpp v155, v159 row_ror:1 row_mask:0xf bank_mask:0xf bound_ctrl:1
	v_lshl_add_u64 v[144:145], v[152:153], 2, s[6:7]
	global_load_dword v140, v[144:145], off
	v_mov_b32_dpp v153, v156 row_ror:2 row_mask:0xf bank_mask:0xf bound_ctrl:1
	v_mov_b32_dpp v146, v156 row_ror:1 row_mask:0xf bank_mask:0xf bound_ctrl:1
	v_mov_b32_dpp v147, v182 row_shr:2 row_mask:0xf bank_mask:0xf bound_ctrl:1
	v_cndmask_b32_e64 v153, 0, v153, s[38:39]
	v_mov_b32_dpp v141, v182 row_shr:1 row_mask:0xf bank_mask:0xf bound_ctrl:1
	v_cndmask_b32_e64 v165, 0, v146, s[36:37]
	v_or_b32_sdwa v154, v153, v147 dst_sel:WORD_1 dst_unused:UNUSED_PAD src0_sel:DWORD src1_sel:DWORD
	v_mov_b32_dpp v169, v183 row_shr:1 row_mask:0xf bank_mask:0xf bound_ctrl:1
	v_mov_b32_dpp v167, v183 row_shr:2 row_mask:0xf bank_mask:0xf bound_ctrl:1
	v_cndmask_b32_e64 v157, 0, v157, s[38:39]
	v_cndmask_b32_e64 v190, 0, v168, s[38:39]
	v_mov_b32_dpp v159, v159 row_ror:2 row_mask:0xf bank_mask:0xf bound_ctrl:1
	v_cndmask_b32_e64 v193, 0, v155, s[36:37]
	v_bitop3_b32 v155, v153, s20, v147 bitop3:0xc8
	v_or_b32_sdwa v146, v165, v141 dst_sel:WORD_1 dst_unused:UNUSED_PAD src0_sel:DWORD src1_sel:DWORD
	v_or_b32_sdwa v156, v171, v169 dst_sel:WORD_1 dst_unused:UNUSED_PAD src0_sel:DWORD src1_sel:DWORD
	v_or_b32_sdwa v166, v157, v167 dst_sel:WORD_1 dst_unused:UNUSED_PAD src0_sel:DWORD src1_sel:DWORD
	v_or_b32_sdwa v158, v189, v187 dst_sel:WORD_1 dst_unused:UNUSED_PAD src0_sel:DWORD src1_sel:DWORD
	v_or_b32_sdwa v168, v190, v188 dst_sel:WORD_1 dst_unused:UNUSED_PAD src0_sel:DWORD src1_sel:DWORD
	v_cndmask_b32_e64 v232, 0, v159, s[38:39]
	v_bitop3_b32 v147, v165, s20, v141 bitop3:0xc8
	v_bitop3_b32 v167, v157, s20, v167 bitop3:0xc8
	v_bitop3_b32 v157, v171, s20, v169 bitop3:0xc8
	v_bitop3_b32 v169, v190, s20, v188 bitop3:0xc8
	v_bitop3_b32 v159, v189, s20, v187 bitop3:0xc8
	v_mov_b32_dpp v191, v185 row_shr:1 row_mask:0xf bank_mask:0xf bound_ctrl:1
	v_or_b32_sdwa v186, v232, v192 dst_sel:WORD_1 dst_unused:UNUSED_PAD src0_sel:DWORD src1_sel:DWORD
	v_bitop3_b32 v187, v232, s20, v192 bitop3:0xc8
	v_or_b32_sdwa v170, v193, v191 dst_sel:WORD_1 dst_unused:UNUSED_PAD src0_sel:DWORD src1_sel:DWORD
	v_bitop3_b32 v171, v193, s20, v191 bitop3:0xc8
	v_add_u32_e32 v165, 0x80, v220
	s_waitcnt vmcnt(0) lgkmcnt(0)
	v_pk_mul_f32 v[188:189], v[134:135], v[140:141] op_sel_hi:[1,0]
	v_pk_mul_f32 v[134:135], v[116:117], v[154:155]
	v_pk_mul_f32 v[138:139], v[138:139], v[140:141] op_sel_hi:[1,0]
	v_pk_fma_f32 v[134:135], v[128:129], v[146:147], v[134:135]
	v_lshlrev_b32_e32 v146, 16, v182
	v_and_b32_e32 v147, 0xffff0000, v182
	v_pk_fma_f32 v[134:135], v[120:121], v[146:147], v[134:135]
	v_pk_mul_f32 v[136:137], v[136:137], v[140:141] op_sel_hi:[1,0]
	v_pk_add_f32 v[134:135], v[124:125], v[134:135]
	v_lshlrev_b32_e32 v154, 16, v183
	v_mul_f32_e32 v141, 0xbfb8aa3b, v134
	v_exp_f32_e32 v146, v141
	v_mul_f32_e32 v141, 0xbfb8aa3b, v135
	v_exp_f32_e32 v147, v141
	v_pk_mul_f32 v[140:141], v[132:133], v[140:141] op_sel_hi:[1,0]
	v_add_f32_e32 v132, 1.0, v146
	v_and_b32_e32 v155, 0xffff0000, v183
	v_add_f32_e32 v133, 1.0, v147
	v_pk_mul_f32 v[146:147], v[118:119], v[166:167]
	v_rcp_f32_e32 v132, v132
	v_pk_fma_f32 v[146:147], v[130:131], v[156:157], v[146:147]
	v_rcp_f32_e32 v133, v133
	v_pk_fma_f32 v[146:147], v[122:123], v[154:155], v[146:147]
	v_pk_mul_f32 v[132:133], v[134:135], v[132:133]
	v_pk_add_f32 v[146:147], v[126:127], v[146:147]
	v_pk_mul_f32 v[132:133], v[132:133], v[136:137]
	v_mul_f32_e32 v153, 0xbfb8aa3b, v146
	v_exp_f32_e32 v153, v153
	v_mul_f32_e32 v154, 0xbfb8aa3b, v147
	v_exp_f32_e32 v155, v154
	v_pk_mul_f32 v[136:137], v[44:45], v[168:169]
	v_add_f32_e32 v153, 1.0, v153
	v_rcp_f32_e32 v154, v153
	v_add_f32_e32 v153, 1.0, v155
	v_rcp_f32_e32 v155, v153
	v_pk_fma_f32 v[136:137], v[48:49], v[158:159], v[136:137]
	v_cvt_pk_bf16_f32 v132, v132, v133
	v_add_u32_e32 v159, 0x90, v220
	v_pk_mul_f32 v[134:135], v[146:147], v[154:155]
	v_lshlrev_b32_e32 v146, 16, v185
	v_pk_mul_f32 v[134:135], v[134:135], v[138:139]
	v_lshlrev_b32_e32 v138, 16, v184
	v_and_b32_e32 v139, 0xffff0000, v184
	v_pk_fma_f32 v[136:137], v[36:37], v[138:139], v[136:137]
	v_and_b32_e32 v147, 0xffff0000, v185
	v_pk_add_f32 v[136:137], v[40:41], v[136:137]
	s_nop 0
	v_mul_f32_e32 v133, 0xbfb8aa3b, v136
	v_exp_f32_e32 v138, v133
	v_mul_f32_e32 v133, 0xbfb8aa3b, v137
	v_exp_f32_e32 v139, v133
	v_cvt_pk_bf16_f32 v133, v134, v135
	v_add_f32_e32 v134, 1.0, v138
	v_rcp_f32_e32 v134, v134
	v_add_f32_e32 v135, 1.0, v139
	v_pk_mul_f32 v[138:139], v[46:47], v[186:187]
	v_rcp_f32_e32 v135, v135
	v_pk_fma_f32 v[138:139], v[50:51], v[170:171], v[138:139]
	v_pk_mul_f32 v[134:135], v[136:137], v[134:135]
	v_pk_fma_f32 v[138:139], v[38:39], v[146:147], v[138:139]
	v_pk_mul_f32 v[134:135], v[140:141], v[134:135]
	v_pk_add_f32 v[138:139], v[42:43], v[138:139]
	v_cvt_pk_bf16_f32 v134, v134, v135
	v_mul_f32_e32 v146, 0xbfb8aa3b, v138
	v_mul_f32_e32 v147, 0xbfb8aa3b, v139
	v_exp_f32_e32 v146, v146
	v_exp_f32_e32 v147, v147
	v_add_f32_e32 v146, 1.0, v146
	v_add_f32_e32 v147, 1.0, v147
	v_rcp_f32_e32 v146, v146
	v_rcp_f32_e32 v147, v147
	s_nop 0
	v_pk_mul_f32 v[136:137], v[138:139], v[146:147]
	s_nop 0
	v_pk_mul_f32 v[136:137], v[188:189], v[136:137]
	v_sub_u32_e32 v139, v165, v1
	v_cvt_pk_bf16_f32 v135, v136, v137
	v_mad_i64_i32 v[136:137], s[18:19], v152, s21, v[218:219]
	v_lshl_add_u64 v[136:137], v[136:137], 0, v[206:207]
	global_store_dwordx4 v[136:137], v[132:135], off
	v_and_b32_e32 v139, 0xfff, v139
	s_nop 0
	v_cndmask_b32_e32 v132, 0, v242, vcc
	v_add_u32_e32 v132, s11, v132
	v_mad_i64_i32 v[132:133], s[18:19], v132, s21, v[204:205]
	v_mad_i64_i32 v[134:135], s[18:19], v165, s21, v[224:225]
	global_load_dwordx4 v[166:169], v[134:135], off
	v_lshl_add_u64 v[140:141], v[132:133], 0, v[206:207]
	global_load_dwordx4 v[182:185], v[140:141], off
	global_load_dword v138, v[202:203], off offset:512
	v_cmp_ne_u32_e32 vcc, 0, v139
	v_mad_i64_i32 v[132:133], s[18:19], v159, s21, v[224:225]
	s_nop 0
	v_cndmask_b32_e64 v139, 0, -1, vcc
	v_cndmask_b32_e64 v157, 0, v139, s[38:39]
	v_cndmask_b32_e64 v158, 0, v139, s[36:37]
	global_load_dwordx4 v[132:135], v[132:133], off
	s_waitcnt vmcnt(0) lgkmcnt(0)
	v_mov_b32_dpp v147, v166 row_shr:2 row_mask:0xf bank_mask:0xf bound_ctrl:1
	v_and_b32_dpp v155, v182, v157 row_ror:2 row_mask:0xf bank_mask:0xf bound_ctrl:1
	v_mov_b32_dpp v139, v166 row_shr:1 row_mask:0xf bank_mask:0xf bound_ctrl:1
	v_and_b32_dpp v153, v182, v158 row_ror:1 row_mask:0xf bank_mask:0xf bound_ctrl:1
	v_or_b32_sdwa v154, v155, v147 dst_sel:WORD_1 dst_unused:UNUSED_PAD src0_sel:DWORD src1_sel:DWORD
	v_mov_b32_dpp v156, v167 row_shr:1 row_mask:0xf bank_mask:0xf bound_ctrl:1
	v_mov_b32_dpp v171, v167 row_shr:2 row_mask:0xf bank_mask:0xf bound_ctrl:1
	v_and_b32_dpp v187, v183, v158 row_ror:1 row_mask:0xf bank_mask:0xf bound_ctrl:1
	v_and_b32_dpp v183, v183, v157 row_ror:2 row_mask:0xf bank_mask:0xf bound_ctrl:1
	v_mov_b32_dpp v189, v168 row_shr:1 row_mask:0xf bank_mask:0xf bound_ctrl:1
	v_mov_b32_dpp v191, v168 row_shr:2 row_mask:0xf bank_mask:0xf bound_ctrl:1
	v_and_b32_dpp v192, v184, v158 row_ror:1 row_mask:0xf bank_mask:0xf bound_ctrl:1
	v_and_b32_dpp v193, v184, v157 row_ror:2 row_mask:0xf bank_mask:0xf bound_ctrl:1
	v_bitop3_b32 v155, v155, s20, v147 bitop3:0xc8
	v_or_b32_sdwa v146, v153, v139 dst_sel:WORD_1 dst_unused:UNUSED_PAD src0_sel:DWORD src1_sel:DWORD
	v_or_b32_sdwa v170, v187, v156 dst_sel:WORD_1 dst_unused:UNUSED_PAD src0_sel:DWORD src1_sel:DWORD
	v_or_b32_sdwa v182, v183, v171 dst_sel:WORD_1 dst_unused:UNUSED_PAD src0_sel:DWORD src1_sel:DWORD
	v_or_b32_sdwa v186, v192, v189 dst_sel:WORD_1 dst_unused:UNUSED_PAD src0_sel:DWORD src1_sel:DWORD
	v_or_b32_sdwa v184, v193, v191 dst_sel:WORD_1 dst_unused:UNUSED_PAD src0_sel:DWORD src1_sel:DWORD
	v_and_b32_dpp v234, v185, v158 row_ror:1 row_mask:0xf bank_mask:0xf bound_ctrl:1
	v_and_b32_dpp v235, v185, v157 row_ror:2 row_mask:0xf bank_mask:0xf bound_ctrl:1
	v_bitop3_b32 v147, v153, s20, v139 bitop3:0xc8
	v_bitop3_b32 v183, v183, s20, v171 bitop3:0xc8
	v_bitop3_b32 v171, v187, s20, v156 bitop3:0xc8
	v_bitop3_b32 v185, v193, s20, v191 bitop3:0xc8
	v_bitop3_b32 v187, v192, s20, v189 bitop3:0xc8
	v_pk_mul_f32 v[192:193], v[110:111], v[138:139] op_sel_hi:[1,0]
	v_pk_mul_f32 v[110:111], v[116:117], v[154:155]
	v_pk_mul_f32 v[114:115], v[114:115], v[138:139] op_sel_hi:[1,0]
	v_pk_fma_f32 v[110:111], v[128:129], v[146:147], v[110:111]
	v_lshlrev_b32_e32 v146, 16, v166
	v_and_b32_e32 v147, 0xffff0000, v166
	v_pk_fma_f32 v[110:111], v[120:121], v[146:147], v[110:111]
	v_pk_mul_f32 v[112:113], v[112:113], v[138:139] op_sel_hi:[1,0]
	v_pk_add_f32 v[110:111], v[124:125], v[110:111]
	v_lshlrev_b32_e32 v154, 16, v167
	v_mul_f32_e32 v139, 0xbfb8aa3b, v110
	v_exp_f32_e32 v146, v139
	v_mul_f32_e32 v139, 0xbfb8aa3b, v111
	v_exp_f32_e32 v147, v139
	v_pk_mul_f32 v[138:139], v[108:109], v[138:139] op_sel_hi:[1,0]
	v_add_f32_e32 v108, 1.0, v146
	v_and_b32_e32 v155, 0xffff0000, v167
	v_add_f32_e32 v109, 1.0, v147
	v_pk_mul_f32 v[146:147], v[118:119], v[182:183]
	v_rcp_f32_e32 v108, v108
	v_pk_fma_f32 v[146:147], v[130:131], v[170:171], v[146:147]
	v_rcp_f32_e32 v109, v109
	v_pk_fma_f32 v[146:147], v[122:123], v[154:155], v[146:147]
	v_mov_b32_dpp v233, v169 row_shr:2 row_mask:0xf bank_mask:0xf bound_ctrl:1
	v_pk_add_f32 v[146:147], v[126:127], v[146:147]
	v_pk_mul_f32 v[108:109], v[110:111], v[108:109]
	v_mul_f32_e32 v153, 0xbfb8aa3b, v146
	v_exp_f32_e32 v153, v153
	v_mul_f32_e32 v154, 0xbfb8aa3b, v147
	v_exp_f32_e32 v155, v154
	v_pk_mul_f32 v[108:109], v[108:109], v[112:113]
	v_add_f32_e32 v153, 1.0, v153
	v_rcp_f32_e32 v154, v153
	v_add_f32_e32 v153, 1.0, v155
	v_rcp_f32_e32 v155, v153
	v_pk_mul_f32 v[112:113], v[44:45], v[184:185]
	v_cvt_pk_bf16_f32 v108, v108, v109
	v_pk_fma_f32 v[112:113], v[48:49], v[186:187], v[112:113]
	v_pk_mul_f32 v[110:111], v[146:147], v[154:155]
	v_mov_b32_dpp v232, v169 row_shr:1 row_mask:0xf bank_mask:0xf bound_ctrl:1
	v_pk_mul_f32 v[110:111], v[110:111], v[114:115]
	v_lshlrev_b32_e32 v114, 16, v168
	v_and_b32_e32 v115, 0xffff0000, v168
	v_pk_fma_f32 v[112:113], v[36:37], v[114:115], v[112:113]
	v_or_b32_sdwa v190, v235, v233 dst_sel:WORD_1 dst_unused:UNUSED_PAD src0_sel:DWORD src1_sel:DWORD
	v_pk_add_f32 v[112:113], v[40:41], v[112:113]
	v_bitop3_b32 v191, v235, s20, v233 bitop3:0xc8
	v_mul_f32_e32 v109, 0xbfb8aa3b, v112
	v_exp_f32_e32 v114, v109
	v_mul_f32_e32 v109, 0xbfb8aa3b, v113
	v_exp_f32_e32 v115, v109
	v_or_b32_sdwa v188, v234, v232 dst_sel:WORD_1 dst_unused:UNUSED_PAD src0_sel:DWORD src1_sel:DWORD
	v_bitop3_b32 v189, v234, s20, v232 bitop3:0xc8
	v_cvt_pk_bf16_f32 v109, v110, v111
	v_add_f32_e32 v110, 1.0, v114
	v_add_f32_e32 v111, 1.0, v115
	v_pk_mul_f32 v[114:115], v[46:47], v[190:191]
	v_lshlrev_b32_e32 v146, 16, v169
	v_pk_fma_f32 v[114:115], v[50:51], v[188:189], v[114:115]
	v_and_b32_e32 v147, 0xffff0000, v169
	v_pk_fma_f32 v[114:115], v[38:39], v[146:147], v[114:115]
	v_rcp_f32_e32 v110, v110
	v_pk_add_f32 v[114:115], v[42:43], v[114:115]
	v_rcp_f32_e32 v111, v111
	v_mul_f32_e32 v146, 0xbfb8aa3b, v114
	v_mul_f32_e32 v147, 0xbfb8aa3b, v115
	v_exp_f32_e32 v146, v146
	v_exp_f32_e32 v147, v147
	v_pk_mul_f32 v[110:111], v[112:113], v[110:111]
	v_add_u32_e32 v156, 0xa0, v220
	v_add_f32_e32 v146, 1.0, v146
	v_add_f32_e32 v147, 1.0, v147
	v_rcp_f32_e32 v146, v146
	v_rcp_f32_e32 v147, v147
	v_pk_mul_f32 v[110:111], v[138:139], v[110:111]
	v_pk_mul_f32 v[112:113], v[114:115], v[146:147]
	s_nop 0
	v_pk_mul_f32 v[112:113], v[192:193], v[112:113]
	v_cvt_pk_bf16_f32 v110, v110, v111
	v_cvt_pk_bf16_f32 v111, v112, v113
	v_mad_i64_i32 v[112:113], s[18:19], v165, s21, v[218:219]
	v_lshl_add_u64 v[138:139], v[112:113], 0, v[206:207]
	global_store_dwordx4 v[138:139], v[108:111], off
	global_load_dword v112, v[202:203], off offset:576
	v_sub_u32_e32 v113, v159, v1
	v_and_b32_e32 v113, 0xfdf, v113
	v_cmp_ne_u32_e32 vcc, 0, v113
	v_mov_b32_dpp v115, v132 row_shr:2 row_mask:0xf bank_mask:0xf bound_ctrl:1
	v_mov_b32_dpp v183, v133 row_shr:1 row_mask:0xf bank_mask:0xf bound_ctrl:1
	v_cndmask_b32_e64 v113, 0, -1, vcc
	v_cndmask_b32_e64 v154, 0, v113, s[38:39]
	v_cndmask_b32_e64 v155, 0, v113, s[36:37]
	v_mov_b32_dpp v113, v132 row_shr:1 row_mask:0xf bank_mask:0xf bound_ctrl:1
	v_and_b32_dpp v147, v166, v154 row_ror:2 row_mask:0xf bank_mask:0xf bound_ctrl:1
	v_and_b32_dpp v153, v166, v155 row_ror:1 row_mask:0xf bank_mask:0xf bound_ctrl:1
	v_or_b32_sdwa v146, v147, v115 dst_sel:WORD_1 dst_unused:UNUSED_PAD src0_sel:DWORD src1_sel:DWORD
	v_mov_b32_dpp v171, v133 row_shr:2 row_mask:0xf bank_mask:0xf bound_ctrl:1
	v_and_b32_dpp v185, v167, v155 row_ror:1 row_mask:0xf bank_mask:0xf bound_ctrl:1
	v_and_b32_dpp v167, v167, v154 row_ror:2 row_mask:0xf bank_mask:0xf bound_ctrl:1
	v_mov_b32_dpp v187, v134 row_shr:1 row_mask:0xf bank_mask:0xf bound_ctrl:1
	v_mov_b32_dpp v188, v134 row_shr:2 row_mask:0xf bank_mask:0xf bound_ctrl:1
	v_and_b32_dpp v189, v168, v155 row_ror:1 row_mask:0xf bank_mask:0xf bound_ctrl:1
	v_and_b32_dpp v190, v168, v154 row_ror:2 row_mask:0xf bank_mask:0xf bound_ctrl:1
	v_bitop3_b32 v147, v147, s20, v115 bitop3:0xc8
	v_or_b32_sdwa v114, v153, v113 dst_sel:WORD_1 dst_unused:UNUSED_PAD src0_sel:DWORD src1_sel:DWORD
	v_or_b32_sdwa v166, v185, v183 dst_sel:WORD_1 dst_unused:UNUSED_PAD src0_sel:DWORD src1_sel:DWORD
	v_or_b32_sdwa v170, v167, v171 dst_sel:WORD_1 dst_unused:UNUSED_PAD src0_sel:DWORD src1_sel:DWORD
	v_or_b32_sdwa v182, v189, v187 dst_sel:WORD_1 dst_unused:UNUSED_PAD src0_sel:DWORD src1_sel:DWORD
	v_or_b32_sdwa v168, v190, v188 dst_sel:WORD_1 dst_unused:UNUSED_PAD src0_sel:DWORD src1_sel:DWORD
	v_and_b32_dpp v193, v169, v155 row_ror:1 row_mask:0xf bank_mask:0xf bound_ctrl:1
	v_and_b32_dpp v232, v169, v154 row_ror:2 row_mask:0xf bank_mask:0xf bound_ctrl:1
	v_bitop3_b32 v115, v153, s20, v113 bitop3:0xc8
	v_bitop3_b32 v171, v167, s20, v171 bitop3:0xc8
	v_bitop3_b32 v167, v185, s20, v183 bitop3:0xc8
	v_bitop3_b32 v169, v190, s20, v188 bitop3:0xc8
	v_bitop3_b32 v183, v189, s20, v187 bitop3:0xc8
	v_mov_b32_dpp v192, v135 row_shr:2 row_mask:0xf bank_mask:0xf bound_ctrl:1
	v_mov_b32_dpp v191, v135 row_shr:1 row_mask:0xf bank_mask:0xf bound_ctrl:1
	v_or_b32_sdwa v186, v232, v192 dst_sel:WORD_1 dst_unused:UNUSED_PAD src0_sel:DWORD src1_sel:DWORD
	v_bitop3_b32 v187, v232, s20, v192 bitop3:0xc8
	v_or_b32_sdwa v184, v193, v191 dst_sel:WORD_1 dst_unused:UNUSED_PAD src0_sel:DWORD src1_sel:DWORD
	v_bitop3_b32 v185, v193, s20, v191 bitop3:0xc8
	v_mad_i64_i32 v[108:109], s[18:19], v156, s21, v[224:225]
	global_load_dwordx4 v[108:111], v[108:109], off
	v_add_u32_e32 v153, 0xb0, v220
	s_waitcnt vmcnt(0) lgkmcnt(0)
	v_pk_mul_f32 v[188:189], v[102:103], v[112:113] op_sel_hi:[1,0]
	v_pk_mul_f32 v[102:103], v[116:117], v[146:147]
	v_pk_mul_f32 v[106:107], v[106:107], v[112:113] op_sel_hi:[1,0]
	v_pk_fma_f32 v[102:103], v[128:129], v[114:115], v[102:103]
	v_lshlrev_b32_e32 v114, 16, v132
	v_and_b32_e32 v115, 0xffff0000, v132
	v_pk_fma_f32 v[102:103], v[120:121], v[114:115], v[102:103]
	v_pk_mul_f32 v[104:105], v[104:105], v[112:113] op_sel_hi:[1,0]
	v_pk_add_f32 v[102:103], v[124:125], v[102:103]
	v_lshlrev_b32_e32 v146, 16, v133
	v_mul_f32_e32 v113, 0xbfb8aa3b, v102
	v_exp_f32_e32 v114, v113
	v_mul_f32_e32 v113, 0xbfb8aa3b, v103
	v_exp_f32_e32 v115, v113
	v_pk_mul_f32 v[112:113], v[100:101], v[112:113] op_sel_hi:[1,0]
	v_add_f32_e32 v100, 1.0, v114
	v_and_b32_e32 v147, 0xffff0000, v133
	v_add_f32_e32 v101, 1.0, v115
	v_pk_mul_f32 v[114:115], v[118:119], v[170:171]
	v_rcp_f32_e32 v100, v100
	v_pk_fma_f32 v[114:115], v[130:131], v[166:167], v[114:115]
	v_rcp_f32_e32 v101, v101
	v_pk_fma_f32 v[114:115], v[122:123], v[146:147], v[114:115]
	v_pk_mul_f32 v[100:101], v[102:103], v[100:101]
	v_pk_add_f32 v[114:115], v[126:127], v[114:115]
	v_pk_mul_f32 v[100:101], v[100:101], v[104:105]
	v_mul_f32_e32 v146, 0xbfb8aa3b, v114
	v_mul_f32_e32 v147, 0xbfb8aa3b, v115
	v_exp_f32_e32 v146, v146
	v_exp_f32_e32 v147, v147
	v_pk_mul_f32 v[104:105], v[44:45], v[168:169]
	v_cvt_pk_bf16_f32 v100, v100, v101
	v_add_f32_e32 v146, 1.0, v146
	v_add_f32_e32 v147, 1.0, v147
	v_rcp_f32_e32 v146, v146
	v_rcp_f32_e32 v147, v147
	v_pk_fma_f32 v[104:105], v[48:49], v[182:183], v[104:105]
	v_pk_mul_f32 v[102:103], v[114:115], v[146:147]
	s_nop 0
	v_pk_mul_f32 v[102:103], v[102:103], v[106:107]
	v_lshlrev_b32_e32 v106, 16, v134
	v_and_b32_e32 v107, 0xffff0000, v134
	v_pk_fma_f32 v[104:105], v[36:37], v[106:107], v[104:105]
	v_lshlrev_b32_e32 v114, 16, v135
	v_pk_add_f32 v[104:105], v[40:41], v[104:105]
	v_and_b32_e32 v115, 0xffff0000, v135
	v_mul_f32_e32 v101, 0xbfb8aa3b, v104
	v_exp_f32_e32 v106, v101
	v_mul_f32_e32 v101, 0xbfb8aa3b, v105
	v_exp_f32_e32 v107, v101
	v_cvt_pk_bf16_f32 v101, v102, v103
	v_add_f32_e32 v102, 1.0, v106
	v_rcp_f32_e32 v102, v102
	v_add_f32_e32 v103, 1.0, v107
	v_pk_mul_f32 v[106:107], v[46:47], v[186:187]
	v_rcp_f32_e32 v103, v103
	v_pk_fma_f32 v[106:107], v[50:51], v[184:185], v[106:107]
	v_pk_mul_f32 v[102:103], v[104:105], v[102:103]
	v_pk_fma_f32 v[106:107], v[38:39], v[114:115], v[106:107]
	v_pk_mul_f32 v[102:103], v[112:113], v[102:103]
	v_pk_add_f32 v[106:107], v[42:43], v[106:107]
	v_cvt_pk_bf16_f32 v102, v102, v103
	v_mul_f32_e32 v114, 0xbfb8aa3b, v106
	v_mul_f32_e32 v115, 0xbfb8aa3b, v107
	v_exp_f32_e32 v114, v114
	v_exp_f32_e32 v115, v115
	v_add_f32_e32 v114, 1.0, v114
	v_add_f32_e32 v115, 1.0, v115
	v_rcp_f32_e32 v114, v114
	v_rcp_f32_e32 v115, v115
	s_nop 0
	v_pk_mul_f32 v[104:105], v[106:107], v[114:115]
	s_nop 0
	v_pk_mul_f32 v[104:105], v[188:189], v[104:105]
	s_nop 0
	v_cvt_pk_bf16_f32 v103, v104, v105
	v_mad_i64_i32 v[104:105], s[18:19], v159, s21, v[218:219]
	v_lshl_add_u64 v[114:115], v[104:105], 0, v[206:207]
	global_store_dwordx4 v[114:115], v[100:103], off
	global_load_dword v100, v[202:203], off offset:640
	s_nop 0
	v_sub_u32_e32 v101, v156, v1
	v_and_b32_e32 v101, 0xfff, v101
	v_cmp_ne_u32_e32 vcc, 0, v101
	v_mad_i64_i32 v[102:103], s[18:19], v153, s21, v[224:225]
	s_nop 0
	v_cndmask_b32_e64 v101, 0, -1, vcc
	v_cndmask_b32_e64 v146, 0, v101, s[38:39]
	global_load_dwordx4 v[102:105], v[102:103], off
	v_cndmask_b32_e64 v147, 0, v101, s[36:37]
	v_mov_b32_dpp v107, v108 row_shr:2 row_mask:0xf bank_mask:0xf bound_ctrl:1
	v_and_b32_dpp v113, v132, v146 row_ror:2 row_mask:0xf bank_mask:0xf bound_ctrl:1
	v_mov_b32_dpp v101, v108 row_shr:1 row_mask:0xf bank_mask:0xf bound_ctrl:1
	v_and_b32_dpp v167, v132, v147 row_ror:1 row_mask:0xf bank_mask:0xf bound_ctrl:1
	v_or_b32_sdwa v112, v113, v107 dst_sel:WORD_1 dst_unused:UNUSED_PAD src0_sel:DWORD src1_sel:DWORD
	v_mov_b32_dpp v169, v109 row_shr:1 row_mask:0xf bank_mask:0xf bound_ctrl:1
	v_mov_b32_dpp v171, v109 row_shr:2 row_mask:0xf bank_mask:0xf bound_ctrl:1
	v_and_b32_dpp v183, v133, v147 row_ror:1 row_mask:0xf bank_mask:0xf bound_ctrl:1
	v_and_b32_dpp v133, v133, v146 row_ror:2 row_mask:0xf bank_mask:0xf bound_ctrl:1
	v_mov_b32_dpp v184, v110 row_shr:1 row_mask:0xf bank_mask:0xf bound_ctrl:1
	v_mov_b32_dpp v185, v110 row_shr:2 row_mask:0xf bank_mask:0xf bound_ctrl:1
	v_and_b32_dpp v186, v134, v147 row_ror:1 row_mask:0xf bank_mask:0xf bound_ctrl:1
	v_and_b32_dpp v187, v134, v146 row_ror:2 row_mask:0xf bank_mask:0xf bound_ctrl:1
	v_bitop3_b32 v113, v113, s20, v107 bitop3:0xc8
	v_or_b32_sdwa v106, v167, v101 dst_sel:WORD_1 dst_unused:UNUSED_PAD src0_sel:DWORD src1_sel:DWORD
	v_or_b32_sdwa v132, v183, v169 dst_sel:WORD_1 dst_unused:UNUSED_PAD src0_sel:DWORD src1_sel:DWORD
	v_or_b32_sdwa v166, v133, v171 dst_sel:WORD_1 dst_unused:UNUSED_PAD src0_sel:DWORD src1_sel:DWORD
	v_or_b32_sdwa v168, v186, v184 dst_sel:WORD_1 dst_unused:UNUSED_PAD src0_sel:DWORD src1_sel:DWORD
	v_or_b32_sdwa v134, v187, v185 dst_sel:WORD_1 dst_unused:UNUSED_PAD src0_sel:DWORD src1_sel:DWORD
	v_and_b32_dpp v190, v135, v147 row_ror:1 row_mask:0xf bank_mask:0xf bound_ctrl:1
	v_and_b32_dpp v191, v135, v146 row_ror:2 row_mask:0xf bank_mask:0xf bound_ctrl:1
	v_bitop3_b32 v107, v167, s20, v101 bitop3:0xc8
	v_bitop3_b32 v167, v133, s20, v171 bitop3:0xc8
	v_bitop3_b32 v133, v183, s20, v169 bitop3:0xc8
	v_bitop3_b32 v135, v187, s20, v185 bitop3:0xc8
	v_bitop3_b32 v169, v186, s20, v184 bitop3:0xc8
	v_mov_b32_dpp v189, v111 row_shr:2 row_mask:0xf bank_mask:0xf bound_ctrl:1
	v_mov_b32_dpp v188, v111 row_shr:1 row_mask:0xf bank_mask:0xf bound_ctrl:1
	v_or_b32_sdwa v182, v191, v189 dst_sel:WORD_1 dst_unused:UNUSED_PAD src0_sel:DWORD src1_sel:DWORD
	v_bitop3_b32 v183, v191, s20, v189 bitop3:0xc8
	v_or_b32_sdwa v170, v190, v188 dst_sel:WORD_1 dst_unused:UNUSED_PAD src0_sel:DWORD src1_sel:DWORD
	v_bitop3_b32 v171, v190, s20, v188 bitop3:0xc8
	s_andn2_b64 vcc, exec, s[40:41]
	s_waitcnt vmcnt(0) lgkmcnt(0)
	v_pk_mul_f32 v[184:185], v[62:63], v[100:101] op_sel_hi:[1,0]
	v_pk_mul_f32 v[62:63], v[116:117], v[112:113]
	v_pk_mul_f32 v[66:67], v[66:67], v[100:101] op_sel_hi:[1,0]
	v_pk_fma_f32 v[62:63], v[128:129], v[106:107], v[62:63]
	v_lshlrev_b32_e32 v106, 16, v108
	v_and_b32_e32 v107, 0xffff0000, v108
	v_pk_fma_f32 v[62:63], v[120:121], v[106:107], v[62:63]
	v_pk_mul_f32 v[64:65], v[64:65], v[100:101] op_sel_hi:[1,0]
	v_pk_add_f32 v[62:63], v[124:125], v[62:63]
	v_lshlrev_b32_e32 v112, 16, v109
	v_mul_f32_e32 v101, 0xbfb8aa3b, v62
	v_exp_f32_e32 v106, v101
	v_mul_f32_e32 v101, 0xbfb8aa3b, v63
	v_exp_f32_e32 v107, v101
	v_pk_mul_f32 v[100:101], v[60:61], v[100:101] op_sel_hi:[1,0]
	v_add_f32_e32 v60, 1.0, v106
	v_and_b32_e32 v113, 0xffff0000, v109
	v_add_f32_e32 v61, 1.0, v107
	v_pk_mul_f32 v[106:107], v[118:119], v[166:167]
	v_rcp_f32_e32 v60, v60
	v_pk_fma_f32 v[106:107], v[130:131], v[132:133], v[106:107]
	v_rcp_f32_e32 v61, v61
	v_pk_fma_f32 v[106:107], v[122:123], v[112:113], v[106:107]
	v_mov_b32_dpp v133, v103 row_shr:2 row_mask:0xf bank_mask:0xf bound_ctrl:1
	v_pk_add_f32 v[106:107], v[126:127], v[106:107]
	v_pk_mul_f32 v[60:61], v[62:63], v[60:61]
	v_mul_f32_e32 v112, 0xbfb8aa3b, v106
	v_mul_f32_e32 v113, 0xbfb8aa3b, v107
	v_exp_f32_e32 v112, v112
	v_exp_f32_e32 v113, v113
	v_pk_mul_f32 v[60:61], v[60:61], v[64:65]
	v_pk_mul_f32 v[64:65], v[44:45], v[134:135]
	v_add_f32_e32 v112, 1.0, v112
	v_add_f32_e32 v113, 1.0, v113
	v_rcp_f32_e32 v112, v112
	v_rcp_f32_e32 v113, v113
	v_pk_fma_f32 v[64:65], v[48:49], v[168:169], v[64:65]
	v_cvt_pk_bf16_f32 v60, v60, v61
	v_mov_b32_dpp v135, v104 row_shr:1 row_mask:0xf bank_mask:0xf bound_ctrl:1
	v_pk_mul_f32 v[62:63], v[106:107], v[112:113]
	v_lshlrev_b32_e32 v106, 16, v111
	v_pk_mul_f32 v[62:63], v[62:63], v[66:67]
	v_lshlrev_b32_e32 v66, 16, v110
	v_and_b32_e32 v67, 0xffff0000, v110
	v_pk_fma_f32 v[64:65], v[36:37], v[66:67], v[64:65]
	v_and_b32_e32 v107, 0xffff0000, v111
	v_pk_add_f32 v[64:65], v[40:41], v[64:65]
	v_mov_b32_dpp v166, v104 row_shr:2 row_mask:0xf bank_mask:0xf bound_ctrl:1
	v_mul_f32_e32 v61, 0xbfb8aa3b, v64
	v_exp_f32_e32 v66, v61
	v_mul_f32_e32 v61, 0xbfb8aa3b, v65
	v_exp_f32_e32 v67, v61
	v_cvt_pk_bf16_f32 v61, v62, v63
	v_add_f32_e32 v62, 1.0, v66
	v_rcp_f32_e32 v62, v62
	v_add_f32_e32 v63, 1.0, v67
	v_pk_mul_f32 v[66:67], v[46:47], v[182:183]
	v_rcp_f32_e32 v63, v63
	v_pk_fma_f32 v[66:67], v[50:51], v[170:171], v[66:67]
	v_mov_b32_dpp v170, v105 row_shr:2 row_mask:0xf bank_mask:0xf bound_ctrl:1
	v_pk_fma_f32 v[66:67], v[38:39], v[106:107], v[66:67]
	v_pk_mul_f32 v[62:63], v[64:65], v[62:63]
	v_pk_add_f32 v[66:67], v[42:43], v[66:67]
	v_pk_mul_f32 v[62:63], v[100:101], v[62:63]
	v_mul_f32_e32 v106, 0xbfb8aa3b, v66
	v_mul_f32_e32 v107, 0xbfb8aa3b, v67
	v_exp_f32_e32 v106, v106
	v_exp_f32_e32 v107, v107
	v_cvt_pk_bf16_f32 v62, v62, v63
	v_mov_b32_dpp v169, v105 row_shr:1 row_mask:0xf bank_mask:0xf bound_ctrl:1
	v_add_f32_e32 v106, 1.0, v106
	v_add_f32_e32 v107, 1.0, v107
	v_rcp_f32_e32 v106, v106
	v_rcp_f32_e32 v107, v107
	s_nop 0
	v_pk_mul_f32 v[64:65], v[66:67], v[106:107]
	s_nop 0
	v_pk_mul_f32 v[64:65], v[184:185], v[64:65]
	v_mov_b32_dpp v107, v103 row_shr:1 row_mask:0xf bank_mask:0xf bound_ctrl:1
	v_cvt_pk_bf16_f32 v63, v64, v65
	v_mad_i64_i32 v[64:65], s[18:19], v156, s21, v[218:219]
	v_lshl_add_u64 v[112:113], v[64:65], 0, v[206:207]
	global_store_dwordx4 v[112:113], v[60:63], off
	global_load_dword v64, v[202:203], off offset:704
	s_nop 0
	v_mov_b32_dpp v60, v108 row_ror:1 row_mask:0xf bank_mask:0xf bound_ctrl:1
	v_mov_b32_dpp v62, v108 row_ror:2 row_mask:0xf bank_mask:0xf bound_ctrl:1
	v_cndmask_b32_e64 v65, 0, v60, s[36:37]
	v_mov_b32_dpp v60, v109 row_ror:1 row_mask:0xf bank_mask:0xf bound_ctrl:1
	v_mov_b32_dpp v63, v102 row_shr:2 row_mask:0xf bank_mask:0xf bound_ctrl:1
	v_cndmask_b32_e64 v67, 0, v62, s[38:39]
	v_mov_b32_dpp v62, v109 row_ror:2 row_mask:0xf bank_mask:0xf bound_ctrl:1
	v_cndmask_b32_e64 v134, 0, v60, s[36:37]
	v_mov_b32_dpp v60, v110 row_ror:1 row_mask:0xf bank_mask:0xf bound_ctrl:1
	v_mov_b32_dpp v61, v102 row_shr:1 row_mask:0xf bank_mask:0xf bound_ctrl:1
	v_or_b32_sdwa v100, v67, v63 dst_sel:WORD_1 dst_unused:UNUSED_PAD src0_sel:DWORD src1_sel:DWORD
	v_cndmask_b32_e64 v109, 0, v62, s[38:39]
	v_mov_b32_dpp v62, v110 row_ror:2 row_mask:0xf bank_mask:0xf bound_ctrl:1
	v_cndmask_b32_e64 v167, 0, v60, s[36:37]
	v_bitop3_b32 v101, v67, s20, v63 bitop3:0xc8
	v_or_b32_sdwa v66, v65, v61 dst_sel:WORD_1 dst_unused:UNUSED_PAD src0_sel:DWORD src1_sel:DWORD
	v_or_b32_sdwa v106, v134, v107 dst_sel:WORD_1 dst_unused:UNUSED_PAD src0_sel:DWORD src1_sel:DWORD
	v_or_b32_sdwa v110, v167, v135 dst_sel:WORD_1 dst_unused:UNUSED_PAD src0_sel:DWORD src1_sel:DWORD
	v_cndmask_b32_e64 v168, 0, v62, s[38:39]
	v_mov_b32_dpp v60, v111 row_ror:1 row_mask:0xf bank_mask:0xf bound_ctrl:1
	v_mov_b32_dpp v62, v111 row_ror:2 row_mask:0xf bank_mask:0xf bound_ctrl:1
	v_bitop3_b32 v67, v65, s20, v61 bitop3:0xc8
	v_bitop3_b32 v107, v134, s20, v107 bitop3:0xc8
	v_bitop3_b32 v111, v167, s20, v135 bitop3:0xc8
	v_or_b32_sdwa v108, v109, v133 dst_sel:WORD_1 dst_unused:UNUSED_PAD src0_sel:DWORD src1_sel:DWORD
	v_bitop3_b32 v109, v109, s20, v133 bitop3:0xc8
	v_or_b32_sdwa v132, v168, v166 dst_sel:WORD_1 dst_unused:UNUSED_PAD src0_sel:DWORD src1_sel:DWORD
	v_bitop3_b32 v133, v168, s20, v166 bitop3:0xc8
	v_pk_mul_f32 v[44:45], v[44:45], v[132:133]
	v_cndmask_b32_e64 v182, 0, v62, s[38:39]
	v_pk_fma_f32 v[44:45], v[48:49], v[110:111], v[44:45]
	v_lshlrev_b32_e32 v48, 16, v104
	v_and_b32_e32 v49, 0xffff0000, v104
	v_pk_fma_f32 v[36:37], v[36:37], v[48:49], v[44:45]
	v_cndmask_b32_e64 v171, 0, v60, s[36:37]
	v_pk_add_f32 v[40:41], v[40:41], v[36:37]
	v_or_b32_sdwa v62, v182, v170 dst_sel:WORD_1 dst_unused:UNUSED_PAD src0_sel:DWORD src1_sel:DWORD
	v_mul_f32_e32 v36, 0xbfb8aa3b, v40
	v_exp_f32_e32 v44, v36
	v_or_b32_e32 v36, 0x80, v222
	v_ashrrev_i32_e32 v37, 31, v36
	v_bitop3_b32 v63, v182, s20, v170 bitop3:0xc8
	v_mad_i64_i32 v[48:49], s[18:19], v220, s21, v[204:205]
	v_or_b32_sdwa v60, v171, v169 dst_sel:WORD_1 dst_unused:UNUSED_PAD src0_sel:DWORD src1_sel:DWORD
	v_bitop3_b32 v61, v171, s20, v169 bitop3:0xc8
	v_pk_mul_f32 v[46:47], v[46:47], v[62:63]
	v_mul_f32_e32 v45, 0xbfb8aa3b, v41
	v_pk_fma_f32 v[46:47], v[50:51], v[60:61], v[46:47]
	v_exp_f32_e32 v45, v45
	v_add_f32_e32 v44, 1.0, v44
	v_rcp_f32_e32 v44, v44
	v_add_f32_e32 v45, 1.0, v45
	v_rcp_f32_e32 v45, v45
	s_waitcnt vmcnt(0) lgkmcnt(0)
	v_pk_mul_f32 v[134:135], v[56:57], v[64:65] op_sel_hi:[1,0]
	v_pk_mul_f32 v[56:57], v[54:55], v[64:65] op_sel_hi:[1,0]
	v_pk_mul_f32 v[54:55], v[116:117], v[100:101]
	v_pk_mul_f32 v[58:59], v[58:59], v[64:65] op_sel_hi:[1,0]
	v_pk_fma_f32 v[54:55], v[128:129], v[66:67], v[54:55]
	v_lshlrev_b32_e32 v66, 16, v102
	v_and_b32_e32 v67, 0xffff0000, v102
	v_pk_fma_f32 v[54:55], v[120:121], v[66:67], v[54:55]
	v_and_b32_e32 v101, 0xffff0000, v103
	v_pk_add_f32 v[66:67], v[124:125], v[54:55]
	v_pk_mul_f32 v[40:41], v[40:41], v[44:45]
	v_mul_f32_e32 v54, 0xbfb8aa3b, v66
	v_exp_f32_e32 v65, v54
	v_mul_f32_e32 v54, 0xbfb8aa3b, v67
	v_exp_f32_e32 v100, v54
	v_pk_mul_f32 v[54:55], v[52:53], v[64:65] op_sel_hi:[1,0]
	v_add_f32_e32 v52, 1.0, v65
	v_pk_mul_f32 v[64:65], v[118:119], v[108:109]
	v_add_f32_e32 v53, 1.0, v100
	v_pk_fma_f32 v[64:65], v[130:131], v[106:107], v[64:65]
	v_lshlrev_b32_e32 v100, 16, v103
	v_pk_fma_f32 v[64:65], v[122:123], v[100:101], v[64:65]
	v_lshlrev_b64 v[108:109], 1, v[36:37]
	v_pk_add_f32 v[64:65], v[126:127], v[64:65]
	v_lshl_add_u64 v[48:49], v[48:49], 0, v[108:109]
	v_mul_f32_e32 v100, 0xbfb8aa3b, v64
	v_mul_f32_e32 v101, 0xbfb8aa3b, v65
	v_exp_f32_e32 v100, v100
	v_exp_f32_e32 v101, v101
	global_load_dwordx4 v[116:119], v[216:217], off offset:256
	v_rcp_f32_e32 v52, v52
	v_add_f32_e32 v100, 1.0, v100
	v_add_f32_e32 v101, 1.0, v101
	v_rcp_f32_e32 v100, v100
	v_rcp_f32_e32 v101, v101
	v_rcp_f32_e32 v53, v53
	v_pk_mul_f32 v[40:41], v[54:55], v[40:41]
	v_lshlrev_b64 v[36:37], 2, v[36:37]
	v_pk_mul_f32 v[64:65], v[64:65], v[100:101]
	global_load_dwordx4 v[100:103], v[48:49], off
	v_lshlrev_b32_e32 v48, 16, v105
	v_and_b32_e32 v49, 0xffff0000, v105
	v_pk_fma_f32 v[38:39], v[38:39], v[48:49], v[46:47]
	v_pk_mul_f32 v[52:53], v[66:67], v[52:53]
	v_pk_add_f32 v[38:39], v[42:43], v[38:39]
	v_pk_mul_f32 v[52:53], v[52:53], v[134:135]
	v_mul_f32_e32 v42, 0xbfb8aa3b, v38
	v_mul_f32_e32 v43, 0xbfb8aa3b, v39
	v_exp_f32_e32 v42, v42
	v_exp_f32_e32 v43, v43
	v_pk_mul_f32 v[58:59], v[64:65], v[58:59]
	v_cvt_pk_bf16_f32 v52, v52, v53
	v_add_f32_e32 v42, 1.0, v42
	v_add_f32_e32 v43, 1.0, v43
	v_rcp_f32_e32 v42, v42
	v_rcp_f32_e32 v43, v43
	v_cvt_pk_bf16_f32 v53, v58, v59
	v_cvt_pk_bf16_f32 v54, v40, v41
	v_mad_i64_i32 v[104:105], s[18:19], v212, s21, v[204:205]
	v_pk_mul_f32 v[38:39], v[38:39], v[42:43]
	v_lshl_add_u64 v[104:105], v[104:105], 0, v[108:109]
	v_pk_mul_f32 v[38:39], v[56:57], v[38:39]
	s_waitcnt vmcnt(0) lgkmcnt(0)
	v_and_b32_dpp v127, v116, v223 row_ror:2 row_mask:0xf bank_mask:0xf bound_ctrl:1
	v_cvt_pk_bf16_f32 v55, v38, v39
	v_mad_i64_i32 v[38:39], s[18:19], v153, s21, v[218:219]
	v_lshl_add_u64 v[110:111], v[38:39], 0, v[206:207]
	global_store_dwordx4 v[110:111], v[52:55], off
	global_load_dword v120, v[202:203], off
	v_lshl_add_u64 v[38:39], v[194:195], 0, v[36:37]
	global_load_dwordx4 v[64:67], v[208:209], off offset:512
	global_load_dwordx4 v[60:63], v[38:39], off
	v_lshl_add_u64 v[36:37], v[196:197], 0, v[36:37]
	global_load_dwordx4 v[52:55], v[36:37], off
	global_load_dwordx4 v[56:59], v[210:211], off offset:512
	global_load_dwordx4 v[48:51], v[208:209], off offset:528
	global_load_dwordx4 v[44:47], v[38:39], off offset:16
	s_nop 0
	global_load_dwordx4 v[36:39], v[36:37], off offset:16
	s_nop 0
	global_load_dwordx4 v[40:43], v[210:211], off offset:528
	v_mov_b32_dpp v123, v100 row_shr:2 row_mask:0xf bank_mask:0xf bound_ctrl:1
	v_mov_b32_dpp v121, v100 row_shr:1 row_mask:0xf bank_mask:0xf bound_ctrl:1
	v_and_b32_dpp v125, v116, v245 row_ror:1 row_mask:0xf bank_mask:0xf bound_ctrl:1
	v_or_b32_sdwa v116, v127, v123 dst_sel:WORD_1 dst_unused:UNUSED_PAD src0_sel:DWORD src1_sel:DWORD
	v_mov_b32_dpp v129, v101 row_shr:1 row_mask:0xf bank_mask:0xf bound_ctrl:1
	v_mov_b32_dpp v131, v101 row_shr:2 row_mask:0xf bank_mask:0xf bound_ctrl:1
	v_and_b32_dpp v133, v117, v245 row_ror:1 row_mask:0xf bank_mask:0xf bound_ctrl:1
	v_and_b32_dpp v134, v117, v223 row_ror:2 row_mask:0xf bank_mask:0xf bound_ctrl:1
	v_mov_b32_dpp v135, v102 row_shr:1 row_mask:0xf bank_mask:0xf bound_ctrl:1
	v_and_b32_dpp v167, v118, v245 row_ror:1 row_mask:0xf bank_mask:0xf bound_ctrl:1
	v_bitop3_b32 v117, v127, s20, v123 bitop3:0xc8
	v_or_b32_sdwa v122, v125, v121 dst_sel:WORD_1 dst_unused:UNUSED_PAD src0_sel:DWORD src1_sel:DWORD
	v_or_b32_sdwa v124, v133, v129 dst_sel:WORD_1 dst_unused:UNUSED_PAD src0_sel:DWORD src1_sel:DWORD
	v_or_b32_sdwa v126, v134, v131 dst_sel:WORD_1 dst_unused:UNUSED_PAD src0_sel:DWORD src1_sel:DWORD
	v_or_b32_sdwa v128, v167, v135 dst_sel:WORD_1 dst_unused:UNUSED_PAD src0_sel:DWORD src1_sel:DWORD
	v_bitop3_b32 v123, v125, s20, v121 bitop3:0xc8
	v_bitop3_b32 v127, v134, s20, v131 bitop3:0xc8
	v_bitop3_b32 v125, v133, s20, v129 bitop3:0xc8
	v_bitop3_b32 v129, v167, s20, v135 bitop3:0xc8
	v_mov_b32_dpp v166, v102 row_shr:2 row_mask:0xf bank_mask:0xf bound_ctrl:1
	v_and_b32_dpp v168, v118, v223 row_ror:2 row_mask:0xf bank_mask:0xf bound_ctrl:1
	v_or_b32_sdwa v118, v168, v166 dst_sel:WORD_1 dst_unused:UNUSED_PAD src0_sel:DWORD src1_sel:DWORD
	v_and_b32_dpp v171, v119, v245 row_ror:1 row_mask:0xf bank_mask:0xf bound_ctrl:1
	v_and_b32_dpp v182, v119, v223 row_ror:2 row_mask:0xf bank_mask:0xf bound_ctrl:1
	v_bitop3_b32 v119, v168, s20, v166 bitop3:0xc8
	v_mov_b32_dpp v170, v103 row_shr:2 row_mask:0xf bank_mask:0xf bound_ctrl:1
	v_mov_b32_dpp v169, v103 row_shr:1 row_mask:0xf bank_mask:0xf bound_ctrl:1
	v_or_b32_sdwa v132, v182, v170 dst_sel:WORD_1 dst_unused:UNUSED_PAD src0_sel:DWORD src1_sel:DWORD
	v_bitop3_b32 v133, v182, s20, v170 bitop3:0xc8
	v_or_b32_sdwa v130, v171, v169 dst_sel:WORD_1 dst_unused:UNUSED_PAD src0_sel:DWORD src1_sel:DWORD
	v_bitop3_b32 v131, v171, s20, v169 bitop3:0xc8
	global_load_dwordx4 v[104:107], v[104:105], off
	s_waitcnt vmcnt(0) lgkmcnt(0)
	v_pk_mul_f32 v[134:135], v[94:95], v[120:121] op_sel_hi:[1,0]
	v_pk_mul_f32 v[94:95], v[64:65], v[116:117]
	v_lshlrev_b32_e32 v116, 16, v100
	v_pk_fma_f32 v[94:95], v[60:61], v[122:123], v[94:95]
	v_and_b32_e32 v117, 0xffff0000, v100
	v_pk_fma_f32 v[94:95], v[52:53], v[116:117], v[94:95]
	v_pk_mul_f32 v[98:99], v[98:99], v[120:121] op_sel_hi:[1,0]
	v_pk_add_f32 v[94:95], v[56:57], v[94:95]
	v_pk_mul_f32 v[96:97], v[96:97], v[120:121] op_sel_hi:[1,0]
	v_mul_f32_e32 v116, 0xbfb8aa3b, v94
	v_exp_f32_e32 v121, v116
	v_mul_f32_e32 v116, 0xbfb8aa3b, v95
	v_exp_f32_e32 v122, v116
	v_and_b32_e32 v123, 0xffff0000, v101
	v_pk_mul_f32 v[116:117], v[92:93], v[120:121] op_sel_hi:[1,0]
	v_add_f32_e32 v92, 1.0, v121
	v_pk_mul_f32 v[120:121], v[66:67], v[126:127]
	v_add_f32_e32 v93, 1.0, v122
	v_pk_fma_f32 v[120:121], v[62:63], v[124:125], v[120:121]
	v_lshlrev_b32_e32 v122, 16, v101
	v_pk_fma_f32 v[120:121], v[54:55], v[122:123], v[120:121]
	v_rcp_f32_e32 v92, v92
	v_pk_add_f32 v[120:121], v[58:59], v[120:121]
	v_rcp_f32_e32 v93, v93
	v_mul_f32_e32 v122, 0xbfb8aa3b, v120
	v_mul_f32_e32 v123, 0xbfb8aa3b, v121
	v_exp_f32_e32 v122, v122
	v_exp_f32_e32 v123, v123
	v_pk_mul_f32 v[92:93], v[94:95], v[92:93]
	v_and_b32_dpp v125, v101, v221 row_ror:1 row_mask:0xf bank_mask:0xf bound_ctrl:1
	v_add_f32_e32 v122, 1.0, v122
	v_add_f32_e32 v123, 1.0, v123
	v_rcp_f32_e32 v122, v122
	v_rcp_f32_e32 v123, v123
	v_pk_mul_f32 v[92:93], v[92:93], v[96:97]
	v_pk_mul_f32 v[96:97], v[48:49], v[118:119]
	v_cvt_pk_bf16_f32 v92, v92, v93
	v_pk_mul_f32 v[94:95], v[120:121], v[122:123]
	v_pk_fma_f32 v[96:97], v[44:45], v[128:129], v[96:97]
	v_pk_mul_f32 v[94:95], v[98:99], v[94:95]
	v_lshlrev_b32_e32 v98, 16, v102
	v_and_b32_e32 v99, 0xffff0000, v102
	v_pk_fma_f32 v[96:97], v[36:37], v[98:99], v[96:97]
	v_lshlrev_b32_e32 v118, 16, v103
	v_pk_add_f32 v[96:97], v[40:41], v[96:97]
	v_and_b32_e32 v119, 0xffff0000, v103
	v_mul_f32_e32 v93, 0xbfb8aa3b, v96
	v_exp_f32_e32 v98, v93
	v_mul_f32_e32 v93, 0xbfb8aa3b, v97
	v_exp_f32_e32 v99, v93
	v_cvt_pk_bf16_f32 v93, v94, v95
	v_add_f32_e32 v94, 1.0, v98
	v_rcp_f32_e32 v94, v94
	v_add_f32_e32 v95, 1.0, v99
	v_pk_mul_f32 v[98:99], v[50:51], v[132:133]
	v_rcp_f32_e32 v95, v95
	v_pk_fma_f32 v[98:99], v[46:47], v[130:131], v[98:99]
	v_and_b32_dpp v126, v101, v213 row_ror:2 row_mask:0xf bank_mask:0xf bound_ctrl:1
	v_pk_fma_f32 v[98:99], v[38:39], v[118:119], v[98:99]
	v_pk_mul_f32 v[94:95], v[96:97], v[94:95]
	v_pk_add_f32 v[98:99], v[42:43], v[98:99]
	v_pk_mul_f32 v[94:95], v[116:117], v[94:95]
	v_mul_f32_e32 v118, 0xbfb8aa3b, v98
	v_mul_f32_e32 v119, 0xbfb8aa3b, v99
	v_exp_f32_e32 v118, v118
	v_exp_f32_e32 v119, v119
	v_cvt_pk_bf16_f32 v94, v94, v95
	v_and_b32_dpp v117, v100, v221 row_ror:1 row_mask:0xf bank_mask:0xf bound_ctrl:1
	v_add_f32_e32 v118, 1.0, v118
	v_add_f32_e32 v119, 1.0, v119
	v_rcp_f32_e32 v118, v118
	v_rcp_f32_e32 v119, v119
	v_and_b32_dpp v129, v102, v221 row_ror:1 row_mask:0xf bank_mask:0xf bound_ctrl:1
	v_and_b32_dpp v130, v102, v213 row_ror:2 row_mask:0xf bank_mask:0xf bound_ctrl:1
	v_and_b32_dpp v133, v103, v221 row_ror:1 row_mask:0xf bank_mask:0xf bound_ctrl:1
	v_pk_mul_f32 v[96:97], v[98:99], v[118:119]
	v_and_b32_dpp v119, v100, v213 row_ror:2 row_mask:0xf bank_mask:0xf bound_ctrl:1
	v_pk_mul_f32 v[96:97], v[134:135], v[96:97]
	v_and_b32_dpp v134, v103, v213 row_ror:2 row_mask:0xf bank_mask:0xf bound_ctrl:1
	v_cvt_pk_bf16_f32 v95, v96, v97
	global_store_dwordx4 v[162:163], v[92:95], off offset:256
	global_load_dword v92, v[214:215], off
	v_mov_b32_dpp v99, v104 row_shr:2 row_mask:0xf bank_mask:0xf bound_ctrl:1
	v_mov_b32_dpp v93, v104 row_shr:1 row_mask:0xf bank_mask:0xf bound_ctrl:1
	v_or_b32_sdwa v100, v119, v99 dst_sel:WORD_1 dst_unused:UNUSED_PAD src0_sel:DWORD src1_sel:DWORD
	v_mov_b32_dpp v121, v105 row_shr:1 row_mask:0xf bank_mask:0xf bound_ctrl:1
	v_mov_b32_dpp v123, v105 row_shr:2 row_mask:0xf bank_mask:0xf bound_ctrl:1
	v_mov_b32_dpp v127, v106 row_shr:1 row_mask:0xf bank_mask:0xf bound_ctrl:1
	v_bitop3_b32 v101, v119, s20, v99 bitop3:0xc8
	v_or_b32_sdwa v98, v117, v93 dst_sel:WORD_1 dst_unused:UNUSED_PAD src0_sel:DWORD src1_sel:DWORD
	v_or_b32_sdwa v116, v125, v121 dst_sel:WORD_1 dst_unused:UNUSED_PAD src0_sel:DWORD src1_sel:DWORD
	v_or_b32_sdwa v118, v126, v123 dst_sel:WORD_1 dst_unused:UNUSED_PAD src0_sel:DWORD src1_sel:DWORD
	v_or_b32_sdwa v120, v129, v127 dst_sel:WORD_1 dst_unused:UNUSED_PAD src0_sel:DWORD src1_sel:DWORD
	v_bitop3_b32 v99, v117, s20, v93 bitop3:0xc8
	v_bitop3_b32 v119, v126, s20, v123 bitop3:0xc8
	v_bitop3_b32 v117, v125, s20, v121 bitop3:0xc8
	v_bitop3_b32 v121, v129, s20, v127 bitop3:0xc8
	v_mov_b32_dpp v128, v106 row_shr:2 row_mask:0xf bank_mask:0xf bound_ctrl:1
	v_or_b32_sdwa v102, v130, v128 dst_sel:WORD_1 dst_unused:UNUSED_PAD src0_sel:DWORD src1_sel:DWORD
	v_bitop3_b32 v103, v130, s20, v128 bitop3:0xc8
	v_mov_b32_dpp v132, v107 row_shr:2 row_mask:0xf bank_mask:0xf bound_ctrl:1
	v_mov_b32_dpp v131, v107 row_shr:1 row_mask:0xf bank_mask:0xf bound_ctrl:1
	v_or_b32_sdwa v124, v134, v132 dst_sel:WORD_1 dst_unused:UNUSED_PAD src0_sel:DWORD src1_sel:DWORD
	v_bitop3_b32 v125, v134, s20, v132 bitop3:0xc8
	v_or_b32_sdwa v122, v133, v131 dst_sel:WORD_1 dst_unused:UNUSED_PAD src0_sel:DWORD src1_sel:DWORD
	v_bitop3_b32 v123, v133, s20, v131 bitop3:0xc8
	v_mad_i64_i32 v[94:95], s[18:19], v160, s21, v[204:205]
	v_lshl_add_u64 v[94:95], v[94:95], 0, v[108:109]
	global_load_dwordx4 v[94:97], v[94:95], off
	s_waitcnt vmcnt(0) lgkmcnt(0)
	v_pk_mul_f32 v[126:127], v[86:87], v[92:93] op_sel_hi:[1,0]
	v_pk_mul_f32 v[86:87], v[64:65], v[100:101]
	v_pk_mul_f32 v[90:91], v[90:91], v[92:93] op_sel_hi:[1,0]
	v_pk_fma_f32 v[86:87], v[60:61], v[98:99], v[86:87]
	v_lshlrev_b32_e32 v98, 16, v104
	v_and_b32_e32 v99, 0xffff0000, v104
	v_pk_fma_f32 v[86:87], v[52:53], v[98:99], v[86:87]
	v_pk_mul_f32 v[88:89], v[88:89], v[92:93] op_sel_hi:[1,0]
	v_pk_add_f32 v[86:87], v[56:57], v[86:87]
	v_lshlrev_b32_e32 v100, 16, v105
	v_mul_f32_e32 v93, 0xbfb8aa3b, v86
	v_exp_f32_e32 v98, v93
	v_mul_f32_e32 v93, 0xbfb8aa3b, v87
	v_exp_f32_e32 v99, v93
	v_pk_mul_f32 v[92:93], v[84:85], v[92:93] op_sel_hi:[1,0]
	v_add_f32_e32 v84, 1.0, v98
	v_and_b32_e32 v101, 0xffff0000, v105
	v_add_f32_e32 v85, 1.0, v99
	v_pk_mul_f32 v[98:99], v[66:67], v[118:119]
	v_rcp_f32_e32 v84, v84
	v_pk_fma_f32 v[98:99], v[62:63], v[116:117], v[98:99]
	v_rcp_f32_e32 v85, v85
	v_pk_fma_f32 v[98:99], v[54:55], v[100:101], v[98:99]
	v_and_b32_dpp v117, v105, v164 row_ror:1 row_mask:0xf bank_mask:0xf bound_ctrl:1
	v_pk_add_f32 v[98:99], v[58:59], v[98:99]
	v_pk_mul_f32 v[84:85], v[86:87], v[84:85]
	v_mul_f32_e32 v100, 0xbfb8aa3b, v98
	v_mul_f32_e32 v101, 0xbfb8aa3b, v99
	v_exp_f32_e32 v100, v100
	v_exp_f32_e32 v101, v101
	v_pk_mul_f32 v[84:85], v[84:85], v[88:89]
	v_pk_mul_f32 v[88:89], v[48:49], v[102:103]
	v_add_f32_e32 v100, 1.0, v100
	v_add_f32_e32 v101, 1.0, v101
	v_rcp_f32_e32 v100, v100
	v_rcp_f32_e32 v101, v101
	v_pk_fma_f32 v[88:89], v[44:45], v[120:121], v[88:89]
	v_cvt_pk_bf16_f32 v84, v84, v85
	v_and_b32_dpp v105, v105, v161 row_ror:2 row_mask:0xf bank_mask:0xf bound_ctrl:1
	v_pk_mul_f32 v[86:87], v[98:99], v[100:101]
	v_lshlrev_b32_e32 v98, 16, v107
	v_pk_mul_f32 v[86:87], v[90:91], v[86:87]
	v_lshlrev_b32_e32 v90, 16, v106
	v_and_b32_e32 v91, 0xffff0000, v106
	v_pk_fma_f32 v[88:89], v[36:37], v[90:91], v[88:89]
	v_and_b32_e32 v99, 0xffff0000, v107
	v_pk_add_f32 v[88:89], v[40:41], v[88:89]
	v_and_b32_dpp v120, v106, v164 row_ror:1 row_mask:0xf bank_mask:0xf bound_ctrl:1
	v_mul_f32_e32 v85, 0xbfb8aa3b, v88
	v_exp_f32_e32 v90, v85
	v_mul_f32_e32 v85, 0xbfb8aa3b, v89
	v_exp_f32_e32 v91, v85
	v_cvt_pk_bf16_f32 v85, v86, v87
	v_add_f32_e32 v86, 1.0, v90
	v_rcp_f32_e32 v86, v86
	v_add_f32_e32 v87, 1.0, v91
	v_pk_mul_f32 v[90:91], v[50:51], v[124:125]
	v_rcp_f32_e32 v87, v87
	v_pk_fma_f32 v[90:91], v[46:47], v[122:123], v[90:91]
	v_and_b32_dpp v121, v106, v161 row_ror:2 row_mask:0xf bank_mask:0xf bound_ctrl:1
	v_pk_fma_f32 v[90:91], v[38:39], v[98:99], v[90:91]
	v_pk_mul_f32 v[86:87], v[88:89], v[86:87]
	v_pk_add_f32 v[90:91], v[42:43], v[90:91]
	v_pk_mul_f32 v[86:87], v[92:93], v[86:87]
	v_mul_f32_e32 v98, 0xbfb8aa3b, v90
	v_mul_f32_e32 v99, 0xbfb8aa3b, v91
	v_exp_f32_e32 v98, v98
	v_exp_f32_e32 v99, v99
	v_cvt_pk_bf16_f32 v86, v86, v87
	v_and_b32_dpp v93, v104, v161 row_ror:2 row_mask:0xf bank_mask:0xf bound_ctrl:1
	v_add_f32_e32 v98, 1.0, v98
	v_add_f32_e32 v99, 1.0, v99
	v_rcp_f32_e32 v98, v98
	v_rcp_f32_e32 v99, v99
	v_and_b32_dpp v124, v107, v164 row_ror:1 row_mask:0xf bank_mask:0xf bound_ctrl:1
	v_and_b32_dpp v107, v107, v161 row_ror:2 row_mask:0xf bank_mask:0xf bound_ctrl:1
	v_pk_mul_f32 v[88:89], v[90:91], v[98:99]
	s_nop 0
	v_pk_mul_f32 v[88:89], v[126:127], v[88:89]
	v_and_b32_dpp v99, v104, v164 row_ror:1 row_mask:0xf bank_mask:0xf bound_ctrl:1
	v_cvt_pk_bf16_f32 v87, v88, v89
	global_store_dwordx4 v[148:149], v[84:87], off offset:256
	global_load_dword v88, v[150:151], off
	s_nop 0
	v_mad_i64_i32 v[84:85], s[18:19], v152, s21, v[204:205]
	v_lshl_add_u64 v[84:85], v[84:85], 0, v[108:109]
	global_load_dwordx4 v[84:87], v[84:85], off
	v_mov_b32_dpp v91, v94 row_shr:2 row_mask:0xf bank_mask:0xf bound_ctrl:1
	v_mov_b32_dpp v89, v94 row_shr:1 row_mask:0xf bank_mask:0xf bound_ctrl:1
	v_or_b32_sdwa v92, v93, v91 dst_sel:WORD_1 dst_unused:UNUSED_PAD src0_sel:DWORD src1_sel:DWORD
	v_mov_b32_dpp v103, v95 row_shr:1 row_mask:0xf bank_mask:0xf bound_ctrl:1
	v_mov_b32_dpp v101, v95 row_shr:2 row_mask:0xf bank_mask:0xf bound_ctrl:1
	v_mov_b32_dpp v118, v96 row_shr:1 row_mask:0xf bank_mask:0xf bound_ctrl:1
	v_mov_b32_dpp v119, v96 row_shr:2 row_mask:0xf bank_mask:0xf bound_ctrl:1
	v_bitop3_b32 v93, v93, s20, v91 bitop3:0xc8
	v_or_b32_sdwa v90, v99, v89 dst_sel:WORD_1 dst_unused:UNUSED_PAD src0_sel:DWORD src1_sel:DWORD
	v_or_b32_sdwa v98, v117, v103 dst_sel:WORD_1 dst_unused:UNUSED_PAD src0_sel:DWORD src1_sel:DWORD
	v_or_b32_sdwa v100, v105, v101 dst_sel:WORD_1 dst_unused:UNUSED_PAD src0_sel:DWORD src1_sel:DWORD
	v_or_b32_sdwa v102, v120, v118 dst_sel:WORD_1 dst_unused:UNUSED_PAD src0_sel:DWORD src1_sel:DWORD
	v_or_b32_sdwa v104, v121, v119 dst_sel:WORD_1 dst_unused:UNUSED_PAD src0_sel:DWORD src1_sel:DWORD
	v_bitop3_b32 v91, v99, s20, v89 bitop3:0xc8
	v_bitop3_b32 v101, v105, s20, v101 bitop3:0xc8
	v_bitop3_b32 v99, v117, s20, v103 bitop3:0xc8
	v_bitop3_b32 v105, v121, s20, v119 bitop3:0xc8
	v_bitop3_b32 v103, v120, s20, v118 bitop3:0xc8
	v_mov_b32_dpp v123, v97 row_shr:2 row_mask:0xf bank_mask:0xf bound_ctrl:1
	v_mov_b32_dpp v122, v97 row_shr:1 row_mask:0xf bank_mask:0xf bound_ctrl:1
	v_or_b32_sdwa v116, v107, v123 dst_sel:WORD_1 dst_unused:UNUSED_PAD src0_sel:DWORD src1_sel:DWORD
	v_bitop3_b32 v117, v107, s20, v123 bitop3:0xc8
	v_or_b32_sdwa v106, v124, v122 dst_sel:WORD_1 dst_unused:UNUSED_PAD src0_sel:DWORD src1_sel:DWORD
	v_bitop3_b32 v107, v124, s20, v122 bitop3:0xc8
	s_waitcnt vmcnt(0) lgkmcnt(0)
	v_pk_mul_f32 v[118:119], v[78:79], v[88:89] op_sel_hi:[1,0]
	v_pk_mul_f32 v[78:79], v[64:65], v[92:93]
	v_pk_mul_f32 v[82:83], v[82:83], v[88:89] op_sel_hi:[1,0]
	v_pk_fma_f32 v[78:79], v[60:61], v[90:91], v[78:79]
	v_lshlrev_b32_e32 v90, 16, v94
	v_and_b32_e32 v91, 0xffff0000, v94
	v_pk_fma_f32 v[78:79], v[52:53], v[90:91], v[78:79]
	v_pk_mul_f32 v[80:81], v[80:81], v[88:89] op_sel_hi:[1,0]
	v_pk_add_f32 v[78:79], v[56:57], v[78:79]
	v_lshlrev_b32_e32 v92, 16, v95
	v_mul_f32_e32 v89, 0xbfb8aa3b, v78
	v_exp_f32_e32 v90, v89
	v_mul_f32_e32 v89, 0xbfb8aa3b, v79
	v_exp_f32_e32 v91, v89
	v_pk_mul_f32 v[88:89], v[76:77], v[88:89] op_sel_hi:[1,0]
	v_add_f32_e32 v76, 1.0, v90
	v_and_b32_e32 v93, 0xffff0000, v95
	v_add_f32_e32 v77, 1.0, v91
	v_pk_mul_f32 v[90:91], v[66:67], v[100:101]
	v_rcp_f32_e32 v76, v76
	v_pk_fma_f32 v[90:91], v[62:63], v[98:99], v[90:91]
	v_rcp_f32_e32 v77, v77
	v_pk_fma_f32 v[90:91], v[54:55], v[92:93], v[90:91]
	v_mov_b32_dpp v98, v86 row_shr:1 row_mask:0xf bank_mask:0xf bound_ctrl:1
	v_pk_add_f32 v[90:91], v[58:59], v[90:91]
	v_pk_mul_f32 v[76:77], v[78:79], v[76:77]
	v_mul_f32_e32 v92, 0xbfb8aa3b, v90
	v_mul_f32_e32 v93, 0xbfb8aa3b, v91
	v_exp_f32_e32 v92, v92
	v_exp_f32_e32 v93, v93
	v_pk_mul_f32 v[76:77], v[76:77], v[80:81]
	v_pk_mul_f32 v[80:81], v[48:49], v[104:105]
	v_add_f32_e32 v92, 1.0, v92
	v_add_f32_e32 v93, 1.0, v93
	v_rcp_f32_e32 v92, v92
	v_rcp_f32_e32 v93, v93
	v_pk_fma_f32 v[80:81], v[44:45], v[102:103], v[80:81]
	v_cvt_pk_bf16_f32 v76, v76, v77
	v_mov_b32_dpp v99, v86 row_shr:2 row_mask:0xf bank_mask:0xf bound_ctrl:1
	v_pk_mul_f32 v[78:79], v[90:91], v[92:93]
	v_lshlrev_b32_e32 v90, 16, v97
	v_pk_mul_f32 v[78:79], v[82:83], v[78:79]
	v_lshlrev_b32_e32 v82, 16, v96
	v_and_b32_e32 v83, 0xffff0000, v96
	v_pk_fma_f32 v[80:81], v[36:37], v[82:83], v[80:81]
	v_and_b32_e32 v91, 0xffff0000, v97
	v_pk_add_f32 v[80:81], v[40:41], v[80:81]
	v_mov_b32_dpp v92, v96 row_ror:2 row_mask:0xf bank_mask:0xf bound_ctrl:1
	v_mul_f32_e32 v77, 0xbfb8aa3b, v80
	v_exp_f32_e32 v82, v77
	v_mul_f32_e32 v77, 0xbfb8aa3b, v81
	v_exp_f32_e32 v83, v77
	v_cvt_pk_bf16_f32 v77, v78, v79
	v_add_f32_e32 v78, 1.0, v82
	v_rcp_f32_e32 v78, v78
	v_add_f32_e32 v79, 1.0, v83
	v_pk_mul_f32 v[82:83], v[50:51], v[116:117]
	v_rcp_f32_e32 v79, v79
	v_pk_fma_f32 v[82:83], v[46:47], v[106:107], v[82:83]
	v_cndmask_b32_e64 v101, 0, v92, s[38:39]
	v_pk_fma_f32 v[82:83], v[38:39], v[90:91], v[82:83]
	v_pk_mul_f32 v[78:79], v[80:81], v[78:79]
	v_pk_add_f32 v[82:83], v[42:43], v[82:83]
	v_pk_mul_f32 v[78:79], v[88:89], v[78:79]
	v_mul_f32_e32 v90, 0xbfb8aa3b, v82
	v_mul_f32_e32 v91, 0xbfb8aa3b, v83
	v_exp_f32_e32 v90, v90
	v_exp_f32_e32 v91, v91
	v_cvt_pk_bf16_f32 v78, v78, v79
	v_or_b32_sdwa v92, v101, v99 dst_sel:WORD_1 dst_unused:UNUSED_PAD src0_sel:DWORD src1_sel:DWORD
	v_add_f32_e32 v90, 1.0, v90
	v_add_f32_e32 v91, 1.0, v91
	v_rcp_f32_e32 v90, v90
	v_rcp_f32_e32 v91, v91
	v_mov_b32_dpp v88, v95 row_ror:2 row_mask:0xf bank_mask:0xf bound_ctrl:1
	v_mov_b32_dpp v89, v85 row_shr:2 row_mask:0xf bank_mask:0xf bound_ctrl:1
	v_mov_b32_dpp v103, v87 row_shr:2 row_mask:0xf bank_mask:0xf bound_ctrl:1
	v_pk_mul_f32 v[80:81], v[82:83], v[90:91]
	v_mov_b32_dpp v82, v95 row_ror:1 row_mask:0xf bank_mask:0xf bound_ctrl:1
	v_pk_mul_f32 v[80:81], v[118:119], v[80:81]
	v_mov_b32_dpp v90, v96 row_ror:1 row_mask:0xf bank_mask:0xf bound_ctrl:1
	v_cvt_pk_bf16_f32 v79, v80, v81
	global_store_dwordx4 v[142:143], v[76:79], off offset:256
	global_load_dword v76, v[144:145], off
	v_mov_b32_dpp v80, v94 row_ror:2 row_mask:0xf bank_mask:0xf bound_ctrl:1
	v_mov_b32_dpp v78, v94 row_ror:1 row_mask:0xf bank_mask:0xf bound_ctrl:1
	v_mov_b32_dpp v79, v84 row_shr:2 row_mask:0xf bank_mask:0xf bound_ctrl:1
	v_cndmask_b32_e64 v81, 0, v80, s[38:39]
	v_mov_b32_dpp v77, v84 row_shr:1 row_mask:0xf bank_mask:0xf bound_ctrl:1
	v_cndmask_b32_e64 v83, 0, v78, s[36:37]
	v_or_b32_sdwa v80, v81, v79 dst_sel:WORD_1 dst_unused:UNUSED_PAD src0_sel:DWORD src1_sel:DWORD
	v_mov_b32_dpp v91, v85 row_shr:1 row_mask:0xf bank_mask:0xf bound_ctrl:1
	v_cndmask_b32_e64 v93, 0, v82, s[36:37]
	v_cndmask_b32_e64 v100, 0, v90, s[36:37]
	v_bitop3_b32 v81, v81, s20, v79 bitop3:0xc8
	v_or_b32_sdwa v78, v83, v77 dst_sel:WORD_1 dst_unused:UNUSED_PAD src0_sel:DWORD src1_sel:DWORD
	v_or_b32_sdwa v82, v93, v91 dst_sel:WORD_1 dst_unused:UNUSED_PAD src0_sel:DWORD src1_sel:DWORD
	v_or_b32_sdwa v90, v100, v98 dst_sel:WORD_1 dst_unused:UNUSED_PAD src0_sel:DWORD src1_sel:DWORD
	v_bitop3_b32 v79, v83, s20, v77 bitop3:0xc8
	v_bitop3_b32 v83, v93, s20, v91 bitop3:0xc8
	v_bitop3_b32 v93, v101, s20, v99 bitop3:0xc8
	v_bitop3_b32 v91, v100, s20, v98 bitop3:0xc8
	v_cndmask_b32_e64 v95, 0, v88, s[38:39]
	v_or_b32_sdwa v88, v95, v89 dst_sel:WORD_1 dst_unused:UNUSED_PAD src0_sel:DWORD src1_sel:DWORD
	v_bitop3_b32 v89, v95, s20, v89 bitop3:0xc8
	v_mov_b32_dpp v96, v97 row_ror:2 row_mask:0xf bank_mask:0xf bound_ctrl:1
	v_mov_b32_dpp v94, v97 row_ror:1 row_mask:0xf bank_mask:0xf bound_ctrl:1
	v_cndmask_b32_e64 v97, 0, v96, s[38:39]
	v_mov_b32_dpp v102, v87 row_shr:1 row_mask:0xf bank_mask:0xf bound_ctrl:1
	v_cndmask_b32_e64 v104, 0, v94, s[36:37]
	v_or_b32_sdwa v96, v97, v103 dst_sel:WORD_1 dst_unused:UNUSED_PAD src0_sel:DWORD src1_sel:DWORD
	v_bitop3_b32 v97, v97, s20, v103 bitop3:0xc8
	v_or_b32_sdwa v94, v104, v102 dst_sel:WORD_1 dst_unused:UNUSED_PAD src0_sel:DWORD src1_sel:DWORD
	v_bitop3_b32 v95, v104, s20, v102 bitop3:0xc8
	s_waitcnt vmcnt(0) lgkmcnt(0)
	v_pk_mul_f32 v[98:99], v[70:71], v[76:77] op_sel_hi:[1,0]
	v_pk_mul_f32 v[70:71], v[64:65], v[80:81]
	v_pk_mul_f32 v[74:75], v[74:75], v[76:77] op_sel_hi:[1,0]
	v_pk_fma_f32 v[70:71], v[60:61], v[78:79], v[70:71]
	v_lshlrev_b32_e32 v78, 16, v84
	v_and_b32_e32 v79, 0xffff0000, v84
	v_pk_fma_f32 v[70:71], v[52:53], v[78:79], v[70:71]
	v_pk_mul_f32 v[72:73], v[72:73], v[76:77] op_sel_hi:[1,0]
	v_pk_add_f32 v[70:71], v[56:57], v[70:71]
	v_lshlrev_b32_e32 v80, 16, v85
	v_mul_f32_e32 v77, 0xbfb8aa3b, v70
	v_exp_f32_e32 v78, v77
	v_mul_f32_e32 v77, 0xbfb8aa3b, v71
	v_exp_f32_e32 v79, v77
	v_pk_mul_f32 v[76:77], v[68:69], v[76:77] op_sel_hi:[1,0]
	v_add_f32_e32 v68, 1.0, v78
	v_and_b32_e32 v81, 0xffff0000, v85
	v_add_f32_e32 v69, 1.0, v79
	v_pk_mul_f32 v[78:79], v[66:67], v[88:89]
	v_rcp_f32_e32 v68, v68
	v_pk_fma_f32 v[78:79], v[62:63], v[82:83], v[78:79]
	v_rcp_f32_e32 v69, v69
	v_pk_fma_f32 v[78:79], v[54:55], v[80:81], v[78:79]
	v_pk_mul_f32 v[68:69], v[70:71], v[68:69]
	v_pk_add_f32 v[78:79], v[58:59], v[78:79]
	v_pk_mul_f32 v[68:69], v[68:69], v[72:73]
	v_mul_f32_e32 v80, 0xbfb8aa3b, v78
	v_mul_f32_e32 v81, 0xbfb8aa3b, v79
	v_exp_f32_e32 v80, v80
	v_exp_f32_e32 v81, v81
	v_pk_mul_f32 v[72:73], v[48:49], v[92:93]
	v_cvt_pk_bf16_f32 v68, v68, v69
	v_add_f32_e32 v80, 1.0, v80
	v_add_f32_e32 v81, 1.0, v81
	v_rcp_f32_e32 v80, v80
	v_rcp_f32_e32 v81, v81
	v_pk_fma_f32 v[72:73], v[44:45], v[90:91], v[72:73]
	v_pk_mul_f32 v[70:71], v[78:79], v[80:81]
	s_nop 0
	v_pk_mul_f32 v[70:71], v[74:75], v[70:71]
	v_lshlrev_b32_e32 v74, 16, v86
	v_and_b32_e32 v75, 0xffff0000, v86
	v_pk_fma_f32 v[72:73], v[36:37], v[74:75], v[72:73]
	v_lshlrev_b32_e32 v78, 16, v87
	v_pk_add_f32 v[72:73], v[40:41], v[72:73]
	v_and_b32_e32 v79, 0xffff0000, v87
	v_mul_f32_e32 v69, 0xbfb8aa3b, v72
	v_exp_f32_e32 v74, v69
	v_mul_f32_e32 v69, 0xbfb8aa3b, v73
	v_exp_f32_e32 v75, v69
	v_cvt_pk_bf16_f32 v69, v70, v71
	v_add_f32_e32 v70, 1.0, v74
	v_rcp_f32_e32 v70, v70
	v_add_f32_e32 v71, 1.0, v75
	v_pk_mul_f32 v[74:75], v[50:51], v[96:97]
	v_rcp_f32_e32 v71, v71
	v_pk_fma_f32 v[74:75], v[46:47], v[94:95], v[74:75]
	v_pk_mul_f32 v[70:71], v[72:73], v[70:71]
	v_pk_fma_f32 v[74:75], v[38:39], v[78:79], v[74:75]
	v_pk_mul_f32 v[70:71], v[76:77], v[70:71]
	v_pk_add_f32 v[74:75], v[42:43], v[74:75]
	v_cvt_pk_bf16_f32 v70, v70, v71
	v_mul_f32_e32 v78, 0xbfb8aa3b, v74
	v_mul_f32_e32 v79, 0xbfb8aa3b, v75
	v_exp_f32_e32 v78, v78
	v_exp_f32_e32 v79, v79
	v_mad_i64_i32 v[76:77], s[18:19], v159, s21, v[204:205]
	v_add_f32_e32 v78, 1.0, v78
	v_add_f32_e32 v79, 1.0, v79
	v_rcp_f32_e32 v78, v78
	v_rcp_f32_e32 v79, v79
	v_lshl_add_u64 v[76:77], v[76:77], 0, v[108:109]
	v_pk_mul_f32 v[72:73], v[74:75], v[78:79]
	s_nop 0
	v_pk_mul_f32 v[72:73], v[98:99], v[72:73]
	s_nop 0
	v_cvt_pk_bf16_f32 v71, v72, v73
	v_mad_i64_i32 v[72:73], s[18:19], v165, s21, v[204:205]
	v_lshl_add_u64 v[72:73], v[72:73], 0, v[108:109]
	global_load_dwordx4 v[72:75], v[72:73], off
	s_nop 0
	global_store_dwordx4 v[136:137], v[68:71], off offset:256
	global_load_dwordx4 v[68:71], v[140:141], off offset:256
	s_nop 0
	global_load_dword v80, v[202:203], off offset:512
	s_waitcnt vmcnt(0) lgkmcnt(0)
	v_mov_b32_dpp v83, v72 row_shr:2 row_mask:0xf bank_mask:0xf bound_ctrl:1
	v_mov_b32_dpp v81, v72 row_shr:1 row_mask:0xf bank_mask:0xf bound_ctrl:1
	v_and_b32_dpp v87, v68, v157 row_ror:2 row_mask:0xf bank_mask:0xf bound_ctrl:1
	v_and_b32_dpp v85, v68, v158 row_ror:1 row_mask:0xf bank_mask:0xf bound_ctrl:1
	v_or_b32_sdwa v68, v87, v83 dst_sel:WORD_1 dst_unused:UNUSED_PAD src0_sel:DWORD src1_sel:DWORD
	v_mov_b32_dpp v89, v73 row_shr:1 row_mask:0xf bank_mask:0xf bound_ctrl:1
	v_mov_b32_dpp v91, v73 row_shr:2 row_mask:0xf bank_mask:0xf bound_ctrl:1
	v_and_b32_dpp v93, v69, v158 row_ror:1 row_mask:0xf bank_mask:0xf bound_ctrl:1
	v_and_b32_dpp v94, v69, v157 row_ror:2 row_mask:0xf bank_mask:0xf bound_ctrl:1
	v_mov_b32_dpp v95, v74 row_shr:1 row_mask:0xf bank_mask:0xf bound_ctrl:1
	v_and_b32_dpp v97, v70, v158 row_ror:1 row_mask:0xf bank_mask:0xf bound_ctrl:1
	v_bitop3_b32 v69, v87, s20, v83 bitop3:0xc8
	v_or_b32_sdwa v82, v85, v81 dst_sel:WORD_1 dst_unused:UNUSED_PAD src0_sel:DWORD src1_sel:DWORD
	v_or_b32_sdwa v84, v93, v89 dst_sel:WORD_1 dst_unused:UNUSED_PAD src0_sel:DWORD src1_sel:DWORD
	v_or_b32_sdwa v86, v94, v91 dst_sel:WORD_1 dst_unused:UNUSED_PAD src0_sel:DWORD src1_sel:DWORD
	v_or_b32_sdwa v88, v97, v95 dst_sel:WORD_1 dst_unused:UNUSED_PAD src0_sel:DWORD src1_sel:DWORD
	v_bitop3_b32 v83, v85, s20, v81 bitop3:0xc8
	v_bitop3_b32 v87, v94, s20, v91 bitop3:0xc8
	v_bitop3_b32 v85, v93, s20, v89 bitop3:0xc8
	v_bitop3_b32 v89, v97, s20, v95 bitop3:0xc8
	v_pk_mul_f32 v[94:95], v[30:31], v[80:81] op_sel_hi:[1,0]
	v_pk_mul_f32 v[30:31], v[64:65], v[68:69]
	v_lshlrev_b32_e32 v68, 16, v72
	v_pk_fma_f32 v[30:31], v[60:61], v[82:83], v[30:31]
	v_and_b32_e32 v69, 0xffff0000, v72
	v_pk_fma_f32 v[30:31], v[52:53], v[68:69], v[30:31]
	v_pk_mul_f32 v[34:35], v[34:35], v[80:81] op_sel_hi:[1,0]
	v_pk_add_f32 v[30:31], v[56:57], v[30:31]
	v_pk_mul_f32 v[32:33], v[32:33], v[80:81] op_sel_hi:[1,0]
	v_mul_f32_e32 v68, 0xbfb8aa3b, v30
	v_exp_f32_e32 v81, v68
	v_mul_f32_e32 v68, 0xbfb8aa3b, v31
	v_exp_f32_e32 v82, v68
	v_and_b32_e32 v83, 0xffff0000, v73
	v_pk_mul_f32 v[68:69], v[28:29], v[80:81] op_sel_hi:[1,0]
	v_add_f32_e32 v28, 1.0, v81
	v_pk_mul_f32 v[80:81], v[66:67], v[86:87]
	v_add_f32_e32 v29, 1.0, v82
	v_pk_fma_f32 v[80:81], v[62:63], v[84:85], v[80:81]
	v_lshlrev_b32_e32 v82, 16, v73
	v_pk_fma_f32 v[80:81], v[54:55], v[82:83], v[80:81]
	v_rcp_f32_e32 v28, v28
	v_pk_add_f32 v[80:81], v[58:59], v[80:81]
	v_rcp_f32_e32 v29, v29
	v_mul_f32_e32 v82, 0xbfb8aa3b, v80
	v_mul_f32_e32 v83, 0xbfb8aa3b, v81
	v_exp_f32_e32 v82, v82
	v_exp_f32_e32 v83, v83
	v_mov_b32_dpp v96, v74 row_shr:2 row_mask:0xf bank_mask:0xf bound_ctrl:1
	v_and_b32_dpp v98, v70, v157 row_ror:2 row_mask:0xf bank_mask:0xf bound_ctrl:1
	v_add_f32_e32 v82, 1.0, v82
	v_add_f32_e32 v83, 1.0, v83
	v_rcp_f32_e32 v82, v82
	v_rcp_f32_e32 v83, v83
	v_or_b32_sdwa v70, v98, v96 dst_sel:WORD_1 dst_unused:UNUSED_PAD src0_sel:DWORD src1_sel:DWORD
	v_and_b32_dpp v101, v71, v158 row_ror:1 row_mask:0xf bank_mask:0xf bound_ctrl:1
	v_and_b32_dpp v102, v71, v157 row_ror:2 row_mask:0xf bank_mask:0xf bound_ctrl:1
	v_bitop3_b32 v71, v98, s20, v96 bitop3:0xc8
	v_pk_mul_f32 v[28:29], v[30:31], v[28:29]
	v_pk_mul_f32 v[30:31], v[80:81], v[82:83]
	v_pk_mul_f32 v[28:29], v[28:29], v[32:33]
	v_pk_mul_f32 v[32:33], v[48:49], v[70:71]
	v_pk_mul_f32 v[30:31], v[34:35], v[30:31]
	v_pk_fma_f32 v[32:33], v[44:45], v[88:89], v[32:33]
	v_lshlrev_b32_e32 v34, 16, v74
	v_and_b32_e32 v35, 0xffff0000, v74
	v_pk_fma_f32 v[32:33], v[36:37], v[34:35], v[32:33]
	v_cvt_pk_bf16_f32 v28, v28, v29
	v_pk_add_f32 v[32:33], v[40:41], v[32:33]
	v_mov_b32_dpp v100, v75 row_shr:2 row_mask:0xf bank_mask:0xf bound_ctrl:1
	v_mul_f32_e32 v29, 0xbfb8aa3b, v32
	v_exp_f32_e32 v34, v29
	v_mul_f32_e32 v29, 0xbfb8aa3b, v33
	v_exp_f32_e32 v35, v29
	v_mov_b32_dpp v99, v75 row_shr:1 row_mask:0xf bank_mask:0xf bound_ctrl:1
	v_or_b32_sdwa v92, v102, v100 dst_sel:WORD_1 dst_unused:UNUSED_PAD src0_sel:DWORD src1_sel:DWORD
	v_bitop3_b32 v93, v102, s20, v100 bitop3:0xc8
	v_or_b32_sdwa v90, v101, v99 dst_sel:WORD_1 dst_unused:UNUSED_PAD src0_sel:DWORD src1_sel:DWORD
	v_bitop3_b32 v91, v101, s20, v99 bitop3:0xc8
	v_cvt_pk_bf16_f32 v29, v30, v31
	v_add_f32_e32 v30, 1.0, v34
	v_add_f32_e32 v31, 1.0, v35
	v_pk_mul_f32 v[34:35], v[50:51], v[92:93]
	v_lshlrev_b32_e32 v70, 16, v75
	v_pk_fma_f32 v[34:35], v[46:47], v[90:91], v[34:35]
	v_and_b32_e32 v71, 0xffff0000, v75
	v_pk_fma_f32 v[34:35], v[38:39], v[70:71], v[34:35]
	v_rcp_f32_e32 v30, v30
	v_pk_add_f32 v[34:35], v[42:43], v[34:35]
	v_rcp_f32_e32 v31, v31
	v_mul_f32_e32 v70, 0xbfb8aa3b, v34
	v_mul_f32_e32 v71, 0xbfb8aa3b, v35
	v_exp_f32_e32 v70, v70
	v_exp_f32_e32 v71, v71
	v_pk_mul_f32 v[30:31], v[32:33], v[30:31]
	global_load_dwordx4 v[76:79], v[76:77], off
	v_add_f32_e32 v70, 1.0, v70
	v_add_f32_e32 v71, 1.0, v71
	v_rcp_f32_e32 v70, v70
	v_rcp_f32_e32 v71, v71
	v_pk_mul_f32 v[30:31], v[68:69], v[30:31]
	v_and_b32_dpp v69, v72, v154 row_ror:2 row_mask:0xf bank_mask:0xf bound_ctrl:1
	v_cvt_pk_bf16_f32 v30, v30, v31
	v_pk_mul_f32 v[32:33], v[34:35], v[70:71]
	v_and_b32_dpp v71, v72, v155 row_ror:1 row_mask:0xf bank_mask:0xf bound_ctrl:1
	v_pk_mul_f32 v[32:33], v[94:95], v[32:33]
	v_and_b32_dpp v85, v73, v155 row_ror:1 row_mask:0xf bank_mask:0xf bound_ctrl:1
	v_cvt_pk_bf16_f32 v31, v32, v33
	global_store_dwordx4 v[138:139], v[28:31], off offset:256
	global_load_dword v32, v[202:203], off offset:576
	v_and_b32_dpp v88, v74, v155 row_ror:1 row_mask:0xf bank_mask:0xf bound_ctrl:1
	v_and_b32_dpp v89, v74, v154 row_ror:2 row_mask:0xf bank_mask:0xf bound_ctrl:1
	v_and_b32_dpp v92, v75, v155 row_ror:1 row_mask:0xf bank_mask:0xf bound_ctrl:1
	v_and_b32_dpp v93, v75, v154 row_ror:2 row_mask:0xf bank_mask:0xf bound_ctrl:1
	v_and_b32_dpp v73, v73, v154 row_ror:2 row_mask:0xf bank_mask:0xf bound_ctrl:1
	v_mad_i64_i32 v[28:29], s[18:19], v156, s21, v[204:205]
	v_lshl_add_u64 v[28:29], v[28:29], 0, v[108:109]
	global_load_dwordx4 v[28:31], v[28:29], off
	s_waitcnt vmcnt(0) lgkmcnt(0)
	v_mov_b32_dpp v35, v76 row_shr:2 row_mask:0xf bank_mask:0xf bound_ctrl:1
	v_mov_b32_dpp v33, v76 row_shr:1 row_mask:0xf bank_mask:0xf bound_ctrl:1
	v_or_b32_sdwa v68, v69, v35 dst_sel:WORD_1 dst_unused:UNUSED_PAD src0_sel:DWORD src1_sel:DWORD
	v_mov_b32_dpp v81, v77 row_shr:1 row_mask:0xf bank_mask:0xf bound_ctrl:1
	v_mov_b32_dpp v86, v78 row_shr:1 row_mask:0xf bank_mask:0xf bound_ctrl:1
	v_mov_b32_dpp v87, v78 row_shr:2 row_mask:0xf bank_mask:0xf bound_ctrl:1
	v_bitop3_b32 v69, v69, s20, v35 bitop3:0xc8
	v_or_b32_sdwa v34, v71, v33 dst_sel:WORD_1 dst_unused:UNUSED_PAD src0_sel:DWORD src1_sel:DWORD
	v_or_b32_sdwa v70, v85, v81 dst_sel:WORD_1 dst_unused:UNUSED_PAD src0_sel:DWORD src1_sel:DWORD
	v_or_b32_sdwa v80, v88, v86 dst_sel:WORD_1 dst_unused:UNUSED_PAD src0_sel:DWORD src1_sel:DWORD
	v_or_b32_sdwa v74, v89, v87 dst_sel:WORD_1 dst_unused:UNUSED_PAD src0_sel:DWORD src1_sel:DWORD
	v_bitop3_b32 v35, v71, s20, v33 bitop3:0xc8
	v_bitop3_b32 v71, v85, s20, v81 bitop3:0xc8
	v_bitop3_b32 v75, v89, s20, v87 bitop3:0xc8
	v_bitop3_b32 v81, v88, s20, v86 bitop3:0xc8
	v_pk_mul_f32 v[86:87], v[22:23], v[32:33] op_sel_hi:[1,0]
	v_pk_mul_f32 v[22:23], v[64:65], v[68:69]
	v_pk_mul_f32 v[26:27], v[26:27], v[32:33] op_sel_hi:[1,0]
	v_pk_fma_f32 v[22:23], v[60:61], v[34:35], v[22:23]
	v_lshlrev_b32_e32 v34, 16, v76
	v_and_b32_e32 v35, 0xffff0000, v76
	v_pk_fma_f32 v[22:23], v[52:53], v[34:35], v[22:23]
	v_pk_mul_f32 v[24:25], v[24:25], v[32:33] op_sel_hi:[1,0]
	v_pk_add_f32 v[22:23], v[56:57], v[22:23]
	v_mov_b32_dpp v83, v77 row_shr:2 row_mask:0xf bank_mask:0xf bound_ctrl:1
	v_mul_f32_e32 v33, 0xbfb8aa3b, v22
	v_exp_f32_e32 v34, v33
	v_mul_f32_e32 v33, 0xbfb8aa3b, v23
	v_exp_f32_e32 v35, v33
	v_or_b32_sdwa v72, v73, v83 dst_sel:WORD_1 dst_unused:UNUSED_PAD src0_sel:DWORD src1_sel:DWORD
	v_bitop3_b32 v73, v73, s20, v83 bitop3:0xc8
	v_pk_mul_f32 v[32:33], v[20:21], v[32:33] op_sel_hi:[1,0]
	v_add_f32_e32 v20, 1.0, v34
	v_add_f32_e32 v21, 1.0, v35
	v_pk_mul_f32 v[34:35], v[66:67], v[72:73]
	v_lshlrev_b32_e32 v68, 16, v77
	v_pk_fma_f32 v[34:35], v[62:63], v[70:71], v[34:35]
	v_and_b32_e32 v69, 0xffff0000, v77
	v_pk_fma_f32 v[34:35], v[54:55], v[68:69], v[34:35]
	v_rcp_f32_e32 v20, v20
	v_pk_add_f32 v[34:35], v[58:59], v[34:35]
	v_rcp_f32_e32 v21, v21
	v_mul_f32_e32 v68, 0xbfb8aa3b, v34
	v_mul_f32_e32 v69, 0xbfb8aa3b, v35
	v_exp_f32_e32 v68, v68
	v_exp_f32_e32 v69, v69
	v_pk_mul_f32 v[20:21], v[22:23], v[20:21]
	v_mov_b32_dpp v91, v79 row_shr:2 row_mask:0xf bank_mask:0xf bound_ctrl:1
	v_add_f32_e32 v68, 1.0, v68
	v_add_f32_e32 v69, 1.0, v69
	v_rcp_f32_e32 v68, v68
	v_rcp_f32_e32 v69, v69
	v_pk_mul_f32 v[20:21], v[20:21], v[24:25]
	v_pk_mul_f32 v[24:25], v[48:49], v[74:75]
	v_cvt_pk_bf16_f32 v20, v20, v21
	v_pk_mul_f32 v[22:23], v[34:35], v[68:69]
	v_pk_fma_f32 v[24:25], v[44:45], v[80:81], v[24:25]
	v_pk_mul_f32 v[22:23], v[26:27], v[22:23]
	v_lshlrev_b32_e32 v26, 16, v78
	v_and_b32_e32 v27, 0xffff0000, v78
	v_pk_fma_f32 v[24:25], v[36:37], v[26:27], v[24:25]
	v_mov_b32_dpp v90, v79 row_shr:1 row_mask:0xf bank_mask:0xf bound_ctrl:1
	v_pk_add_f32 v[24:25], v[40:41], v[24:25]
	v_or_b32_sdwa v84, v93, v91 dst_sel:WORD_1 dst_unused:UNUSED_PAD src0_sel:DWORD src1_sel:DWORD
	v_mul_f32_e32 v21, 0xbfb8aa3b, v24
	v_exp_f32_e32 v26, v21
	v_mul_f32_e32 v21, 0xbfb8aa3b, v25
	v_exp_f32_e32 v27, v21
	v_bitop3_b32 v85, v93, s20, v91 bitop3:0xc8
	v_or_b32_sdwa v82, v92, v90 dst_sel:WORD_1 dst_unused:UNUSED_PAD src0_sel:DWORD src1_sel:DWORD
	v_bitop3_b32 v83, v92, s20, v90 bitop3:0xc8
	v_cvt_pk_bf16_f32 v21, v22, v23
	v_add_f32_e32 v22, 1.0, v26
	v_add_f32_e32 v23, 1.0, v27
	v_pk_mul_f32 v[26:27], v[50:51], v[84:85]
	v_lshlrev_b32_e32 v34, 16, v79
	v_pk_fma_f32 v[26:27], v[46:47], v[82:83], v[26:27]
	v_and_b32_e32 v35, 0xffff0000, v79
	v_pk_fma_f32 v[26:27], v[38:39], v[34:35], v[26:27]
	v_rcp_f32_e32 v22, v22
	v_pk_add_f32 v[26:27], v[42:43], v[26:27]
	v_rcp_f32_e32 v23, v23
	v_mul_f32_e32 v34, 0xbfb8aa3b, v26
	v_mul_f32_e32 v35, 0xbfb8aa3b, v27
	v_exp_f32_e32 v34, v34
	v_exp_f32_e32 v35, v35
	v_pk_mul_f32 v[22:23], v[24:25], v[22:23]
	v_and_b32_dpp v73, v77, v147 row_ror:1 row_mask:0xf bank_mask:0xf bound_ctrl:1
	v_add_f32_e32 v34, 1.0, v34
	v_add_f32_e32 v35, 1.0, v35
	v_rcp_f32_e32 v34, v34
	v_rcp_f32_e32 v35, v35
	v_pk_mul_f32 v[22:23], v[32:33], v[22:23]
	v_and_b32_dpp v33, v76, v146 row_ror:2 row_mask:0xf bank_mask:0xf bound_ctrl:1
	v_cvt_pk_bf16_f32 v22, v22, v23
	v_pk_mul_f32 v[24:25], v[26:27], v[34:35]
	v_and_b32_dpp v35, v76, v147 row_ror:1 row_mask:0xf bank_mask:0xf bound_ctrl:1
	v_pk_mul_f32 v[24:25], v[86:87], v[24:25]
	v_and_b32_dpp v75, v77, v146 row_ror:2 row_mask:0xf bank_mask:0xf bound_ctrl:1
	v_cvt_pk_bf16_f32 v23, v24, v25
	global_store_dwordx4 v[114:115], v[20:23], off offset:256
	global_load_dword v24, v[202:203], off offset:640
	v_and_b32_dpp v81, v78, v147 row_ror:1 row_mask:0xf bank_mask:0xf bound_ctrl:1
	v_mad_i64_i32 v[20:21], s[18:19], v153, s21, v[204:205]
	v_lshl_add_u64 v[20:21], v[20:21], 0, v[108:109]
	global_load_dwordx4 v[20:23], v[20:21], off
	v_mov_b32_dpp v27, v28 row_shr:2 row_mask:0xf bank_mask:0xf bound_ctrl:1
	v_mov_b32_dpp v25, v28 row_shr:1 row_mask:0xf bank_mask:0xf bound_ctrl:1
	v_or_b32_sdwa v32, v33, v27 dst_sel:WORD_1 dst_unused:UNUSED_PAD src0_sel:DWORD src1_sel:DWORD
	v_mov_b32_dpp v71, v29 row_shr:1 row_mask:0xf bank_mask:0xf bound_ctrl:1
	v_mov_b32_dpp v77, v30 row_shr:1 row_mask:0xf bank_mask:0xf bound_ctrl:1
	v_mov_b32_dpp v80, v30 row_shr:2 row_mask:0xf bank_mask:0xf bound_ctrl:1
	v_and_b32_dpp v78, v78, v146 row_ror:2 row_mask:0xf bank_mask:0xf bound_ctrl:1
	v_mov_b32_dpp v83, v31 row_shr:2 row_mask:0xf bank_mask:0xf bound_ctrl:1
	v_and_b32_dpp v84, v79, v147 row_ror:1 row_mask:0xf bank_mask:0xf bound_ctrl:1
	v_and_b32_dpp v79, v79, v146 row_ror:2 row_mask:0xf bank_mask:0xf bound_ctrl:1
	v_bitop3_b32 v33, v33, s20, v27 bitop3:0xc8
	v_or_b32_sdwa v26, v35, v25 dst_sel:WORD_1 dst_unused:UNUSED_PAD src0_sel:DWORD src1_sel:DWORD
	v_or_b32_sdwa v34, v73, v71 dst_sel:WORD_1 dst_unused:UNUSED_PAD src0_sel:DWORD src1_sel:DWORD
	v_or_b32_sdwa v70, v81, v77 dst_sel:WORD_1 dst_unused:UNUSED_PAD src0_sel:DWORD src1_sel:DWORD
	v_or_b32_sdwa v72, v78, v80 dst_sel:WORD_1 dst_unused:UNUSED_PAD src0_sel:DWORD src1_sel:DWORD
	v_or_b32_sdwa v76, v79, v83 dst_sel:WORD_1 dst_unused:UNUSED_PAD src0_sel:DWORD src1_sel:DWORD
	v_bitop3_b32 v27, v35, s20, v25 bitop3:0xc8
	v_bitop3_b32 v35, v73, s20, v71 bitop3:0xc8
	v_bitop3_b32 v73, v78, s20, v80 bitop3:0xc8
	v_bitop3_b32 v71, v81, s20, v77 bitop3:0xc8
	v_bitop3_b32 v77, v79, s20, v83 bitop3:0xc8
	v_mov_b32_dpp v69, v29 row_shr:2 row_mask:0xf bank_mask:0xf bound_ctrl:1
	v_or_b32_sdwa v68, v75, v69 dst_sel:WORD_1 dst_unused:UNUSED_PAD src0_sel:DWORD src1_sel:DWORD
	v_bitop3_b32 v69, v75, s20, v69 bitop3:0xc8
	v_mov_b32_dpp v82, v31 row_shr:1 row_mask:0xf bank_mask:0xf bound_ctrl:1
	v_or_b32_sdwa v74, v84, v82 dst_sel:WORD_1 dst_unused:UNUSED_PAD src0_sel:DWORD src1_sel:DWORD
	v_bitop3_b32 v75, v84, s20, v82 bitop3:0xc8
	s_mov_b64 s[18:19], -1
	s_waitcnt vmcnt(0) lgkmcnt(0)
	v_pk_mul_f32 v[78:79], v[14:15], v[24:25] op_sel_hi:[1,0]
	v_pk_mul_f32 v[14:15], v[64:65], v[32:33]
	v_pk_mul_f32 v[18:19], v[18:19], v[24:25] op_sel_hi:[1,0]
	v_pk_fma_f32 v[14:15], v[60:61], v[26:27], v[14:15]
	v_lshlrev_b32_e32 v26, 16, v28
	v_and_b32_e32 v27, 0xffff0000, v28
	v_pk_fma_f32 v[14:15], v[52:53], v[26:27], v[14:15]
	v_pk_mul_f32 v[16:17], v[16:17], v[24:25] op_sel_hi:[1,0]
	v_pk_add_f32 v[14:15], v[56:57], v[14:15]
	v_lshlrev_b32_e32 v32, 16, v29
	v_mul_f32_e32 v25, 0xbfb8aa3b, v14
	v_exp_f32_e32 v26, v25
	v_mul_f32_e32 v25, 0xbfb8aa3b, v15
	v_exp_f32_e32 v27, v25
	v_pk_mul_f32 v[24:25], v[12:13], v[24:25] op_sel_hi:[1,0]
	v_add_f32_e32 v12, 1.0, v26
	v_and_b32_e32 v33, 0xffff0000, v29
	v_add_f32_e32 v13, 1.0, v27
	v_pk_mul_f32 v[26:27], v[66:67], v[68:69]
	v_rcp_f32_e32 v12, v12
	v_pk_fma_f32 v[26:27], v[62:63], v[34:35], v[26:27]
	v_rcp_f32_e32 v13, v13
	v_pk_fma_f32 v[26:27], v[54:55], v[32:33], v[26:27]
	v_mov_b32_dpp v34, v22 row_shr:1 row_mask:0xf bank_mask:0xf bound_ctrl:1
	v_pk_add_f32 v[26:27], v[58:59], v[26:27]
	v_pk_mul_f32 v[12:13], v[14:15], v[12:13]
	v_mul_f32_e32 v32, 0xbfb8aa3b, v26
	v_mul_f32_e32 v33, 0xbfb8aa3b, v27
	v_exp_f32_e32 v32, v32
	v_exp_f32_e32 v33, v33
	v_pk_mul_f32 v[12:13], v[12:13], v[16:17]
	v_pk_mul_f32 v[16:17], v[48:49], v[72:73]
	v_add_f32_e32 v32, 1.0, v32
	v_add_f32_e32 v33, 1.0, v33
	v_rcp_f32_e32 v32, v32
	v_rcp_f32_e32 v33, v33
	v_pk_fma_f32 v[16:17], v[44:45], v[70:71], v[16:17]
	v_cvt_pk_bf16_f32 v12, v12, v13
	v_mov_b32_dpp v35, v22 row_shr:2 row_mask:0xf bank_mask:0xf bound_ctrl:1
	v_pk_mul_f32 v[14:15], v[26:27], v[32:33]
	v_lshlrev_b32_e32 v26, 16, v31
	v_pk_mul_f32 v[14:15], v[18:19], v[14:15]
	v_lshlrev_b32_e32 v18, 16, v30
	v_and_b32_e32 v19, 0xffff0000, v30
	v_pk_fma_f32 v[16:17], v[36:37], v[18:19], v[16:17]
	v_and_b32_e32 v27, 0xffff0000, v31
	v_pk_add_f32 v[16:17], v[40:41], v[16:17]
	v_mov_b32_dpp v71, v23 row_shr:2 row_mask:0xf bank_mask:0xf bound_ctrl:1
	v_mul_f32_e32 v13, 0xbfb8aa3b, v16
	v_exp_f32_e32 v18, v13
	v_mul_f32_e32 v13, 0xbfb8aa3b, v17
	v_exp_f32_e32 v19, v13
	v_cvt_pk_bf16_f32 v13, v14, v15
	v_add_f32_e32 v14, 1.0, v18
	v_rcp_f32_e32 v14, v14
	v_add_f32_e32 v15, 1.0, v19
	v_pk_mul_f32 v[18:19], v[50:51], v[76:77]
	v_rcp_f32_e32 v15, v15
	v_pk_fma_f32 v[18:19], v[46:47], v[74:75], v[18:19]
	v_mov_b32_dpp v70, v23 row_shr:1 row_mask:0xf bank_mask:0xf bound_ctrl:1
	v_pk_fma_f32 v[18:19], v[38:39], v[26:27], v[18:19]
	v_pk_mul_f32 v[14:15], v[16:17], v[14:15]
	v_pk_add_f32 v[18:19], v[42:43], v[18:19]
	v_pk_mul_f32 v[14:15], v[24:25], v[14:15]
	v_mul_f32_e32 v26, 0xbfb8aa3b, v18
	v_mul_f32_e32 v27, 0xbfb8aa3b, v19
	v_exp_f32_e32 v26, v26
	v_exp_f32_e32 v27, v27
	v_cvt_pk_bf16_f32 v14, v14, v15
	v_mov_b32_dpp v24, v29 row_ror:2 row_mask:0xf bank_mask:0xf bound_ctrl:1
	v_add_f32_e32 v26, 1.0, v26
	v_add_f32_e32 v27, 1.0, v27
	v_rcp_f32_e32 v26, v26
	v_rcp_f32_e32 v27, v27
	v_mov_b32_dpp v25, v21 row_shr:2 row_mask:0xf bank_mask:0xf bound_ctrl:1
	v_cndmask_b32_e64 v33, 0, v24, s[38:39]
	v_or_b32_sdwa v24, v33, v25 dst_sel:WORD_1 dst_unused:UNUSED_PAD src0_sel:DWORD src1_sel:DWORD
	v_pk_mul_f32 v[16:17], v[18:19], v[26:27]
	v_mov_b32_dpp v18, v29 row_ror:1 row_mask:0xf bank_mask:0xf bound_ctrl:1
	v_pk_mul_f32 v[16:17], v[78:79], v[16:17]
	v_mov_b32_dpp v26, v30 row_ror:1 row_mask:0xf bank_mask:0xf bound_ctrl:1
	v_cvt_pk_bf16_f32 v15, v16, v17
	global_store_dwordx4 v[112:113], v[12:15], off offset:256
	global_load_dword v12, v[202:203], off offset:704
	v_mov_b32_dpp v16, v28 row_ror:2 row_mask:0xf bank_mask:0xf bound_ctrl:1
	v_mov_b32_dpp v14, v28 row_ror:1 row_mask:0xf bank_mask:0xf bound_ctrl:1
	v_mov_b32_dpp v15, v20 row_shr:2 row_mask:0xf bank_mask:0xf bound_ctrl:1
	v_cndmask_b32_e64 v17, 0, v16, s[38:39]
	v_mov_b32_dpp v28, v30 row_ror:2 row_mask:0xf bank_mask:0xf bound_ctrl:1
	v_mov_b32_dpp v13, v20 row_shr:1 row_mask:0xf bank_mask:0xf bound_ctrl:1
	v_cndmask_b32_e64 v19, 0, v14, s[36:37]
	v_or_b32_sdwa v16, v17, v15 dst_sel:WORD_1 dst_unused:UNUSED_PAD src0_sel:DWORD src1_sel:DWORD
	v_mov_b32_dpp v27, v21 row_shr:1 row_mask:0xf bank_mask:0xf bound_ctrl:1
	v_cndmask_b32_e64 v29, 0, v18, s[36:37]
	v_cndmask_b32_e64 v68, 0, v26, s[36:37]
	v_cndmask_b32_e64 v69, 0, v28, s[38:39]
	v_bitop3_b32 v17, v17, s20, v15 bitop3:0xc8
	v_or_b32_sdwa v14, v19, v13 dst_sel:WORD_1 dst_unused:UNUSED_PAD src0_sel:DWORD src1_sel:DWORD
	v_or_b32_sdwa v18, v29, v27 dst_sel:WORD_1 dst_unused:UNUSED_PAD src0_sel:DWORD src1_sel:DWORD
	v_or_b32_sdwa v26, v68, v34 dst_sel:WORD_1 dst_unused:UNUSED_PAD src0_sel:DWORD src1_sel:DWORD
	v_or_b32_sdwa v28, v69, v35 dst_sel:WORD_1 dst_unused:UNUSED_PAD src0_sel:DWORD src1_sel:DWORD
	v_bitop3_b32 v15, v19, s20, v13 bitop3:0xc8
	v_bitop3_b32 v19, v29, s20, v27 bitop3:0xc8
	v_bitop3_b32 v29, v69, s20, v35 bitop3:0xc8
	v_bitop3_b32 v27, v68, s20, v34 bitop3:0xc8
	v_bitop3_b32 v25, v33, s20, v25 bitop3:0xc8
	v_mov_b32_dpp v30, v31 row_ror:1 row_mask:0xf bank_mask:0xf bound_ctrl:1
	v_mov_b32_dpp v31, v31 row_ror:2 row_mask:0xf bank_mask:0xf bound_ctrl:1
	v_cndmask_b32_e64 v31, 0, v31, s[38:39]
	v_cndmask_b32_e64 v72, 0, v30, s[36:37]
	v_or_b32_sdwa v32, v31, v71 dst_sel:WORD_1 dst_unused:UNUSED_PAD src0_sel:DWORD src1_sel:DWORD
	v_bitop3_b32 v33, v31, s20, v71 bitop3:0xc8
	v_or_b32_sdwa v30, v72, v70 dst_sel:WORD_1 dst_unused:UNUSED_PAD src0_sel:DWORD src1_sel:DWORD
	v_bitop3_b32 v31, v72, s20, v70 bitop3:0xc8
	s_waitcnt vmcnt(0) lgkmcnt(0)
	v_pk_mul_f32 v[34:35], v[6:7], v[12:13] op_sel_hi:[1,0]
	v_pk_mul_f32 v[6:7], v[64:65], v[16:17]
	v_pk_mul_f32 v[10:11], v[10:11], v[12:13] op_sel_hi:[1,0]
	v_pk_fma_f32 v[6:7], v[60:61], v[14:15], v[6:7]
	v_lshlrev_b32_e32 v14, 16, v20
	v_and_b32_e32 v15, 0xffff0000, v20
	v_pk_fma_f32 v[6:7], v[52:53], v[14:15], v[6:7]
	v_pk_mul_f32 v[8:9], v[8:9], v[12:13] op_sel_hi:[1,0]
	v_pk_add_f32 v[6:7], v[56:57], v[6:7]
	v_lshlrev_b32_e32 v16, 16, v21
	v_mul_f32_e32 v13, 0xbfb8aa3b, v6
	v_exp_f32_e32 v14, v13
	v_mul_f32_e32 v13, 0xbfb8aa3b, v7
	v_exp_f32_e32 v15, v13
	v_pk_mul_f32 v[12:13], v[4:5], v[12:13] op_sel_hi:[1,0]
	v_add_f32_e32 v4, 1.0, v14
	v_and_b32_e32 v17, 0xffff0000, v21
	v_add_f32_e32 v5, 1.0, v15
	v_pk_mul_f32 v[14:15], v[66:67], v[24:25]
	v_rcp_f32_e32 v4, v4
	v_pk_fma_f32 v[14:15], v[62:63], v[18:19], v[14:15]
	v_rcp_f32_e32 v5, v5
	v_pk_fma_f32 v[14:15], v[54:55], v[16:17], v[14:15]
	v_pk_mul_f32 v[4:5], v[6:7], v[4:5]
	v_pk_add_f32 v[14:15], v[58:59], v[14:15]
	v_pk_mul_f32 v[4:5], v[4:5], v[8:9]
	v_mul_f32_e32 v16, 0xbfb8aa3b, v14
	v_mul_f32_e32 v17, 0xbfb8aa3b, v15
	v_exp_f32_e32 v16, v16
	v_exp_f32_e32 v17, v17
	v_pk_mul_f32 v[8:9], v[48:49], v[28:29]
	v_cvt_pk_bf16_f32 v4, v4, v5
	v_add_f32_e32 v16, 1.0, v16
	v_add_f32_e32 v17, 1.0, v17
	v_rcp_f32_e32 v16, v16
	v_rcp_f32_e32 v17, v17
	v_pk_fma_f32 v[8:9], v[44:45], v[26:27], v[8:9]
	v_pk_mul_f32 v[6:7], v[14:15], v[16:17]
	s_nop 0
	v_pk_mul_f32 v[6:7], v[10:11], v[6:7]
	v_lshlrev_b32_e32 v10, 16, v22
	v_and_b32_e32 v11, 0xffff0000, v22
	v_pk_fma_f32 v[8:9], v[36:37], v[10:11], v[8:9]
	v_lshlrev_b32_e32 v14, 16, v23
	v_pk_add_f32 v[8:9], v[40:41], v[8:9]
	v_and_b32_e32 v15, 0xffff0000, v23
	v_mul_f32_e32 v5, 0xbfb8aa3b, v8
	v_exp_f32_e32 v10, v5
	v_mul_f32_e32 v5, 0xbfb8aa3b, v9
	v_exp_f32_e32 v11, v5
	v_cvt_pk_bf16_f32 v5, v6, v7
	v_add_f32_e32 v6, 1.0, v10
	v_rcp_f32_e32 v6, v6
	v_add_f32_e32 v7, 1.0, v11
	v_pk_mul_f32 v[10:11], v[50:51], v[32:33]
	v_rcp_f32_e32 v7, v7
	v_pk_fma_f32 v[10:11], v[46:47], v[30:31], v[10:11]
	v_pk_mul_f32 v[6:7], v[8:9], v[6:7]
	v_pk_fma_f32 v[10:11], v[38:39], v[14:15], v[10:11]
	v_pk_mul_f32 v[6:7], v[12:13], v[6:7]
	v_pk_add_f32 v[10:11], v[42:43], v[10:11]
	v_cvt_pk_bf16_f32 v6, v6, v7
	v_mul_f32_e32 v14, 0xbfb8aa3b, v10
	v_mul_f32_e32 v15, 0xbfb8aa3b, v11
	v_exp_f32_e32 v14, v14
	v_exp_f32_e32 v15, v15
	v_add_f32_e32 v14, 1.0, v14
	v_add_f32_e32 v15, 1.0, v15
	v_rcp_f32_e32 v14, v14
	v_rcp_f32_e32 v15, v15
	s_nop 0
	v_pk_mul_f32 v[8:9], v[10:11], v[14:15]
	s_nop 0
	v_pk_mul_f32 v[8:9], v[34:35], v[8:9]
	s_nop 0
	v_cvt_pk_bf16_f32 v7, v8, v9
	global_store_dwordx4 v[110:111], v[4:7], off offset:256
	s_cbranch_vccnz .LBB0_1916
	s_andn2_b64 vcc, exec, s[0:1]
	s_cbranch_vccnz .LBB0_1915
	s_barrier
	s_branch .LBB0_1915

.LBB0_2008:
	v_lshl_or_b32 v170, s57, 8, v197
	v_lshl_add_u32 v172, s58, 8, v1
	v_ashrrev_i32_e32 v171, 31, v170
	v_lshlrev_b64 v[186:187], 1, v[170:171]
	v_ashrrev_i32_e32 v173, 31, v172
	v_lshl_add_u64 v[174:175], s[4:5], 0, v[186:187]
	v_lshlrev_b64 v[188:189], 12, v[172:173]
	v_lshl_add_u64 v[116:117], v[174:175], 0, v[188:189]
	global_load_dwordx4 v[182:185], v[116:117], off
	global_load_dwordx4 v[156:159], v[116:117], off offset:256
	v_or_b32_e32 v180, 16, v172
	v_ashrrev_i32_e32 v181, 31, v180
	v_lshlrev_b64 v[116:117], 12, v[180:181]
	v_or_b32_e32 v178, 32, v172
	v_lshl_add_u64 v[116:117], v[174:175], 0, v[116:117]
	v_ashrrev_i32_e32 v179, 31, v178
	global_load_dwordx4 v[144:147], v[116:117], off
	global_load_dwordx4 v[140:143], v[116:117], off offset:256
	v_lshlrev_b64 v[116:117], 12, v[178:179]
	v_or_b32_e32 v176, 48, v172
	v_lshl_add_u64 v[116:117], v[174:175], 0, v[116:117]
	v_ashrrev_i32_e32 v177, 31, v176
	global_load_dwordx4 v[128:131], v[116:117], off
	global_load_dwordx4 v[124:127], v[116:117], off offset:256
	v_lshlrev_b64 v[116:117], 12, v[176:177]
	v_lshl_add_u64 v[116:117], v[174:175], 0, v[116:117]
	global_load_dwordx4 v[120:123], v[116:117], off
	s_nop 0
	global_load_dwordx4 v[116:119], v[116:117], off offset:256
	v_lshlrev_b64 v[194:195], 11, v[172:173]
	s_lshl_b32 s14, s57, 2
	s_ashr_i32 s15, s14, 31
	s_waitcnt vmcnt(0) lgkmcnt(0)
	v_lshlrev_b32_e32 v190, 16, v182
	v_and_b32_e32 v191, 0xffff0000, v182
	v_lshlrev_b32_e32 v182, 16, v183
	v_and_b32_e32 v183, 0xffff0000, v183
	v_pk_add_f32 v[182:183], v[154:155], v[182:183]
	v_pk_add_f32 v[190:191], v[152:153], v[190:191]
	v_lshlrev_b32_e32 v152, 16, v184
	v_and_b32_e32 v153, 0xffff0000, v184
	v_lshlrev_b32_e32 v154, 16, v185
	v_and_b32_e32 v155, 0xffff0000, v185
	v_pk_add_f32 v[184:185], v[150:151], v[154:155]
	v_pk_add_f32 v[192:193], v[148:149], v[152:153]
	v_lshl_add_u64 v[148:149], s[4:5], 0, v[188:189]
	v_cvt_pk_bf16_f32 v152, v190, v191
	v_cvt_pk_bf16_f32 v153, v182, v183
	v_cvt_pk_bf16_f32 v154, v192, v193
	v_cvt_pk_bf16_f32 v155, v184, v185
	v_lshl_add_u64 v[150:151], v[148:149], 0, v[186:187]
	global_store_dwordx4 v[150:151], v[152:155], off
	v_med3_f32 v148, v190, s63, v240
	v_med3_f32 v149, v191, s63, v240
	v_mov_b32_e32 v152, v3
	v_cvt_pk_fp8_f32 v152, v148, v149
	v_med3_f32 v153, v182, s63, v240
	v_med3_f32 v154, v183, s63, v240
	v_med3_f32 v148, v192, s63, v240
	v_cvt_pk_fp8_f32 v152, v153, v154 op_sel:[0,0,1]
	v_med3_f32 v149, v193, s63, v240
	v_mov_b32_e32 v153, v3
	v_cvt_pk_fp8_f32 v153, v148, v149
	v_med3_f32 v154, v184, s63, v240
	v_med3_f32 v155, v185, s63, v240
	v_lshl_add_u64 v[148:149], s[8:9], 0, v[194:195]
	v_cvt_pk_fp8_f32 v153, v154, v155 op_sel:[0,0,1]
	v_lshl_add_u64 v[148:149], v[148:149], 0, v[170:171]
	v_mul_f32_e32 v154, v185, v185
	v_fmac_f32_e32 v154, v184, v184
	global_store_dwordx2 v[148:149], v[152:153], off
	v_mul_f32_e32 v152, v191, v191
	v_mul_f32_e32 v153, v183, v183
	v_fmac_f32_e32 v152, v190, v190
	v_fmac_f32_e32 v153, v182, v182
	v_add_f32_e32 v152, v152, v153
	v_mul_f32_e32 v153, v193, v193
	v_fmac_f32_e32 v153, v192, v192
	v_add_f32_e32 v153, v153, v154
	v_lshlrev_b32_e32 v154, 16, v156
	v_and_b32_e32 v155, 0xffff0000, v156
	v_lshlrev_b32_e32 v156, 16, v157
	v_and_b32_e32 v157, 0xffff0000, v157
	v_pk_add_f32 v[138:139], v[138:139], v[156:157]
	v_pk_add_f32 v[136:137], v[136:137], v[154:155]
	v_lshlrev_b32_e32 v154, 16, v158
	v_and_b32_e32 v155, 0xffff0000, v158
	v_lshlrev_b32_e32 v156, 16, v159
	v_and_b32_e32 v157, 0xffff0000, v159
	v_pk_add_f32 v[134:135], v[134:135], v[156:157]
	v_pk_add_f32 v[132:133], v[132:133], v[154:155]
	v_cvt_pk_bf16_f32 v154, v136, v137
	v_cvt_pk_bf16_f32 v155, v138, v139
	v_cvt_pk_bf16_f32 v156, v132, v133
	v_cvt_pk_bf16_f32 v157, v134, v135
	v_add_f32_e32 v152, v152, v153
	global_store_dwordx4 v[150:151], v[154:157], off offset:256
	v_med3_f32 v151, v136, s63, v240
	v_med3_f32 v153, v137, s63, v240
	v_mov_b32_e32 v150, v3
	v_cvt_pk_fp8_f32 v150, v151, v153
	v_med3_f32 v154, v138, s63, v240
	v_med3_f32 v155, v139, s63, v240
	v_mul_f32_e32 v137, v137, v137
	v_cvt_pk_fp8_f32 v150, v154, v155 op_sel:[0,0,1]
	v_med3_f32 v154, v133, s63, v240
	v_mul_f32_e32 v133, v133, v133
	v_med3_f32 v153, v132, s63, v240
	v_fmac_f32_e32 v137, v136, v136
	v_mul_f32_e32 v136, v139, v139
	v_fmac_f32_e32 v133, v132, v132
	v_mul_f32_e32 v132, v135, v135
	v_fmac_f32_e32 v136, v138, v138
	v_fmac_f32_e32 v132, v134, v134
	v_add_f32_e32 v136, v137, v136
	v_add_f32_e32 v132, v133, v132
	v_add_f32_e32 v132, v136, v132
	v_add_f32_e32 v133, v152, v132
	v_xor_b32_e32 v132, 16, v230
	v_cmp_lt_i32_e32 vcc, v132, v231
	v_med3_f32 v155, v134, s63, v240
	v_mov_b32_e32 v151, v3
	v_cndmask_b32_e32 v132, v230, v132, vcc
	v_lshlrev_b32_e32 v132, 2, v132
	ds_bpermute_b32 v134, v132, v133
	v_cvt_pk_fp8_f32 v151, v153, v154
	v_med3_f32 v156, v135, s63, v240
	s_waitcnt lgkmcnt(0)
	v_add_f32_e32 v134, v133, v134
	v_xor_b32_e32 v133, 32, v230
	v_cmp_lt_i32_e32 vcc, v133, v231
	v_cvt_pk_fp8_f32 v151, v155, v156 op_sel:[0,0,1]
	global_store_dwordx2 v[148:149], v[150:151], off offset:128
	v_cndmask_b32_e32 v133, v230, v133, vcc
	v_lshlrev_b32_e32 v133, 2, v133
	ds_bpermute_b32 v135, v133, v134
	s_and_saveexec_b64 s[16:17], s[36:37]
	s_cbranch_execz .LBB0_2010
	v_readlane_b32 s64, v253, 17
	v_readlane_b32 s65, v253, 18
	s_mov_b32 s21, s65
	v_lshlrev_b64 v[136:137], 7, v[172:173]
	v_readlane_b32 s66, v253, 19
	v_readlane_b32 s67, v253, 20
	v_writelane_b32 v253, s20, 17
	v_lshl_add_u64 v[136:137], s[6:7], 0, v[136:137]
	v_lshl_add_u64 v[136:137], s[14:15], 2, v[136:137]
	v_writelane_b32 v253, s21, 18
	s_mov_b32 s61, s65
	s_lshl_b32 s60, s43, 2
	v_writelane_b32 v253, s22, 19
	v_writelane_b32 v253, s23, 20
	v_lshl_add_u64 v[136:137], v[136:137], 0, s[60:61]
	s_waitcnt lgkmcnt(0)
	v_add_f32_e32 v134, v134, v135
	global_store_dword v[136:137], v134, off
.LBB0_2010:
	s_or_b64 exec, exec, s[16:17]
	v_lshlrev_b32_e32 v136, 16, v144
	v_and_b32_e32 v137, 0xffff0000, v144
	v_lshlrev_b32_e32 v138, 16, v145
	v_and_b32_e32 v139, 0xffff0000, v145
	s_waitcnt lgkmcnt(0)
	v_lshlrev_b64 v[134:135], 11, v[180:181]
	v_pk_add_f32 v[114:115], v[114:115], v[138:139]
	v_pk_add_f32 v[112:113], v[112:113], v[136:137]
	v_lshlrev_b32_e32 v136, 16, v146
	v_and_b32_e32 v137, 0xffff0000, v146
	v_lshlrev_b32_e32 v138, 16, v147
	v_and_b32_e32 v139, 0xffff0000, v147
	v_pk_add_f32 v[138:139], v[110:111], v[138:139]
	v_pk_add_f32 v[136:137], v[108:109], v[136:137]
	v_lshl_add_u64 v[144:145], v[134:135], 1, s[4:5]
	v_cvt_pk_bf16_f32 v108, v112, v113
	v_cvt_pk_bf16_f32 v109, v114, v115
	v_cvt_pk_bf16_f32 v110, v136, v137
	v_cvt_pk_bf16_f32 v111, v138, v139
	v_lshl_add_u64 v[144:145], v[170:171], 1, v[144:145]
	global_store_dwordx4 v[144:145], v[108:111], off
	v_med3_f32 v146, v115, s63, v240
	v_med3_f32 v147, v139, s63, v240
	v_med3_f32 v109, v112, s63, v240
	v_med3_f32 v110, v113, s63, v240
	v_mov_b32_e32 v108, v3
	v_cvt_pk_fp8_f32 v108, v109, v110
	v_med3_f32 v111, v114, s63, v240
	v_med3_f32 v110, v136, s63, v240
	v_mov_b32_e32 v109, v3
	v_cvt_pk_fp8_f32 v108, v111, v146 op_sel:[0,0,1]
	v_med3_f32 v111, v137, s63, v240
	v_cvt_pk_fp8_f32 v109, v110, v111
	v_med3_f32 v146, v138, s63, v240
	v_lshl_add_u64 v[110:111], s[8:9], 0, v[134:135]
	v_lshl_add_u64 v[110:111], v[110:111], 0, v[170:171]
	v_cvt_pk_fp8_f32 v109, v146, v147 op_sel:[0,0,1]
	global_store_dwordx2 v[110:111], v[108:109], off
	v_mul_f32_e32 v108, v113, v113
	v_mul_f32_e32 v109, v115, v115
	v_fmac_f32_e32 v108, v112, v112
	v_fmac_f32_e32 v109, v114, v114
	v_add_f32_e32 v108, v108, v109
	v_mul_f32_e32 v109, v137, v137
	v_mul_f32_e32 v112, v139, v139
	v_fmac_f32_e32 v109, v136, v136
	v_fmac_f32_e32 v112, v138, v138
	v_add_f32_e32 v109, v109, v112
	v_add_f32_e32 v114, v108, v109
	v_lshlrev_b32_e32 v108, 16, v140
	v_and_b32_e32 v109, 0xffff0000, v140
	v_lshlrev_b32_e32 v112, 16, v141
	v_and_b32_e32 v113, 0xffff0000, v141
	v_pk_add_f32 v[106:107], v[106:107], v[112:113]
	v_pk_add_f32 v[104:105], v[104:105], v[108:109]
	v_lshlrev_b32_e32 v108, 16, v142
	v_and_b32_e32 v109, 0xffff0000, v142
	v_lshlrev_b32_e32 v112, 16, v143
	v_and_b32_e32 v113, 0xffff0000, v143
	v_pk_add_f32 v[112:113], v[102:103], v[112:113]
	v_pk_add_f32 v[108:109], v[100:101], v[108:109]
	v_cvt_pk_bf16_f32 v100, v104, v105
	v_cvt_pk_bf16_f32 v101, v106, v107
	v_cvt_pk_bf16_f32 v102, v108, v109
	v_cvt_pk_bf16_f32 v103, v112, v113
	global_store_dwordx4 v[144:145], v[100:103], off offset:256
	v_med3_f32 v115, v107, s63, v240
	v_med3_f32 v134, v113, s63, v240
	v_med3_f32 v101, v104, s63, v240
	v_med3_f32 v102, v105, s63, v240
	v_mov_b32_e32 v100, v3
	v_cvt_pk_fp8_f32 v100, v101, v102
	v_med3_f32 v103, v106, s63, v240
	v_med3_f32 v102, v108, s63, v240
	v_mov_b32_e32 v101, v3
	v_cvt_pk_fp8_f32 v100, v103, v115 op_sel:[0,0,1]
	v_med3_f32 v103, v109, s63, v240
	v_cvt_pk_fp8_f32 v101, v102, v103
	v_med3_f32 v115, v112, s63, v240
	v_mul_f32_e32 v102, v113, v113
	v_fmac_f32_e32 v102, v112, v112
	v_cvt_pk_fp8_f32 v101, v115, v134 op_sel:[0,0,1]
	global_store_dwordx2 v[110:111], v[100:101], off offset:128
	v_mul_f32_e32 v100, v105, v105
	v_mul_f32_e32 v101, v107, v107
	v_fmac_f32_e32 v100, v104, v104
	v_fmac_f32_e32 v101, v106, v106
	v_add_f32_e32 v100, v100, v101
	v_mul_f32_e32 v101, v109, v109
	v_fmac_f32_e32 v101, v108, v108
	v_add_f32_e32 v101, v101, v102
	v_add_f32_e32 v100, v100, v101
	v_add_f32_e32 v100, v114, v100
	ds_bpermute_b32 v101, v132, v100
	s_waitcnt lgkmcnt(0)
	v_add_f32_e32 v100, v100, v101
	ds_bpermute_b32 v101, v133, v100
	s_and_saveexec_b64 s[16:17], s[36:37]
	s_cbranch_execz .LBB0_2012
	v_readlane_b32 s64, v253, 17
	v_readlane_b32 s65, v253, 18
	s_mov_b32 s21, s65
	v_lshlrev_b64 v[102:103], 7, v[180:181]
	v_readlane_b32 s66, v253, 19
	v_readlane_b32 s67, v253, 20
	v_writelane_b32 v253, s20, 17
	v_lshl_add_u64 v[102:103], s[6:7], 0, v[102:103]
	v_lshl_add_u64 v[102:103], s[14:15], 2, v[102:103]
	v_writelane_b32 v253, s21, 18
	s_mov_b32 s61, s65
	s_lshl_b32 s60, s43, 2
	v_writelane_b32 v253, s22, 19
	v_writelane_b32 v253, s23, 20
	v_lshl_add_u64 v[102:103], v[102:103], 0, s[60:61]
	s_waitcnt lgkmcnt(0)
	v_add_f32_e32 v100, v100, v101
	global_store_dword v[102:103], v100, off
.LBB0_2012:
	s_or_b64 exec, exec, s[16:17]
	v_lshlrev_b32_e32 v102, 16, v128
	v_and_b32_e32 v103, 0xffff0000, v128
	v_lshlrev_b32_e32 v104, 16, v129
	v_and_b32_e32 v105, 0xffff0000, v129
	s_waitcnt lgkmcnt(0)
	v_lshlrev_b64 v[100:101], 11, v[178:179]
	v_pk_add_f32 v[98:99], v[98:99], v[104:105]
	v_pk_add_f32 v[96:97], v[96:97], v[102:103]
	v_lshlrev_b32_e32 v102, 16, v130
	v_and_b32_e32 v103, 0xffff0000, v130
	v_lshlrev_b32_e32 v104, 16, v131
	v_and_b32_e32 v105, 0xffff0000, v131
	v_pk_add_f32 v[104:105], v[94:95], v[104:105]
	v_pk_add_f32 v[102:103], v[92:93], v[102:103]
	v_lshl_add_u64 v[106:107], v[100:101], 1, s[4:5]
	v_cvt_pk_bf16_f32 v92, v96, v97
	v_cvt_pk_bf16_f32 v93, v98, v99
	v_cvt_pk_bf16_f32 v94, v102, v103
	v_cvt_pk_bf16_f32 v95, v104, v105
	v_lshl_add_u64 v[106:107], v[170:171], 1, v[106:107]
	global_store_dwordx4 v[106:107], v[92:95], off
	v_med3_f32 v108, v99, s63, v240
	v_med3_f32 v109, v105, s63, v240
	v_med3_f32 v93, v96, s63, v240
	v_med3_f32 v94, v97, s63, v240
	v_mov_b32_e32 v92, v3
	v_cvt_pk_fp8_f32 v92, v93, v94
	v_med3_f32 v95, v98, s63, v240
	v_med3_f32 v94, v102, s63, v240
	v_mov_b32_e32 v93, v3
	v_cvt_pk_fp8_f32 v92, v95, v108 op_sel:[0,0,1]
	v_med3_f32 v95, v103, s63, v240
	v_cvt_pk_fp8_f32 v93, v94, v95
	v_med3_f32 v108, v104, s63, v240
	v_lshl_add_u64 v[94:95], s[8:9], 0, v[100:101]
	v_lshl_add_u64 v[94:95], v[94:95], 0, v[170:171]
	v_cvt_pk_fp8_f32 v93, v108, v109 op_sel:[0,0,1]
	global_store_dwordx2 v[94:95], v[92:93], off
	v_mul_f32_e32 v92, v97, v97
	v_mul_f32_e32 v93, v99, v99
	v_fmac_f32_e32 v92, v96, v96
	v_fmac_f32_e32 v93, v98, v98
	v_add_f32_e32 v92, v92, v93
	v_mul_f32_e32 v93, v103, v103
	v_mul_f32_e32 v96, v105, v105
	v_fmac_f32_e32 v93, v102, v102
	v_fmac_f32_e32 v96, v104, v104
	v_add_f32_e32 v93, v93, v96
	v_add_f32_e32 v98, v92, v93
	v_lshlrev_b32_e32 v92, 16, v124
	v_and_b32_e32 v93, 0xffff0000, v124
	v_lshlrev_b32_e32 v96, 16, v125
	v_and_b32_e32 v97, 0xffff0000, v125
	v_pk_add_f32 v[90:91], v[90:91], v[96:97]
	v_pk_add_f32 v[88:89], v[88:89], v[92:93]
	v_lshlrev_b32_e32 v92, 16, v126
	v_and_b32_e32 v93, 0xffff0000, v126
	v_lshlrev_b32_e32 v96, 16, v127
	v_and_b32_e32 v97, 0xffff0000, v127
	v_pk_add_f32 v[96:97], v[86:87], v[96:97]
	v_pk_add_f32 v[92:93], v[84:85], v[92:93]
	v_cvt_pk_bf16_f32 v84, v88, v89
	v_cvt_pk_bf16_f32 v85, v90, v91
	v_cvt_pk_bf16_f32 v86, v92, v93
	v_cvt_pk_bf16_f32 v87, v96, v97
	global_store_dwordx4 v[106:107], v[84:87], off offset:256
	v_med3_f32 v99, v91, s63, v240
	v_med3_f32 v100, v97, s63, v240
	v_med3_f32 v85, v88, s63, v240
	v_med3_f32 v86, v89, s63, v240
	v_mov_b32_e32 v84, v3
	v_cvt_pk_fp8_f32 v84, v85, v86
	v_med3_f32 v87, v90, s63, v240
	v_med3_f32 v86, v92, s63, v240
	v_mov_b32_e32 v85, v3
	v_cvt_pk_fp8_f32 v84, v87, v99 op_sel:[0,0,1]
	v_med3_f32 v87, v93, s63, v240
	v_cvt_pk_fp8_f32 v85, v86, v87
	v_med3_f32 v99, v96, s63, v240
	v_mul_f32_e32 v86, v97, v97
	v_fmac_f32_e32 v86, v96, v96
	v_cvt_pk_fp8_f32 v85, v99, v100 op_sel:[0,0,1]
	global_store_dwordx2 v[94:95], v[84:85], off offset:128
	v_mul_f32_e32 v84, v89, v89
	v_mul_f32_e32 v85, v91, v91
	v_fmac_f32_e32 v84, v88, v88
	v_fmac_f32_e32 v85, v90, v90
	v_add_f32_e32 v84, v84, v85
	v_mul_f32_e32 v85, v93, v93
	v_fmac_f32_e32 v85, v92, v92
	v_add_f32_e32 v85, v85, v86
	v_add_f32_e32 v84, v84, v85
	v_add_f32_e32 v84, v98, v84
	ds_bpermute_b32 v85, v132, v84
	s_waitcnt lgkmcnt(0)
	v_add_f32_e32 v84, v84, v85
	ds_bpermute_b32 v85, v133, v84
	s_and_saveexec_b64 s[16:17], s[36:37]
	s_movk_i32 s20, 0x110
	s_cbranch_execz .LBB0_2014
	v_readlane_b32 s64, v253, 17
	v_readlane_b32 s65, v253, 18
	s_mov_b32 s21, s65
	v_lshlrev_b64 v[86:87], 7, v[178:179]
	v_readlane_b32 s66, v253, 19
	v_readlane_b32 s67, v253, 20
	v_writelane_b32 v253, s20, 17
	v_lshl_add_u64 v[86:87], s[6:7], 0, v[86:87]
	v_lshl_add_u64 v[86:87], s[14:15], 2, v[86:87]
	v_writelane_b32 v253, s21, 18
	s_mov_b32 s61, s65
	s_lshl_b32 s60, s43, 2
	v_writelane_b32 v253, s22, 19
	v_writelane_b32 v253, s23, 20
	v_lshl_add_u64 v[86:87], v[86:87], 0, s[60:61]
	s_waitcnt lgkmcnt(0)
	v_add_f32_e32 v84, v84, v85
	global_store_dword v[86:87], v84, off
.LBB0_2014:
	s_or_b64 exec, exec, s[16:17]
	v_lshlrev_b32_e32 v86, 16, v120
	v_and_b32_e32 v87, 0xffff0000, v120
	v_lshlrev_b32_e32 v88, 16, v121
	v_and_b32_e32 v89, 0xffff0000, v121
	s_waitcnt lgkmcnt(0)
	v_lshlrev_b64 v[84:85], 11, v[176:177]
	v_pk_add_f32 v[82:83], v[82:83], v[88:89]
	v_pk_add_f32 v[80:81], v[80:81], v[86:87]
	v_lshlrev_b32_e32 v86, 16, v122
	v_and_b32_e32 v87, 0xffff0000, v122
	v_lshlrev_b32_e32 v88, 16, v123
	v_and_b32_e32 v89, 0xffff0000, v123
	v_pk_add_f32 v[88:89], v[78:79], v[88:89]
	v_pk_add_f32 v[86:87], v[76:77], v[86:87]
	v_lshl_add_u64 v[90:91], v[84:85], 1, s[4:5]
	v_cvt_pk_bf16_f32 v76, v80, v81
	v_cvt_pk_bf16_f32 v77, v82, v83
	v_cvt_pk_bf16_f32 v78, v86, v87
	v_cvt_pk_bf16_f32 v79, v88, v89
	v_lshl_add_u64 v[90:91], v[170:171], 1, v[90:91]
	global_store_dwordx4 v[90:91], v[76:79], off
	v_med3_f32 v92, v83, s63, v240
	v_med3_f32 v93, v89, s63, v240
	v_med3_f32 v77, v80, s63, v240
	v_med3_f32 v78, v81, s63, v240
	v_mov_b32_e32 v76, v3
	v_cvt_pk_fp8_f32 v76, v77, v78
	v_med3_f32 v79, v82, s63, v240
	v_med3_f32 v78, v86, s63, v240
	v_mov_b32_e32 v77, v3
	v_cvt_pk_fp8_f32 v76, v79, v92 op_sel:[0,0,1]
	v_med3_f32 v79, v87, s63, v240
	v_cvt_pk_fp8_f32 v77, v78, v79
	v_med3_f32 v92, v88, s63, v240
	v_lshl_add_u64 v[78:79], s[8:9], 0, v[84:85]
	v_lshl_add_u64 v[78:79], v[78:79], 0, v[170:171]
	v_cvt_pk_fp8_f32 v77, v92, v93 op_sel:[0,0,1]
	global_store_dwordx2 v[78:79], v[76:77], off
	v_mul_f32_e32 v76, v81, v81
	v_mul_f32_e32 v77, v83, v83
	v_fmac_f32_e32 v76, v80, v80
	v_fmac_f32_e32 v77, v82, v82
	v_add_f32_e32 v76, v76, v77
	v_mul_f32_e32 v77, v87, v87
	v_mul_f32_e32 v80, v89, v89
	v_fmac_f32_e32 v77, v86, v86
	v_fmac_f32_e32 v80, v88, v88
	v_add_f32_e32 v77, v77, v80
	v_add_f32_e32 v82, v76, v77
	v_lshlrev_b32_e32 v76, 16, v116
	v_and_b32_e32 v77, 0xffff0000, v116
	v_lshlrev_b32_e32 v80, 16, v117
	v_and_b32_e32 v81, 0xffff0000, v117
	v_pk_add_f32 v[74:75], v[74:75], v[80:81]
	v_pk_add_f32 v[72:73], v[72:73], v[76:77]
	v_lshlrev_b32_e32 v76, 16, v118
	v_and_b32_e32 v77, 0xffff0000, v118
	v_lshlrev_b32_e32 v80, 16, v119
	v_and_b32_e32 v81, 0xffff0000, v119
	v_pk_add_f32 v[80:81], v[70:71], v[80:81]
	v_pk_add_f32 v[76:77], v[68:69], v[76:77]
	v_cvt_pk_bf16_f32 v68, v72, v73
	v_cvt_pk_bf16_f32 v69, v74, v75
	v_cvt_pk_bf16_f32 v70, v76, v77
	v_cvt_pk_bf16_f32 v71, v80, v81
	global_store_dwordx4 v[90:91], v[68:71], off offset:256
	v_med3_f32 v83, v75, s63, v240
	v_med3_f32 v84, v81, s63, v240
	v_med3_f32 v69, v72, s63, v240
	v_med3_f32 v70, v73, s63, v240
	v_mov_b32_e32 v68, v3
	v_cvt_pk_fp8_f32 v68, v69, v70
	v_med3_f32 v71, v74, s63, v240
	v_med3_f32 v70, v76, s63, v240
	v_mov_b32_e32 v69, v3
	v_cvt_pk_fp8_f32 v68, v71, v83 op_sel:[0,0,1]
	v_med3_f32 v71, v77, s63, v240
	v_cvt_pk_fp8_f32 v69, v70, v71
	v_med3_f32 v83, v80, s63, v240
	v_mul_f32_e32 v70, v81, v81
	v_fmac_f32_e32 v70, v80, v80
	v_cvt_pk_fp8_f32 v69, v83, v84 op_sel:[0,0,1]
	global_store_dwordx2 v[78:79], v[68:69], off offset:128
	v_mul_f32_e32 v68, v73, v73
	v_mul_f32_e32 v69, v75, v75
	v_fmac_f32_e32 v68, v72, v72
	v_fmac_f32_e32 v69, v74, v74
	v_add_f32_e32 v68, v68, v69
	v_mul_f32_e32 v69, v77, v77
	v_fmac_f32_e32 v69, v76, v76
	v_add_f32_e32 v69, v69, v70
	v_add_f32_e32 v68, v68, v69
	v_add_f32_e32 v68, v82, v68
	ds_bpermute_b32 v69, v132, v68
	s_waitcnt lgkmcnt(0)
	v_add_f32_e32 v68, v68, v69
	ds_bpermute_b32 v69, v133, v68
	s_and_saveexec_b64 s[16:17], s[36:37]
	s_cbranch_execz .LBB0_2016
	v_readlane_b32 s64, v253, 17
	v_readlane_b32 s65, v253, 18
	s_mov_b32 s21, s65
	v_lshlrev_b64 v[70:71], 7, v[176:177]
	v_readlane_b32 s66, v253, 19
	v_readlane_b32 s67, v253, 20
	v_writelane_b32 v253, s20, 17
	v_lshl_add_u64 v[70:71], s[6:7], 0, v[70:71]
	v_lshl_add_u64 v[70:71], s[14:15], 2, v[70:71]
	v_writelane_b32 v253, s21, 18
	s_mov_b32 s61, s65
	s_lshl_b32 s60, s43, 2
	v_writelane_b32 v253, s22, 19
	v_writelane_b32 v253, s23, 20
	v_lshl_add_u64 v[70:71], v[70:71], 0, s[60:61]
	s_waitcnt lgkmcnt(0)
	v_add_f32_e32 v68, v68, v69
	global_store_dword v[70:71], v68, off
.LBB0_2016:
	s_or_b64 exec, exec, s[16:17]
	v_add_u32_e32 v102, 0x80, v172
	v_ashrrev_i32_e32 v103, 31, v102
	v_lshlrev_b64 v[110:111], 12, v[102:103]
	s_waitcnt lgkmcnt(0)
	v_lshl_add_u64 v[68:69], v[174:175], 0, v[110:111]
	global_load_dwordx4 v[106:109], v[68:69], off
	global_load_dwordx4 v[92:95], v[68:69], off offset:256
	v_add_u32_e32 v100, 0x90, v172
	v_ashrrev_i32_e32 v101, 31, v100
	v_lshlrev_b64 v[68:69], 12, v[100:101]
	v_add_u32_e32 v98, 0xa0, v172
	v_lshl_add_u64 v[68:69], v[174:175], 0, v[68:69]
	v_ashrrev_i32_e32 v99, 31, v98
	global_load_dwordx4 v[88:91], v[68:69], off
	global_load_dwordx4 v[84:87], v[68:69], off offset:256
	v_lshlrev_b64 v[68:69], 12, v[98:99]
	v_add_u32_e32 v96, 0xb0, v172
	v_lshl_add_u64 v[68:69], v[174:175], 0, v[68:69]
	v_ashrrev_i32_e32 v97, 31, v96
	global_load_dwordx4 v[80:83], v[68:69], off
	global_load_dwordx4 v[76:79], v[68:69], off offset:256
	v_lshlrev_b64 v[68:69], 12, v[96:97]
	v_lshl_add_u64 v[68:69], v[174:175], 0, v[68:69]
	global_load_dwordx4 v[72:75], v[68:69], off
	s_nop 0
	global_load_dwordx4 v[68:71], v[68:69], off offset:256
	v_lshl_add_u64 v[110:111], s[4:5], 0, v[110:111]
	v_lshl_add_u64 v[110:111], v[170:171], 1, v[110:111]
	v_lshlrev_b64 v[104:105], 11, v[102:103]
	s_waitcnt vmcnt(0) lgkmcnt(0)
	v_lshlrev_b32_e32 v112, 16, v106
	v_and_b32_e32 v113, 0xffff0000, v106
	v_lshlrev_b32_e32 v106, 16, v107
	v_and_b32_e32 v107, 0xffff0000, v107
	v_pk_add_f32 v[66:67], v[66:67], v[106:107]
	v_lshlrev_b32_e32 v106, 16, v108
	v_and_b32_e32 v107, 0xffff0000, v108
	v_lshlrev_b32_e32 v108, 16, v109
	v_and_b32_e32 v109, 0xffff0000, v109
	v_pk_add_f32 v[64:65], v[64:65], v[112:113]
	v_pk_add_f32 v[108:109], v[62:63], v[108:109]
	v_pk_add_f32 v[106:107], v[60:61], v[106:107]
	v_cvt_pk_bf16_f32 v60, v64, v65
	v_cvt_pk_bf16_f32 v61, v66, v67
	v_cvt_pk_bf16_f32 v62, v106, v107
	v_cvt_pk_bf16_f32 v63, v108, v109
	global_store_dwordx4 v[110:111], v[60:63], off
	v_med3_f32 v112, v67, s63, v240
	v_med3_f32 v113, v109, s63, v240
	v_med3_f32 v60, v64, s63, v240
	v_med3_f32 v61, v65, s63, v240
	v_mov_b32_e32 v62, v3
	v_cvt_pk_fp8_f32 v62, v60, v61
	v_med3_f32 v63, v66, s63, v240
	v_med3_f32 v60, v106, s63, v240
	v_med3_f32 v61, v107, s63, v240
	v_cvt_pk_fp8_f32 v62, v63, v112 op_sel:[0,0,1]
	v_mov_b32_e32 v63, v3
	v_cvt_pk_fp8_f32 v63, v60, v61
	v_med3_f32 v112, v108, s63, v240
	v_lshl_add_u64 v[60:61], s[8:9], 0, v[104:105]
	v_lshl_add_u64 v[60:61], v[60:61], 0, v[170:171]
	v_cvt_pk_fp8_f32 v63, v112, v113 op_sel:[0,0,1]
	global_store_dwordx2 v[60:61], v[62:63], off
	v_mul_f32_e32 v62, v65, v65
	v_mul_f32_e32 v63, v67, v67
	v_fmac_f32_e32 v62, v64, v64
	v_fmac_f32_e32 v63, v66, v66
	v_add_f32_e32 v62, v62, v63
	v_mul_f32_e32 v63, v107, v107
	v_mul_f32_e32 v64, v109, v109
	v_fmac_f32_e32 v63, v106, v106
	v_fmac_f32_e32 v64, v108, v108
	v_add_f32_e32 v63, v63, v64
	v_add_f32_e32 v64, v62, v63
	v_lshlrev_b32_e32 v62, 16, v92
	v_and_b32_e32 v63, 0xffff0000, v92
	v_pk_add_f32 v[56:57], v[56:57], v[62:63]
	v_lshlrev_b32_e32 v62, 16, v94
	v_and_b32_e32 v63, 0xffff0000, v94
	v_pk_add_f32 v[52:53], v[52:53], v[62:63]
	v_med3_f32 v63, v56, s63, v240
	v_med3_f32 v65, v57, s63, v240
	v_mov_b32_e32 v62, v3
	v_cvt_pk_fp8_f32 v62, v63, v65
	v_lshlrev_b32_e32 v66, 16, v93
	v_and_b32_e32 v67, 0xffff0000, v93
	v_pk_add_f32 v[58:59], v[58:59], v[66:67]
	v_lshlrev_b32_e32 v66, 16, v95
	v_and_b32_e32 v67, 0xffff0000, v95
	v_pk_add_f32 v[54:55], v[54:55], v[66:67]
	v_med3_f32 v66, v58, s63, v240
	v_med3_f32 v67, v59, s63, v240
	v_cvt_pk_bf16_f32 v92, v56, v57
	v_cvt_pk_bf16_f32 v94, v52, v53
	v_cvt_pk_fp8_f32 v62, v66, v67 op_sel:[0,0,1]
	v_med3_f32 v66, v53, s63, v240
	v_mul_f32_e32 v57, v57, v57
	v_mul_f32_e32 v53, v53, v53
	v_med3_f32 v65, v52, s63, v240
	v_fmac_f32_e32 v57, v56, v56
	v_mul_f32_e32 v56, v59, v59
	v_fmac_f32_e32 v53, v52, v52
	v_mul_f32_e32 v52, v55, v55
	v_fmac_f32_e32 v56, v58, v58
	v_fmac_f32_e32 v52, v54, v54
	v_add_f32_e32 v56, v57, v56
	v_add_f32_e32 v52, v53, v52
	v_add_f32_e32 v52, v56, v52
	v_add_f32_e32 v52, v64, v52
	ds_bpermute_b32 v53, v132, v52
	v_mov_b32_e32 v63, v3
	v_cvt_pk_fp8_f32 v63, v65, v66
	v_cvt_pk_bf16_f32 v93, v58, v59
	v_cvt_pk_bf16_f32 v95, v54, v55
	s_waitcnt lgkmcnt(0)
	v_add_f32_e32 v52, v52, v53
	global_store_dwordx4 v[110:111], v[92:95], off offset:256
	v_med3_f32 v67, v54, s63, v240
	ds_bpermute_b32 v53, v133, v52
	v_med3_f32 v92, v55, s63, v240
	v_cvt_pk_fp8_f32 v63, v67, v92 op_sel:[0,0,1]
	global_store_dwordx2 v[60:61], v[62:63], off offset:128
	s_and_saveexec_b64 s[16:17], s[36:37]
	s_cbranch_execz .LBB0_2018
	v_readlane_b32 s64, v253, 17
	v_readlane_b32 s65, v253, 18
	s_mov_b32 s21, s65
	v_lshlrev_b64 v[54:55], 7, v[102:103]
	v_readlane_b32 s66, v253, 19
	v_readlane_b32 s67, v253, 20
	v_writelane_b32 v253, s20, 17
	v_lshl_add_u64 v[54:55], s[6:7], 0, v[54:55]
	v_lshl_add_u64 v[54:55], s[14:15], 2, v[54:55]
	v_writelane_b32 v253, s21, 18
	s_mov_b32 s61, s65
	s_lshl_b32 s60, s43, 2
	v_writelane_b32 v253, s22, 19
	v_writelane_b32 v253, s23, 20
	v_lshl_add_u64 v[54:55], v[54:55], 0, s[60:61]
	s_waitcnt lgkmcnt(0)
	v_add_f32_e32 v52, v52, v53
	global_store_dword v[54:55], v52, off
.LBB0_2018:
	s_or_b64 exec, exec, s[16:17]
	v_lshlrev_b32_e32 v54, 16, v88
	v_and_b32_e32 v55, 0xffff0000, v88
	v_lshlrev_b32_e32 v56, 16, v89
	v_and_b32_e32 v57, 0xffff0000, v89
	s_waitcnt lgkmcnt(0)
	v_lshlrev_b64 v[52:53], 11, v[100:101]
	v_pk_add_f32 v[50:51], v[50:51], v[56:57]
	v_pk_add_f32 v[48:49], v[48:49], v[54:55]
	v_lshlrev_b32_e32 v54, 16, v90
	v_and_b32_e32 v55, 0xffff0000, v90
	v_lshlrev_b32_e32 v56, 16, v91
	v_and_b32_e32 v57, 0xffff0000, v91
	v_pk_add_f32 v[56:57], v[46:47], v[56:57]
	v_pk_add_f32 v[54:55], v[44:45], v[54:55]
	v_lshl_add_u64 v[58:59], v[52:53], 1, s[4:5]
	v_cvt_pk_bf16_f32 v44, v48, v49
	v_cvt_pk_bf16_f32 v45, v50, v51
	v_cvt_pk_bf16_f32 v46, v54, v55
	v_cvt_pk_bf16_f32 v47, v56, v57
	v_lshl_add_u64 v[58:59], v[170:171], 1, v[58:59]
	global_store_dwordx4 v[58:59], v[44:47], off
	v_med3_f32 v60, v51, s63, v240
	v_med3_f32 v61, v57, s63, v240
	v_med3_f32 v45, v48, s63, v240
	v_med3_f32 v46, v49, s63, v240
	v_mov_b32_e32 v44, v3
	v_cvt_pk_fp8_f32 v44, v45, v46
	v_med3_f32 v47, v50, s63, v240
	v_med3_f32 v46, v54, s63, v240
	v_mov_b32_e32 v45, v3
	v_cvt_pk_fp8_f32 v44, v47, v60 op_sel:[0,0,1]
	v_med3_f32 v47, v55, s63, v240
	v_cvt_pk_fp8_f32 v45, v46, v47
	v_med3_f32 v60, v56, s63, v240
	v_lshl_add_u64 v[46:47], s[8:9], 0, v[52:53]
	v_lshl_add_u64 v[46:47], v[46:47], 0, v[170:171]
	v_cvt_pk_fp8_f32 v45, v60, v61 op_sel:[0,0,1]
	global_store_dwordx2 v[46:47], v[44:45], off
	v_mul_f32_e32 v44, v49, v49
	v_mul_f32_e32 v45, v51, v51
	v_fmac_f32_e32 v44, v48, v48
	v_fmac_f32_e32 v45, v50, v50
	v_add_f32_e32 v44, v44, v45
	v_mul_f32_e32 v45, v55, v55
	v_mul_f32_e32 v48, v57, v57
	v_fmac_f32_e32 v45, v54, v54
	v_fmac_f32_e32 v48, v56, v56
	v_add_f32_e32 v45, v45, v48
	v_add_f32_e32 v50, v44, v45
	v_lshlrev_b32_e32 v44, 16, v84
	v_and_b32_e32 v45, 0xffff0000, v84
	v_lshlrev_b32_e32 v48, 16, v85
	v_and_b32_e32 v49, 0xffff0000, v85
	v_pk_add_f32 v[42:43], v[42:43], v[48:49]
	v_pk_add_f32 v[40:41], v[40:41], v[44:45]
	v_lshlrev_b32_e32 v44, 16, v86
	v_and_b32_e32 v45, 0xffff0000, v86
	v_lshlrev_b32_e32 v48, 16, v87
	v_and_b32_e32 v49, 0xffff0000, v87
	v_pk_add_f32 v[48:49], v[38:39], v[48:49]
	v_pk_add_f32 v[44:45], v[36:37], v[44:45]
	v_cvt_pk_bf16_f32 v36, v40, v41
	v_cvt_pk_bf16_f32 v37, v42, v43
	v_cvt_pk_bf16_f32 v38, v44, v45
	v_cvt_pk_bf16_f32 v39, v48, v49
	global_store_dwordx4 v[58:59], v[36:39], off offset:256
	v_med3_f32 v51, v43, s63, v240
	v_med3_f32 v52, v49, s63, v240
	v_med3_f32 v37, v40, s63, v240
	v_med3_f32 v38, v41, s63, v240
	v_mov_b32_e32 v36, v3
	v_cvt_pk_fp8_f32 v36, v37, v38
	v_med3_f32 v39, v42, s63, v240
	v_med3_f32 v38, v44, s63, v240
	v_mov_b32_e32 v37, v3
	v_cvt_pk_fp8_f32 v36, v39, v51 op_sel:[0,0,1]
	v_med3_f32 v39, v45, s63, v240
	v_cvt_pk_fp8_f32 v37, v38, v39
	v_med3_f32 v51, v48, s63, v240
	v_mul_f32_e32 v38, v49, v49
	v_fmac_f32_e32 v38, v48, v48
	v_cvt_pk_fp8_f32 v37, v51, v52 op_sel:[0,0,1]
	global_store_dwordx2 v[46:47], v[36:37], off offset:128
	v_mul_f32_e32 v36, v41, v41
	v_mul_f32_e32 v37, v43, v43
	v_fmac_f32_e32 v36, v40, v40
	v_fmac_f32_e32 v37, v42, v42
	v_add_f32_e32 v36, v36, v37
	v_mul_f32_e32 v37, v45, v45
	v_fmac_f32_e32 v37, v44, v44
	v_add_f32_e32 v37, v37, v38
	v_add_f32_e32 v36, v36, v37
	v_add_f32_e32 v36, v50, v36
	ds_bpermute_b32 v37, v132, v36
	s_waitcnt lgkmcnt(0)
	v_add_f32_e32 v36, v36, v37
	ds_bpermute_b32 v37, v133, v36
	s_and_saveexec_b64 s[16:17], s[36:37]
	s_cbranch_execz .LBB0_2020
	v_readlane_b32 s64, v253, 17
	v_readlane_b32 s65, v253, 18
	s_mov_b32 s21, s65
	v_lshlrev_b64 v[38:39], 7, v[100:101]
	v_readlane_b32 s66, v253, 19
	v_readlane_b32 s67, v253, 20
	v_writelane_b32 v253, s20, 17
	v_lshl_add_u64 v[38:39], s[6:7], 0, v[38:39]
	v_lshl_add_u64 v[38:39], s[14:15], 2, v[38:39]
	v_writelane_b32 v253, s21, 18
	s_mov_b32 s61, s65
	s_lshl_b32 s60, s43, 2
	v_writelane_b32 v253, s22, 19
	v_writelane_b32 v253, s23, 20
	v_lshl_add_u64 v[38:39], v[38:39], 0, s[60:61]
	s_waitcnt lgkmcnt(0)
	v_add_f32_e32 v36, v36, v37
	global_store_dword v[38:39], v36, off
.LBB0_2020:
	s_or_b64 exec, exec, s[16:17]
	v_lshlrev_b32_e32 v38, 16, v80
	v_and_b32_e32 v39, 0xffff0000, v80
	v_lshlrev_b32_e32 v40, 16, v81
	v_and_b32_e32 v41, 0xffff0000, v81
	s_waitcnt lgkmcnt(0)
	v_lshlrev_b64 v[36:37], 11, v[98:99]
	v_pk_add_f32 v[34:35], v[34:35], v[40:41]
	v_pk_add_f32 v[32:33], v[32:33], v[38:39]
	v_lshlrev_b32_e32 v38, 16, v82
	v_and_b32_e32 v39, 0xffff0000, v82
	v_lshlrev_b32_e32 v40, 16, v83
	v_and_b32_e32 v41, 0xffff0000, v83
	v_pk_add_f32 v[40:41], v[30:31], v[40:41]
	v_pk_add_f32 v[38:39], v[28:29], v[38:39]
	v_lshl_add_u64 v[42:43], v[36:37], 1, s[4:5]
	v_cvt_pk_bf16_f32 v28, v32, v33
	v_cvt_pk_bf16_f32 v29, v34, v35
	v_cvt_pk_bf16_f32 v30, v38, v39
	v_cvt_pk_bf16_f32 v31, v40, v41
	v_lshl_add_u64 v[42:43], v[170:171], 1, v[42:43]
	global_store_dwordx4 v[42:43], v[28:31], off
	v_med3_f32 v44, v35, s63, v240
	v_med3_f32 v45, v41, s63, v240
	v_med3_f32 v29, v32, s63, v240
	v_med3_f32 v30, v33, s63, v240
	v_mov_b32_e32 v28, v3
	v_cvt_pk_fp8_f32 v28, v29, v30
	v_med3_f32 v31, v34, s63, v240
	v_med3_f32 v30, v38, s63, v240
	v_mov_b32_e32 v29, v3
	v_cvt_pk_fp8_f32 v28, v31, v44 op_sel:[0,0,1]
	v_med3_f32 v31, v39, s63, v240
	v_cvt_pk_fp8_f32 v29, v30, v31
	v_med3_f32 v44, v40, s63, v240
	v_lshl_add_u64 v[30:31], s[8:9], 0, v[36:37]
	v_lshl_add_u64 v[30:31], v[30:31], 0, v[170:171]
	v_cvt_pk_fp8_f32 v29, v44, v45 op_sel:[0,0,1]
	global_store_dwordx2 v[30:31], v[28:29], off
	v_mul_f32_e32 v28, v33, v33
	v_mul_f32_e32 v29, v35, v35
	v_fmac_f32_e32 v28, v32, v32
	v_fmac_f32_e32 v29, v34, v34
	v_add_f32_e32 v28, v28, v29
	v_mul_f32_e32 v29, v39, v39
	v_mul_f32_e32 v32, v41, v41
	v_fmac_f32_e32 v29, v38, v38
	v_fmac_f32_e32 v32, v40, v40
	v_add_f32_e32 v29, v29, v32
	v_add_f32_e32 v34, v28, v29
	v_lshlrev_b32_e32 v28, 16, v76
	v_and_b32_e32 v29, 0xffff0000, v76
	v_lshlrev_b32_e32 v32, 16, v77
	v_and_b32_e32 v33, 0xffff0000, v77
	v_pk_add_f32 v[26:27], v[26:27], v[32:33]
	v_pk_add_f32 v[24:25], v[24:25], v[28:29]
	v_lshlrev_b32_e32 v28, 16, v78
	v_and_b32_e32 v29, 0xffff0000, v78
	v_lshlrev_b32_e32 v32, 16, v79
	v_and_b32_e32 v33, 0xffff0000, v79
	v_pk_add_f32 v[32:33], v[22:23], v[32:33]
	v_pk_add_f32 v[28:29], v[20:21], v[28:29]
	v_cvt_pk_bf16_f32 v20, v24, v25
	v_cvt_pk_bf16_f32 v21, v26, v27
	v_cvt_pk_bf16_f32 v22, v28, v29
	v_cvt_pk_bf16_f32 v23, v32, v33
	global_store_dwordx4 v[42:43], v[20:23], off offset:256
	v_med3_f32 v35, v27, s63, v240
	v_med3_f32 v36, v33, s63, v240
	v_med3_f32 v21, v24, s63, v240
	v_med3_f32 v22, v25, s63, v240
	v_mov_b32_e32 v20, v3
	v_cvt_pk_fp8_f32 v20, v21, v22
	v_med3_f32 v23, v26, s63, v240
	v_med3_f32 v22, v28, s63, v240
	v_mov_b32_e32 v21, v3
	v_cvt_pk_fp8_f32 v20, v23, v35 op_sel:[0,0,1]
	v_med3_f32 v23, v29, s63, v240
	v_cvt_pk_fp8_f32 v21, v22, v23
	v_med3_f32 v35, v32, s63, v240
	v_mul_f32_e32 v22, v33, v33
	v_fmac_f32_e32 v22, v32, v32
	v_cvt_pk_fp8_f32 v21, v35, v36 op_sel:[0,0,1]
	global_store_dwordx2 v[30:31], v[20:21], off offset:128
	v_mul_f32_e32 v20, v25, v25
	v_mul_f32_e32 v21, v27, v27
	v_fmac_f32_e32 v20, v24, v24
	v_fmac_f32_e32 v21, v26, v26
	v_add_f32_e32 v20, v20, v21
	v_mul_f32_e32 v21, v29, v29
	v_fmac_f32_e32 v21, v28, v28
	v_add_f32_e32 v21, v21, v22
	v_add_f32_e32 v20, v20, v21
	v_add_f32_e32 v20, v34, v20
	ds_bpermute_b32 v21, v132, v20
	s_waitcnt lgkmcnt(0)
	v_add_f32_e32 v20, v20, v21
	ds_bpermute_b32 v21, v133, v20
	s_and_saveexec_b64 s[16:17], s[36:37]
	s_cbranch_execz .LBB0_2022
	v_readlane_b32 s64, v253, 17
	v_readlane_b32 s65, v253, 18
	s_mov_b32 s21, s65
	v_lshlrev_b64 v[22:23], 7, v[98:99]
	v_readlane_b32 s66, v253, 19
	v_readlane_b32 s67, v253, 20
	v_writelane_b32 v253, s20, 17
	v_lshl_add_u64 v[22:23], s[6:7], 0, v[22:23]
	v_lshl_add_u64 v[22:23], s[14:15], 2, v[22:23]
	v_writelane_b32 v253, s21, 18
	s_mov_b32 s61, s65
	s_lshl_b32 s60, s43, 2
	v_writelane_b32 v253, s22, 19
	v_writelane_b32 v253, s23, 20
	v_lshl_add_u64 v[22:23], v[22:23], 0, s[60:61]
	s_waitcnt lgkmcnt(0)
	v_add_f32_e32 v20, v20, v21
	global_store_dword v[22:23], v20, off
.LBB0_2022:
	s_or_b64 exec, exec, s[16:17]
	v_lshlrev_b32_e32 v22, 16, v72
	v_and_b32_e32 v23, 0xffff0000, v72
	v_lshlrev_b32_e32 v24, 16, v73
	v_and_b32_e32 v25, 0xffff0000, v73
	s_waitcnt lgkmcnt(0)
	v_lshlrev_b64 v[20:21], 11, v[96:97]
	v_pk_add_f32 v[18:19], v[18:19], v[24:25]
	v_pk_add_f32 v[16:17], v[16:17], v[22:23]
	v_lshlrev_b32_e32 v22, 16, v74
	v_and_b32_e32 v23, 0xffff0000, v74
	v_lshlrev_b32_e32 v24, 16, v75
	v_and_b32_e32 v25, 0xffff0000, v75
	v_pk_add_f32 v[24:25], v[14:15], v[24:25]
	v_pk_add_f32 v[22:23], v[12:13], v[22:23]
	v_lshl_add_u64 v[26:27], v[20:21], 1, s[4:5]
	v_cvt_pk_bf16_f32 v12, v16, v17
	v_cvt_pk_bf16_f32 v13, v18, v19
	v_cvt_pk_bf16_f32 v14, v22, v23
	v_cvt_pk_bf16_f32 v15, v24, v25
	v_lshl_add_u64 v[26:27], v[170:171], 1, v[26:27]
	global_store_dwordx4 v[26:27], v[12:15], off
	v_med3_f32 v28, v19, s63, v240
	v_med3_f32 v29, v25, s63, v240
	v_med3_f32 v13, v16, s63, v240
	v_med3_f32 v14, v17, s63, v240
	v_mov_b32_e32 v12, v3
	v_cvt_pk_fp8_f32 v12, v13, v14
	v_med3_f32 v15, v18, s63, v240
	v_med3_f32 v14, v22, s63, v240
	v_mov_b32_e32 v13, v3
	v_cvt_pk_fp8_f32 v12, v15, v28 op_sel:[0,0,1]
	v_med3_f32 v15, v23, s63, v240
	v_cvt_pk_fp8_f32 v13, v14, v15
	v_med3_f32 v28, v24, s63, v240
	v_lshl_add_u64 v[14:15], s[8:9], 0, v[20:21]
	v_lshl_add_u64 v[14:15], v[14:15], 0, v[170:171]
	v_cvt_pk_fp8_f32 v13, v28, v29 op_sel:[0,0,1]
	global_store_dwordx2 v[14:15], v[12:13], off
	v_mul_f32_e32 v12, v17, v17
	v_mul_f32_e32 v13, v19, v19
	v_fmac_f32_e32 v12, v16, v16
	v_fmac_f32_e32 v13, v18, v18
	v_add_f32_e32 v12, v12, v13
	v_mul_f32_e32 v13, v23, v23
	v_mul_f32_e32 v16, v25, v25
	v_fmac_f32_e32 v13, v22, v22
	v_fmac_f32_e32 v16, v24, v24
	v_add_f32_e32 v13, v13, v16
	v_add_f32_e32 v18, v12, v13
	v_lshlrev_b32_e32 v12, 16, v68
	v_and_b32_e32 v13, 0xffff0000, v68
	v_lshlrev_b32_e32 v16, 16, v69
	v_and_b32_e32 v17, 0xffff0000, v69
	v_pk_add_f32 v[10:11], v[10:11], v[16:17]
	v_pk_add_f32 v[8:9], v[8:9], v[12:13]
	v_lshlrev_b32_e32 v12, 16, v70
	v_and_b32_e32 v13, 0xffff0000, v70
	v_lshlrev_b32_e32 v16, 16, v71
	v_and_b32_e32 v17, 0xffff0000, v71
	v_pk_add_f32 v[16:17], v[6:7], v[16:17]
	v_pk_add_f32 v[12:13], v[4:5], v[12:13]
	v_cvt_pk_bf16_f32 v4, v8, v9
	v_cvt_pk_bf16_f32 v5, v10, v11
	v_cvt_pk_bf16_f32 v6, v12, v13
	v_cvt_pk_bf16_f32 v7, v16, v17
	global_store_dwordx4 v[26:27], v[4:7], off offset:256
	v_med3_f32 v19, v11, s63, v240
	v_med3_f32 v20, v17, s63, v240
	v_med3_f32 v5, v8, s63, v240
	v_med3_f32 v6, v9, s63, v240
	v_mov_b32_e32 v4, v3
	v_cvt_pk_fp8_f32 v4, v5, v6
	v_med3_f32 v7, v10, s63, v240
	v_med3_f32 v6, v12, s63, v240
	v_mov_b32_e32 v5, v3
	v_cvt_pk_fp8_f32 v4, v7, v19 op_sel:[0,0,1]
	v_med3_f32 v7, v13, s63, v240
	v_cvt_pk_fp8_f32 v5, v6, v7
	v_med3_f32 v19, v16, s63, v240
	v_mul_f32_e32 v6, v17, v17
	v_fmac_f32_e32 v6, v16, v16
	v_cvt_pk_fp8_f32 v5, v19, v20 op_sel:[0,0,1]
	global_store_dwordx2 v[14:15], v[4:5], off offset:128
	v_mul_f32_e32 v4, v9, v9
	v_mul_f32_e32 v5, v11, v11
	v_fmac_f32_e32 v4, v8, v8
	v_fmac_f32_e32 v5, v10, v10
	v_add_f32_e32 v4, v4, v5
	v_mul_f32_e32 v5, v13, v13
	v_fmac_f32_e32 v5, v12, v12
	v_add_f32_e32 v5, v5, v6
	v_add_f32_e32 v4, v4, v5
	v_add_f32_e32 v4, v18, v4
	ds_bpermute_b32 v5, v132, v4
	s_waitcnt lgkmcnt(0)
	v_add_f32_e32 v4, v4, v5
	ds_bpermute_b32 v5, v133, v4
	s_and_saveexec_b64 s[16:17], s[36:37]
	s_cbranch_execz .LBB0_2024
	v_readlane_b32 s64, v253, 17
	v_readlane_b32 s65, v253, 18
	s_mov_b32 s21, s65
	v_lshlrev_b64 v[6:7], 7, v[96:97]
	v_readlane_b32 s66, v253, 19
	v_readlane_b32 s67, v253, 20
	v_writelane_b32 v253, s20, 17
	v_lshl_add_u64 v[6:7], s[6:7], 0, v[6:7]
	v_lshl_add_u64 v[6:7], s[14:15], 2, v[6:7]
	v_writelane_b32 v253, s21, 18
	s_mov_b32 s61, s65
	s_lshl_b32 s60, s43, 2
	v_writelane_b32 v253, s22, 19
	v_writelane_b32 v253, s23, 20
	v_lshl_add_u64 v[6:7], v[6:7], 0, s[60:61]
	s_waitcnt lgkmcnt(0)
	v_add_f32_e32 v4, v4, v5
	global_store_dword v[6:7], v4, off

.LBB0_2080:
	s_cmp_lt_i32 s90, 50
	s_cselect_b64 s[0:1], -1, 0
	s_cmp_gt_i32 s91, 49
	s_cselect_b64 s[2:3], -1, 0
	s_and_b64 s[0:1], s[0:1], s[2:3]
	s_and_b64 vcc, exec, s[0:1]
	s_cbranch_vccz .LBB0_2084
	v_readlane_b32 s1, v252, 0
	s_nop 0
	v_readfirstlane_b32 s0, v0
	s_ashr_i32 s0, s0, 6
	v_writelane_b32 v252, s1, 0
	s_lshl_b32 s1, s88, 3
	s_add_i32 s0, s1, s0
	s_cmpk_gt_i32 s0, 0x3fff
	s_cbranch_scc1 .LBB0_2084
	s_add_i32 s1, s72, 0x210e0
	v_mov_b32_e32 v1, s1
	ds_read_b64 v[2:3], v1
	v_and_b32_e32 v36, 63, v0
	v_mov_b32_e32 v35, 0
	v_lshlrev_b32_e32 v34, 4, v36
	v_readlane_b32 s1, v252, 0
	s_waitcnt lgkmcnt(0)
	v_lshl_add_u64 v[16:17], v[2:3], 0, v[34:35]
	v_add_co_u32_e32 v32, vcc, 0x1000, v16
	global_load_dwordx4 v[0:3], v[16:17], off
	global_load_dwordx4 v[4:7], v[16:17], off offset:1024
	global_load_dwordx4 v[8:11], v[16:17], off offset:2048
	global_load_dwordx4 v[12:15], v[16:17], off offset:3072
	v_addc_co_u32_e32 v33, vcc, 0, v17, vcc
	global_load_dwordx4 v[16:19], v[32:33], off
	global_load_dwordx4 v[20:23], v[32:33], off offset:1024
	global_load_dwordx4 v[24:27], v[32:33], off offset:2048
	global_load_dwordx4 v[28:31], v[32:33], off offset:3072
	v_xor_b32_e32 v32, 1, v230
	v_cmp_lt_i32_e32 vcc, v32, v231
	s_lshl_b32 s2, s1, 3
	s_ashr_i32 s1, s0, 31
	v_cndmask_b32_e32 v32, v230, v32, vcc
	v_lshlrev_b32_e32 v46, 2, v32
	v_xor_b32_e32 v32, 2, v230
	v_cmp_lt_i32_e32 vcc, v32, v231
	s_lshl_b64 s[4:5], s[0:1], 13
	s_add_u32 s4, s84, s4
	v_cndmask_b32_e32 v32, v230, v32, vcc
	v_lshlrev_b32_e32 v47, 2, v32
	v_xor_b32_e32 v32, 4, v230
	v_cmp_lt_i32_e32 vcc, v32, v231
	s_addc_u32 s5, s85, s5
	s_ashr_i32 s3, s2, 31
	v_cndmask_b32_e32 v32, v230, v32, vcc
	v_lshlrev_b32_e32 v48, 2, v32
	v_xor_b32_e32 v32, 8, v230
	v_cmp_lt_i32_e32 vcc, v32, v231
	s_lshl_b64 s[6:7], s[0:1], 12
	v_mov_b32_e32 v52, 0x358637bd
	v_cndmask_b32_e32 v32, v230, v32, vcc
	v_lshlrev_b32_e32 v49, 2, v32
	v_xor_b32_e32 v32, 16, v230
	v_cmp_lt_i32_e32 vcc, v32, v231
	s_mov_b32 s1, 0x800000
	s_movk_i32 s8, 0xf400
	v_cndmask_b32_e32 v32, v230, v32, vcc
	v_lshlrev_b32_e32 v50, 2, v32
	v_xor_b32_e32 v32, 32, v230
	v_cmp_lt_i32_e32 vcc, v32, v231
	s_movk_i32 s9, 0xf800
	s_movk_i32 s10, 0xfc00
	v_cndmask_b32_e32 v32, v230, v32, vcc
	v_lshlrev_b32_e32 v51, 2, v32
	v_lshl_add_u64 v[32:33], s[4:5], 0, v[34:35]
	s_mov_b64 s[4:5], 0x1000
	v_lshl_add_u64 v[32:33], v[32:33], 0, s[4:5]
	s_lshl_b64 s[4:5], s[2:3], 13
	s_add_u32 s6, s68, s6
	v_lshlrev_b32_e32 v34, 3, v36
	s_addc_u32 s7, s69, s7
	v_lshl_add_u64 v[34:35], s[6:7], 0, v[34:35]
	s_mov_b64 s[6:7], 0x5000000
	v_lshl_add_u64 v[34:35], v[34:35], 0, s[6:7]
	s_lshl_b64 s[6:7], s[2:3], 12
	s_movk_i32 s3, 0xf000
.LBB0_2083:
	global_load_dwordx2 v[36:37], v[34:35], off
	global_load_dwordx2 v[38:39], v[34:35], off offset:512
	global_load_dwordx2 v[40:41], v[34:35], off offset:1024
	global_load_dwordx2 v[44:45], v[34:35], off offset:1536
	global_load_dwordx2 v[54:55], v[34:35], off offset:2048
	global_load_dwordx2 v[56:57], v[34:35], off offset:2560
	global_load_dwordx2 v[58:59], v[34:35], off offset:3072
	global_load_dwordx2 v[60:61], v[34:35], off offset:3584
	v_add_co_u32_e32 v42, vcc, s3, v32
	s_add_i32 s0, s0, s2
	s_nop 0
	v_addc_co_u32_e32 v43, vcc, -1, v33, vcc
	v_add_co_u32_e32 v82, vcc, s8, v32
	v_lshl_add_u64 v[34:35], v[34:35], 0, s[6:7]
	s_nop 0
	v_addc_co_u32_e32 v83, vcc, -1, v33, vcc
	v_add_co_u32_e32 v84, vcc, s9, v32
	s_cmpk_lt_i32 s0, 0x4000
	s_nop 0
	v_addc_co_u32_e32 v85, vcc, -1, v33, vcc
	v_add_co_u32_e32 v86, vcc, s10, v32
	s_waitcnt vmcnt(0) lgkmcnt(0)
	v_lshlrev_b32_e32 v62, 16, v36
	v_and_b32_e32 v63, 0xffff0000, v36
	v_lshlrev_b32_e32 v36, 16, v37
	v_and_b32_e32 v37, 0xffff0000, v37
	v_lshlrev_b32_e32 v65, 16, v39
	v_lshlrev_b32_e32 v64, 16, v38
	v_and_b32_e32 v39, 0xffff0000, v39
	v_and_b32_e32 v38, 0xffff0000, v38
	v_and_b32_e32 v67, 0xffff0000, v40
	v_lshlrev_b32_e32 v69, 16, v44
	v_lshlrev_b32_e32 v79, 16, v60
	v_mul_f32_e32 v68, v37, v37
	v_pk_mul_f32 v[88:89], v[38:39], v[38:39]
	v_mul_f32_e32 v78, v63, v63
	v_lshlrev_b32_e32 v66, 16, v40
	v_lshlrev_b32_e32 v40, 16, v41
	v_and_b32_e32 v41, 0xffff0000, v41
	v_mov_b32_e32 v91, v69
	v_mul_f32_e32 v90, v67, v67
	v_mov_b32_e32 v102, v64
	v_mov_b32_e32 v103, v38
	v_mov_b32_e32 v38, v65
	v_pk_fma_f32 v[108:109], v[36:37], v[36:37], v[68:69] op_sel_hi:[1,1,0]
	v_pk_fma_f32 v[64:65], v[64:65], v[64:65], v[88:89]
	v_pk_fma_f32 v[88:89], v[62:63], v[62:63], v[78:79] op_sel_hi:[1,1,0]
	v_and_b32_e32 v71, 0xffff0000, v44
	v_lshlrev_b32_e32 v44, 16, v45
	v_and_b32_e32 v45, 0xffff0000, v45
	v_mul_f32_e32 v92, v41, v41
	v_mov_b32_e32 v93, v79
	v_pk_fma_f32 v[110:111], v[66:67], v[66:67], v[90:91] op_sel_hi:[1,1,0]
	v_mov_b32_e32 v68, v88
	v_mov_b32_e32 v90, v108
	v_mul_f32_e32 v53, v71, v71
	v_mul_f32_e32 v99, v44, v44
	v_mul_f32_e32 v101, v45, v45
	v_mov_b32_e32 v70, v69
	v_pk_fma_f32 v[112:113], v[40:41], v[40:41], v[92:93] op_sel_hi:[1,1,0]
	v_pk_add_f32 v[88:89], v[88:89], v[108:109]
	v_pk_add_f32 v[64:65], v[64:65], v[64:65] op_sel:[0,1] op_sel_hi:[1,0]
	v_pk_mul_f32 v[68:69], v[68:69], v[90:91]
	v_lshlrev_b32_e32 v73, 16, v55
	v_lshlrev_b32_e32 v72, 16, v54
	v_and_b32_e32 v55, 0xffff0000, v55
	v_and_b32_e32 v54, 0xffff0000, v54
	v_mov_b32_e32 v111, v99
	v_mov_b32_e32 v113, v101
	v_mov_b32_e32 v65, v53
	v_mov_b32_e32 v89, v69
	v_pk_mul_f32 v[94:95], v[54:55], v[54:55]
	v_pk_add_f32 v[90:91], v[110:111], v[112:113]
	v_pk_add_f32 v[64:65], v[88:89], v[64:65]
	v_lshlrev_b32_e32 v75, 16, v57
	v_lshlrev_b32_e32 v74, 16, v56
	v_and_b32_e32 v57, 0xffff0000, v57
	v_and_b32_e32 v56, 0xffff0000, v56
	v_mov_b32_e32 v104, v72
	v_mov_b32_e32 v105, v54
	v_mov_b32_e32 v54, v73
	v_pk_fma_f32 v[72:73], v[72:73], v[72:73], v[94:95]
	v_pk_add_f32 v[64:65], v[64:65], v[90:91]
	v_lshlrev_b32_e32 v76, 16, v58
	v_and_b32_e32 v77, 0xffff0000, v58
	v_lshlrev_b32_e32 v58, 16, v59
	v_and_b32_e32 v59, 0xffff0000, v59
	v_pk_mul_f32 v[96:97], v[56:57], v[56:57]
	v_pk_add_f32 v[72:73], v[72:73], v[72:73] op_sel:[0,1] op_sel_hi:[1,0]
	v_pk_add_f32 v[64:65], v[64:65], v[64:65] op_sel:[0,1] op_sel_hi:[1,0]
	v_and_b32_e32 v81, 0xffff0000, v60
	v_lshlrev_b32_e32 v60, 16, v61
	v_and_b32_e32 v61, 0xffff0000, v61
	v_mul_f32_e32 v98, v77, v77
	v_mul_f32_e32 v100, v59, v59
	v_mov_b32_e32 v106, v74
	v_mov_b32_e32 v107, v56
	v_mov_b32_e32 v56, v75
	v_pk_fma_f32 v[74:75], v[74:75], v[74:75], v[96:97]
	v_mov_b32_e32 v92, v72
	v_mov_b32_e32 v78, v64
	v_mul_f32_e32 v114, v81, v81
	v_mul_f32_e32 v115, v60, v60
	v_mul_f32_e32 v116, v61, v61
	v_pk_fma_f32 v[94:95], v[76:77], v[76:77], v[98:99] op_sel_hi:[1,1,0]
	v_pk_fma_f32 v[96:97], v[58:59], v[58:59], v[100:101] op_sel_hi:[1,1,0]
	v_pk_add_f32 v[74:75], v[74:75], v[74:75] op_sel:[0,1] op_sel_hi:[1,0]
	v_pk_add_f32 v[64:65], v[64:65], v[72:73]
	v_pk_mul_f32 v[68:69], v[78:79], v[92:93]
	v_mov_b32_e32 v95, v115
	v_mov_b32_e32 v97, v116
	v_mov_b32_e32 v75, v114
	v_mov_b32_e32 v65, v69
	v_pk_add_f32 v[94:95], v[94:95], v[96:97]
	v_pk_add_f32 v[64:65], v[64:65], v[74:75]
	v_addc_co_u32_e32 v87, vcc, -1, v33, vcc
	v_pk_add_f32 v[64:65], v[64:65], v[94:95]
	v_mov_b32_e32 v80, v79
	v_add_f32_e32 v53, v64, v65
	ds_bpermute_b32 v64, v46, v53
	s_waitcnt lgkmcnt(0)
	v_add_f32_e32 v53, v53, v64
	ds_bpermute_b32 v64, v47, v53
	s_waitcnt lgkmcnt(0)
	v_add_f32_e32 v53, v53, v64
	ds_bpermute_b32 v64, v48, v53
	s_waitcnt lgkmcnt(0)
	v_add_f32_e32 v53, v53, v64
	ds_bpermute_b32 v64, v49, v53
	s_waitcnt lgkmcnt(0)
	v_add_f32_e32 v53, v53, v64
	ds_bpermute_b32 v64, v50, v53
	s_waitcnt lgkmcnt(0)
	v_add_f32_e32 v53, v53, v64
	ds_bpermute_b32 v64, v51, v53
	s_waitcnt lgkmcnt(0)
	v_add_f32_e32 v53, v53, v64
	v_fmamk_f32 v53, v53, 0x3a000000, v52
	v_mul_f32_e32 v64, 0x4b800000, v53
	v_cmp_gt_f32_e32 vcc, s1, v53
	s_nop 1
	v_cndmask_b32_e32 v53, v53, v64, vcc
	v_rsq_f32_e32 v53, v53
	s_nop 0
	v_mul_f32_e32 v64, 0x45800000, v53
	v_cndmask_b32_e32 v64, v53, v64, vcc
	v_pk_mul_f32 v[62:63], v[64:65], v[62:63] op_sel_hi:[0,1]
	v_pk_mul_f32 v[36:37], v[64:65], v[36:37] op_sel_hi:[0,1]
	v_pk_mul_f32 v[68:69], v[64:65], v[102:103] op_sel_hi:[0,1]
	v_pk_mul_f32 v[72:73], v[64:65], v[38:39] op_sel_hi:[0,1]
	v_pk_mul_f32 v[66:67], v[64:65], v[66:67] op_sel_hi:[0,1]
	v_pk_mul_f32 v[40:41], v[64:65], v[40:41] op_sel_hi:[0,1]
	v_pk_mul_f32 v[70:71], v[70:71], v[64:65] op_sel_hi:[1,0]
	v_pk_mul_f32 v[44:45], v[44:45], v[64:65] op_sel_hi:[1,0]
	v_pk_mul_f32 v[74:75], v[64:65], v[104:105] op_sel_hi:[0,1]
	v_pk_mul_f32 v[78:79], v[64:65], v[54:55] op_sel_hi:[0,1]
	v_pk_mul_f32 v[88:89], v[64:65], v[106:107] op_sel_hi:[0,1]
	v_pk_mul_f32 v[90:91], v[64:65], v[56:57] op_sel_hi:[0,1]
	v_pk_mul_f32 v[92:93], v[64:65], v[76:77] op_sel_hi:[0,1]
	v_pk_mul_f32 v[76:77], v[64:65], v[58:59] op_sel_hi:[0,1]
	v_pk_mul_f32 v[94:95], v[80:81], v[64:65] op_sel_hi:[1,0]
	v_pk_mul_f32 v[80:81], v[60:61], v[64:65] op_sel_hi:[1,0]
	v_pk_mul_f32 v[38:39], v[2:3], v[36:37]
	v_pk_mul_f32 v[36:37], v[0:1], v[62:63]
	v_pk_mul_f32 v[56:57], v[6:7], v[72:73]
	v_pk_mul_f32 v[54:55], v[4:5], v[68:69]
	v_pk_mul_f32 v[60:61], v[10:11], v[40:41]
	v_pk_mul_f32 v[58:59], v[8:9], v[66:67]
	v_pk_mul_f32 v[64:65], v[14:15], v[44:45]
	v_pk_mul_f32 v[62:63], v[12:13], v[70:71]
	v_pk_mul_f32 v[68:69], v[18:19], v[78:79]
	v_pk_mul_f32 v[66:67], v[16:17], v[74:75]
	v_pk_mul_f32 v[72:73], v[22:23], v[90:91]
	v_pk_mul_f32 v[70:71], v[20:21], v[88:89]
	v_pk_mul_f32 v[76:77], v[26:27], v[76:77]
	v_pk_mul_f32 v[74:75], v[24:25], v[92:93]
	v_pk_mul_f32 v[80:81], v[30:31], v[80:81]
	v_pk_mul_f32 v[78:79], v[28:29], v[94:95]
	global_store_dwordx4 v[42:43], v[36:39], off
	global_store_dwordx4 v[82:83], v[54:57], off
	global_store_dwordx4 v[84:85], v[58:61], off
	global_store_dwordx4 v[86:87], v[62:65], off
	global_store_dwordx4 v[32:33], v[66:69], off
	global_store_dwordx4 v[32:33], v[70:73], off offset:1024
	global_store_dwordx4 v[32:33], v[74:77], off offset:2048
	global_store_dwordx4 v[32:33], v[78:81], off offset:3072
	v_lshl_add_u64 v[32:33], v[32:33], 0, s[4:5]
	s_cbranch_scc1 .LBB0_2083

	.amdhsa_kernel _Z10fwd_kernel6Params
		.amdhsa_group_segment_fixed_size 0
		.amdhsa_private_segment_fixed_size 0
		.amdhsa_kernarg_size 448
		.amdhsa_user_sgpr_count 2
		.amdhsa_user_sgpr_dispatch_ptr 0
		.amdhsa_user_sgpr_queue_ptr 0
		.amdhsa_user_sgpr_kernarg_segment_ptr 1
		.amdhsa_user_sgpr_dispatch_id 0
		.amdhsa_user_sgpr_kernarg_preload_length 0
		.amdhsa_user_sgpr_kernarg_preload_offset 0
		.amdhsa_user_sgpr_private_segment_size 0
		.amdhsa_uses_dynamic_stack 0
		.amdhsa_enable_private_segment 0
		.amdhsa_system_sgpr_workgroup_id_x 1
		.amdhsa_system_sgpr_workgroup_id_y 0
		.amdhsa_system_sgpr_workgroup_id_z 0
		.amdhsa_system_sgpr_workgroup_info 0
		.amdhsa_system_vgpr_workitem_id 0
		.amdhsa_next_free_vgpr 256
		.amdhsa_next_free_sgpr 102
		.amdhsa_accum_offset 256
		.amdhsa_reserve_vcc 1
		.amdhsa_float_round_mode_32 0
		.amdhsa_float_round_mode_16_64 0
		.amdhsa_float_denorm_mode_32 3
		.amdhsa_float_denorm_mode_16_64 3
		.amdhsa_dx10_clamp 1
		.amdhsa_ieee_mode 1
		.amdhsa_fp16_overflow 0
		.amdhsa_tg_split 0
		.amdhsa_exception_fp_ieee_invalid_op 0
		.amdhsa_exception_fp_denorm_src 0
		.amdhsa_exception_fp_ieee_div_zero 0
		.amdhsa_exception_fp_ieee_overflow 0
		.amdhsa_exception_fp_ieee_underflow 0
		.amdhsa_exception_fp_ieee_inexact 0
		.amdhsa_exception_int_div_zero 0
	.end_amdhsa_kernel

amdhsa.kernels:
  - .agpr_count:     0
    .args:
      - .offset:         0
        .size:           192
        .value_kind:     by_value
      - .offset:         192
        .size:           4
        .value_kind:     hidden_block_count_x
      - .offset:         196
        .size:           4
        .value_kind:     hidden_block_count_y
      - .offset:         200
        .size:           4
        .value_kind:     hidden_block_count_z
      - .offset:         204
        .size:           2
        .value_kind:     hidden_group_size_x
      - .offset:         206
        .size:           2
        .value_kind:     hidden_group_size_y
      - .offset:         208
        .size:           2
        .value_kind:     hidden_group_size_z
      - .offset:         210
        .size:           2
        .value_kind:     hidden_remainder_x
      - .offset:         212
        .size:           2
        .value_kind:     hidden_remainder_y
      - .offset:         214
        .size:           2
        .value_kind:     hidden_remainder_z
      - .offset:         232
        .size:           8
        .value_kind:     hidden_global_offset_x
      - .offset:         240
        .size:           8
        .value_kind:     hidden_global_offset_y
      - .offset:         248
        .size:           8
        .value_kind:     hidden_global_offset_z
      - .offset:         256
        .size:           2
        .value_kind:     hidden_grid_dims
      - .offset:         312
        .size:           4
        .value_kind:     hidden_dynamic_lds_size
    .group_segment_fixed_size: 0
    .kernarg_segment_align: 8
    .kernarg_segment_size: 448
    .language:       OpenCL C
    .language_version:
      - 2
      - 0
    .max_flat_workgroup_size: 512
    .name:           _Z10fwd_kernel6Params
    .private_segment_fixed_size: 0
    .sgpr_count:     108
    .sgpr_spill_count: 347
    .symbol:         _Z10fwd_kernel6Params.kd
    .uniform_work_group_size: 1
    .uses_dynamic_stack: false
    .vgpr_count:     256
    .vgpr_spill_count: 0
    .wavefront_size: 64
